# a quarter of the layer-1 w_down transposition moved out of the prologue into the idle slot of the 96 workgroups without a last-round tile in the layer-1 in-projection
# speedup vs baseline: 1.0022x; 1.0022x over previous
;     const int pr = item >> 1, kb = 2 * (pr / nblk) + (item & 1), nb = pr % nblk, k0 = 64 * kb, n0 = 32 * nb;
;     const int nr = n0 + (lane & 31); const int sc = MAP == 1 ? src_col_in(nr) : nr;
;     float v[32];
; #pragma unroll
;     for (int i = 0; i < 32; ++i) v[i] = sc >= 0 ? W[(size_t)(k0 + 2 * i + (lane >> 5)) * Nsrc + sc] : 0.f;
; #pragma unroll
;     for (int i = 0; i < 32; ++i) { const int k = k0 + 2 * i + (lane >> 5); float x = v[i] * wscale; if (KS) x *= (k < ksplit ? ksA[k] : ksB[k - ksplit]); scr[(2 * i + (lane >> 5)) * 33 + (lane & 31)] = x; }
;     LDS_WAIT(); asm volatile("" ::: "memory");
;     const int c = lane & 7;
; #pragma unroll
;     for (int j = 0; j < 4; ++j) { const int n = (lane >> 3) + 8 * j; const LAS float* s = scr + (8 * c) * 33 + n;
;         const unsigned long long o = (unsigned long long)pg8::pk4_fp8(s[0 * 33], s[1 * 33], s[2 * 33], s[3 * 33]) | ((unsigned long long)pg8::pk4_fp8(s[4 * 33], s[5 * 33], s[6 * 33], s[7 * 33]) << 32);
;         *(GAS unsigned long long*)(WT + (size_t)(n0 + n) * K + k0 + 8 * c) = o; }
;     LDS_WAIT(); asm volatile("" ::: "memory");
; }
; __global__ void __launch_bounds__(NWAVES * 64, 2) hybrid_fwd(Args args) {
;     ...
;     {
;         PHASE_IDS();
;         LAS float* scr = (LAS float*)(F.lds + RING_OFF + wave * 16384);
;         constexpr int I_IN = (DM / 64) * (NPROJ / 32), I_O = (DM / 64) * (DM / 32), I_UP = (DM / 64) * (FF / 32), I_DN = (FF / 64) * (DM / 32);
;         constexpr int I_L = I_IN + I_O + I_UP + I_DN;
;         for (int rep = 0; rep < REP_PRO; ++rep)
;         for (int it = gw; it < DEPTH * I_L; it += NGW) {
;             const int l = it / I_L; int r = it % I_L;
;             if (r < I_IN) { if (l >= PROJ_F8_FROM) p0_transpose_item_f8<true, 1>(args.in[2] + (size_t)l * DM * NSRC, DM, NSRC, NPROJ / 32, (unsigned char*)(ws + WS_WIN + l * SZ_WIN), WUP8_SCALE, args.in[1] + l * DM, args.in[1] + l * DM, DM, scr, r, lane);
;                 else p0_transpose_item<1, true>(args.in[2] + (size_t)l * DM * NSRC, DM, NSRC, NPROJ / 32, (bf16*)(ws + WS_WIN + l * SZ_WIN), args.in[1] + l * DM, args.in[1] + l * DM, DM, scr, r, lane); continue; } r -= I_IN;
;             if (r < I_O) { if (l >= WO_F8_FROM) p0_transpose_item_f8<true>(args.in[13] + (size_t)l * DM * DM, DM, DM, DM / 32, (unsigned char*)(ws + WS_WO + l * SZ_WO), 64.f, args.in[6] + l * 2048, args.in[12] + l * 2048, 2048, scr, r, lane);
.LBB0_11:
	s_or_b64 exec, exec, s[0:1]
	v_mov_b32_e32 v1, v0
	v_readlane_b32 s1, v253, 2
	v_readfirstlane_b32 s0, v1
	s_ashr_i32 s0, s0, 6
	s_lshl_b32 s1, s1, 3
	s_add_i32 s80, s0, s1
	s_lshl_b32 s0, s0, 14
	v_lshlrev_b32_e32 v2, 3, v1
	v_writelane_b32 v253, s1, 46
	s_add_i32 s1, s0, 0
	v_and_b32_e32 v18, 31, v1
	v_bfe_u32 v20, v1, 3, 3
	v_and_b32_e32 v8, 56, v2
	s_lshl_b32 s96, s83, 3
	s_lshl_b32 s76, s83, 9
	v_bfe_u32 v6, v1, 5, 1
	v_lshl_add_u32 v25, v18, 2, s1
	s_movk_i32 s0, 0x84
	v_mul_u32_u24_e32 v2, 0x84, v8
	v_lshlrev_b32_e32 v3, 2, v20
	s_cmp_gt_i32 s80, 0x2f3ff
	v_mad_u32_u24 v19, v6, s0, v25
	v_mov_b32_e32 v11, 0
	v_add3_u32 v21, s1, v2, v3
	v_or_b32_e32 v22, 8, v20
	v_or_b32_e32 v23, 16, v20
	v_or_b32_e32 v24, 24, v20
	s_cbranch_scc1 .Lco3_hop_192
	v_and_b32_e32 v249, 63, v0
	v_lshrrev_b32_e32 v250, 6, v0
	v_readlane_b32 s15, v253, 2
	s_lshr_b32 s22, s15, 3
	s_and_b32 s23, s15, 7
	v_lshrrev_b32_e32 v246, 5, v249
	v_lshl_add_u32 v247, v250, 4, v246
	v_and_b32_e32 v248, 31, v249
	v_xor_b32_e32 v248, v248, v250
	v_lshlrev_b32_e32 v248, 4, v248
	v_lshl_add_u32 v209, v247, 9, v248
	v_add_u32_e32 v210, 0x10000, v209
	v_lshlrev_b32_e32 v96, 2, v247
	v_and_b32_e32 v248, 31, v249
	v_lshlrev_b32_e32 v248, 4, v248
	s_mov_b32 s20, 0x10000
	v_mad_u32_u24 v74, v247, s20, v248
	s_mov_b32 s20, 0x4000
	v_mad_u32_u24 v75, v247, s20, v248
	s_mov_b32 s20, 0xb140
	v_mad_u32_u24 v76, v247, s20, v248
	v_and_b32_e32 v246, 7, v249
	v_lshrrev_b32_e32 v247, 5, v249
	v_lshl_add_u32 v247, v250, 2, v247
	v_xor_b32_e32 v247, v247, v246
	v_lshlrev_b32_e32 v247, 4, v247
	v_lshl_add_u32 v247, v246, 13, v247
	v_bfe_u32 v248, v249, 3, 2
	v_lshl_add_u32 v211, v248, 2, v247
	v_add_u32_e32 v212, 0x10000, v211
	v_and_b32_e32 v246, 7, v249
	v_lshrrev_b32_e32 v247, 5, v249
	v_lshl_add_u32 v247, v250, 2, v247
	v_add_u32_e32 v247, 2, v247
	v_xor_b32_e32 v247, v247, v246
	v_lshlrev_b32_e32 v247, 4, v247
	v_lshl_add_u32 v247, v246, 13, v247
	v_bfe_u32 v248, v249, 3, 2
	v_lshl_add_u32 v213, v248, 2, v247
	v_add_u32_e32 v214, 0x10000, v213
	v_and_b32_e32 v246, 15, v249
	v_lshrrev_b32_e32 v247, 1, v246
	v_lshlrev_b32_e32 v248, 2, v250
	v_xor_b32_e32 v248, v248, v247
	v_lshlrev_b32_e32 v248, 4, v248
	v_lshl_add_u32 v248, v246, 12, v248
	v_lshrrev_b32_e32 v247, 4, v249
	v_lshl_add_u32 v112, v247, 2, v248
	v_add_u32_e32 v113, 0x10000, v112
	v_and_b32_e32 v246, 15, v249
	v_lshrrev_b32_e32 v247, 1, v246
	v_lshlrev_b32_e32 v248, 2, v250
	v_add_u32_e32 v248, 1, v248
	v_xor_b32_e32 v248, v248, v247
	v_lshlrev_b32_e32 v248, 4, v248
	v_lshl_add_u32 v248, v246, 12, v248
	v_lshrrev_b32_e32 v247, 4, v249
	v_lshl_add_u32 v114, v247, 2, v248
	v_add_u32_e32 v115, 0x10000, v114
	v_and_b32_e32 v246, 15, v249
	v_lshrrev_b32_e32 v247, 1, v246
	v_lshlrev_b32_e32 v248, 2, v250
	v_add_u32_e32 v248, 2, v248
	v_xor_b32_e32 v248, v248, v247
	v_lshlrev_b32_e32 v248, 4, v248
	v_lshl_add_u32 v248, v246, 12, v248
	v_lshrrev_b32_e32 v247, 4, v249
	v_lshl_add_u32 v116, v247, 2, v248
	v_add_u32_e32 v117, 0x10000, v116
	v_and_b32_e32 v246, 15, v249
	v_lshrrev_b32_e32 v247, 1, v246
	v_lshlrev_b32_e32 v248, 2, v250
	v_add_u32_e32 v248, 3, v248
	v_xor_b32_e32 v248, v248, v247
	v_lshlrev_b32_e32 v248, 4, v248
	v_lshl_add_u32 v248, v246, 12, v248
	v_lshrrev_b32_e32 v247, 4, v249
	v_lshl_add_u32 v118, v247, 2, v248
	v_add_u32_e32 v119, 0x10000, v118
	v_lshrrev_b32_e32 v246, 3, v249
	v_lshl_add_u32 v246, v250, 4, v246
	v_and_b32_e32 v247, 7, v249
	v_lshlrev_b32_e32 v247, 4, v247
	v_lshl_add_u32 v77, v246, 12, v247
	v_lshl_add_u32 v79, v246, 14, v247
	v_and_b32_e32 v248, 63, v246
	v_lshlrev_b32_e32 v248, 1, v248
	v_lshrrev_b32_e32 v246, 6, v246
	v_or_b32_e32 v248, v248, v246
	v_lshl_add_u32 v81, v248, 12, v247
	v_lshrrev_b32_e32 v246, 3, v249
	v_lshl_add_u32 v246, v250, 4, v246
	v_add_u32_e32 v246, 8, v246
	v_and_b32_e32 v247, 7, v249
	v_lshlrev_b32_e32 v247, 4, v247
	v_lshl_add_u32 v78, v246, 12, v247
	v_lshl_add_u32 v80, v246, 14, v247
	v_and_b32_e32 v248, 63, v246
	v_lshlrev_b32_e32 v248, 1, v248
	v_lshrrev_b32_e32 v246, 6, v246
	v_or_b32_e32 v248, v248, v246
	v_lshl_add_u32 v82, v248, 12, v247
	v_lshrrev_b32_e32 v246, 4, v249
	v_lshl_add_u32 v246, v250, 4, v246
	v_and_b32_e32 v247, 15, v249
	v_lshlrev_b32_e32 v247, 4, v247
	v_lshl_add_u32 v83, v246, 13, v247
	v_and_b32_e32 v248, 63, v246
	v_lshlrev_b32_e32 v248, 1, v248
	v_lshrrev_b32_e32 v246, 6, v246
	v_or_b32_e32 v248, v248, v246
	v_lshl_add_u32 v87, v248, 13, v247
	v_lshrrev_b32_e32 v246, 4, v249
	v_lshl_add_u32 v246, v250, 4, v246
	v_add_u32_e32 v246, 4, v246
	v_and_b32_e32 v247, 15, v249
	v_lshlrev_b32_e32 v247, 4, v247
	v_lshl_add_u32 v84, v246, 13, v247
	v_and_b32_e32 v248, 63, v246
	v_lshlrev_b32_e32 v248, 1, v248
	v_lshrrev_b32_e32 v246, 6, v246
	v_or_b32_e32 v248, v248, v246
	v_lshl_add_u32 v88, v248, 13, v247
	v_lshrrev_b32_e32 v246, 4, v249
	v_lshl_add_u32 v246, v250, 4, v246
	v_add_u32_e32 v246, 8, v246
	v_and_b32_e32 v247, 15, v249
	v_lshlrev_b32_e32 v247, 4, v247
	v_lshl_add_u32 v85, v246, 13, v247
	v_and_b32_e32 v248, 63, v246
	v_lshlrev_b32_e32 v248, 1, v248
	v_lshrrev_b32_e32 v246, 6, v246
	v_or_b32_e32 v248, v248, v246
	v_lshl_add_u32 v89, v248, 13, v247
	v_lshrrev_b32_e32 v246, 4, v249
	v_lshl_add_u32 v246, v250, 4, v246
	v_add_u32_e32 v246, 12, v246
	v_and_b32_e32 v247, 15, v249
	v_lshlrev_b32_e32 v247, 4, v247
	v_lshl_add_u32 v86, v246, 13, v247
	v_and_b32_e32 v248, 63, v246
	v_lshlrev_b32_e32 v248, 1, v248
	v_lshrrev_b32_e32 v246, 6, v246
	v_or_b32_e32 v248, v248, v246
	v_lshl_add_u32 v90, v248, 13, v247
	v_mov_b32_e32 v95, 0x43e00000
	s_mov_b32 s62, 0xc3e00000
	s_mov_b32 s63, 0x7fff
	s_mov_b32 s64, 0x07060302
	v_readlane_b32 s10, v253, 5
;     ...
;     for (int i = 0; i < 32; ++i) v[i] = sc >= 0 ? W[(size_t)(k0 + 2 * i + (lane >> 5)) * Nsrc + sc] : 0.f;
; #pragma unroll
;     for (int i = 0; i < 32; ++i) { const int k = k0 + 2 * i + (lane >> 5); float x = v[i] * wscale; if (KS) x *= (k < ksplit ? ksA[k] : ksB[k - ksplit]); scr[(2 * i + (lane >> 5)) * 33 + (lane & 31)] = x; }
; __global__ void __launch_bounds__(NWAVES * 64, 2) hybrid_fwd(Args args) {
;     ...
;         for (int rep = 0; rep < REP_PRO; ++rep)
;         for (int it = gw; it < DEPTH * I_L; it += NGW) {
;             const int l = it / I_L; int r = it % I_L;
;             if (r < I_IN) { if (l >= PROJ_F8_FROM) p0_transpose_item_f8<true, 1>(args.in[2] + (size_t)l * DM * NSRC, DM, NSRC, NPROJ / 32, (unsigned char*)(ws + WS_WIN + l * SZ_WIN), WUP8_SCALE, args.in[1] + l * DM, args.in[1] + l * DM, DM, scr, r, lane);
;                 else p0_transpose_item<1, true>(args.in[2] + (size_t)l * DM * NSRC, DM, NSRC, NPROJ / 32, (bf16*)(ws + WS_WIN + l * SZ_WIN), args.in[1] + l * DM, args.in[1] + l * DM, DM, scr, r, lane); continue; } r -= I_IN;
;             if (r < I_O) { if (l >= WO_F8_FROM) p0_transpose_item_f8<true>(args.in[13] + (size_t)l * DM * DM, DM, DM, DM / 32, (unsigned char*)(ws + WS_WO + l * SZ_WO), 64.f, args.in[6] + l * 2048, args.in[12] + l * 2048, 2048, scr, r, lane);
;                 else p0_transpose_item<0, true>(args.in[13] + (size_t)l * DM * DM, DM, DM, DM / 32, (bf16*)(ws + WS_WO + l * SZ_WO), args.in[6] + l * 2048, args.in[12] + l * 2048, 2048, scr, r, lane); continue; } r -= I_O;
;             if (r < I_UP) { p0_transpose_item_f8<true>(args.in[15] + (size_t)l * DM * FF, DM, FF, FF / 32, (unsigned char*)(ws + WS_WUP + l * SZ_WUP), WUP8_SCALE, args.in[14] + l * DM, args.in[14] + l * DM, DM, scr, r, lane); continue; } r -= I_UP;
;             p0_transpose_item_f8<false>(args.in[16] + (size_t)l * FF * DM, FF, DM, DM / 32, (unsigned char*)(ws + WS_WDN + l * SZ_WDN), 128.f, args.in[16], args.in[16], 0, scr, r, lane);
	v_readlane_b32 s11, v253, 6
	s_lshl_b32 s20, s22, 9
	s_add_u32 s10, s10, s20
	s_addc_u32 s11, s11, 0
	global_load_dword v42, v96, s[10:11] offset:0
	global_load_dword v43, v96, s[10:11] offset:8
	global_load_dword v44, v96, s[10:11] offset:16
	global_load_dword v45, v96, s[10:11] offset:24
	global_load_dword v46, v96, s[10:11] offset:32
	global_load_dword v47, v96, s[10:11] offset:40
	global_load_dword v48, v96, s[10:11] offset:48
	global_load_dword v49, v96, s[10:11] offset:56
	v_readlane_b32 s10, v253, 5
	v_readlane_b32 s11, v253, 6
	s_lshl_b32 s20, s22, 9
	s_add_i32 s20, s20, 0x4000
	s_add_u32 s10, s10, s20
	s_addc_u32 s11, s11, 0
	global_load_dword v50, v96, s[10:11] offset:0
	global_load_dword v51, v96, s[10:11] offset:8
	global_load_dword v52, v96, s[10:11] offset:16
	global_load_dword v53, v96, s[10:11] offset:24
	global_load_dword v54, v96, s[10:11] offset:32
	global_load_dword v55, v96, s[10:11] offset:40
	global_load_dword v56, v96, s[10:11] offset:48
	global_load_dword v57, v96, s[10:11] offset:56
	v_readlane_b32 s10, v253, 15
	v_readlane_b32 s11, v253, 16
	v_readlane_b32 s20, v253, 27
	v_readlane_b32 s21, v253, 28
	s_sub_i32 s26, s22, 16
	s_cmp_lt_u32 s22, 16
	s_cselect_b32 s10, s10, s20
	s_cselect_b32 s11, s11, s21
	s_cselect_b32 s26, s22, s26
	s_lshl_b32 s20, s26, 9
	s_add_u32 s10, s10, s20
	s_addc_u32 s11, s11, 0
	global_load_dword v58, v96, s[10:11] offset:0
	global_load_dword v59, v96, s[10:11] offset:8
	global_load_dword v60, v96, s[10:11] offset:16
	global_load_dword v61, v96, s[10:11] offset:24
	global_load_dword v62, v96, s[10:11] offset:32
	global_load_dword v63, v96, s[10:11] offset:40
	global_load_dword v64, v96, s[10:11] offset:48
	global_load_dword v65, v96, s[10:11] offset:56
	v_readlane_b32 s10, v253, 15
	v_readlane_b32 s11, v253, 16
	v_readlane_b32 s20, v253, 27
	v_readlane_b32 s21, v253, 28
	s_sub_i32 s26, s22, 16
	s_cmp_lt_u32 s22, 16
	s_cselect_b32 s10, s10, s20
	s_cselect_b32 s11, s11, s21
	s_cselect_b32 s26, s22, s26
	s_lshl_b32 s20, s26, 9
	s_add_i32 s20, s20, 0x2000
	s_add_u32 s10, s10, s20
	s_addc_u32 s11, s11, 0
	global_load_dword v66, v96, s[10:11] offset:0
	global_load_dword v67, v96, s[10:11] offset:8
	global_load_dword v68, v96, s[10:11] offset:16
	global_load_dword v69, v96, s[10:11] offset:24
	global_load_dword v70, v96, s[10:11] offset:32
	global_load_dword v71, v96, s[10:11] offset:40
	global_load_dword v72, v96, s[10:11] offset:48
	global_load_dword v73, v96, s[10:11] offset:56
	v_readlane_b32 s10, v253, 31
	v_readlane_b32 s11, v253, 32
	s_lshl_b32 s20, s22, 9
	s_add_u32 s10, s10, s20
	s_addc_u32 s11, s11, 0
	global_load_dword v26, v96, s[10:11] offset:0
	global_load_dword v27, v96, s[10:11] offset:8
	global_load_dword v28, v96, s[10:11] offset:16
	global_load_dword v29, v96, s[10:11] offset:24
	global_load_dword v30, v96, s[10:11] offset:32
	global_load_dword v31, v96, s[10:11] offset:40
	global_load_dword v32, v96, s[10:11] offset:48
	global_load_dword v33, v96, s[10:11] offset:56
	v_readlane_b32 s10, v253, 31
	v_readlane_b32 s11, v253, 32
	s_lshl_b32 s20, s22, 9
	s_add_i32 s20, s20, 0x4000
	s_add_u32 s10, s10, s20
	s_addc_u32 s11, s11, 0
	global_load_dword v34, v96, s[10:11] offset:0
	global_load_dword v35, v96, s[10:11] offset:8
	global_load_dword v36, v96, s[10:11] offset:16
	global_load_dword v37, v96, s[10:11] offset:24
	global_load_dword v38, v96, s[10:11] offset:32
	global_load_dword v39, v96, s[10:11] offset:40
	global_load_dword v40, v96, s[10:11] offset:48
	global_load_dword v41, v96, s[10:11] offset:56
	s_waitcnt vmcnt(0)
	v_mul_f32_e32 v50, 0x42800000, v50
	v_mul_f32_e32 v51, 0x42800000, v51
	v_mul_f32_e32 v52, 0x42800000, v52
	v_mul_f32_e32 v53, 0x42800000, v53
	v_mul_f32_e32 v54, 0x42800000, v54
	v_mul_f32_e32 v55, 0x42800000, v55
	v_mul_f32_e32 v56, 0x42800000, v56
	v_mul_f32_e32 v57, 0x42800000, v57
	v_mul_f32_e32 v66, 0x42800000, v66
	v_mul_f32_e32 v67, 0x42800000, v67
	v_mul_f32_e32 v68, 0x42800000, v68
	v_mul_f32_e32 v69, 0x42800000, v69
	v_mul_f32_e32 v70, 0x42800000, v70
	v_mul_f32_e32 v71, 0x42800000, v71
	v_mul_f32_e32 v72, 0x42800000, v72
	v_mul_f32_e32 v73, 0x42800000, v73
	v_mul_f32_e32 v26, 0x42800000, v26
	v_mul_f32_e32 v27, 0x42800000, v27
	v_mul_f32_e32 v28, 0x42800000, v28
	v_mul_f32_e32 v29, 0x42800000, v29
	v_mul_f32_e32 v30, 0x42800000, v30
	v_mul_f32_e32 v31, 0x42800000, v31
	v_mul_f32_e32 v32, 0x42800000, v32
	v_mul_f32_e32 v33, 0x42800000, v33
	v_mul_f32_e32 v34, 0x42800000, v34
	v_mul_f32_e32 v35, 0x42800000, v35
	v_mul_f32_e32 v36, 0x42800000, v36
	v_mul_f32_e32 v37, 0x42800000, v37
	v_mul_f32_e32 v38, 0x42800000, v38
	v_mul_f32_e32 v39, 0x42800000, v39
	v_mul_f32_e32 v40, 0x42800000, v40
	v_mul_f32_e32 v41, 0x42800000, v41
	v_readlane_b32 s30, v253, 33
	v_readlane_b32 s31, v253, 34
	v_readlane_b32 s32, v253, 41
	v_readlane_b32 s33, v253, 42
	s_mul_i32 s20, s22, 0x800000
	s_lshl_b32 s21, s23, 9
	s_add_u32 s20, s20, s21
	s_add_u32 s30, s30, s20
	s_addc_u32 s31, s31, 0
	s_add_u32 s32, s32, 0xf600000
	s_addc_u32 s33, s33, 0
	s_lshl_b32 s20, s22, 7
	s_mul_i32 s21, s23, 0x80000
	s_add_u32 s20, s20, s21
	s_add_u32 s32, s32, s20
	s_addc_u32 s33, s33, 0
	v_readlane_b32 s34, v253, 33
	v_readlane_b32 s35, v253, 34
	v_readlane_b32 s36, v253, 41
	v_readlane_b32 s37, v253, 42
	s_add_u32 s34, s34, 0x10000000
	s_addc_u32 s35, s35, 0
	s_mul_i32 s20, s22, 0x800000
	s_lshl_b32 s21, s23, 9
	s_add_u32 s20, s20, s21
	s_add_u32 s34, s34, s20
	s_addc_u32 s35, s35, 0
	s_add_u32 s36, s36, 0x17600000
	s_addc_u32 s37, s37, 0
	s_lshl_b32 s20, s22, 7
	s_mul_i32 s21, s23, 0x80000
	s_add_u32 s20, s20, s21
	s_add_u32 s36, s36, s20
	s_addc_u32 s37, s37, 0
	v_readlane_b32 s38, v253, 35
;     const int pr = item >> 1, kb = 2 * (pr / nblk) + (item & 1), nb = pr % nblk, k0 = 64 * kb, n0 = 32 * nb;
;     const int nr = n0 + (lane & 31); const int sc = MAP == 1 ? src_col_in(nr) : nr;
;     float v[32];
; #pragma unroll
;     for (int i = 0; i < 32; ++i) v[i] = sc >= 0 ? W[(size_t)(k0 + 2 * i + (lane >> 5)) * Nsrc + sc] : 0.f;
; #pragma unroll
;     for (int i = 0; i < 32; ++i) { const int k = k0 + 2 * i + (lane >> 5); float x = v[i] * wscale; if (KS) x *= (k < ksplit ? ksA[k] : ksB[k - ksplit]); scr[(2 * i + (lane >> 5)) * 33 + (lane & 31)] = x; }
; __global__ void __launch_bounds__(NWAVES * 64, 2) hybrid_fwd(Args args) {
;     ...
;             if (r < I_UP) { p0_transpose_item_f8<true>(args.in[15] + (size_t)l * DM * FF, DM, FF, FF / 32, (unsigned char*)(ws + WS_WUP + l * SZ_WUP), WUP8_SCALE, args.in[14] + l * DM, args.in[14] + l * DM, DM, scr, r, lane); continue; } r -= I_UP;
;             p0_transpose_item_f8<false>(args.in[16] + (size_t)l * FF * DM, FF, DM, DM / 32, (unsigned char*)(ws + WS_WDN + l * SZ_WDN), 128.f, args.in[16], args.in[16], 0, scr, r, lane);
	v_readlane_b32 s39, v253, 36
	v_readlane_b32 s40, v253, 41
	v_readlane_b32 s41, v253, 42
	s_mul_i32 s20, s22, 0x200000
	s_lshl_b32 s21, s23, 9
	s_add_u32 s20, s20, s21
	s_add_u32 s38, s38, s20
	s_addc_u32 s39, s39, 0
	s_add_u32 s40, s40, 0x1f600000
	s_addc_u32 s41, s41, 0
	s_lshl_b32 s20, s22, 7
	s_mul_i32 s21, s23, 0x200000
	s_add_u32 s20, s20, s21
	s_add_u32 s40, s40, s20
	s_addc_u32 s41, s41, 0
	v_readlane_b32 s42, v253, 35
	v_readlane_b32 s43, v253, 36
	v_readlane_b32 s44, v253, 41
	v_readlane_b32 s45, v253, 42
	s_add_u32 s42, s42, 0x10000000
	s_addc_u32 s43, s43, 0
	s_mul_i32 s20, s22, 0x200000
	s_lshl_b32 s21, s23, 9
	s_add_u32 s20, s20, s21
	s_add_u32 s42, s42, s20
	s_addc_u32 s43, s43, 0
	s_add_u32 s44, s44, 0x27600000
	s_addc_u32 s45, s45, 0
	s_lshl_b32 s20, s22, 7
	s_mul_i32 s21, s23, 0x200000
	s_add_u32 s20, s20, s21
	s_add_u32 s44, s44, s20
	s_addc_u32 s45, s45, 0
	v_readlane_b32 s46, v253, 7
	v_readlane_b32 s47, v253, 8
	v_readlane_b32 s48, v253, 41
	v_readlane_b32 s49, v253, 42
	s_mul_i32 s20, s22, 0x58a000
	s_add_u32 s46, s46, s20
	s_addc_u32 s47, s47, 0
	s_add_u32 s48, s48, 0x200000
	s_addc_u32 s49, s49, 0
	s_lshl_b32 s20, s22, 8
	s_add_u32 s48, s48, s20
	s_addc_u32 s49, s49, 0
	v_readlane_b32 s50, v253, 7
	v_readlane_b32 s51, v253, 8
	v_readlane_b32 s52, v253, 41
	v_readlane_b32 s53, v253, 42
	s_add_u32 s50, s50, 0xb140000
	s_addc_u32 s51, s51, 0
	s_mul_i32 s20, s22, 0x58a000
	s_add_u32 s50, s50, s20
	s_addc_u32 s51, s51, 0
	s_add_u32 s52, s52, 0x5c00000
	s_addc_u32 s53, s53, 0
	s_lshl_b32 s20, s22, 7
	s_add_u32 s52, s52, s20
	s_addc_u32 s53, s53, 0
	v_readlane_b32 s54, v253, 29
	v_readlane_b32 s55, v253, 30
	v_readlane_b32 s56, v253, 41
	v_readlane_b32 s57, v253, 42
	s_mul_i32 s20, s22, 0x200000
	s_lshl_b32 s21, s23, 9
	s_add_u32 s20, s20, s21
	s_add_u32 s54, s54, s20
	s_addc_u32 s55, s55, 0
	s_add_u32 s56, s56, 0xb600000
	s_addc_u32 s57, s57, 0
	s_lshl_b32 s20, s22, 8
	s_mul_i32 s21, s23, 0x100000
	s_add_u32 s20, s20, s21
	s_add_u32 s56, s56, s20
	s_addc_u32 s57, s57, 0
	v_readlane_b32 s58, v253, 29
	v_readlane_b32 s59, v253, 30
	v_readlane_b32 s60, v253, 41
	v_readlane_b32 s61, v253, 42
	s_add_u32 s58, s58, 0x4000000
	s_addc_u32 s59, s59, 0
	s_mul_i32 s20, s22, 0x200000
	s_lshl_b32 s21, s23, 9
	s_add_u32 s20, s20, s21
	s_add_u32 s58, s58, s20
	s_addc_u32 s59, s59, 0
	s_add_u32 s60, s60, 0xd600000
	s_addc_u32 s61, s61, 0
	s_lshl_b32 s20, s22, 7
	s_mul_i32 s21, s23, 0x80000
	s_add_u32 s20, s20, s21
	s_add_u32 s60, s60, s20
	s_addc_u32 s61, s61, 0
	s_mov_b64 s[8:9], s[30:31]
	global_load_dwordx4 v[144:147], v74, s[8:9]
	s_add_u32 s8, s8, 0x20000
	s_addc_u32 s9, s9, 0
	global_load_dwordx4 v[148:151], v74, s[8:9]
	s_add_u32 s8, s8, 0x20000
	s_addc_u32 s9, s9, 0
	global_load_dwordx4 v[152:155], v74, s[8:9]
	s_add_u32 s8, s8, 0x20000
	s_addc_u32 s9, s9, 0
	global_load_dwordx4 v[156:159], v74, s[8:9]
	s_add_u32 s8, s8, 0x20000
	s_addc_u32 s9, s9, 0
	global_load_dwordx4 v[160:163], v74, s[8:9]
	s_add_u32 s8, s8, 0x20000
	s_addc_u32 s9, s9, 0
	global_load_dwordx4 v[164:167], v74, s[8:9]
	s_add_u32 s8, s8, 0x20000
	s_addc_u32 s9, s9, 0
	global_load_dwordx4 v[168:171], v74, s[8:9]
	s_add_u32 s8, s8, 0x20000
	s_addc_u32 s9, s9, 0
	global_load_dwordx4 v[172:175], v74, s[8:9]
	s_add_u32 s8, s30, 0x1000
	s_addc_u32 s9, s31, 0
	global_load_dwordx4 v[176:179], v74, s[8:9]
	s_add_u32 s8, s8, 0x20000
	s_addc_u32 s9, s9, 0
	global_load_dwordx4 v[180:183], v74, s[8:9]
	s_add_u32 s8, s8, 0x20000
	s_addc_u32 s9, s9, 0
	global_load_dwordx4 v[184:187], v74, s[8:9]
	s_add_u32 s8, s8, 0x20000
	s_addc_u32 s9, s9, 0
	global_load_dwordx4 v[188:191], v74, s[8:9]
	s_add_u32 s8, s8, 0x20000
	s_addc_u32 s9, s9, 0
	global_load_dwordx4 v[192:195], v74, s[8:9]
	s_add_u32 s8, s8, 0x20000
	s_addc_u32 s9, s9, 0
	global_load_dwordx4 v[196:199], v74, s[8:9]
	s_add_u32 s8, s8, 0x20000
	s_addc_u32 s9, s9, 0
	global_load_dwordx4 v[200:203], v74, s[8:9]
	s_add_u32 s8, s8, 0x20000
	s_addc_u32 s9, s9, 0
	global_load_dwordx4 v[204:207], v74, s[8:9]
	s_waitcnt vmcnt(8)
	v_mul_f32_e32 v144, v26, v144
	v_mul_f32_e32 v145, v26, v145
	v_mul_f32_e32 v146, v26, v146
	v_mul_f32_e32 v147, v26, v147
	ds_write_b128 v209, v[144:147]
	v_mul_f32_e32 v148, v27, v148
	v_mul_f32_e32 v149, v27, v149
	v_mul_f32_e32 v150, v27, v150
	v_mul_f32_e32 v151, v27, v151
	ds_write_b128 v209, v[148:151] offset:1024
	v_mul_f32_e32 v152, v28, v152
	v_mul_f32_e32 v153, v28, v153
	v_mul_f32_e32 v154, v28, v154
	v_mul_f32_e32 v155, v28, v155
	ds_write_b128 v209, v[152:155] offset:2048
	v_mul_f32_e32 v156, v29, v156
	v_mul_f32_e32 v157, v29, v157
	v_mul_f32_e32 v158, v29, v158
	v_mul_f32_e32 v159, v29, v159
	ds_write_b128 v209, v[156:159] offset:3072
	v_mul_f32_e32 v160, v30, v160
	v_mul_f32_e32 v161, v30, v161
	v_mul_f32_e32 v162, v30, v162
	v_mul_f32_e32 v163, v30, v163
	ds_write_b128 v209, v[160:163] offset:4096
	v_mul_f32_e32 v164, v31, v164
	v_mul_f32_e32 v165, v31, v165
	v_mul_f32_e32 v166, v31, v166
	v_mul_f32_e32 v167, v31, v167
	ds_write_b128 v209, v[164:167] offset:5120
	v_mul_f32_e32 v168, v32, v168
	v_mul_f32_e32 v169, v32, v169
	v_mul_f32_e32 v170, v32, v170
	v_mul_f32_e32 v171, v32, v171
	ds_write_b128 v209, v[168:171] offset:6144
	v_mul_f32_e32 v172, v33, v172
	v_mul_f32_e32 v173, v33, v173
	v_mul_f32_e32 v174, v33, v174
	v_mul_f32_e32 v175, v33, v175
	ds_write_b128 v209, v[172:175] offset:7168
	s_waitcnt lgkmcnt(0)
	s_barrier
; #define GAS __attribute__((address_space(1)))
; #define LAS __attribute__((address_space(3)))
; #define LDS_WAIT() asm volatile("s_waitcnt lgkmcnt(0)" ::: "memory")
;     const int pr = item >> 1, kb = 2 * (pr / nblk) + (item & 1), nb = pr % nblk, k0 = 64 * kb, n0 = 32 * nb;
;     const int nr = n0 + (lane & 31); const int sc = MAP == 1 ? src_col_in(nr) : nr;
;     float v[32];
; #pragma unroll
;     for (int i = 0; i < 32; ++i) v[i] = sc >= 0 ? W[(size_t)(k0 + 2 * i + (lane >> 5)) * Nsrc + sc] : 0.f;
; #pragma unroll
;     for (int i = 0; i < 32; ++i) { const int k = k0 + 2 * i + (lane >> 5); float x = v[i] * wscale; if (KS) x *= (k < ksplit ? ksA[k] : ksB[k - ksplit]); scr[(2 * i + (lane >> 5)) * 33 + (lane & 31)] = x; }
;     LDS_WAIT(); asm volatile("" ::: "memory");
;     const int c = lane & 7;
; #pragma unroll
;     for (int j = 0; j < 4; ++j) { const int n = (lane >> 3) + 8 * j; const LAS float* s = scr + (8 * c) * 33 + n;
;         const unsigned long long o = (unsigned long long)pg8::pk4_fp8(s[0 * 33], s[1 * 33], s[2 * 33], s[3 * 33]) | ((unsigned long long)pg8::pk4_fp8(s[4 * 33], s[5 * 33], s[6 * 33], s[7 * 33]) << 32);
;         *(GAS unsigned long long*)(WT + (size_t)(n0 + n) * K + k0 + 8 * c) = o; }
	s_add_u32 s8, s30, 0x2000
	s_addc_u32 s9, s31, 0
	global_load_dwordx4 v[144:147], v74, s[8:9]
	s_add_u32 s8, s8, 0x20000
	s_addc_u32 s9, s9, 0
	global_load_dwordx4 v[148:151], v74, s[8:9]
	s_add_u32 s8, s8, 0x20000
	s_addc_u32 s9, s9, 0
	global_load_dwordx4 v[152:155], v74, s[8:9]
	s_add_u32 s8, s8, 0x20000
	s_addc_u32 s9, s9, 0
	global_load_dwordx4 v[156:159], v74, s[8:9]
	s_add_u32 s8, s8, 0x20000
	s_addc_u32 s9, s9, 0
	global_load_dwordx4 v[160:163], v74, s[8:9]
	s_add_u32 s8, s8, 0x20000
	s_addc_u32 s9, s9, 0
	global_load_dwordx4 v[164:167], v74, s[8:9]
	s_add_u32 s8, s8, 0x20000
	s_addc_u32 s9, s9, 0
	global_load_dwordx4 v[168:171], v74, s[8:9]
	s_add_u32 s8, s8, 0x20000
	s_addc_u32 s9, s9, 0
	global_load_dwordx4 v[172:175], v74, s[8:9]
	s_mov_b64 s[6:7], s[32:33]
	ds_read_b32 v226, v211
	ds_read_b32 v227, v211 offset:512
	ds_read_b32 v228, v211 offset:1024
	ds_read_b32 v229, v211 offset:1536
	ds_read_b32 v230, v211 offset:2048
	ds_read_b32 v231, v211 offset:2560
	ds_read_b32 v232, v211 offset:3072
	ds_read_b32 v233, v211 offset:3584
	ds_read_b32 v234, v211 offset:4096
	ds_read_b32 v235, v211 offset:4608
	ds_read_b32 v236, v211 offset:5120
	ds_read_b32 v237, v211 offset:5632
	ds_read_b32 v238, v211 offset:6144
	ds_read_b32 v239, v211 offset:6656
	ds_read_b32 v240, v211 offset:7168
	ds_read_b32 v241, v211 offset:7680
	s_waitcnt lgkmcnt(0)
	v_max_f32_e32 v226, v226, v226
	v_max_f32_e32 v227, v227, v227
	v_max_f32_e32 v228, v228, v228
	v_max_f32_e32 v229, v229, v229
	v_max_f32_e32 v230, v230, v230
	v_max_f32_e32 v231, v231, v231
	v_max_f32_e32 v232, v232, v232
	v_max_f32_e32 v233, v233, v233
	v_max_f32_e32 v234, v234, v234
	v_max_f32_e32 v235, v235, v235
	v_max_f32_e32 v236, v236, v236
	v_max_f32_e32 v237, v237, v237
	v_max_f32_e32 v238, v238, v238
	v_max_f32_e32 v239, v239, v239
	v_max_f32_e32 v240, v240, v240
	v_max_f32_e32 v241, v241, v241
	v_med3_f32 v226, v226, s62, v95
	v_med3_f32 v227, v227, s62, v95
	v_med3_f32 v228, v228, s62, v95
	v_med3_f32 v229, v229, s62, v95
	v_med3_f32 v230, v230, s62, v95
	v_med3_f32 v231, v231, s62, v95
	v_med3_f32 v232, v232, s62, v95
	v_med3_f32 v233, v233, s62, v95
	v_med3_f32 v234, v234, s62, v95
	v_med3_f32 v235, v235, s62, v95
	v_med3_f32 v236, v236, s62, v95
	v_med3_f32 v237, v237, s62, v95
	v_med3_f32 v238, v238, s62, v95
	v_med3_f32 v239, v239, s62, v95
	v_med3_f32 v240, v240, s62, v95
	v_med3_f32 v241, v241, s62, v95
	v_mov_b32_e32 v242, 0
	v_mov_b32_e32 v243, 0
	v_mov_b32_e32 v244, 0
	v_mov_b32_e32 v245, 0
	v_cvt_pk_fp8_f32 v242, v226, v227
	v_cvt_pk_fp8_f32 v243, v230, v231
	v_cvt_pk_fp8_f32 v244, v234, v235
	v_cvt_pk_fp8_f32 v245, v238, v239
	v_cvt_pk_fp8_f32 v242, v228, v229 op_sel:[0,0,1]
	v_cvt_pk_fp8_f32 v243, v232, v233 op_sel:[0,0,1]
	v_cvt_pk_fp8_f32 v244, v236, v237 op_sel:[0,0,1]
	v_cvt_pk_fp8_f32 v245, v240, v241 op_sel:[0,0,1]
	s_nop 0
	global_store_dwordx4 v77, v[242:245], s[6:7]
	ds_read_b32 v226, v213
	ds_read_b32 v227, v213 offset:512
	ds_read_b32 v228, v213 offset:1024
	ds_read_b32 v229, v213 offset:1536
	ds_read_b32 v230, v213 offset:2048
	ds_read_b32 v231, v213 offset:2560
	ds_read_b32 v232, v213 offset:3072
	ds_read_b32 v233, v213 offset:3584
	ds_read_b32 v234, v213 offset:4096
	ds_read_b32 v235, v213 offset:4608
	ds_read_b32 v236, v213 offset:5120
	ds_read_b32 v237, v213 offset:5632
	ds_read_b32 v238, v213 offset:6144
	ds_read_b32 v239, v213 offset:6656
	ds_read_b32 v240, v213 offset:7168
	ds_read_b32 v241, v213 offset:7680
	s_waitcnt lgkmcnt(0)
	v_max_f32_e32 v226, v226, v226
	v_max_f32_e32 v227, v227, v227
	v_max_f32_e32 v228, v228, v228
	v_max_f32_e32 v229, v229, v229
	v_max_f32_e32 v230, v230, v230
	v_max_f32_e32 v231, v231, v231
	v_max_f32_e32 v232, v232, v232
	v_max_f32_e32 v233, v233, v233
	v_max_f32_e32 v234, v234, v234
	v_max_f32_e32 v235, v235, v235
	v_max_f32_e32 v236, v236, v236
	v_max_f32_e32 v237, v237, v237
	v_max_f32_e32 v238, v238, v238
	v_max_f32_e32 v239, v239, v239
	v_max_f32_e32 v240, v240, v240
	v_max_f32_e32 v241, v241, v241
	v_med3_f32 v226, v226, s62, v95
	v_med3_f32 v227, v227, s62, v95
	v_med3_f32 v228, v228, s62, v95
	v_med3_f32 v229, v229, s62, v95
	v_med3_f32 v230, v230, s62, v95
	v_med3_f32 v231, v231, s62, v95
	v_med3_f32 v232, v232, s62, v95
	v_med3_f32 v233, v233, s62, v95
	v_med3_f32 v234, v234, s62, v95
	v_med3_f32 v235, v235, s62, v95
	v_med3_f32 v236, v236, s62, v95
	v_med3_f32 v237, v237, s62, v95
	v_med3_f32 v238, v238, s62, v95
	v_med3_f32 v239, v239, s62, v95
	v_med3_f32 v240, v240, s62, v95
	v_med3_f32 v241, v241, s62, v95
	v_mov_b32_e32 v242, 0
	v_mov_b32_e32 v243, 0
	v_mov_b32_e32 v244, 0
	v_mov_b32_e32 v245, 0
	v_cvt_pk_fp8_f32 v242, v226, v227
	v_cvt_pk_fp8_f32 v243, v230, v231
	v_cvt_pk_fp8_f32 v244, v234, v235
	v_cvt_pk_fp8_f32 v245, v238, v239
	v_cvt_pk_fp8_f32 v242, v228, v229 op_sel:[0,0,1]
	v_cvt_pk_fp8_f32 v243, v232, v233 op_sel:[0,0,1]
	v_cvt_pk_fp8_f32 v244, v236, v237 op_sel:[0,0,1]
	v_cvt_pk_fp8_f32 v245, v240, v241 op_sel:[0,0,1]
	s_nop 0
	global_store_dwordx4 v78, v[242:245], s[6:7]
	s_waitcnt vmcnt(10)
	v_mul_f32_e32 v176, v26, v176
	v_mul_f32_e32 v177, v26, v177
	v_mul_f32_e32 v178, v26, v178
	v_mul_f32_e32 v179, v26, v179
	ds_write_b128 v210, v[176:179]
	v_mul_f32_e32 v180, v27, v180
	v_mul_f32_e32 v181, v27, v181
	v_mul_f32_e32 v182, v27, v182
	v_mul_f32_e32 v183, v27, v183
	ds_write_b128 v210, v[180:183] offset:1024
	v_mul_f32_e32 v184, v28, v184
	v_mul_f32_e32 v185, v28, v185
	v_mul_f32_e32 v186, v28, v186
	v_mul_f32_e32 v187, v28, v187
	ds_write_b128 v210, v[184:187] offset:2048
	v_mul_f32_e32 v188, v29, v188
	v_mul_f32_e32 v189, v29, v189
	v_mul_f32_e32 v190, v29, v190
	v_mul_f32_e32 v191, v29, v191
	ds_write_b128 v210, v[188:191] offset:3072
	v_mul_f32_e32 v192, v30, v192
	v_mul_f32_e32 v193, v30, v193
	v_mul_f32_e32 v194, v30, v194
	v_mul_f32_e32 v195, v30, v195
	ds_write_b128 v210, v[192:195] offset:4096
	v_mul_f32_e32 v196, v31, v196
	v_mul_f32_e32 v197, v31, v197
	v_mul_f32_e32 v198, v31, v198
	v_mul_f32_e32 v199, v31, v199
	ds_write_b128 v210, v[196:199] offset:5120
	v_mul_f32_e32 v200, v32, v200
	v_mul_f32_e32 v201, v32, v201
	v_mul_f32_e32 v202, v32, v202
	v_mul_f32_e32 v203, v32, v203
	ds_write_b128 v210, v[200:203] offset:6144
	v_mul_f32_e32 v204, v33, v204
	v_mul_f32_e32 v205, v33, v205
	v_mul_f32_e32 v206, v33, v206
	v_mul_f32_e32 v207, v33, v207
	ds_write_b128 v210, v[204:207] offset:7168
	s_waitcnt lgkmcnt(0)
	s_barrier
; #define GAS __attribute__((address_space(1)))
; #define LAS __attribute__((address_space(3)))
; #define LDS_WAIT() asm volatile("s_waitcnt lgkmcnt(0)" ::: "memory")
;     const int pr = item >> 1, kb = 2 * (pr / nblk) + (item & 1), nb = pr % nblk, k0 = 64 * kb, n0 = 32 * nb;
;     const int nr = n0 + (lane & 31); const int sc = MAP == 1 ? src_col_in(nr) : nr;
;     float v[32];
; #pragma unroll
;     for (int i = 0; i < 32; ++i) v[i] = sc >= 0 ? W[(size_t)(k0 + 2 * i + (lane >> 5)) * Nsrc + sc] : 0.f;
; #pragma unroll
;     for (int i = 0; i < 32; ++i) { const int k = k0 + 2 * i + (lane >> 5); float x = v[i] * wscale; if (KS) x *= (k < ksplit ? ksA[k] : ksB[k - ksplit]); scr[(2 * i + (lane >> 5)) * 33 + (lane & 31)] = x; }
;     LDS_WAIT(); asm volatile("" ::: "memory");
;     const int c = lane & 7;
; #pragma unroll
;     for (int j = 0; j < 4; ++j) { const int n = (lane >> 3) + 8 * j; const LAS float* s = scr + (8 * c) * 33 + n;
;         const unsigned long long o = (unsigned long long)pg8::pk4_fp8(s[0 * 33], s[1 * 33], s[2 * 33], s[3 * 33]) | ((unsigned long long)pg8::pk4_fp8(s[4 * 33], s[5 * 33], s[6 * 33], s[7 * 33]) << 32);
;         *(GAS unsigned long long*)(WT + (size_t)(n0 + n) * K + k0 + 8 * c) = o; }
	s_add_u32 s8, s30, 0x3000
	s_addc_u32 s9, s31, 0
	global_load_dwordx4 v[176:179], v74, s[8:9]
	s_add_u32 s8, s8, 0x20000
	s_addc_u32 s9, s9, 0
	global_load_dwordx4 v[180:183], v74, s[8:9]
	s_add_u32 s8, s8, 0x20000
	s_addc_u32 s9, s9, 0
	global_load_dwordx4 v[184:187], v74, s[8:9]
	s_add_u32 s8, s8, 0x20000
	s_addc_u32 s9, s9, 0
	global_load_dwordx4 v[188:191], v74, s[8:9]
	s_add_u32 s8, s8, 0x20000
	s_addc_u32 s9, s9, 0
	global_load_dwordx4 v[192:195], v74, s[8:9]
	s_add_u32 s8, s8, 0x20000
	s_addc_u32 s9, s9, 0
	global_load_dwordx4 v[196:199], v74, s[8:9]
	s_add_u32 s8, s8, 0x20000
	s_addc_u32 s9, s9, 0
	global_load_dwordx4 v[200:203], v74, s[8:9]
	s_add_u32 s8, s8, 0x20000
	s_addc_u32 s9, s9, 0
	global_load_dwordx4 v[204:207], v74, s[8:9]
	s_add_u32 s6, s32, 0x400000
	s_addc_u32 s7, s33, 0
	ds_read_b32 v226, v212
	ds_read_b32 v227, v212 offset:512
	ds_read_b32 v228, v212 offset:1024
	ds_read_b32 v229, v212 offset:1536
	ds_read_b32 v230, v212 offset:2048
	ds_read_b32 v231, v212 offset:2560
	ds_read_b32 v232, v212 offset:3072
	ds_read_b32 v233, v212 offset:3584
	ds_read_b32 v234, v212 offset:4096
	ds_read_b32 v235, v212 offset:4608
	ds_read_b32 v236, v212 offset:5120
	ds_read_b32 v237, v212 offset:5632
	ds_read_b32 v238, v212 offset:6144
	ds_read_b32 v239, v212 offset:6656
	ds_read_b32 v240, v212 offset:7168
	ds_read_b32 v241, v212 offset:7680
	s_waitcnt lgkmcnt(0)
	v_max_f32_e32 v226, v226, v226
	v_max_f32_e32 v227, v227, v227
	v_max_f32_e32 v228, v228, v228
	v_max_f32_e32 v229, v229, v229
	v_max_f32_e32 v230, v230, v230
	v_max_f32_e32 v231, v231, v231
	v_max_f32_e32 v232, v232, v232
	v_max_f32_e32 v233, v233, v233
	v_max_f32_e32 v234, v234, v234
	v_max_f32_e32 v235, v235, v235
	v_max_f32_e32 v236, v236, v236
	v_max_f32_e32 v237, v237, v237
	v_max_f32_e32 v238, v238, v238
	v_max_f32_e32 v239, v239, v239
	v_max_f32_e32 v240, v240, v240
	v_max_f32_e32 v241, v241, v241
	v_med3_f32 v226, v226, s62, v95
	v_med3_f32 v227, v227, s62, v95
	v_med3_f32 v228, v228, s62, v95
	v_med3_f32 v229, v229, s62, v95
	v_med3_f32 v230, v230, s62, v95
	v_med3_f32 v231, v231, s62, v95
	v_med3_f32 v232, v232, s62, v95
	v_med3_f32 v233, v233, s62, v95
	v_med3_f32 v234, v234, s62, v95
	v_med3_f32 v235, v235, s62, v95
	v_med3_f32 v236, v236, s62, v95
	v_med3_f32 v237, v237, s62, v95
	v_med3_f32 v238, v238, s62, v95
	v_med3_f32 v239, v239, s62, v95
	v_med3_f32 v240, v240, s62, v95
	v_med3_f32 v241, v241, s62, v95
	v_mov_b32_e32 v242, 0
	v_mov_b32_e32 v243, 0
	v_mov_b32_e32 v244, 0
	v_mov_b32_e32 v245, 0
	v_cvt_pk_fp8_f32 v242, v226, v227
	v_cvt_pk_fp8_f32 v243, v230, v231
	v_cvt_pk_fp8_f32 v244, v234, v235
	v_cvt_pk_fp8_f32 v245, v238, v239
	v_cvt_pk_fp8_f32 v242, v228, v229 op_sel:[0,0,1]
	v_cvt_pk_fp8_f32 v243, v232, v233 op_sel:[0,0,1]
	v_cvt_pk_fp8_f32 v244, v236, v237 op_sel:[0,0,1]
	v_cvt_pk_fp8_f32 v245, v240, v241 op_sel:[0,0,1]
	s_nop 0
	global_store_dwordx4 v77, v[242:245], s[6:7]
	ds_read_b32 v226, v214
	ds_read_b32 v227, v214 offset:512
	ds_read_b32 v228, v214 offset:1024
	ds_read_b32 v229, v214 offset:1536
	ds_read_b32 v230, v214 offset:2048
	ds_read_b32 v231, v214 offset:2560
	ds_read_b32 v232, v214 offset:3072
	ds_read_b32 v233, v214 offset:3584
	ds_read_b32 v234, v214 offset:4096
	ds_read_b32 v235, v214 offset:4608
	ds_read_b32 v236, v214 offset:5120
	ds_read_b32 v237, v214 offset:5632
	ds_read_b32 v238, v214 offset:6144
	ds_read_b32 v239, v214 offset:6656
	ds_read_b32 v240, v214 offset:7168
	ds_read_b32 v241, v214 offset:7680
	s_waitcnt lgkmcnt(0)
	v_max_f32_e32 v226, v226, v226
	v_max_f32_e32 v227, v227, v227
	v_max_f32_e32 v228, v228, v228
	v_max_f32_e32 v229, v229, v229
	v_max_f32_e32 v230, v230, v230
	v_max_f32_e32 v231, v231, v231
	v_max_f32_e32 v232, v232, v232
	v_max_f32_e32 v233, v233, v233
	v_max_f32_e32 v234, v234, v234
	v_max_f32_e32 v235, v235, v235
	v_max_f32_e32 v236, v236, v236
	v_max_f32_e32 v237, v237, v237
	v_max_f32_e32 v238, v238, v238
	v_max_f32_e32 v239, v239, v239
	v_max_f32_e32 v240, v240, v240
	v_max_f32_e32 v241, v241, v241
	v_med3_f32 v226, v226, s62, v95
	v_med3_f32 v227, v227, s62, v95
	v_med3_f32 v228, v228, s62, v95
	v_med3_f32 v229, v229, s62, v95
	v_med3_f32 v230, v230, s62, v95
	v_med3_f32 v231, v231, s62, v95
	v_med3_f32 v232, v232, s62, v95
	v_med3_f32 v233, v233, s62, v95
	v_med3_f32 v234, v234, s62, v95
	v_med3_f32 v235, v235, s62, v95
	v_med3_f32 v236, v236, s62, v95
	v_med3_f32 v237, v237, s62, v95
	v_med3_f32 v238, v238, s62, v95
	v_med3_f32 v239, v239, s62, v95
	v_med3_f32 v240, v240, s62, v95
	v_med3_f32 v241, v241, s62, v95
	v_mov_b32_e32 v242, 0
	v_mov_b32_e32 v243, 0
	v_mov_b32_e32 v244, 0
	v_mov_b32_e32 v245, 0
	v_cvt_pk_fp8_f32 v242, v226, v227
	v_cvt_pk_fp8_f32 v243, v230, v231
	v_cvt_pk_fp8_f32 v244, v234, v235
	v_cvt_pk_fp8_f32 v245, v238, v239
	v_cvt_pk_fp8_f32 v242, v228, v229 op_sel:[0,0,1]
	v_cvt_pk_fp8_f32 v243, v232, v233 op_sel:[0,0,1]
	v_cvt_pk_fp8_f32 v244, v236, v237 op_sel:[0,0,1]
	v_cvt_pk_fp8_f32 v245, v240, v241 op_sel:[0,0,1]
	s_nop 0
	global_store_dwordx4 v78, v[242:245], s[6:7]
	s_waitcnt vmcnt(12)
	v_mul_f32_e32 v144, v26, v144
	v_mul_f32_e32 v145, v26, v145
	v_mul_f32_e32 v146, v26, v146
	v_mul_f32_e32 v147, v26, v147
	ds_write_b128 v209, v[144:147]
	v_mul_f32_e32 v148, v27, v148
	v_mul_f32_e32 v149, v27, v149
	v_mul_f32_e32 v150, v27, v150
	v_mul_f32_e32 v151, v27, v151
	ds_write_b128 v209, v[148:151] offset:1024
	v_mul_f32_e32 v152, v28, v152
	v_mul_f32_e32 v153, v28, v153
	v_mul_f32_e32 v154, v28, v154
	v_mul_f32_e32 v155, v28, v155
	ds_write_b128 v209, v[152:155] offset:2048
	v_mul_f32_e32 v156, v29, v156
	v_mul_f32_e32 v157, v29, v157
	v_mul_f32_e32 v158, v29, v158
	v_mul_f32_e32 v159, v29, v159
	ds_write_b128 v209, v[156:159] offset:3072
	v_mul_f32_e32 v160, v30, v160
	v_mul_f32_e32 v161, v30, v161
	v_mul_f32_e32 v162, v30, v162
	v_mul_f32_e32 v163, v30, v163
	ds_write_b128 v209, v[160:163] offset:4096
	v_mul_f32_e32 v164, v31, v164
	v_mul_f32_e32 v165, v31, v165
	v_mul_f32_e32 v166, v31, v166
	v_mul_f32_e32 v167, v31, v167
	ds_write_b128 v209, v[164:167] offset:5120
	v_mul_f32_e32 v168, v32, v168
	v_mul_f32_e32 v169, v32, v169
	v_mul_f32_e32 v170, v32, v170
	v_mul_f32_e32 v171, v32, v171
	ds_write_b128 v209, v[168:171] offset:6144
	v_mul_f32_e32 v172, v33, v172
	v_mul_f32_e32 v173, v33, v173
	v_mul_f32_e32 v174, v33, v174
	v_mul_f32_e32 v175, v33, v175
	ds_write_b128 v209, v[172:175] offset:7168
	s_waitcnt lgkmcnt(0)
	s_barrier
; #define GAS __attribute__((address_space(1)))
; #define LAS __attribute__((address_space(3)))
; #define LDS_WAIT() asm volatile("s_waitcnt lgkmcnt(0)" ::: "memory")
;     const int pr = item >> 1, kb = 2 * (pr / nblk) + (item & 1), nb = pr % nblk, k0 = 64 * kb, n0 = 32 * nb;
;     const int nr = n0 + (lane & 31); const int sc = MAP == 1 ? src_col_in(nr) : nr;
;     float v[32];
; #pragma unroll
;     for (int i = 0; i < 32; ++i) v[i] = sc >= 0 ? W[(size_t)(k0 + 2 * i + (lane >> 5)) * Nsrc + sc] : 0.f;
; #pragma unroll
;     for (int i = 0; i < 32; ++i) { const int k = k0 + 2 * i + (lane >> 5); float x = v[i] * wscale; if (KS) x *= (k < ksplit ? ksA[k] : ksB[k - ksplit]); scr[(2 * i + (lane >> 5)) * 33 + (lane & 31)] = x; }
;     LDS_WAIT(); asm volatile("" ::: "memory");
;     const int c = lane & 7;
; #pragma unroll
;     for (int j = 0; j < 4; ++j) { const int n = (lane >> 3) + 8 * j; const LAS float* s = scr + (8 * c) * 33 + n;
;         const unsigned long long o = (unsigned long long)pg8::pk4_fp8(s[0 * 33], s[1 * 33], s[2 * 33], s[3 * 33]) | ((unsigned long long)pg8::pk4_fp8(s[4 * 33], s[5 * 33], s[6 * 33], s[7 * 33]) << 32);
;         *(GAS unsigned long long*)(WT + (size_t)(n0 + n) * K + k0 + 8 * c) = o; }
	s_add_u32 s8, s30, 0x4000
	s_addc_u32 s9, s31, 0
	global_load_dwordx4 v[144:147], v74, s[8:9]
	s_add_u32 s8, s8, 0x20000
	s_addc_u32 s9, s9, 0
	global_load_dwordx4 v[148:151], v74, s[8:9]
	s_add_u32 s8, s8, 0x20000
	s_addc_u32 s9, s9, 0
	global_load_dwordx4 v[152:155], v74, s[8:9]
	s_add_u32 s8, s8, 0x20000
	s_addc_u32 s9, s9, 0
	global_load_dwordx4 v[156:159], v74, s[8:9]
	s_add_u32 s8, s8, 0x20000
	s_addc_u32 s9, s9, 0
	global_load_dwordx4 v[160:163], v74, s[8:9]
	s_add_u32 s8, s8, 0x20000
	s_addc_u32 s9, s9, 0
	global_load_dwordx4 v[164:167], v74, s[8:9]
	s_add_u32 s8, s8, 0x20000
	s_addc_u32 s9, s9, 0
	global_load_dwordx4 v[168:171], v74, s[8:9]
	s_add_u32 s8, s8, 0x20000
	s_addc_u32 s9, s9, 0
	global_load_dwordx4 v[172:175], v74, s[8:9]
	s_add_u32 s6, s32, 0x800000
	s_addc_u32 s7, s33, 0
	ds_read_b32 v226, v211
	ds_read_b32 v227, v211 offset:512
	ds_read_b32 v228, v211 offset:1024
	ds_read_b32 v229, v211 offset:1536
	ds_read_b32 v230, v211 offset:2048
	ds_read_b32 v231, v211 offset:2560
	ds_read_b32 v232, v211 offset:3072
	ds_read_b32 v233, v211 offset:3584
	ds_read_b32 v234, v211 offset:4096
	ds_read_b32 v235, v211 offset:4608
	ds_read_b32 v236, v211 offset:5120
	ds_read_b32 v237, v211 offset:5632
	ds_read_b32 v238, v211 offset:6144
	ds_read_b32 v239, v211 offset:6656
	ds_read_b32 v240, v211 offset:7168
	ds_read_b32 v241, v211 offset:7680
	s_waitcnt lgkmcnt(0)
	v_max_f32_e32 v226, v226, v226
	v_max_f32_e32 v227, v227, v227
	v_max_f32_e32 v228, v228, v228
	v_max_f32_e32 v229, v229, v229
	v_max_f32_e32 v230, v230, v230
	v_max_f32_e32 v231, v231, v231
	v_max_f32_e32 v232, v232, v232
	v_max_f32_e32 v233, v233, v233
	v_max_f32_e32 v234, v234, v234
	v_max_f32_e32 v235, v235, v235
	v_max_f32_e32 v236, v236, v236
	v_max_f32_e32 v237, v237, v237
	v_max_f32_e32 v238, v238, v238
	v_max_f32_e32 v239, v239, v239
	v_max_f32_e32 v240, v240, v240
	v_max_f32_e32 v241, v241, v241
	v_med3_f32 v226, v226, s62, v95
	v_med3_f32 v227, v227, s62, v95
	v_med3_f32 v228, v228, s62, v95
	v_med3_f32 v229, v229, s62, v95
	v_med3_f32 v230, v230, s62, v95
	v_med3_f32 v231, v231, s62, v95
	v_med3_f32 v232, v232, s62, v95
	v_med3_f32 v233, v233, s62, v95
	v_med3_f32 v234, v234, s62, v95
	v_med3_f32 v235, v235, s62, v95
	v_med3_f32 v236, v236, s62, v95
	v_med3_f32 v237, v237, s62, v95
	v_med3_f32 v238, v238, s62, v95
	v_med3_f32 v239, v239, s62, v95
	v_med3_f32 v240, v240, s62, v95
	v_med3_f32 v241, v241, s62, v95
	v_mov_b32_e32 v242, 0
	v_mov_b32_e32 v243, 0
	v_mov_b32_e32 v244, 0
	v_mov_b32_e32 v245, 0
	v_cvt_pk_fp8_f32 v242, v226, v227
	v_cvt_pk_fp8_f32 v243, v230, v231
	v_cvt_pk_fp8_f32 v244, v234, v235
	v_cvt_pk_fp8_f32 v245, v238, v239
	v_cvt_pk_fp8_f32 v242, v228, v229 op_sel:[0,0,1]
	v_cvt_pk_fp8_f32 v243, v232, v233 op_sel:[0,0,1]
	v_cvt_pk_fp8_f32 v244, v236, v237 op_sel:[0,0,1]
	v_cvt_pk_fp8_f32 v245, v240, v241 op_sel:[0,0,1]
	s_nop 0
	global_store_dwordx4 v77, v[242:245], s[6:7]
	ds_read_b32 v226, v213
	ds_read_b32 v227, v213 offset:512
	ds_read_b32 v228, v213 offset:1024
	ds_read_b32 v229, v213 offset:1536
	ds_read_b32 v230, v213 offset:2048
	ds_read_b32 v231, v213 offset:2560
	ds_read_b32 v232, v213 offset:3072
	ds_read_b32 v233, v213 offset:3584
	ds_read_b32 v234, v213 offset:4096
	ds_read_b32 v235, v213 offset:4608
	ds_read_b32 v236, v213 offset:5120
	ds_read_b32 v237, v213 offset:5632
	ds_read_b32 v238, v213 offset:6144
	ds_read_b32 v239, v213 offset:6656
	ds_read_b32 v240, v213 offset:7168
	ds_read_b32 v241, v213 offset:7680
	s_waitcnt lgkmcnt(0)
	v_max_f32_e32 v226, v226, v226
	v_max_f32_e32 v227, v227, v227
	v_max_f32_e32 v228, v228, v228
	v_max_f32_e32 v229, v229, v229
	v_max_f32_e32 v230, v230, v230
	v_max_f32_e32 v231, v231, v231
	v_max_f32_e32 v232, v232, v232
	v_max_f32_e32 v233, v233, v233
	v_max_f32_e32 v234, v234, v234
	v_max_f32_e32 v235, v235, v235
	v_max_f32_e32 v236, v236, v236
	v_max_f32_e32 v237, v237, v237
	v_max_f32_e32 v238, v238, v238
	v_max_f32_e32 v239, v239, v239
	v_max_f32_e32 v240, v240, v240
	v_max_f32_e32 v241, v241, v241
	v_med3_f32 v226, v226, s62, v95
	v_med3_f32 v227, v227, s62, v95
	v_med3_f32 v228, v228, s62, v95
	v_med3_f32 v229, v229, s62, v95
	v_med3_f32 v230, v230, s62, v95
	v_med3_f32 v231, v231, s62, v95
	v_med3_f32 v232, v232, s62, v95
	v_med3_f32 v233, v233, s62, v95
	v_med3_f32 v234, v234, s62, v95
	v_med3_f32 v235, v235, s62, v95
	v_med3_f32 v236, v236, s62, v95
	v_med3_f32 v237, v237, s62, v95
	v_med3_f32 v238, v238, s62, v95
	v_med3_f32 v239, v239, s62, v95
	v_med3_f32 v240, v240, s62, v95
	v_med3_f32 v241, v241, s62, v95
	v_mov_b32_e32 v242, 0
	v_mov_b32_e32 v243, 0
	v_mov_b32_e32 v244, 0
	v_mov_b32_e32 v245, 0
	v_cvt_pk_fp8_f32 v242, v226, v227
	v_cvt_pk_fp8_f32 v243, v230, v231
	v_cvt_pk_fp8_f32 v244, v234, v235
	v_cvt_pk_fp8_f32 v245, v238, v239
	v_cvt_pk_fp8_f32 v242, v228, v229 op_sel:[0,0,1]
	v_cvt_pk_fp8_f32 v243, v232, v233 op_sel:[0,0,1]
	v_cvt_pk_fp8_f32 v244, v236, v237 op_sel:[0,0,1]
	v_cvt_pk_fp8_f32 v245, v240, v241 op_sel:[0,0,1]
	s_nop 0
	global_store_dwordx4 v78, v[242:245], s[6:7]
	s_waitcnt vmcnt(12)
	v_mul_f32_e32 v176, v26, v176
	v_mul_f32_e32 v177, v26, v177
	v_mul_f32_e32 v178, v26, v178
	v_mul_f32_e32 v179, v26, v179
	ds_write_b128 v210, v[176:179]
	v_mul_f32_e32 v180, v27, v180
	v_mul_f32_e32 v181, v27, v181
	v_mul_f32_e32 v182, v27, v182
	v_mul_f32_e32 v183, v27, v183
	ds_write_b128 v210, v[180:183] offset:1024
	v_mul_f32_e32 v184, v28, v184
	v_mul_f32_e32 v185, v28, v185
	v_mul_f32_e32 v186, v28, v186
	v_mul_f32_e32 v187, v28, v187
	ds_write_b128 v210, v[184:187] offset:2048
	v_mul_f32_e32 v188, v29, v188
	v_mul_f32_e32 v189, v29, v189
	v_mul_f32_e32 v190, v29, v190
	v_mul_f32_e32 v191, v29, v191
	ds_write_b128 v210, v[188:191] offset:3072
	v_mul_f32_e32 v192, v30, v192
	v_mul_f32_e32 v193, v30, v193
	v_mul_f32_e32 v194, v30, v194
	v_mul_f32_e32 v195, v30, v195
	ds_write_b128 v210, v[192:195] offset:4096
	v_mul_f32_e32 v196, v31, v196
	v_mul_f32_e32 v197, v31, v197
	v_mul_f32_e32 v198, v31, v198
	v_mul_f32_e32 v199, v31, v199
	ds_write_b128 v210, v[196:199] offset:5120
	v_mul_f32_e32 v200, v32, v200
	v_mul_f32_e32 v201, v32, v201
	v_mul_f32_e32 v202, v32, v202
	v_mul_f32_e32 v203, v32, v203
	ds_write_b128 v210, v[200:203] offset:6144
	v_mul_f32_e32 v204, v33, v204
	v_mul_f32_e32 v205, v33, v205
	v_mul_f32_e32 v206, v33, v206
	v_mul_f32_e32 v207, v33, v207
	ds_write_b128 v210, v[204:207] offset:7168
	s_waitcnt lgkmcnt(0)
	s_barrier
; #define GAS __attribute__((address_space(1)))
; #define LAS __attribute__((address_space(3)))
; #define LDS_WAIT() asm volatile("s_waitcnt lgkmcnt(0)" ::: "memory")
;     const int pr = item >> 1, kb = 2 * (pr / nblk) + (item & 1), nb = pr % nblk, k0 = 64 * kb, n0 = 32 * nb;
;     const int nr = n0 + (lane & 31); const int sc = MAP == 1 ? src_col_in(nr) : nr;
;     float v[32];
; #pragma unroll
;     for (int i = 0; i < 32; ++i) v[i] = sc >= 0 ? W[(size_t)(k0 + 2 * i + (lane >> 5)) * Nsrc + sc] : 0.f;
; #pragma unroll
;     for (int i = 0; i < 32; ++i) { const int k = k0 + 2 * i + (lane >> 5); float x = v[i] * wscale; if (KS) x *= (k < ksplit ? ksA[k] : ksB[k - ksplit]); scr[(2 * i + (lane >> 5)) * 33 + (lane & 31)] = x; }
;     LDS_WAIT(); asm volatile("" ::: "memory");
;     const int c = lane & 7;
; #pragma unroll
;     for (int j = 0; j < 4; ++j) { const int n = (lane >> 3) + 8 * j; const LAS float* s = scr + (8 * c) * 33 + n;
;         const unsigned long long o = (unsigned long long)pg8::pk4_fp8(s[0 * 33], s[1 * 33], s[2 * 33], s[3 * 33]) | ((unsigned long long)pg8::pk4_fp8(s[4 * 33], s[5 * 33], s[6 * 33], s[7 * 33]) << 32);
;         *(GAS unsigned long long*)(WT + (size_t)(n0 + n) * K + k0 + 8 * c) = o; }
	s_add_u32 s8, s30, 0x5000
	s_addc_u32 s9, s31, 0
	global_load_dwordx4 v[176:179], v74, s[8:9]
	s_add_u32 s8, s8, 0x20000
	s_addc_u32 s9, s9, 0
	global_load_dwordx4 v[180:183], v74, s[8:9]
	s_add_u32 s8, s8, 0x20000
	s_addc_u32 s9, s9, 0
	global_load_dwordx4 v[184:187], v74, s[8:9]
	s_add_u32 s8, s8, 0x20000
	s_addc_u32 s9, s9, 0
	global_load_dwordx4 v[188:191], v74, s[8:9]
	s_add_u32 s8, s8, 0x20000
	s_addc_u32 s9, s9, 0
	global_load_dwordx4 v[192:195], v74, s[8:9]
	s_add_u32 s8, s8, 0x20000
	s_addc_u32 s9, s9, 0
	global_load_dwordx4 v[196:199], v74, s[8:9]
	s_add_u32 s8, s8, 0x20000
	s_addc_u32 s9, s9, 0
	global_load_dwordx4 v[200:203], v74, s[8:9]
	s_add_u32 s8, s8, 0x20000
	s_addc_u32 s9, s9, 0
	global_load_dwordx4 v[204:207], v74, s[8:9]
	s_add_u32 s6, s32, 0xc00000
	s_addc_u32 s7, s33, 0
	ds_read_b32 v226, v212
	ds_read_b32 v227, v212 offset:512
	ds_read_b32 v228, v212 offset:1024
	ds_read_b32 v229, v212 offset:1536
	ds_read_b32 v230, v212 offset:2048
	ds_read_b32 v231, v212 offset:2560
	ds_read_b32 v232, v212 offset:3072
	ds_read_b32 v233, v212 offset:3584
	ds_read_b32 v234, v212 offset:4096
	ds_read_b32 v235, v212 offset:4608
	ds_read_b32 v236, v212 offset:5120
	ds_read_b32 v237, v212 offset:5632
	ds_read_b32 v238, v212 offset:6144
	ds_read_b32 v239, v212 offset:6656
	ds_read_b32 v240, v212 offset:7168
	ds_read_b32 v241, v212 offset:7680
	s_waitcnt lgkmcnt(0)
	v_max_f32_e32 v226, v226, v226
	v_max_f32_e32 v227, v227, v227
	v_max_f32_e32 v228, v228, v228
	v_max_f32_e32 v229, v229, v229
	v_max_f32_e32 v230, v230, v230
	v_max_f32_e32 v231, v231, v231
	v_max_f32_e32 v232, v232, v232
	v_max_f32_e32 v233, v233, v233
	v_max_f32_e32 v234, v234, v234
	v_max_f32_e32 v235, v235, v235
	v_max_f32_e32 v236, v236, v236
	v_max_f32_e32 v237, v237, v237
	v_max_f32_e32 v238, v238, v238
	v_max_f32_e32 v239, v239, v239
	v_max_f32_e32 v240, v240, v240
	v_max_f32_e32 v241, v241, v241
	v_med3_f32 v226, v226, s62, v95
	v_med3_f32 v227, v227, s62, v95
	v_med3_f32 v228, v228, s62, v95
	v_med3_f32 v229, v229, s62, v95
	v_med3_f32 v230, v230, s62, v95
	v_med3_f32 v231, v231, s62, v95
	v_med3_f32 v232, v232, s62, v95
	v_med3_f32 v233, v233, s62, v95
	v_med3_f32 v234, v234, s62, v95
	v_med3_f32 v235, v235, s62, v95
	v_med3_f32 v236, v236, s62, v95
	v_med3_f32 v237, v237, s62, v95
	v_med3_f32 v238, v238, s62, v95
	v_med3_f32 v239, v239, s62, v95
	v_med3_f32 v240, v240, s62, v95
	v_med3_f32 v241, v241, s62, v95
	v_mov_b32_e32 v242, 0
	v_mov_b32_e32 v243, 0
	v_mov_b32_e32 v244, 0
	v_mov_b32_e32 v245, 0
	v_cvt_pk_fp8_f32 v242, v226, v227
	v_cvt_pk_fp8_f32 v243, v230, v231
	v_cvt_pk_fp8_f32 v244, v234, v235
	v_cvt_pk_fp8_f32 v245, v238, v239
	v_cvt_pk_fp8_f32 v242, v228, v229 op_sel:[0,0,1]
	v_cvt_pk_fp8_f32 v243, v232, v233 op_sel:[0,0,1]
	v_cvt_pk_fp8_f32 v244, v236, v237 op_sel:[0,0,1]
	v_cvt_pk_fp8_f32 v245, v240, v241 op_sel:[0,0,1]
	s_nop 0
	global_store_dwordx4 v77, v[242:245], s[6:7]
	ds_read_b32 v226, v214
	ds_read_b32 v227, v214 offset:512
	ds_read_b32 v228, v214 offset:1024
	ds_read_b32 v229, v214 offset:1536
	ds_read_b32 v230, v214 offset:2048
	ds_read_b32 v231, v214 offset:2560
	ds_read_b32 v232, v214 offset:3072
	ds_read_b32 v233, v214 offset:3584
	ds_read_b32 v234, v214 offset:4096
	ds_read_b32 v235, v214 offset:4608
	ds_read_b32 v236, v214 offset:5120
	ds_read_b32 v237, v214 offset:5632
	ds_read_b32 v238, v214 offset:6144
	ds_read_b32 v239, v214 offset:6656
	ds_read_b32 v240, v214 offset:7168
	ds_read_b32 v241, v214 offset:7680
	s_waitcnt lgkmcnt(0)
	v_max_f32_e32 v226, v226, v226
	v_max_f32_e32 v227, v227, v227
	v_max_f32_e32 v228, v228, v228
	v_max_f32_e32 v229, v229, v229
	v_max_f32_e32 v230, v230, v230
	v_max_f32_e32 v231, v231, v231
	v_max_f32_e32 v232, v232, v232
	v_max_f32_e32 v233, v233, v233
	v_max_f32_e32 v234, v234, v234
	v_max_f32_e32 v235, v235, v235
	v_max_f32_e32 v236, v236, v236
	v_max_f32_e32 v237, v237, v237
	v_max_f32_e32 v238, v238, v238
	v_max_f32_e32 v239, v239, v239
	v_max_f32_e32 v240, v240, v240
	v_max_f32_e32 v241, v241, v241
	v_med3_f32 v226, v226, s62, v95
	v_med3_f32 v227, v227, s62, v95
	v_med3_f32 v228, v228, s62, v95
	v_med3_f32 v229, v229, s62, v95
	v_med3_f32 v230, v230, s62, v95
	v_med3_f32 v231, v231, s62, v95
	v_med3_f32 v232, v232, s62, v95
	v_med3_f32 v233, v233, s62, v95
	v_med3_f32 v234, v234, s62, v95
	v_med3_f32 v235, v235, s62, v95
	v_med3_f32 v236, v236, s62, v95
	v_med3_f32 v237, v237, s62, v95
	v_med3_f32 v238, v238, s62, v95
	v_med3_f32 v239, v239, s62, v95
	v_med3_f32 v240, v240, s62, v95
	v_med3_f32 v241, v241, s62, v95
	v_mov_b32_e32 v242, 0
	v_mov_b32_e32 v243, 0
	v_mov_b32_e32 v244, 0
	v_mov_b32_e32 v245, 0
	v_cvt_pk_fp8_f32 v242, v226, v227
	v_cvt_pk_fp8_f32 v243, v230, v231
	v_cvt_pk_fp8_f32 v244, v234, v235
	v_cvt_pk_fp8_f32 v245, v238, v239
	v_cvt_pk_fp8_f32 v242, v228, v229 op_sel:[0,0,1]
	v_cvt_pk_fp8_f32 v243, v232, v233 op_sel:[0,0,1]
	v_cvt_pk_fp8_f32 v244, v236, v237 op_sel:[0,0,1]
	v_cvt_pk_fp8_f32 v245, v240, v241 op_sel:[0,0,1]
	s_nop 0
	global_store_dwordx4 v78, v[242:245], s[6:7]
	s_waitcnt vmcnt(12)
	v_mul_f32_e32 v144, v26, v144
	v_mul_f32_e32 v145, v26, v145
	v_mul_f32_e32 v146, v26, v146
	v_mul_f32_e32 v147, v26, v147
	ds_write_b128 v209, v[144:147]
	v_mul_f32_e32 v148, v27, v148
	v_mul_f32_e32 v149, v27, v149
	v_mul_f32_e32 v150, v27, v150
	v_mul_f32_e32 v151, v27, v151
	ds_write_b128 v209, v[148:151] offset:1024
	v_mul_f32_e32 v152, v28, v152
	v_mul_f32_e32 v153, v28, v153
	v_mul_f32_e32 v154, v28, v154
	v_mul_f32_e32 v155, v28, v155
	ds_write_b128 v209, v[152:155] offset:2048
	v_mul_f32_e32 v156, v29, v156
	v_mul_f32_e32 v157, v29, v157
	v_mul_f32_e32 v158, v29, v158
	v_mul_f32_e32 v159, v29, v159
	ds_write_b128 v209, v[156:159] offset:3072
	v_mul_f32_e32 v160, v30, v160
	v_mul_f32_e32 v161, v30, v161
	v_mul_f32_e32 v162, v30, v162
	v_mul_f32_e32 v163, v30, v163
	ds_write_b128 v209, v[160:163] offset:4096
	v_mul_f32_e32 v164, v31, v164
	v_mul_f32_e32 v165, v31, v165
	v_mul_f32_e32 v166, v31, v166
	v_mul_f32_e32 v167, v31, v167
	ds_write_b128 v209, v[164:167] offset:5120
	v_mul_f32_e32 v168, v32, v168
	v_mul_f32_e32 v169, v32, v169
	v_mul_f32_e32 v170, v32, v170
	v_mul_f32_e32 v171, v32, v171
	ds_write_b128 v209, v[168:171] offset:6144
	v_mul_f32_e32 v172, v33, v172
	v_mul_f32_e32 v173, v33, v173
	v_mul_f32_e32 v174, v33, v174
	v_mul_f32_e32 v175, v33, v175
	ds_write_b128 v209, v[172:175] offset:7168
	s_waitcnt lgkmcnt(0)
	s_barrier
; #define GAS __attribute__((address_space(1)))
; #define LAS __attribute__((address_space(3)))
; #define LDS_WAIT() asm volatile("s_waitcnt lgkmcnt(0)" ::: "memory")
; __device__ __forceinline__ unsigned pk4_fp8(float a, float b, float c, float d) {
;     a = fminf(fmaxf(a, -448.f), 448.f); b = fminf(fmaxf(b, -448.f), 448.f); c = fminf(fmaxf(c, -448.f), 448.f); d = fminf(fmaxf(d, -448.f), 448.f);
;     int w = __builtin_amdgcn_cvt_pk_fp8_f32(a, b, 0, false); w = __builtin_amdgcn_cvt_pk_fp8_f32(c, d, w, true); return (unsigned)w; }
;     ...
;     for (int i = 0; i < 32; ++i) v[i] = sc >= 0 ? W[(size_t)(k0 + 2 * i + (lane >> 5)) * Nsrc + sc] : 0.f;
; #pragma unroll
;     for (int i = 0; i < 32; ++i) { const int k = k0 + 2 * i + (lane >> 5); float x = v[i] * wscale; if (KS) x *= (k < ksplit ? ksA[k] : ksB[k - ksplit]); scr[(2 * i + (lane >> 5)) * 33 + (lane & 31)] = x; }
;     LDS_WAIT(); asm volatile("" ::: "memory");
;     const int c = lane & 7;
; #pragma unroll
;     for (int j = 0; j < 4; ++j) { const int n = (lane >> 3) + 8 * j; const LAS float* s = scr + (8 * c) * 33 + n;
;         const unsigned long long o = (unsigned long long)pg8::pk4_fp8(s[0 * 33], s[1 * 33], s[2 * 33], s[3 * 33]) | ((unsigned long long)pg8::pk4_fp8(s[4 * 33], s[5 * 33], s[6 * 33], s[7 * 33]) << 32);
;         *(GAS unsigned long long*)(WT + (size_t)(n0 + n) * K + k0 + 8 * c) = o; }
	s_add_u32 s8, s30, 0x6000
	s_addc_u32 s9, s31, 0
	global_load_dwordx4 v[144:147], v74, s[8:9]
	s_add_u32 s8, s8, 0x20000
	s_addc_u32 s9, s9, 0
	global_load_dwordx4 v[148:151], v74, s[8:9]
	s_add_u32 s8, s8, 0x20000
	s_addc_u32 s9, s9, 0
	global_load_dwordx4 v[152:155], v74, s[8:9]
	s_add_u32 s8, s8, 0x20000
	s_addc_u32 s9, s9, 0
	global_load_dwordx4 v[156:159], v74, s[8:9]
	s_add_u32 s8, s8, 0x20000
	s_addc_u32 s9, s9, 0
	global_load_dwordx4 v[160:163], v74, s[8:9]
	s_add_u32 s8, s8, 0x20000
	s_addc_u32 s9, s9, 0
	global_load_dwordx4 v[164:167], v74, s[8:9]
	s_add_u32 s8, s8, 0x20000
	s_addc_u32 s9, s9, 0
	global_load_dwordx4 v[168:171], v74, s[8:9]
	s_add_u32 s8, s8, 0x20000
	s_addc_u32 s9, s9, 0
	global_load_dwordx4 v[172:175], v74, s[8:9]
	s_add_u32 s6, s32, 0x1000000
	s_addc_u32 s7, s33, 0
	ds_read_b32 v226, v211
	ds_read_b32 v227, v211 offset:512
	ds_read_b32 v228, v211 offset:1024
	ds_read_b32 v229, v211 offset:1536
	ds_read_b32 v230, v211 offset:2048
	ds_read_b32 v231, v211 offset:2560
	ds_read_b32 v232, v211 offset:3072
	ds_read_b32 v233, v211 offset:3584
	ds_read_b32 v234, v211 offset:4096
	ds_read_b32 v235, v211 offset:4608
	ds_read_b32 v236, v211 offset:5120
	ds_read_b32 v237, v211 offset:5632
	ds_read_b32 v238, v211 offset:6144
	ds_read_b32 v239, v211 offset:6656
	ds_read_b32 v240, v211 offset:7168
	ds_read_b32 v241, v211 offset:7680
	s_waitcnt lgkmcnt(0)
	v_max_f32_e32 v226, v226, v226
	v_max_f32_e32 v227, v227, v227
	v_max_f32_e32 v228, v228, v228
	v_max_f32_e32 v229, v229, v229
	v_max_f32_e32 v230, v230, v230
	v_max_f32_e32 v231, v231, v231
	v_max_f32_e32 v232, v232, v232
	v_max_f32_e32 v233, v233, v233
	v_max_f32_e32 v234, v234, v234
	v_max_f32_e32 v235, v235, v235
	v_max_f32_e32 v236, v236, v236
	v_max_f32_e32 v237, v237, v237
	v_max_f32_e32 v238, v238, v238
	v_max_f32_e32 v239, v239, v239
	v_max_f32_e32 v240, v240, v240
	v_max_f32_e32 v241, v241, v241
	v_med3_f32 v226, v226, s62, v95
	v_med3_f32 v227, v227, s62, v95
	v_med3_f32 v228, v228, s62, v95
	v_med3_f32 v229, v229, s62, v95
	v_med3_f32 v230, v230, s62, v95
	v_med3_f32 v231, v231, s62, v95
	v_med3_f32 v232, v232, s62, v95
	v_med3_f32 v233, v233, s62, v95
	v_med3_f32 v234, v234, s62, v95
	v_med3_f32 v235, v235, s62, v95
	v_med3_f32 v236, v236, s62, v95
	v_med3_f32 v237, v237, s62, v95
	v_med3_f32 v238, v238, s62, v95
	v_med3_f32 v239, v239, s62, v95
	v_med3_f32 v240, v240, s62, v95
	v_med3_f32 v241, v241, s62, v95
	v_mov_b32_e32 v242, 0
	v_mov_b32_e32 v243, 0
	v_mov_b32_e32 v244, 0
	v_mov_b32_e32 v245, 0
	v_cvt_pk_fp8_f32 v242, v226, v227
	v_cvt_pk_fp8_f32 v243, v230, v231
	v_cvt_pk_fp8_f32 v244, v234, v235
	v_cvt_pk_fp8_f32 v245, v238, v239
	v_cvt_pk_fp8_f32 v242, v228, v229 op_sel:[0,0,1]
	v_cvt_pk_fp8_f32 v243, v232, v233 op_sel:[0,0,1]
	v_cvt_pk_fp8_f32 v244, v236, v237 op_sel:[0,0,1]
	v_cvt_pk_fp8_f32 v245, v240, v241 op_sel:[0,0,1]
	s_nop 0
	global_store_dwordx4 v77, v[242:245], s[6:7]
	ds_read_b32 v226, v213
	ds_read_b32 v227, v213 offset:512
	ds_read_b32 v228, v213 offset:1024
	ds_read_b32 v229, v213 offset:1536
	ds_read_b32 v230, v213 offset:2048
	ds_read_b32 v231, v213 offset:2560
	ds_read_b32 v232, v213 offset:3072
	ds_read_b32 v233, v213 offset:3584
	ds_read_b32 v234, v213 offset:4096
	ds_read_b32 v235, v213 offset:4608
	ds_read_b32 v236, v213 offset:5120
	ds_read_b32 v237, v213 offset:5632
	ds_read_b32 v238, v213 offset:6144
	ds_read_b32 v239, v213 offset:6656
	ds_read_b32 v240, v213 offset:7168
	ds_read_b32 v241, v213 offset:7680
	s_waitcnt lgkmcnt(0)
	v_max_f32_e32 v226, v226, v226
	v_max_f32_e32 v227, v227, v227
	v_max_f32_e32 v228, v228, v228
	v_max_f32_e32 v229, v229, v229
	v_max_f32_e32 v230, v230, v230
	v_max_f32_e32 v231, v231, v231
	v_max_f32_e32 v232, v232, v232
	v_max_f32_e32 v233, v233, v233
	v_max_f32_e32 v234, v234, v234
	v_max_f32_e32 v235, v235, v235
	v_max_f32_e32 v236, v236, v236
	v_max_f32_e32 v237, v237, v237
	v_max_f32_e32 v238, v238, v238
	v_max_f32_e32 v239, v239, v239
	v_max_f32_e32 v240, v240, v240
	v_max_f32_e32 v241, v241, v241
	v_med3_f32 v226, v226, s62, v95
	v_med3_f32 v227, v227, s62, v95
	v_med3_f32 v228, v228, s62, v95
	v_med3_f32 v229, v229, s62, v95
	v_med3_f32 v230, v230, s62, v95
	v_med3_f32 v231, v231, s62, v95
	v_med3_f32 v232, v232, s62, v95
	v_med3_f32 v233, v233, s62, v95
	v_med3_f32 v234, v234, s62, v95
	v_med3_f32 v235, v235, s62, v95
	v_med3_f32 v236, v236, s62, v95
	v_med3_f32 v237, v237, s62, v95
	v_med3_f32 v238, v238, s62, v95
	v_med3_f32 v239, v239, s62, v95
	v_med3_f32 v240, v240, s62, v95
	v_med3_f32 v241, v241, s62, v95
	v_mov_b32_e32 v242, 0
	v_mov_b32_e32 v243, 0
	v_mov_b32_e32 v244, 0
	v_mov_b32_e32 v245, 0
	v_cvt_pk_fp8_f32 v242, v226, v227
	v_cvt_pk_fp8_f32 v243, v230, v231
	v_cvt_pk_fp8_f32 v244, v234, v235
	v_cvt_pk_fp8_f32 v245, v238, v239
	v_cvt_pk_fp8_f32 v242, v228, v229 op_sel:[0,0,1]
	v_cvt_pk_fp8_f32 v243, v232, v233 op_sel:[0,0,1]
	v_cvt_pk_fp8_f32 v244, v236, v237 op_sel:[0,0,1]
	v_cvt_pk_fp8_f32 v245, v240, v241 op_sel:[0,0,1]
	s_nop 0
	global_store_dwordx4 v78, v[242:245], s[6:7]
	s_waitcnt vmcnt(12)
	v_mul_f32_e32 v176, v26, v176
	v_mul_f32_e32 v177, v26, v177
	v_mul_f32_e32 v178, v26, v178
	v_mul_f32_e32 v179, v26, v179
	ds_write_b128 v210, v[176:179]
	v_mul_f32_e32 v180, v27, v180
	v_mul_f32_e32 v181, v27, v181
	v_mul_f32_e32 v182, v27, v182
	v_mul_f32_e32 v183, v27, v183
	ds_write_b128 v210, v[180:183] offset:1024
	v_mul_f32_e32 v184, v28, v184
	v_mul_f32_e32 v185, v28, v185
	v_mul_f32_e32 v186, v28, v186
	v_mul_f32_e32 v187, v28, v187
	ds_write_b128 v210, v[184:187] offset:2048
	v_mul_f32_e32 v188, v29, v188
	v_mul_f32_e32 v189, v29, v189
	v_mul_f32_e32 v190, v29, v190
	v_mul_f32_e32 v191, v29, v191
	ds_write_b128 v210, v[188:191] offset:3072
	v_mul_f32_e32 v192, v30, v192
	v_mul_f32_e32 v193, v30, v193
	v_mul_f32_e32 v194, v30, v194
	v_mul_f32_e32 v195, v30, v195
	ds_write_b128 v210, v[192:195] offset:4096
	v_mul_f32_e32 v196, v31, v196
	v_mul_f32_e32 v197, v31, v197
	v_mul_f32_e32 v198, v31, v198
	v_mul_f32_e32 v199, v31, v199
	ds_write_b128 v210, v[196:199] offset:5120
	v_mul_f32_e32 v200, v32, v200
	v_mul_f32_e32 v201, v32, v201
	v_mul_f32_e32 v202, v32, v202
	v_mul_f32_e32 v203, v32, v203
	ds_write_b128 v210, v[200:203] offset:6144
	v_mul_f32_e32 v204, v33, v204
	v_mul_f32_e32 v205, v33, v205
	v_mul_f32_e32 v206, v33, v206
	v_mul_f32_e32 v207, v33, v207
	ds_write_b128 v210, v[204:207] offset:7168
	s_waitcnt lgkmcnt(0)
	s_barrier
; #define GAS __attribute__((address_space(1)))
; #define LAS __attribute__((address_space(3)))
; #define LDS_WAIT() asm volatile("s_waitcnt lgkmcnt(0)" ::: "memory")
; __device__ __forceinline__ unsigned pk4_fp8(float a, float b, float c, float d) {
;     a = fminf(fmaxf(a, -448.f), 448.f); b = fminf(fmaxf(b, -448.f), 448.f); c = fminf(fmaxf(c, -448.f), 448.f); d = fminf(fmaxf(d, -448.f), 448.f);
;     int w = __builtin_amdgcn_cvt_pk_fp8_f32(a, b, 0, false); w = __builtin_amdgcn_cvt_pk_fp8_f32(c, d, w, true); return (unsigned)w; }
;     ...
;     for (int i = 0; i < 32; ++i) v[i] = sc >= 0 ? W[(size_t)(k0 + 2 * i + (lane >> 5)) * Nsrc + sc] : 0.f;
; #pragma unroll
;     for (int i = 0; i < 32; ++i) { const int k = k0 + 2 * i + (lane >> 5); float x = v[i] * wscale; if (KS) x *= (k < ksplit ? ksA[k] : ksB[k - ksplit]); scr[(2 * i + (lane >> 5)) * 33 + (lane & 31)] = x; }
;     LDS_WAIT(); asm volatile("" ::: "memory");
;     const int c = lane & 7;
; #pragma unroll
;     for (int j = 0; j < 4; ++j) { const int n = (lane >> 3) + 8 * j; const LAS float* s = scr + (8 * c) * 33 + n;
;         const unsigned long long o = (unsigned long long)pg8::pk4_fp8(s[0 * 33], s[1 * 33], s[2 * 33], s[3 * 33]) | ((unsigned long long)pg8::pk4_fp8(s[4 * 33], s[5 * 33], s[6 * 33], s[7 * 33]) << 32);
;         *(GAS unsigned long long*)(WT + (size_t)(n0 + n) * K + k0 + 8 * c) = o; }
	s_add_u32 s8, s30, 0x7000
	s_addc_u32 s9, s31, 0
	global_load_dwordx4 v[176:179], v74, s[8:9]
	s_add_u32 s8, s8, 0x20000
	s_addc_u32 s9, s9, 0
	global_load_dwordx4 v[180:183], v74, s[8:9]
	s_add_u32 s8, s8, 0x20000
	s_addc_u32 s9, s9, 0
	global_load_dwordx4 v[184:187], v74, s[8:9]
	s_add_u32 s8, s8, 0x20000
	s_addc_u32 s9, s9, 0
	global_load_dwordx4 v[188:191], v74, s[8:9]
	s_add_u32 s8, s8, 0x20000
	s_addc_u32 s9, s9, 0
	global_load_dwordx4 v[192:195], v74, s[8:9]
	s_add_u32 s8, s8, 0x20000
	s_addc_u32 s9, s9, 0
	global_load_dwordx4 v[196:199], v74, s[8:9]
	s_add_u32 s8, s8, 0x20000
	s_addc_u32 s9, s9, 0
	global_load_dwordx4 v[200:203], v74, s[8:9]
	s_add_u32 s8, s8, 0x20000
	s_addc_u32 s9, s9, 0
	global_load_dwordx4 v[204:207], v74, s[8:9]
	s_add_u32 s6, s32, 0x1400000
	s_addc_u32 s7, s33, 0
	ds_read_b32 v226, v212
	ds_read_b32 v227, v212 offset:512
	ds_read_b32 v228, v212 offset:1024
	ds_read_b32 v229, v212 offset:1536
	ds_read_b32 v230, v212 offset:2048
	ds_read_b32 v231, v212 offset:2560
	ds_read_b32 v232, v212 offset:3072
	ds_read_b32 v233, v212 offset:3584
	ds_read_b32 v234, v212 offset:4096
	ds_read_b32 v235, v212 offset:4608
	ds_read_b32 v236, v212 offset:5120
	ds_read_b32 v237, v212 offset:5632
	ds_read_b32 v238, v212 offset:6144
	ds_read_b32 v239, v212 offset:6656
	ds_read_b32 v240, v212 offset:7168
	ds_read_b32 v241, v212 offset:7680
	s_waitcnt lgkmcnt(0)
	v_max_f32_e32 v226, v226, v226
	v_max_f32_e32 v227, v227, v227
	v_max_f32_e32 v228, v228, v228
	v_max_f32_e32 v229, v229, v229
	v_max_f32_e32 v230, v230, v230
	v_max_f32_e32 v231, v231, v231
	v_max_f32_e32 v232, v232, v232
	v_max_f32_e32 v233, v233, v233
	v_max_f32_e32 v234, v234, v234
	v_max_f32_e32 v235, v235, v235
	v_max_f32_e32 v236, v236, v236
	v_max_f32_e32 v237, v237, v237
	v_max_f32_e32 v238, v238, v238
	v_max_f32_e32 v239, v239, v239
	v_max_f32_e32 v240, v240, v240
	v_max_f32_e32 v241, v241, v241
	v_med3_f32 v226, v226, s62, v95
	v_med3_f32 v227, v227, s62, v95
	v_med3_f32 v228, v228, s62, v95
	v_med3_f32 v229, v229, s62, v95
	v_med3_f32 v230, v230, s62, v95
	v_med3_f32 v231, v231, s62, v95
	v_med3_f32 v232, v232, s62, v95
	v_med3_f32 v233, v233, s62, v95
	v_med3_f32 v234, v234, s62, v95
	v_med3_f32 v235, v235, s62, v95
	v_med3_f32 v236, v236, s62, v95
	v_med3_f32 v237, v237, s62, v95
	v_med3_f32 v238, v238, s62, v95
	v_med3_f32 v239, v239, s62, v95
	v_med3_f32 v240, v240, s62, v95
	v_med3_f32 v241, v241, s62, v95
	v_mov_b32_e32 v242, 0
	v_mov_b32_e32 v243, 0
	v_mov_b32_e32 v244, 0
	v_mov_b32_e32 v245, 0
	v_cvt_pk_fp8_f32 v242, v226, v227
	v_cvt_pk_fp8_f32 v243, v230, v231
	v_cvt_pk_fp8_f32 v244, v234, v235
	v_cvt_pk_fp8_f32 v245, v238, v239
	v_cvt_pk_fp8_f32 v242, v228, v229 op_sel:[0,0,1]
	v_cvt_pk_fp8_f32 v243, v232, v233 op_sel:[0,0,1]
	v_cvt_pk_fp8_f32 v244, v236, v237 op_sel:[0,0,1]
	v_cvt_pk_fp8_f32 v245, v240, v241 op_sel:[0,0,1]
	s_nop 0
	global_store_dwordx4 v77, v[242:245], s[6:7]
	ds_read_b32 v226, v214
	ds_read_b32 v227, v214 offset:512
	ds_read_b32 v228, v214 offset:1024
	ds_read_b32 v229, v214 offset:1536
	ds_read_b32 v230, v214 offset:2048
	ds_read_b32 v231, v214 offset:2560
	ds_read_b32 v232, v214 offset:3072
	ds_read_b32 v233, v214 offset:3584
	ds_read_b32 v234, v214 offset:4096
	ds_read_b32 v235, v214 offset:4608
	ds_read_b32 v236, v214 offset:5120
	ds_read_b32 v237, v214 offset:5632
	ds_read_b32 v238, v214 offset:6144
	ds_read_b32 v239, v214 offset:6656
	ds_read_b32 v240, v214 offset:7168
	ds_read_b32 v241, v214 offset:7680
	s_waitcnt lgkmcnt(0)
	v_max_f32_e32 v226, v226, v226
	v_max_f32_e32 v227, v227, v227
	v_max_f32_e32 v228, v228, v228
	v_max_f32_e32 v229, v229, v229
	v_max_f32_e32 v230, v230, v230
	v_max_f32_e32 v231, v231, v231
	v_max_f32_e32 v232, v232, v232
	v_max_f32_e32 v233, v233, v233
	v_max_f32_e32 v234, v234, v234
	v_max_f32_e32 v235, v235, v235
	v_max_f32_e32 v236, v236, v236
	v_max_f32_e32 v237, v237, v237
	v_max_f32_e32 v238, v238, v238
	v_max_f32_e32 v239, v239, v239
	v_max_f32_e32 v240, v240, v240
	v_max_f32_e32 v241, v241, v241
	v_med3_f32 v226, v226, s62, v95
	v_med3_f32 v227, v227, s62, v95
	v_med3_f32 v228, v228, s62, v95
	v_med3_f32 v229, v229, s62, v95
	v_med3_f32 v230, v230, s62, v95
	v_med3_f32 v231, v231, s62, v95
	v_med3_f32 v232, v232, s62, v95
	v_med3_f32 v233, v233, s62, v95
	v_med3_f32 v234, v234, s62, v95
	v_med3_f32 v235, v235, s62, v95
	v_med3_f32 v236, v236, s62, v95
	v_med3_f32 v237, v237, s62, v95
	v_med3_f32 v238, v238, s62, v95
	v_med3_f32 v239, v239, s62, v95
	v_med3_f32 v240, v240, s62, v95
	v_med3_f32 v241, v241, s62, v95
	v_mov_b32_e32 v242, 0
	v_mov_b32_e32 v243, 0
	v_mov_b32_e32 v244, 0
	v_mov_b32_e32 v245, 0
	v_cvt_pk_fp8_f32 v242, v226, v227
	v_cvt_pk_fp8_f32 v243, v230, v231
	v_cvt_pk_fp8_f32 v244, v234, v235
	v_cvt_pk_fp8_f32 v245, v238, v239
	v_cvt_pk_fp8_f32 v242, v228, v229 op_sel:[0,0,1]
	v_cvt_pk_fp8_f32 v243, v232, v233 op_sel:[0,0,1]
	v_cvt_pk_fp8_f32 v244, v236, v237 op_sel:[0,0,1]
	v_cvt_pk_fp8_f32 v245, v240, v241 op_sel:[0,0,1]
	s_nop 0
	global_store_dwordx4 v78, v[242:245], s[6:7]
	s_waitcnt vmcnt(12)
	v_mul_f32_e32 v144, v26, v144
	v_mul_f32_e32 v145, v26, v145
	v_mul_f32_e32 v146, v26, v146
	v_mul_f32_e32 v147, v26, v147
	ds_write_b128 v209, v[144:147]
	v_mul_f32_e32 v148, v27, v148
	v_mul_f32_e32 v149, v27, v149
	v_mul_f32_e32 v150, v27, v150
	v_mul_f32_e32 v151, v27, v151
	ds_write_b128 v209, v[148:151] offset:1024
	v_mul_f32_e32 v152, v28, v152
	v_mul_f32_e32 v153, v28, v153
	v_mul_f32_e32 v154, v28, v154
	v_mul_f32_e32 v155, v28, v155
	ds_write_b128 v209, v[152:155] offset:2048
	v_mul_f32_e32 v156, v29, v156
	v_mul_f32_e32 v157, v29, v157
	v_mul_f32_e32 v158, v29, v158
	v_mul_f32_e32 v159, v29, v159
	ds_write_b128 v209, v[156:159] offset:3072
	v_mul_f32_e32 v160, v30, v160
	v_mul_f32_e32 v161, v30, v161
	v_mul_f32_e32 v162, v30, v162
	v_mul_f32_e32 v163, v30, v163
	ds_write_b128 v209, v[160:163] offset:4096
	v_mul_f32_e32 v164, v31, v164
	v_mul_f32_e32 v165, v31, v165
	v_mul_f32_e32 v166, v31, v166
	v_mul_f32_e32 v167, v31, v167
	ds_write_b128 v209, v[164:167] offset:5120
	v_mul_f32_e32 v168, v32, v168
	v_mul_f32_e32 v169, v32, v169
	v_mul_f32_e32 v170, v32, v170
	v_mul_f32_e32 v171, v32, v171
	ds_write_b128 v209, v[168:171] offset:6144
	v_mul_f32_e32 v172, v33, v172
	v_mul_f32_e32 v173, v33, v173
	v_mul_f32_e32 v174, v33, v174
	v_mul_f32_e32 v175, v33, v175
	ds_write_b128 v209, v[172:175] offset:7168
	s_waitcnt lgkmcnt(0)
	s_barrier
; #define GAS __attribute__((address_space(1)))
; #define LAS __attribute__((address_space(3)))
; #define LDS_WAIT() asm volatile("s_waitcnt lgkmcnt(0)" ::: "memory")
; __device__ __forceinline__ unsigned pk4_fp8(float a, float b, float c, float d) {
;     a = fminf(fmaxf(a, -448.f), 448.f); b = fminf(fmaxf(b, -448.f), 448.f); c = fminf(fmaxf(c, -448.f), 448.f); d = fminf(fmaxf(d, -448.f), 448.f);
;     int w = __builtin_amdgcn_cvt_pk_fp8_f32(a, b, 0, false); w = __builtin_amdgcn_cvt_pk_fp8_f32(c, d, w, true); return (unsigned)w; }
;     ...
;     for (int i = 0; i < 32; ++i) v[i] = sc >= 0 ? W[(size_t)(k0 + 2 * i + (lane >> 5)) * Nsrc + sc] : 0.f;
; #pragma unroll
;     for (int i = 0; i < 32; ++i) { const int k = k0 + 2 * i + (lane >> 5); float x = v[i] * wscale; if (KS) x *= (k < ksplit ? ksA[k] : ksB[k - ksplit]); scr[(2 * i + (lane >> 5)) * 33 + (lane & 31)] = x; }
;     LDS_WAIT(); asm volatile("" ::: "memory");
;     const int c = lane & 7;
; #pragma unroll
;     for (int j = 0; j < 4; ++j) { const int n = (lane >> 3) + 8 * j; const LAS float* s = scr + (8 * c) * 33 + n;
;         const unsigned long long o = (unsigned long long)pg8::pk4_fp8(s[0 * 33], s[1 * 33], s[2 * 33], s[3 * 33]) | ((unsigned long long)pg8::pk4_fp8(s[4 * 33], s[5 * 33], s[6 * 33], s[7 * 33]) << 32);
;         *(GAS unsigned long long*)(WT + (size_t)(n0 + n) * K + k0 + 8 * c) = o; }
	s_add_u32 s8, s30, 0x8000
	s_addc_u32 s9, s31, 0
	global_load_dwordx4 v[144:147], v74, s[8:9]
	s_add_u32 s8, s8, 0x20000
	s_addc_u32 s9, s9, 0
	global_load_dwordx4 v[148:151], v74, s[8:9]
	s_add_u32 s8, s8, 0x20000
	s_addc_u32 s9, s9, 0
	global_load_dwordx4 v[152:155], v74, s[8:9]
	s_add_u32 s8, s8, 0x20000
	s_addc_u32 s9, s9, 0
	global_load_dwordx4 v[156:159], v74, s[8:9]
	s_add_u32 s8, s8, 0x20000
	s_addc_u32 s9, s9, 0
	global_load_dwordx4 v[160:163], v74, s[8:9]
	s_add_u32 s8, s8, 0x20000
	s_addc_u32 s9, s9, 0
	global_load_dwordx4 v[164:167], v74, s[8:9]
	s_add_u32 s8, s8, 0x20000
	s_addc_u32 s9, s9, 0
	global_load_dwordx4 v[168:171], v74, s[8:9]
	s_add_u32 s8, s8, 0x20000
	s_addc_u32 s9, s9, 0
	global_load_dwordx4 v[172:175], v74, s[8:9]
	s_add_u32 s6, s32, 0x1800000
	s_addc_u32 s7, s33, 0
	ds_read_b32 v226, v211
	ds_read_b32 v227, v211 offset:512
	ds_read_b32 v228, v211 offset:1024
	ds_read_b32 v229, v211 offset:1536
	ds_read_b32 v230, v211 offset:2048
	ds_read_b32 v231, v211 offset:2560
	ds_read_b32 v232, v211 offset:3072
	ds_read_b32 v233, v211 offset:3584
	ds_read_b32 v234, v211 offset:4096
	ds_read_b32 v235, v211 offset:4608
	ds_read_b32 v236, v211 offset:5120
	ds_read_b32 v237, v211 offset:5632
	ds_read_b32 v238, v211 offset:6144
	ds_read_b32 v239, v211 offset:6656
	ds_read_b32 v240, v211 offset:7168
	ds_read_b32 v241, v211 offset:7680
	s_waitcnt lgkmcnt(0)
	v_max_f32_e32 v226, v226, v226
	v_max_f32_e32 v227, v227, v227
	v_max_f32_e32 v228, v228, v228
	v_max_f32_e32 v229, v229, v229
	v_max_f32_e32 v230, v230, v230
	v_max_f32_e32 v231, v231, v231
	v_max_f32_e32 v232, v232, v232
	v_max_f32_e32 v233, v233, v233
	v_max_f32_e32 v234, v234, v234
	v_max_f32_e32 v235, v235, v235
	v_max_f32_e32 v236, v236, v236
	v_max_f32_e32 v237, v237, v237
	v_max_f32_e32 v238, v238, v238
	v_max_f32_e32 v239, v239, v239
	v_max_f32_e32 v240, v240, v240
	v_max_f32_e32 v241, v241, v241
	v_med3_f32 v226, v226, s62, v95
	v_med3_f32 v227, v227, s62, v95
	v_med3_f32 v228, v228, s62, v95
	v_med3_f32 v229, v229, s62, v95
	v_med3_f32 v230, v230, s62, v95
	v_med3_f32 v231, v231, s62, v95
	v_med3_f32 v232, v232, s62, v95
	v_med3_f32 v233, v233, s62, v95
	v_med3_f32 v234, v234, s62, v95
	v_med3_f32 v235, v235, s62, v95
	v_med3_f32 v236, v236, s62, v95
	v_med3_f32 v237, v237, s62, v95
	v_med3_f32 v238, v238, s62, v95
	v_med3_f32 v239, v239, s62, v95
	v_med3_f32 v240, v240, s62, v95
	v_med3_f32 v241, v241, s62, v95
	v_mov_b32_e32 v242, 0
	v_mov_b32_e32 v243, 0
	v_mov_b32_e32 v244, 0
	v_mov_b32_e32 v245, 0
	v_cvt_pk_fp8_f32 v242, v226, v227
	v_cvt_pk_fp8_f32 v243, v230, v231
	v_cvt_pk_fp8_f32 v244, v234, v235
	v_cvt_pk_fp8_f32 v245, v238, v239
	v_cvt_pk_fp8_f32 v242, v228, v229 op_sel:[0,0,1]
	v_cvt_pk_fp8_f32 v243, v232, v233 op_sel:[0,0,1]
	v_cvt_pk_fp8_f32 v244, v236, v237 op_sel:[0,0,1]
	v_cvt_pk_fp8_f32 v245, v240, v241 op_sel:[0,0,1]
	s_nop 0
	global_store_dwordx4 v77, v[242:245], s[6:7]
	ds_read_b32 v226, v213
	ds_read_b32 v227, v213 offset:512
	ds_read_b32 v228, v213 offset:1024
	ds_read_b32 v229, v213 offset:1536
	ds_read_b32 v230, v213 offset:2048
	ds_read_b32 v231, v213 offset:2560
	ds_read_b32 v232, v213 offset:3072
	ds_read_b32 v233, v213 offset:3584
	ds_read_b32 v234, v213 offset:4096
	ds_read_b32 v235, v213 offset:4608
	ds_read_b32 v236, v213 offset:5120
	ds_read_b32 v237, v213 offset:5632
	ds_read_b32 v238, v213 offset:6144
	ds_read_b32 v239, v213 offset:6656
	ds_read_b32 v240, v213 offset:7168
	ds_read_b32 v241, v213 offset:7680
	s_waitcnt lgkmcnt(0)
	v_max_f32_e32 v226, v226, v226
	v_max_f32_e32 v227, v227, v227
	v_max_f32_e32 v228, v228, v228
	v_max_f32_e32 v229, v229, v229
	v_max_f32_e32 v230, v230, v230
	v_max_f32_e32 v231, v231, v231
	v_max_f32_e32 v232, v232, v232
	v_max_f32_e32 v233, v233, v233
	v_max_f32_e32 v234, v234, v234
	v_max_f32_e32 v235, v235, v235
	v_max_f32_e32 v236, v236, v236
	v_max_f32_e32 v237, v237, v237
	v_max_f32_e32 v238, v238, v238
	v_max_f32_e32 v239, v239, v239
	v_max_f32_e32 v240, v240, v240
	v_max_f32_e32 v241, v241, v241
	v_med3_f32 v226, v226, s62, v95
	v_med3_f32 v227, v227, s62, v95
	v_med3_f32 v228, v228, s62, v95
	v_med3_f32 v229, v229, s62, v95
	v_med3_f32 v230, v230, s62, v95
	v_med3_f32 v231, v231, s62, v95
	v_med3_f32 v232, v232, s62, v95
	v_med3_f32 v233, v233, s62, v95
	v_med3_f32 v234, v234, s62, v95
	v_med3_f32 v235, v235, s62, v95
	v_med3_f32 v236, v236, s62, v95
	v_med3_f32 v237, v237, s62, v95
	v_med3_f32 v238, v238, s62, v95
	v_med3_f32 v239, v239, s62, v95
	v_med3_f32 v240, v240, s62, v95
	v_med3_f32 v241, v241, s62, v95
	v_mov_b32_e32 v242, 0
	v_mov_b32_e32 v243, 0
	v_mov_b32_e32 v244, 0
	v_mov_b32_e32 v245, 0
	v_cvt_pk_fp8_f32 v242, v226, v227
	v_cvt_pk_fp8_f32 v243, v230, v231
	v_cvt_pk_fp8_f32 v244, v234, v235
	v_cvt_pk_fp8_f32 v245, v238, v239
	v_cvt_pk_fp8_f32 v242, v228, v229 op_sel:[0,0,1]
	v_cvt_pk_fp8_f32 v243, v232, v233 op_sel:[0,0,1]
	v_cvt_pk_fp8_f32 v244, v236, v237 op_sel:[0,0,1]
	v_cvt_pk_fp8_f32 v245, v240, v241 op_sel:[0,0,1]
	s_nop 0
	global_store_dwordx4 v78, v[242:245], s[6:7]
	s_waitcnt vmcnt(12)
	v_mul_f32_e32 v176, v26, v176
	v_mul_f32_e32 v177, v26, v177
	v_mul_f32_e32 v178, v26, v178
	v_mul_f32_e32 v179, v26, v179
	ds_write_b128 v210, v[176:179]
	v_mul_f32_e32 v180, v27, v180
	v_mul_f32_e32 v181, v27, v181
	v_mul_f32_e32 v182, v27, v182
	v_mul_f32_e32 v183, v27, v183
	ds_write_b128 v210, v[180:183] offset:1024
	v_mul_f32_e32 v184, v28, v184
	v_mul_f32_e32 v185, v28, v185
	v_mul_f32_e32 v186, v28, v186
	v_mul_f32_e32 v187, v28, v187
	ds_write_b128 v210, v[184:187] offset:2048
	v_mul_f32_e32 v188, v29, v188
	v_mul_f32_e32 v189, v29, v189
	v_mul_f32_e32 v190, v29, v190
	v_mul_f32_e32 v191, v29, v191
	ds_write_b128 v210, v[188:191] offset:3072
	v_mul_f32_e32 v192, v30, v192
	v_mul_f32_e32 v193, v30, v193
	v_mul_f32_e32 v194, v30, v194
	v_mul_f32_e32 v195, v30, v195
	ds_write_b128 v210, v[192:195] offset:4096
	v_mul_f32_e32 v196, v31, v196
	v_mul_f32_e32 v197, v31, v197
	v_mul_f32_e32 v198, v31, v198
	v_mul_f32_e32 v199, v31, v199
	ds_write_b128 v210, v[196:199] offset:5120
	v_mul_f32_e32 v200, v32, v200
	v_mul_f32_e32 v201, v32, v201
	v_mul_f32_e32 v202, v32, v202
	v_mul_f32_e32 v203, v32, v203
	ds_write_b128 v210, v[200:203] offset:6144
	v_mul_f32_e32 v204, v33, v204
	v_mul_f32_e32 v205, v33, v205
	v_mul_f32_e32 v206, v33, v206
	v_mul_f32_e32 v207, v33, v207
	ds_write_b128 v210, v[204:207] offset:7168
	s_waitcnt lgkmcnt(0)
	s_barrier
; #define GAS __attribute__((address_space(1)))
; #define LAS __attribute__((address_space(3)))
; #define LDS_WAIT() asm volatile("s_waitcnt lgkmcnt(0)" ::: "memory")
; __device__ __forceinline__ unsigned pk4_fp8(float a, float b, float c, float d) {
;     a = fminf(fmaxf(a, -448.f), 448.f); b = fminf(fmaxf(b, -448.f), 448.f); c = fminf(fmaxf(c, -448.f), 448.f); d = fminf(fmaxf(d, -448.f), 448.f);
;     int w = __builtin_amdgcn_cvt_pk_fp8_f32(a, b, 0, false); w = __builtin_amdgcn_cvt_pk_fp8_f32(c, d, w, true); return (unsigned)w; }
;     ...
;     for (int i = 0; i < 32; ++i) v[i] = sc >= 0 ? W[(size_t)(k0 + 2 * i + (lane >> 5)) * Nsrc + sc] : 0.f;
; #pragma unroll
;     for (int i = 0; i < 32; ++i) { const int k = k0 + 2 * i + (lane >> 5); float x = v[i] * wscale; if (KS) x *= (k < ksplit ? ksA[k] : ksB[k - ksplit]); scr[(2 * i + (lane >> 5)) * 33 + (lane & 31)] = x; }
;     LDS_WAIT(); asm volatile("" ::: "memory");
;     const int c = lane & 7;
; #pragma unroll
;     for (int j = 0; j < 4; ++j) { const int n = (lane >> 3) + 8 * j; const LAS float* s = scr + (8 * c) * 33 + n;
;         const unsigned long long o = (unsigned long long)pg8::pk4_fp8(s[0 * 33], s[1 * 33], s[2 * 33], s[3 * 33]) | ((unsigned long long)pg8::pk4_fp8(s[4 * 33], s[5 * 33], s[6 * 33], s[7 * 33]) << 32);
;         *(GAS unsigned long long*)(WT + (size_t)(n0 + n) * K + k0 + 8 * c) = o; }
	s_add_u32 s8, s30, 0x9000
	s_addc_u32 s9, s31, 0
	global_load_dwordx4 v[176:179], v74, s[8:9]
	s_add_u32 s8, s8, 0x20000
	s_addc_u32 s9, s9, 0
	global_load_dwordx4 v[180:183], v74, s[8:9]
	s_add_u32 s8, s8, 0x20000
	s_addc_u32 s9, s9, 0
	global_load_dwordx4 v[184:187], v74, s[8:9]
	s_add_u32 s8, s8, 0x20000
	s_addc_u32 s9, s9, 0
	global_load_dwordx4 v[188:191], v74, s[8:9]
	s_add_u32 s8, s8, 0x20000
	s_addc_u32 s9, s9, 0
	global_load_dwordx4 v[192:195], v74, s[8:9]
	s_add_u32 s8, s8, 0x20000
	s_addc_u32 s9, s9, 0
	global_load_dwordx4 v[196:199], v74, s[8:9]
	s_add_u32 s8, s8, 0x20000
	s_addc_u32 s9, s9, 0
	global_load_dwordx4 v[200:203], v74, s[8:9]
	s_add_u32 s8, s8, 0x20000
	s_addc_u32 s9, s9, 0
	global_load_dwordx4 v[204:207], v74, s[8:9]
	s_add_u32 s6, s32, 0x1c00000
	s_addc_u32 s7, s33, 0
	ds_read_b32 v226, v212
	ds_read_b32 v227, v212 offset:512
	ds_read_b32 v228, v212 offset:1024
	ds_read_b32 v229, v212 offset:1536
	ds_read_b32 v230, v212 offset:2048
	ds_read_b32 v231, v212 offset:2560
	ds_read_b32 v232, v212 offset:3072
	ds_read_b32 v233, v212 offset:3584
	ds_read_b32 v234, v212 offset:4096
	ds_read_b32 v235, v212 offset:4608
	ds_read_b32 v236, v212 offset:5120
	ds_read_b32 v237, v212 offset:5632
	ds_read_b32 v238, v212 offset:6144
	ds_read_b32 v239, v212 offset:6656
	ds_read_b32 v240, v212 offset:7168
	ds_read_b32 v241, v212 offset:7680
	s_waitcnt lgkmcnt(0)
	v_max_f32_e32 v226, v226, v226
	v_max_f32_e32 v227, v227, v227
	v_max_f32_e32 v228, v228, v228
	v_max_f32_e32 v229, v229, v229
	v_max_f32_e32 v230, v230, v230
	v_max_f32_e32 v231, v231, v231
	v_max_f32_e32 v232, v232, v232
	v_max_f32_e32 v233, v233, v233
	v_max_f32_e32 v234, v234, v234
	v_max_f32_e32 v235, v235, v235
	v_max_f32_e32 v236, v236, v236
	v_max_f32_e32 v237, v237, v237
	v_max_f32_e32 v238, v238, v238
	v_max_f32_e32 v239, v239, v239
	v_max_f32_e32 v240, v240, v240
	v_max_f32_e32 v241, v241, v241
	v_med3_f32 v226, v226, s62, v95
	v_med3_f32 v227, v227, s62, v95
	v_med3_f32 v228, v228, s62, v95
	v_med3_f32 v229, v229, s62, v95
	v_med3_f32 v230, v230, s62, v95
	v_med3_f32 v231, v231, s62, v95
	v_med3_f32 v232, v232, s62, v95
	v_med3_f32 v233, v233, s62, v95
	v_med3_f32 v234, v234, s62, v95
	v_med3_f32 v235, v235, s62, v95
	v_med3_f32 v236, v236, s62, v95
	v_med3_f32 v237, v237, s62, v95
	v_med3_f32 v238, v238, s62, v95
	v_med3_f32 v239, v239, s62, v95
	v_med3_f32 v240, v240, s62, v95
	v_med3_f32 v241, v241, s62, v95
	v_mov_b32_e32 v242, 0
	v_mov_b32_e32 v243, 0
	v_mov_b32_e32 v244, 0
	v_mov_b32_e32 v245, 0
	v_cvt_pk_fp8_f32 v242, v226, v227
	v_cvt_pk_fp8_f32 v243, v230, v231
	v_cvt_pk_fp8_f32 v244, v234, v235
	v_cvt_pk_fp8_f32 v245, v238, v239
	v_cvt_pk_fp8_f32 v242, v228, v229 op_sel:[0,0,1]
	v_cvt_pk_fp8_f32 v243, v232, v233 op_sel:[0,0,1]
	v_cvt_pk_fp8_f32 v244, v236, v237 op_sel:[0,0,1]
	v_cvt_pk_fp8_f32 v245, v240, v241 op_sel:[0,0,1]
	s_nop 0
	global_store_dwordx4 v77, v[242:245], s[6:7]
	ds_read_b32 v226, v214
	ds_read_b32 v227, v214 offset:512
	ds_read_b32 v228, v214 offset:1024
	ds_read_b32 v229, v214 offset:1536
	ds_read_b32 v230, v214 offset:2048
	ds_read_b32 v231, v214 offset:2560
	ds_read_b32 v232, v214 offset:3072
	ds_read_b32 v233, v214 offset:3584
	ds_read_b32 v234, v214 offset:4096
	ds_read_b32 v235, v214 offset:4608
	ds_read_b32 v236, v214 offset:5120
	ds_read_b32 v237, v214 offset:5632
	ds_read_b32 v238, v214 offset:6144
	ds_read_b32 v239, v214 offset:6656
	ds_read_b32 v240, v214 offset:7168
	ds_read_b32 v241, v214 offset:7680
	s_waitcnt lgkmcnt(0)
	v_max_f32_e32 v226, v226, v226
	v_max_f32_e32 v227, v227, v227
	v_max_f32_e32 v228, v228, v228
	v_max_f32_e32 v229, v229, v229
	v_max_f32_e32 v230, v230, v230
	v_max_f32_e32 v231, v231, v231
	v_max_f32_e32 v232, v232, v232
	v_max_f32_e32 v233, v233, v233
	v_max_f32_e32 v234, v234, v234
	v_max_f32_e32 v235, v235, v235
	v_max_f32_e32 v236, v236, v236
	v_max_f32_e32 v237, v237, v237
	v_max_f32_e32 v238, v238, v238
	v_max_f32_e32 v239, v239, v239
	v_max_f32_e32 v240, v240, v240
	v_max_f32_e32 v241, v241, v241
	v_med3_f32 v226, v226, s62, v95
	v_med3_f32 v227, v227, s62, v95
	v_med3_f32 v228, v228, s62, v95
	v_med3_f32 v229, v229, s62, v95
	v_med3_f32 v230, v230, s62, v95
	v_med3_f32 v231, v231, s62, v95
	v_med3_f32 v232, v232, s62, v95
	v_med3_f32 v233, v233, s62, v95
	v_med3_f32 v234, v234, s62, v95
	v_med3_f32 v235, v235, s62, v95
	v_med3_f32 v236, v236, s62, v95
	v_med3_f32 v237, v237, s62, v95
	v_med3_f32 v238, v238, s62, v95
	v_med3_f32 v239, v239, s62, v95
	v_med3_f32 v240, v240, s62, v95
	v_med3_f32 v241, v241, s62, v95
	v_mov_b32_e32 v242, 0
	v_mov_b32_e32 v243, 0
	v_mov_b32_e32 v244, 0
	v_mov_b32_e32 v245, 0
	v_cvt_pk_fp8_f32 v242, v226, v227
	v_cvt_pk_fp8_f32 v243, v230, v231
	v_cvt_pk_fp8_f32 v244, v234, v235
	v_cvt_pk_fp8_f32 v245, v238, v239
	v_cvt_pk_fp8_f32 v242, v228, v229 op_sel:[0,0,1]
	v_cvt_pk_fp8_f32 v243, v232, v233 op_sel:[0,0,1]
	v_cvt_pk_fp8_f32 v244, v236, v237 op_sel:[0,0,1]
	v_cvt_pk_fp8_f32 v245, v240, v241 op_sel:[0,0,1]
	s_nop 0
	global_store_dwordx4 v78, v[242:245], s[6:7]
	s_waitcnt vmcnt(12)
	v_mul_f32_e32 v144, v26, v144
	v_mul_f32_e32 v145, v26, v145
	v_mul_f32_e32 v146, v26, v146
	v_mul_f32_e32 v147, v26, v147
	ds_write_b128 v209, v[144:147]
	v_mul_f32_e32 v148, v27, v148
	v_mul_f32_e32 v149, v27, v149
	v_mul_f32_e32 v150, v27, v150
	v_mul_f32_e32 v151, v27, v151
	ds_write_b128 v209, v[148:151] offset:1024
	v_mul_f32_e32 v152, v28, v152
	v_mul_f32_e32 v153, v28, v153
	v_mul_f32_e32 v154, v28, v154
	v_mul_f32_e32 v155, v28, v155
	ds_write_b128 v209, v[152:155] offset:2048
	v_mul_f32_e32 v156, v29, v156
	v_mul_f32_e32 v157, v29, v157
	v_mul_f32_e32 v158, v29, v158
	v_mul_f32_e32 v159, v29, v159
	ds_write_b128 v209, v[156:159] offset:3072
	v_mul_f32_e32 v160, v30, v160
	v_mul_f32_e32 v161, v30, v161
	v_mul_f32_e32 v162, v30, v162
	v_mul_f32_e32 v163, v30, v163
	ds_write_b128 v209, v[160:163] offset:4096
	v_mul_f32_e32 v164, v31, v164
	v_mul_f32_e32 v165, v31, v165
	v_mul_f32_e32 v166, v31, v166
	v_mul_f32_e32 v167, v31, v167
	ds_write_b128 v209, v[164:167] offset:5120
	v_mul_f32_e32 v168, v32, v168
	v_mul_f32_e32 v169, v32, v169
	v_mul_f32_e32 v170, v32, v170
	v_mul_f32_e32 v171, v32, v171
	ds_write_b128 v209, v[168:171] offset:6144
	v_mul_f32_e32 v172, v33, v172
	v_mul_f32_e32 v173, v33, v173
	v_mul_f32_e32 v174, v33, v174
	v_mul_f32_e32 v175, v33, v175
	ds_write_b128 v209, v[172:175] offset:7168
	s_waitcnt lgkmcnt(0)
	s_barrier
; #define GAS __attribute__((address_space(1)))
; #define LAS __attribute__((address_space(3)))
; #define LDS_WAIT() asm volatile("s_waitcnt lgkmcnt(0)" ::: "memory")
; __device__ __forceinline__ unsigned pk4_fp8(float a, float b, float c, float d) {
;     a = fminf(fmaxf(a, -448.f), 448.f); b = fminf(fmaxf(b, -448.f), 448.f); c = fminf(fmaxf(c, -448.f), 448.f); d = fminf(fmaxf(d, -448.f), 448.f);
;     int w = __builtin_amdgcn_cvt_pk_fp8_f32(a, b, 0, false); w = __builtin_amdgcn_cvt_pk_fp8_f32(c, d, w, true); return (unsigned)w; }
;     ...
;     for (int i = 0; i < 32; ++i) v[i] = sc >= 0 ? W[(size_t)(k0 + 2 * i + (lane >> 5)) * Nsrc + sc] : 0.f;
; #pragma unroll
;     for (int i = 0; i < 32; ++i) { const int k = k0 + 2 * i + (lane >> 5); float x = v[i] * wscale; if (KS) x *= (k < ksplit ? ksA[k] : ksB[k - ksplit]); scr[(2 * i + (lane >> 5)) * 33 + (lane & 31)] = x; }
;     LDS_WAIT(); asm volatile("" ::: "memory");
;     const int c = lane & 7;
; #pragma unroll
;     for (int j = 0; j < 4; ++j) { const int n = (lane >> 3) + 8 * j; const LAS float* s = scr + (8 * c) * 33 + n;
;         const unsigned long long o = (unsigned long long)pg8::pk4_fp8(s[0 * 33], s[1 * 33], s[2 * 33], s[3 * 33]) | ((unsigned long long)pg8::pk4_fp8(s[4 * 33], s[5 * 33], s[6 * 33], s[7 * 33]) << 32);
;         *(GAS unsigned long long*)(WT + (size_t)(n0 + n) * K + k0 + 8 * c) = o; }
	s_add_u32 s8, s30, 0xa000
	s_addc_u32 s9, s31, 0
	global_load_dwordx4 v[144:147], v74, s[8:9]
	s_add_u32 s8, s8, 0x20000
	s_addc_u32 s9, s9, 0
	global_load_dwordx4 v[148:151], v74, s[8:9]
	s_add_u32 s8, s8, 0x20000
	s_addc_u32 s9, s9, 0
	global_load_dwordx4 v[152:155], v74, s[8:9]
	s_add_u32 s8, s8, 0x20000
	s_addc_u32 s9, s9, 0
	global_load_dwordx4 v[156:159], v74, s[8:9]
	s_add_u32 s8, s8, 0x20000
	s_addc_u32 s9, s9, 0
	global_load_dwordx4 v[160:163], v74, s[8:9]
	s_add_u32 s8, s8, 0x20000
	s_addc_u32 s9, s9, 0
	global_load_dwordx4 v[164:167], v74, s[8:9]
	s_add_u32 s8, s8, 0x20000
	s_addc_u32 s9, s9, 0
	global_load_dwordx4 v[168:171], v74, s[8:9]
	s_add_u32 s8, s8, 0x20000
	s_addc_u32 s9, s9, 0
	global_load_dwordx4 v[172:175], v74, s[8:9]
	s_add_u32 s6, s32, 0x2000000
	s_addc_u32 s7, s33, 0
	ds_read_b32 v226, v211
	ds_read_b32 v227, v211 offset:512
	ds_read_b32 v228, v211 offset:1024
	ds_read_b32 v229, v211 offset:1536
	ds_read_b32 v230, v211 offset:2048
	ds_read_b32 v231, v211 offset:2560
	ds_read_b32 v232, v211 offset:3072
	ds_read_b32 v233, v211 offset:3584
	ds_read_b32 v234, v211 offset:4096
	ds_read_b32 v235, v211 offset:4608
	ds_read_b32 v236, v211 offset:5120
	ds_read_b32 v237, v211 offset:5632
	ds_read_b32 v238, v211 offset:6144
	ds_read_b32 v239, v211 offset:6656
	ds_read_b32 v240, v211 offset:7168
	ds_read_b32 v241, v211 offset:7680
	s_waitcnt lgkmcnt(0)
	v_max_f32_e32 v226, v226, v226
	v_max_f32_e32 v227, v227, v227
	v_max_f32_e32 v228, v228, v228
	v_max_f32_e32 v229, v229, v229
	v_max_f32_e32 v230, v230, v230
	v_max_f32_e32 v231, v231, v231
	v_max_f32_e32 v232, v232, v232
	v_max_f32_e32 v233, v233, v233
	v_max_f32_e32 v234, v234, v234
	v_max_f32_e32 v235, v235, v235
	v_max_f32_e32 v236, v236, v236
	v_max_f32_e32 v237, v237, v237
	v_max_f32_e32 v238, v238, v238
	v_max_f32_e32 v239, v239, v239
	v_max_f32_e32 v240, v240, v240
	v_max_f32_e32 v241, v241, v241
	v_med3_f32 v226, v226, s62, v95
	v_med3_f32 v227, v227, s62, v95
	v_med3_f32 v228, v228, s62, v95
	v_med3_f32 v229, v229, s62, v95
	v_med3_f32 v230, v230, s62, v95
	v_med3_f32 v231, v231, s62, v95
	v_med3_f32 v232, v232, s62, v95
	v_med3_f32 v233, v233, s62, v95
	v_med3_f32 v234, v234, s62, v95
	v_med3_f32 v235, v235, s62, v95
	v_med3_f32 v236, v236, s62, v95
	v_med3_f32 v237, v237, s62, v95
	v_med3_f32 v238, v238, s62, v95
	v_med3_f32 v239, v239, s62, v95
	v_med3_f32 v240, v240, s62, v95
	v_med3_f32 v241, v241, s62, v95
	v_mov_b32_e32 v242, 0
	v_mov_b32_e32 v243, 0
	v_mov_b32_e32 v244, 0
	v_mov_b32_e32 v245, 0
	v_cvt_pk_fp8_f32 v242, v226, v227
	v_cvt_pk_fp8_f32 v243, v230, v231
	v_cvt_pk_fp8_f32 v244, v234, v235
	v_cvt_pk_fp8_f32 v245, v238, v239
	v_cvt_pk_fp8_f32 v242, v228, v229 op_sel:[0,0,1]
	v_cvt_pk_fp8_f32 v243, v232, v233 op_sel:[0,0,1]
	v_cvt_pk_fp8_f32 v244, v236, v237 op_sel:[0,0,1]
	v_cvt_pk_fp8_f32 v245, v240, v241 op_sel:[0,0,1]
	s_nop 0
	global_store_dwordx4 v77, v[242:245], s[6:7]
	ds_read_b32 v226, v213
	ds_read_b32 v227, v213 offset:512
	ds_read_b32 v228, v213 offset:1024
	ds_read_b32 v229, v213 offset:1536
	ds_read_b32 v230, v213 offset:2048
	ds_read_b32 v231, v213 offset:2560
	ds_read_b32 v232, v213 offset:3072
	ds_read_b32 v233, v213 offset:3584
	ds_read_b32 v234, v213 offset:4096
	ds_read_b32 v235, v213 offset:4608
	ds_read_b32 v236, v213 offset:5120
	ds_read_b32 v237, v213 offset:5632
	ds_read_b32 v238, v213 offset:6144
	ds_read_b32 v239, v213 offset:6656
	ds_read_b32 v240, v213 offset:7168
	ds_read_b32 v241, v213 offset:7680
	s_waitcnt lgkmcnt(0)
	v_max_f32_e32 v226, v226, v226
	v_max_f32_e32 v227, v227, v227
	v_max_f32_e32 v228, v228, v228
	v_max_f32_e32 v229, v229, v229
	v_max_f32_e32 v230, v230, v230
	v_max_f32_e32 v231, v231, v231
	v_max_f32_e32 v232, v232, v232
	v_max_f32_e32 v233, v233, v233
	v_max_f32_e32 v234, v234, v234
	v_max_f32_e32 v235, v235, v235
	v_max_f32_e32 v236, v236, v236
	v_max_f32_e32 v237, v237, v237
	v_max_f32_e32 v238, v238, v238
	v_max_f32_e32 v239, v239, v239
	v_max_f32_e32 v240, v240, v240
	v_max_f32_e32 v241, v241, v241
	v_med3_f32 v226, v226, s62, v95
	v_med3_f32 v227, v227, s62, v95
	v_med3_f32 v228, v228, s62, v95
	v_med3_f32 v229, v229, s62, v95
	v_med3_f32 v230, v230, s62, v95
	v_med3_f32 v231, v231, s62, v95
	v_med3_f32 v232, v232, s62, v95
	v_med3_f32 v233, v233, s62, v95
	v_med3_f32 v234, v234, s62, v95
	v_med3_f32 v235, v235, s62, v95
	v_med3_f32 v236, v236, s62, v95
	v_med3_f32 v237, v237, s62, v95
	v_med3_f32 v238, v238, s62, v95
	v_med3_f32 v239, v239, s62, v95
	v_med3_f32 v240, v240, s62, v95
	v_med3_f32 v241, v241, s62, v95
	v_mov_b32_e32 v242, 0
	v_mov_b32_e32 v243, 0
	v_mov_b32_e32 v244, 0
	v_mov_b32_e32 v245, 0
	v_cvt_pk_fp8_f32 v242, v226, v227
	v_cvt_pk_fp8_f32 v243, v230, v231
	v_cvt_pk_fp8_f32 v244, v234, v235
	v_cvt_pk_fp8_f32 v245, v238, v239
	v_cvt_pk_fp8_f32 v242, v228, v229 op_sel:[0,0,1]
	v_cvt_pk_fp8_f32 v243, v232, v233 op_sel:[0,0,1]
	v_cvt_pk_fp8_f32 v244, v236, v237 op_sel:[0,0,1]
	v_cvt_pk_fp8_f32 v245, v240, v241 op_sel:[0,0,1]
	s_nop 0
	global_store_dwordx4 v78, v[242:245], s[6:7]
	s_waitcnt vmcnt(12)
	v_mul_f32_e32 v176, v26, v176
	v_mul_f32_e32 v177, v26, v177
	v_mul_f32_e32 v178, v26, v178
	v_mul_f32_e32 v179, v26, v179
	ds_write_b128 v210, v[176:179]
	v_mul_f32_e32 v180, v27, v180
	v_mul_f32_e32 v181, v27, v181
	v_mul_f32_e32 v182, v27, v182
	v_mul_f32_e32 v183, v27, v183
	ds_write_b128 v210, v[180:183] offset:1024
	v_mul_f32_e32 v184, v28, v184
	v_mul_f32_e32 v185, v28, v185
	v_mul_f32_e32 v186, v28, v186
	v_mul_f32_e32 v187, v28, v187
	ds_write_b128 v210, v[184:187] offset:2048
	v_mul_f32_e32 v188, v29, v188
	v_mul_f32_e32 v189, v29, v189
	v_mul_f32_e32 v190, v29, v190
	v_mul_f32_e32 v191, v29, v191
	ds_write_b128 v210, v[188:191] offset:3072
	v_mul_f32_e32 v192, v30, v192
	v_mul_f32_e32 v193, v30, v193
	v_mul_f32_e32 v194, v30, v194
	v_mul_f32_e32 v195, v30, v195
	ds_write_b128 v210, v[192:195] offset:4096
	v_mul_f32_e32 v196, v31, v196
	v_mul_f32_e32 v197, v31, v197
	v_mul_f32_e32 v198, v31, v198
	v_mul_f32_e32 v199, v31, v199
	ds_write_b128 v210, v[196:199] offset:5120
	v_mul_f32_e32 v200, v32, v200
	v_mul_f32_e32 v201, v32, v201
	v_mul_f32_e32 v202, v32, v202
	v_mul_f32_e32 v203, v32, v203
	ds_write_b128 v210, v[200:203] offset:6144
	v_mul_f32_e32 v204, v33, v204
	v_mul_f32_e32 v205, v33, v205
	v_mul_f32_e32 v206, v33, v206
	v_mul_f32_e32 v207, v33, v207
	ds_write_b128 v210, v[204:207] offset:7168
	s_waitcnt lgkmcnt(0)
	s_barrier
; #define GAS __attribute__((address_space(1)))
; #define LAS __attribute__((address_space(3)))
; #define LDS_WAIT() asm volatile("s_waitcnt lgkmcnt(0)" ::: "memory")
; __device__ __forceinline__ unsigned pk4_fp8(float a, float b, float c, float d) {
;     a = fminf(fmaxf(a, -448.f), 448.f); b = fminf(fmaxf(b, -448.f), 448.f); c = fminf(fmaxf(c, -448.f), 448.f); d = fminf(fmaxf(d, -448.f), 448.f);
;     int w = __builtin_amdgcn_cvt_pk_fp8_f32(a, b, 0, false); w = __builtin_amdgcn_cvt_pk_fp8_f32(c, d, w, true); return (unsigned)w; }
;     ...
;     for (int i = 0; i < 32; ++i) v[i] = sc >= 0 ? W[(size_t)(k0 + 2 * i + (lane >> 5)) * Nsrc + sc] : 0.f;
; #pragma unroll
;     for (int i = 0; i < 32; ++i) { const int k = k0 + 2 * i + (lane >> 5); float x = v[i] * wscale; if (KS) x *= (k < ksplit ? ksA[k] : ksB[k - ksplit]); scr[(2 * i + (lane >> 5)) * 33 + (lane & 31)] = x; }
;     LDS_WAIT(); asm volatile("" ::: "memory");
;     const int c = lane & 7;
; #pragma unroll
;     for (int j = 0; j < 4; ++j) { const int n = (lane >> 3) + 8 * j; const LAS float* s = scr + (8 * c) * 33 + n;
;         const unsigned long long o = (unsigned long long)pg8::pk4_fp8(s[0 * 33], s[1 * 33], s[2 * 33], s[3 * 33]) | ((unsigned long long)pg8::pk4_fp8(s[4 * 33], s[5 * 33], s[6 * 33], s[7 * 33]) << 32);
;         *(GAS unsigned long long*)(WT + (size_t)(n0 + n) * K + k0 + 8 * c) = o; }
	s_add_u32 s8, s30, 0xb000
	s_addc_u32 s9, s31, 0
	global_load_dwordx4 v[176:179], v74, s[8:9]
	s_add_u32 s8, s8, 0x20000
	s_addc_u32 s9, s9, 0
	global_load_dwordx4 v[180:183], v74, s[8:9]
	s_add_u32 s8, s8, 0x20000
	s_addc_u32 s9, s9, 0
	global_load_dwordx4 v[184:187], v74, s[8:9]
	s_add_u32 s8, s8, 0x20000
	s_addc_u32 s9, s9, 0
	global_load_dwordx4 v[188:191], v74, s[8:9]
	s_add_u32 s8, s8, 0x20000
	s_addc_u32 s9, s9, 0
	global_load_dwordx4 v[192:195], v74, s[8:9]
	s_add_u32 s8, s8, 0x20000
	s_addc_u32 s9, s9, 0
	global_load_dwordx4 v[196:199], v74, s[8:9]
	s_add_u32 s8, s8, 0x20000
	s_addc_u32 s9, s9, 0
	global_load_dwordx4 v[200:203], v74, s[8:9]
	s_add_u32 s8, s8, 0x20000
	s_addc_u32 s9, s9, 0
	global_load_dwordx4 v[204:207], v74, s[8:9]
	s_add_u32 s6, s32, 0x2400000
	s_addc_u32 s7, s33, 0
	ds_read_b32 v226, v212
	ds_read_b32 v227, v212 offset:512
	ds_read_b32 v228, v212 offset:1024
	ds_read_b32 v229, v212 offset:1536
	ds_read_b32 v230, v212 offset:2048
	ds_read_b32 v231, v212 offset:2560
	ds_read_b32 v232, v212 offset:3072
	ds_read_b32 v233, v212 offset:3584
	ds_read_b32 v234, v212 offset:4096
	ds_read_b32 v235, v212 offset:4608
	ds_read_b32 v236, v212 offset:5120
	ds_read_b32 v237, v212 offset:5632
	ds_read_b32 v238, v212 offset:6144
	ds_read_b32 v239, v212 offset:6656
	ds_read_b32 v240, v212 offset:7168
	ds_read_b32 v241, v212 offset:7680
	s_waitcnt lgkmcnt(0)
	v_max_f32_e32 v226, v226, v226
	v_max_f32_e32 v227, v227, v227
	v_max_f32_e32 v228, v228, v228
	v_max_f32_e32 v229, v229, v229
	v_max_f32_e32 v230, v230, v230
	v_max_f32_e32 v231, v231, v231
	v_max_f32_e32 v232, v232, v232
	v_max_f32_e32 v233, v233, v233
	v_max_f32_e32 v234, v234, v234
	v_max_f32_e32 v235, v235, v235
	v_max_f32_e32 v236, v236, v236
	v_max_f32_e32 v237, v237, v237
	v_max_f32_e32 v238, v238, v238
	v_max_f32_e32 v239, v239, v239
	v_max_f32_e32 v240, v240, v240
	v_max_f32_e32 v241, v241, v241
	v_med3_f32 v226, v226, s62, v95
	v_med3_f32 v227, v227, s62, v95
	v_med3_f32 v228, v228, s62, v95
	v_med3_f32 v229, v229, s62, v95
	v_med3_f32 v230, v230, s62, v95
	v_med3_f32 v231, v231, s62, v95
	v_med3_f32 v232, v232, s62, v95
	v_med3_f32 v233, v233, s62, v95
	v_med3_f32 v234, v234, s62, v95
	v_med3_f32 v235, v235, s62, v95
	v_med3_f32 v236, v236, s62, v95
	v_med3_f32 v237, v237, s62, v95
	v_med3_f32 v238, v238, s62, v95
	v_med3_f32 v239, v239, s62, v95
	v_med3_f32 v240, v240, s62, v95
	v_med3_f32 v241, v241, s62, v95
	v_mov_b32_e32 v242, 0
	v_mov_b32_e32 v243, 0
	v_mov_b32_e32 v244, 0
	v_mov_b32_e32 v245, 0
	v_cvt_pk_fp8_f32 v242, v226, v227
	v_cvt_pk_fp8_f32 v243, v230, v231
	v_cvt_pk_fp8_f32 v244, v234, v235
	v_cvt_pk_fp8_f32 v245, v238, v239
	v_cvt_pk_fp8_f32 v242, v228, v229 op_sel:[0,0,1]
	v_cvt_pk_fp8_f32 v243, v232, v233 op_sel:[0,0,1]
	v_cvt_pk_fp8_f32 v244, v236, v237 op_sel:[0,0,1]
	v_cvt_pk_fp8_f32 v245, v240, v241 op_sel:[0,0,1]
	s_nop 0
	global_store_dwordx4 v77, v[242:245], s[6:7]
	ds_read_b32 v226, v214
	ds_read_b32 v227, v214 offset:512
	ds_read_b32 v228, v214 offset:1024
	ds_read_b32 v229, v214 offset:1536
	ds_read_b32 v230, v214 offset:2048
	ds_read_b32 v231, v214 offset:2560
	ds_read_b32 v232, v214 offset:3072
	ds_read_b32 v233, v214 offset:3584
	ds_read_b32 v234, v214 offset:4096
	ds_read_b32 v235, v214 offset:4608
	ds_read_b32 v236, v214 offset:5120
	ds_read_b32 v237, v214 offset:5632
	ds_read_b32 v238, v214 offset:6144
	ds_read_b32 v239, v214 offset:6656
	ds_read_b32 v240, v214 offset:7168
	ds_read_b32 v241, v214 offset:7680
	s_waitcnt lgkmcnt(0)
	v_max_f32_e32 v226, v226, v226
	v_max_f32_e32 v227, v227, v227
	v_max_f32_e32 v228, v228, v228
	v_max_f32_e32 v229, v229, v229
	v_max_f32_e32 v230, v230, v230
	v_max_f32_e32 v231, v231, v231
	v_max_f32_e32 v232, v232, v232
	v_max_f32_e32 v233, v233, v233
	v_max_f32_e32 v234, v234, v234
	v_max_f32_e32 v235, v235, v235
	v_max_f32_e32 v236, v236, v236
	v_max_f32_e32 v237, v237, v237
	v_max_f32_e32 v238, v238, v238
	v_max_f32_e32 v239, v239, v239
	v_max_f32_e32 v240, v240, v240
	v_max_f32_e32 v241, v241, v241
	v_med3_f32 v226, v226, s62, v95
	v_med3_f32 v227, v227, s62, v95
	v_med3_f32 v228, v228, s62, v95
	v_med3_f32 v229, v229, s62, v95
	v_med3_f32 v230, v230, s62, v95
	v_med3_f32 v231, v231, s62, v95
	v_med3_f32 v232, v232, s62, v95
	v_med3_f32 v233, v233, s62, v95
	v_med3_f32 v234, v234, s62, v95
	v_med3_f32 v235, v235, s62, v95
	v_med3_f32 v236, v236, s62, v95
	v_med3_f32 v237, v237, s62, v95
	v_med3_f32 v238, v238, s62, v95
	v_med3_f32 v239, v239, s62, v95
	v_med3_f32 v240, v240, s62, v95
	v_med3_f32 v241, v241, s62, v95
	v_mov_b32_e32 v242, 0
	v_mov_b32_e32 v243, 0
	v_mov_b32_e32 v244, 0
	v_mov_b32_e32 v245, 0
	v_cvt_pk_fp8_f32 v242, v226, v227
	v_cvt_pk_fp8_f32 v243, v230, v231
	v_cvt_pk_fp8_f32 v244, v234, v235
	v_cvt_pk_fp8_f32 v245, v238, v239
	v_cvt_pk_fp8_f32 v242, v228, v229 op_sel:[0,0,1]
	v_cvt_pk_fp8_f32 v243, v232, v233 op_sel:[0,0,1]
	v_cvt_pk_fp8_f32 v244, v236, v237 op_sel:[0,0,1]
	v_cvt_pk_fp8_f32 v245, v240, v241 op_sel:[0,0,1]
	s_nop 0
	global_store_dwordx4 v78, v[242:245], s[6:7]
	s_waitcnt vmcnt(12)
	v_mul_f32_e32 v144, v26, v144
	v_mul_f32_e32 v145, v26, v145
	v_mul_f32_e32 v146, v26, v146
	v_mul_f32_e32 v147, v26, v147
	ds_write_b128 v209, v[144:147]
	v_mul_f32_e32 v148, v27, v148
	v_mul_f32_e32 v149, v27, v149
	v_mul_f32_e32 v150, v27, v150
	v_mul_f32_e32 v151, v27, v151
	ds_write_b128 v209, v[148:151] offset:1024
	v_mul_f32_e32 v152, v28, v152
	v_mul_f32_e32 v153, v28, v153
	v_mul_f32_e32 v154, v28, v154
	v_mul_f32_e32 v155, v28, v155
	ds_write_b128 v209, v[152:155] offset:2048
	v_mul_f32_e32 v156, v29, v156
	v_mul_f32_e32 v157, v29, v157
	v_mul_f32_e32 v158, v29, v158
	v_mul_f32_e32 v159, v29, v159
	ds_write_b128 v209, v[156:159] offset:3072
	v_mul_f32_e32 v160, v30, v160
	v_mul_f32_e32 v161, v30, v161
	v_mul_f32_e32 v162, v30, v162
	v_mul_f32_e32 v163, v30, v163
	ds_write_b128 v209, v[160:163] offset:4096
	v_mul_f32_e32 v164, v31, v164
	v_mul_f32_e32 v165, v31, v165
	v_mul_f32_e32 v166, v31, v166
	v_mul_f32_e32 v167, v31, v167
	ds_write_b128 v209, v[164:167] offset:5120
	v_mul_f32_e32 v168, v32, v168
	v_mul_f32_e32 v169, v32, v169
	v_mul_f32_e32 v170, v32, v170
	v_mul_f32_e32 v171, v32, v171
	ds_write_b128 v209, v[168:171] offset:6144
	v_mul_f32_e32 v172, v33, v172
	v_mul_f32_e32 v173, v33, v173
	v_mul_f32_e32 v174, v33, v174
	v_mul_f32_e32 v175, v33, v175
	ds_write_b128 v209, v[172:175] offset:7168
	s_waitcnt lgkmcnt(0)
	s_barrier
; #define GAS __attribute__((address_space(1)))
; #define LAS __attribute__((address_space(3)))
; #define LDS_WAIT() asm volatile("s_waitcnt lgkmcnt(0)" ::: "memory")
; __device__ __forceinline__ unsigned pk4_fp8(float a, float b, float c, float d) {
;     a = fminf(fmaxf(a, -448.f), 448.f); b = fminf(fmaxf(b, -448.f), 448.f); c = fminf(fmaxf(c, -448.f), 448.f); d = fminf(fmaxf(d, -448.f), 448.f);
;     int w = __builtin_amdgcn_cvt_pk_fp8_f32(a, b, 0, false); w = __builtin_amdgcn_cvt_pk_fp8_f32(c, d, w, true); return (unsigned)w; }
;     ...
;     for (int i = 0; i < 32; ++i) v[i] = sc >= 0 ? W[(size_t)(k0 + 2 * i + (lane >> 5)) * Nsrc + sc] : 0.f;
; #pragma unroll
;     for (int i = 0; i < 32; ++i) { const int k = k0 + 2 * i + (lane >> 5); float x = v[i] * wscale; if (KS) x *= (k < ksplit ? ksA[k] : ksB[k - ksplit]); scr[(2 * i + (lane >> 5)) * 33 + (lane & 31)] = x; }
;     LDS_WAIT(); asm volatile("" ::: "memory");
;     const int c = lane & 7;
; #pragma unroll
;     for (int j = 0; j < 4; ++j) { const int n = (lane >> 3) + 8 * j; const LAS float* s = scr + (8 * c) * 33 + n;
;         const unsigned long long o = (unsigned long long)pg8::pk4_fp8(s[0 * 33], s[1 * 33], s[2 * 33], s[3 * 33]) | ((unsigned long long)pg8::pk4_fp8(s[4 * 33], s[5 * 33], s[6 * 33], s[7 * 33]) << 32);
;         *(GAS unsigned long long*)(WT + (size_t)(n0 + n) * K + k0 + 8 * c) = o; }
	s_add_u32 s8, s30, 0xc000
	s_addc_u32 s9, s31, 0
	global_load_dwordx4 v[144:147], v74, s[8:9]
	s_add_u32 s8, s8, 0x20000
	s_addc_u32 s9, s9, 0
	global_load_dwordx4 v[148:151], v74, s[8:9]
	s_add_u32 s8, s8, 0x20000
	s_addc_u32 s9, s9, 0
	global_load_dwordx4 v[152:155], v74, s[8:9]
	s_add_u32 s8, s8, 0x20000
	s_addc_u32 s9, s9, 0
	global_load_dwordx4 v[156:159], v74, s[8:9]
	s_add_u32 s8, s8, 0x20000
	s_addc_u32 s9, s9, 0
	global_load_dwordx4 v[160:163], v74, s[8:9]
	s_add_u32 s8, s8, 0x20000
	s_addc_u32 s9, s9, 0
	global_load_dwordx4 v[164:167], v74, s[8:9]
	s_add_u32 s8, s8, 0x20000
	s_addc_u32 s9, s9, 0
	global_load_dwordx4 v[168:171], v74, s[8:9]
	s_add_u32 s8, s8, 0x20000
	s_addc_u32 s9, s9, 0
	global_load_dwordx4 v[172:175], v74, s[8:9]
	s_add_u32 s6, s32, 0x2800000
	s_addc_u32 s7, s33, 0
	ds_read_b32 v226, v211
	ds_read_b32 v227, v211 offset:512
	ds_read_b32 v228, v211 offset:1024
	ds_read_b32 v229, v211 offset:1536
	ds_read_b32 v230, v211 offset:2048
	ds_read_b32 v231, v211 offset:2560
	ds_read_b32 v232, v211 offset:3072
	ds_read_b32 v233, v211 offset:3584
	ds_read_b32 v234, v211 offset:4096
	ds_read_b32 v235, v211 offset:4608
	ds_read_b32 v236, v211 offset:5120
	ds_read_b32 v237, v211 offset:5632
	ds_read_b32 v238, v211 offset:6144
	ds_read_b32 v239, v211 offset:6656
	ds_read_b32 v240, v211 offset:7168
	ds_read_b32 v241, v211 offset:7680
	s_waitcnt lgkmcnt(0)
	v_max_f32_e32 v226, v226, v226
	v_max_f32_e32 v227, v227, v227
	v_max_f32_e32 v228, v228, v228
	v_max_f32_e32 v229, v229, v229
	v_max_f32_e32 v230, v230, v230
	v_max_f32_e32 v231, v231, v231
	v_max_f32_e32 v232, v232, v232
	v_max_f32_e32 v233, v233, v233
	v_max_f32_e32 v234, v234, v234
	v_max_f32_e32 v235, v235, v235
	v_max_f32_e32 v236, v236, v236
	v_max_f32_e32 v237, v237, v237
	v_max_f32_e32 v238, v238, v238
	v_max_f32_e32 v239, v239, v239
	v_max_f32_e32 v240, v240, v240
	v_max_f32_e32 v241, v241, v241
	v_med3_f32 v226, v226, s62, v95
	v_med3_f32 v227, v227, s62, v95
	v_med3_f32 v228, v228, s62, v95
	v_med3_f32 v229, v229, s62, v95
	v_med3_f32 v230, v230, s62, v95
	v_med3_f32 v231, v231, s62, v95
	v_med3_f32 v232, v232, s62, v95
	v_med3_f32 v233, v233, s62, v95
	v_med3_f32 v234, v234, s62, v95
	v_med3_f32 v235, v235, s62, v95
	v_med3_f32 v236, v236, s62, v95
	v_med3_f32 v237, v237, s62, v95
	v_med3_f32 v238, v238, s62, v95
	v_med3_f32 v239, v239, s62, v95
	v_med3_f32 v240, v240, s62, v95
	v_med3_f32 v241, v241, s62, v95
	v_mov_b32_e32 v242, 0
	v_mov_b32_e32 v243, 0
	v_mov_b32_e32 v244, 0
	v_mov_b32_e32 v245, 0
	v_cvt_pk_fp8_f32 v242, v226, v227
	v_cvt_pk_fp8_f32 v243, v230, v231
	v_cvt_pk_fp8_f32 v244, v234, v235
	v_cvt_pk_fp8_f32 v245, v238, v239
	v_cvt_pk_fp8_f32 v242, v228, v229 op_sel:[0,0,1]
	v_cvt_pk_fp8_f32 v243, v232, v233 op_sel:[0,0,1]
	v_cvt_pk_fp8_f32 v244, v236, v237 op_sel:[0,0,1]
	v_cvt_pk_fp8_f32 v245, v240, v241 op_sel:[0,0,1]
	s_nop 0
	global_store_dwordx4 v77, v[242:245], s[6:7]
	ds_read_b32 v226, v213
	ds_read_b32 v227, v213 offset:512
	ds_read_b32 v228, v213 offset:1024
	ds_read_b32 v229, v213 offset:1536
	ds_read_b32 v230, v213 offset:2048
	ds_read_b32 v231, v213 offset:2560
	ds_read_b32 v232, v213 offset:3072
	ds_read_b32 v233, v213 offset:3584
	ds_read_b32 v234, v213 offset:4096
	ds_read_b32 v235, v213 offset:4608
	ds_read_b32 v236, v213 offset:5120
	ds_read_b32 v237, v213 offset:5632
	ds_read_b32 v238, v213 offset:6144
	ds_read_b32 v239, v213 offset:6656
	ds_read_b32 v240, v213 offset:7168
	ds_read_b32 v241, v213 offset:7680
	s_waitcnt lgkmcnt(0)
	v_max_f32_e32 v226, v226, v226
	v_max_f32_e32 v227, v227, v227
	v_max_f32_e32 v228, v228, v228
	v_max_f32_e32 v229, v229, v229
	v_max_f32_e32 v230, v230, v230
	v_max_f32_e32 v231, v231, v231
	v_max_f32_e32 v232, v232, v232
	v_max_f32_e32 v233, v233, v233
	v_max_f32_e32 v234, v234, v234
	v_max_f32_e32 v235, v235, v235
	v_max_f32_e32 v236, v236, v236
	v_max_f32_e32 v237, v237, v237
	v_max_f32_e32 v238, v238, v238
	v_max_f32_e32 v239, v239, v239
	v_max_f32_e32 v240, v240, v240
	v_max_f32_e32 v241, v241, v241
	v_med3_f32 v226, v226, s62, v95
	v_med3_f32 v227, v227, s62, v95
	v_med3_f32 v228, v228, s62, v95
	v_med3_f32 v229, v229, s62, v95
	v_med3_f32 v230, v230, s62, v95
	v_med3_f32 v231, v231, s62, v95
	v_med3_f32 v232, v232, s62, v95
	v_med3_f32 v233, v233, s62, v95
	v_med3_f32 v234, v234, s62, v95
	v_med3_f32 v235, v235, s62, v95
	v_med3_f32 v236, v236, s62, v95
	v_med3_f32 v237, v237, s62, v95
	v_med3_f32 v238, v238, s62, v95
	v_med3_f32 v239, v239, s62, v95
	v_med3_f32 v240, v240, s62, v95
	v_med3_f32 v241, v241, s62, v95
	v_mov_b32_e32 v242, 0
	v_mov_b32_e32 v243, 0
	v_mov_b32_e32 v244, 0
	v_mov_b32_e32 v245, 0
	v_cvt_pk_fp8_f32 v242, v226, v227
	v_cvt_pk_fp8_f32 v243, v230, v231
	v_cvt_pk_fp8_f32 v244, v234, v235
	v_cvt_pk_fp8_f32 v245, v238, v239
	v_cvt_pk_fp8_f32 v242, v228, v229 op_sel:[0,0,1]
	v_cvt_pk_fp8_f32 v243, v232, v233 op_sel:[0,0,1]
	v_cvt_pk_fp8_f32 v244, v236, v237 op_sel:[0,0,1]
	v_cvt_pk_fp8_f32 v245, v240, v241 op_sel:[0,0,1]
	s_nop 0
	global_store_dwordx4 v78, v[242:245], s[6:7]
	s_waitcnt vmcnt(12)
	v_mul_f32_e32 v176, v26, v176
	v_mul_f32_e32 v177, v26, v177
	v_mul_f32_e32 v178, v26, v178
	v_mul_f32_e32 v179, v26, v179
	ds_write_b128 v210, v[176:179]
	v_mul_f32_e32 v180, v27, v180
	v_mul_f32_e32 v181, v27, v181
	v_mul_f32_e32 v182, v27, v182
	v_mul_f32_e32 v183, v27, v183
	ds_write_b128 v210, v[180:183] offset:1024
	v_mul_f32_e32 v184, v28, v184
	v_mul_f32_e32 v185, v28, v185
	v_mul_f32_e32 v186, v28, v186
	v_mul_f32_e32 v187, v28, v187
	ds_write_b128 v210, v[184:187] offset:2048
	v_mul_f32_e32 v188, v29, v188
	v_mul_f32_e32 v189, v29, v189
	v_mul_f32_e32 v190, v29, v190
	v_mul_f32_e32 v191, v29, v191
	ds_write_b128 v210, v[188:191] offset:3072
	v_mul_f32_e32 v192, v30, v192
	v_mul_f32_e32 v193, v30, v193
	v_mul_f32_e32 v194, v30, v194
	v_mul_f32_e32 v195, v30, v195
	ds_write_b128 v210, v[192:195] offset:4096
	v_mul_f32_e32 v196, v31, v196
	v_mul_f32_e32 v197, v31, v197
	v_mul_f32_e32 v198, v31, v198
	v_mul_f32_e32 v199, v31, v199
	ds_write_b128 v210, v[196:199] offset:5120
	v_mul_f32_e32 v200, v32, v200
	v_mul_f32_e32 v201, v32, v201
	v_mul_f32_e32 v202, v32, v202
	v_mul_f32_e32 v203, v32, v203
	ds_write_b128 v210, v[200:203] offset:6144
	v_mul_f32_e32 v204, v33, v204
	v_mul_f32_e32 v205, v33, v205
	v_mul_f32_e32 v206, v33, v206
	v_mul_f32_e32 v207, v33, v207
	ds_write_b128 v210, v[204:207] offset:7168
	s_waitcnt lgkmcnt(0)
	s_barrier
; #define GAS __attribute__((address_space(1)))
; #define LAS __attribute__((address_space(3)))
; #define LDS_WAIT() asm volatile("s_waitcnt lgkmcnt(0)" ::: "memory")
; __device__ __forceinline__ unsigned pk4_fp8(float a, float b, float c, float d) {
;     a = fminf(fmaxf(a, -448.f), 448.f); b = fminf(fmaxf(b, -448.f), 448.f); c = fminf(fmaxf(c, -448.f), 448.f); d = fminf(fmaxf(d, -448.f), 448.f);
;     int w = __builtin_amdgcn_cvt_pk_fp8_f32(a, b, 0, false); w = __builtin_amdgcn_cvt_pk_fp8_f32(c, d, w, true); return (unsigned)w; }
;     ...
;     for (int i = 0; i < 32; ++i) v[i] = sc >= 0 ? W[(size_t)(k0 + 2 * i + (lane >> 5)) * Nsrc + sc] : 0.f;
; #pragma unroll
;     for (int i = 0; i < 32; ++i) { const int k = k0 + 2 * i + (lane >> 5); float x = v[i] * wscale; if (KS) x *= (k < ksplit ? ksA[k] : ksB[k - ksplit]); scr[(2 * i + (lane >> 5)) * 33 + (lane & 31)] = x; }
;     LDS_WAIT(); asm volatile("" ::: "memory");
;     const int c = lane & 7;
; #pragma unroll
;     for (int j = 0; j < 4; ++j) { const int n = (lane >> 3) + 8 * j; const LAS float* s = scr + (8 * c) * 33 + n;
;         const unsigned long long o = (unsigned long long)pg8::pk4_fp8(s[0 * 33], s[1 * 33], s[2 * 33], s[3 * 33]) | ((unsigned long long)pg8::pk4_fp8(s[4 * 33], s[5 * 33], s[6 * 33], s[7 * 33]) << 32);
;         *(GAS unsigned long long*)(WT + (size_t)(n0 + n) * K + k0 + 8 * c) = o; }
	s_add_u32 s8, s30, 0xd000
	s_addc_u32 s9, s31, 0
	global_load_dwordx4 v[176:179], v74, s[8:9]
	s_add_u32 s8, s8, 0x20000
	s_addc_u32 s9, s9, 0
	global_load_dwordx4 v[180:183], v74, s[8:9]
	s_add_u32 s8, s8, 0x20000
	s_addc_u32 s9, s9, 0
	global_load_dwordx4 v[184:187], v74, s[8:9]
	s_add_u32 s8, s8, 0x20000
	s_addc_u32 s9, s9, 0
	global_load_dwordx4 v[188:191], v74, s[8:9]
	s_add_u32 s8, s8, 0x20000
	s_addc_u32 s9, s9, 0
	global_load_dwordx4 v[192:195], v74, s[8:9]
	s_add_u32 s8, s8, 0x20000
	s_addc_u32 s9, s9, 0
	global_load_dwordx4 v[196:199], v74, s[8:9]
	s_add_u32 s8, s8, 0x20000
	s_addc_u32 s9, s9, 0
	global_load_dwordx4 v[200:203], v74, s[8:9]
	s_add_u32 s8, s8, 0x20000
	s_addc_u32 s9, s9, 0
	global_load_dwordx4 v[204:207], v74, s[8:9]
	s_add_u32 s6, s32, 0x2c00000
	s_addc_u32 s7, s33, 0
	ds_read_b32 v226, v212
	ds_read_b32 v227, v212 offset:512
	ds_read_b32 v228, v212 offset:1024
	ds_read_b32 v229, v212 offset:1536
	ds_read_b32 v230, v212 offset:2048
	ds_read_b32 v231, v212 offset:2560
	ds_read_b32 v232, v212 offset:3072
	ds_read_b32 v233, v212 offset:3584
	ds_read_b32 v234, v212 offset:4096
	ds_read_b32 v235, v212 offset:4608
	ds_read_b32 v236, v212 offset:5120
	ds_read_b32 v237, v212 offset:5632
	ds_read_b32 v238, v212 offset:6144
	ds_read_b32 v239, v212 offset:6656
	ds_read_b32 v240, v212 offset:7168
	ds_read_b32 v241, v212 offset:7680
	s_waitcnt lgkmcnt(0)
	v_max_f32_e32 v226, v226, v226
	v_max_f32_e32 v227, v227, v227
	v_max_f32_e32 v228, v228, v228
	v_max_f32_e32 v229, v229, v229
	v_max_f32_e32 v230, v230, v230
	v_max_f32_e32 v231, v231, v231
	v_max_f32_e32 v232, v232, v232
	v_max_f32_e32 v233, v233, v233
	v_max_f32_e32 v234, v234, v234
	v_max_f32_e32 v235, v235, v235
	v_max_f32_e32 v236, v236, v236
	v_max_f32_e32 v237, v237, v237
	v_max_f32_e32 v238, v238, v238
	v_max_f32_e32 v239, v239, v239
	v_max_f32_e32 v240, v240, v240
	v_max_f32_e32 v241, v241, v241
	v_med3_f32 v226, v226, s62, v95
	v_med3_f32 v227, v227, s62, v95
	v_med3_f32 v228, v228, s62, v95
	v_med3_f32 v229, v229, s62, v95
	v_med3_f32 v230, v230, s62, v95
	v_med3_f32 v231, v231, s62, v95
	v_med3_f32 v232, v232, s62, v95
	v_med3_f32 v233, v233, s62, v95
	v_med3_f32 v234, v234, s62, v95
	v_med3_f32 v235, v235, s62, v95
	v_med3_f32 v236, v236, s62, v95
	v_med3_f32 v237, v237, s62, v95
	v_med3_f32 v238, v238, s62, v95
	v_med3_f32 v239, v239, s62, v95
	v_med3_f32 v240, v240, s62, v95
	v_med3_f32 v241, v241, s62, v95
	v_mov_b32_e32 v242, 0
	v_mov_b32_e32 v243, 0
	v_mov_b32_e32 v244, 0
	v_mov_b32_e32 v245, 0
	v_cvt_pk_fp8_f32 v242, v226, v227
	v_cvt_pk_fp8_f32 v243, v230, v231
	v_cvt_pk_fp8_f32 v244, v234, v235
	v_cvt_pk_fp8_f32 v245, v238, v239
	v_cvt_pk_fp8_f32 v242, v228, v229 op_sel:[0,0,1]
	v_cvt_pk_fp8_f32 v243, v232, v233 op_sel:[0,0,1]
	v_cvt_pk_fp8_f32 v244, v236, v237 op_sel:[0,0,1]
	v_cvt_pk_fp8_f32 v245, v240, v241 op_sel:[0,0,1]
	s_nop 0
	global_store_dwordx4 v77, v[242:245], s[6:7]
	ds_read_b32 v226, v214
	ds_read_b32 v227, v214 offset:512
	ds_read_b32 v228, v214 offset:1024
	ds_read_b32 v229, v214 offset:1536
	ds_read_b32 v230, v214 offset:2048
	ds_read_b32 v231, v214 offset:2560
	ds_read_b32 v232, v214 offset:3072
	ds_read_b32 v233, v214 offset:3584
	ds_read_b32 v234, v214 offset:4096
	ds_read_b32 v235, v214 offset:4608
	ds_read_b32 v236, v214 offset:5120
	ds_read_b32 v237, v214 offset:5632
	ds_read_b32 v238, v214 offset:6144
	ds_read_b32 v239, v214 offset:6656
	ds_read_b32 v240, v214 offset:7168
	ds_read_b32 v241, v214 offset:7680
	s_waitcnt lgkmcnt(0)
	v_max_f32_e32 v226, v226, v226
	v_max_f32_e32 v227, v227, v227
	v_max_f32_e32 v228, v228, v228
	v_max_f32_e32 v229, v229, v229
	v_max_f32_e32 v230, v230, v230
	v_max_f32_e32 v231, v231, v231
	v_max_f32_e32 v232, v232, v232
	v_max_f32_e32 v233, v233, v233
	v_max_f32_e32 v234, v234, v234
	v_max_f32_e32 v235, v235, v235
	v_max_f32_e32 v236, v236, v236
	v_max_f32_e32 v237, v237, v237
	v_max_f32_e32 v238, v238, v238
	v_max_f32_e32 v239, v239, v239
	v_max_f32_e32 v240, v240, v240
	v_max_f32_e32 v241, v241, v241
	v_med3_f32 v226, v226, s62, v95
	v_med3_f32 v227, v227, s62, v95
	v_med3_f32 v228, v228, s62, v95
	v_med3_f32 v229, v229, s62, v95
	v_med3_f32 v230, v230, s62, v95
	v_med3_f32 v231, v231, s62, v95
	v_med3_f32 v232, v232, s62, v95
	v_med3_f32 v233, v233, s62, v95
	v_med3_f32 v234, v234, s62, v95
	v_med3_f32 v235, v235, s62, v95
	v_med3_f32 v236, v236, s62, v95
	v_med3_f32 v237, v237, s62, v95
	v_med3_f32 v238, v238, s62, v95
	v_med3_f32 v239, v239, s62, v95
	v_med3_f32 v240, v240, s62, v95
	v_med3_f32 v241, v241, s62, v95
	v_mov_b32_e32 v242, 0
	v_mov_b32_e32 v243, 0
	v_mov_b32_e32 v244, 0
	v_mov_b32_e32 v245, 0
	v_cvt_pk_fp8_f32 v242, v226, v227
	v_cvt_pk_fp8_f32 v243, v230, v231
	v_cvt_pk_fp8_f32 v244, v234, v235
	v_cvt_pk_fp8_f32 v245, v238, v239
	v_cvt_pk_fp8_f32 v242, v228, v229 op_sel:[0,0,1]
	v_cvt_pk_fp8_f32 v243, v232, v233 op_sel:[0,0,1]
	v_cvt_pk_fp8_f32 v244, v236, v237 op_sel:[0,0,1]
	v_cvt_pk_fp8_f32 v245, v240, v241 op_sel:[0,0,1]
	s_nop 0
	global_store_dwordx4 v78, v[242:245], s[6:7]
	s_waitcnt vmcnt(12)
	v_mul_f32_e32 v144, v26, v144
	v_mul_f32_e32 v145, v26, v145
	v_mul_f32_e32 v146, v26, v146
	v_mul_f32_e32 v147, v26, v147
	ds_write_b128 v209, v[144:147]
	v_mul_f32_e32 v148, v27, v148
	v_mul_f32_e32 v149, v27, v149
	v_mul_f32_e32 v150, v27, v150
	v_mul_f32_e32 v151, v27, v151
	ds_write_b128 v209, v[148:151] offset:1024
	v_mul_f32_e32 v152, v28, v152
	v_mul_f32_e32 v153, v28, v153
	v_mul_f32_e32 v154, v28, v154
	v_mul_f32_e32 v155, v28, v155
	ds_write_b128 v209, v[152:155] offset:2048
	v_mul_f32_e32 v156, v29, v156
	v_mul_f32_e32 v157, v29, v157
	v_mul_f32_e32 v158, v29, v158
	v_mul_f32_e32 v159, v29, v159
	ds_write_b128 v209, v[156:159] offset:3072
	v_mul_f32_e32 v160, v30, v160
	v_mul_f32_e32 v161, v30, v161
	v_mul_f32_e32 v162, v30, v162
	v_mul_f32_e32 v163, v30, v163
	ds_write_b128 v209, v[160:163] offset:4096
	v_mul_f32_e32 v164, v31, v164
	v_mul_f32_e32 v165, v31, v165
	v_mul_f32_e32 v166, v31, v166
	v_mul_f32_e32 v167, v31, v167
	ds_write_b128 v209, v[164:167] offset:5120
	v_mul_f32_e32 v168, v32, v168
	v_mul_f32_e32 v169, v32, v169
	v_mul_f32_e32 v170, v32, v170
	v_mul_f32_e32 v171, v32, v171
	ds_write_b128 v209, v[168:171] offset:6144
	v_mul_f32_e32 v172, v33, v172
	v_mul_f32_e32 v173, v33, v173
	v_mul_f32_e32 v174, v33, v174
	v_mul_f32_e32 v175, v33, v175
	ds_write_b128 v209, v[172:175] offset:7168
	s_waitcnt lgkmcnt(0)
	s_barrier
; #define GAS __attribute__((address_space(1)))
; #define LAS __attribute__((address_space(3)))
; #define LDS_WAIT() asm volatile("s_waitcnt lgkmcnt(0)" ::: "memory")
; __device__ __forceinline__ unsigned pk4_fp8(float a, float b, float c, float d) {
;     a = fminf(fmaxf(a, -448.f), 448.f); b = fminf(fmaxf(b, -448.f), 448.f); c = fminf(fmaxf(c, -448.f), 448.f); d = fminf(fmaxf(d, -448.f), 448.f);
;     int w = __builtin_amdgcn_cvt_pk_fp8_f32(a, b, 0, false); w = __builtin_amdgcn_cvt_pk_fp8_f32(c, d, w, true); return (unsigned)w; }
;     ...
;     for (int i = 0; i < 32; ++i) v[i] = sc >= 0 ? W[(size_t)(k0 + 2 * i + (lane >> 5)) * Nsrc + sc] : 0.f;
; #pragma unroll
;     for (int i = 0; i < 32; ++i) { const int k = k0 + 2 * i + (lane >> 5); float x = v[i] * wscale; if (KS) x *= (k < ksplit ? ksA[k] : ksB[k - ksplit]); scr[(2 * i + (lane >> 5)) * 33 + (lane & 31)] = x; }
;     LDS_WAIT(); asm volatile("" ::: "memory");
;     const int c = lane & 7;
; #pragma unroll
;     for (int j = 0; j < 4; ++j) { const int n = (lane >> 3) + 8 * j; const LAS float* s = scr + (8 * c) * 33 + n;
;         const unsigned long long o = (unsigned long long)pg8::pk4_fp8(s[0 * 33], s[1 * 33], s[2 * 33], s[3 * 33]) | ((unsigned long long)pg8::pk4_fp8(s[4 * 33], s[5 * 33], s[6 * 33], s[7 * 33]) << 32);
;         *(GAS unsigned long long*)(WT + (size_t)(n0 + n) * K + k0 + 8 * c) = o; }
	s_add_u32 s8, s30, 0xe000
	s_addc_u32 s9, s31, 0
	global_load_dwordx4 v[144:147], v74, s[8:9]
	s_add_u32 s8, s8, 0x20000
	s_addc_u32 s9, s9, 0
	global_load_dwordx4 v[148:151], v74, s[8:9]
	s_add_u32 s8, s8, 0x20000
	s_addc_u32 s9, s9, 0
	global_load_dwordx4 v[152:155], v74, s[8:9]
	s_add_u32 s8, s8, 0x20000
	s_addc_u32 s9, s9, 0
	global_load_dwordx4 v[156:159], v74, s[8:9]
	s_add_u32 s8, s8, 0x20000
	s_addc_u32 s9, s9, 0
	global_load_dwordx4 v[160:163], v74, s[8:9]
	s_add_u32 s8, s8, 0x20000
	s_addc_u32 s9, s9, 0
	global_load_dwordx4 v[164:167], v74, s[8:9]
	s_add_u32 s8, s8, 0x20000
	s_addc_u32 s9, s9, 0
	global_load_dwordx4 v[168:171], v74, s[8:9]
	s_add_u32 s8, s8, 0x20000
	s_addc_u32 s9, s9, 0
	global_load_dwordx4 v[172:175], v74, s[8:9]
	s_add_u32 s6, s32, 0x3000000
	s_addc_u32 s7, s33, 0
	ds_read_b32 v226, v211
	ds_read_b32 v227, v211 offset:512
	ds_read_b32 v228, v211 offset:1024
	ds_read_b32 v229, v211 offset:1536
	ds_read_b32 v230, v211 offset:2048
	ds_read_b32 v231, v211 offset:2560
	ds_read_b32 v232, v211 offset:3072
	ds_read_b32 v233, v211 offset:3584
	ds_read_b32 v234, v211 offset:4096
	ds_read_b32 v235, v211 offset:4608
	ds_read_b32 v236, v211 offset:5120
	ds_read_b32 v237, v211 offset:5632
	ds_read_b32 v238, v211 offset:6144
	ds_read_b32 v239, v211 offset:6656
	ds_read_b32 v240, v211 offset:7168
	ds_read_b32 v241, v211 offset:7680
	s_waitcnt lgkmcnt(0)
	v_max_f32_e32 v226, v226, v226
	v_max_f32_e32 v227, v227, v227
	v_max_f32_e32 v228, v228, v228
	v_max_f32_e32 v229, v229, v229
	v_max_f32_e32 v230, v230, v230
	v_max_f32_e32 v231, v231, v231
	v_max_f32_e32 v232, v232, v232
	v_max_f32_e32 v233, v233, v233
	v_max_f32_e32 v234, v234, v234
	v_max_f32_e32 v235, v235, v235
	v_max_f32_e32 v236, v236, v236
	v_max_f32_e32 v237, v237, v237
	v_max_f32_e32 v238, v238, v238
	v_max_f32_e32 v239, v239, v239
	v_max_f32_e32 v240, v240, v240
	v_max_f32_e32 v241, v241, v241
	v_med3_f32 v226, v226, s62, v95
	v_med3_f32 v227, v227, s62, v95
	v_med3_f32 v228, v228, s62, v95
	v_med3_f32 v229, v229, s62, v95
	v_med3_f32 v230, v230, s62, v95
	v_med3_f32 v231, v231, s62, v95
	v_med3_f32 v232, v232, s62, v95
	v_med3_f32 v233, v233, s62, v95
	v_med3_f32 v234, v234, s62, v95
	v_med3_f32 v235, v235, s62, v95
	v_med3_f32 v236, v236, s62, v95
	v_med3_f32 v237, v237, s62, v95
	v_med3_f32 v238, v238, s62, v95
	v_med3_f32 v239, v239, s62, v95
	v_med3_f32 v240, v240, s62, v95
	v_med3_f32 v241, v241, s62, v95
	v_mov_b32_e32 v242, 0
	v_mov_b32_e32 v243, 0
	v_mov_b32_e32 v244, 0
	v_mov_b32_e32 v245, 0
	v_cvt_pk_fp8_f32 v242, v226, v227
	v_cvt_pk_fp8_f32 v243, v230, v231
	v_cvt_pk_fp8_f32 v244, v234, v235
	v_cvt_pk_fp8_f32 v245, v238, v239
	v_cvt_pk_fp8_f32 v242, v228, v229 op_sel:[0,0,1]
	v_cvt_pk_fp8_f32 v243, v232, v233 op_sel:[0,0,1]
	v_cvt_pk_fp8_f32 v244, v236, v237 op_sel:[0,0,1]
	v_cvt_pk_fp8_f32 v245, v240, v241 op_sel:[0,0,1]
	s_nop 0
	global_store_dwordx4 v77, v[242:245], s[6:7]
	ds_read_b32 v226, v213
	ds_read_b32 v227, v213 offset:512
	ds_read_b32 v228, v213 offset:1024
	ds_read_b32 v229, v213 offset:1536
	ds_read_b32 v230, v213 offset:2048
	ds_read_b32 v231, v213 offset:2560
	ds_read_b32 v232, v213 offset:3072
	ds_read_b32 v233, v213 offset:3584
	ds_read_b32 v234, v213 offset:4096
	ds_read_b32 v235, v213 offset:4608
	ds_read_b32 v236, v213 offset:5120
	ds_read_b32 v237, v213 offset:5632
	ds_read_b32 v238, v213 offset:6144
	ds_read_b32 v239, v213 offset:6656
	ds_read_b32 v240, v213 offset:7168
	ds_read_b32 v241, v213 offset:7680
	s_waitcnt lgkmcnt(0)
	v_max_f32_e32 v226, v226, v226
	v_max_f32_e32 v227, v227, v227
	v_max_f32_e32 v228, v228, v228
	v_max_f32_e32 v229, v229, v229
	v_max_f32_e32 v230, v230, v230
	v_max_f32_e32 v231, v231, v231
	v_max_f32_e32 v232, v232, v232
	v_max_f32_e32 v233, v233, v233
	v_max_f32_e32 v234, v234, v234
	v_max_f32_e32 v235, v235, v235
	v_max_f32_e32 v236, v236, v236
	v_max_f32_e32 v237, v237, v237
	v_max_f32_e32 v238, v238, v238
	v_max_f32_e32 v239, v239, v239
	v_max_f32_e32 v240, v240, v240
	v_max_f32_e32 v241, v241, v241
	v_med3_f32 v226, v226, s62, v95
	v_med3_f32 v227, v227, s62, v95
	v_med3_f32 v228, v228, s62, v95
	v_med3_f32 v229, v229, s62, v95
	v_med3_f32 v230, v230, s62, v95
	v_med3_f32 v231, v231, s62, v95
	v_med3_f32 v232, v232, s62, v95
	v_med3_f32 v233, v233, s62, v95
	v_med3_f32 v234, v234, s62, v95
	v_med3_f32 v235, v235, s62, v95
	v_med3_f32 v236, v236, s62, v95
	v_med3_f32 v237, v237, s62, v95
	v_med3_f32 v238, v238, s62, v95
	v_med3_f32 v239, v239, s62, v95
	v_med3_f32 v240, v240, s62, v95
	v_med3_f32 v241, v241, s62, v95
	v_mov_b32_e32 v242, 0
	v_mov_b32_e32 v243, 0
	v_mov_b32_e32 v244, 0
	v_mov_b32_e32 v245, 0
	v_cvt_pk_fp8_f32 v242, v226, v227
	v_cvt_pk_fp8_f32 v243, v230, v231
	v_cvt_pk_fp8_f32 v244, v234, v235
	v_cvt_pk_fp8_f32 v245, v238, v239
	v_cvt_pk_fp8_f32 v242, v228, v229 op_sel:[0,0,1]
	v_cvt_pk_fp8_f32 v243, v232, v233 op_sel:[0,0,1]
	v_cvt_pk_fp8_f32 v244, v236, v237 op_sel:[0,0,1]
	v_cvt_pk_fp8_f32 v245, v240, v241 op_sel:[0,0,1]
	s_nop 0
	global_store_dwordx4 v78, v[242:245], s[6:7]
	s_waitcnt vmcnt(12)
	v_mul_f32_e32 v176, v26, v176
	v_mul_f32_e32 v177, v26, v177
	v_mul_f32_e32 v178, v26, v178
	v_mul_f32_e32 v179, v26, v179
	ds_write_b128 v210, v[176:179]
	v_mul_f32_e32 v180, v27, v180
	v_mul_f32_e32 v181, v27, v181
	v_mul_f32_e32 v182, v27, v182
	v_mul_f32_e32 v183, v27, v183
	ds_write_b128 v210, v[180:183] offset:1024
	v_mul_f32_e32 v184, v28, v184
	v_mul_f32_e32 v185, v28, v185
	v_mul_f32_e32 v186, v28, v186
	v_mul_f32_e32 v187, v28, v187
	ds_write_b128 v210, v[184:187] offset:2048
	v_mul_f32_e32 v188, v29, v188
	v_mul_f32_e32 v189, v29, v189
	v_mul_f32_e32 v190, v29, v190
	v_mul_f32_e32 v191, v29, v191
	ds_write_b128 v210, v[188:191] offset:3072
	v_mul_f32_e32 v192, v30, v192
	v_mul_f32_e32 v193, v30, v193
	v_mul_f32_e32 v194, v30, v194
	v_mul_f32_e32 v195, v30, v195
	ds_write_b128 v210, v[192:195] offset:4096
	v_mul_f32_e32 v196, v31, v196
	v_mul_f32_e32 v197, v31, v197
	v_mul_f32_e32 v198, v31, v198
	v_mul_f32_e32 v199, v31, v199
	ds_write_b128 v210, v[196:199] offset:5120
	v_mul_f32_e32 v200, v32, v200
	v_mul_f32_e32 v201, v32, v201
	v_mul_f32_e32 v202, v32, v202
	v_mul_f32_e32 v203, v32, v203
	ds_write_b128 v210, v[200:203] offset:6144
	v_mul_f32_e32 v204, v33, v204
	v_mul_f32_e32 v205, v33, v205
	v_mul_f32_e32 v206, v33, v206
	v_mul_f32_e32 v207, v33, v207
	ds_write_b128 v210, v[204:207] offset:7168
	s_waitcnt lgkmcnt(0)
	s_barrier
; #define GAS __attribute__((address_space(1)))
; #define LAS __attribute__((address_space(3)))
; #define LDS_WAIT() asm volatile("s_waitcnt lgkmcnt(0)" ::: "memory")
; __device__ __forceinline__ unsigned pk4_fp8(float a, float b, float c, float d) {
;     a = fminf(fmaxf(a, -448.f), 448.f); b = fminf(fmaxf(b, -448.f), 448.f); c = fminf(fmaxf(c, -448.f), 448.f); d = fminf(fmaxf(d, -448.f), 448.f);
;     int w = __builtin_amdgcn_cvt_pk_fp8_f32(a, b, 0, false); w = __builtin_amdgcn_cvt_pk_fp8_f32(c, d, w, true); return (unsigned)w; }
;     ...
;     for (int i = 0; i < 32; ++i) v[i] = sc >= 0 ? W[(size_t)(k0 + 2 * i + (lane >> 5)) * Nsrc + sc] : 0.f;
; #pragma unroll
;     for (int i = 0; i < 32; ++i) { const int k = k0 + 2 * i + (lane >> 5); float x = v[i] * wscale; if (KS) x *= (k < ksplit ? ksA[k] : ksB[k - ksplit]); scr[(2 * i + (lane >> 5)) * 33 + (lane & 31)] = x; }
;     LDS_WAIT(); asm volatile("" ::: "memory");
;     const int c = lane & 7;
; #pragma unroll
;     for (int j = 0; j < 4; ++j) { const int n = (lane >> 3) + 8 * j; const LAS float* s = scr + (8 * c) * 33 + n;
;         const unsigned long long o = (unsigned long long)pg8::pk4_fp8(s[0 * 33], s[1 * 33], s[2 * 33], s[3 * 33]) | ((unsigned long long)pg8::pk4_fp8(s[4 * 33], s[5 * 33], s[6 * 33], s[7 * 33]) << 32);
;         *(GAS unsigned long long*)(WT + (size_t)(n0 + n) * K + k0 + 8 * c) = o; }
	s_add_u32 s8, s30, 0xf000
	s_addc_u32 s9, s31, 0
	global_load_dwordx4 v[176:179], v74, s[8:9]
	s_add_u32 s8, s8, 0x20000
	s_addc_u32 s9, s9, 0
	global_load_dwordx4 v[180:183], v74, s[8:9]
	s_add_u32 s8, s8, 0x20000
	s_addc_u32 s9, s9, 0
	global_load_dwordx4 v[184:187], v74, s[8:9]
	s_add_u32 s8, s8, 0x20000
	s_addc_u32 s9, s9, 0
	global_load_dwordx4 v[188:191], v74, s[8:9]
	s_add_u32 s8, s8, 0x20000
	s_addc_u32 s9, s9, 0
	global_load_dwordx4 v[192:195], v74, s[8:9]
	s_add_u32 s8, s8, 0x20000
	s_addc_u32 s9, s9, 0
	global_load_dwordx4 v[196:199], v74, s[8:9]
	s_add_u32 s8, s8, 0x20000
	s_addc_u32 s9, s9, 0
	global_load_dwordx4 v[200:203], v74, s[8:9]
	s_add_u32 s8, s8, 0x20000
	s_addc_u32 s9, s9, 0
	global_load_dwordx4 v[204:207], v74, s[8:9]
	s_add_u32 s6, s32, 0x3400000
	s_addc_u32 s7, s33, 0
	ds_read_b32 v226, v212
	ds_read_b32 v227, v212 offset:512
	ds_read_b32 v228, v212 offset:1024
	ds_read_b32 v229, v212 offset:1536
	ds_read_b32 v230, v212 offset:2048
	ds_read_b32 v231, v212 offset:2560
	ds_read_b32 v232, v212 offset:3072
	ds_read_b32 v233, v212 offset:3584
	ds_read_b32 v234, v212 offset:4096
	ds_read_b32 v235, v212 offset:4608
	ds_read_b32 v236, v212 offset:5120
	ds_read_b32 v237, v212 offset:5632
	ds_read_b32 v238, v212 offset:6144
	ds_read_b32 v239, v212 offset:6656
	ds_read_b32 v240, v212 offset:7168
	ds_read_b32 v241, v212 offset:7680
	s_waitcnt lgkmcnt(0)
	v_max_f32_e32 v226, v226, v226
	v_max_f32_e32 v227, v227, v227
	v_max_f32_e32 v228, v228, v228
	v_max_f32_e32 v229, v229, v229
	v_max_f32_e32 v230, v230, v230
	v_max_f32_e32 v231, v231, v231
	v_max_f32_e32 v232, v232, v232
	v_max_f32_e32 v233, v233, v233
	v_max_f32_e32 v234, v234, v234
	v_max_f32_e32 v235, v235, v235
	v_max_f32_e32 v236, v236, v236
	v_max_f32_e32 v237, v237, v237
	v_max_f32_e32 v238, v238, v238
	v_max_f32_e32 v239, v239, v239
	v_max_f32_e32 v240, v240, v240
	v_max_f32_e32 v241, v241, v241
	v_med3_f32 v226, v226, s62, v95
	v_med3_f32 v227, v227, s62, v95
	v_med3_f32 v228, v228, s62, v95
	v_med3_f32 v229, v229, s62, v95
	v_med3_f32 v230, v230, s62, v95
	v_med3_f32 v231, v231, s62, v95
	v_med3_f32 v232, v232, s62, v95
	v_med3_f32 v233, v233, s62, v95
	v_med3_f32 v234, v234, s62, v95
	v_med3_f32 v235, v235, s62, v95
	v_med3_f32 v236, v236, s62, v95
	v_med3_f32 v237, v237, s62, v95
	v_med3_f32 v238, v238, s62, v95
	v_med3_f32 v239, v239, s62, v95
	v_med3_f32 v240, v240, s62, v95
	v_med3_f32 v241, v241, s62, v95
	v_mov_b32_e32 v242, 0
	v_mov_b32_e32 v243, 0
	v_mov_b32_e32 v244, 0
	v_mov_b32_e32 v245, 0
	v_cvt_pk_fp8_f32 v242, v226, v227
	v_cvt_pk_fp8_f32 v243, v230, v231
	v_cvt_pk_fp8_f32 v244, v234, v235
	v_cvt_pk_fp8_f32 v245, v238, v239
	v_cvt_pk_fp8_f32 v242, v228, v229 op_sel:[0,0,1]
	v_cvt_pk_fp8_f32 v243, v232, v233 op_sel:[0,0,1]
	v_cvt_pk_fp8_f32 v244, v236, v237 op_sel:[0,0,1]
	v_cvt_pk_fp8_f32 v245, v240, v241 op_sel:[0,0,1]
	s_nop 0
	global_store_dwordx4 v77, v[242:245], s[6:7]
	ds_read_b32 v226, v214
	ds_read_b32 v227, v214 offset:512
	ds_read_b32 v228, v214 offset:1024
	ds_read_b32 v229, v214 offset:1536
	ds_read_b32 v230, v214 offset:2048
	ds_read_b32 v231, v214 offset:2560
	ds_read_b32 v232, v214 offset:3072
	ds_read_b32 v233, v214 offset:3584
	ds_read_b32 v234, v214 offset:4096
	ds_read_b32 v235, v214 offset:4608
	ds_read_b32 v236, v214 offset:5120
	ds_read_b32 v237, v214 offset:5632
	ds_read_b32 v238, v214 offset:6144
	ds_read_b32 v239, v214 offset:6656
	ds_read_b32 v240, v214 offset:7168
	ds_read_b32 v241, v214 offset:7680
	s_waitcnt lgkmcnt(0)
	v_max_f32_e32 v226, v226, v226
	v_max_f32_e32 v227, v227, v227
	v_max_f32_e32 v228, v228, v228
	v_max_f32_e32 v229, v229, v229
	v_max_f32_e32 v230, v230, v230
	v_max_f32_e32 v231, v231, v231
	v_max_f32_e32 v232, v232, v232
	v_max_f32_e32 v233, v233, v233
	v_max_f32_e32 v234, v234, v234
	v_max_f32_e32 v235, v235, v235
	v_max_f32_e32 v236, v236, v236
	v_max_f32_e32 v237, v237, v237
	v_max_f32_e32 v238, v238, v238
	v_max_f32_e32 v239, v239, v239
	v_max_f32_e32 v240, v240, v240
	v_max_f32_e32 v241, v241, v241
	v_med3_f32 v226, v226, s62, v95
	v_med3_f32 v227, v227, s62, v95
	v_med3_f32 v228, v228, s62, v95
	v_med3_f32 v229, v229, s62, v95
	v_med3_f32 v230, v230, s62, v95
	v_med3_f32 v231, v231, s62, v95
	v_med3_f32 v232, v232, s62, v95
	v_med3_f32 v233, v233, s62, v95
	v_med3_f32 v234, v234, s62, v95
	v_med3_f32 v235, v235, s62, v95
	v_med3_f32 v236, v236, s62, v95
	v_med3_f32 v237, v237, s62, v95
	v_med3_f32 v238, v238, s62, v95
	v_med3_f32 v239, v239, s62, v95
	v_med3_f32 v240, v240, s62, v95
	v_med3_f32 v241, v241, s62, v95
	v_mov_b32_e32 v242, 0
	v_mov_b32_e32 v243, 0
	v_mov_b32_e32 v244, 0
	v_mov_b32_e32 v245, 0
	v_cvt_pk_fp8_f32 v242, v226, v227
	v_cvt_pk_fp8_f32 v243, v230, v231
	v_cvt_pk_fp8_f32 v244, v234, v235
	v_cvt_pk_fp8_f32 v245, v238, v239
	v_cvt_pk_fp8_f32 v242, v228, v229 op_sel:[0,0,1]
	v_cvt_pk_fp8_f32 v243, v232, v233 op_sel:[0,0,1]
	v_cvt_pk_fp8_f32 v244, v236, v237 op_sel:[0,0,1]
	v_cvt_pk_fp8_f32 v245, v240, v241 op_sel:[0,0,1]
	s_nop 0
	global_store_dwordx4 v78, v[242:245], s[6:7]
	s_waitcnt vmcnt(12)
	v_mul_f32_e32 v144, v26, v144
	v_mul_f32_e32 v145, v26, v145
	v_mul_f32_e32 v146, v26, v146
	v_mul_f32_e32 v147, v26, v147
	ds_write_b128 v209, v[144:147]
	v_mul_f32_e32 v148, v27, v148
	v_mul_f32_e32 v149, v27, v149
	v_mul_f32_e32 v150, v27, v150
	v_mul_f32_e32 v151, v27, v151
	ds_write_b128 v209, v[148:151] offset:1024
	v_mul_f32_e32 v152, v28, v152
	v_mul_f32_e32 v153, v28, v153
	v_mul_f32_e32 v154, v28, v154
	v_mul_f32_e32 v155, v28, v155
	ds_write_b128 v209, v[152:155] offset:2048
	v_mul_f32_e32 v156, v29, v156
	v_mul_f32_e32 v157, v29, v157
	v_mul_f32_e32 v158, v29, v158
	v_mul_f32_e32 v159, v29, v159
	ds_write_b128 v209, v[156:159] offset:3072
	v_mul_f32_e32 v160, v30, v160
	v_mul_f32_e32 v161, v30, v161
	v_mul_f32_e32 v162, v30, v162
	v_mul_f32_e32 v163, v30, v163
	ds_write_b128 v209, v[160:163] offset:4096
	v_mul_f32_e32 v164, v31, v164
	v_mul_f32_e32 v165, v31, v165
	v_mul_f32_e32 v166, v31, v166
	v_mul_f32_e32 v167, v31, v167
	ds_write_b128 v209, v[164:167] offset:5120
	v_mul_f32_e32 v168, v32, v168
	v_mul_f32_e32 v169, v32, v169
	v_mul_f32_e32 v170, v32, v170
	v_mul_f32_e32 v171, v32, v171
	ds_write_b128 v209, v[168:171] offset:6144
	v_mul_f32_e32 v172, v33, v172
	v_mul_f32_e32 v173, v33, v173
	v_mul_f32_e32 v174, v33, v174
	v_mul_f32_e32 v175, v33, v175
	ds_write_b128 v209, v[172:175] offset:7168
	s_waitcnt lgkmcnt(0)
	s_barrier
; #define GAS __attribute__((address_space(1)))
; #define LAS __attribute__((address_space(3)))
; #define LDS_WAIT() asm volatile("s_waitcnt lgkmcnt(0)" ::: "memory")
; __device__ __forceinline__ unsigned pk4_fp8(float a, float b, float c, float d) {
;     a = fminf(fmaxf(a, -448.f), 448.f); b = fminf(fmaxf(b, -448.f), 448.f); c = fminf(fmaxf(c, -448.f), 448.f); d = fminf(fmaxf(d, -448.f), 448.f);
;     int w = __builtin_amdgcn_cvt_pk_fp8_f32(a, b, 0, false); w = __builtin_amdgcn_cvt_pk_fp8_f32(c, d, w, true); return (unsigned)w; }
;     ...
;     for (int i = 0; i < 32; ++i) v[i] = sc >= 0 ? W[(size_t)(k0 + 2 * i + (lane >> 5)) * Nsrc + sc] : 0.f;
; #pragma unroll
;     for (int i = 0; i < 32; ++i) { const int k = k0 + 2 * i + (lane >> 5); float x = v[i] * wscale; if (KS) x *= (k < ksplit ? ksA[k] : ksB[k - ksplit]); scr[(2 * i + (lane >> 5)) * 33 + (lane & 31)] = x; }
;     LDS_WAIT(); asm volatile("" ::: "memory");
;     const int c = lane & 7;
; #pragma unroll
;     for (int j = 0; j < 4; ++j) { const int n = (lane >> 3) + 8 * j; const LAS float* s = scr + (8 * c) * 33 + n;
;         const unsigned long long o = (unsigned long long)pg8::pk4_fp8(s[0 * 33], s[1 * 33], s[2 * 33], s[3 * 33]) | ((unsigned long long)pg8::pk4_fp8(s[4 * 33], s[5 * 33], s[6 * 33], s[7 * 33]) << 32);
;         *(GAS unsigned long long*)(WT + (size_t)(n0 + n) * K + k0 + 8 * c) = o; }
	s_mov_b64 s[8:9], s[34:35]
	global_load_dwordx4 v[144:147], v74, s[8:9]
	s_add_u32 s8, s8, 0x20000
	s_addc_u32 s9, s9, 0
	global_load_dwordx4 v[148:151], v74, s[8:9]
	s_add_u32 s8, s8, 0x20000
	s_addc_u32 s9, s9, 0
	global_load_dwordx4 v[152:155], v74, s[8:9]
	s_add_u32 s8, s8, 0x20000
	s_addc_u32 s9, s9, 0
	global_load_dwordx4 v[156:159], v74, s[8:9]
	s_add_u32 s8, s8, 0x20000
	s_addc_u32 s9, s9, 0
	global_load_dwordx4 v[160:163], v74, s[8:9]
	s_add_u32 s8, s8, 0x20000
	s_addc_u32 s9, s9, 0
	global_load_dwordx4 v[164:167], v74, s[8:9]
	s_add_u32 s8, s8, 0x20000
	s_addc_u32 s9, s9, 0
	global_load_dwordx4 v[168:171], v74, s[8:9]
	s_add_u32 s8, s8, 0x20000
	s_addc_u32 s9, s9, 0
	global_load_dwordx4 v[172:175], v74, s[8:9]
	s_add_u32 s6, s32, 0x3800000
	s_addc_u32 s7, s33, 0
	ds_read_b32 v226, v211
	ds_read_b32 v227, v211 offset:512
	ds_read_b32 v228, v211 offset:1024
	ds_read_b32 v229, v211 offset:1536
	ds_read_b32 v230, v211 offset:2048
	ds_read_b32 v231, v211 offset:2560
	ds_read_b32 v232, v211 offset:3072
	ds_read_b32 v233, v211 offset:3584
	ds_read_b32 v234, v211 offset:4096
	ds_read_b32 v235, v211 offset:4608
	ds_read_b32 v236, v211 offset:5120
	ds_read_b32 v237, v211 offset:5632
	ds_read_b32 v238, v211 offset:6144
	ds_read_b32 v239, v211 offset:6656
	ds_read_b32 v240, v211 offset:7168
	ds_read_b32 v241, v211 offset:7680
	s_waitcnt lgkmcnt(0)
	v_max_f32_e32 v226, v226, v226
	v_max_f32_e32 v227, v227, v227
	v_max_f32_e32 v228, v228, v228
	v_max_f32_e32 v229, v229, v229
	v_max_f32_e32 v230, v230, v230
	v_max_f32_e32 v231, v231, v231
	v_max_f32_e32 v232, v232, v232
	v_max_f32_e32 v233, v233, v233
	v_max_f32_e32 v234, v234, v234
	v_max_f32_e32 v235, v235, v235
	v_max_f32_e32 v236, v236, v236
	v_max_f32_e32 v237, v237, v237
	v_max_f32_e32 v238, v238, v238
	v_max_f32_e32 v239, v239, v239
	v_max_f32_e32 v240, v240, v240
	v_max_f32_e32 v241, v241, v241
	v_med3_f32 v226, v226, s62, v95
	v_med3_f32 v227, v227, s62, v95
	v_med3_f32 v228, v228, s62, v95
	v_med3_f32 v229, v229, s62, v95
	v_med3_f32 v230, v230, s62, v95
	v_med3_f32 v231, v231, s62, v95
	v_med3_f32 v232, v232, s62, v95
	v_med3_f32 v233, v233, s62, v95
	v_med3_f32 v234, v234, s62, v95
	v_med3_f32 v235, v235, s62, v95
	v_med3_f32 v236, v236, s62, v95
	v_med3_f32 v237, v237, s62, v95
	v_med3_f32 v238, v238, s62, v95
	v_med3_f32 v239, v239, s62, v95
	v_med3_f32 v240, v240, s62, v95
	v_med3_f32 v241, v241, s62, v95
	v_mov_b32_e32 v242, 0
	v_mov_b32_e32 v243, 0
	v_mov_b32_e32 v244, 0
	v_mov_b32_e32 v245, 0
	v_cvt_pk_fp8_f32 v242, v226, v227
	v_cvt_pk_fp8_f32 v243, v230, v231
	v_cvt_pk_fp8_f32 v244, v234, v235
	v_cvt_pk_fp8_f32 v245, v238, v239
	v_cvt_pk_fp8_f32 v242, v228, v229 op_sel:[0,0,1]
	v_cvt_pk_fp8_f32 v243, v232, v233 op_sel:[0,0,1]
	v_cvt_pk_fp8_f32 v244, v236, v237 op_sel:[0,0,1]
	v_cvt_pk_fp8_f32 v245, v240, v241 op_sel:[0,0,1]
	s_nop 0
	global_store_dwordx4 v77, v[242:245], s[6:7]
	ds_read_b32 v226, v213
	ds_read_b32 v227, v213 offset:512
	ds_read_b32 v228, v213 offset:1024
	ds_read_b32 v229, v213 offset:1536
	ds_read_b32 v230, v213 offset:2048
	ds_read_b32 v231, v213 offset:2560
	ds_read_b32 v232, v213 offset:3072
	ds_read_b32 v233, v213 offset:3584
	ds_read_b32 v234, v213 offset:4096
	ds_read_b32 v235, v213 offset:4608
	ds_read_b32 v236, v213 offset:5120
	ds_read_b32 v237, v213 offset:5632
	ds_read_b32 v238, v213 offset:6144
	ds_read_b32 v239, v213 offset:6656
	ds_read_b32 v240, v213 offset:7168
	ds_read_b32 v241, v213 offset:7680
	s_waitcnt lgkmcnt(0)
	v_max_f32_e32 v226, v226, v226
	v_max_f32_e32 v227, v227, v227
	v_max_f32_e32 v228, v228, v228
	v_max_f32_e32 v229, v229, v229
	v_max_f32_e32 v230, v230, v230
	v_max_f32_e32 v231, v231, v231
	v_max_f32_e32 v232, v232, v232
	v_max_f32_e32 v233, v233, v233
	v_max_f32_e32 v234, v234, v234
	v_max_f32_e32 v235, v235, v235
	v_max_f32_e32 v236, v236, v236
	v_max_f32_e32 v237, v237, v237
	v_max_f32_e32 v238, v238, v238
	v_max_f32_e32 v239, v239, v239
	v_max_f32_e32 v240, v240, v240
	v_max_f32_e32 v241, v241, v241
	v_med3_f32 v226, v226, s62, v95
	v_med3_f32 v227, v227, s62, v95
	v_med3_f32 v228, v228, s62, v95
	v_med3_f32 v229, v229, s62, v95
	v_med3_f32 v230, v230, s62, v95
	v_med3_f32 v231, v231, s62, v95
	v_med3_f32 v232, v232, s62, v95
	v_med3_f32 v233, v233, s62, v95
	v_med3_f32 v234, v234, s62, v95
	v_med3_f32 v235, v235, s62, v95
	v_med3_f32 v236, v236, s62, v95
	v_med3_f32 v237, v237, s62, v95
	v_med3_f32 v238, v238, s62, v95
	v_med3_f32 v239, v239, s62, v95
	v_med3_f32 v240, v240, s62, v95
	v_med3_f32 v241, v241, s62, v95
	v_mov_b32_e32 v242, 0
	v_mov_b32_e32 v243, 0
	v_mov_b32_e32 v244, 0
	v_mov_b32_e32 v245, 0
	v_cvt_pk_fp8_f32 v242, v226, v227
	v_cvt_pk_fp8_f32 v243, v230, v231
	v_cvt_pk_fp8_f32 v244, v234, v235
	v_cvt_pk_fp8_f32 v245, v238, v239
	v_cvt_pk_fp8_f32 v242, v228, v229 op_sel:[0,0,1]
	v_cvt_pk_fp8_f32 v243, v232, v233 op_sel:[0,0,1]
	v_cvt_pk_fp8_f32 v244, v236, v237 op_sel:[0,0,1]
	v_cvt_pk_fp8_f32 v245, v240, v241 op_sel:[0,0,1]
	s_nop 0
	global_store_dwordx4 v78, v[242:245], s[6:7]
	s_waitcnt vmcnt(12)
	v_mul_f32_e32 v176, v26, v176
	v_mul_f32_e32 v177, v26, v177
	v_mul_f32_e32 v178, v26, v178
	v_mul_f32_e32 v179, v26, v179
	ds_write_b128 v210, v[176:179]
	v_mul_f32_e32 v180, v27, v180
	v_mul_f32_e32 v181, v27, v181
	v_mul_f32_e32 v182, v27, v182
	v_mul_f32_e32 v183, v27, v183
	ds_write_b128 v210, v[180:183] offset:1024
	v_mul_f32_e32 v184, v28, v184
	v_mul_f32_e32 v185, v28, v185
	v_mul_f32_e32 v186, v28, v186
	v_mul_f32_e32 v187, v28, v187
	ds_write_b128 v210, v[184:187] offset:2048
	v_mul_f32_e32 v188, v29, v188
	v_mul_f32_e32 v189, v29, v189
	v_mul_f32_e32 v190, v29, v190
	v_mul_f32_e32 v191, v29, v191
	ds_write_b128 v210, v[188:191] offset:3072
	v_mul_f32_e32 v192, v30, v192
	v_mul_f32_e32 v193, v30, v193
	v_mul_f32_e32 v194, v30, v194
	v_mul_f32_e32 v195, v30, v195
	ds_write_b128 v210, v[192:195] offset:4096
	v_mul_f32_e32 v196, v31, v196
	v_mul_f32_e32 v197, v31, v197
	v_mul_f32_e32 v198, v31, v198
	v_mul_f32_e32 v199, v31, v199
	ds_write_b128 v210, v[196:199] offset:5120
	v_mul_f32_e32 v200, v32, v200
	v_mul_f32_e32 v201, v32, v201
	v_mul_f32_e32 v202, v32, v202
	v_mul_f32_e32 v203, v32, v203
	ds_write_b128 v210, v[200:203] offset:6144
	v_mul_f32_e32 v204, v33, v204
	v_mul_f32_e32 v205, v33, v205
	v_mul_f32_e32 v206, v33, v206
	v_mul_f32_e32 v207, v33, v207
	ds_write_b128 v210, v[204:207] offset:7168
	s_waitcnt lgkmcnt(0)
	s_barrier
; #define GAS __attribute__((address_space(1)))
; #define LAS __attribute__((address_space(3)))
; #define LDS_WAIT() asm volatile("s_waitcnt lgkmcnt(0)" ::: "memory")
; __device__ __forceinline__ unsigned pk4_fp8(float a, float b, float c, float d) {
;     a = fminf(fmaxf(a, -448.f), 448.f); b = fminf(fmaxf(b, -448.f), 448.f); c = fminf(fmaxf(c, -448.f), 448.f); d = fminf(fmaxf(d, -448.f), 448.f);
;     int w = __builtin_amdgcn_cvt_pk_fp8_f32(a, b, 0, false); w = __builtin_amdgcn_cvt_pk_fp8_f32(c, d, w, true); return (unsigned)w; }
;     ...
;     for (int i = 0; i < 32; ++i) v[i] = sc >= 0 ? W[(size_t)(k0 + 2 * i + (lane >> 5)) * Nsrc + sc] : 0.f;
; #pragma unroll
;     for (int i = 0; i < 32; ++i) { const int k = k0 + 2 * i + (lane >> 5); float x = v[i] * wscale; if (KS) x *= (k < ksplit ? ksA[k] : ksB[k - ksplit]); scr[(2 * i + (lane >> 5)) * 33 + (lane & 31)] = x; }
;     LDS_WAIT(); asm volatile("" ::: "memory");
;     const int c = lane & 7;
; #pragma unroll
;     for (int j = 0; j < 4; ++j) { const int n = (lane >> 3) + 8 * j; const LAS float* s = scr + (8 * c) * 33 + n;
;         const unsigned long long o = (unsigned long long)pg8::pk4_fp8(s[0 * 33], s[1 * 33], s[2 * 33], s[3 * 33]) | ((unsigned long long)pg8::pk4_fp8(s[4 * 33], s[5 * 33], s[6 * 33], s[7 * 33]) << 32);
;         *(GAS unsigned long long*)(WT + (size_t)(n0 + n) * K + k0 + 8 * c) = o; }
	s_add_u32 s8, s34, 0x1000
	s_addc_u32 s9, s35, 0
	global_load_dwordx4 v[176:179], v74, s[8:9]
	s_add_u32 s8, s8, 0x20000
	s_addc_u32 s9, s9, 0
	global_load_dwordx4 v[180:183], v74, s[8:9]
	s_add_u32 s8, s8, 0x20000
	s_addc_u32 s9, s9, 0
	global_load_dwordx4 v[184:187], v74, s[8:9]
	s_add_u32 s8, s8, 0x20000
	s_addc_u32 s9, s9, 0
	global_load_dwordx4 v[188:191], v74, s[8:9]
	s_add_u32 s8, s8, 0x20000
	s_addc_u32 s9, s9, 0
	global_load_dwordx4 v[192:195], v74, s[8:9]
	s_add_u32 s8, s8, 0x20000
	s_addc_u32 s9, s9, 0
	global_load_dwordx4 v[196:199], v74, s[8:9]
	s_add_u32 s8, s8, 0x20000
	s_addc_u32 s9, s9, 0
	global_load_dwordx4 v[200:203], v74, s[8:9]
	s_add_u32 s8, s8, 0x20000
	s_addc_u32 s9, s9, 0
	global_load_dwordx4 v[204:207], v74, s[8:9]
	s_add_u32 s6, s32, 0x3c00000
	s_addc_u32 s7, s33, 0
	ds_read_b32 v226, v212
	ds_read_b32 v227, v212 offset:512
	ds_read_b32 v228, v212 offset:1024
	ds_read_b32 v229, v212 offset:1536
	ds_read_b32 v230, v212 offset:2048
	ds_read_b32 v231, v212 offset:2560
	ds_read_b32 v232, v212 offset:3072
	ds_read_b32 v233, v212 offset:3584
	ds_read_b32 v234, v212 offset:4096
	ds_read_b32 v235, v212 offset:4608
	ds_read_b32 v236, v212 offset:5120
	ds_read_b32 v237, v212 offset:5632
	ds_read_b32 v238, v212 offset:6144
	ds_read_b32 v239, v212 offset:6656
	ds_read_b32 v240, v212 offset:7168
	ds_read_b32 v241, v212 offset:7680
	s_waitcnt lgkmcnt(0)
	v_max_f32_e32 v226, v226, v226
	v_max_f32_e32 v227, v227, v227
	v_max_f32_e32 v228, v228, v228
	v_max_f32_e32 v229, v229, v229
	v_max_f32_e32 v230, v230, v230
	v_max_f32_e32 v231, v231, v231
	v_max_f32_e32 v232, v232, v232
	v_max_f32_e32 v233, v233, v233
	v_max_f32_e32 v234, v234, v234
	v_max_f32_e32 v235, v235, v235
	v_max_f32_e32 v236, v236, v236
	v_max_f32_e32 v237, v237, v237
	v_max_f32_e32 v238, v238, v238
	v_max_f32_e32 v239, v239, v239
	v_max_f32_e32 v240, v240, v240
	v_max_f32_e32 v241, v241, v241
	v_med3_f32 v226, v226, s62, v95
	v_med3_f32 v227, v227, s62, v95
	v_med3_f32 v228, v228, s62, v95
	v_med3_f32 v229, v229, s62, v95
	v_med3_f32 v230, v230, s62, v95
	v_med3_f32 v231, v231, s62, v95
	v_med3_f32 v232, v232, s62, v95
	v_med3_f32 v233, v233, s62, v95
	v_med3_f32 v234, v234, s62, v95
	v_med3_f32 v235, v235, s62, v95
	v_med3_f32 v236, v236, s62, v95
	v_med3_f32 v237, v237, s62, v95
	v_med3_f32 v238, v238, s62, v95
	v_med3_f32 v239, v239, s62, v95
	v_med3_f32 v240, v240, s62, v95
	v_med3_f32 v241, v241, s62, v95
	v_mov_b32_e32 v242, 0
	v_mov_b32_e32 v243, 0
	v_mov_b32_e32 v244, 0
	v_mov_b32_e32 v245, 0
	v_cvt_pk_fp8_f32 v242, v226, v227
	v_cvt_pk_fp8_f32 v243, v230, v231
	v_cvt_pk_fp8_f32 v244, v234, v235
	v_cvt_pk_fp8_f32 v245, v238, v239
	v_cvt_pk_fp8_f32 v242, v228, v229 op_sel:[0,0,1]
	v_cvt_pk_fp8_f32 v243, v232, v233 op_sel:[0,0,1]
	v_cvt_pk_fp8_f32 v244, v236, v237 op_sel:[0,0,1]
	v_cvt_pk_fp8_f32 v245, v240, v241 op_sel:[0,0,1]
	s_nop 0
	global_store_dwordx4 v77, v[242:245], s[6:7]
	ds_read_b32 v226, v214
	ds_read_b32 v227, v214 offset:512
	ds_read_b32 v228, v214 offset:1024
	ds_read_b32 v229, v214 offset:1536
	ds_read_b32 v230, v214 offset:2048
	ds_read_b32 v231, v214 offset:2560
	ds_read_b32 v232, v214 offset:3072
	ds_read_b32 v233, v214 offset:3584
	ds_read_b32 v234, v214 offset:4096
	ds_read_b32 v235, v214 offset:4608
	ds_read_b32 v236, v214 offset:5120
	ds_read_b32 v237, v214 offset:5632
	ds_read_b32 v238, v214 offset:6144
	ds_read_b32 v239, v214 offset:6656
	ds_read_b32 v240, v214 offset:7168
	ds_read_b32 v241, v214 offset:7680
	s_waitcnt lgkmcnt(0)
	v_max_f32_e32 v226, v226, v226
	v_max_f32_e32 v227, v227, v227
	v_max_f32_e32 v228, v228, v228
	v_max_f32_e32 v229, v229, v229
	v_max_f32_e32 v230, v230, v230
	v_max_f32_e32 v231, v231, v231
	v_max_f32_e32 v232, v232, v232
	v_max_f32_e32 v233, v233, v233
	v_max_f32_e32 v234, v234, v234
	v_max_f32_e32 v235, v235, v235
	v_max_f32_e32 v236, v236, v236
	v_max_f32_e32 v237, v237, v237
	v_max_f32_e32 v238, v238, v238
	v_max_f32_e32 v239, v239, v239
	v_max_f32_e32 v240, v240, v240
	v_max_f32_e32 v241, v241, v241
	v_med3_f32 v226, v226, s62, v95
	v_med3_f32 v227, v227, s62, v95
	v_med3_f32 v228, v228, s62, v95
	v_med3_f32 v229, v229, s62, v95
	v_med3_f32 v230, v230, s62, v95
	v_med3_f32 v231, v231, s62, v95
	v_med3_f32 v232, v232, s62, v95
	v_med3_f32 v233, v233, s62, v95
	v_med3_f32 v234, v234, s62, v95
	v_med3_f32 v235, v235, s62, v95
	v_med3_f32 v236, v236, s62, v95
	v_med3_f32 v237, v237, s62, v95
	v_med3_f32 v238, v238, s62, v95
	v_med3_f32 v239, v239, s62, v95
	v_med3_f32 v240, v240, s62, v95
	v_med3_f32 v241, v241, s62, v95
	v_mov_b32_e32 v242, 0
	v_mov_b32_e32 v243, 0
	v_mov_b32_e32 v244, 0
	v_mov_b32_e32 v245, 0
	v_cvt_pk_fp8_f32 v242, v226, v227
	v_cvt_pk_fp8_f32 v243, v230, v231
	v_cvt_pk_fp8_f32 v244, v234, v235
	v_cvt_pk_fp8_f32 v245, v238, v239
	v_cvt_pk_fp8_f32 v242, v228, v229 op_sel:[0,0,1]
	v_cvt_pk_fp8_f32 v243, v232, v233 op_sel:[0,0,1]
	v_cvt_pk_fp8_f32 v244, v236, v237 op_sel:[0,0,1]
	v_cvt_pk_fp8_f32 v245, v240, v241 op_sel:[0,0,1]
	s_nop 0
	global_store_dwordx4 v78, v[242:245], s[6:7]
	s_waitcnt vmcnt(12)
	v_mul_f32_e32 v144, v34, v144
	v_mul_f32_e32 v145, v34, v145
	v_mul_f32_e32 v146, v34, v146
	v_mul_f32_e32 v147, v34, v147
	ds_write_b128 v209, v[144:147]
	v_mul_f32_e32 v148, v35, v148
	v_mul_f32_e32 v149, v35, v149
	v_mul_f32_e32 v150, v35, v150
	v_mul_f32_e32 v151, v35, v151
	ds_write_b128 v209, v[148:151] offset:1024
	v_mul_f32_e32 v152, v36, v152
	v_mul_f32_e32 v153, v36, v153
	v_mul_f32_e32 v154, v36, v154
	v_mul_f32_e32 v155, v36, v155
	ds_write_b128 v209, v[152:155] offset:2048
	v_mul_f32_e32 v156, v37, v156
	v_mul_f32_e32 v157, v37, v157
	v_mul_f32_e32 v158, v37, v158
	v_mul_f32_e32 v159, v37, v159
	ds_write_b128 v209, v[156:159] offset:3072
	v_mul_f32_e32 v160, v38, v160
	v_mul_f32_e32 v161, v38, v161
	v_mul_f32_e32 v162, v38, v162
	v_mul_f32_e32 v163, v38, v163
	ds_write_b128 v209, v[160:163] offset:4096
	v_mul_f32_e32 v164, v39, v164
	v_mul_f32_e32 v165, v39, v165
	v_mul_f32_e32 v166, v39, v166
	v_mul_f32_e32 v167, v39, v167
	ds_write_b128 v209, v[164:167] offset:5120
	v_mul_f32_e32 v168, v40, v168
	v_mul_f32_e32 v169, v40, v169
	v_mul_f32_e32 v170, v40, v170
	v_mul_f32_e32 v171, v40, v171
	ds_write_b128 v209, v[168:171] offset:6144
	v_mul_f32_e32 v172, v41, v172
	v_mul_f32_e32 v173, v41, v173
	v_mul_f32_e32 v174, v41, v174
	v_mul_f32_e32 v175, v41, v175
	ds_write_b128 v209, v[172:175] offset:7168
	s_waitcnt lgkmcnt(0)
	s_barrier
; #define GAS __attribute__((address_space(1)))
; #define LAS __attribute__((address_space(3)))
; #define LDS_WAIT() asm volatile("s_waitcnt lgkmcnt(0)" ::: "memory")
; __device__ __forceinline__ unsigned pk4_fp8(float a, float b, float c, float d) {
;     a = fminf(fmaxf(a, -448.f), 448.f); b = fminf(fmaxf(b, -448.f), 448.f); c = fminf(fmaxf(c, -448.f), 448.f); d = fminf(fmaxf(d, -448.f), 448.f);
;     int w = __builtin_amdgcn_cvt_pk_fp8_f32(a, b, 0, false); w = __builtin_amdgcn_cvt_pk_fp8_f32(c, d, w, true); return (unsigned)w; }
;     ...
;     for (int i = 0; i < 32; ++i) v[i] = sc >= 0 ? W[(size_t)(k0 + 2 * i + (lane >> 5)) * Nsrc + sc] : 0.f;
; #pragma unroll
;     for (int i = 0; i < 32; ++i) { const int k = k0 + 2 * i + (lane >> 5); float x = v[i] * wscale; if (KS) x *= (k < ksplit ? ksA[k] : ksB[k - ksplit]); scr[(2 * i + (lane >> 5)) * 33 + (lane & 31)] = x; }
;     LDS_WAIT(); asm volatile("" ::: "memory");
;     const int c = lane & 7;
; #pragma unroll
;     for (int j = 0; j < 4; ++j) { const int n = (lane >> 3) + 8 * j; const LAS float* s = scr + (8 * c) * 33 + n;
;         const unsigned long long o = (unsigned long long)pg8::pk4_fp8(s[0 * 33], s[1 * 33], s[2 * 33], s[3 * 33]) | ((unsigned long long)pg8::pk4_fp8(s[4 * 33], s[5 * 33], s[6 * 33], s[7 * 33]) << 32);
;         *(GAS unsigned long long*)(WT + (size_t)(n0 + n) * K + k0 + 8 * c) = o; }
	s_add_u32 s8, s34, 0x2000
	s_addc_u32 s9, s35, 0
	global_load_dwordx4 v[144:147], v74, s[8:9]
	s_add_u32 s8, s8, 0x20000
	s_addc_u32 s9, s9, 0
	global_load_dwordx4 v[148:151], v74, s[8:9]
	s_add_u32 s8, s8, 0x20000
	s_addc_u32 s9, s9, 0
	global_load_dwordx4 v[152:155], v74, s[8:9]
	s_add_u32 s8, s8, 0x20000
	s_addc_u32 s9, s9, 0
	global_load_dwordx4 v[156:159], v74, s[8:9]
	s_add_u32 s8, s8, 0x20000
	s_addc_u32 s9, s9, 0
	global_load_dwordx4 v[160:163], v74, s[8:9]
	s_add_u32 s8, s8, 0x20000
	s_addc_u32 s9, s9, 0
	global_load_dwordx4 v[164:167], v74, s[8:9]
	s_add_u32 s8, s8, 0x20000
	s_addc_u32 s9, s9, 0
	global_load_dwordx4 v[168:171], v74, s[8:9]
	s_add_u32 s8, s8, 0x20000
	s_addc_u32 s9, s9, 0
	global_load_dwordx4 v[172:175], v74, s[8:9]
	s_mov_b64 s[6:7], s[36:37]
	ds_read_b32 v226, v211
	ds_read_b32 v227, v211 offset:512
	ds_read_b32 v228, v211 offset:1024
	ds_read_b32 v229, v211 offset:1536
	ds_read_b32 v230, v211 offset:2048
	ds_read_b32 v231, v211 offset:2560
	ds_read_b32 v232, v211 offset:3072
	ds_read_b32 v233, v211 offset:3584
	ds_read_b32 v234, v211 offset:4096
	ds_read_b32 v235, v211 offset:4608
	ds_read_b32 v236, v211 offset:5120
	ds_read_b32 v237, v211 offset:5632
	ds_read_b32 v238, v211 offset:6144
	ds_read_b32 v239, v211 offset:6656
	ds_read_b32 v240, v211 offset:7168
	ds_read_b32 v241, v211 offset:7680
	s_waitcnt lgkmcnt(0)
	v_max_f32_e32 v226, v226, v226
	v_max_f32_e32 v227, v227, v227
	v_max_f32_e32 v228, v228, v228
	v_max_f32_e32 v229, v229, v229
	v_max_f32_e32 v230, v230, v230
	v_max_f32_e32 v231, v231, v231
	v_max_f32_e32 v232, v232, v232
	v_max_f32_e32 v233, v233, v233
	v_max_f32_e32 v234, v234, v234
	v_max_f32_e32 v235, v235, v235
	v_max_f32_e32 v236, v236, v236
	v_max_f32_e32 v237, v237, v237
	v_max_f32_e32 v238, v238, v238
	v_max_f32_e32 v239, v239, v239
	v_max_f32_e32 v240, v240, v240
	v_max_f32_e32 v241, v241, v241
	v_med3_f32 v226, v226, s62, v95
	v_med3_f32 v227, v227, s62, v95
	v_med3_f32 v228, v228, s62, v95
	v_med3_f32 v229, v229, s62, v95
	v_med3_f32 v230, v230, s62, v95
	v_med3_f32 v231, v231, s62, v95
	v_med3_f32 v232, v232, s62, v95
	v_med3_f32 v233, v233, s62, v95
	v_med3_f32 v234, v234, s62, v95
	v_med3_f32 v235, v235, s62, v95
	v_med3_f32 v236, v236, s62, v95
	v_med3_f32 v237, v237, s62, v95
	v_med3_f32 v238, v238, s62, v95
	v_med3_f32 v239, v239, s62, v95
	v_med3_f32 v240, v240, s62, v95
	v_med3_f32 v241, v241, s62, v95
	v_mov_b32_e32 v242, 0
	v_mov_b32_e32 v243, 0
	v_mov_b32_e32 v244, 0
	v_mov_b32_e32 v245, 0
	v_cvt_pk_fp8_f32 v242, v226, v227
	v_cvt_pk_fp8_f32 v243, v230, v231
	v_cvt_pk_fp8_f32 v244, v234, v235
	v_cvt_pk_fp8_f32 v245, v238, v239
	v_cvt_pk_fp8_f32 v242, v228, v229 op_sel:[0,0,1]
	v_cvt_pk_fp8_f32 v243, v232, v233 op_sel:[0,0,1]
	v_cvt_pk_fp8_f32 v244, v236, v237 op_sel:[0,0,1]
	v_cvt_pk_fp8_f32 v245, v240, v241 op_sel:[0,0,1]
	s_nop 0
	global_store_dwordx4 v77, v[242:245], s[6:7]
	ds_read_b32 v226, v213
	ds_read_b32 v227, v213 offset:512
	ds_read_b32 v228, v213 offset:1024
	ds_read_b32 v229, v213 offset:1536
	ds_read_b32 v230, v213 offset:2048
	ds_read_b32 v231, v213 offset:2560
	ds_read_b32 v232, v213 offset:3072
	ds_read_b32 v233, v213 offset:3584
	ds_read_b32 v234, v213 offset:4096
	ds_read_b32 v235, v213 offset:4608
	ds_read_b32 v236, v213 offset:5120
	ds_read_b32 v237, v213 offset:5632
	ds_read_b32 v238, v213 offset:6144
	ds_read_b32 v239, v213 offset:6656
	ds_read_b32 v240, v213 offset:7168
	ds_read_b32 v241, v213 offset:7680
	s_waitcnt lgkmcnt(0)
	v_max_f32_e32 v226, v226, v226
	v_max_f32_e32 v227, v227, v227
	v_max_f32_e32 v228, v228, v228
	v_max_f32_e32 v229, v229, v229
	v_max_f32_e32 v230, v230, v230
	v_max_f32_e32 v231, v231, v231
	v_max_f32_e32 v232, v232, v232
	v_max_f32_e32 v233, v233, v233
	v_max_f32_e32 v234, v234, v234
	v_max_f32_e32 v235, v235, v235
	v_max_f32_e32 v236, v236, v236
	v_max_f32_e32 v237, v237, v237
	v_max_f32_e32 v238, v238, v238
	v_max_f32_e32 v239, v239, v239
	v_max_f32_e32 v240, v240, v240
	v_max_f32_e32 v241, v241, v241
	v_med3_f32 v226, v226, s62, v95
	v_med3_f32 v227, v227, s62, v95
	v_med3_f32 v228, v228, s62, v95
	v_med3_f32 v229, v229, s62, v95
	v_med3_f32 v230, v230, s62, v95
	v_med3_f32 v231, v231, s62, v95
	v_med3_f32 v232, v232, s62, v95
	v_med3_f32 v233, v233, s62, v95
	v_med3_f32 v234, v234, s62, v95
	v_med3_f32 v235, v235, s62, v95
	v_med3_f32 v236, v236, s62, v95
	v_med3_f32 v237, v237, s62, v95
	v_med3_f32 v238, v238, s62, v95
	v_med3_f32 v239, v239, s62, v95
	v_med3_f32 v240, v240, s62, v95
	v_med3_f32 v241, v241, s62, v95
	v_mov_b32_e32 v242, 0
	v_mov_b32_e32 v243, 0
	v_mov_b32_e32 v244, 0
	v_mov_b32_e32 v245, 0
	v_cvt_pk_fp8_f32 v242, v226, v227
	v_cvt_pk_fp8_f32 v243, v230, v231
	v_cvt_pk_fp8_f32 v244, v234, v235
	v_cvt_pk_fp8_f32 v245, v238, v239
	v_cvt_pk_fp8_f32 v242, v228, v229 op_sel:[0,0,1]
	v_cvt_pk_fp8_f32 v243, v232, v233 op_sel:[0,0,1]
	v_cvt_pk_fp8_f32 v244, v236, v237 op_sel:[0,0,1]
	v_cvt_pk_fp8_f32 v245, v240, v241 op_sel:[0,0,1]
	s_nop 0
	global_store_dwordx4 v78, v[242:245], s[6:7]
	s_waitcnt vmcnt(12)
	v_mul_f32_e32 v176, v34, v176
	v_mul_f32_e32 v177, v34, v177
	v_mul_f32_e32 v178, v34, v178
	v_mul_f32_e32 v179, v34, v179
	ds_write_b128 v210, v[176:179]
	v_mul_f32_e32 v180, v35, v180
	v_mul_f32_e32 v181, v35, v181
	v_mul_f32_e32 v182, v35, v182
	v_mul_f32_e32 v183, v35, v183
	ds_write_b128 v210, v[180:183] offset:1024
	v_mul_f32_e32 v184, v36, v184
	v_mul_f32_e32 v185, v36, v185
	v_mul_f32_e32 v186, v36, v186
	v_mul_f32_e32 v187, v36, v187
	ds_write_b128 v210, v[184:187] offset:2048
	v_mul_f32_e32 v188, v37, v188
	v_mul_f32_e32 v189, v37, v189
	v_mul_f32_e32 v190, v37, v190
	v_mul_f32_e32 v191, v37, v191
	ds_write_b128 v210, v[188:191] offset:3072
	v_mul_f32_e32 v192, v38, v192
	v_mul_f32_e32 v193, v38, v193
	v_mul_f32_e32 v194, v38, v194
	v_mul_f32_e32 v195, v38, v195
	ds_write_b128 v210, v[192:195] offset:4096
	v_mul_f32_e32 v196, v39, v196
	v_mul_f32_e32 v197, v39, v197
	v_mul_f32_e32 v198, v39, v198
	v_mul_f32_e32 v199, v39, v199
	ds_write_b128 v210, v[196:199] offset:5120
	v_mul_f32_e32 v200, v40, v200
	v_mul_f32_e32 v201, v40, v201
	v_mul_f32_e32 v202, v40, v202
	v_mul_f32_e32 v203, v40, v203
	ds_write_b128 v210, v[200:203] offset:6144
	v_mul_f32_e32 v204, v41, v204
	v_mul_f32_e32 v205, v41, v205
	v_mul_f32_e32 v206, v41, v206
	v_mul_f32_e32 v207, v41, v207
	ds_write_b128 v210, v[204:207] offset:7168
	s_waitcnt lgkmcnt(0)
	s_barrier
; #define GAS __attribute__((address_space(1)))
; #define LAS __attribute__((address_space(3)))
; #define LDS_WAIT() asm volatile("s_waitcnt lgkmcnt(0)" ::: "memory")
; __device__ __forceinline__ unsigned pk4_fp8(float a, float b, float c, float d) {
;     a = fminf(fmaxf(a, -448.f), 448.f); b = fminf(fmaxf(b, -448.f), 448.f); c = fminf(fmaxf(c, -448.f), 448.f); d = fminf(fmaxf(d, -448.f), 448.f);
;     int w = __builtin_amdgcn_cvt_pk_fp8_f32(a, b, 0, false); w = __builtin_amdgcn_cvt_pk_fp8_f32(c, d, w, true); return (unsigned)w; }
;     ...
;     for (int i = 0; i < 32; ++i) v[i] = sc >= 0 ? W[(size_t)(k0 + 2 * i + (lane >> 5)) * Nsrc + sc] : 0.f;
; #pragma unroll
;     for (int i = 0; i < 32; ++i) { const int k = k0 + 2 * i + (lane >> 5); float x = v[i] * wscale; if (KS) x *= (k < ksplit ? ksA[k] : ksB[k - ksplit]); scr[(2 * i + (lane >> 5)) * 33 + (lane & 31)] = x; }
;     LDS_WAIT(); asm volatile("" ::: "memory");
;     const int c = lane & 7;
; #pragma unroll
;     for (int j = 0; j < 4; ++j) { const int n = (lane >> 3) + 8 * j; const LAS float* s = scr + (8 * c) * 33 + n;
;         const unsigned long long o = (unsigned long long)pg8::pk4_fp8(s[0 * 33], s[1 * 33], s[2 * 33], s[3 * 33]) | ((unsigned long long)pg8::pk4_fp8(s[4 * 33], s[5 * 33], s[6 * 33], s[7 * 33]) << 32);
;         *(GAS unsigned long long*)(WT + (size_t)(n0 + n) * K + k0 + 8 * c) = o; }
	s_add_u32 s8, s34, 0x3000
	s_addc_u32 s9, s35, 0
	global_load_dwordx4 v[176:179], v74, s[8:9]
	s_add_u32 s8, s8, 0x20000
	s_addc_u32 s9, s9, 0
	global_load_dwordx4 v[180:183], v74, s[8:9]
	s_add_u32 s8, s8, 0x20000
	s_addc_u32 s9, s9, 0
	global_load_dwordx4 v[184:187], v74, s[8:9]
	s_add_u32 s8, s8, 0x20000
	s_addc_u32 s9, s9, 0
	global_load_dwordx4 v[188:191], v74, s[8:9]
	s_add_u32 s8, s8, 0x20000
	s_addc_u32 s9, s9, 0
	global_load_dwordx4 v[192:195], v74, s[8:9]
	s_add_u32 s8, s8, 0x20000
	s_addc_u32 s9, s9, 0
	global_load_dwordx4 v[196:199], v74, s[8:9]
	s_add_u32 s8, s8, 0x20000
	s_addc_u32 s9, s9, 0
	global_load_dwordx4 v[200:203], v74, s[8:9]
	s_add_u32 s8, s8, 0x20000
	s_addc_u32 s9, s9, 0
	global_load_dwordx4 v[204:207], v74, s[8:9]
	s_add_u32 s6, s36, 0x400000
	s_addc_u32 s7, s37, 0
	ds_read_b32 v226, v212
	ds_read_b32 v227, v212 offset:512
	ds_read_b32 v228, v212 offset:1024
	ds_read_b32 v229, v212 offset:1536
	ds_read_b32 v230, v212 offset:2048
	ds_read_b32 v231, v212 offset:2560
	ds_read_b32 v232, v212 offset:3072
	ds_read_b32 v233, v212 offset:3584
	ds_read_b32 v234, v212 offset:4096
	ds_read_b32 v235, v212 offset:4608
	ds_read_b32 v236, v212 offset:5120
	ds_read_b32 v237, v212 offset:5632
	ds_read_b32 v238, v212 offset:6144
	ds_read_b32 v239, v212 offset:6656
	ds_read_b32 v240, v212 offset:7168
	ds_read_b32 v241, v212 offset:7680
	s_waitcnt lgkmcnt(0)
	v_max_f32_e32 v226, v226, v226
	v_max_f32_e32 v227, v227, v227
	v_max_f32_e32 v228, v228, v228
	v_max_f32_e32 v229, v229, v229
	v_max_f32_e32 v230, v230, v230
	v_max_f32_e32 v231, v231, v231
	v_max_f32_e32 v232, v232, v232
	v_max_f32_e32 v233, v233, v233
	v_max_f32_e32 v234, v234, v234
	v_max_f32_e32 v235, v235, v235
	v_max_f32_e32 v236, v236, v236
	v_max_f32_e32 v237, v237, v237
	v_max_f32_e32 v238, v238, v238
	v_max_f32_e32 v239, v239, v239
	v_max_f32_e32 v240, v240, v240
	v_max_f32_e32 v241, v241, v241
	v_med3_f32 v226, v226, s62, v95
	v_med3_f32 v227, v227, s62, v95
	v_med3_f32 v228, v228, s62, v95
	v_med3_f32 v229, v229, s62, v95
	v_med3_f32 v230, v230, s62, v95
	v_med3_f32 v231, v231, s62, v95
	v_med3_f32 v232, v232, s62, v95
	v_med3_f32 v233, v233, s62, v95
	v_med3_f32 v234, v234, s62, v95
	v_med3_f32 v235, v235, s62, v95
	v_med3_f32 v236, v236, s62, v95
	v_med3_f32 v237, v237, s62, v95
	v_med3_f32 v238, v238, s62, v95
	v_med3_f32 v239, v239, s62, v95
	v_med3_f32 v240, v240, s62, v95
	v_med3_f32 v241, v241, s62, v95
	v_mov_b32_e32 v242, 0
	v_mov_b32_e32 v243, 0
	v_mov_b32_e32 v244, 0
	v_mov_b32_e32 v245, 0
	v_cvt_pk_fp8_f32 v242, v226, v227
	v_cvt_pk_fp8_f32 v243, v230, v231
	v_cvt_pk_fp8_f32 v244, v234, v235
	v_cvt_pk_fp8_f32 v245, v238, v239
	v_cvt_pk_fp8_f32 v242, v228, v229 op_sel:[0,0,1]
	v_cvt_pk_fp8_f32 v243, v232, v233 op_sel:[0,0,1]
	v_cvt_pk_fp8_f32 v244, v236, v237 op_sel:[0,0,1]
	v_cvt_pk_fp8_f32 v245, v240, v241 op_sel:[0,0,1]
	s_nop 0
	global_store_dwordx4 v77, v[242:245], s[6:7]
	ds_read_b32 v226, v214
	ds_read_b32 v227, v214 offset:512
	ds_read_b32 v228, v214 offset:1024
	ds_read_b32 v229, v214 offset:1536
	ds_read_b32 v230, v214 offset:2048
	ds_read_b32 v231, v214 offset:2560
	ds_read_b32 v232, v214 offset:3072
	ds_read_b32 v233, v214 offset:3584
	ds_read_b32 v234, v214 offset:4096
	ds_read_b32 v235, v214 offset:4608
	ds_read_b32 v236, v214 offset:5120
	ds_read_b32 v237, v214 offset:5632
	ds_read_b32 v238, v214 offset:6144
	ds_read_b32 v239, v214 offset:6656
	ds_read_b32 v240, v214 offset:7168
	ds_read_b32 v241, v214 offset:7680
	s_waitcnt lgkmcnt(0)
	v_max_f32_e32 v226, v226, v226
	v_max_f32_e32 v227, v227, v227
	v_max_f32_e32 v228, v228, v228
	v_max_f32_e32 v229, v229, v229
	v_max_f32_e32 v230, v230, v230
	v_max_f32_e32 v231, v231, v231
	v_max_f32_e32 v232, v232, v232
	v_max_f32_e32 v233, v233, v233
	v_max_f32_e32 v234, v234, v234
	v_max_f32_e32 v235, v235, v235
	v_max_f32_e32 v236, v236, v236
	v_max_f32_e32 v237, v237, v237
	v_max_f32_e32 v238, v238, v238
	v_max_f32_e32 v239, v239, v239
	v_max_f32_e32 v240, v240, v240
	v_max_f32_e32 v241, v241, v241
	v_med3_f32 v226, v226, s62, v95
	v_med3_f32 v227, v227, s62, v95
	v_med3_f32 v228, v228, s62, v95
	v_med3_f32 v229, v229, s62, v95
	v_med3_f32 v230, v230, s62, v95
	v_med3_f32 v231, v231, s62, v95
	v_med3_f32 v232, v232, s62, v95
	v_med3_f32 v233, v233, s62, v95
	v_med3_f32 v234, v234, s62, v95
	v_med3_f32 v235, v235, s62, v95
	v_med3_f32 v236, v236, s62, v95
	v_med3_f32 v237, v237, s62, v95
	v_med3_f32 v238, v238, s62, v95
	v_med3_f32 v239, v239, s62, v95
	v_med3_f32 v240, v240, s62, v95
	v_med3_f32 v241, v241, s62, v95
	v_mov_b32_e32 v242, 0
	v_mov_b32_e32 v243, 0
	v_mov_b32_e32 v244, 0
	v_mov_b32_e32 v245, 0
	v_cvt_pk_fp8_f32 v242, v226, v227
	v_cvt_pk_fp8_f32 v243, v230, v231
	v_cvt_pk_fp8_f32 v244, v234, v235
	v_cvt_pk_fp8_f32 v245, v238, v239
	v_cvt_pk_fp8_f32 v242, v228, v229 op_sel:[0,0,1]
	v_cvt_pk_fp8_f32 v243, v232, v233 op_sel:[0,0,1]
	v_cvt_pk_fp8_f32 v244, v236, v237 op_sel:[0,0,1]
	v_cvt_pk_fp8_f32 v245, v240, v241 op_sel:[0,0,1]
	s_nop 0
	global_store_dwordx4 v78, v[242:245], s[6:7]
	s_waitcnt vmcnt(12)
	v_mul_f32_e32 v144, v34, v144
	v_mul_f32_e32 v145, v34, v145
	v_mul_f32_e32 v146, v34, v146
	v_mul_f32_e32 v147, v34, v147
	ds_write_b128 v209, v[144:147]
	v_mul_f32_e32 v148, v35, v148
	v_mul_f32_e32 v149, v35, v149
	v_mul_f32_e32 v150, v35, v150
	v_mul_f32_e32 v151, v35, v151
	ds_write_b128 v209, v[148:151] offset:1024
	v_mul_f32_e32 v152, v36, v152
	v_mul_f32_e32 v153, v36, v153
	v_mul_f32_e32 v154, v36, v154
	v_mul_f32_e32 v155, v36, v155
	ds_write_b128 v209, v[152:155] offset:2048
	v_mul_f32_e32 v156, v37, v156
	v_mul_f32_e32 v157, v37, v157
	v_mul_f32_e32 v158, v37, v158
	v_mul_f32_e32 v159, v37, v159
	ds_write_b128 v209, v[156:159] offset:3072
	v_mul_f32_e32 v160, v38, v160
	v_mul_f32_e32 v161, v38, v161
	v_mul_f32_e32 v162, v38, v162
	v_mul_f32_e32 v163, v38, v163
	ds_write_b128 v209, v[160:163] offset:4096
	v_mul_f32_e32 v164, v39, v164
	v_mul_f32_e32 v165, v39, v165
	v_mul_f32_e32 v166, v39, v166
	v_mul_f32_e32 v167, v39, v167
	ds_write_b128 v209, v[164:167] offset:5120
	v_mul_f32_e32 v168, v40, v168
	v_mul_f32_e32 v169, v40, v169
	v_mul_f32_e32 v170, v40, v170
	v_mul_f32_e32 v171, v40, v171
	ds_write_b128 v209, v[168:171] offset:6144
	v_mul_f32_e32 v172, v41, v172
	v_mul_f32_e32 v173, v41, v173
	v_mul_f32_e32 v174, v41, v174
	v_mul_f32_e32 v175, v41, v175
	ds_write_b128 v209, v[172:175] offset:7168
	s_waitcnt lgkmcnt(0)
	s_barrier
; #define GAS __attribute__((address_space(1)))
; #define LAS __attribute__((address_space(3)))
; #define LDS_WAIT() asm volatile("s_waitcnt lgkmcnt(0)" ::: "memory")
; __device__ __forceinline__ unsigned pk4_fp8(float a, float b, float c, float d) {
;     a = fminf(fmaxf(a, -448.f), 448.f); b = fminf(fmaxf(b, -448.f), 448.f); c = fminf(fmaxf(c, -448.f), 448.f); d = fminf(fmaxf(d, -448.f), 448.f);
;     int w = __builtin_amdgcn_cvt_pk_fp8_f32(a, b, 0, false); w = __builtin_amdgcn_cvt_pk_fp8_f32(c, d, w, true); return (unsigned)w; }
;     ...
;     for (int i = 0; i < 32; ++i) v[i] = sc >= 0 ? W[(size_t)(k0 + 2 * i + (lane >> 5)) * Nsrc + sc] : 0.f;
; #pragma unroll
;     for (int i = 0; i < 32; ++i) { const int k = k0 + 2 * i + (lane >> 5); float x = v[i] * wscale; if (KS) x *= (k < ksplit ? ksA[k] : ksB[k - ksplit]); scr[(2 * i + (lane >> 5)) * 33 + (lane & 31)] = x; }
;     LDS_WAIT(); asm volatile("" ::: "memory");
;     const int c = lane & 7;
; #pragma unroll
;     for (int j = 0; j < 4; ++j) { const int n = (lane >> 3) + 8 * j; const LAS float* s = scr + (8 * c) * 33 + n;
;         const unsigned long long o = (unsigned long long)pg8::pk4_fp8(s[0 * 33], s[1 * 33], s[2 * 33], s[3 * 33]) | ((unsigned long long)pg8::pk4_fp8(s[4 * 33], s[5 * 33], s[6 * 33], s[7 * 33]) << 32);
;         *(GAS unsigned long long*)(WT + (size_t)(n0 + n) * K + k0 + 8 * c) = o; }
	s_add_u32 s8, s34, 0x4000
	s_addc_u32 s9, s35, 0
	global_load_dwordx4 v[144:147], v74, s[8:9]
	s_add_u32 s8, s8, 0x20000
	s_addc_u32 s9, s9, 0
	global_load_dwordx4 v[148:151], v74, s[8:9]
	s_add_u32 s8, s8, 0x20000
	s_addc_u32 s9, s9, 0
	global_load_dwordx4 v[152:155], v74, s[8:9]
	s_add_u32 s8, s8, 0x20000
	s_addc_u32 s9, s9, 0
	global_load_dwordx4 v[156:159], v74, s[8:9]
	s_add_u32 s8, s8, 0x20000
	s_addc_u32 s9, s9, 0
	global_load_dwordx4 v[160:163], v74, s[8:9]
	s_add_u32 s8, s8, 0x20000
	s_addc_u32 s9, s9, 0
	global_load_dwordx4 v[164:167], v74, s[8:9]
	s_add_u32 s8, s8, 0x20000
	s_addc_u32 s9, s9, 0
	global_load_dwordx4 v[168:171], v74, s[8:9]
	s_add_u32 s8, s8, 0x20000
	s_addc_u32 s9, s9, 0
	global_load_dwordx4 v[172:175], v74, s[8:9]
	s_add_u32 s6, s36, 0x800000
	s_addc_u32 s7, s37, 0
	ds_read_b32 v226, v211
	ds_read_b32 v227, v211 offset:512
	ds_read_b32 v228, v211 offset:1024
	ds_read_b32 v229, v211 offset:1536
	ds_read_b32 v230, v211 offset:2048
	ds_read_b32 v231, v211 offset:2560
	ds_read_b32 v232, v211 offset:3072
	ds_read_b32 v233, v211 offset:3584
	ds_read_b32 v234, v211 offset:4096
	ds_read_b32 v235, v211 offset:4608
	ds_read_b32 v236, v211 offset:5120
	ds_read_b32 v237, v211 offset:5632
	ds_read_b32 v238, v211 offset:6144
	ds_read_b32 v239, v211 offset:6656
	ds_read_b32 v240, v211 offset:7168
	ds_read_b32 v241, v211 offset:7680
	s_waitcnt lgkmcnt(0)
	v_max_f32_e32 v226, v226, v226
	v_max_f32_e32 v227, v227, v227
	v_max_f32_e32 v228, v228, v228
	v_max_f32_e32 v229, v229, v229
	v_max_f32_e32 v230, v230, v230
	v_max_f32_e32 v231, v231, v231
	v_max_f32_e32 v232, v232, v232
	v_max_f32_e32 v233, v233, v233
	v_max_f32_e32 v234, v234, v234
	v_max_f32_e32 v235, v235, v235
	v_max_f32_e32 v236, v236, v236
	v_max_f32_e32 v237, v237, v237
	v_max_f32_e32 v238, v238, v238
	v_max_f32_e32 v239, v239, v239
	v_max_f32_e32 v240, v240, v240
	v_max_f32_e32 v241, v241, v241
	v_med3_f32 v226, v226, s62, v95
	v_med3_f32 v227, v227, s62, v95
	v_med3_f32 v228, v228, s62, v95
	v_med3_f32 v229, v229, s62, v95
	v_med3_f32 v230, v230, s62, v95
	v_med3_f32 v231, v231, s62, v95
	v_med3_f32 v232, v232, s62, v95
	v_med3_f32 v233, v233, s62, v95
	v_med3_f32 v234, v234, s62, v95
	v_med3_f32 v235, v235, s62, v95
	v_med3_f32 v236, v236, s62, v95
	v_med3_f32 v237, v237, s62, v95
	v_med3_f32 v238, v238, s62, v95
	v_med3_f32 v239, v239, s62, v95
	v_med3_f32 v240, v240, s62, v95
	v_med3_f32 v241, v241, s62, v95
	v_mov_b32_e32 v242, 0
	v_mov_b32_e32 v243, 0
	v_mov_b32_e32 v244, 0
	v_mov_b32_e32 v245, 0
	v_cvt_pk_fp8_f32 v242, v226, v227
	v_cvt_pk_fp8_f32 v243, v230, v231
	v_cvt_pk_fp8_f32 v244, v234, v235
	v_cvt_pk_fp8_f32 v245, v238, v239
	v_cvt_pk_fp8_f32 v242, v228, v229 op_sel:[0,0,1]
	v_cvt_pk_fp8_f32 v243, v232, v233 op_sel:[0,0,1]
	v_cvt_pk_fp8_f32 v244, v236, v237 op_sel:[0,0,1]
	v_cvt_pk_fp8_f32 v245, v240, v241 op_sel:[0,0,1]
	s_nop 0
	global_store_dwordx4 v77, v[242:245], s[6:7]
	ds_read_b32 v226, v213
	ds_read_b32 v227, v213 offset:512
	ds_read_b32 v228, v213 offset:1024
	ds_read_b32 v229, v213 offset:1536
	ds_read_b32 v230, v213 offset:2048
	ds_read_b32 v231, v213 offset:2560
	ds_read_b32 v232, v213 offset:3072
	ds_read_b32 v233, v213 offset:3584
	ds_read_b32 v234, v213 offset:4096
	ds_read_b32 v235, v213 offset:4608
	ds_read_b32 v236, v213 offset:5120
	ds_read_b32 v237, v213 offset:5632
	ds_read_b32 v238, v213 offset:6144
	ds_read_b32 v239, v213 offset:6656
	ds_read_b32 v240, v213 offset:7168
	ds_read_b32 v241, v213 offset:7680
	s_waitcnt lgkmcnt(0)
	v_max_f32_e32 v226, v226, v226
	v_max_f32_e32 v227, v227, v227
	v_max_f32_e32 v228, v228, v228
	v_max_f32_e32 v229, v229, v229
	v_max_f32_e32 v230, v230, v230
	v_max_f32_e32 v231, v231, v231
	v_max_f32_e32 v232, v232, v232
	v_max_f32_e32 v233, v233, v233
	v_max_f32_e32 v234, v234, v234
	v_max_f32_e32 v235, v235, v235
	v_max_f32_e32 v236, v236, v236
	v_max_f32_e32 v237, v237, v237
	v_max_f32_e32 v238, v238, v238
	v_max_f32_e32 v239, v239, v239
	v_max_f32_e32 v240, v240, v240
	v_max_f32_e32 v241, v241, v241
	v_med3_f32 v226, v226, s62, v95
	v_med3_f32 v227, v227, s62, v95
	v_med3_f32 v228, v228, s62, v95
	v_med3_f32 v229, v229, s62, v95
	v_med3_f32 v230, v230, s62, v95
	v_med3_f32 v231, v231, s62, v95
	v_med3_f32 v232, v232, s62, v95
	v_med3_f32 v233, v233, s62, v95
	v_med3_f32 v234, v234, s62, v95
	v_med3_f32 v235, v235, s62, v95
	v_med3_f32 v236, v236, s62, v95
	v_med3_f32 v237, v237, s62, v95
	v_med3_f32 v238, v238, s62, v95
	v_med3_f32 v239, v239, s62, v95
	v_med3_f32 v240, v240, s62, v95
	v_med3_f32 v241, v241, s62, v95
	v_mov_b32_e32 v242, 0
	v_mov_b32_e32 v243, 0
	v_mov_b32_e32 v244, 0
	v_mov_b32_e32 v245, 0
	v_cvt_pk_fp8_f32 v242, v226, v227
	v_cvt_pk_fp8_f32 v243, v230, v231
	v_cvt_pk_fp8_f32 v244, v234, v235
	v_cvt_pk_fp8_f32 v245, v238, v239
	v_cvt_pk_fp8_f32 v242, v228, v229 op_sel:[0,0,1]
	v_cvt_pk_fp8_f32 v243, v232, v233 op_sel:[0,0,1]
	v_cvt_pk_fp8_f32 v244, v236, v237 op_sel:[0,0,1]
	v_cvt_pk_fp8_f32 v245, v240, v241 op_sel:[0,0,1]
	s_nop 0
	global_store_dwordx4 v78, v[242:245], s[6:7]
	s_waitcnt vmcnt(12)
	v_mul_f32_e32 v176, v34, v176
	v_mul_f32_e32 v177, v34, v177
	v_mul_f32_e32 v178, v34, v178
	v_mul_f32_e32 v179, v34, v179
	ds_write_b128 v210, v[176:179]
	v_mul_f32_e32 v180, v35, v180
	v_mul_f32_e32 v181, v35, v181
	v_mul_f32_e32 v182, v35, v182
	v_mul_f32_e32 v183, v35, v183
	ds_write_b128 v210, v[180:183] offset:1024
	v_mul_f32_e32 v184, v36, v184
	v_mul_f32_e32 v185, v36, v185
	v_mul_f32_e32 v186, v36, v186
	v_mul_f32_e32 v187, v36, v187
	ds_write_b128 v210, v[184:187] offset:2048
	v_mul_f32_e32 v188, v37, v188
	v_mul_f32_e32 v189, v37, v189
	v_mul_f32_e32 v190, v37, v190
	v_mul_f32_e32 v191, v37, v191
	ds_write_b128 v210, v[188:191] offset:3072
	v_mul_f32_e32 v192, v38, v192
	v_mul_f32_e32 v193, v38, v193
	v_mul_f32_e32 v194, v38, v194
	v_mul_f32_e32 v195, v38, v195
	ds_write_b128 v210, v[192:195] offset:4096
	v_mul_f32_e32 v196, v39, v196
	v_mul_f32_e32 v197, v39, v197
	v_mul_f32_e32 v198, v39, v198
	v_mul_f32_e32 v199, v39, v199
	ds_write_b128 v210, v[196:199] offset:5120
	v_mul_f32_e32 v200, v40, v200
	v_mul_f32_e32 v201, v40, v201
	v_mul_f32_e32 v202, v40, v202
	v_mul_f32_e32 v203, v40, v203
	ds_write_b128 v210, v[200:203] offset:6144
	v_mul_f32_e32 v204, v41, v204
	v_mul_f32_e32 v205, v41, v205
	v_mul_f32_e32 v206, v41, v206
	v_mul_f32_e32 v207, v41, v207
	ds_write_b128 v210, v[204:207] offset:7168
	s_waitcnt lgkmcnt(0)
	s_barrier
; #define GAS __attribute__((address_space(1)))
; #define LAS __attribute__((address_space(3)))
; #define LDS_WAIT() asm volatile("s_waitcnt lgkmcnt(0)" ::: "memory")
; __device__ __forceinline__ unsigned pk4_fp8(float a, float b, float c, float d) {
;     a = fminf(fmaxf(a, -448.f), 448.f); b = fminf(fmaxf(b, -448.f), 448.f); c = fminf(fmaxf(c, -448.f), 448.f); d = fminf(fmaxf(d, -448.f), 448.f);
;     int w = __builtin_amdgcn_cvt_pk_fp8_f32(a, b, 0, false); w = __builtin_amdgcn_cvt_pk_fp8_f32(c, d, w, true); return (unsigned)w; }
;     ...
;     for (int i = 0; i < 32; ++i) v[i] = sc >= 0 ? W[(size_t)(k0 + 2 * i + (lane >> 5)) * Nsrc + sc] : 0.f;
; #pragma unroll
;     for (int i = 0; i < 32; ++i) { const int k = k0 + 2 * i + (lane >> 5); float x = v[i] * wscale; if (KS) x *= (k < ksplit ? ksA[k] : ksB[k - ksplit]); scr[(2 * i + (lane >> 5)) * 33 + (lane & 31)] = x; }
;     LDS_WAIT(); asm volatile("" ::: "memory");
;     const int c = lane & 7;
; #pragma unroll
;     for (int j = 0; j < 4; ++j) { const int n = (lane >> 3) + 8 * j; const LAS float* s = scr + (8 * c) * 33 + n;
;         const unsigned long long o = (unsigned long long)pg8::pk4_fp8(s[0 * 33], s[1 * 33], s[2 * 33], s[3 * 33]) | ((unsigned long long)pg8::pk4_fp8(s[4 * 33], s[5 * 33], s[6 * 33], s[7 * 33]) << 32);
;         *(GAS unsigned long long*)(WT + (size_t)(n0 + n) * K + k0 + 8 * c) = o; }
	s_add_u32 s8, s34, 0x5000
	s_addc_u32 s9, s35, 0
	global_load_dwordx4 v[176:179], v74, s[8:9]
	s_add_u32 s8, s8, 0x20000
	s_addc_u32 s9, s9, 0
	global_load_dwordx4 v[180:183], v74, s[8:9]
	s_add_u32 s8, s8, 0x20000
	s_addc_u32 s9, s9, 0
	global_load_dwordx4 v[184:187], v74, s[8:9]
	s_add_u32 s8, s8, 0x20000
	s_addc_u32 s9, s9, 0
	global_load_dwordx4 v[188:191], v74, s[8:9]
	s_add_u32 s8, s8, 0x20000
	s_addc_u32 s9, s9, 0
	global_load_dwordx4 v[192:195], v74, s[8:9]
	s_add_u32 s8, s8, 0x20000
	s_addc_u32 s9, s9, 0
	global_load_dwordx4 v[196:199], v74, s[8:9]
	s_add_u32 s8, s8, 0x20000
	s_addc_u32 s9, s9, 0
	global_load_dwordx4 v[200:203], v74, s[8:9]
	s_add_u32 s8, s8, 0x20000
	s_addc_u32 s9, s9, 0
	global_load_dwordx4 v[204:207], v74, s[8:9]
	s_add_u32 s6, s36, 0xc00000
	s_addc_u32 s7, s37, 0
	ds_read_b32 v226, v212
	ds_read_b32 v227, v212 offset:512
	ds_read_b32 v228, v212 offset:1024
	ds_read_b32 v229, v212 offset:1536
	ds_read_b32 v230, v212 offset:2048
	ds_read_b32 v231, v212 offset:2560
	ds_read_b32 v232, v212 offset:3072
	ds_read_b32 v233, v212 offset:3584
	ds_read_b32 v234, v212 offset:4096
	ds_read_b32 v235, v212 offset:4608
	ds_read_b32 v236, v212 offset:5120
	ds_read_b32 v237, v212 offset:5632
	ds_read_b32 v238, v212 offset:6144
	ds_read_b32 v239, v212 offset:6656
	ds_read_b32 v240, v212 offset:7168
	ds_read_b32 v241, v212 offset:7680
	s_waitcnt lgkmcnt(0)
	v_max_f32_e32 v226, v226, v226
	v_max_f32_e32 v227, v227, v227
	v_max_f32_e32 v228, v228, v228
	v_max_f32_e32 v229, v229, v229
	v_max_f32_e32 v230, v230, v230
	v_max_f32_e32 v231, v231, v231
	v_max_f32_e32 v232, v232, v232
	v_max_f32_e32 v233, v233, v233
	v_max_f32_e32 v234, v234, v234
	v_max_f32_e32 v235, v235, v235
	v_max_f32_e32 v236, v236, v236
	v_max_f32_e32 v237, v237, v237
	v_max_f32_e32 v238, v238, v238
	v_max_f32_e32 v239, v239, v239
	v_max_f32_e32 v240, v240, v240
	v_max_f32_e32 v241, v241, v241
	v_med3_f32 v226, v226, s62, v95
	v_med3_f32 v227, v227, s62, v95
	v_med3_f32 v228, v228, s62, v95
	v_med3_f32 v229, v229, s62, v95
	v_med3_f32 v230, v230, s62, v95
	v_med3_f32 v231, v231, s62, v95
	v_med3_f32 v232, v232, s62, v95
	v_med3_f32 v233, v233, s62, v95
	v_med3_f32 v234, v234, s62, v95
	v_med3_f32 v235, v235, s62, v95
	v_med3_f32 v236, v236, s62, v95
	v_med3_f32 v237, v237, s62, v95
	v_med3_f32 v238, v238, s62, v95
	v_med3_f32 v239, v239, s62, v95
	v_med3_f32 v240, v240, s62, v95
	v_med3_f32 v241, v241, s62, v95
	v_mov_b32_e32 v242, 0
	v_mov_b32_e32 v243, 0
	v_mov_b32_e32 v244, 0
	v_mov_b32_e32 v245, 0
	v_cvt_pk_fp8_f32 v242, v226, v227
	v_cvt_pk_fp8_f32 v243, v230, v231
	v_cvt_pk_fp8_f32 v244, v234, v235
	v_cvt_pk_fp8_f32 v245, v238, v239
	v_cvt_pk_fp8_f32 v242, v228, v229 op_sel:[0,0,1]
	v_cvt_pk_fp8_f32 v243, v232, v233 op_sel:[0,0,1]
	v_cvt_pk_fp8_f32 v244, v236, v237 op_sel:[0,0,1]
	v_cvt_pk_fp8_f32 v245, v240, v241 op_sel:[0,0,1]
	s_nop 0
	global_store_dwordx4 v77, v[242:245], s[6:7]
	ds_read_b32 v226, v214
	ds_read_b32 v227, v214 offset:512
	ds_read_b32 v228, v214 offset:1024
	ds_read_b32 v229, v214 offset:1536
	ds_read_b32 v230, v214 offset:2048
	ds_read_b32 v231, v214 offset:2560
	ds_read_b32 v232, v214 offset:3072
	ds_read_b32 v233, v214 offset:3584
	ds_read_b32 v234, v214 offset:4096
	ds_read_b32 v235, v214 offset:4608
	ds_read_b32 v236, v214 offset:5120
	ds_read_b32 v237, v214 offset:5632
	ds_read_b32 v238, v214 offset:6144
	ds_read_b32 v239, v214 offset:6656
	ds_read_b32 v240, v214 offset:7168
	ds_read_b32 v241, v214 offset:7680
	s_waitcnt lgkmcnt(0)
	v_max_f32_e32 v226, v226, v226
	v_max_f32_e32 v227, v227, v227
	v_max_f32_e32 v228, v228, v228
	v_max_f32_e32 v229, v229, v229
	v_max_f32_e32 v230, v230, v230
	v_max_f32_e32 v231, v231, v231
	v_max_f32_e32 v232, v232, v232
	v_max_f32_e32 v233, v233, v233
	v_max_f32_e32 v234, v234, v234
	v_max_f32_e32 v235, v235, v235
	v_max_f32_e32 v236, v236, v236
	v_max_f32_e32 v237, v237, v237
	v_max_f32_e32 v238, v238, v238
	v_max_f32_e32 v239, v239, v239
	v_max_f32_e32 v240, v240, v240
	v_max_f32_e32 v241, v241, v241
	v_med3_f32 v226, v226, s62, v95
	v_med3_f32 v227, v227, s62, v95
	v_med3_f32 v228, v228, s62, v95
	v_med3_f32 v229, v229, s62, v95
	v_med3_f32 v230, v230, s62, v95
	v_med3_f32 v231, v231, s62, v95
	v_med3_f32 v232, v232, s62, v95
	v_med3_f32 v233, v233, s62, v95
	v_med3_f32 v234, v234, s62, v95
	v_med3_f32 v235, v235, s62, v95
	v_med3_f32 v236, v236, s62, v95
	v_med3_f32 v237, v237, s62, v95
	v_med3_f32 v238, v238, s62, v95
	v_med3_f32 v239, v239, s62, v95
	v_med3_f32 v240, v240, s62, v95
	v_med3_f32 v241, v241, s62, v95
	v_mov_b32_e32 v242, 0
	v_mov_b32_e32 v243, 0
	v_mov_b32_e32 v244, 0
	v_mov_b32_e32 v245, 0
	v_cvt_pk_fp8_f32 v242, v226, v227
	v_cvt_pk_fp8_f32 v243, v230, v231
	v_cvt_pk_fp8_f32 v244, v234, v235
	v_cvt_pk_fp8_f32 v245, v238, v239
	v_cvt_pk_fp8_f32 v242, v228, v229 op_sel:[0,0,1]
	v_cvt_pk_fp8_f32 v243, v232, v233 op_sel:[0,0,1]
	v_cvt_pk_fp8_f32 v244, v236, v237 op_sel:[0,0,1]
	v_cvt_pk_fp8_f32 v245, v240, v241 op_sel:[0,0,1]
	s_nop 0
	global_store_dwordx4 v78, v[242:245], s[6:7]
	s_waitcnt vmcnt(12)
	v_mul_f32_e32 v144, v34, v144
	v_mul_f32_e32 v145, v34, v145
	v_mul_f32_e32 v146, v34, v146
	v_mul_f32_e32 v147, v34, v147
	ds_write_b128 v209, v[144:147]
	v_mul_f32_e32 v148, v35, v148
	v_mul_f32_e32 v149, v35, v149
	v_mul_f32_e32 v150, v35, v150
	v_mul_f32_e32 v151, v35, v151
	ds_write_b128 v209, v[148:151] offset:1024
	v_mul_f32_e32 v152, v36, v152
	v_mul_f32_e32 v153, v36, v153
	v_mul_f32_e32 v154, v36, v154
	v_mul_f32_e32 v155, v36, v155
	ds_write_b128 v209, v[152:155] offset:2048
	v_mul_f32_e32 v156, v37, v156
	v_mul_f32_e32 v157, v37, v157
	v_mul_f32_e32 v158, v37, v158
	v_mul_f32_e32 v159, v37, v159
	ds_write_b128 v209, v[156:159] offset:3072
	v_mul_f32_e32 v160, v38, v160
	v_mul_f32_e32 v161, v38, v161
	v_mul_f32_e32 v162, v38, v162
	v_mul_f32_e32 v163, v38, v163
	ds_write_b128 v209, v[160:163] offset:4096
	v_mul_f32_e32 v164, v39, v164
	v_mul_f32_e32 v165, v39, v165
	v_mul_f32_e32 v166, v39, v166
	v_mul_f32_e32 v167, v39, v167
	ds_write_b128 v209, v[164:167] offset:5120
	v_mul_f32_e32 v168, v40, v168
	v_mul_f32_e32 v169, v40, v169
	v_mul_f32_e32 v170, v40, v170
	v_mul_f32_e32 v171, v40, v171
	ds_write_b128 v209, v[168:171] offset:6144
	v_mul_f32_e32 v172, v41, v172
	v_mul_f32_e32 v173, v41, v173
	v_mul_f32_e32 v174, v41, v174
	v_mul_f32_e32 v175, v41, v175
	ds_write_b128 v209, v[172:175] offset:7168
	s_waitcnt lgkmcnt(0)
	s_barrier
; #define GAS __attribute__((address_space(1)))
; #define LAS __attribute__((address_space(3)))
; #define LDS_WAIT() asm volatile("s_waitcnt lgkmcnt(0)" ::: "memory")
; __device__ __forceinline__ unsigned pk4_fp8(float a, float b, float c, float d) {
;     a = fminf(fmaxf(a, -448.f), 448.f); b = fminf(fmaxf(b, -448.f), 448.f); c = fminf(fmaxf(c, -448.f), 448.f); d = fminf(fmaxf(d, -448.f), 448.f);
;     int w = __builtin_amdgcn_cvt_pk_fp8_f32(a, b, 0, false); w = __builtin_amdgcn_cvt_pk_fp8_f32(c, d, w, true); return (unsigned)w; }
;     ...
;     for (int i = 0; i < 32; ++i) v[i] = sc >= 0 ? W[(size_t)(k0 + 2 * i + (lane >> 5)) * Nsrc + sc] : 0.f;
; #pragma unroll
;     for (int i = 0; i < 32; ++i) { const int k = k0 + 2 * i + (lane >> 5); float x = v[i] * wscale; if (KS) x *= (k < ksplit ? ksA[k] : ksB[k - ksplit]); scr[(2 * i + (lane >> 5)) * 33 + (lane & 31)] = x; }
;     LDS_WAIT(); asm volatile("" ::: "memory");
;     const int c = lane & 7;
; #pragma unroll
;     for (int j = 0; j < 4; ++j) { const int n = (lane >> 3) + 8 * j; const LAS float* s = scr + (8 * c) * 33 + n;
;         const unsigned long long o = (unsigned long long)pg8::pk4_fp8(s[0 * 33], s[1 * 33], s[2 * 33], s[3 * 33]) | ((unsigned long long)pg8::pk4_fp8(s[4 * 33], s[5 * 33], s[6 * 33], s[7 * 33]) << 32);
;         *(GAS unsigned long long*)(WT + (size_t)(n0 + n) * K + k0 + 8 * c) = o; }
	s_add_u32 s8, s34, 0x6000
	s_addc_u32 s9, s35, 0
	global_load_dwordx4 v[144:147], v74, s[8:9]
	s_add_u32 s8, s8, 0x20000
	s_addc_u32 s9, s9, 0
	global_load_dwordx4 v[148:151], v74, s[8:9]
	s_add_u32 s8, s8, 0x20000
	s_addc_u32 s9, s9, 0
	global_load_dwordx4 v[152:155], v74, s[8:9]
	s_add_u32 s8, s8, 0x20000
	s_addc_u32 s9, s9, 0
	global_load_dwordx4 v[156:159], v74, s[8:9]
	s_add_u32 s8, s8, 0x20000
	s_addc_u32 s9, s9, 0
	global_load_dwordx4 v[160:163], v74, s[8:9]
	s_add_u32 s8, s8, 0x20000
	s_addc_u32 s9, s9, 0
	global_load_dwordx4 v[164:167], v74, s[8:9]
	s_add_u32 s8, s8, 0x20000
	s_addc_u32 s9, s9, 0
	global_load_dwordx4 v[168:171], v74, s[8:9]
	s_add_u32 s8, s8, 0x20000
	s_addc_u32 s9, s9, 0
	global_load_dwordx4 v[172:175], v74, s[8:9]
	s_add_u32 s6, s36, 0x1000000
	s_addc_u32 s7, s37, 0
	ds_read_b32 v226, v211
	ds_read_b32 v227, v211 offset:512
	ds_read_b32 v228, v211 offset:1024
	ds_read_b32 v229, v211 offset:1536
	ds_read_b32 v230, v211 offset:2048
	ds_read_b32 v231, v211 offset:2560
	ds_read_b32 v232, v211 offset:3072
	ds_read_b32 v233, v211 offset:3584
	ds_read_b32 v234, v211 offset:4096
	ds_read_b32 v235, v211 offset:4608
	ds_read_b32 v236, v211 offset:5120
	ds_read_b32 v237, v211 offset:5632
	ds_read_b32 v238, v211 offset:6144
	ds_read_b32 v239, v211 offset:6656
	ds_read_b32 v240, v211 offset:7168
	ds_read_b32 v241, v211 offset:7680
	s_waitcnt lgkmcnt(0)
	v_max_f32_e32 v226, v226, v226
	v_max_f32_e32 v227, v227, v227
	v_max_f32_e32 v228, v228, v228
	v_max_f32_e32 v229, v229, v229
	v_max_f32_e32 v230, v230, v230
	v_max_f32_e32 v231, v231, v231
	v_max_f32_e32 v232, v232, v232
	v_max_f32_e32 v233, v233, v233
	v_max_f32_e32 v234, v234, v234
	v_max_f32_e32 v235, v235, v235
	v_max_f32_e32 v236, v236, v236
	v_max_f32_e32 v237, v237, v237
	v_max_f32_e32 v238, v238, v238
	v_max_f32_e32 v239, v239, v239
	v_max_f32_e32 v240, v240, v240
	v_max_f32_e32 v241, v241, v241
	v_med3_f32 v226, v226, s62, v95
	v_med3_f32 v227, v227, s62, v95
	v_med3_f32 v228, v228, s62, v95
	v_med3_f32 v229, v229, s62, v95
	v_med3_f32 v230, v230, s62, v95
	v_med3_f32 v231, v231, s62, v95
	v_med3_f32 v232, v232, s62, v95
	v_med3_f32 v233, v233, s62, v95
	v_med3_f32 v234, v234, s62, v95
	v_med3_f32 v235, v235, s62, v95
	v_med3_f32 v236, v236, s62, v95
	v_med3_f32 v237, v237, s62, v95
	v_med3_f32 v238, v238, s62, v95
	v_med3_f32 v239, v239, s62, v95
	v_med3_f32 v240, v240, s62, v95
	v_med3_f32 v241, v241, s62, v95
	v_mov_b32_e32 v242, 0
	v_mov_b32_e32 v243, 0
	v_mov_b32_e32 v244, 0
	v_mov_b32_e32 v245, 0
	v_cvt_pk_fp8_f32 v242, v226, v227
	v_cvt_pk_fp8_f32 v243, v230, v231
	v_cvt_pk_fp8_f32 v244, v234, v235
	v_cvt_pk_fp8_f32 v245, v238, v239
	v_cvt_pk_fp8_f32 v242, v228, v229 op_sel:[0,0,1]
	v_cvt_pk_fp8_f32 v243, v232, v233 op_sel:[0,0,1]
	v_cvt_pk_fp8_f32 v244, v236, v237 op_sel:[0,0,1]
	v_cvt_pk_fp8_f32 v245, v240, v241 op_sel:[0,0,1]
	s_nop 0
	global_store_dwordx4 v77, v[242:245], s[6:7]
	ds_read_b32 v226, v213
	ds_read_b32 v227, v213 offset:512
	ds_read_b32 v228, v213 offset:1024
	ds_read_b32 v229, v213 offset:1536
	ds_read_b32 v230, v213 offset:2048
	ds_read_b32 v231, v213 offset:2560
	ds_read_b32 v232, v213 offset:3072
	ds_read_b32 v233, v213 offset:3584
	ds_read_b32 v234, v213 offset:4096
	ds_read_b32 v235, v213 offset:4608
	ds_read_b32 v236, v213 offset:5120
	ds_read_b32 v237, v213 offset:5632
	ds_read_b32 v238, v213 offset:6144
	ds_read_b32 v239, v213 offset:6656
	ds_read_b32 v240, v213 offset:7168
	ds_read_b32 v241, v213 offset:7680
	s_waitcnt lgkmcnt(0)
	v_max_f32_e32 v226, v226, v226
	v_max_f32_e32 v227, v227, v227
	v_max_f32_e32 v228, v228, v228
	v_max_f32_e32 v229, v229, v229
	v_max_f32_e32 v230, v230, v230
	v_max_f32_e32 v231, v231, v231
	v_max_f32_e32 v232, v232, v232
	v_max_f32_e32 v233, v233, v233
	v_max_f32_e32 v234, v234, v234
	v_max_f32_e32 v235, v235, v235
	v_max_f32_e32 v236, v236, v236
	v_max_f32_e32 v237, v237, v237
	v_max_f32_e32 v238, v238, v238
	v_max_f32_e32 v239, v239, v239
	v_max_f32_e32 v240, v240, v240
	v_max_f32_e32 v241, v241, v241
	v_med3_f32 v226, v226, s62, v95
	v_med3_f32 v227, v227, s62, v95
	v_med3_f32 v228, v228, s62, v95
	v_med3_f32 v229, v229, s62, v95
	v_med3_f32 v230, v230, s62, v95
	v_med3_f32 v231, v231, s62, v95
	v_med3_f32 v232, v232, s62, v95
	v_med3_f32 v233, v233, s62, v95
	v_med3_f32 v234, v234, s62, v95
	v_med3_f32 v235, v235, s62, v95
	v_med3_f32 v236, v236, s62, v95
	v_med3_f32 v237, v237, s62, v95
	v_med3_f32 v238, v238, s62, v95
	v_med3_f32 v239, v239, s62, v95
	v_med3_f32 v240, v240, s62, v95
	v_med3_f32 v241, v241, s62, v95
	v_mov_b32_e32 v242, 0
	v_mov_b32_e32 v243, 0
	v_mov_b32_e32 v244, 0
	v_mov_b32_e32 v245, 0
	v_cvt_pk_fp8_f32 v242, v226, v227
	v_cvt_pk_fp8_f32 v243, v230, v231
	v_cvt_pk_fp8_f32 v244, v234, v235
	v_cvt_pk_fp8_f32 v245, v238, v239
	v_cvt_pk_fp8_f32 v242, v228, v229 op_sel:[0,0,1]
	v_cvt_pk_fp8_f32 v243, v232, v233 op_sel:[0,0,1]
	v_cvt_pk_fp8_f32 v244, v236, v237 op_sel:[0,0,1]
	v_cvt_pk_fp8_f32 v245, v240, v241 op_sel:[0,0,1]
	s_nop 0
	global_store_dwordx4 v78, v[242:245], s[6:7]
	s_waitcnt vmcnt(12)
	v_mul_f32_e32 v176, v34, v176
	v_mul_f32_e32 v177, v34, v177
	v_mul_f32_e32 v178, v34, v178
	v_mul_f32_e32 v179, v34, v179
	ds_write_b128 v210, v[176:179]
	v_mul_f32_e32 v180, v35, v180
	v_mul_f32_e32 v181, v35, v181
	v_mul_f32_e32 v182, v35, v182
	v_mul_f32_e32 v183, v35, v183
	ds_write_b128 v210, v[180:183] offset:1024
	v_mul_f32_e32 v184, v36, v184
	v_mul_f32_e32 v185, v36, v185
	v_mul_f32_e32 v186, v36, v186
	v_mul_f32_e32 v187, v36, v187
	ds_write_b128 v210, v[184:187] offset:2048
	v_mul_f32_e32 v188, v37, v188
	v_mul_f32_e32 v189, v37, v189
	v_mul_f32_e32 v190, v37, v190
	v_mul_f32_e32 v191, v37, v191
	ds_write_b128 v210, v[188:191] offset:3072
	v_mul_f32_e32 v192, v38, v192
	v_mul_f32_e32 v193, v38, v193
	v_mul_f32_e32 v194, v38, v194
	v_mul_f32_e32 v195, v38, v195
	ds_write_b128 v210, v[192:195] offset:4096
	v_mul_f32_e32 v196, v39, v196
	v_mul_f32_e32 v197, v39, v197
	v_mul_f32_e32 v198, v39, v198
	v_mul_f32_e32 v199, v39, v199
	ds_write_b128 v210, v[196:199] offset:5120
	v_mul_f32_e32 v200, v40, v200
	v_mul_f32_e32 v201, v40, v201
	v_mul_f32_e32 v202, v40, v202
	v_mul_f32_e32 v203, v40, v203
	ds_write_b128 v210, v[200:203] offset:6144
	v_mul_f32_e32 v204, v41, v204
	v_mul_f32_e32 v205, v41, v205
	v_mul_f32_e32 v206, v41, v206
	v_mul_f32_e32 v207, v41, v207
	ds_write_b128 v210, v[204:207] offset:7168
	s_waitcnt lgkmcnt(0)
	s_barrier
; #define GAS __attribute__((address_space(1)))
; #define LAS __attribute__((address_space(3)))
; #define LDS_WAIT() asm volatile("s_waitcnt lgkmcnt(0)" ::: "memory")
; __device__ __forceinline__ unsigned pk4_fp8(float a, float b, float c, float d) {
;     a = fminf(fmaxf(a, -448.f), 448.f); b = fminf(fmaxf(b, -448.f), 448.f); c = fminf(fmaxf(c, -448.f), 448.f); d = fminf(fmaxf(d, -448.f), 448.f);
;     int w = __builtin_amdgcn_cvt_pk_fp8_f32(a, b, 0, false); w = __builtin_amdgcn_cvt_pk_fp8_f32(c, d, w, true); return (unsigned)w; }
;     ...
;     for (int i = 0; i < 32; ++i) v[i] = sc >= 0 ? W[(size_t)(k0 + 2 * i + (lane >> 5)) * Nsrc + sc] : 0.f;
; #pragma unroll
;     for (int i = 0; i < 32; ++i) { const int k = k0 + 2 * i + (lane >> 5); float x = v[i] * wscale; if (KS) x *= (k < ksplit ? ksA[k] : ksB[k - ksplit]); scr[(2 * i + (lane >> 5)) * 33 + (lane & 31)] = x; }
;     LDS_WAIT(); asm volatile("" ::: "memory");
;     const int c = lane & 7;
; #pragma unroll
;     for (int j = 0; j < 4; ++j) { const int n = (lane >> 3) + 8 * j; const LAS float* s = scr + (8 * c) * 33 + n;
;         const unsigned long long o = (unsigned long long)pg8::pk4_fp8(s[0 * 33], s[1 * 33], s[2 * 33], s[3 * 33]) | ((unsigned long long)pg8::pk4_fp8(s[4 * 33], s[5 * 33], s[6 * 33], s[7 * 33]) << 32);
;         *(GAS unsigned long long*)(WT + (size_t)(n0 + n) * K + k0 + 8 * c) = o; }
	s_add_u32 s8, s34, 0x7000
	s_addc_u32 s9, s35, 0
	global_load_dwordx4 v[176:179], v74, s[8:9]
	s_add_u32 s8, s8, 0x20000
	s_addc_u32 s9, s9, 0
	global_load_dwordx4 v[180:183], v74, s[8:9]
	s_add_u32 s8, s8, 0x20000
	s_addc_u32 s9, s9, 0
	global_load_dwordx4 v[184:187], v74, s[8:9]
	s_add_u32 s8, s8, 0x20000
	s_addc_u32 s9, s9, 0
	global_load_dwordx4 v[188:191], v74, s[8:9]
	s_add_u32 s8, s8, 0x20000
	s_addc_u32 s9, s9, 0
	global_load_dwordx4 v[192:195], v74, s[8:9]
	s_add_u32 s8, s8, 0x20000
	s_addc_u32 s9, s9, 0
	global_load_dwordx4 v[196:199], v74, s[8:9]
	s_add_u32 s8, s8, 0x20000
	s_addc_u32 s9, s9, 0
	global_load_dwordx4 v[200:203], v74, s[8:9]
	s_add_u32 s8, s8, 0x20000
	s_addc_u32 s9, s9, 0
	global_load_dwordx4 v[204:207], v74, s[8:9]
	s_add_u32 s6, s36, 0x1400000
	s_addc_u32 s7, s37, 0
	ds_read_b32 v226, v212
	ds_read_b32 v227, v212 offset:512
	ds_read_b32 v228, v212 offset:1024
	ds_read_b32 v229, v212 offset:1536
	ds_read_b32 v230, v212 offset:2048
	ds_read_b32 v231, v212 offset:2560
	ds_read_b32 v232, v212 offset:3072
	ds_read_b32 v233, v212 offset:3584
	ds_read_b32 v234, v212 offset:4096
	ds_read_b32 v235, v212 offset:4608
	ds_read_b32 v236, v212 offset:5120
	ds_read_b32 v237, v212 offset:5632
	ds_read_b32 v238, v212 offset:6144
	ds_read_b32 v239, v212 offset:6656
	ds_read_b32 v240, v212 offset:7168
	ds_read_b32 v241, v212 offset:7680
	s_waitcnt lgkmcnt(0)
	v_max_f32_e32 v226, v226, v226
	v_max_f32_e32 v227, v227, v227
	v_max_f32_e32 v228, v228, v228
	v_max_f32_e32 v229, v229, v229
	v_max_f32_e32 v230, v230, v230
	v_max_f32_e32 v231, v231, v231
	v_max_f32_e32 v232, v232, v232
	v_max_f32_e32 v233, v233, v233
	v_max_f32_e32 v234, v234, v234
	v_max_f32_e32 v235, v235, v235
	v_max_f32_e32 v236, v236, v236
	v_max_f32_e32 v237, v237, v237
	v_max_f32_e32 v238, v238, v238
	v_max_f32_e32 v239, v239, v239
	v_max_f32_e32 v240, v240, v240
	v_max_f32_e32 v241, v241, v241
	v_med3_f32 v226, v226, s62, v95
	v_med3_f32 v227, v227, s62, v95
	v_med3_f32 v228, v228, s62, v95
	v_med3_f32 v229, v229, s62, v95
	v_med3_f32 v230, v230, s62, v95
	v_med3_f32 v231, v231, s62, v95
	v_med3_f32 v232, v232, s62, v95
	v_med3_f32 v233, v233, s62, v95
	v_med3_f32 v234, v234, s62, v95
	v_med3_f32 v235, v235, s62, v95
	v_med3_f32 v236, v236, s62, v95
	v_med3_f32 v237, v237, s62, v95
	v_med3_f32 v238, v238, s62, v95
	v_med3_f32 v239, v239, s62, v95
	v_med3_f32 v240, v240, s62, v95
	v_med3_f32 v241, v241, s62, v95
	v_mov_b32_e32 v242, 0
	v_mov_b32_e32 v243, 0
	v_mov_b32_e32 v244, 0
	v_mov_b32_e32 v245, 0
	v_cvt_pk_fp8_f32 v242, v226, v227
	v_cvt_pk_fp8_f32 v243, v230, v231
	v_cvt_pk_fp8_f32 v244, v234, v235
	v_cvt_pk_fp8_f32 v245, v238, v239
	v_cvt_pk_fp8_f32 v242, v228, v229 op_sel:[0,0,1]
	v_cvt_pk_fp8_f32 v243, v232, v233 op_sel:[0,0,1]
	v_cvt_pk_fp8_f32 v244, v236, v237 op_sel:[0,0,1]
	v_cvt_pk_fp8_f32 v245, v240, v241 op_sel:[0,0,1]
	s_nop 0
	global_store_dwordx4 v77, v[242:245], s[6:7]
	ds_read_b32 v226, v214
	ds_read_b32 v227, v214 offset:512
	ds_read_b32 v228, v214 offset:1024
	ds_read_b32 v229, v214 offset:1536
	ds_read_b32 v230, v214 offset:2048
	ds_read_b32 v231, v214 offset:2560
	ds_read_b32 v232, v214 offset:3072
	ds_read_b32 v233, v214 offset:3584
	ds_read_b32 v234, v214 offset:4096
	ds_read_b32 v235, v214 offset:4608
	ds_read_b32 v236, v214 offset:5120
	ds_read_b32 v237, v214 offset:5632
	ds_read_b32 v238, v214 offset:6144
	ds_read_b32 v239, v214 offset:6656
	ds_read_b32 v240, v214 offset:7168
	ds_read_b32 v241, v214 offset:7680
	s_waitcnt lgkmcnt(0)
	v_max_f32_e32 v226, v226, v226
	v_max_f32_e32 v227, v227, v227
	v_max_f32_e32 v228, v228, v228
	v_max_f32_e32 v229, v229, v229
	v_max_f32_e32 v230, v230, v230
	v_max_f32_e32 v231, v231, v231
	v_max_f32_e32 v232, v232, v232
	v_max_f32_e32 v233, v233, v233
	v_max_f32_e32 v234, v234, v234
	v_max_f32_e32 v235, v235, v235
	v_max_f32_e32 v236, v236, v236
	v_max_f32_e32 v237, v237, v237
	v_max_f32_e32 v238, v238, v238
	v_max_f32_e32 v239, v239, v239
	v_max_f32_e32 v240, v240, v240
	v_max_f32_e32 v241, v241, v241
	v_med3_f32 v226, v226, s62, v95
	v_med3_f32 v227, v227, s62, v95
	v_med3_f32 v228, v228, s62, v95
	v_med3_f32 v229, v229, s62, v95
	v_med3_f32 v230, v230, s62, v95
	v_med3_f32 v231, v231, s62, v95
	v_med3_f32 v232, v232, s62, v95
	v_med3_f32 v233, v233, s62, v95
	v_med3_f32 v234, v234, s62, v95
	v_med3_f32 v235, v235, s62, v95
	v_med3_f32 v236, v236, s62, v95
	v_med3_f32 v237, v237, s62, v95
	v_med3_f32 v238, v238, s62, v95
	v_med3_f32 v239, v239, s62, v95
	v_med3_f32 v240, v240, s62, v95
	v_med3_f32 v241, v241, s62, v95
	v_mov_b32_e32 v242, 0
	v_mov_b32_e32 v243, 0
	v_mov_b32_e32 v244, 0
	v_mov_b32_e32 v245, 0
	v_cvt_pk_fp8_f32 v242, v226, v227
	v_cvt_pk_fp8_f32 v243, v230, v231
	v_cvt_pk_fp8_f32 v244, v234, v235
	v_cvt_pk_fp8_f32 v245, v238, v239
	v_cvt_pk_fp8_f32 v242, v228, v229 op_sel:[0,0,1]
	v_cvt_pk_fp8_f32 v243, v232, v233 op_sel:[0,0,1]
	v_cvt_pk_fp8_f32 v244, v236, v237 op_sel:[0,0,1]
	v_cvt_pk_fp8_f32 v245, v240, v241 op_sel:[0,0,1]
	s_nop 0
	global_store_dwordx4 v78, v[242:245], s[6:7]
	s_waitcnt vmcnt(12)
	v_mul_f32_e32 v144, v34, v144
	v_mul_f32_e32 v145, v34, v145
	v_mul_f32_e32 v146, v34, v146
	v_mul_f32_e32 v147, v34, v147
	ds_write_b128 v209, v[144:147]
	v_mul_f32_e32 v148, v35, v148
	v_mul_f32_e32 v149, v35, v149
	v_mul_f32_e32 v150, v35, v150
	v_mul_f32_e32 v151, v35, v151
	ds_write_b128 v209, v[148:151] offset:1024
	v_mul_f32_e32 v152, v36, v152
	v_mul_f32_e32 v153, v36, v153
	v_mul_f32_e32 v154, v36, v154
	v_mul_f32_e32 v155, v36, v155
	ds_write_b128 v209, v[152:155] offset:2048
	v_mul_f32_e32 v156, v37, v156
	v_mul_f32_e32 v157, v37, v157
	v_mul_f32_e32 v158, v37, v158
	v_mul_f32_e32 v159, v37, v159
	ds_write_b128 v209, v[156:159] offset:3072
	v_mul_f32_e32 v160, v38, v160
	v_mul_f32_e32 v161, v38, v161
	v_mul_f32_e32 v162, v38, v162
	v_mul_f32_e32 v163, v38, v163
	ds_write_b128 v209, v[160:163] offset:4096
	v_mul_f32_e32 v164, v39, v164
	v_mul_f32_e32 v165, v39, v165
	v_mul_f32_e32 v166, v39, v166
	v_mul_f32_e32 v167, v39, v167
	ds_write_b128 v209, v[164:167] offset:5120
	v_mul_f32_e32 v168, v40, v168
	v_mul_f32_e32 v169, v40, v169
	v_mul_f32_e32 v170, v40, v170
	v_mul_f32_e32 v171, v40, v171
	ds_write_b128 v209, v[168:171] offset:6144
	v_mul_f32_e32 v172, v41, v172
	v_mul_f32_e32 v173, v41, v173
	v_mul_f32_e32 v174, v41, v174
	v_mul_f32_e32 v175, v41, v175
	ds_write_b128 v209, v[172:175] offset:7168
	s_waitcnt lgkmcnt(0)
	s_barrier
; #define GAS __attribute__((address_space(1)))
; #define LAS __attribute__((address_space(3)))
; #define LDS_WAIT() asm volatile("s_waitcnt lgkmcnt(0)" ::: "memory")
; __device__ __forceinline__ unsigned pk4_fp8(float a, float b, float c, float d) {
;     a = fminf(fmaxf(a, -448.f), 448.f); b = fminf(fmaxf(b, -448.f), 448.f); c = fminf(fmaxf(c, -448.f), 448.f); d = fminf(fmaxf(d, -448.f), 448.f);
;     int w = __builtin_amdgcn_cvt_pk_fp8_f32(a, b, 0, false); w = __builtin_amdgcn_cvt_pk_fp8_f32(c, d, w, true); return (unsigned)w; }
;     ...
;     for (int i = 0; i < 32; ++i) v[i] = sc >= 0 ? W[(size_t)(k0 + 2 * i + (lane >> 5)) * Nsrc + sc] : 0.f;
; #pragma unroll
;     for (int i = 0; i < 32; ++i) { const int k = k0 + 2 * i + (lane >> 5); float x = v[i] * wscale; if (KS) x *= (k < ksplit ? ksA[k] : ksB[k - ksplit]); scr[(2 * i + (lane >> 5)) * 33 + (lane & 31)] = x; }
;     LDS_WAIT(); asm volatile("" ::: "memory");
;     const int c = lane & 7;
; #pragma unroll
;     for (int j = 0; j < 4; ++j) { const int n = (lane >> 3) + 8 * j; const LAS float* s = scr + (8 * c) * 33 + n;
;         const unsigned long long o = (unsigned long long)pg8::pk4_fp8(s[0 * 33], s[1 * 33], s[2 * 33], s[3 * 33]) | ((unsigned long long)pg8::pk4_fp8(s[4 * 33], s[5 * 33], s[6 * 33], s[7 * 33]) << 32);
;         *(GAS unsigned long long*)(WT + (size_t)(n0 + n) * K + k0 + 8 * c) = o; }
	s_add_u32 s8, s34, 0x8000
	s_addc_u32 s9, s35, 0
	global_load_dwordx4 v[144:147], v74, s[8:9]
	s_add_u32 s8, s8, 0x20000
	s_addc_u32 s9, s9, 0
	global_load_dwordx4 v[148:151], v74, s[8:9]
	s_add_u32 s8, s8, 0x20000
	s_addc_u32 s9, s9, 0
	global_load_dwordx4 v[152:155], v74, s[8:9]
	s_add_u32 s8, s8, 0x20000
	s_addc_u32 s9, s9, 0
	global_load_dwordx4 v[156:159], v74, s[8:9]
	s_add_u32 s8, s8, 0x20000
	s_addc_u32 s9, s9, 0
	global_load_dwordx4 v[160:163], v74, s[8:9]
	s_add_u32 s8, s8, 0x20000
	s_addc_u32 s9, s9, 0
	global_load_dwordx4 v[164:167], v74, s[8:9]
	s_add_u32 s8, s8, 0x20000
	s_addc_u32 s9, s9, 0
	global_load_dwordx4 v[168:171], v74, s[8:9]
	s_add_u32 s8, s8, 0x20000
	s_addc_u32 s9, s9, 0
	global_load_dwordx4 v[172:175], v74, s[8:9]
	s_add_u32 s6, s36, 0x1800000
	s_addc_u32 s7, s37, 0
	ds_read_b32 v226, v211
	ds_read_b32 v227, v211 offset:512
	ds_read_b32 v228, v211 offset:1024
	ds_read_b32 v229, v211 offset:1536
	ds_read_b32 v230, v211 offset:2048
	ds_read_b32 v231, v211 offset:2560
	ds_read_b32 v232, v211 offset:3072
	ds_read_b32 v233, v211 offset:3584
	ds_read_b32 v234, v211 offset:4096
	ds_read_b32 v235, v211 offset:4608
	ds_read_b32 v236, v211 offset:5120
	ds_read_b32 v237, v211 offset:5632
	ds_read_b32 v238, v211 offset:6144
	ds_read_b32 v239, v211 offset:6656
	ds_read_b32 v240, v211 offset:7168
	ds_read_b32 v241, v211 offset:7680
	s_waitcnt lgkmcnt(0)
	v_max_f32_e32 v226, v226, v226
	v_max_f32_e32 v227, v227, v227
	v_max_f32_e32 v228, v228, v228
	v_max_f32_e32 v229, v229, v229
	v_max_f32_e32 v230, v230, v230
	v_max_f32_e32 v231, v231, v231
	v_max_f32_e32 v232, v232, v232
	v_max_f32_e32 v233, v233, v233
	v_max_f32_e32 v234, v234, v234
	v_max_f32_e32 v235, v235, v235
	v_max_f32_e32 v236, v236, v236
	v_max_f32_e32 v237, v237, v237
	v_max_f32_e32 v238, v238, v238
	v_max_f32_e32 v239, v239, v239
	v_max_f32_e32 v240, v240, v240
	v_max_f32_e32 v241, v241, v241
	v_med3_f32 v226, v226, s62, v95
	v_med3_f32 v227, v227, s62, v95
	v_med3_f32 v228, v228, s62, v95
	v_med3_f32 v229, v229, s62, v95
	v_med3_f32 v230, v230, s62, v95
	v_med3_f32 v231, v231, s62, v95
	v_med3_f32 v232, v232, s62, v95
	v_med3_f32 v233, v233, s62, v95
	v_med3_f32 v234, v234, s62, v95
	v_med3_f32 v235, v235, s62, v95
	v_med3_f32 v236, v236, s62, v95
	v_med3_f32 v237, v237, s62, v95
	v_med3_f32 v238, v238, s62, v95
	v_med3_f32 v239, v239, s62, v95
	v_med3_f32 v240, v240, s62, v95
	v_med3_f32 v241, v241, s62, v95
	v_mov_b32_e32 v242, 0
	v_mov_b32_e32 v243, 0
	v_mov_b32_e32 v244, 0
	v_mov_b32_e32 v245, 0
	v_cvt_pk_fp8_f32 v242, v226, v227
	v_cvt_pk_fp8_f32 v243, v230, v231
	v_cvt_pk_fp8_f32 v244, v234, v235
	v_cvt_pk_fp8_f32 v245, v238, v239
	v_cvt_pk_fp8_f32 v242, v228, v229 op_sel:[0,0,1]
	v_cvt_pk_fp8_f32 v243, v232, v233 op_sel:[0,0,1]
	v_cvt_pk_fp8_f32 v244, v236, v237 op_sel:[0,0,1]
	v_cvt_pk_fp8_f32 v245, v240, v241 op_sel:[0,0,1]
	s_nop 0
	global_store_dwordx4 v77, v[242:245], s[6:7]
	ds_read_b32 v226, v213
	ds_read_b32 v227, v213 offset:512
	ds_read_b32 v228, v213 offset:1024
	ds_read_b32 v229, v213 offset:1536
	ds_read_b32 v230, v213 offset:2048
	ds_read_b32 v231, v213 offset:2560
	ds_read_b32 v232, v213 offset:3072
	ds_read_b32 v233, v213 offset:3584
	ds_read_b32 v234, v213 offset:4096
	ds_read_b32 v235, v213 offset:4608
	ds_read_b32 v236, v213 offset:5120
	ds_read_b32 v237, v213 offset:5632
	ds_read_b32 v238, v213 offset:6144
	ds_read_b32 v239, v213 offset:6656
	ds_read_b32 v240, v213 offset:7168
	ds_read_b32 v241, v213 offset:7680
	s_waitcnt lgkmcnt(0)
	v_max_f32_e32 v226, v226, v226
	v_max_f32_e32 v227, v227, v227
	v_max_f32_e32 v228, v228, v228
	v_max_f32_e32 v229, v229, v229
	v_max_f32_e32 v230, v230, v230
	v_max_f32_e32 v231, v231, v231
	v_max_f32_e32 v232, v232, v232
	v_max_f32_e32 v233, v233, v233
	v_max_f32_e32 v234, v234, v234
	v_max_f32_e32 v235, v235, v235
	v_max_f32_e32 v236, v236, v236
	v_max_f32_e32 v237, v237, v237
	v_max_f32_e32 v238, v238, v238
	v_max_f32_e32 v239, v239, v239
	v_max_f32_e32 v240, v240, v240
	v_max_f32_e32 v241, v241, v241
	v_med3_f32 v226, v226, s62, v95
	v_med3_f32 v227, v227, s62, v95
	v_med3_f32 v228, v228, s62, v95
	v_med3_f32 v229, v229, s62, v95
	v_med3_f32 v230, v230, s62, v95
	v_med3_f32 v231, v231, s62, v95
	v_med3_f32 v232, v232, s62, v95
	v_med3_f32 v233, v233, s62, v95
	v_med3_f32 v234, v234, s62, v95
	v_med3_f32 v235, v235, s62, v95
	v_med3_f32 v236, v236, s62, v95
	v_med3_f32 v237, v237, s62, v95
	v_med3_f32 v238, v238, s62, v95
	v_med3_f32 v239, v239, s62, v95
	v_med3_f32 v240, v240, s62, v95
	v_med3_f32 v241, v241, s62, v95
	v_mov_b32_e32 v242, 0
	v_mov_b32_e32 v243, 0
	v_mov_b32_e32 v244, 0
	v_mov_b32_e32 v245, 0
	v_cvt_pk_fp8_f32 v242, v226, v227
	v_cvt_pk_fp8_f32 v243, v230, v231
	v_cvt_pk_fp8_f32 v244, v234, v235
	v_cvt_pk_fp8_f32 v245, v238, v239
	v_cvt_pk_fp8_f32 v242, v228, v229 op_sel:[0,0,1]
	v_cvt_pk_fp8_f32 v243, v232, v233 op_sel:[0,0,1]
	v_cvt_pk_fp8_f32 v244, v236, v237 op_sel:[0,0,1]
	v_cvt_pk_fp8_f32 v245, v240, v241 op_sel:[0,0,1]
	s_nop 0
	global_store_dwordx4 v78, v[242:245], s[6:7]
	s_waitcnt vmcnt(12)
	v_mul_f32_e32 v176, v34, v176
	v_mul_f32_e32 v177, v34, v177
	v_mul_f32_e32 v178, v34, v178
	v_mul_f32_e32 v179, v34, v179
	ds_write_b128 v210, v[176:179]
	v_mul_f32_e32 v180, v35, v180
	v_mul_f32_e32 v181, v35, v181
	v_mul_f32_e32 v182, v35, v182
	v_mul_f32_e32 v183, v35, v183
	ds_write_b128 v210, v[180:183] offset:1024
	v_mul_f32_e32 v184, v36, v184
	v_mul_f32_e32 v185, v36, v185
	v_mul_f32_e32 v186, v36, v186
	v_mul_f32_e32 v187, v36, v187
	ds_write_b128 v210, v[184:187] offset:2048
	v_mul_f32_e32 v188, v37, v188
	v_mul_f32_e32 v189, v37, v189
	v_mul_f32_e32 v190, v37, v190
	v_mul_f32_e32 v191, v37, v191
	ds_write_b128 v210, v[188:191] offset:3072
	v_mul_f32_e32 v192, v38, v192
	v_mul_f32_e32 v193, v38, v193
	v_mul_f32_e32 v194, v38, v194
	v_mul_f32_e32 v195, v38, v195
	ds_write_b128 v210, v[192:195] offset:4096
	v_mul_f32_e32 v196, v39, v196
	v_mul_f32_e32 v197, v39, v197
	v_mul_f32_e32 v198, v39, v198
	v_mul_f32_e32 v199, v39, v199
	ds_write_b128 v210, v[196:199] offset:5120
	v_mul_f32_e32 v200, v40, v200
	v_mul_f32_e32 v201, v40, v201
	v_mul_f32_e32 v202, v40, v202
	v_mul_f32_e32 v203, v40, v203
	ds_write_b128 v210, v[200:203] offset:6144
	v_mul_f32_e32 v204, v41, v204
	v_mul_f32_e32 v205, v41, v205
	v_mul_f32_e32 v206, v41, v206
	v_mul_f32_e32 v207, v41, v207
	ds_write_b128 v210, v[204:207] offset:7168
	s_waitcnt lgkmcnt(0)
	s_barrier
; #define GAS __attribute__((address_space(1)))
; #define LAS __attribute__((address_space(3)))
; #define LDS_WAIT() asm volatile("s_waitcnt lgkmcnt(0)" ::: "memory")
; __device__ __forceinline__ unsigned pk4_fp8(float a, float b, float c, float d) {
;     a = fminf(fmaxf(a, -448.f), 448.f); b = fminf(fmaxf(b, -448.f), 448.f); c = fminf(fmaxf(c, -448.f), 448.f); d = fminf(fmaxf(d, -448.f), 448.f);
;     int w = __builtin_amdgcn_cvt_pk_fp8_f32(a, b, 0, false); w = __builtin_amdgcn_cvt_pk_fp8_f32(c, d, w, true); return (unsigned)w; }
;     ...
; #pragma unroll
;     for (int i = 0; i < 32; ++i) v[i] = sc >= 0 ? W[(size_t)(k0 + 2 * i + (lane >> 5)) * Nsrc + sc] : 0.f;
; #pragma unroll
;     for (int i = 0; i < 32; ++i) { const int k = k0 + 2 * i + (lane >> 5); float x = v[i] * wscale; if (KS) x *= (k < ksplit ? ksA[k] : ksB[k - ksplit]); scr[(2 * i + (lane >> 5)) * 33 + (lane & 31)] = x; }
;     LDS_WAIT(); asm volatile("" ::: "memory");
;     const int c = lane & 7;
; #pragma unroll
;     for (int j = 0; j < 4; ++j) { const int n = (lane >> 3) + 8 * j; const LAS float* s = scr + (8 * c) * 33 + n;
;         const unsigned long long o = (unsigned long long)pg8::pk4_fp8(s[0 * 33], s[1 * 33], s[2 * 33], s[3 * 33]) | ((unsigned long long)pg8::pk4_fp8(s[4 * 33], s[5 * 33], s[6 * 33], s[7 * 33]) << 32);
;         *(GAS unsigned long long*)(WT + (size_t)(n0 + n) * K + k0 + 8 * c) = o; }
	s_add_u32 s8, s34, 0x9000
	s_addc_u32 s9, s35, 0
	global_load_dwordx4 v[176:179], v74, s[8:9]
	s_add_u32 s8, s8, 0x20000
	s_addc_u32 s9, s9, 0
	global_load_dwordx4 v[180:183], v74, s[8:9]
	s_add_u32 s8, s8, 0x20000
	s_addc_u32 s9, s9, 0
	global_load_dwordx4 v[184:187], v74, s[8:9]
	s_add_u32 s8, s8, 0x20000
	s_addc_u32 s9, s9, 0
	global_load_dwordx4 v[188:191], v74, s[8:9]
	s_add_u32 s8, s8, 0x20000
	s_addc_u32 s9, s9, 0
	global_load_dwordx4 v[192:195], v74, s[8:9]
	s_add_u32 s8, s8, 0x20000
	s_addc_u32 s9, s9, 0
	global_load_dwordx4 v[196:199], v74, s[8:9]
	s_add_u32 s8, s8, 0x20000
	s_addc_u32 s9, s9, 0
	global_load_dwordx4 v[200:203], v74, s[8:9]
	s_add_u32 s8, s8, 0x20000
	s_addc_u32 s9, s9, 0
	global_load_dwordx4 v[204:207], v74, s[8:9]
	s_add_u32 s6, s36, 0x1c00000
	s_addc_u32 s7, s37, 0
	ds_read_b32 v226, v212
	ds_read_b32 v227, v212 offset:512
	ds_read_b32 v228, v212 offset:1024
	ds_read_b32 v229, v212 offset:1536
	ds_read_b32 v230, v212 offset:2048
	ds_read_b32 v231, v212 offset:2560
	ds_read_b32 v232, v212 offset:3072
	ds_read_b32 v233, v212 offset:3584
	ds_read_b32 v234, v212 offset:4096
	ds_read_b32 v235, v212 offset:4608
	ds_read_b32 v236, v212 offset:5120
	ds_read_b32 v237, v212 offset:5632
	ds_read_b32 v238, v212 offset:6144
	ds_read_b32 v239, v212 offset:6656
	ds_read_b32 v240, v212 offset:7168
	ds_read_b32 v241, v212 offset:7680
	s_waitcnt lgkmcnt(0)
	v_max_f32_e32 v226, v226, v226
	v_max_f32_e32 v227, v227, v227
	v_max_f32_e32 v228, v228, v228
	v_max_f32_e32 v229, v229, v229
	v_max_f32_e32 v230, v230, v230
	v_max_f32_e32 v231, v231, v231
	v_max_f32_e32 v232, v232, v232
	v_max_f32_e32 v233, v233, v233
	v_max_f32_e32 v234, v234, v234
	v_max_f32_e32 v235, v235, v235
	v_max_f32_e32 v236, v236, v236
	v_max_f32_e32 v237, v237, v237
	v_max_f32_e32 v238, v238, v238
	v_max_f32_e32 v239, v239, v239
	v_max_f32_e32 v240, v240, v240
	v_max_f32_e32 v241, v241, v241
	v_med3_f32 v226, v226, s62, v95
	v_med3_f32 v227, v227, s62, v95
	v_med3_f32 v228, v228, s62, v95
	v_med3_f32 v229, v229, s62, v95
	v_med3_f32 v230, v230, s62, v95
	v_med3_f32 v231, v231, s62, v95
	v_med3_f32 v232, v232, s62, v95
	v_med3_f32 v233, v233, s62, v95
	v_med3_f32 v234, v234, s62, v95
	v_med3_f32 v235, v235, s62, v95
	v_med3_f32 v236, v236, s62, v95
	v_med3_f32 v237, v237, s62, v95
	v_med3_f32 v238, v238, s62, v95
	v_med3_f32 v239, v239, s62, v95
	v_med3_f32 v240, v240, s62, v95
	v_med3_f32 v241, v241, s62, v95
	v_mov_b32_e32 v242, 0
	v_mov_b32_e32 v243, 0
	v_mov_b32_e32 v244, 0
	v_mov_b32_e32 v245, 0
	v_cvt_pk_fp8_f32 v242, v226, v227
	v_cvt_pk_fp8_f32 v243, v230, v231
	v_cvt_pk_fp8_f32 v244, v234, v235
	v_cvt_pk_fp8_f32 v245, v238, v239
	v_cvt_pk_fp8_f32 v242, v228, v229 op_sel:[0,0,1]
	v_cvt_pk_fp8_f32 v243, v232, v233 op_sel:[0,0,1]
	v_cvt_pk_fp8_f32 v244, v236, v237 op_sel:[0,0,1]
	v_cvt_pk_fp8_f32 v245, v240, v241 op_sel:[0,0,1]
	s_nop 0
	global_store_dwordx4 v77, v[242:245], s[6:7]
	ds_read_b32 v226, v214
	ds_read_b32 v227, v214 offset:512
	ds_read_b32 v228, v214 offset:1024
	ds_read_b32 v229, v214 offset:1536
	ds_read_b32 v230, v214 offset:2048
	ds_read_b32 v231, v214 offset:2560
	ds_read_b32 v232, v214 offset:3072
	ds_read_b32 v233, v214 offset:3584
	ds_read_b32 v234, v214 offset:4096
	ds_read_b32 v235, v214 offset:4608
	ds_read_b32 v236, v214 offset:5120
	ds_read_b32 v237, v214 offset:5632
	ds_read_b32 v238, v214 offset:6144
	ds_read_b32 v239, v214 offset:6656
	ds_read_b32 v240, v214 offset:7168
	ds_read_b32 v241, v214 offset:7680
	s_waitcnt lgkmcnt(0)
	v_max_f32_e32 v226, v226, v226
	v_max_f32_e32 v227, v227, v227
	v_max_f32_e32 v228, v228, v228
	v_max_f32_e32 v229, v229, v229
	v_max_f32_e32 v230, v230, v230
	v_max_f32_e32 v231, v231, v231
	v_max_f32_e32 v232, v232, v232
	v_max_f32_e32 v233, v233, v233
	v_max_f32_e32 v234, v234, v234
	v_max_f32_e32 v235, v235, v235
	v_max_f32_e32 v236, v236, v236
	v_max_f32_e32 v237, v237, v237
	v_max_f32_e32 v238, v238, v238
	v_max_f32_e32 v239, v239, v239
	v_max_f32_e32 v240, v240, v240
	v_max_f32_e32 v241, v241, v241
	v_med3_f32 v226, v226, s62, v95
	v_med3_f32 v227, v227, s62, v95
	v_med3_f32 v228, v228, s62, v95
	v_med3_f32 v229, v229, s62, v95
	v_med3_f32 v230, v230, s62, v95
	v_med3_f32 v231, v231, s62, v95
	v_med3_f32 v232, v232, s62, v95
	v_med3_f32 v233, v233, s62, v95
	v_med3_f32 v234, v234, s62, v95
	v_med3_f32 v235, v235, s62, v95
	v_med3_f32 v236, v236, s62, v95
	v_med3_f32 v237, v237, s62, v95
	v_med3_f32 v238, v238, s62, v95
	v_med3_f32 v239, v239, s62, v95
	v_med3_f32 v240, v240, s62, v95
	v_med3_f32 v241, v241, s62, v95
	v_mov_b32_e32 v242, 0
	v_mov_b32_e32 v243, 0
	v_mov_b32_e32 v244, 0
	v_mov_b32_e32 v245, 0
	v_cvt_pk_fp8_f32 v242, v226, v227
	v_cvt_pk_fp8_f32 v243, v230, v231
	v_cvt_pk_fp8_f32 v244, v234, v235
	v_cvt_pk_fp8_f32 v245, v238, v239
	v_cvt_pk_fp8_f32 v242, v228, v229 op_sel:[0,0,1]
	v_cvt_pk_fp8_f32 v243, v232, v233 op_sel:[0,0,1]
	v_cvt_pk_fp8_f32 v244, v236, v237 op_sel:[0,0,1]
	v_cvt_pk_fp8_f32 v245, v240, v241 op_sel:[0,0,1]
	s_nop 0
	global_store_dwordx4 v78, v[242:245], s[6:7]
	s_waitcnt vmcnt(12)
	v_mul_f32_e32 v144, v34, v144
	v_mul_f32_e32 v145, v34, v145
	v_mul_f32_e32 v146, v34, v146
	v_mul_f32_e32 v147, v34, v147
	ds_write_b128 v209, v[144:147]
	v_mul_f32_e32 v148, v35, v148
	v_mul_f32_e32 v149, v35, v149
	v_mul_f32_e32 v150, v35, v150
	v_mul_f32_e32 v151, v35, v151
	ds_write_b128 v209, v[148:151] offset:1024
	v_mul_f32_e32 v152, v36, v152
	v_mul_f32_e32 v153, v36, v153
	v_mul_f32_e32 v154, v36, v154
	v_mul_f32_e32 v155, v36, v155
	ds_write_b128 v209, v[152:155] offset:2048
	v_mul_f32_e32 v156, v37, v156
	v_mul_f32_e32 v157, v37, v157
	v_mul_f32_e32 v158, v37, v158
	v_mul_f32_e32 v159, v37, v159
	ds_write_b128 v209, v[156:159] offset:3072
	v_mul_f32_e32 v160, v38, v160
	v_mul_f32_e32 v161, v38, v161
	v_mul_f32_e32 v162, v38, v162
	v_mul_f32_e32 v163, v38, v163
	ds_write_b128 v209, v[160:163] offset:4096
	v_mul_f32_e32 v164, v39, v164
	v_mul_f32_e32 v165, v39, v165
	v_mul_f32_e32 v166, v39, v166
	v_mul_f32_e32 v167, v39, v167
	ds_write_b128 v209, v[164:167] offset:5120
	v_mul_f32_e32 v168, v40, v168
	v_mul_f32_e32 v169, v40, v169
	v_mul_f32_e32 v170, v40, v170
	v_mul_f32_e32 v171, v40, v171
	ds_write_b128 v209, v[168:171] offset:6144
	v_mul_f32_e32 v172, v41, v172
	v_mul_f32_e32 v173, v41, v173
	v_mul_f32_e32 v174, v41, v174
	v_mul_f32_e32 v175, v41, v175
	ds_write_b128 v209, v[172:175] offset:7168
	s_waitcnt lgkmcnt(0)
	s_barrier
; #define GAS __attribute__((address_space(1)))
; #define LAS __attribute__((address_space(3)))
; #define LDS_WAIT() asm volatile("s_waitcnt lgkmcnt(0)" ::: "memory")
; __device__ __forceinline__ unsigned pk4_fp8(float a, float b, float c, float d) {
;     a = fminf(fmaxf(a, -448.f), 448.f); b = fminf(fmaxf(b, -448.f), 448.f); c = fminf(fmaxf(c, -448.f), 448.f); d = fminf(fmaxf(d, -448.f), 448.f);
;     int w = __builtin_amdgcn_cvt_pk_fp8_f32(a, b, 0, false); w = __builtin_amdgcn_cvt_pk_fp8_f32(c, d, w, true); return (unsigned)w; }
;     ...
; #pragma unroll
;     for (int i = 0; i < 32; ++i) v[i] = sc >= 0 ? W[(size_t)(k0 + 2 * i + (lane >> 5)) * Nsrc + sc] : 0.f;
; #pragma unroll
;     for (int i = 0; i < 32; ++i) { const int k = k0 + 2 * i + (lane >> 5); float x = v[i] * wscale; if (KS) x *= (k < ksplit ? ksA[k] : ksB[k - ksplit]); scr[(2 * i + (lane >> 5)) * 33 + (lane & 31)] = x; }
;     LDS_WAIT(); asm volatile("" ::: "memory");
;     const int c = lane & 7;
; #pragma unroll
;     for (int j = 0; j < 4; ++j) { const int n = (lane >> 3) + 8 * j; const LAS float* s = scr + (8 * c) * 33 + n;
;         const unsigned long long o = (unsigned long long)pg8::pk4_fp8(s[0 * 33], s[1 * 33], s[2 * 33], s[3 * 33]) | ((unsigned long long)pg8::pk4_fp8(s[4 * 33], s[5 * 33], s[6 * 33], s[7 * 33]) << 32);
;         *(GAS unsigned long long*)(WT + (size_t)(n0 + n) * K + k0 + 8 * c) = o; }
	s_add_u32 s8, s34, 0xa000
	s_addc_u32 s9, s35, 0
	global_load_dwordx4 v[144:147], v74, s[8:9]
	s_add_u32 s8, s8, 0x20000
	s_addc_u32 s9, s9, 0
	global_load_dwordx4 v[148:151], v74, s[8:9]
	s_add_u32 s8, s8, 0x20000
	s_addc_u32 s9, s9, 0
	global_load_dwordx4 v[152:155], v74, s[8:9]
	s_add_u32 s8, s8, 0x20000
	s_addc_u32 s9, s9, 0
	global_load_dwordx4 v[156:159], v74, s[8:9]
	s_add_u32 s8, s8, 0x20000
	s_addc_u32 s9, s9, 0
	global_load_dwordx4 v[160:163], v74, s[8:9]
	s_add_u32 s8, s8, 0x20000
	s_addc_u32 s9, s9, 0
	global_load_dwordx4 v[164:167], v74, s[8:9]
	s_add_u32 s8, s8, 0x20000
	s_addc_u32 s9, s9, 0
	global_load_dwordx4 v[168:171], v74, s[8:9]
	s_add_u32 s8, s8, 0x20000
	s_addc_u32 s9, s9, 0
	global_load_dwordx4 v[172:175], v74, s[8:9]
	s_add_u32 s6, s36, 0x2000000
	s_addc_u32 s7, s37, 0
	ds_read_b32 v226, v211
	ds_read_b32 v227, v211 offset:512
	ds_read_b32 v228, v211 offset:1024
	ds_read_b32 v229, v211 offset:1536
	ds_read_b32 v230, v211 offset:2048
	ds_read_b32 v231, v211 offset:2560
	ds_read_b32 v232, v211 offset:3072
	ds_read_b32 v233, v211 offset:3584
	ds_read_b32 v234, v211 offset:4096
	ds_read_b32 v235, v211 offset:4608
	ds_read_b32 v236, v211 offset:5120
	ds_read_b32 v237, v211 offset:5632
	ds_read_b32 v238, v211 offset:6144
	ds_read_b32 v239, v211 offset:6656
	ds_read_b32 v240, v211 offset:7168
	ds_read_b32 v241, v211 offset:7680
	s_waitcnt lgkmcnt(0)
	v_max_f32_e32 v226, v226, v226
	v_max_f32_e32 v227, v227, v227
	v_max_f32_e32 v228, v228, v228
	v_max_f32_e32 v229, v229, v229
	v_max_f32_e32 v230, v230, v230
	v_max_f32_e32 v231, v231, v231
	v_max_f32_e32 v232, v232, v232
	v_max_f32_e32 v233, v233, v233
	v_max_f32_e32 v234, v234, v234
	v_max_f32_e32 v235, v235, v235
	v_max_f32_e32 v236, v236, v236
	v_max_f32_e32 v237, v237, v237
	v_max_f32_e32 v238, v238, v238
	v_max_f32_e32 v239, v239, v239
	v_max_f32_e32 v240, v240, v240
	v_max_f32_e32 v241, v241, v241
	v_med3_f32 v226, v226, s62, v95
	v_med3_f32 v227, v227, s62, v95
	v_med3_f32 v228, v228, s62, v95
	v_med3_f32 v229, v229, s62, v95
	v_med3_f32 v230, v230, s62, v95
	v_med3_f32 v231, v231, s62, v95
	v_med3_f32 v232, v232, s62, v95
	v_med3_f32 v233, v233, s62, v95
	v_med3_f32 v234, v234, s62, v95
	v_med3_f32 v235, v235, s62, v95
	v_med3_f32 v236, v236, s62, v95
	v_med3_f32 v237, v237, s62, v95
	v_med3_f32 v238, v238, s62, v95
	v_med3_f32 v239, v239, s62, v95
	v_med3_f32 v240, v240, s62, v95
	v_med3_f32 v241, v241, s62, v95
	v_mov_b32_e32 v242, 0
	v_mov_b32_e32 v243, 0
	v_mov_b32_e32 v244, 0
	v_mov_b32_e32 v245, 0
	v_cvt_pk_fp8_f32 v242, v226, v227
	v_cvt_pk_fp8_f32 v243, v230, v231
	v_cvt_pk_fp8_f32 v244, v234, v235
	v_cvt_pk_fp8_f32 v245, v238, v239
	v_cvt_pk_fp8_f32 v242, v228, v229 op_sel:[0,0,1]
	v_cvt_pk_fp8_f32 v243, v232, v233 op_sel:[0,0,1]
	v_cvt_pk_fp8_f32 v244, v236, v237 op_sel:[0,0,1]
	v_cvt_pk_fp8_f32 v245, v240, v241 op_sel:[0,0,1]
	s_nop 0
	global_store_dwordx4 v77, v[242:245], s[6:7]
	ds_read_b32 v226, v213
	ds_read_b32 v227, v213 offset:512
	ds_read_b32 v228, v213 offset:1024
	ds_read_b32 v229, v213 offset:1536
	ds_read_b32 v230, v213 offset:2048
	ds_read_b32 v231, v213 offset:2560
	ds_read_b32 v232, v213 offset:3072
	ds_read_b32 v233, v213 offset:3584
	ds_read_b32 v234, v213 offset:4096
	ds_read_b32 v235, v213 offset:4608
	ds_read_b32 v236, v213 offset:5120
	ds_read_b32 v237, v213 offset:5632
	ds_read_b32 v238, v213 offset:6144
	ds_read_b32 v239, v213 offset:6656
	ds_read_b32 v240, v213 offset:7168
	ds_read_b32 v241, v213 offset:7680
	s_waitcnt lgkmcnt(0)
	v_max_f32_e32 v226, v226, v226
	v_max_f32_e32 v227, v227, v227
	v_max_f32_e32 v228, v228, v228
	v_max_f32_e32 v229, v229, v229
	v_max_f32_e32 v230, v230, v230
	v_max_f32_e32 v231, v231, v231
	v_max_f32_e32 v232, v232, v232
	v_max_f32_e32 v233, v233, v233
	v_max_f32_e32 v234, v234, v234
	v_max_f32_e32 v235, v235, v235
	v_max_f32_e32 v236, v236, v236
	v_max_f32_e32 v237, v237, v237
	v_max_f32_e32 v238, v238, v238
	v_max_f32_e32 v239, v239, v239
	v_max_f32_e32 v240, v240, v240
	v_max_f32_e32 v241, v241, v241
	v_med3_f32 v226, v226, s62, v95
	v_med3_f32 v227, v227, s62, v95
	v_med3_f32 v228, v228, s62, v95
	v_med3_f32 v229, v229, s62, v95
	v_med3_f32 v230, v230, s62, v95
	v_med3_f32 v231, v231, s62, v95
	v_med3_f32 v232, v232, s62, v95
	v_med3_f32 v233, v233, s62, v95
	v_med3_f32 v234, v234, s62, v95
	v_med3_f32 v235, v235, s62, v95
	v_med3_f32 v236, v236, s62, v95
	v_med3_f32 v237, v237, s62, v95
	v_med3_f32 v238, v238, s62, v95
	v_med3_f32 v239, v239, s62, v95
	v_med3_f32 v240, v240, s62, v95
	v_med3_f32 v241, v241, s62, v95
	v_mov_b32_e32 v242, 0
	v_mov_b32_e32 v243, 0
	v_mov_b32_e32 v244, 0
	v_mov_b32_e32 v245, 0
	v_cvt_pk_fp8_f32 v242, v226, v227
	v_cvt_pk_fp8_f32 v243, v230, v231
	v_cvt_pk_fp8_f32 v244, v234, v235
	v_cvt_pk_fp8_f32 v245, v238, v239
	v_cvt_pk_fp8_f32 v242, v228, v229 op_sel:[0,0,1]
	v_cvt_pk_fp8_f32 v243, v232, v233 op_sel:[0,0,1]
	v_cvt_pk_fp8_f32 v244, v236, v237 op_sel:[0,0,1]
	v_cvt_pk_fp8_f32 v245, v240, v241 op_sel:[0,0,1]
	s_nop 0
	global_store_dwordx4 v78, v[242:245], s[6:7]
	s_waitcnt vmcnt(12)
	v_mul_f32_e32 v176, v34, v176
	v_mul_f32_e32 v177, v34, v177
	v_mul_f32_e32 v178, v34, v178
	v_mul_f32_e32 v179, v34, v179
	ds_write_b128 v210, v[176:179]
	v_mul_f32_e32 v180, v35, v180
	v_mul_f32_e32 v181, v35, v181
	v_mul_f32_e32 v182, v35, v182
	v_mul_f32_e32 v183, v35, v183
	ds_write_b128 v210, v[180:183] offset:1024
	v_mul_f32_e32 v184, v36, v184
	v_mul_f32_e32 v185, v36, v185
	v_mul_f32_e32 v186, v36, v186
	v_mul_f32_e32 v187, v36, v187
	ds_write_b128 v210, v[184:187] offset:2048
	v_mul_f32_e32 v188, v37, v188
	v_mul_f32_e32 v189, v37, v189
	v_mul_f32_e32 v190, v37, v190
	v_mul_f32_e32 v191, v37, v191
	ds_write_b128 v210, v[188:191] offset:3072
	v_mul_f32_e32 v192, v38, v192
	v_mul_f32_e32 v193, v38, v193
	v_mul_f32_e32 v194, v38, v194
	v_mul_f32_e32 v195, v38, v195
	ds_write_b128 v210, v[192:195] offset:4096
	v_mul_f32_e32 v196, v39, v196
	v_mul_f32_e32 v197, v39, v197
	v_mul_f32_e32 v198, v39, v198
	v_mul_f32_e32 v199, v39, v199
	ds_write_b128 v210, v[196:199] offset:5120
	v_mul_f32_e32 v200, v40, v200
	v_mul_f32_e32 v201, v40, v201
	v_mul_f32_e32 v202, v40, v202
	v_mul_f32_e32 v203, v40, v203
	ds_write_b128 v210, v[200:203] offset:6144
	v_mul_f32_e32 v204, v41, v204
	v_mul_f32_e32 v205, v41, v205
	v_mul_f32_e32 v206, v41, v206
	v_mul_f32_e32 v207, v41, v207
	ds_write_b128 v210, v[204:207] offset:7168
	s_waitcnt lgkmcnt(0)
	s_barrier
; #define GAS __attribute__((address_space(1)))
; #define LAS __attribute__((address_space(3)))
; #define LDS_WAIT() asm volatile("s_waitcnt lgkmcnt(0)" ::: "memory")
; __device__ __forceinline__ unsigned pk4_fp8(float a, float b, float c, float d) {
;     a = fminf(fmaxf(a, -448.f), 448.f); b = fminf(fmaxf(b, -448.f), 448.f); c = fminf(fmaxf(c, -448.f), 448.f); d = fminf(fmaxf(d, -448.f), 448.f);
;     int w = __builtin_amdgcn_cvt_pk_fp8_f32(a, b, 0, false); w = __builtin_amdgcn_cvt_pk_fp8_f32(c, d, w, true); return (unsigned)w; }
;     ...
; #pragma unroll
;     for (int i = 0; i < 32; ++i) v[i] = sc >= 0 ? W[(size_t)(k0 + 2 * i + (lane >> 5)) * Nsrc + sc] : 0.f;
; #pragma unroll
;     for (int i = 0; i < 32; ++i) { const int k = k0 + 2 * i + (lane >> 5); float x = v[i] * wscale; if (KS) x *= (k < ksplit ? ksA[k] : ksB[k - ksplit]); scr[(2 * i + (lane >> 5)) * 33 + (lane & 31)] = x; }
;     LDS_WAIT(); asm volatile("" ::: "memory");
;     const int c = lane & 7;
; #pragma unroll
;     for (int j = 0; j < 4; ++j) { const int n = (lane >> 3) + 8 * j; const LAS float* s = scr + (8 * c) * 33 + n;
;         const unsigned long long o = (unsigned long long)pg8::pk4_fp8(s[0 * 33], s[1 * 33], s[2 * 33], s[3 * 33]) | ((unsigned long long)pg8::pk4_fp8(s[4 * 33], s[5 * 33], s[6 * 33], s[7 * 33]) << 32);
;         *(GAS unsigned long long*)(WT + (size_t)(n0 + n) * K + k0 + 8 * c) = o; }
	s_add_u32 s8, s34, 0xb000
	s_addc_u32 s9, s35, 0
	global_load_dwordx4 v[176:179], v74, s[8:9]
	s_add_u32 s8, s8, 0x20000
	s_addc_u32 s9, s9, 0
	global_load_dwordx4 v[180:183], v74, s[8:9]
	s_add_u32 s8, s8, 0x20000
	s_addc_u32 s9, s9, 0
	global_load_dwordx4 v[184:187], v74, s[8:9]
	s_add_u32 s8, s8, 0x20000
	s_addc_u32 s9, s9, 0
	global_load_dwordx4 v[188:191], v74, s[8:9]
	s_add_u32 s8, s8, 0x20000
	s_addc_u32 s9, s9, 0
	global_load_dwordx4 v[192:195], v74, s[8:9]
	s_add_u32 s8, s8, 0x20000
	s_addc_u32 s9, s9, 0
	global_load_dwordx4 v[196:199], v74, s[8:9]
	s_add_u32 s8, s8, 0x20000
	s_addc_u32 s9, s9, 0
	global_load_dwordx4 v[200:203], v74, s[8:9]
	s_add_u32 s8, s8, 0x20000
	s_addc_u32 s9, s9, 0
	global_load_dwordx4 v[204:207], v74, s[8:9]
	s_add_u32 s6, s36, 0x2400000
	s_addc_u32 s7, s37, 0
	ds_read_b32 v226, v212
	ds_read_b32 v227, v212 offset:512
	ds_read_b32 v228, v212 offset:1024
	ds_read_b32 v229, v212 offset:1536
	ds_read_b32 v230, v212 offset:2048
	ds_read_b32 v231, v212 offset:2560
	ds_read_b32 v232, v212 offset:3072
	ds_read_b32 v233, v212 offset:3584
	ds_read_b32 v234, v212 offset:4096
	ds_read_b32 v235, v212 offset:4608
	ds_read_b32 v236, v212 offset:5120
	ds_read_b32 v237, v212 offset:5632
	ds_read_b32 v238, v212 offset:6144
	ds_read_b32 v239, v212 offset:6656
	ds_read_b32 v240, v212 offset:7168
	ds_read_b32 v241, v212 offset:7680
	s_waitcnt lgkmcnt(0)
	v_max_f32_e32 v226, v226, v226
	v_max_f32_e32 v227, v227, v227
	v_max_f32_e32 v228, v228, v228
	v_max_f32_e32 v229, v229, v229
	v_max_f32_e32 v230, v230, v230
	v_max_f32_e32 v231, v231, v231
	v_max_f32_e32 v232, v232, v232
	v_max_f32_e32 v233, v233, v233
	v_max_f32_e32 v234, v234, v234
	v_max_f32_e32 v235, v235, v235
	v_max_f32_e32 v236, v236, v236
	v_max_f32_e32 v237, v237, v237
	v_max_f32_e32 v238, v238, v238
	v_max_f32_e32 v239, v239, v239
	v_max_f32_e32 v240, v240, v240
	v_max_f32_e32 v241, v241, v241
	v_med3_f32 v226, v226, s62, v95
	v_med3_f32 v227, v227, s62, v95
	v_med3_f32 v228, v228, s62, v95
	v_med3_f32 v229, v229, s62, v95
	v_med3_f32 v230, v230, s62, v95
	v_med3_f32 v231, v231, s62, v95
	v_med3_f32 v232, v232, s62, v95
	v_med3_f32 v233, v233, s62, v95
	v_med3_f32 v234, v234, s62, v95
	v_med3_f32 v235, v235, s62, v95
	v_med3_f32 v236, v236, s62, v95
	v_med3_f32 v237, v237, s62, v95
	v_med3_f32 v238, v238, s62, v95
	v_med3_f32 v239, v239, s62, v95
	v_med3_f32 v240, v240, s62, v95
	v_med3_f32 v241, v241, s62, v95
	v_mov_b32_e32 v242, 0
	v_mov_b32_e32 v243, 0
	v_mov_b32_e32 v244, 0
	v_mov_b32_e32 v245, 0
	v_cvt_pk_fp8_f32 v242, v226, v227
	v_cvt_pk_fp8_f32 v243, v230, v231
	v_cvt_pk_fp8_f32 v244, v234, v235
	v_cvt_pk_fp8_f32 v245, v238, v239
	v_cvt_pk_fp8_f32 v242, v228, v229 op_sel:[0,0,1]
	v_cvt_pk_fp8_f32 v243, v232, v233 op_sel:[0,0,1]
	v_cvt_pk_fp8_f32 v244, v236, v237 op_sel:[0,0,1]
	v_cvt_pk_fp8_f32 v245, v240, v241 op_sel:[0,0,1]
	s_nop 0
	global_store_dwordx4 v77, v[242:245], s[6:7]
	ds_read_b32 v226, v214
	ds_read_b32 v227, v214 offset:512
	ds_read_b32 v228, v214 offset:1024
	ds_read_b32 v229, v214 offset:1536
	ds_read_b32 v230, v214 offset:2048
	ds_read_b32 v231, v214 offset:2560
	ds_read_b32 v232, v214 offset:3072
	ds_read_b32 v233, v214 offset:3584
	ds_read_b32 v234, v214 offset:4096
	ds_read_b32 v235, v214 offset:4608
	ds_read_b32 v236, v214 offset:5120
	ds_read_b32 v237, v214 offset:5632
	ds_read_b32 v238, v214 offset:6144
	ds_read_b32 v239, v214 offset:6656
	ds_read_b32 v240, v214 offset:7168
	ds_read_b32 v241, v214 offset:7680
	s_waitcnt lgkmcnt(0)
	v_max_f32_e32 v226, v226, v226
	v_max_f32_e32 v227, v227, v227
	v_max_f32_e32 v228, v228, v228
	v_max_f32_e32 v229, v229, v229
	v_max_f32_e32 v230, v230, v230
	v_max_f32_e32 v231, v231, v231
	v_max_f32_e32 v232, v232, v232
	v_max_f32_e32 v233, v233, v233
	v_max_f32_e32 v234, v234, v234
	v_max_f32_e32 v235, v235, v235
	v_max_f32_e32 v236, v236, v236
	v_max_f32_e32 v237, v237, v237
	v_max_f32_e32 v238, v238, v238
	v_max_f32_e32 v239, v239, v239
	v_max_f32_e32 v240, v240, v240
	v_max_f32_e32 v241, v241, v241
	v_med3_f32 v226, v226, s62, v95
	v_med3_f32 v227, v227, s62, v95
	v_med3_f32 v228, v228, s62, v95
	v_med3_f32 v229, v229, s62, v95
	v_med3_f32 v230, v230, s62, v95
	v_med3_f32 v231, v231, s62, v95
	v_med3_f32 v232, v232, s62, v95
	v_med3_f32 v233, v233, s62, v95
	v_med3_f32 v234, v234, s62, v95
	v_med3_f32 v235, v235, s62, v95
	v_med3_f32 v236, v236, s62, v95
	v_med3_f32 v237, v237, s62, v95
	v_med3_f32 v238, v238, s62, v95
	v_med3_f32 v239, v239, s62, v95
	v_med3_f32 v240, v240, s62, v95
	v_med3_f32 v241, v241, s62, v95
	v_mov_b32_e32 v242, 0
	v_mov_b32_e32 v243, 0
	v_mov_b32_e32 v244, 0
	v_mov_b32_e32 v245, 0
	v_cvt_pk_fp8_f32 v242, v226, v227
	v_cvt_pk_fp8_f32 v243, v230, v231
	v_cvt_pk_fp8_f32 v244, v234, v235
	v_cvt_pk_fp8_f32 v245, v238, v239
	v_cvt_pk_fp8_f32 v242, v228, v229 op_sel:[0,0,1]
	v_cvt_pk_fp8_f32 v243, v232, v233 op_sel:[0,0,1]
	v_cvt_pk_fp8_f32 v244, v236, v237 op_sel:[0,0,1]
	v_cvt_pk_fp8_f32 v245, v240, v241 op_sel:[0,0,1]
	s_nop 0
	global_store_dwordx4 v78, v[242:245], s[6:7]
	s_waitcnt vmcnt(12)
	v_mul_f32_e32 v144, v34, v144
	v_mul_f32_e32 v145, v34, v145
	v_mul_f32_e32 v146, v34, v146
	v_mul_f32_e32 v147, v34, v147
	ds_write_b128 v209, v[144:147]
	v_mul_f32_e32 v148, v35, v148
	v_mul_f32_e32 v149, v35, v149
	v_mul_f32_e32 v150, v35, v150
	v_mul_f32_e32 v151, v35, v151
	ds_write_b128 v209, v[148:151] offset:1024
	v_mul_f32_e32 v152, v36, v152
	v_mul_f32_e32 v153, v36, v153
	v_mul_f32_e32 v154, v36, v154
	v_mul_f32_e32 v155, v36, v155
	ds_write_b128 v209, v[152:155] offset:2048
	v_mul_f32_e32 v156, v37, v156
	v_mul_f32_e32 v157, v37, v157
	v_mul_f32_e32 v158, v37, v158
	v_mul_f32_e32 v159, v37, v159
	ds_write_b128 v209, v[156:159] offset:3072
	v_mul_f32_e32 v160, v38, v160
	v_mul_f32_e32 v161, v38, v161
	v_mul_f32_e32 v162, v38, v162
	v_mul_f32_e32 v163, v38, v163
	ds_write_b128 v209, v[160:163] offset:4096
	v_mul_f32_e32 v164, v39, v164
	v_mul_f32_e32 v165, v39, v165
	v_mul_f32_e32 v166, v39, v166
	v_mul_f32_e32 v167, v39, v167
	ds_write_b128 v209, v[164:167] offset:5120
	v_mul_f32_e32 v168, v40, v168
	v_mul_f32_e32 v169, v40, v169
	v_mul_f32_e32 v170, v40, v170
	v_mul_f32_e32 v171, v40, v171
	ds_write_b128 v209, v[168:171] offset:6144
	v_mul_f32_e32 v172, v41, v172
	v_mul_f32_e32 v173, v41, v173
	v_mul_f32_e32 v174, v41, v174
	v_mul_f32_e32 v175, v41, v175
	ds_write_b128 v209, v[172:175] offset:7168
	s_waitcnt lgkmcnt(0)
	s_barrier
; #define GAS __attribute__((address_space(1)))
; #define LAS __attribute__((address_space(3)))
; #define LDS_WAIT() asm volatile("s_waitcnt lgkmcnt(0)" ::: "memory")
; __device__ __forceinline__ unsigned pk4_fp8(float a, float b, float c, float d) {
;     a = fminf(fmaxf(a, -448.f), 448.f); b = fminf(fmaxf(b, -448.f), 448.f); c = fminf(fmaxf(c, -448.f), 448.f); d = fminf(fmaxf(d, -448.f), 448.f);
;     int w = __builtin_amdgcn_cvt_pk_fp8_f32(a, b, 0, false); w = __builtin_amdgcn_cvt_pk_fp8_f32(c, d, w, true); return (unsigned)w; }
;     ...
; #pragma unroll
;     for (int i = 0; i < 32; ++i) v[i] = sc >= 0 ? W[(size_t)(k0 + 2 * i + (lane >> 5)) * Nsrc + sc] : 0.f;
; #pragma unroll
;     for (int i = 0; i < 32; ++i) { const int k = k0 + 2 * i + (lane >> 5); float x = v[i] * wscale; if (KS) x *= (k < ksplit ? ksA[k] : ksB[k - ksplit]); scr[(2 * i + (lane >> 5)) * 33 + (lane & 31)] = x; }
;     LDS_WAIT(); asm volatile("" ::: "memory");
;     const int c = lane & 7;
; #pragma unroll
;     for (int j = 0; j < 4; ++j) { const int n = (lane >> 3) + 8 * j; const LAS float* s = scr + (8 * c) * 33 + n;
;         const unsigned long long o = (unsigned long long)pg8::pk4_fp8(s[0 * 33], s[1 * 33], s[2 * 33], s[3 * 33]) | ((unsigned long long)pg8::pk4_fp8(s[4 * 33], s[5 * 33], s[6 * 33], s[7 * 33]) << 32);
;         *(GAS unsigned long long*)(WT + (size_t)(n0 + n) * K + k0 + 8 * c) = o; }
	s_add_u32 s8, s34, 0xc000
	s_addc_u32 s9, s35, 0
	global_load_dwordx4 v[144:147], v74, s[8:9]
	s_add_u32 s8, s8, 0x20000
	s_addc_u32 s9, s9, 0
	global_load_dwordx4 v[148:151], v74, s[8:9]
	s_add_u32 s8, s8, 0x20000
	s_addc_u32 s9, s9, 0
	global_load_dwordx4 v[152:155], v74, s[8:9]
	s_add_u32 s8, s8, 0x20000
	s_addc_u32 s9, s9, 0
	global_load_dwordx4 v[156:159], v74, s[8:9]
	s_add_u32 s8, s8, 0x20000
	s_addc_u32 s9, s9, 0
	global_load_dwordx4 v[160:163], v74, s[8:9]
	s_add_u32 s8, s8, 0x20000
	s_addc_u32 s9, s9, 0
	global_load_dwordx4 v[164:167], v74, s[8:9]
	s_add_u32 s8, s8, 0x20000
	s_addc_u32 s9, s9, 0
	global_load_dwordx4 v[168:171], v74, s[8:9]
	s_add_u32 s8, s8, 0x20000
	s_addc_u32 s9, s9, 0
	global_load_dwordx4 v[172:175], v74, s[8:9]
	s_add_u32 s6, s36, 0x2800000
	s_addc_u32 s7, s37, 0
	ds_read_b32 v226, v211
	ds_read_b32 v227, v211 offset:512
	ds_read_b32 v228, v211 offset:1024
	ds_read_b32 v229, v211 offset:1536
	ds_read_b32 v230, v211 offset:2048
	ds_read_b32 v231, v211 offset:2560
	ds_read_b32 v232, v211 offset:3072
	ds_read_b32 v233, v211 offset:3584
	ds_read_b32 v234, v211 offset:4096
	ds_read_b32 v235, v211 offset:4608
	ds_read_b32 v236, v211 offset:5120
	ds_read_b32 v237, v211 offset:5632
	ds_read_b32 v238, v211 offset:6144
	ds_read_b32 v239, v211 offset:6656
	ds_read_b32 v240, v211 offset:7168
	ds_read_b32 v241, v211 offset:7680
	s_waitcnt lgkmcnt(0)
	v_max_f32_e32 v226, v226, v226
	v_max_f32_e32 v227, v227, v227
	v_max_f32_e32 v228, v228, v228
	v_max_f32_e32 v229, v229, v229
	v_max_f32_e32 v230, v230, v230
	v_max_f32_e32 v231, v231, v231
	v_max_f32_e32 v232, v232, v232
	v_max_f32_e32 v233, v233, v233
	v_max_f32_e32 v234, v234, v234
	v_max_f32_e32 v235, v235, v235
	v_max_f32_e32 v236, v236, v236
	v_max_f32_e32 v237, v237, v237
	v_max_f32_e32 v238, v238, v238
	v_max_f32_e32 v239, v239, v239
	v_max_f32_e32 v240, v240, v240
	v_max_f32_e32 v241, v241, v241
	v_med3_f32 v226, v226, s62, v95
	v_med3_f32 v227, v227, s62, v95
	v_med3_f32 v228, v228, s62, v95
	v_med3_f32 v229, v229, s62, v95
	v_med3_f32 v230, v230, s62, v95
	v_med3_f32 v231, v231, s62, v95
	v_med3_f32 v232, v232, s62, v95
	v_med3_f32 v233, v233, s62, v95
	v_med3_f32 v234, v234, s62, v95
	v_med3_f32 v235, v235, s62, v95
	v_med3_f32 v236, v236, s62, v95
	v_med3_f32 v237, v237, s62, v95
	v_med3_f32 v238, v238, s62, v95
	v_med3_f32 v239, v239, s62, v95
	v_med3_f32 v240, v240, s62, v95
	v_med3_f32 v241, v241, s62, v95
	v_mov_b32_e32 v242, 0
	v_mov_b32_e32 v243, 0
	v_mov_b32_e32 v244, 0
	v_mov_b32_e32 v245, 0
	v_cvt_pk_fp8_f32 v242, v226, v227
	v_cvt_pk_fp8_f32 v243, v230, v231
	v_cvt_pk_fp8_f32 v244, v234, v235
	v_cvt_pk_fp8_f32 v245, v238, v239
	v_cvt_pk_fp8_f32 v242, v228, v229 op_sel:[0,0,1]
	v_cvt_pk_fp8_f32 v243, v232, v233 op_sel:[0,0,1]
	v_cvt_pk_fp8_f32 v244, v236, v237 op_sel:[0,0,1]
	v_cvt_pk_fp8_f32 v245, v240, v241 op_sel:[0,0,1]
	s_nop 0
	global_store_dwordx4 v77, v[242:245], s[6:7]
	ds_read_b32 v226, v213
	ds_read_b32 v227, v213 offset:512
	ds_read_b32 v228, v213 offset:1024
	ds_read_b32 v229, v213 offset:1536
	ds_read_b32 v230, v213 offset:2048
	ds_read_b32 v231, v213 offset:2560
	ds_read_b32 v232, v213 offset:3072
	ds_read_b32 v233, v213 offset:3584
	ds_read_b32 v234, v213 offset:4096
	ds_read_b32 v235, v213 offset:4608
	ds_read_b32 v236, v213 offset:5120
	ds_read_b32 v237, v213 offset:5632
	ds_read_b32 v238, v213 offset:6144
	ds_read_b32 v239, v213 offset:6656
	ds_read_b32 v240, v213 offset:7168
	ds_read_b32 v241, v213 offset:7680
	s_waitcnt lgkmcnt(0)
	v_max_f32_e32 v226, v226, v226
	v_max_f32_e32 v227, v227, v227
	v_max_f32_e32 v228, v228, v228
	v_max_f32_e32 v229, v229, v229
	v_max_f32_e32 v230, v230, v230
	v_max_f32_e32 v231, v231, v231
	v_max_f32_e32 v232, v232, v232
	v_max_f32_e32 v233, v233, v233
	v_max_f32_e32 v234, v234, v234
	v_max_f32_e32 v235, v235, v235
	v_max_f32_e32 v236, v236, v236
	v_max_f32_e32 v237, v237, v237
	v_max_f32_e32 v238, v238, v238
	v_max_f32_e32 v239, v239, v239
	v_max_f32_e32 v240, v240, v240
	v_max_f32_e32 v241, v241, v241
	v_med3_f32 v226, v226, s62, v95
	v_med3_f32 v227, v227, s62, v95
	v_med3_f32 v228, v228, s62, v95
	v_med3_f32 v229, v229, s62, v95
	v_med3_f32 v230, v230, s62, v95
	v_med3_f32 v231, v231, s62, v95
	v_med3_f32 v232, v232, s62, v95
	v_med3_f32 v233, v233, s62, v95
	v_med3_f32 v234, v234, s62, v95
	v_med3_f32 v235, v235, s62, v95
	v_med3_f32 v236, v236, s62, v95
	v_med3_f32 v237, v237, s62, v95
	v_med3_f32 v238, v238, s62, v95
	v_med3_f32 v239, v239, s62, v95
	v_med3_f32 v240, v240, s62, v95
	v_med3_f32 v241, v241, s62, v95
	v_mov_b32_e32 v242, 0
	v_mov_b32_e32 v243, 0
	v_mov_b32_e32 v244, 0
	v_mov_b32_e32 v245, 0
	v_cvt_pk_fp8_f32 v242, v226, v227
	v_cvt_pk_fp8_f32 v243, v230, v231
	v_cvt_pk_fp8_f32 v244, v234, v235
	v_cvt_pk_fp8_f32 v245, v238, v239
	v_cvt_pk_fp8_f32 v242, v228, v229 op_sel:[0,0,1]
	v_cvt_pk_fp8_f32 v243, v232, v233 op_sel:[0,0,1]
	v_cvt_pk_fp8_f32 v244, v236, v237 op_sel:[0,0,1]
	v_cvt_pk_fp8_f32 v245, v240, v241 op_sel:[0,0,1]
	s_nop 0
	global_store_dwordx4 v78, v[242:245], s[6:7]
	s_waitcnt vmcnt(12)
	v_mul_f32_e32 v176, v34, v176
	v_mul_f32_e32 v177, v34, v177
	v_mul_f32_e32 v178, v34, v178
	v_mul_f32_e32 v179, v34, v179
	ds_write_b128 v210, v[176:179]
	v_mul_f32_e32 v180, v35, v180
	v_mul_f32_e32 v181, v35, v181
	v_mul_f32_e32 v182, v35, v182
	v_mul_f32_e32 v183, v35, v183
	ds_write_b128 v210, v[180:183] offset:1024
	v_mul_f32_e32 v184, v36, v184
	v_mul_f32_e32 v185, v36, v185
	v_mul_f32_e32 v186, v36, v186
	v_mul_f32_e32 v187, v36, v187
	ds_write_b128 v210, v[184:187] offset:2048
	v_mul_f32_e32 v188, v37, v188
	v_mul_f32_e32 v189, v37, v189
	v_mul_f32_e32 v190, v37, v190
	v_mul_f32_e32 v191, v37, v191
	ds_write_b128 v210, v[188:191] offset:3072
	v_mul_f32_e32 v192, v38, v192
	v_mul_f32_e32 v193, v38, v193
	v_mul_f32_e32 v194, v38, v194
	v_mul_f32_e32 v195, v38, v195
	ds_write_b128 v210, v[192:195] offset:4096
	v_mul_f32_e32 v196, v39, v196
	v_mul_f32_e32 v197, v39, v197
	v_mul_f32_e32 v198, v39, v198
	v_mul_f32_e32 v199, v39, v199
	ds_write_b128 v210, v[196:199] offset:5120
	v_mul_f32_e32 v200, v40, v200
	v_mul_f32_e32 v201, v40, v201
	v_mul_f32_e32 v202, v40, v202
	v_mul_f32_e32 v203, v40, v203
	ds_write_b128 v210, v[200:203] offset:6144
	v_mul_f32_e32 v204, v41, v204
	v_mul_f32_e32 v205, v41, v205
	v_mul_f32_e32 v206, v41, v206
	v_mul_f32_e32 v207, v41, v207
	ds_write_b128 v210, v[204:207] offset:7168
	s_waitcnt lgkmcnt(0)
	s_barrier
; #define GAS __attribute__((address_space(1)))
; #define LAS __attribute__((address_space(3)))
; #define LDS_WAIT() asm volatile("s_waitcnt lgkmcnt(0)" ::: "memory")
; __device__ __forceinline__ unsigned pk4_fp8(float a, float b, float c, float d) {
;     a = fminf(fmaxf(a, -448.f), 448.f); b = fminf(fmaxf(b, -448.f), 448.f); c = fminf(fmaxf(c, -448.f), 448.f); d = fminf(fmaxf(d, -448.f), 448.f);
;     int w = __builtin_amdgcn_cvt_pk_fp8_f32(a, b, 0, false); w = __builtin_amdgcn_cvt_pk_fp8_f32(c, d, w, true); return (unsigned)w; }
;     ...
; #pragma unroll
;     for (int i = 0; i < 32; ++i) v[i] = sc >= 0 ? W[(size_t)(k0 + 2 * i + (lane >> 5)) * Nsrc + sc] : 0.f;
; #pragma unroll
;     for (int i = 0; i < 32; ++i) { const int k = k0 + 2 * i + (lane >> 5); float x = v[i] * wscale; if (KS) x *= (k < ksplit ? ksA[k] : ksB[k - ksplit]); scr[(2 * i + (lane >> 5)) * 33 + (lane & 31)] = x; }
;     LDS_WAIT(); asm volatile("" ::: "memory");
;     const int c = lane & 7;
; #pragma unroll
;     for (int j = 0; j < 4; ++j) { const int n = (lane >> 3) + 8 * j; const LAS float* s = scr + (8 * c) * 33 + n;
;         const unsigned long long o = (unsigned long long)pg8::pk4_fp8(s[0 * 33], s[1 * 33], s[2 * 33], s[3 * 33]) | ((unsigned long long)pg8::pk4_fp8(s[4 * 33], s[5 * 33], s[6 * 33], s[7 * 33]) << 32);
;         *(GAS unsigned long long*)(WT + (size_t)(n0 + n) * K + k0 + 8 * c) = o; }
	s_add_u32 s8, s34, 0xd000
	s_addc_u32 s9, s35, 0
	global_load_dwordx4 v[176:179], v74, s[8:9]
	s_add_u32 s8, s8, 0x20000
	s_addc_u32 s9, s9, 0
	global_load_dwordx4 v[180:183], v74, s[8:9]
	s_add_u32 s8, s8, 0x20000
	s_addc_u32 s9, s9, 0
	global_load_dwordx4 v[184:187], v74, s[8:9]
	s_add_u32 s8, s8, 0x20000
	s_addc_u32 s9, s9, 0
	global_load_dwordx4 v[188:191], v74, s[8:9]
	s_add_u32 s8, s8, 0x20000
	s_addc_u32 s9, s9, 0
	global_load_dwordx4 v[192:195], v74, s[8:9]
	s_add_u32 s8, s8, 0x20000
	s_addc_u32 s9, s9, 0
	global_load_dwordx4 v[196:199], v74, s[8:9]
	s_add_u32 s8, s8, 0x20000
	s_addc_u32 s9, s9, 0
	global_load_dwordx4 v[200:203], v74, s[8:9]
	s_add_u32 s8, s8, 0x20000
	s_addc_u32 s9, s9, 0
	global_load_dwordx4 v[204:207], v74, s[8:9]
	s_add_u32 s6, s36, 0x2c00000
	s_addc_u32 s7, s37, 0
	ds_read_b32 v226, v212
	ds_read_b32 v227, v212 offset:512
	ds_read_b32 v228, v212 offset:1024
	ds_read_b32 v229, v212 offset:1536
	ds_read_b32 v230, v212 offset:2048
	ds_read_b32 v231, v212 offset:2560
	ds_read_b32 v232, v212 offset:3072
	ds_read_b32 v233, v212 offset:3584
	ds_read_b32 v234, v212 offset:4096
	ds_read_b32 v235, v212 offset:4608
	ds_read_b32 v236, v212 offset:5120
	ds_read_b32 v237, v212 offset:5632
	ds_read_b32 v238, v212 offset:6144
	ds_read_b32 v239, v212 offset:6656
	ds_read_b32 v240, v212 offset:7168
	ds_read_b32 v241, v212 offset:7680
	s_waitcnt lgkmcnt(0)
	v_max_f32_e32 v226, v226, v226
	v_max_f32_e32 v227, v227, v227
	v_max_f32_e32 v228, v228, v228
	v_max_f32_e32 v229, v229, v229
	v_max_f32_e32 v230, v230, v230
	v_max_f32_e32 v231, v231, v231
	v_max_f32_e32 v232, v232, v232
	v_max_f32_e32 v233, v233, v233
	v_max_f32_e32 v234, v234, v234
	v_max_f32_e32 v235, v235, v235
	v_max_f32_e32 v236, v236, v236
	v_max_f32_e32 v237, v237, v237
	v_max_f32_e32 v238, v238, v238
	v_max_f32_e32 v239, v239, v239
	v_max_f32_e32 v240, v240, v240
	v_max_f32_e32 v241, v241, v241
	v_med3_f32 v226, v226, s62, v95
	v_med3_f32 v227, v227, s62, v95
	v_med3_f32 v228, v228, s62, v95
	v_med3_f32 v229, v229, s62, v95
	v_med3_f32 v230, v230, s62, v95
	v_med3_f32 v231, v231, s62, v95
	v_med3_f32 v232, v232, s62, v95
	v_med3_f32 v233, v233, s62, v95
	v_med3_f32 v234, v234, s62, v95
	v_med3_f32 v235, v235, s62, v95
	v_med3_f32 v236, v236, s62, v95
	v_med3_f32 v237, v237, s62, v95
	v_med3_f32 v238, v238, s62, v95
	v_med3_f32 v239, v239, s62, v95
	v_med3_f32 v240, v240, s62, v95
	v_med3_f32 v241, v241, s62, v95
	v_mov_b32_e32 v242, 0
	v_mov_b32_e32 v243, 0
	v_mov_b32_e32 v244, 0
	v_mov_b32_e32 v245, 0
	v_cvt_pk_fp8_f32 v242, v226, v227
	v_cvt_pk_fp8_f32 v243, v230, v231
	v_cvt_pk_fp8_f32 v244, v234, v235
	v_cvt_pk_fp8_f32 v245, v238, v239
	v_cvt_pk_fp8_f32 v242, v228, v229 op_sel:[0,0,1]
	v_cvt_pk_fp8_f32 v243, v232, v233 op_sel:[0,0,1]
	v_cvt_pk_fp8_f32 v244, v236, v237 op_sel:[0,0,1]
	v_cvt_pk_fp8_f32 v245, v240, v241 op_sel:[0,0,1]
	s_nop 0
	global_store_dwordx4 v77, v[242:245], s[6:7]
	ds_read_b32 v226, v214
	ds_read_b32 v227, v214 offset:512
	ds_read_b32 v228, v214 offset:1024
	ds_read_b32 v229, v214 offset:1536
	ds_read_b32 v230, v214 offset:2048
	ds_read_b32 v231, v214 offset:2560
	ds_read_b32 v232, v214 offset:3072
	ds_read_b32 v233, v214 offset:3584
	ds_read_b32 v234, v214 offset:4096
	ds_read_b32 v235, v214 offset:4608
	ds_read_b32 v236, v214 offset:5120
	ds_read_b32 v237, v214 offset:5632
	ds_read_b32 v238, v214 offset:6144
	ds_read_b32 v239, v214 offset:6656
	ds_read_b32 v240, v214 offset:7168
	ds_read_b32 v241, v214 offset:7680
	s_waitcnt lgkmcnt(0)
	v_max_f32_e32 v226, v226, v226
	v_max_f32_e32 v227, v227, v227
	v_max_f32_e32 v228, v228, v228
	v_max_f32_e32 v229, v229, v229
	v_max_f32_e32 v230, v230, v230
	v_max_f32_e32 v231, v231, v231
	v_max_f32_e32 v232, v232, v232
	v_max_f32_e32 v233, v233, v233
	v_max_f32_e32 v234, v234, v234
	v_max_f32_e32 v235, v235, v235
	v_max_f32_e32 v236, v236, v236
	v_max_f32_e32 v237, v237, v237
	v_max_f32_e32 v238, v238, v238
	v_max_f32_e32 v239, v239, v239
	v_max_f32_e32 v240, v240, v240
	v_max_f32_e32 v241, v241, v241
	v_med3_f32 v226, v226, s62, v95
	v_med3_f32 v227, v227, s62, v95
	v_med3_f32 v228, v228, s62, v95
	v_med3_f32 v229, v229, s62, v95
	v_med3_f32 v230, v230, s62, v95
	v_med3_f32 v231, v231, s62, v95
	v_med3_f32 v232, v232, s62, v95
	v_med3_f32 v233, v233, s62, v95
	v_med3_f32 v234, v234, s62, v95
	v_med3_f32 v235, v235, s62, v95
	v_med3_f32 v236, v236, s62, v95
	v_med3_f32 v237, v237, s62, v95
	v_med3_f32 v238, v238, s62, v95
	v_med3_f32 v239, v239, s62, v95
	v_med3_f32 v240, v240, s62, v95
	v_med3_f32 v241, v241, s62, v95
	v_mov_b32_e32 v242, 0
	v_mov_b32_e32 v243, 0
	v_mov_b32_e32 v244, 0
	v_mov_b32_e32 v245, 0
	v_cvt_pk_fp8_f32 v242, v226, v227
	v_cvt_pk_fp8_f32 v243, v230, v231
	v_cvt_pk_fp8_f32 v244, v234, v235
	v_cvt_pk_fp8_f32 v245, v238, v239
	v_cvt_pk_fp8_f32 v242, v228, v229 op_sel:[0,0,1]
	v_cvt_pk_fp8_f32 v243, v232, v233 op_sel:[0,0,1]
	v_cvt_pk_fp8_f32 v244, v236, v237 op_sel:[0,0,1]
	v_cvt_pk_fp8_f32 v245, v240, v241 op_sel:[0,0,1]
	s_nop 0
	global_store_dwordx4 v78, v[242:245], s[6:7]
	s_waitcnt vmcnt(12)
	v_mul_f32_e32 v144, v34, v144
	v_mul_f32_e32 v145, v34, v145
	v_mul_f32_e32 v146, v34, v146
	v_mul_f32_e32 v147, v34, v147
	ds_write_b128 v209, v[144:147]
	v_mul_f32_e32 v148, v35, v148
	v_mul_f32_e32 v149, v35, v149
	v_mul_f32_e32 v150, v35, v150
	v_mul_f32_e32 v151, v35, v151
	ds_write_b128 v209, v[148:151] offset:1024
	v_mul_f32_e32 v152, v36, v152
	v_mul_f32_e32 v153, v36, v153
	v_mul_f32_e32 v154, v36, v154
	v_mul_f32_e32 v155, v36, v155
	ds_write_b128 v209, v[152:155] offset:2048
	v_mul_f32_e32 v156, v37, v156
	v_mul_f32_e32 v157, v37, v157
	v_mul_f32_e32 v158, v37, v158
	v_mul_f32_e32 v159, v37, v159
	ds_write_b128 v209, v[156:159] offset:3072
	v_mul_f32_e32 v160, v38, v160
	v_mul_f32_e32 v161, v38, v161
	v_mul_f32_e32 v162, v38, v162
	v_mul_f32_e32 v163, v38, v163
	ds_write_b128 v209, v[160:163] offset:4096
	v_mul_f32_e32 v164, v39, v164
	v_mul_f32_e32 v165, v39, v165
	v_mul_f32_e32 v166, v39, v166
	v_mul_f32_e32 v167, v39, v167
	ds_write_b128 v209, v[164:167] offset:5120
	v_mul_f32_e32 v168, v40, v168
	v_mul_f32_e32 v169, v40, v169
	v_mul_f32_e32 v170, v40, v170
	v_mul_f32_e32 v171, v40, v171
	ds_write_b128 v209, v[168:171] offset:6144
	v_mul_f32_e32 v172, v41, v172
	v_mul_f32_e32 v173, v41, v173
	v_mul_f32_e32 v174, v41, v174
	v_mul_f32_e32 v175, v41, v175
	ds_write_b128 v209, v[172:175] offset:7168
	s_waitcnt lgkmcnt(0)
	s_barrier
; #define GAS __attribute__((address_space(1)))
; #define LAS __attribute__((address_space(3)))
; #define LDS_WAIT() asm volatile("s_waitcnt lgkmcnt(0)" ::: "memory")
; __device__ __forceinline__ unsigned pk4_fp8(float a, float b, float c, float d) {
;     a = fminf(fmaxf(a, -448.f), 448.f); b = fminf(fmaxf(b, -448.f), 448.f); c = fminf(fmaxf(c, -448.f), 448.f); d = fminf(fmaxf(d, -448.f), 448.f);
;     int w = __builtin_amdgcn_cvt_pk_fp8_f32(a, b, 0, false); w = __builtin_amdgcn_cvt_pk_fp8_f32(c, d, w, true); return (unsigned)w; }
;     ...
; #pragma unroll
;     for (int i = 0; i < 32; ++i) v[i] = sc >= 0 ? W[(size_t)(k0 + 2 * i + (lane >> 5)) * Nsrc + sc] : 0.f;
; #pragma unroll
;     for (int i = 0; i < 32; ++i) { const int k = k0 + 2 * i + (lane >> 5); float x = v[i] * wscale; if (KS) x *= (k < ksplit ? ksA[k] : ksB[k - ksplit]); scr[(2 * i + (lane >> 5)) * 33 + (lane & 31)] = x; }
;     LDS_WAIT(); asm volatile("" ::: "memory");
;     const int c = lane & 7;
; #pragma unroll
;     for (int j = 0; j < 4; ++j) { const int n = (lane >> 3) + 8 * j; const LAS float* s = scr + (8 * c) * 33 + n;
;         const unsigned long long o = (unsigned long long)pg8::pk4_fp8(s[0 * 33], s[1 * 33], s[2 * 33], s[3 * 33]) | ((unsigned long long)pg8::pk4_fp8(s[4 * 33], s[5 * 33], s[6 * 33], s[7 * 33]) << 32);
;         *(GAS unsigned long long*)(WT + (size_t)(n0 + n) * K + k0 + 8 * c) = o; }
	s_add_u32 s8, s34, 0xe000
	s_addc_u32 s9, s35, 0
	global_load_dwordx4 v[144:147], v74, s[8:9]
	s_add_u32 s8, s8, 0x20000
	s_addc_u32 s9, s9, 0
	global_load_dwordx4 v[148:151], v74, s[8:9]
	s_add_u32 s8, s8, 0x20000
	s_addc_u32 s9, s9, 0
	global_load_dwordx4 v[152:155], v74, s[8:9]
	s_add_u32 s8, s8, 0x20000
	s_addc_u32 s9, s9, 0
	global_load_dwordx4 v[156:159], v74, s[8:9]
	s_add_u32 s8, s8, 0x20000
	s_addc_u32 s9, s9, 0
	global_load_dwordx4 v[160:163], v74, s[8:9]
	s_add_u32 s8, s8, 0x20000
	s_addc_u32 s9, s9, 0
	global_load_dwordx4 v[164:167], v74, s[8:9]
	s_add_u32 s8, s8, 0x20000
	s_addc_u32 s9, s9, 0
	global_load_dwordx4 v[168:171], v74, s[8:9]
	s_add_u32 s8, s8, 0x20000
	s_addc_u32 s9, s9, 0
	global_load_dwordx4 v[172:175], v74, s[8:9]
	s_add_u32 s6, s36, 0x3000000
	s_addc_u32 s7, s37, 0
	ds_read_b32 v226, v211
	ds_read_b32 v227, v211 offset:512
	ds_read_b32 v228, v211 offset:1024
	ds_read_b32 v229, v211 offset:1536
	ds_read_b32 v230, v211 offset:2048
	ds_read_b32 v231, v211 offset:2560
	ds_read_b32 v232, v211 offset:3072
	ds_read_b32 v233, v211 offset:3584
	ds_read_b32 v234, v211 offset:4096
	ds_read_b32 v235, v211 offset:4608
	ds_read_b32 v236, v211 offset:5120
	ds_read_b32 v237, v211 offset:5632
	ds_read_b32 v238, v211 offset:6144
	ds_read_b32 v239, v211 offset:6656
	ds_read_b32 v240, v211 offset:7168
	ds_read_b32 v241, v211 offset:7680
	s_waitcnt lgkmcnt(0)
	v_max_f32_e32 v226, v226, v226
	v_max_f32_e32 v227, v227, v227
	v_max_f32_e32 v228, v228, v228
	v_max_f32_e32 v229, v229, v229
	v_max_f32_e32 v230, v230, v230
	v_max_f32_e32 v231, v231, v231
	v_max_f32_e32 v232, v232, v232
	v_max_f32_e32 v233, v233, v233
	v_max_f32_e32 v234, v234, v234
	v_max_f32_e32 v235, v235, v235
	v_max_f32_e32 v236, v236, v236
	v_max_f32_e32 v237, v237, v237
	v_max_f32_e32 v238, v238, v238
	v_max_f32_e32 v239, v239, v239
	v_max_f32_e32 v240, v240, v240
	v_max_f32_e32 v241, v241, v241
	v_med3_f32 v226, v226, s62, v95
	v_med3_f32 v227, v227, s62, v95
	v_med3_f32 v228, v228, s62, v95
	v_med3_f32 v229, v229, s62, v95
	v_med3_f32 v230, v230, s62, v95
	v_med3_f32 v231, v231, s62, v95
	v_med3_f32 v232, v232, s62, v95
	v_med3_f32 v233, v233, s62, v95
	v_med3_f32 v234, v234, s62, v95
	v_med3_f32 v235, v235, s62, v95
	v_med3_f32 v236, v236, s62, v95
	v_med3_f32 v237, v237, s62, v95
	v_med3_f32 v238, v238, s62, v95
	v_med3_f32 v239, v239, s62, v95
	v_med3_f32 v240, v240, s62, v95
	v_med3_f32 v241, v241, s62, v95
	v_mov_b32_e32 v242, 0
	v_mov_b32_e32 v243, 0
	v_mov_b32_e32 v244, 0
	v_mov_b32_e32 v245, 0
	v_cvt_pk_fp8_f32 v242, v226, v227
	v_cvt_pk_fp8_f32 v243, v230, v231
	v_cvt_pk_fp8_f32 v244, v234, v235
	v_cvt_pk_fp8_f32 v245, v238, v239
	v_cvt_pk_fp8_f32 v242, v228, v229 op_sel:[0,0,1]
	v_cvt_pk_fp8_f32 v243, v232, v233 op_sel:[0,0,1]
	v_cvt_pk_fp8_f32 v244, v236, v237 op_sel:[0,0,1]
	v_cvt_pk_fp8_f32 v245, v240, v241 op_sel:[0,0,1]
	s_nop 0
	global_store_dwordx4 v77, v[242:245], s[6:7]
	ds_read_b32 v226, v213
	ds_read_b32 v227, v213 offset:512
	ds_read_b32 v228, v213 offset:1024
	ds_read_b32 v229, v213 offset:1536
	ds_read_b32 v230, v213 offset:2048
	ds_read_b32 v231, v213 offset:2560
	ds_read_b32 v232, v213 offset:3072
	ds_read_b32 v233, v213 offset:3584
	ds_read_b32 v234, v213 offset:4096
	ds_read_b32 v235, v213 offset:4608
	ds_read_b32 v236, v213 offset:5120
	ds_read_b32 v237, v213 offset:5632
	ds_read_b32 v238, v213 offset:6144
	ds_read_b32 v239, v213 offset:6656
	ds_read_b32 v240, v213 offset:7168
	ds_read_b32 v241, v213 offset:7680
	s_waitcnt lgkmcnt(0)
	v_max_f32_e32 v226, v226, v226
	v_max_f32_e32 v227, v227, v227
	v_max_f32_e32 v228, v228, v228
	v_max_f32_e32 v229, v229, v229
	v_max_f32_e32 v230, v230, v230
	v_max_f32_e32 v231, v231, v231
	v_max_f32_e32 v232, v232, v232
	v_max_f32_e32 v233, v233, v233
	v_max_f32_e32 v234, v234, v234
	v_max_f32_e32 v235, v235, v235
	v_max_f32_e32 v236, v236, v236
	v_max_f32_e32 v237, v237, v237
	v_max_f32_e32 v238, v238, v238
	v_max_f32_e32 v239, v239, v239
	v_max_f32_e32 v240, v240, v240
	v_max_f32_e32 v241, v241, v241
	v_med3_f32 v226, v226, s62, v95
	v_med3_f32 v227, v227, s62, v95
	v_med3_f32 v228, v228, s62, v95
	v_med3_f32 v229, v229, s62, v95
	v_med3_f32 v230, v230, s62, v95
	v_med3_f32 v231, v231, s62, v95
	v_med3_f32 v232, v232, s62, v95
	v_med3_f32 v233, v233, s62, v95
	v_med3_f32 v234, v234, s62, v95
	v_med3_f32 v235, v235, s62, v95
	v_med3_f32 v236, v236, s62, v95
	v_med3_f32 v237, v237, s62, v95
	v_med3_f32 v238, v238, s62, v95
	v_med3_f32 v239, v239, s62, v95
	v_med3_f32 v240, v240, s62, v95
	v_med3_f32 v241, v241, s62, v95
	v_mov_b32_e32 v242, 0
	v_mov_b32_e32 v243, 0
	v_mov_b32_e32 v244, 0
	v_mov_b32_e32 v245, 0
	v_cvt_pk_fp8_f32 v242, v226, v227
	v_cvt_pk_fp8_f32 v243, v230, v231
	v_cvt_pk_fp8_f32 v244, v234, v235
	v_cvt_pk_fp8_f32 v245, v238, v239
	v_cvt_pk_fp8_f32 v242, v228, v229 op_sel:[0,0,1]
	v_cvt_pk_fp8_f32 v243, v232, v233 op_sel:[0,0,1]
	v_cvt_pk_fp8_f32 v244, v236, v237 op_sel:[0,0,1]
	v_cvt_pk_fp8_f32 v245, v240, v241 op_sel:[0,0,1]
	s_nop 0
	global_store_dwordx4 v78, v[242:245], s[6:7]
	s_waitcnt vmcnt(12)
	v_mul_f32_e32 v176, v34, v176
	v_mul_f32_e32 v177, v34, v177
	v_mul_f32_e32 v178, v34, v178
	v_mul_f32_e32 v179, v34, v179
	ds_write_b128 v210, v[176:179]
	v_mul_f32_e32 v180, v35, v180
	v_mul_f32_e32 v181, v35, v181
	v_mul_f32_e32 v182, v35, v182
	v_mul_f32_e32 v183, v35, v183
	ds_write_b128 v210, v[180:183] offset:1024
	v_mul_f32_e32 v184, v36, v184
	v_mul_f32_e32 v185, v36, v185
	v_mul_f32_e32 v186, v36, v186
	v_mul_f32_e32 v187, v36, v187
	ds_write_b128 v210, v[184:187] offset:2048
	v_mul_f32_e32 v188, v37, v188
	v_mul_f32_e32 v189, v37, v189
	v_mul_f32_e32 v190, v37, v190
	v_mul_f32_e32 v191, v37, v191
	ds_write_b128 v210, v[188:191] offset:3072
	v_mul_f32_e32 v192, v38, v192
	v_mul_f32_e32 v193, v38, v193
	v_mul_f32_e32 v194, v38, v194
	v_mul_f32_e32 v195, v38, v195
	ds_write_b128 v210, v[192:195] offset:4096
	v_mul_f32_e32 v196, v39, v196
	v_mul_f32_e32 v197, v39, v197
	v_mul_f32_e32 v198, v39, v198
	v_mul_f32_e32 v199, v39, v199
	ds_write_b128 v210, v[196:199] offset:5120
	v_mul_f32_e32 v200, v40, v200
	v_mul_f32_e32 v201, v40, v201
	v_mul_f32_e32 v202, v40, v202
	v_mul_f32_e32 v203, v40, v203
	ds_write_b128 v210, v[200:203] offset:6144
	v_mul_f32_e32 v204, v41, v204
	v_mul_f32_e32 v205, v41, v205
	v_mul_f32_e32 v206, v41, v206
	v_mul_f32_e32 v207, v41, v207
	ds_write_b128 v210, v[204:207] offset:7168
	s_waitcnt lgkmcnt(0)
	s_barrier
; #define GAS __attribute__((address_space(1)))
; #define LAS __attribute__((address_space(3)))
; #define LDS_WAIT() asm volatile("s_waitcnt lgkmcnt(0)" ::: "memory")
; __device__ __forceinline__ unsigned pk4_fp8(float a, float b, float c, float d) {
;     a = fminf(fmaxf(a, -448.f), 448.f); b = fminf(fmaxf(b, -448.f), 448.f); c = fminf(fmaxf(c, -448.f), 448.f); d = fminf(fmaxf(d, -448.f), 448.f);
;     int w = __builtin_amdgcn_cvt_pk_fp8_f32(a, b, 0, false); w = __builtin_amdgcn_cvt_pk_fp8_f32(c, d, w, true); return (unsigned)w; }
;     ...
; #pragma unroll
;     for (int i = 0; i < 32; ++i) v[i] = sc >= 0 ? W[(size_t)(k0 + 2 * i + (lane >> 5)) * Nsrc + sc] : 0.f;
; #pragma unroll
;     for (int i = 0; i < 32; ++i) { const int k = k0 + 2 * i + (lane >> 5); float x = v[i] * wscale; if (KS) x *= (k < ksplit ? ksA[k] : ksB[k - ksplit]); scr[(2 * i + (lane >> 5)) * 33 + (lane & 31)] = x; }
;     LDS_WAIT(); asm volatile("" ::: "memory");
;     const int c = lane & 7;
; #pragma unroll
;     for (int j = 0; j < 4; ++j) { const int n = (lane >> 3) + 8 * j; const LAS float* s = scr + (8 * c) * 33 + n;
;         const unsigned long long o = (unsigned long long)pg8::pk4_fp8(s[0 * 33], s[1 * 33], s[2 * 33], s[3 * 33]) | ((unsigned long long)pg8::pk4_fp8(s[4 * 33], s[5 * 33], s[6 * 33], s[7 * 33]) << 32);
;         *(GAS unsigned long long*)(WT + (size_t)(n0 + n) * K + k0 + 8 * c) = o; }
	s_add_u32 s8, s34, 0xf000
	s_addc_u32 s9, s35, 0
	global_load_dwordx4 v[176:179], v74, s[8:9]
	s_add_u32 s8, s8, 0x20000
	s_addc_u32 s9, s9, 0
	global_load_dwordx4 v[180:183], v74, s[8:9]
	s_add_u32 s8, s8, 0x20000
	s_addc_u32 s9, s9, 0
	global_load_dwordx4 v[184:187], v74, s[8:9]
	s_add_u32 s8, s8, 0x20000
	s_addc_u32 s9, s9, 0
	global_load_dwordx4 v[188:191], v74, s[8:9]
	s_add_u32 s8, s8, 0x20000
	s_addc_u32 s9, s9, 0
	global_load_dwordx4 v[192:195], v74, s[8:9]
	s_add_u32 s8, s8, 0x20000
	s_addc_u32 s9, s9, 0
	global_load_dwordx4 v[196:199], v74, s[8:9]
	s_add_u32 s8, s8, 0x20000
	s_addc_u32 s9, s9, 0
	global_load_dwordx4 v[200:203], v74, s[8:9]
	s_add_u32 s8, s8, 0x20000
	s_addc_u32 s9, s9, 0
	global_load_dwordx4 v[204:207], v74, s[8:9]
	s_add_u32 s6, s36, 0x3400000
	s_addc_u32 s7, s37, 0
	ds_read_b32 v226, v212
	ds_read_b32 v227, v212 offset:512
	ds_read_b32 v228, v212 offset:1024
	ds_read_b32 v229, v212 offset:1536
	ds_read_b32 v230, v212 offset:2048
	ds_read_b32 v231, v212 offset:2560
	ds_read_b32 v232, v212 offset:3072
	ds_read_b32 v233, v212 offset:3584
	ds_read_b32 v234, v212 offset:4096
	ds_read_b32 v235, v212 offset:4608
	ds_read_b32 v236, v212 offset:5120
	ds_read_b32 v237, v212 offset:5632
	ds_read_b32 v238, v212 offset:6144
	ds_read_b32 v239, v212 offset:6656
	ds_read_b32 v240, v212 offset:7168
	ds_read_b32 v241, v212 offset:7680
	s_waitcnt lgkmcnt(0)
	v_max_f32_e32 v226, v226, v226
	v_max_f32_e32 v227, v227, v227
	v_max_f32_e32 v228, v228, v228
	v_max_f32_e32 v229, v229, v229
	v_max_f32_e32 v230, v230, v230
	v_max_f32_e32 v231, v231, v231
	v_max_f32_e32 v232, v232, v232
	v_max_f32_e32 v233, v233, v233
	v_max_f32_e32 v234, v234, v234
	v_max_f32_e32 v235, v235, v235
	v_max_f32_e32 v236, v236, v236
	v_max_f32_e32 v237, v237, v237
	v_max_f32_e32 v238, v238, v238
	v_max_f32_e32 v239, v239, v239
	v_max_f32_e32 v240, v240, v240
	v_max_f32_e32 v241, v241, v241
	v_med3_f32 v226, v226, s62, v95
	v_med3_f32 v227, v227, s62, v95
	v_med3_f32 v228, v228, s62, v95
	v_med3_f32 v229, v229, s62, v95
	v_med3_f32 v230, v230, s62, v95
	v_med3_f32 v231, v231, s62, v95
	v_med3_f32 v232, v232, s62, v95
	v_med3_f32 v233, v233, s62, v95
	v_med3_f32 v234, v234, s62, v95
	v_med3_f32 v235, v235, s62, v95
	v_med3_f32 v236, v236, s62, v95
	v_med3_f32 v237, v237, s62, v95
	v_med3_f32 v238, v238, s62, v95
	v_med3_f32 v239, v239, s62, v95
	v_med3_f32 v240, v240, s62, v95
	v_med3_f32 v241, v241, s62, v95
	v_mov_b32_e32 v242, 0
	v_mov_b32_e32 v243, 0
	v_mov_b32_e32 v244, 0
	v_mov_b32_e32 v245, 0
	v_cvt_pk_fp8_f32 v242, v226, v227
	v_cvt_pk_fp8_f32 v243, v230, v231
	v_cvt_pk_fp8_f32 v244, v234, v235
	v_cvt_pk_fp8_f32 v245, v238, v239
	v_cvt_pk_fp8_f32 v242, v228, v229 op_sel:[0,0,1]
	v_cvt_pk_fp8_f32 v243, v232, v233 op_sel:[0,0,1]
	v_cvt_pk_fp8_f32 v244, v236, v237 op_sel:[0,0,1]
	v_cvt_pk_fp8_f32 v245, v240, v241 op_sel:[0,0,1]
	s_nop 0
	global_store_dwordx4 v77, v[242:245], s[6:7]
	ds_read_b32 v226, v214
	ds_read_b32 v227, v214 offset:512
	ds_read_b32 v228, v214 offset:1024
	ds_read_b32 v229, v214 offset:1536
	ds_read_b32 v230, v214 offset:2048
	ds_read_b32 v231, v214 offset:2560
	ds_read_b32 v232, v214 offset:3072
	ds_read_b32 v233, v214 offset:3584
	ds_read_b32 v234, v214 offset:4096
	ds_read_b32 v235, v214 offset:4608
	ds_read_b32 v236, v214 offset:5120
	ds_read_b32 v237, v214 offset:5632
	ds_read_b32 v238, v214 offset:6144
	ds_read_b32 v239, v214 offset:6656
	ds_read_b32 v240, v214 offset:7168
	ds_read_b32 v241, v214 offset:7680
	s_waitcnt lgkmcnt(0)
	v_max_f32_e32 v226, v226, v226
	v_max_f32_e32 v227, v227, v227
	v_max_f32_e32 v228, v228, v228
	v_max_f32_e32 v229, v229, v229
	v_max_f32_e32 v230, v230, v230
	v_max_f32_e32 v231, v231, v231
	v_max_f32_e32 v232, v232, v232
	v_max_f32_e32 v233, v233, v233
	v_max_f32_e32 v234, v234, v234
	v_max_f32_e32 v235, v235, v235
	v_max_f32_e32 v236, v236, v236
	v_max_f32_e32 v237, v237, v237
	v_max_f32_e32 v238, v238, v238
	v_max_f32_e32 v239, v239, v239
	v_max_f32_e32 v240, v240, v240
	v_max_f32_e32 v241, v241, v241
	v_med3_f32 v226, v226, s62, v95
	v_med3_f32 v227, v227, s62, v95
	v_med3_f32 v228, v228, s62, v95
	v_med3_f32 v229, v229, s62, v95
	v_med3_f32 v230, v230, s62, v95
	v_med3_f32 v231, v231, s62, v95
	v_med3_f32 v232, v232, s62, v95
	v_med3_f32 v233, v233, s62, v95
	v_med3_f32 v234, v234, s62, v95
	v_med3_f32 v235, v235, s62, v95
	v_med3_f32 v236, v236, s62, v95
	v_med3_f32 v237, v237, s62, v95
	v_med3_f32 v238, v238, s62, v95
	v_med3_f32 v239, v239, s62, v95
	v_med3_f32 v240, v240, s62, v95
	v_med3_f32 v241, v241, s62, v95
	v_mov_b32_e32 v242, 0
	v_mov_b32_e32 v243, 0
	v_mov_b32_e32 v244, 0
	v_mov_b32_e32 v245, 0
	v_cvt_pk_fp8_f32 v242, v226, v227
	v_cvt_pk_fp8_f32 v243, v230, v231
	v_cvt_pk_fp8_f32 v244, v234, v235
	v_cvt_pk_fp8_f32 v245, v238, v239
	v_cvt_pk_fp8_f32 v242, v228, v229 op_sel:[0,0,1]
	v_cvt_pk_fp8_f32 v243, v232, v233 op_sel:[0,0,1]
	v_cvt_pk_fp8_f32 v244, v236, v237 op_sel:[0,0,1]
	v_cvt_pk_fp8_f32 v245, v240, v241 op_sel:[0,0,1]
	s_nop 0
	global_store_dwordx4 v78, v[242:245], s[6:7]
	s_waitcnt vmcnt(12)
	v_mul_f32_e32 v144, v34, v144
	v_mul_f32_e32 v145, v34, v145
	v_mul_f32_e32 v146, v34, v146
	v_mul_f32_e32 v147, v34, v147
	ds_write_b128 v209, v[144:147]
	v_mul_f32_e32 v148, v35, v148
	v_mul_f32_e32 v149, v35, v149
	v_mul_f32_e32 v150, v35, v150
	v_mul_f32_e32 v151, v35, v151
	ds_write_b128 v209, v[148:151] offset:1024
	v_mul_f32_e32 v152, v36, v152
	v_mul_f32_e32 v153, v36, v153
	v_mul_f32_e32 v154, v36, v154
	v_mul_f32_e32 v155, v36, v155
	ds_write_b128 v209, v[152:155] offset:2048
	v_mul_f32_e32 v156, v37, v156
	v_mul_f32_e32 v157, v37, v157
	v_mul_f32_e32 v158, v37, v158
	v_mul_f32_e32 v159, v37, v159
	ds_write_b128 v209, v[156:159] offset:3072
	v_mul_f32_e32 v160, v38, v160
	v_mul_f32_e32 v161, v38, v161
	v_mul_f32_e32 v162, v38, v162
	v_mul_f32_e32 v163, v38, v163
	ds_write_b128 v209, v[160:163] offset:4096
	v_mul_f32_e32 v164, v39, v164
	v_mul_f32_e32 v165, v39, v165
	v_mul_f32_e32 v166, v39, v166
	v_mul_f32_e32 v167, v39, v167
	ds_write_b128 v209, v[164:167] offset:5120
	v_mul_f32_e32 v168, v40, v168
	v_mul_f32_e32 v169, v40, v169
	v_mul_f32_e32 v170, v40, v170
	v_mul_f32_e32 v171, v40, v171
	ds_write_b128 v209, v[168:171] offset:6144
	v_mul_f32_e32 v172, v41, v172
	v_mul_f32_e32 v173, v41, v173
	v_mul_f32_e32 v174, v41, v174
	v_mul_f32_e32 v175, v41, v175
	ds_write_b128 v209, v[172:175] offset:7168
	s_waitcnt lgkmcnt(0)
	s_barrier
; #define GAS __attribute__((address_space(1)))
; #define LAS __attribute__((address_space(3)))
; #define LDS_WAIT() asm volatile("s_waitcnt lgkmcnt(0)" ::: "memory")
;     ...
; #pragma unroll
;     for (int i = 0; i < 32; ++i) v[i] = sc >= 0 ? W[(size_t)(k0 + 2 * i + (lane >> 5)) * Nsrc + sc] : 0.f;
; #pragma unroll
;     for (int i = 0; i < 32; ++i) { const int k = k0 + 2 * i + (lane >> 5); float x = v[i] * wscale; if (KS) x *= (k < ksplit ? ksA[k] : ksB[k - ksplit]); scr[(2 * i + (lane >> 5)) * 33 + (lane & 31)] = x; }
;     LDS_WAIT(); asm volatile("" ::: "memory");
;     const int c = lane & 7;
; #pragma unroll
;     for (int j = 0; j < 4; ++j) { const int n = (lane >> 3) + 8 * j; const LAS float* s = scr + (8 * c) * 33 + n;
;         const unsigned long long o = (unsigned long long)pg8::pk4_fp8(s[0 * 33], s[1 * 33], s[2 * 33], s[3 * 33]) | ((unsigned long long)pg8::pk4_fp8(s[4 * 33], s[5 * 33], s[6 * 33], s[7 * 33]) << 32);
;         *(GAS unsigned long long*)(WT + (size_t)(n0 + n) * K + k0 + 8 * c) = o; }
; __global__ void __launch_bounds__(NWAVES * 64, 2) hybrid_fwd(Args args) {
;     ...
;             if (r < I_UP) { p0_transpose_item_f8<true>(args.in[15] + (size_t)l * DM * FF, DM, FF, FF / 32, (unsigned char*)(ws + WS_WUP + l * SZ_WUP), WUP8_SCALE, args.in[14] + l * DM, args.in[14] + l * DM, DM, scr, r, lane); continue; } r -= I_UP;
;             p0_transpose_item_f8<false>(args.in[16] + (size_t)l * FF * DM, FF, DM, DM / 32, (unsigned char*)(ws + WS_WDN + l * SZ_WDN), 128.f, args.in[16], args.in[16], 0, scr, r, lane);
	s_mov_b64 s[8:9], s[38:39]
	global_load_dwordx4 v[144:147], v75, s[8:9]
	s_add_u32 s8, s8, 0x8000
	s_addc_u32 s9, s9, 0
	global_load_dwordx4 v[148:151], v75, s[8:9]
	s_add_u32 s8, s8, 0x8000
	s_addc_u32 s9, s9, 0
	global_load_dwordx4 v[152:155], v75, s[8:9]
	s_add_u32 s8, s8, 0x8000
	s_addc_u32 s9, s9, 0
	global_load_dwordx4 v[156:159], v75, s[8:9]
	s_add_u32 s8, s8, 0x8000
	s_addc_u32 s9, s9, 0
	global_load_dwordx4 v[160:163], v75, s[8:9]
	s_add_u32 s8, s8, 0x8000
	s_addc_u32 s9, s9, 0
	global_load_dwordx4 v[164:167], v75, s[8:9]
	s_add_u32 s8, s8, 0x8000
	s_addc_u32 s9, s9, 0
	global_load_dwordx4 v[168:171], v75, s[8:9]
	s_add_u32 s8, s8, 0x8000
	s_addc_u32 s9, s9, 0
	global_load_dwordx4 v[172:175], v75, s[8:9]
	s_add_u32 s6, s36, 0x3800000
	s_addc_u32 s7, s37, 0
	ds_read_b32 v226, v211
	ds_read_b32 v227, v211 offset:512
	ds_read_b32 v228, v211 offset:1024
	ds_read_b32 v229, v211 offset:1536
	ds_read_b32 v230, v211 offset:2048
	ds_read_b32 v231, v211 offset:2560
	ds_read_b32 v232, v211 offset:3072
	ds_read_b32 v233, v211 offset:3584
	ds_read_b32 v234, v211 offset:4096
	ds_read_b32 v235, v211 offset:4608
	ds_read_b32 v236, v211 offset:5120
	ds_read_b32 v237, v211 offset:5632
	ds_read_b32 v238, v211 offset:6144
	ds_read_b32 v239, v211 offset:6656
	ds_read_b32 v240, v211 offset:7168
	ds_read_b32 v241, v211 offset:7680
	s_waitcnt lgkmcnt(0)
	v_max_f32_e32 v226, v226, v226
	v_max_f32_e32 v227, v227, v227
	v_max_f32_e32 v228, v228, v228
	v_max_f32_e32 v229, v229, v229
	v_max_f32_e32 v230, v230, v230
	v_max_f32_e32 v231, v231, v231
	v_max_f32_e32 v232, v232, v232
	v_max_f32_e32 v233, v233, v233
	v_max_f32_e32 v234, v234, v234
	v_max_f32_e32 v235, v235, v235
	v_max_f32_e32 v236, v236, v236
	v_max_f32_e32 v237, v237, v237
	v_max_f32_e32 v238, v238, v238
	v_max_f32_e32 v239, v239, v239
	v_max_f32_e32 v240, v240, v240
	v_max_f32_e32 v241, v241, v241
	v_med3_f32 v226, v226, s62, v95
	v_med3_f32 v227, v227, s62, v95
	v_med3_f32 v228, v228, s62, v95
	v_med3_f32 v229, v229, s62, v95
	v_med3_f32 v230, v230, s62, v95
	v_med3_f32 v231, v231, s62, v95
	v_med3_f32 v232, v232, s62, v95
	v_med3_f32 v233, v233, s62, v95
	v_med3_f32 v234, v234, s62, v95
	v_med3_f32 v235, v235, s62, v95
	v_med3_f32 v236, v236, s62, v95
	v_med3_f32 v237, v237, s62, v95
	v_med3_f32 v238, v238, s62, v95
	v_med3_f32 v239, v239, s62, v95
	v_med3_f32 v240, v240, s62, v95
	v_med3_f32 v241, v241, s62, v95
	v_mov_b32_e32 v242, 0
	v_mov_b32_e32 v243, 0
	v_mov_b32_e32 v244, 0
	v_mov_b32_e32 v245, 0
	v_cvt_pk_fp8_f32 v242, v226, v227
	v_cvt_pk_fp8_f32 v243, v230, v231
	v_cvt_pk_fp8_f32 v244, v234, v235
	v_cvt_pk_fp8_f32 v245, v238, v239
	v_cvt_pk_fp8_f32 v242, v228, v229 op_sel:[0,0,1]
	v_cvt_pk_fp8_f32 v243, v232, v233 op_sel:[0,0,1]
	v_cvt_pk_fp8_f32 v244, v236, v237 op_sel:[0,0,1]
	v_cvt_pk_fp8_f32 v245, v240, v241 op_sel:[0,0,1]
	s_nop 0
	global_store_dwordx4 v77, v[242:245], s[6:7]
	ds_read_b32 v226, v213
	ds_read_b32 v227, v213 offset:512
	ds_read_b32 v228, v213 offset:1024
	ds_read_b32 v229, v213 offset:1536
	ds_read_b32 v230, v213 offset:2048
	ds_read_b32 v231, v213 offset:2560
	ds_read_b32 v232, v213 offset:3072
	ds_read_b32 v233, v213 offset:3584
	ds_read_b32 v234, v213 offset:4096
	ds_read_b32 v235, v213 offset:4608
	ds_read_b32 v236, v213 offset:5120
	ds_read_b32 v237, v213 offset:5632
	ds_read_b32 v238, v213 offset:6144
	ds_read_b32 v239, v213 offset:6656
	ds_read_b32 v240, v213 offset:7168
	ds_read_b32 v241, v213 offset:7680
	s_waitcnt lgkmcnt(0)
	v_max_f32_e32 v226, v226, v226
	v_max_f32_e32 v227, v227, v227
	v_max_f32_e32 v228, v228, v228
	v_max_f32_e32 v229, v229, v229
	v_max_f32_e32 v230, v230, v230
	v_max_f32_e32 v231, v231, v231
	v_max_f32_e32 v232, v232, v232
	v_max_f32_e32 v233, v233, v233
	v_max_f32_e32 v234, v234, v234
	v_max_f32_e32 v235, v235, v235
	v_max_f32_e32 v236, v236, v236
	v_max_f32_e32 v237, v237, v237
	v_max_f32_e32 v238, v238, v238
	v_max_f32_e32 v239, v239, v239
	v_max_f32_e32 v240, v240, v240
	v_max_f32_e32 v241, v241, v241
	v_med3_f32 v226, v226, s62, v95
	v_med3_f32 v227, v227, s62, v95
	v_med3_f32 v228, v228, s62, v95
	v_med3_f32 v229, v229, s62, v95
	v_med3_f32 v230, v230, s62, v95
	v_med3_f32 v231, v231, s62, v95
	v_med3_f32 v232, v232, s62, v95
	v_med3_f32 v233, v233, s62, v95
	v_med3_f32 v234, v234, s62, v95
	v_med3_f32 v235, v235, s62, v95
	v_med3_f32 v236, v236, s62, v95
	v_med3_f32 v237, v237, s62, v95
	v_med3_f32 v238, v238, s62, v95
	v_med3_f32 v239, v239, s62, v95
	v_med3_f32 v240, v240, s62, v95
	v_med3_f32 v241, v241, s62, v95
	v_mov_b32_e32 v242, 0
	v_mov_b32_e32 v243, 0
	v_mov_b32_e32 v244, 0
	v_mov_b32_e32 v245, 0
	v_cvt_pk_fp8_f32 v242, v226, v227
	v_cvt_pk_fp8_f32 v243, v230, v231
	v_cvt_pk_fp8_f32 v244, v234, v235
	v_cvt_pk_fp8_f32 v245, v238, v239
	v_cvt_pk_fp8_f32 v242, v228, v229 op_sel:[0,0,1]
	v_cvt_pk_fp8_f32 v243, v232, v233 op_sel:[0,0,1]
	v_cvt_pk_fp8_f32 v244, v236, v237 op_sel:[0,0,1]
	v_cvt_pk_fp8_f32 v245, v240, v241 op_sel:[0,0,1]
	s_nop 0
	global_store_dwordx4 v78, v[242:245], s[6:7]
	s_waitcnt vmcnt(12)
	v_mul_f32_e32 v176, v34, v176
	v_mul_f32_e32 v177, v34, v177
	v_mul_f32_e32 v178, v34, v178
	v_mul_f32_e32 v179, v34, v179
	ds_write_b128 v210, v[176:179]
	v_mul_f32_e32 v180, v35, v180
	v_mul_f32_e32 v181, v35, v181
	v_mul_f32_e32 v182, v35, v182
	v_mul_f32_e32 v183, v35, v183
	ds_write_b128 v210, v[180:183] offset:1024
	v_mul_f32_e32 v184, v36, v184
	v_mul_f32_e32 v185, v36, v185
	v_mul_f32_e32 v186, v36, v186
	v_mul_f32_e32 v187, v36, v187
	ds_write_b128 v210, v[184:187] offset:2048
	v_mul_f32_e32 v188, v37, v188
	v_mul_f32_e32 v189, v37, v189
	v_mul_f32_e32 v190, v37, v190
	v_mul_f32_e32 v191, v37, v191
	ds_write_b128 v210, v[188:191] offset:3072
	v_mul_f32_e32 v192, v38, v192
	v_mul_f32_e32 v193, v38, v193
	v_mul_f32_e32 v194, v38, v194
	v_mul_f32_e32 v195, v38, v195
	ds_write_b128 v210, v[192:195] offset:4096
	v_mul_f32_e32 v196, v39, v196
	v_mul_f32_e32 v197, v39, v197
	v_mul_f32_e32 v198, v39, v198
	v_mul_f32_e32 v199, v39, v199
	ds_write_b128 v210, v[196:199] offset:5120
	v_mul_f32_e32 v200, v40, v200
	v_mul_f32_e32 v201, v40, v201
	v_mul_f32_e32 v202, v40, v202
	v_mul_f32_e32 v203, v40, v203
	ds_write_b128 v210, v[200:203] offset:6144
	v_mul_f32_e32 v204, v41, v204
	v_mul_f32_e32 v205, v41, v205
	v_mul_f32_e32 v206, v41, v206
	v_mul_f32_e32 v207, v41, v207
	ds_write_b128 v210, v[204:207] offset:7168
	s_waitcnt lgkmcnt(0)
	s_barrier
; #define GAS __attribute__((address_space(1)))
; #define LAS __attribute__((address_space(3)))
; #define LDS_WAIT() asm volatile("s_waitcnt lgkmcnt(0)" ::: "memory")
;     ...
; #pragma unroll
;     for (int i = 0; i < 32; ++i) v[i] = sc >= 0 ? W[(size_t)(k0 + 2 * i + (lane >> 5)) * Nsrc + sc] : 0.f;
; #pragma unroll
;     for (int i = 0; i < 32; ++i) { const int k = k0 + 2 * i + (lane >> 5); float x = v[i] * wscale; if (KS) x *= (k < ksplit ? ksA[k] : ksB[k - ksplit]); scr[(2 * i + (lane >> 5)) * 33 + (lane & 31)] = x; }
;     LDS_WAIT(); asm volatile("" ::: "memory");
;     const int c = lane & 7;
; #pragma unroll
;     for (int j = 0; j < 4; ++j) { const int n = (lane >> 3) + 8 * j; const LAS float* s = scr + (8 * c) * 33 + n;
;         const unsigned long long o = (unsigned long long)pg8::pk4_fp8(s[0 * 33], s[1 * 33], s[2 * 33], s[3 * 33]) | ((unsigned long long)pg8::pk4_fp8(s[4 * 33], s[5 * 33], s[6 * 33], s[7 * 33]) << 32);
;         *(GAS unsigned long long*)(WT + (size_t)(n0 + n) * K + k0 + 8 * c) = o; }
; __global__ void __launch_bounds__(NWAVES * 64, 2) hybrid_fwd(Args args) {
;     ...
;             p0_transpose_item_f8<false>(args.in[16] + (size_t)l * FF * DM, FF, DM, DM / 32, (unsigned char*)(ws + WS_WDN + l * SZ_WDN), 128.f, args.in[16], args.in[16], 0, scr, r, lane);
	s_add_u32 s8, s38, 0x1000
	s_addc_u32 s9, s39, 0
	global_load_dwordx4 v[176:179], v75, s[8:9]
	s_add_u32 s8, s8, 0x8000
	s_addc_u32 s9, s9, 0
	global_load_dwordx4 v[180:183], v75, s[8:9]
	s_add_u32 s8, s8, 0x8000
	s_addc_u32 s9, s9, 0
	global_load_dwordx4 v[184:187], v75, s[8:9]
	s_add_u32 s8, s8, 0x8000
	s_addc_u32 s9, s9, 0
	global_load_dwordx4 v[188:191], v75, s[8:9]
	s_add_u32 s8, s8, 0x8000
	s_addc_u32 s9, s9, 0
	global_load_dwordx4 v[192:195], v75, s[8:9]
	s_add_u32 s8, s8, 0x8000
	s_addc_u32 s9, s9, 0
	global_load_dwordx4 v[196:199], v75, s[8:9]
	s_add_u32 s8, s8, 0x8000
	s_addc_u32 s9, s9, 0
	global_load_dwordx4 v[200:203], v75, s[8:9]
	s_add_u32 s8, s8, 0x8000
	s_addc_u32 s9, s9, 0
	global_load_dwordx4 v[204:207], v75, s[8:9]
	s_add_u32 s6, s36, 0x3c00000
	s_addc_u32 s7, s37, 0
	ds_read_b32 v226, v212
	ds_read_b32 v227, v212 offset:512
	ds_read_b32 v228, v212 offset:1024
	ds_read_b32 v229, v212 offset:1536
	ds_read_b32 v230, v212 offset:2048
	ds_read_b32 v231, v212 offset:2560
	ds_read_b32 v232, v212 offset:3072
	ds_read_b32 v233, v212 offset:3584
	ds_read_b32 v234, v212 offset:4096
	ds_read_b32 v235, v212 offset:4608
	ds_read_b32 v236, v212 offset:5120
	ds_read_b32 v237, v212 offset:5632
	ds_read_b32 v238, v212 offset:6144
	ds_read_b32 v239, v212 offset:6656
	ds_read_b32 v240, v212 offset:7168
	ds_read_b32 v241, v212 offset:7680
	s_waitcnt lgkmcnt(0)
	v_max_f32_e32 v226, v226, v226
	v_max_f32_e32 v227, v227, v227
	v_max_f32_e32 v228, v228, v228
	v_max_f32_e32 v229, v229, v229
	v_max_f32_e32 v230, v230, v230
	v_max_f32_e32 v231, v231, v231
	v_max_f32_e32 v232, v232, v232
	v_max_f32_e32 v233, v233, v233
	v_max_f32_e32 v234, v234, v234
	v_max_f32_e32 v235, v235, v235
	v_max_f32_e32 v236, v236, v236
	v_max_f32_e32 v237, v237, v237
	v_max_f32_e32 v238, v238, v238
	v_max_f32_e32 v239, v239, v239
	v_max_f32_e32 v240, v240, v240
	v_max_f32_e32 v241, v241, v241
	v_med3_f32 v226, v226, s62, v95
	v_med3_f32 v227, v227, s62, v95
	v_med3_f32 v228, v228, s62, v95
	v_med3_f32 v229, v229, s62, v95
	v_med3_f32 v230, v230, s62, v95
	v_med3_f32 v231, v231, s62, v95
	v_med3_f32 v232, v232, s62, v95
	v_med3_f32 v233, v233, s62, v95
	v_med3_f32 v234, v234, s62, v95
	v_med3_f32 v235, v235, s62, v95
	v_med3_f32 v236, v236, s62, v95
	v_med3_f32 v237, v237, s62, v95
	v_med3_f32 v238, v238, s62, v95
	v_med3_f32 v239, v239, s62, v95
	v_med3_f32 v240, v240, s62, v95
	v_med3_f32 v241, v241, s62, v95
	v_mov_b32_e32 v242, 0
	v_mov_b32_e32 v243, 0
	v_mov_b32_e32 v244, 0
	v_mov_b32_e32 v245, 0
	v_cvt_pk_fp8_f32 v242, v226, v227
	v_cvt_pk_fp8_f32 v243, v230, v231
	v_cvt_pk_fp8_f32 v244, v234, v235
	v_cvt_pk_fp8_f32 v245, v238, v239
	v_cvt_pk_fp8_f32 v242, v228, v229 op_sel:[0,0,1]
	v_cvt_pk_fp8_f32 v243, v232, v233 op_sel:[0,0,1]
	v_cvt_pk_fp8_f32 v244, v236, v237 op_sel:[0,0,1]
	v_cvt_pk_fp8_f32 v245, v240, v241 op_sel:[0,0,1]
	s_nop 0
	global_store_dwordx4 v77, v[242:245], s[6:7]
	ds_read_b32 v226, v214
	ds_read_b32 v227, v214 offset:512
	ds_read_b32 v228, v214 offset:1024
	ds_read_b32 v229, v214 offset:1536
	ds_read_b32 v230, v214 offset:2048
	ds_read_b32 v231, v214 offset:2560
	ds_read_b32 v232, v214 offset:3072
	ds_read_b32 v233, v214 offset:3584
	ds_read_b32 v234, v214 offset:4096
	ds_read_b32 v235, v214 offset:4608
	ds_read_b32 v236, v214 offset:5120
	ds_read_b32 v237, v214 offset:5632
	ds_read_b32 v238, v214 offset:6144
	ds_read_b32 v239, v214 offset:6656
	ds_read_b32 v240, v214 offset:7168
	ds_read_b32 v241, v214 offset:7680
	s_waitcnt lgkmcnt(0)
	v_max_f32_e32 v226, v226, v226
	v_max_f32_e32 v227, v227, v227
	v_max_f32_e32 v228, v228, v228
	v_max_f32_e32 v229, v229, v229
	v_max_f32_e32 v230, v230, v230
	v_max_f32_e32 v231, v231, v231
	v_max_f32_e32 v232, v232, v232
	v_max_f32_e32 v233, v233, v233
	v_max_f32_e32 v234, v234, v234
	v_max_f32_e32 v235, v235, v235
	v_max_f32_e32 v236, v236, v236
	v_max_f32_e32 v237, v237, v237
	v_max_f32_e32 v238, v238, v238
	v_max_f32_e32 v239, v239, v239
	v_max_f32_e32 v240, v240, v240
	v_max_f32_e32 v241, v241, v241
	v_med3_f32 v226, v226, s62, v95
	v_med3_f32 v227, v227, s62, v95
	v_med3_f32 v228, v228, s62, v95
	v_med3_f32 v229, v229, s62, v95
	v_med3_f32 v230, v230, s62, v95
	v_med3_f32 v231, v231, s62, v95
	v_med3_f32 v232, v232, s62, v95
	v_med3_f32 v233, v233, s62, v95
	v_med3_f32 v234, v234, s62, v95
	v_med3_f32 v235, v235, s62, v95
	v_med3_f32 v236, v236, s62, v95
	v_med3_f32 v237, v237, s62, v95
	v_med3_f32 v238, v238, s62, v95
	v_med3_f32 v239, v239, s62, v95
	v_med3_f32 v240, v240, s62, v95
	v_med3_f32 v241, v241, s62, v95
	v_mov_b32_e32 v242, 0
	v_mov_b32_e32 v243, 0
	v_mov_b32_e32 v244, 0
	v_mov_b32_e32 v245, 0
	v_cvt_pk_fp8_f32 v242, v226, v227
	v_cvt_pk_fp8_f32 v243, v230, v231
	v_cvt_pk_fp8_f32 v244, v234, v235
	v_cvt_pk_fp8_f32 v245, v238, v239
	v_cvt_pk_fp8_f32 v242, v228, v229 op_sel:[0,0,1]
	v_cvt_pk_fp8_f32 v243, v232, v233 op_sel:[0,0,1]
	v_cvt_pk_fp8_f32 v244, v236, v237 op_sel:[0,0,1]
	v_cvt_pk_fp8_f32 v245, v240, v241 op_sel:[0,0,1]
	s_nop 0
	global_store_dwordx4 v78, v[242:245], s[6:7]
	s_waitcnt vmcnt(12)
	v_mul_f32_e32 v144, 0x43000000, v144
	v_mul_f32_e32 v145, 0x43000000, v145
	v_mul_f32_e32 v146, 0x43000000, v146
	v_mul_f32_e32 v147, 0x43000000, v147
	ds_write_b128 v209, v[144:147]
	v_mul_f32_e32 v148, 0x43000000, v148
	v_mul_f32_e32 v149, 0x43000000, v149
	v_mul_f32_e32 v150, 0x43000000, v150
	v_mul_f32_e32 v151, 0x43000000, v151
	ds_write_b128 v209, v[148:151] offset:1024
	v_mul_f32_e32 v152, 0x43000000, v152
	v_mul_f32_e32 v153, 0x43000000, v153
	v_mul_f32_e32 v154, 0x43000000, v154
	v_mul_f32_e32 v155, 0x43000000, v155
	ds_write_b128 v209, v[152:155] offset:2048
	v_mul_f32_e32 v156, 0x43000000, v156
	v_mul_f32_e32 v157, 0x43000000, v157
	v_mul_f32_e32 v158, 0x43000000, v158
	v_mul_f32_e32 v159, 0x43000000, v159
	ds_write_b128 v209, v[156:159] offset:3072
	v_mul_f32_e32 v160, 0x43000000, v160
	v_mul_f32_e32 v161, 0x43000000, v161
	v_mul_f32_e32 v162, 0x43000000, v162
	v_mul_f32_e32 v163, 0x43000000, v163
	ds_write_b128 v209, v[160:163] offset:4096
	v_mul_f32_e32 v164, 0x43000000, v164
	v_mul_f32_e32 v165, 0x43000000, v165
	v_mul_f32_e32 v166, 0x43000000, v166
	v_mul_f32_e32 v167, 0x43000000, v167
	ds_write_b128 v209, v[164:167] offset:5120
	v_mul_f32_e32 v168, 0x43000000, v168
	v_mul_f32_e32 v169, 0x43000000, v169
	v_mul_f32_e32 v170, 0x43000000, v170
	v_mul_f32_e32 v171, 0x43000000, v171
	ds_write_b128 v209, v[168:171] offset:6144
	v_mul_f32_e32 v172, 0x43000000, v172
	v_mul_f32_e32 v173, 0x43000000, v173
	v_mul_f32_e32 v174, 0x43000000, v174
	v_mul_f32_e32 v175, 0x43000000, v175
	ds_write_b128 v209, v[172:175] offset:7168
	s_waitcnt lgkmcnt(0)
	s_barrier
; #define GAS __attribute__((address_space(1)))
; #define LAS __attribute__((address_space(3)))
; #define LDS_WAIT() asm volatile("s_waitcnt lgkmcnt(0)" ::: "memory")
; __device__ __forceinline__ unsigned pk4_fp8(float a, float b, float c, float d) {
;     a = fminf(fmaxf(a, -448.f), 448.f); b = fminf(fmaxf(b, -448.f), 448.f); c = fminf(fmaxf(c, -448.f), 448.f); d = fminf(fmaxf(d, -448.f), 448.f);
;     int w = __builtin_amdgcn_cvt_pk_fp8_f32(a, b, 0, false); w = __builtin_amdgcn_cvt_pk_fp8_f32(c, d, w, true); return (unsigned)w; }
;     ...
; #pragma unroll
;     for (int i = 0; i < 32; ++i) v[i] = sc >= 0 ? W[(size_t)(k0 + 2 * i + (lane >> 5)) * Nsrc + sc] : 0.f;
; #pragma unroll
;     for (int i = 0; i < 32; ++i) { const int k = k0 + 2 * i + (lane >> 5); float x = v[i] * wscale; if (KS) x *= (k < ksplit ? ksA[k] : ksB[k - ksplit]); scr[(2 * i + (lane >> 5)) * 33 + (lane & 31)] = x; }
;     LDS_WAIT(); asm volatile("" ::: "memory");
;     const int c = lane & 7;
; #pragma unroll
;     for (int j = 0; j < 4; ++j) { const int n = (lane >> 3) + 8 * j; const LAS float* s = scr + (8 * c) * 33 + n;
;         const unsigned long long o = (unsigned long long)pg8::pk4_fp8(s[0 * 33], s[1 * 33], s[2 * 33], s[3 * 33]) | ((unsigned long long)pg8::pk4_fp8(s[4 * 33], s[5 * 33], s[6 * 33], s[7 * 33]) << 32);
;         *(GAS unsigned long long*)(WT + (size_t)(n0 + n) * K + k0 + 8 * c) = o; }
	s_add_u32 s8, s38, 0x2000
	s_addc_u32 s9, s39, 0
	global_load_dwordx4 v[144:147], v75, s[8:9]
	s_add_u32 s8, s8, 0x8000
	s_addc_u32 s9, s9, 0
	global_load_dwordx4 v[148:151], v75, s[8:9]
	s_add_u32 s8, s8, 0x8000
	s_addc_u32 s9, s9, 0
	global_load_dwordx4 v[152:155], v75, s[8:9]
	s_add_u32 s8, s8, 0x8000
	s_addc_u32 s9, s9, 0
	global_load_dwordx4 v[156:159], v75, s[8:9]
	s_add_u32 s8, s8, 0x8000
	s_addc_u32 s9, s9, 0
	global_load_dwordx4 v[160:163], v75, s[8:9]
	s_add_u32 s8, s8, 0x8000
	s_addc_u32 s9, s9, 0
	global_load_dwordx4 v[164:167], v75, s[8:9]
	s_add_u32 s8, s8, 0x8000
	s_addc_u32 s9, s9, 0
	global_load_dwordx4 v[168:171], v75, s[8:9]
	s_add_u32 s8, s8, 0x8000
	s_addc_u32 s9, s9, 0
	global_load_dwordx4 v[172:175], v75, s[8:9]
	s_mov_b64 s[6:7], s[40:41]
	ds_read_b32 v226, v211
	ds_read_b32 v227, v211 offset:512
	ds_read_b32 v228, v211 offset:1024
	ds_read_b32 v229, v211 offset:1536
	ds_read_b32 v230, v211 offset:2048
	ds_read_b32 v231, v211 offset:2560
	ds_read_b32 v232, v211 offset:3072
	ds_read_b32 v233, v211 offset:3584
	ds_read_b32 v234, v211 offset:4096
	ds_read_b32 v235, v211 offset:4608
	ds_read_b32 v236, v211 offset:5120
	ds_read_b32 v237, v211 offset:5632
	ds_read_b32 v238, v211 offset:6144
	ds_read_b32 v239, v211 offset:6656
	ds_read_b32 v240, v211 offset:7168
	ds_read_b32 v241, v211 offset:7680
	s_waitcnt lgkmcnt(0)
	v_max_f32_e32 v226, v226, v226
	v_max_f32_e32 v227, v227, v227
	v_max_f32_e32 v228, v228, v228
	v_max_f32_e32 v229, v229, v229
	v_max_f32_e32 v230, v230, v230
	v_max_f32_e32 v231, v231, v231
	v_max_f32_e32 v232, v232, v232
	v_max_f32_e32 v233, v233, v233
	v_max_f32_e32 v234, v234, v234
	v_max_f32_e32 v235, v235, v235
	v_max_f32_e32 v236, v236, v236
	v_max_f32_e32 v237, v237, v237
	v_max_f32_e32 v238, v238, v238
	v_max_f32_e32 v239, v239, v239
	v_max_f32_e32 v240, v240, v240
	v_max_f32_e32 v241, v241, v241
	v_med3_f32 v226, v226, s62, v95
	v_med3_f32 v227, v227, s62, v95
	v_med3_f32 v228, v228, s62, v95
	v_med3_f32 v229, v229, s62, v95
	v_med3_f32 v230, v230, s62, v95
	v_med3_f32 v231, v231, s62, v95
	v_med3_f32 v232, v232, s62, v95
	v_med3_f32 v233, v233, s62, v95
	v_med3_f32 v234, v234, s62, v95
	v_med3_f32 v235, v235, s62, v95
	v_med3_f32 v236, v236, s62, v95
	v_med3_f32 v237, v237, s62, v95
	v_med3_f32 v238, v238, s62, v95
	v_med3_f32 v239, v239, s62, v95
	v_med3_f32 v240, v240, s62, v95
	v_med3_f32 v241, v241, s62, v95
	v_mov_b32_e32 v242, 0
	v_mov_b32_e32 v243, 0
	v_mov_b32_e32 v244, 0
	v_mov_b32_e32 v245, 0
	v_cvt_pk_fp8_f32 v242, v226, v227
	v_cvt_pk_fp8_f32 v243, v230, v231
	v_cvt_pk_fp8_f32 v244, v234, v235
	v_cvt_pk_fp8_f32 v245, v238, v239
	v_cvt_pk_fp8_f32 v242, v228, v229 op_sel:[0,0,1]
	v_cvt_pk_fp8_f32 v243, v232, v233 op_sel:[0,0,1]
	v_cvt_pk_fp8_f32 v244, v236, v237 op_sel:[0,0,1]
	v_cvt_pk_fp8_f32 v245, v240, v241 op_sel:[0,0,1]
	s_nop 0
	global_store_dwordx4 v79, v[242:245], s[6:7]
	ds_read_b32 v226, v213
	ds_read_b32 v227, v213 offset:512
	ds_read_b32 v228, v213 offset:1024
	ds_read_b32 v229, v213 offset:1536
	ds_read_b32 v230, v213 offset:2048
	ds_read_b32 v231, v213 offset:2560
	ds_read_b32 v232, v213 offset:3072
	ds_read_b32 v233, v213 offset:3584
	ds_read_b32 v234, v213 offset:4096
	ds_read_b32 v235, v213 offset:4608
	ds_read_b32 v236, v213 offset:5120
	ds_read_b32 v237, v213 offset:5632
	ds_read_b32 v238, v213 offset:6144
	ds_read_b32 v239, v213 offset:6656
	ds_read_b32 v240, v213 offset:7168
	ds_read_b32 v241, v213 offset:7680
	s_waitcnt lgkmcnt(0)
	v_max_f32_e32 v226, v226, v226
	v_max_f32_e32 v227, v227, v227
	v_max_f32_e32 v228, v228, v228
	v_max_f32_e32 v229, v229, v229
	v_max_f32_e32 v230, v230, v230
	v_max_f32_e32 v231, v231, v231
	v_max_f32_e32 v232, v232, v232
	v_max_f32_e32 v233, v233, v233
	v_max_f32_e32 v234, v234, v234
	v_max_f32_e32 v235, v235, v235
	v_max_f32_e32 v236, v236, v236
	v_max_f32_e32 v237, v237, v237
	v_max_f32_e32 v238, v238, v238
	v_max_f32_e32 v239, v239, v239
	v_max_f32_e32 v240, v240, v240
	v_max_f32_e32 v241, v241, v241
	v_med3_f32 v226, v226, s62, v95
	v_med3_f32 v227, v227, s62, v95
	v_med3_f32 v228, v228, s62, v95
	v_med3_f32 v229, v229, s62, v95
	v_med3_f32 v230, v230, s62, v95
	v_med3_f32 v231, v231, s62, v95
	v_med3_f32 v232, v232, s62, v95
	v_med3_f32 v233, v233, s62, v95
	v_med3_f32 v234, v234, s62, v95
	v_med3_f32 v235, v235, s62, v95
	v_med3_f32 v236, v236, s62, v95
	v_med3_f32 v237, v237, s62, v95
	v_med3_f32 v238, v238, s62, v95
	v_med3_f32 v239, v239, s62, v95
	v_med3_f32 v240, v240, s62, v95
	v_med3_f32 v241, v241, s62, v95
	v_mov_b32_e32 v242, 0
	v_mov_b32_e32 v243, 0
	v_mov_b32_e32 v244, 0
	v_mov_b32_e32 v245, 0
	v_cvt_pk_fp8_f32 v242, v226, v227
	v_cvt_pk_fp8_f32 v243, v230, v231
	v_cvt_pk_fp8_f32 v244, v234, v235
	v_cvt_pk_fp8_f32 v245, v238, v239
	v_cvt_pk_fp8_f32 v242, v228, v229 op_sel:[0,0,1]
	v_cvt_pk_fp8_f32 v243, v232, v233 op_sel:[0,0,1]
	v_cvt_pk_fp8_f32 v244, v236, v237 op_sel:[0,0,1]
	v_cvt_pk_fp8_f32 v245, v240, v241 op_sel:[0,0,1]
	s_nop 0
	global_store_dwordx4 v80, v[242:245], s[6:7]
	s_waitcnt vmcnt(12)
	v_mul_f32_e32 v176, 0x43000000, v176
	v_mul_f32_e32 v177, 0x43000000, v177
	v_mul_f32_e32 v178, 0x43000000, v178
	v_mul_f32_e32 v179, 0x43000000, v179
	ds_write_b128 v210, v[176:179]
	v_mul_f32_e32 v180, 0x43000000, v180
	v_mul_f32_e32 v181, 0x43000000, v181
	v_mul_f32_e32 v182, 0x43000000, v182
	v_mul_f32_e32 v183, 0x43000000, v183
	ds_write_b128 v210, v[180:183] offset:1024
	v_mul_f32_e32 v184, 0x43000000, v184
	v_mul_f32_e32 v185, 0x43000000, v185
	v_mul_f32_e32 v186, 0x43000000, v186
	v_mul_f32_e32 v187, 0x43000000, v187
	ds_write_b128 v210, v[184:187] offset:2048
	v_mul_f32_e32 v188, 0x43000000, v188
	v_mul_f32_e32 v189, 0x43000000, v189
	v_mul_f32_e32 v190, 0x43000000, v190
	v_mul_f32_e32 v191, 0x43000000, v191
	ds_write_b128 v210, v[188:191] offset:3072
	v_mul_f32_e32 v192, 0x43000000, v192
	v_mul_f32_e32 v193, 0x43000000, v193
	v_mul_f32_e32 v194, 0x43000000, v194
	v_mul_f32_e32 v195, 0x43000000, v195
	ds_write_b128 v210, v[192:195] offset:4096
	v_mul_f32_e32 v196, 0x43000000, v196
	v_mul_f32_e32 v197, 0x43000000, v197
	v_mul_f32_e32 v198, 0x43000000, v198
	v_mul_f32_e32 v199, 0x43000000, v199
	ds_write_b128 v210, v[196:199] offset:5120
	v_mul_f32_e32 v200, 0x43000000, v200
	v_mul_f32_e32 v201, 0x43000000, v201
	v_mul_f32_e32 v202, 0x43000000, v202
	v_mul_f32_e32 v203, 0x43000000, v203
	ds_write_b128 v210, v[200:203] offset:6144
	v_mul_f32_e32 v204, 0x43000000, v204
	v_mul_f32_e32 v205, 0x43000000, v205
	v_mul_f32_e32 v206, 0x43000000, v206
	v_mul_f32_e32 v207, 0x43000000, v207
	ds_write_b128 v210, v[204:207] offset:7168
	s_waitcnt lgkmcnt(0)
	s_barrier
; #define GAS __attribute__((address_space(1)))
; #define LAS __attribute__((address_space(3)))
; #define LDS_WAIT() asm volatile("s_waitcnt lgkmcnt(0)" ::: "memory")
; __device__ __forceinline__ unsigned pk4_fp8(float a, float b, float c, float d) {
;     a = fminf(fmaxf(a, -448.f), 448.f); b = fminf(fmaxf(b, -448.f), 448.f); c = fminf(fmaxf(c, -448.f), 448.f); d = fminf(fmaxf(d, -448.f), 448.f);
;     int w = __builtin_amdgcn_cvt_pk_fp8_f32(a, b, 0, false); w = __builtin_amdgcn_cvt_pk_fp8_f32(c, d, w, true); return (unsigned)w; }
;     ...
; #pragma unroll
;     for (int i = 0; i < 32; ++i) v[i] = sc >= 0 ? W[(size_t)(k0 + 2 * i + (lane >> 5)) * Nsrc + sc] : 0.f;
; #pragma unroll
;     for (int i = 0; i < 32; ++i) { const int k = k0 + 2 * i + (lane >> 5); float x = v[i] * wscale; if (KS) x *= (k < ksplit ? ksA[k] : ksB[k - ksplit]); scr[(2 * i + (lane >> 5)) * 33 + (lane & 31)] = x; }
;     LDS_WAIT(); asm volatile("" ::: "memory");
;     const int c = lane & 7;
; #pragma unroll
;     for (int j = 0; j < 4; ++j) { const int n = (lane >> 3) + 8 * j; const LAS float* s = scr + (8 * c) * 33 + n;
;         const unsigned long long o = (unsigned long long)pg8::pk4_fp8(s[0 * 33], s[1 * 33], s[2 * 33], s[3 * 33]) | ((unsigned long long)pg8::pk4_fp8(s[4 * 33], s[5 * 33], s[6 * 33], s[7 * 33]) << 32);
;         *(GAS unsigned long long*)(WT + (size_t)(n0 + n) * K + k0 + 8 * c) = o; }
	s_add_u32 s8, s38, 0x3000
	s_addc_u32 s9, s39, 0
	global_load_dwordx4 v[176:179], v75, s[8:9]
	s_add_u32 s8, s8, 0x8000
	s_addc_u32 s9, s9, 0
	global_load_dwordx4 v[180:183], v75, s[8:9]
	s_add_u32 s8, s8, 0x8000
	s_addc_u32 s9, s9, 0
	global_load_dwordx4 v[184:187], v75, s[8:9]
	s_add_u32 s8, s8, 0x8000
	s_addc_u32 s9, s9, 0
	global_load_dwordx4 v[188:191], v75, s[8:9]
	s_add_u32 s8, s8, 0x8000
	s_addc_u32 s9, s9, 0
	global_load_dwordx4 v[192:195], v75, s[8:9]
	s_add_u32 s8, s8, 0x8000
	s_addc_u32 s9, s9, 0
	global_load_dwordx4 v[196:199], v75, s[8:9]
	s_add_u32 s8, s8, 0x8000
	s_addc_u32 s9, s9, 0
	global_load_dwordx4 v[200:203], v75, s[8:9]
	s_add_u32 s8, s8, 0x8000
	s_addc_u32 s9, s9, 0
	global_load_dwordx4 v[204:207], v75, s[8:9]
	s_add_u32 s6, s40, 0x1000000
	s_addc_u32 s7, s41, 0
	ds_read_b32 v226, v212
	ds_read_b32 v227, v212 offset:512
	ds_read_b32 v228, v212 offset:1024
	ds_read_b32 v229, v212 offset:1536
	ds_read_b32 v230, v212 offset:2048
	ds_read_b32 v231, v212 offset:2560
	ds_read_b32 v232, v212 offset:3072
	ds_read_b32 v233, v212 offset:3584
	ds_read_b32 v234, v212 offset:4096
	ds_read_b32 v235, v212 offset:4608
	ds_read_b32 v236, v212 offset:5120
	ds_read_b32 v237, v212 offset:5632
	ds_read_b32 v238, v212 offset:6144
	ds_read_b32 v239, v212 offset:6656
	ds_read_b32 v240, v212 offset:7168
	ds_read_b32 v241, v212 offset:7680
	s_waitcnt lgkmcnt(0)
	v_max_f32_e32 v226, v226, v226
	v_max_f32_e32 v227, v227, v227
	v_max_f32_e32 v228, v228, v228
	v_max_f32_e32 v229, v229, v229
	v_max_f32_e32 v230, v230, v230
	v_max_f32_e32 v231, v231, v231
	v_max_f32_e32 v232, v232, v232
	v_max_f32_e32 v233, v233, v233
	v_max_f32_e32 v234, v234, v234
	v_max_f32_e32 v235, v235, v235
	v_max_f32_e32 v236, v236, v236
	v_max_f32_e32 v237, v237, v237
	v_max_f32_e32 v238, v238, v238
	v_max_f32_e32 v239, v239, v239
	v_max_f32_e32 v240, v240, v240
	v_max_f32_e32 v241, v241, v241
	v_med3_f32 v226, v226, s62, v95
	v_med3_f32 v227, v227, s62, v95
	v_med3_f32 v228, v228, s62, v95
	v_med3_f32 v229, v229, s62, v95
	v_med3_f32 v230, v230, s62, v95
	v_med3_f32 v231, v231, s62, v95
	v_med3_f32 v232, v232, s62, v95
	v_med3_f32 v233, v233, s62, v95
	v_med3_f32 v234, v234, s62, v95
	v_med3_f32 v235, v235, s62, v95
	v_med3_f32 v236, v236, s62, v95
	v_med3_f32 v237, v237, s62, v95
	v_med3_f32 v238, v238, s62, v95
	v_med3_f32 v239, v239, s62, v95
	v_med3_f32 v240, v240, s62, v95
	v_med3_f32 v241, v241, s62, v95
	v_mov_b32_e32 v242, 0
	v_mov_b32_e32 v243, 0
	v_mov_b32_e32 v244, 0
	v_mov_b32_e32 v245, 0
	v_cvt_pk_fp8_f32 v242, v226, v227
	v_cvt_pk_fp8_f32 v243, v230, v231
	v_cvt_pk_fp8_f32 v244, v234, v235
	v_cvt_pk_fp8_f32 v245, v238, v239
	v_cvt_pk_fp8_f32 v242, v228, v229 op_sel:[0,0,1]
	v_cvt_pk_fp8_f32 v243, v232, v233 op_sel:[0,0,1]
	v_cvt_pk_fp8_f32 v244, v236, v237 op_sel:[0,0,1]
	v_cvt_pk_fp8_f32 v245, v240, v241 op_sel:[0,0,1]
	s_nop 0
	global_store_dwordx4 v79, v[242:245], s[6:7]
	ds_read_b32 v226, v214
	ds_read_b32 v227, v214 offset:512
	ds_read_b32 v228, v214 offset:1024
	ds_read_b32 v229, v214 offset:1536
	ds_read_b32 v230, v214 offset:2048
	ds_read_b32 v231, v214 offset:2560
	ds_read_b32 v232, v214 offset:3072
	ds_read_b32 v233, v214 offset:3584
	ds_read_b32 v234, v214 offset:4096
	ds_read_b32 v235, v214 offset:4608
	ds_read_b32 v236, v214 offset:5120
	ds_read_b32 v237, v214 offset:5632
	ds_read_b32 v238, v214 offset:6144
	ds_read_b32 v239, v214 offset:6656
	ds_read_b32 v240, v214 offset:7168
	ds_read_b32 v241, v214 offset:7680
	s_waitcnt lgkmcnt(0)
	v_max_f32_e32 v226, v226, v226
	v_max_f32_e32 v227, v227, v227
	v_max_f32_e32 v228, v228, v228
	v_max_f32_e32 v229, v229, v229
	v_max_f32_e32 v230, v230, v230
	v_max_f32_e32 v231, v231, v231
	v_max_f32_e32 v232, v232, v232
	v_max_f32_e32 v233, v233, v233
	v_max_f32_e32 v234, v234, v234
	v_max_f32_e32 v235, v235, v235
	v_max_f32_e32 v236, v236, v236
	v_max_f32_e32 v237, v237, v237
	v_max_f32_e32 v238, v238, v238
	v_max_f32_e32 v239, v239, v239
	v_max_f32_e32 v240, v240, v240
	v_max_f32_e32 v241, v241, v241
	v_med3_f32 v226, v226, s62, v95
	v_med3_f32 v227, v227, s62, v95
	v_med3_f32 v228, v228, s62, v95
	v_med3_f32 v229, v229, s62, v95
	v_med3_f32 v230, v230, s62, v95
	v_med3_f32 v231, v231, s62, v95
	v_med3_f32 v232, v232, s62, v95
	v_med3_f32 v233, v233, s62, v95
	v_med3_f32 v234, v234, s62, v95
	v_med3_f32 v235, v235, s62, v95
	v_med3_f32 v236, v236, s62, v95
	v_med3_f32 v237, v237, s62, v95
	v_med3_f32 v238, v238, s62, v95
	v_med3_f32 v239, v239, s62, v95
	v_med3_f32 v240, v240, s62, v95
	v_med3_f32 v241, v241, s62, v95
	v_mov_b32_e32 v242, 0
	v_mov_b32_e32 v243, 0
	v_mov_b32_e32 v244, 0
	v_mov_b32_e32 v245, 0
	v_cvt_pk_fp8_f32 v242, v226, v227
	v_cvt_pk_fp8_f32 v243, v230, v231
	v_cvt_pk_fp8_f32 v244, v234, v235
	v_cvt_pk_fp8_f32 v245, v238, v239
	v_cvt_pk_fp8_f32 v242, v228, v229 op_sel:[0,0,1]
	v_cvt_pk_fp8_f32 v243, v232, v233 op_sel:[0,0,1]
	v_cvt_pk_fp8_f32 v244, v236, v237 op_sel:[0,0,1]
	v_cvt_pk_fp8_f32 v245, v240, v241 op_sel:[0,0,1]
	s_nop 0
	global_store_dwordx4 v80, v[242:245], s[6:7]
	s_waitcnt vmcnt(12)
	v_mul_f32_e32 v144, 0x43000000, v144
	v_mul_f32_e32 v145, 0x43000000, v145
	v_mul_f32_e32 v146, 0x43000000, v146
	v_mul_f32_e32 v147, 0x43000000, v147
	ds_write_b128 v209, v[144:147]
	v_mul_f32_e32 v148, 0x43000000, v148
	v_mul_f32_e32 v149, 0x43000000, v149
	v_mul_f32_e32 v150, 0x43000000, v150
	v_mul_f32_e32 v151, 0x43000000, v151
	ds_write_b128 v209, v[148:151] offset:1024
	v_mul_f32_e32 v152, 0x43000000, v152
	v_mul_f32_e32 v153, 0x43000000, v153
	v_mul_f32_e32 v154, 0x43000000, v154
	v_mul_f32_e32 v155, 0x43000000, v155
	ds_write_b128 v209, v[152:155] offset:2048
	v_mul_f32_e32 v156, 0x43000000, v156
	v_mul_f32_e32 v157, 0x43000000, v157
	v_mul_f32_e32 v158, 0x43000000, v158
	v_mul_f32_e32 v159, 0x43000000, v159
	ds_write_b128 v209, v[156:159] offset:3072
	v_mul_f32_e32 v160, 0x43000000, v160
	v_mul_f32_e32 v161, 0x43000000, v161
	v_mul_f32_e32 v162, 0x43000000, v162
	v_mul_f32_e32 v163, 0x43000000, v163
	ds_write_b128 v209, v[160:163] offset:4096
	v_mul_f32_e32 v164, 0x43000000, v164
	v_mul_f32_e32 v165, 0x43000000, v165
	v_mul_f32_e32 v166, 0x43000000, v166
	v_mul_f32_e32 v167, 0x43000000, v167
	ds_write_b128 v209, v[164:167] offset:5120
	v_mul_f32_e32 v168, 0x43000000, v168
	v_mul_f32_e32 v169, 0x43000000, v169
	v_mul_f32_e32 v170, 0x43000000, v170
	v_mul_f32_e32 v171, 0x43000000, v171
	ds_write_b128 v209, v[168:171] offset:6144
	v_mul_f32_e32 v172, 0x43000000, v172
	v_mul_f32_e32 v173, 0x43000000, v173
	v_mul_f32_e32 v174, 0x43000000, v174
	v_mul_f32_e32 v175, 0x43000000, v175
	ds_write_b128 v209, v[172:175] offset:7168
	s_waitcnt lgkmcnt(0)
	s_barrier
; #define GAS __attribute__((address_space(1)))
; #define LAS __attribute__((address_space(3)))
; #define LDS_WAIT() asm volatile("s_waitcnt lgkmcnt(0)" ::: "memory")
; __device__ __forceinline__ unsigned pk4_fp8(float a, float b, float c, float d) {
;     a = fminf(fmaxf(a, -448.f), 448.f); b = fminf(fmaxf(b, -448.f), 448.f); c = fminf(fmaxf(c, -448.f), 448.f); d = fminf(fmaxf(d, -448.f), 448.f);
;     int w = __builtin_amdgcn_cvt_pk_fp8_f32(a, b, 0, false); w = __builtin_amdgcn_cvt_pk_fp8_f32(c, d, w, true); return (unsigned)w; }
;     ...
; #pragma unroll
;     for (int i = 0; i < 32; ++i) v[i] = sc >= 0 ? W[(size_t)(k0 + 2 * i + (lane >> 5)) * Nsrc + sc] : 0.f;
; #pragma unroll
;     for (int i = 0; i < 32; ++i) { const int k = k0 + 2 * i + (lane >> 5); float x = v[i] * wscale; if (KS) x *= (k < ksplit ? ksA[k] : ksB[k - ksplit]); scr[(2 * i + (lane >> 5)) * 33 + (lane & 31)] = x; }
;     LDS_WAIT(); asm volatile("" ::: "memory");
;     const int c = lane & 7;
; #pragma unroll
;     for (int j = 0; j < 4; ++j) { const int n = (lane >> 3) + 8 * j; const LAS float* s = scr + (8 * c) * 33 + n;
;         const unsigned long long o = (unsigned long long)pg8::pk4_fp8(s[0 * 33], s[1 * 33], s[2 * 33], s[3 * 33]) | ((unsigned long long)pg8::pk4_fp8(s[4 * 33], s[5 * 33], s[6 * 33], s[7 * 33]) << 32);
;         *(GAS unsigned long long*)(WT + (size_t)(n0 + n) * K + k0 + 8 * c) = o; }
	s_add_u32 s8, s38, 0x4000000
	s_addc_u32 s9, s39, 0
	global_load_dwordx4 v[144:147], v75, s[8:9]
	s_add_u32 s8, s8, 0x8000
	s_addc_u32 s9, s9, 0
	global_load_dwordx4 v[148:151], v75, s[8:9]
	s_add_u32 s8, s8, 0x8000
	s_addc_u32 s9, s9, 0
	global_load_dwordx4 v[152:155], v75, s[8:9]
	s_add_u32 s8, s8, 0x8000
	s_addc_u32 s9, s9, 0
	global_load_dwordx4 v[156:159], v75, s[8:9]
	s_add_u32 s8, s8, 0x8000
	s_addc_u32 s9, s9, 0
	global_load_dwordx4 v[160:163], v75, s[8:9]
	s_add_u32 s8, s8, 0x8000
	s_addc_u32 s9, s9, 0
	global_load_dwordx4 v[164:167], v75, s[8:9]
	s_add_u32 s8, s8, 0x8000
	s_addc_u32 s9, s9, 0
	global_load_dwordx4 v[168:171], v75, s[8:9]
	s_add_u32 s8, s8, 0x8000
	s_addc_u32 s9, s9, 0
	global_load_dwordx4 v[172:175], v75, s[8:9]
	s_add_u32 s6, s40, 0x2000000
	s_addc_u32 s7, s41, 0
	ds_read_b32 v226, v211
	ds_read_b32 v227, v211 offset:512
	ds_read_b32 v228, v211 offset:1024
	ds_read_b32 v229, v211 offset:1536
	ds_read_b32 v230, v211 offset:2048
	ds_read_b32 v231, v211 offset:2560
	ds_read_b32 v232, v211 offset:3072
	ds_read_b32 v233, v211 offset:3584
	ds_read_b32 v234, v211 offset:4096
	ds_read_b32 v235, v211 offset:4608
	ds_read_b32 v236, v211 offset:5120
	ds_read_b32 v237, v211 offset:5632
	ds_read_b32 v238, v211 offset:6144
	ds_read_b32 v239, v211 offset:6656
	ds_read_b32 v240, v211 offset:7168
	ds_read_b32 v241, v211 offset:7680
	s_waitcnt lgkmcnt(0)
	v_max_f32_e32 v226, v226, v226
	v_max_f32_e32 v227, v227, v227
	v_max_f32_e32 v228, v228, v228
	v_max_f32_e32 v229, v229, v229
	v_max_f32_e32 v230, v230, v230
	v_max_f32_e32 v231, v231, v231
	v_max_f32_e32 v232, v232, v232
	v_max_f32_e32 v233, v233, v233
	v_max_f32_e32 v234, v234, v234
	v_max_f32_e32 v235, v235, v235
	v_max_f32_e32 v236, v236, v236
	v_max_f32_e32 v237, v237, v237
	v_max_f32_e32 v238, v238, v238
	v_max_f32_e32 v239, v239, v239
	v_max_f32_e32 v240, v240, v240
	v_max_f32_e32 v241, v241, v241
	v_med3_f32 v226, v226, s62, v95
	v_med3_f32 v227, v227, s62, v95
	v_med3_f32 v228, v228, s62, v95
	v_med3_f32 v229, v229, s62, v95
	v_med3_f32 v230, v230, s62, v95
	v_med3_f32 v231, v231, s62, v95
	v_med3_f32 v232, v232, s62, v95
	v_med3_f32 v233, v233, s62, v95
	v_med3_f32 v234, v234, s62, v95
	v_med3_f32 v235, v235, s62, v95
	v_med3_f32 v236, v236, s62, v95
	v_med3_f32 v237, v237, s62, v95
	v_med3_f32 v238, v238, s62, v95
	v_med3_f32 v239, v239, s62, v95
	v_med3_f32 v240, v240, s62, v95
	v_med3_f32 v241, v241, s62, v95
	v_mov_b32_e32 v242, 0
	v_mov_b32_e32 v243, 0
	v_mov_b32_e32 v244, 0
	v_mov_b32_e32 v245, 0
	v_cvt_pk_fp8_f32 v242, v226, v227
	v_cvt_pk_fp8_f32 v243, v230, v231
	v_cvt_pk_fp8_f32 v244, v234, v235
	v_cvt_pk_fp8_f32 v245, v238, v239
	v_cvt_pk_fp8_f32 v242, v228, v229 op_sel:[0,0,1]
	v_cvt_pk_fp8_f32 v243, v232, v233 op_sel:[0,0,1]
	v_cvt_pk_fp8_f32 v244, v236, v237 op_sel:[0,0,1]
	v_cvt_pk_fp8_f32 v245, v240, v241 op_sel:[0,0,1]
	s_nop 0
	global_store_dwordx4 v79, v[242:245], s[6:7]
	ds_read_b32 v226, v213
	ds_read_b32 v227, v213 offset:512
	ds_read_b32 v228, v213 offset:1024
	ds_read_b32 v229, v213 offset:1536
	ds_read_b32 v230, v213 offset:2048
	ds_read_b32 v231, v213 offset:2560
	ds_read_b32 v232, v213 offset:3072
	ds_read_b32 v233, v213 offset:3584
	ds_read_b32 v234, v213 offset:4096
	ds_read_b32 v235, v213 offset:4608
	ds_read_b32 v236, v213 offset:5120
	ds_read_b32 v237, v213 offset:5632
	ds_read_b32 v238, v213 offset:6144
	ds_read_b32 v239, v213 offset:6656
	ds_read_b32 v240, v213 offset:7168
	ds_read_b32 v241, v213 offset:7680
	s_waitcnt lgkmcnt(0)
	v_max_f32_e32 v226, v226, v226
	v_max_f32_e32 v227, v227, v227
	v_max_f32_e32 v228, v228, v228
	v_max_f32_e32 v229, v229, v229
	v_max_f32_e32 v230, v230, v230
	v_max_f32_e32 v231, v231, v231
	v_max_f32_e32 v232, v232, v232
	v_max_f32_e32 v233, v233, v233
	v_max_f32_e32 v234, v234, v234
	v_max_f32_e32 v235, v235, v235
	v_max_f32_e32 v236, v236, v236
	v_max_f32_e32 v237, v237, v237
	v_max_f32_e32 v238, v238, v238
	v_max_f32_e32 v239, v239, v239
	v_max_f32_e32 v240, v240, v240
	v_max_f32_e32 v241, v241, v241
	v_med3_f32 v226, v226, s62, v95
	v_med3_f32 v227, v227, s62, v95
	v_med3_f32 v228, v228, s62, v95
	v_med3_f32 v229, v229, s62, v95
	v_med3_f32 v230, v230, s62, v95
	v_med3_f32 v231, v231, s62, v95
	v_med3_f32 v232, v232, s62, v95
	v_med3_f32 v233, v233, s62, v95
	v_med3_f32 v234, v234, s62, v95
	v_med3_f32 v235, v235, s62, v95
	v_med3_f32 v236, v236, s62, v95
	v_med3_f32 v237, v237, s62, v95
	v_med3_f32 v238, v238, s62, v95
	v_med3_f32 v239, v239, s62, v95
	v_med3_f32 v240, v240, s62, v95
	v_med3_f32 v241, v241, s62, v95
	v_mov_b32_e32 v242, 0
	v_mov_b32_e32 v243, 0
	v_mov_b32_e32 v244, 0
	v_mov_b32_e32 v245, 0
	v_cvt_pk_fp8_f32 v242, v226, v227
	v_cvt_pk_fp8_f32 v243, v230, v231
	v_cvt_pk_fp8_f32 v244, v234, v235
	v_cvt_pk_fp8_f32 v245, v238, v239
	v_cvt_pk_fp8_f32 v242, v228, v229 op_sel:[0,0,1]
	v_cvt_pk_fp8_f32 v243, v232, v233 op_sel:[0,0,1]
	v_cvt_pk_fp8_f32 v244, v236, v237 op_sel:[0,0,1]
	v_cvt_pk_fp8_f32 v245, v240, v241 op_sel:[0,0,1]
	s_nop 0
	global_store_dwordx4 v80, v[242:245], s[6:7]
	s_waitcnt vmcnt(12)
	v_mul_f32_e32 v176, 0x43000000, v176
	v_mul_f32_e32 v177, 0x43000000, v177
	v_mul_f32_e32 v178, 0x43000000, v178
	v_mul_f32_e32 v179, 0x43000000, v179
	ds_write_b128 v210, v[176:179]
	v_mul_f32_e32 v180, 0x43000000, v180
	v_mul_f32_e32 v181, 0x43000000, v181
	v_mul_f32_e32 v182, 0x43000000, v182
	v_mul_f32_e32 v183, 0x43000000, v183
	ds_write_b128 v210, v[180:183] offset:1024
	v_mul_f32_e32 v184, 0x43000000, v184
	v_mul_f32_e32 v185, 0x43000000, v185
	v_mul_f32_e32 v186, 0x43000000, v186
	v_mul_f32_e32 v187, 0x43000000, v187
	ds_write_b128 v210, v[184:187] offset:2048
	v_mul_f32_e32 v188, 0x43000000, v188
	v_mul_f32_e32 v189, 0x43000000, v189
	v_mul_f32_e32 v190, 0x43000000, v190
	v_mul_f32_e32 v191, 0x43000000, v191
	ds_write_b128 v210, v[188:191] offset:3072
	v_mul_f32_e32 v192, 0x43000000, v192
	v_mul_f32_e32 v193, 0x43000000, v193
	v_mul_f32_e32 v194, 0x43000000, v194
	v_mul_f32_e32 v195, 0x43000000, v195
	ds_write_b128 v210, v[192:195] offset:4096
	v_mul_f32_e32 v196, 0x43000000, v196
	v_mul_f32_e32 v197, 0x43000000, v197
	v_mul_f32_e32 v198, 0x43000000, v198
	v_mul_f32_e32 v199, 0x43000000, v199
	ds_write_b128 v210, v[196:199] offset:5120
	v_mul_f32_e32 v200, 0x43000000, v200
	v_mul_f32_e32 v201, 0x43000000, v201
	v_mul_f32_e32 v202, 0x43000000, v202
	v_mul_f32_e32 v203, 0x43000000, v203
	ds_write_b128 v210, v[200:203] offset:6144
	v_mul_f32_e32 v204, 0x43000000, v204
	v_mul_f32_e32 v205, 0x43000000, v205
	v_mul_f32_e32 v206, 0x43000000, v206
	v_mul_f32_e32 v207, 0x43000000, v207
	ds_write_b128 v210, v[204:207] offset:7168
	s_waitcnt lgkmcnt(0)
	s_barrier
; #define GAS __attribute__((address_space(1)))
; #define LAS __attribute__((address_space(3)))
; #define LDS_WAIT() asm volatile("s_waitcnt lgkmcnt(0)" ::: "memory")
; __device__ __forceinline__ unsigned pk4_fp8(float a, float b, float c, float d) {
;     a = fminf(fmaxf(a, -448.f), 448.f); b = fminf(fmaxf(b, -448.f), 448.f); c = fminf(fmaxf(c, -448.f), 448.f); d = fminf(fmaxf(d, -448.f), 448.f);
;     int w = __builtin_amdgcn_cvt_pk_fp8_f32(a, b, 0, false); w = __builtin_amdgcn_cvt_pk_fp8_f32(c, d, w, true); return (unsigned)w; }
;     ...
; #pragma unroll
;     for (int i = 0; i < 32; ++i) v[i] = sc >= 0 ? W[(size_t)(k0 + 2 * i + (lane >> 5)) * Nsrc + sc] : 0.f;
; #pragma unroll
;     for (int i = 0; i < 32; ++i) { const int k = k0 + 2 * i + (lane >> 5); float x = v[i] * wscale; if (KS) x *= (k < ksplit ? ksA[k] : ksB[k - ksplit]); scr[(2 * i + (lane >> 5)) * 33 + (lane & 31)] = x; }
;     LDS_WAIT(); asm volatile("" ::: "memory");
;     const int c = lane & 7;
; #pragma unroll
;     for (int j = 0; j < 4; ++j) { const int n = (lane >> 3) + 8 * j; const LAS float* s = scr + (8 * c) * 33 + n;
;         const unsigned long long o = (unsigned long long)pg8::pk4_fp8(s[0 * 33], s[1 * 33], s[2 * 33], s[3 * 33]) | ((unsigned long long)pg8::pk4_fp8(s[4 * 33], s[5 * 33], s[6 * 33], s[7 * 33]) << 32);
;         *(GAS unsigned long long*)(WT + (size_t)(n0 + n) * K + k0 + 8 * c) = o; }
	s_add_u32 s8, s38, 0x4001000
	s_addc_u32 s9, s39, 0
	global_load_dwordx4 v[176:179], v75, s[8:9]
	s_add_u32 s8, s8, 0x8000
	s_addc_u32 s9, s9, 0
	global_load_dwordx4 v[180:183], v75, s[8:9]
	s_add_u32 s8, s8, 0x8000
	s_addc_u32 s9, s9, 0
	global_load_dwordx4 v[184:187], v75, s[8:9]
	s_add_u32 s8, s8, 0x8000
	s_addc_u32 s9, s9, 0
	global_load_dwordx4 v[188:191], v75, s[8:9]
	s_add_u32 s8, s8, 0x8000
	s_addc_u32 s9, s9, 0
	global_load_dwordx4 v[192:195], v75, s[8:9]
	s_add_u32 s8, s8, 0x8000
	s_addc_u32 s9, s9, 0
	global_load_dwordx4 v[196:199], v75, s[8:9]
	s_add_u32 s8, s8, 0x8000
	s_addc_u32 s9, s9, 0
	global_load_dwordx4 v[200:203], v75, s[8:9]
	s_add_u32 s8, s8, 0x8000
	s_addc_u32 s9, s9, 0
	global_load_dwordx4 v[204:207], v75, s[8:9]
	s_add_u32 s6, s40, 0x3000000
	s_addc_u32 s7, s41, 0
	ds_read_b32 v226, v212
	ds_read_b32 v227, v212 offset:512
	ds_read_b32 v228, v212 offset:1024
	ds_read_b32 v229, v212 offset:1536
	ds_read_b32 v230, v212 offset:2048
	ds_read_b32 v231, v212 offset:2560
	ds_read_b32 v232, v212 offset:3072
	ds_read_b32 v233, v212 offset:3584
	ds_read_b32 v234, v212 offset:4096
	ds_read_b32 v235, v212 offset:4608
	ds_read_b32 v236, v212 offset:5120
	ds_read_b32 v237, v212 offset:5632
	ds_read_b32 v238, v212 offset:6144
	ds_read_b32 v239, v212 offset:6656
	ds_read_b32 v240, v212 offset:7168
	ds_read_b32 v241, v212 offset:7680
	s_waitcnt lgkmcnt(0)
	v_max_f32_e32 v226, v226, v226
	v_max_f32_e32 v227, v227, v227
	v_max_f32_e32 v228, v228, v228
	v_max_f32_e32 v229, v229, v229
	v_max_f32_e32 v230, v230, v230
	v_max_f32_e32 v231, v231, v231
	v_max_f32_e32 v232, v232, v232
	v_max_f32_e32 v233, v233, v233
	v_max_f32_e32 v234, v234, v234
	v_max_f32_e32 v235, v235, v235
	v_max_f32_e32 v236, v236, v236
	v_max_f32_e32 v237, v237, v237
	v_max_f32_e32 v238, v238, v238
	v_max_f32_e32 v239, v239, v239
	v_max_f32_e32 v240, v240, v240
	v_max_f32_e32 v241, v241, v241
	v_med3_f32 v226, v226, s62, v95
	v_med3_f32 v227, v227, s62, v95
	v_med3_f32 v228, v228, s62, v95
	v_med3_f32 v229, v229, s62, v95
	v_med3_f32 v230, v230, s62, v95
	v_med3_f32 v231, v231, s62, v95
	v_med3_f32 v232, v232, s62, v95
	v_med3_f32 v233, v233, s62, v95
	v_med3_f32 v234, v234, s62, v95
	v_med3_f32 v235, v235, s62, v95
	v_med3_f32 v236, v236, s62, v95
	v_med3_f32 v237, v237, s62, v95
	v_med3_f32 v238, v238, s62, v95
	v_med3_f32 v239, v239, s62, v95
	v_med3_f32 v240, v240, s62, v95
	v_med3_f32 v241, v241, s62, v95
	v_mov_b32_e32 v242, 0
	v_mov_b32_e32 v243, 0
	v_mov_b32_e32 v244, 0
	v_mov_b32_e32 v245, 0
	v_cvt_pk_fp8_f32 v242, v226, v227
	v_cvt_pk_fp8_f32 v243, v230, v231
	v_cvt_pk_fp8_f32 v244, v234, v235
	v_cvt_pk_fp8_f32 v245, v238, v239
	v_cvt_pk_fp8_f32 v242, v228, v229 op_sel:[0,0,1]
	v_cvt_pk_fp8_f32 v243, v232, v233 op_sel:[0,0,1]
	v_cvt_pk_fp8_f32 v244, v236, v237 op_sel:[0,0,1]
	v_cvt_pk_fp8_f32 v245, v240, v241 op_sel:[0,0,1]
	s_nop 0
	global_store_dwordx4 v79, v[242:245], s[6:7]
	ds_read_b32 v226, v214
	ds_read_b32 v227, v214 offset:512
	ds_read_b32 v228, v214 offset:1024
	ds_read_b32 v229, v214 offset:1536
	ds_read_b32 v230, v214 offset:2048
	ds_read_b32 v231, v214 offset:2560
	ds_read_b32 v232, v214 offset:3072
	ds_read_b32 v233, v214 offset:3584
	ds_read_b32 v234, v214 offset:4096
	ds_read_b32 v235, v214 offset:4608
	ds_read_b32 v236, v214 offset:5120
	ds_read_b32 v237, v214 offset:5632
	ds_read_b32 v238, v214 offset:6144
	ds_read_b32 v239, v214 offset:6656
	ds_read_b32 v240, v214 offset:7168
	ds_read_b32 v241, v214 offset:7680
	s_waitcnt lgkmcnt(0)
	v_max_f32_e32 v226, v226, v226
	v_max_f32_e32 v227, v227, v227
	v_max_f32_e32 v228, v228, v228
	v_max_f32_e32 v229, v229, v229
	v_max_f32_e32 v230, v230, v230
	v_max_f32_e32 v231, v231, v231
	v_max_f32_e32 v232, v232, v232
	v_max_f32_e32 v233, v233, v233
	v_max_f32_e32 v234, v234, v234
	v_max_f32_e32 v235, v235, v235
	v_max_f32_e32 v236, v236, v236
	v_max_f32_e32 v237, v237, v237
	v_max_f32_e32 v238, v238, v238
	v_max_f32_e32 v239, v239, v239
	v_max_f32_e32 v240, v240, v240
	v_max_f32_e32 v241, v241, v241
	v_med3_f32 v226, v226, s62, v95
	v_med3_f32 v227, v227, s62, v95
	v_med3_f32 v228, v228, s62, v95
	v_med3_f32 v229, v229, s62, v95
	v_med3_f32 v230, v230, s62, v95
	v_med3_f32 v231, v231, s62, v95
	v_med3_f32 v232, v232, s62, v95
	v_med3_f32 v233, v233, s62, v95
	v_med3_f32 v234, v234, s62, v95
	v_med3_f32 v235, v235, s62, v95
	v_med3_f32 v236, v236, s62, v95
	v_med3_f32 v237, v237, s62, v95
	v_med3_f32 v238, v238, s62, v95
	v_med3_f32 v239, v239, s62, v95
	v_med3_f32 v240, v240, s62, v95
	v_med3_f32 v241, v241, s62, v95
	v_mov_b32_e32 v242, 0
	v_mov_b32_e32 v243, 0
	v_mov_b32_e32 v244, 0
	v_mov_b32_e32 v245, 0
	v_cvt_pk_fp8_f32 v242, v226, v227
	v_cvt_pk_fp8_f32 v243, v230, v231
	v_cvt_pk_fp8_f32 v244, v234, v235
	v_cvt_pk_fp8_f32 v245, v238, v239
	v_cvt_pk_fp8_f32 v242, v228, v229 op_sel:[0,0,1]
	v_cvt_pk_fp8_f32 v243, v232, v233 op_sel:[0,0,1]
	v_cvt_pk_fp8_f32 v244, v236, v237 op_sel:[0,0,1]
	v_cvt_pk_fp8_f32 v245, v240, v241 op_sel:[0,0,1]
	s_nop 0
	global_store_dwordx4 v80, v[242:245], s[6:7]
	s_waitcnt vmcnt(12)
	v_mul_f32_e32 v144, 0x43000000, v144
	v_mul_f32_e32 v145, 0x43000000, v145
	v_mul_f32_e32 v146, 0x43000000, v146
	v_mul_f32_e32 v147, 0x43000000, v147
	ds_write_b128 v209, v[144:147]
	v_mul_f32_e32 v148, 0x43000000, v148
	v_mul_f32_e32 v149, 0x43000000, v149
	v_mul_f32_e32 v150, 0x43000000, v150
	v_mul_f32_e32 v151, 0x43000000, v151
	ds_write_b128 v209, v[148:151] offset:1024
	v_mul_f32_e32 v152, 0x43000000, v152
	v_mul_f32_e32 v153, 0x43000000, v153
	v_mul_f32_e32 v154, 0x43000000, v154
	v_mul_f32_e32 v155, 0x43000000, v155
	ds_write_b128 v209, v[152:155] offset:2048
	v_mul_f32_e32 v156, 0x43000000, v156
	v_mul_f32_e32 v157, 0x43000000, v157
	v_mul_f32_e32 v158, 0x43000000, v158
	v_mul_f32_e32 v159, 0x43000000, v159
	ds_write_b128 v209, v[156:159] offset:3072
	v_mul_f32_e32 v160, 0x43000000, v160
	v_mul_f32_e32 v161, 0x43000000, v161
	v_mul_f32_e32 v162, 0x43000000, v162
	v_mul_f32_e32 v163, 0x43000000, v163
	ds_write_b128 v209, v[160:163] offset:4096
	v_mul_f32_e32 v164, 0x43000000, v164
	v_mul_f32_e32 v165, 0x43000000, v165
	v_mul_f32_e32 v166, 0x43000000, v166
	v_mul_f32_e32 v167, 0x43000000, v167
	ds_write_b128 v209, v[164:167] offset:5120
	v_mul_f32_e32 v168, 0x43000000, v168
	v_mul_f32_e32 v169, 0x43000000, v169
	v_mul_f32_e32 v170, 0x43000000, v170
	v_mul_f32_e32 v171, 0x43000000, v171
	ds_write_b128 v209, v[168:171] offset:6144
	v_mul_f32_e32 v172, 0x43000000, v172
	v_mul_f32_e32 v173, 0x43000000, v173
	v_mul_f32_e32 v174, 0x43000000, v174
	v_mul_f32_e32 v175, 0x43000000, v175
	ds_write_b128 v209, v[172:175] offset:7168
	s_waitcnt lgkmcnt(0)
	s_barrier
; #define GAS __attribute__((address_space(1)))
; #define LAS __attribute__((address_space(3)))
; #define LDS_WAIT() asm volatile("s_waitcnt lgkmcnt(0)" ::: "memory")
; __device__ __forceinline__ unsigned pk4_fp8(float a, float b, float c, float d) {
;     a = fminf(fmaxf(a, -448.f), 448.f); b = fminf(fmaxf(b, -448.f), 448.f); c = fminf(fmaxf(c, -448.f), 448.f); d = fminf(fmaxf(d, -448.f), 448.f);
;     int w = __builtin_amdgcn_cvt_pk_fp8_f32(a, b, 0, false); w = __builtin_amdgcn_cvt_pk_fp8_f32(c, d, w, true); return (unsigned)w; }
;     ...
; #pragma unroll
;     for (int i = 0; i < 32; ++i) v[i] = sc >= 0 ? W[(size_t)(k0 + 2 * i + (lane >> 5)) * Nsrc + sc] : 0.f;
; #pragma unroll
;     for (int i = 0; i < 32; ++i) { const int k = k0 + 2 * i + (lane >> 5); float x = v[i] * wscale; if (KS) x *= (k < ksplit ? ksA[k] : ksB[k - ksplit]); scr[(2 * i + (lane >> 5)) * 33 + (lane & 31)] = x; }
;     LDS_WAIT(); asm volatile("" ::: "memory");
;     const int c = lane & 7;
; #pragma unroll
;     for (int j = 0; j < 4; ++j) { const int n = (lane >> 3) + 8 * j; const LAS float* s = scr + (8 * c) * 33 + n;
;         const unsigned long long o = (unsigned long long)pg8::pk4_fp8(s[0 * 33], s[1 * 33], s[2 * 33], s[3 * 33]) | ((unsigned long long)pg8::pk4_fp8(s[4 * 33], s[5 * 33], s[6 * 33], s[7 * 33]) << 32);
;         *(GAS unsigned long long*)(WT + (size_t)(n0 + n) * K + k0 + 8 * c) = o; }
	s_add_u32 s8, s38, 0x4002000
	s_addc_u32 s9, s39, 0
	global_load_dwordx4 v[144:147], v75, s[8:9]
	s_add_u32 s8, s8, 0x8000
	s_addc_u32 s9, s9, 0
	global_load_dwordx4 v[148:151], v75, s[8:9]
	s_add_u32 s8, s8, 0x8000
	s_addc_u32 s9, s9, 0
	global_load_dwordx4 v[152:155], v75, s[8:9]
	s_add_u32 s8, s8, 0x8000
	s_addc_u32 s9, s9, 0
	global_load_dwordx4 v[156:159], v75, s[8:9]
	s_add_u32 s8, s8, 0x8000
	s_addc_u32 s9, s9, 0
	global_load_dwordx4 v[160:163], v75, s[8:9]
	s_add_u32 s8, s8, 0x8000
	s_addc_u32 s9, s9, 0
	global_load_dwordx4 v[164:167], v75, s[8:9]
	s_add_u32 s8, s8, 0x8000
	s_addc_u32 s9, s9, 0
	global_load_dwordx4 v[168:171], v75, s[8:9]
	s_add_u32 s8, s8, 0x8000
	s_addc_u32 s9, s9, 0
	global_load_dwordx4 v[172:175], v75, s[8:9]
	s_add_u32 s6, s40, 0x1000
	s_addc_u32 s7, s41, 0
	ds_read_b32 v226, v211
	ds_read_b32 v227, v211 offset:512
	ds_read_b32 v228, v211 offset:1024
	ds_read_b32 v229, v211 offset:1536
	ds_read_b32 v230, v211 offset:2048
	ds_read_b32 v231, v211 offset:2560
	ds_read_b32 v232, v211 offset:3072
	ds_read_b32 v233, v211 offset:3584
	ds_read_b32 v234, v211 offset:4096
	ds_read_b32 v235, v211 offset:4608
	ds_read_b32 v236, v211 offset:5120
	ds_read_b32 v237, v211 offset:5632
	ds_read_b32 v238, v211 offset:6144
	ds_read_b32 v239, v211 offset:6656
	ds_read_b32 v240, v211 offset:7168
	ds_read_b32 v241, v211 offset:7680
	s_waitcnt lgkmcnt(0)
	v_max_f32_e32 v226, v226, v226
	v_max_f32_e32 v227, v227, v227
	v_max_f32_e32 v228, v228, v228
	v_max_f32_e32 v229, v229, v229
	v_max_f32_e32 v230, v230, v230
	v_max_f32_e32 v231, v231, v231
	v_max_f32_e32 v232, v232, v232
	v_max_f32_e32 v233, v233, v233
	v_max_f32_e32 v234, v234, v234
	v_max_f32_e32 v235, v235, v235
	v_max_f32_e32 v236, v236, v236
	v_max_f32_e32 v237, v237, v237
	v_max_f32_e32 v238, v238, v238
	v_max_f32_e32 v239, v239, v239
	v_max_f32_e32 v240, v240, v240
	v_max_f32_e32 v241, v241, v241
	v_med3_f32 v226, v226, s62, v95
	v_med3_f32 v227, v227, s62, v95
	v_med3_f32 v228, v228, s62, v95
	v_med3_f32 v229, v229, s62, v95
	v_med3_f32 v230, v230, s62, v95
	v_med3_f32 v231, v231, s62, v95
	v_med3_f32 v232, v232, s62, v95
	v_med3_f32 v233, v233, s62, v95
	v_med3_f32 v234, v234, s62, v95
	v_med3_f32 v235, v235, s62, v95
	v_med3_f32 v236, v236, s62, v95
	v_med3_f32 v237, v237, s62, v95
	v_med3_f32 v238, v238, s62, v95
	v_med3_f32 v239, v239, s62, v95
	v_med3_f32 v240, v240, s62, v95
	v_med3_f32 v241, v241, s62, v95
	v_mov_b32_e32 v242, 0
	v_mov_b32_e32 v243, 0
	v_mov_b32_e32 v244, 0
	v_mov_b32_e32 v245, 0
	v_cvt_pk_fp8_f32 v242, v226, v227
	v_cvt_pk_fp8_f32 v243, v230, v231
	v_cvt_pk_fp8_f32 v244, v234, v235
	v_cvt_pk_fp8_f32 v245, v238, v239
	v_cvt_pk_fp8_f32 v242, v228, v229 op_sel:[0,0,1]
	v_cvt_pk_fp8_f32 v243, v232, v233 op_sel:[0,0,1]
	v_cvt_pk_fp8_f32 v244, v236, v237 op_sel:[0,0,1]
	v_cvt_pk_fp8_f32 v245, v240, v241 op_sel:[0,0,1]
	s_nop 0
	global_store_dwordx4 v79, v[242:245], s[6:7]
	ds_read_b32 v226, v213
	ds_read_b32 v227, v213 offset:512
	ds_read_b32 v228, v213 offset:1024
	ds_read_b32 v229, v213 offset:1536
	ds_read_b32 v230, v213 offset:2048
	ds_read_b32 v231, v213 offset:2560
	ds_read_b32 v232, v213 offset:3072
	ds_read_b32 v233, v213 offset:3584
	ds_read_b32 v234, v213 offset:4096
	ds_read_b32 v235, v213 offset:4608
	ds_read_b32 v236, v213 offset:5120
	ds_read_b32 v237, v213 offset:5632
	ds_read_b32 v238, v213 offset:6144
	ds_read_b32 v239, v213 offset:6656
	ds_read_b32 v240, v213 offset:7168
	ds_read_b32 v241, v213 offset:7680
	s_waitcnt lgkmcnt(0)
	v_max_f32_e32 v226, v226, v226
	v_max_f32_e32 v227, v227, v227
	v_max_f32_e32 v228, v228, v228
	v_max_f32_e32 v229, v229, v229
	v_max_f32_e32 v230, v230, v230
	v_max_f32_e32 v231, v231, v231
	v_max_f32_e32 v232, v232, v232
	v_max_f32_e32 v233, v233, v233
	v_max_f32_e32 v234, v234, v234
	v_max_f32_e32 v235, v235, v235
	v_max_f32_e32 v236, v236, v236
	v_max_f32_e32 v237, v237, v237
	v_max_f32_e32 v238, v238, v238
	v_max_f32_e32 v239, v239, v239
	v_max_f32_e32 v240, v240, v240
	v_max_f32_e32 v241, v241, v241
	v_med3_f32 v226, v226, s62, v95
	v_med3_f32 v227, v227, s62, v95
	v_med3_f32 v228, v228, s62, v95
	v_med3_f32 v229, v229, s62, v95
	v_med3_f32 v230, v230, s62, v95
	v_med3_f32 v231, v231, s62, v95
	v_med3_f32 v232, v232, s62, v95
	v_med3_f32 v233, v233, s62, v95
	v_med3_f32 v234, v234, s62, v95
	v_med3_f32 v235, v235, s62, v95
	v_med3_f32 v236, v236, s62, v95
	v_med3_f32 v237, v237, s62, v95
	v_med3_f32 v238, v238, s62, v95
	v_med3_f32 v239, v239, s62, v95
	v_med3_f32 v240, v240, s62, v95
	v_med3_f32 v241, v241, s62, v95
	v_mov_b32_e32 v242, 0
	v_mov_b32_e32 v243, 0
	v_mov_b32_e32 v244, 0
	v_mov_b32_e32 v245, 0
	v_cvt_pk_fp8_f32 v242, v226, v227
	v_cvt_pk_fp8_f32 v243, v230, v231
	v_cvt_pk_fp8_f32 v244, v234, v235
	v_cvt_pk_fp8_f32 v245, v238, v239
	v_cvt_pk_fp8_f32 v242, v228, v229 op_sel:[0,0,1]
	v_cvt_pk_fp8_f32 v243, v232, v233 op_sel:[0,0,1]
	v_cvt_pk_fp8_f32 v244, v236, v237 op_sel:[0,0,1]
	v_cvt_pk_fp8_f32 v245, v240, v241 op_sel:[0,0,1]
	s_nop 0
	global_store_dwordx4 v80, v[242:245], s[6:7]
	s_waitcnt vmcnt(12)
	v_mul_f32_e32 v176, 0x43000000, v176
	v_mul_f32_e32 v177, 0x43000000, v177
	v_mul_f32_e32 v178, 0x43000000, v178
	v_mul_f32_e32 v179, 0x43000000, v179
	ds_write_b128 v210, v[176:179]
	v_mul_f32_e32 v180, 0x43000000, v180
	v_mul_f32_e32 v181, 0x43000000, v181
	v_mul_f32_e32 v182, 0x43000000, v182
	v_mul_f32_e32 v183, 0x43000000, v183
	ds_write_b128 v210, v[180:183] offset:1024
	v_mul_f32_e32 v184, 0x43000000, v184
	v_mul_f32_e32 v185, 0x43000000, v185
	v_mul_f32_e32 v186, 0x43000000, v186
	v_mul_f32_e32 v187, 0x43000000, v187
	ds_write_b128 v210, v[184:187] offset:2048
	v_mul_f32_e32 v188, 0x43000000, v188
	v_mul_f32_e32 v189, 0x43000000, v189
	v_mul_f32_e32 v190, 0x43000000, v190
	v_mul_f32_e32 v191, 0x43000000, v191
	ds_write_b128 v210, v[188:191] offset:3072
	v_mul_f32_e32 v192, 0x43000000, v192
	v_mul_f32_e32 v193, 0x43000000, v193
	v_mul_f32_e32 v194, 0x43000000, v194
	v_mul_f32_e32 v195, 0x43000000, v195
	ds_write_b128 v210, v[192:195] offset:4096
	v_mul_f32_e32 v196, 0x43000000, v196
	v_mul_f32_e32 v197, 0x43000000, v197
	v_mul_f32_e32 v198, 0x43000000, v198
	v_mul_f32_e32 v199, 0x43000000, v199
	ds_write_b128 v210, v[196:199] offset:5120
	v_mul_f32_e32 v200, 0x43000000, v200
	v_mul_f32_e32 v201, 0x43000000, v201
	v_mul_f32_e32 v202, 0x43000000, v202
	v_mul_f32_e32 v203, 0x43000000, v203
	ds_write_b128 v210, v[200:203] offset:6144
	v_mul_f32_e32 v204, 0x43000000, v204
	v_mul_f32_e32 v205, 0x43000000, v205
	v_mul_f32_e32 v206, 0x43000000, v206
	v_mul_f32_e32 v207, 0x43000000, v207
	ds_write_b128 v210, v[204:207] offset:7168
	s_waitcnt lgkmcnt(0)
	s_barrier
; #define GAS __attribute__((address_space(1)))
; #define LAS __attribute__((address_space(3)))
; #define LDS_WAIT() asm volatile("s_waitcnt lgkmcnt(0)" ::: "memory")
; __device__ __forceinline__ unsigned pk4_fp8(float a, float b, float c, float d) {
;     a = fminf(fmaxf(a, -448.f), 448.f); b = fminf(fmaxf(b, -448.f), 448.f); c = fminf(fmaxf(c, -448.f), 448.f); d = fminf(fmaxf(d, -448.f), 448.f);
;     int w = __builtin_amdgcn_cvt_pk_fp8_f32(a, b, 0, false); w = __builtin_amdgcn_cvt_pk_fp8_f32(c, d, w, true); return (unsigned)w; }
;     ...
; #pragma unroll
;     for (int i = 0; i < 32; ++i) v[i] = sc >= 0 ? W[(size_t)(k0 + 2 * i + (lane >> 5)) * Nsrc + sc] : 0.f;
; #pragma unroll
;     for (int i = 0; i < 32; ++i) { const int k = k0 + 2 * i + (lane >> 5); float x = v[i] * wscale; if (KS) x *= (k < ksplit ? ksA[k] : ksB[k - ksplit]); scr[(2 * i + (lane >> 5)) * 33 + (lane & 31)] = x; }
;     LDS_WAIT(); asm volatile("" ::: "memory");
;     const int c = lane & 7;
; #pragma unroll
;     for (int j = 0; j < 4; ++j) { const int n = (lane >> 3) + 8 * j; const LAS float* s = scr + (8 * c) * 33 + n;
;         const unsigned long long o = (unsigned long long)pg8::pk4_fp8(s[0 * 33], s[1 * 33], s[2 * 33], s[3 * 33]) | ((unsigned long long)pg8::pk4_fp8(s[4 * 33], s[5 * 33], s[6 * 33], s[7 * 33]) << 32);
;         *(GAS unsigned long long*)(WT + (size_t)(n0 + n) * K + k0 + 8 * c) = o; }
	s_add_u32 s8, s38, 0x4003000
	s_addc_u32 s9, s39, 0
	global_load_dwordx4 v[176:179], v75, s[8:9]
	s_add_u32 s8, s8, 0x8000
	s_addc_u32 s9, s9, 0
	global_load_dwordx4 v[180:183], v75, s[8:9]
	s_add_u32 s8, s8, 0x8000
	s_addc_u32 s9, s9, 0
	global_load_dwordx4 v[184:187], v75, s[8:9]
	s_add_u32 s8, s8, 0x8000
	s_addc_u32 s9, s9, 0
	global_load_dwordx4 v[188:191], v75, s[8:9]
	s_add_u32 s8, s8, 0x8000
	s_addc_u32 s9, s9, 0
	global_load_dwordx4 v[192:195], v75, s[8:9]
	s_add_u32 s8, s8, 0x8000
	s_addc_u32 s9, s9, 0
	global_load_dwordx4 v[196:199], v75, s[8:9]
	s_add_u32 s8, s8, 0x8000
	s_addc_u32 s9, s9, 0
	global_load_dwordx4 v[200:203], v75, s[8:9]
	s_add_u32 s8, s8, 0x8000
	s_addc_u32 s9, s9, 0
	global_load_dwordx4 v[204:207], v75, s[8:9]
	s_add_u32 s6, s40, 0x1001000
	s_addc_u32 s7, s41, 0
	ds_read_b32 v226, v212
	ds_read_b32 v227, v212 offset:512
	ds_read_b32 v228, v212 offset:1024
	ds_read_b32 v229, v212 offset:1536
	ds_read_b32 v230, v212 offset:2048
	ds_read_b32 v231, v212 offset:2560
	ds_read_b32 v232, v212 offset:3072
	ds_read_b32 v233, v212 offset:3584
	ds_read_b32 v234, v212 offset:4096
	ds_read_b32 v235, v212 offset:4608
	ds_read_b32 v236, v212 offset:5120
	ds_read_b32 v237, v212 offset:5632
	ds_read_b32 v238, v212 offset:6144
	ds_read_b32 v239, v212 offset:6656
	ds_read_b32 v240, v212 offset:7168
	ds_read_b32 v241, v212 offset:7680
	s_waitcnt lgkmcnt(0)
	v_max_f32_e32 v226, v226, v226
	v_max_f32_e32 v227, v227, v227
	v_max_f32_e32 v228, v228, v228
	v_max_f32_e32 v229, v229, v229
	v_max_f32_e32 v230, v230, v230
	v_max_f32_e32 v231, v231, v231
	v_max_f32_e32 v232, v232, v232
	v_max_f32_e32 v233, v233, v233
	v_max_f32_e32 v234, v234, v234
	v_max_f32_e32 v235, v235, v235
	v_max_f32_e32 v236, v236, v236
	v_max_f32_e32 v237, v237, v237
	v_max_f32_e32 v238, v238, v238
	v_max_f32_e32 v239, v239, v239
	v_max_f32_e32 v240, v240, v240
	v_max_f32_e32 v241, v241, v241
	v_med3_f32 v226, v226, s62, v95
	v_med3_f32 v227, v227, s62, v95
	v_med3_f32 v228, v228, s62, v95
	v_med3_f32 v229, v229, s62, v95
	v_med3_f32 v230, v230, s62, v95
	v_med3_f32 v231, v231, s62, v95
	v_med3_f32 v232, v232, s62, v95
	v_med3_f32 v233, v233, s62, v95
	v_med3_f32 v234, v234, s62, v95
	v_med3_f32 v235, v235, s62, v95
	v_med3_f32 v236, v236, s62, v95
	v_med3_f32 v237, v237, s62, v95
	v_med3_f32 v238, v238, s62, v95
	v_med3_f32 v239, v239, s62, v95
	v_med3_f32 v240, v240, s62, v95
	v_med3_f32 v241, v241, s62, v95
	v_mov_b32_e32 v242, 0
	v_mov_b32_e32 v243, 0
	v_mov_b32_e32 v244, 0
	v_mov_b32_e32 v245, 0
	v_cvt_pk_fp8_f32 v242, v226, v227
	v_cvt_pk_fp8_f32 v243, v230, v231
	v_cvt_pk_fp8_f32 v244, v234, v235
	v_cvt_pk_fp8_f32 v245, v238, v239
	v_cvt_pk_fp8_f32 v242, v228, v229 op_sel:[0,0,1]
	v_cvt_pk_fp8_f32 v243, v232, v233 op_sel:[0,0,1]
	v_cvt_pk_fp8_f32 v244, v236, v237 op_sel:[0,0,1]
	v_cvt_pk_fp8_f32 v245, v240, v241 op_sel:[0,0,1]
	s_nop 0
	global_store_dwordx4 v79, v[242:245], s[6:7]
	ds_read_b32 v226, v214
	ds_read_b32 v227, v214 offset:512
	ds_read_b32 v228, v214 offset:1024
	ds_read_b32 v229, v214 offset:1536
	ds_read_b32 v230, v214 offset:2048
	ds_read_b32 v231, v214 offset:2560
	ds_read_b32 v232, v214 offset:3072
	ds_read_b32 v233, v214 offset:3584
	ds_read_b32 v234, v214 offset:4096
	ds_read_b32 v235, v214 offset:4608
	ds_read_b32 v236, v214 offset:5120
	ds_read_b32 v237, v214 offset:5632
	ds_read_b32 v238, v214 offset:6144
	ds_read_b32 v239, v214 offset:6656
	ds_read_b32 v240, v214 offset:7168
	ds_read_b32 v241, v214 offset:7680
	s_waitcnt lgkmcnt(0)
	v_max_f32_e32 v226, v226, v226
	v_max_f32_e32 v227, v227, v227
	v_max_f32_e32 v228, v228, v228
	v_max_f32_e32 v229, v229, v229
	v_max_f32_e32 v230, v230, v230
	v_max_f32_e32 v231, v231, v231
	v_max_f32_e32 v232, v232, v232
	v_max_f32_e32 v233, v233, v233
	v_max_f32_e32 v234, v234, v234
	v_max_f32_e32 v235, v235, v235
	v_max_f32_e32 v236, v236, v236
	v_max_f32_e32 v237, v237, v237
	v_max_f32_e32 v238, v238, v238
	v_max_f32_e32 v239, v239, v239
	v_max_f32_e32 v240, v240, v240
	v_max_f32_e32 v241, v241, v241
	v_med3_f32 v226, v226, s62, v95
	v_med3_f32 v227, v227, s62, v95
	v_med3_f32 v228, v228, s62, v95
	v_med3_f32 v229, v229, s62, v95
	v_med3_f32 v230, v230, s62, v95
	v_med3_f32 v231, v231, s62, v95
	v_med3_f32 v232, v232, s62, v95
	v_med3_f32 v233, v233, s62, v95
	v_med3_f32 v234, v234, s62, v95
	v_med3_f32 v235, v235, s62, v95
	v_med3_f32 v236, v236, s62, v95
	v_med3_f32 v237, v237, s62, v95
	v_med3_f32 v238, v238, s62, v95
	v_med3_f32 v239, v239, s62, v95
	v_med3_f32 v240, v240, s62, v95
	v_med3_f32 v241, v241, s62, v95
	v_mov_b32_e32 v242, 0
	v_mov_b32_e32 v243, 0
	v_mov_b32_e32 v244, 0
	v_mov_b32_e32 v245, 0
	v_cvt_pk_fp8_f32 v242, v226, v227
	v_cvt_pk_fp8_f32 v243, v230, v231
	v_cvt_pk_fp8_f32 v244, v234, v235
	v_cvt_pk_fp8_f32 v245, v238, v239
	v_cvt_pk_fp8_f32 v242, v228, v229 op_sel:[0,0,1]
	v_cvt_pk_fp8_f32 v243, v232, v233 op_sel:[0,0,1]
	v_cvt_pk_fp8_f32 v244, v236, v237 op_sel:[0,0,1]
	v_cvt_pk_fp8_f32 v245, v240, v241 op_sel:[0,0,1]
	s_nop 0
	global_store_dwordx4 v80, v[242:245], s[6:7]
	s_waitcnt vmcnt(12)
	v_mul_f32_e32 v144, 0x43000000, v144
	v_mul_f32_e32 v145, 0x43000000, v145
	v_mul_f32_e32 v146, 0x43000000, v146
	v_mul_f32_e32 v147, 0x43000000, v147
	ds_write_b128 v209, v[144:147]
	v_mul_f32_e32 v148, 0x43000000, v148
	v_mul_f32_e32 v149, 0x43000000, v149
	v_mul_f32_e32 v150, 0x43000000, v150
	v_mul_f32_e32 v151, 0x43000000, v151
	ds_write_b128 v209, v[148:151] offset:1024
	v_mul_f32_e32 v152, 0x43000000, v152
	v_mul_f32_e32 v153, 0x43000000, v153
	v_mul_f32_e32 v154, 0x43000000, v154
	v_mul_f32_e32 v155, 0x43000000, v155
	ds_write_b128 v209, v[152:155] offset:2048
	v_mul_f32_e32 v156, 0x43000000, v156
	v_mul_f32_e32 v157, 0x43000000, v157
	v_mul_f32_e32 v158, 0x43000000, v158
	v_mul_f32_e32 v159, 0x43000000, v159
	ds_write_b128 v209, v[156:159] offset:3072
	v_mul_f32_e32 v160, 0x43000000, v160
	v_mul_f32_e32 v161, 0x43000000, v161
	v_mul_f32_e32 v162, 0x43000000, v162
	v_mul_f32_e32 v163, 0x43000000, v163
	ds_write_b128 v209, v[160:163] offset:4096
	v_mul_f32_e32 v164, 0x43000000, v164
	v_mul_f32_e32 v165, 0x43000000, v165
	v_mul_f32_e32 v166, 0x43000000, v166
	v_mul_f32_e32 v167, 0x43000000, v167
	ds_write_b128 v209, v[164:167] offset:5120
	v_mul_f32_e32 v168, 0x43000000, v168
	v_mul_f32_e32 v169, 0x43000000, v169
	v_mul_f32_e32 v170, 0x43000000, v170
	v_mul_f32_e32 v171, 0x43000000, v171
	ds_write_b128 v209, v[168:171] offset:6144
	v_mul_f32_e32 v172, 0x43000000, v172
	v_mul_f32_e32 v173, 0x43000000, v173
	v_mul_f32_e32 v174, 0x43000000, v174
	v_mul_f32_e32 v175, 0x43000000, v175
	ds_write_b128 v209, v[172:175] offset:7168
	s_waitcnt lgkmcnt(0)
	s_barrier
; #define GAS __attribute__((address_space(1)))
; #define LAS __attribute__((address_space(3)))
; #define LDS_WAIT() asm volatile("s_waitcnt lgkmcnt(0)" ::: "memory")
; __device__ __forceinline__ unsigned pk4_fp8(float a, float b, float c, float d) {
;     a = fminf(fmaxf(a, -448.f), 448.f); b = fminf(fmaxf(b, -448.f), 448.f); c = fminf(fmaxf(c, -448.f), 448.f); d = fminf(fmaxf(d, -448.f), 448.f);
;     int w = __builtin_amdgcn_cvt_pk_fp8_f32(a, b, 0, false); w = __builtin_amdgcn_cvt_pk_fp8_f32(c, d, w, true); return (unsigned)w; }
;     ...
; #pragma unroll
;     for (int i = 0; i < 32; ++i) v[i] = sc >= 0 ? W[(size_t)(k0 + 2 * i + (lane >> 5)) * Nsrc + sc] : 0.f;
; #pragma unroll
;     for (int i = 0; i < 32; ++i) { const int k = k0 + 2 * i + (lane >> 5); float x = v[i] * wscale; if (KS) x *= (k < ksplit ? ksA[k] : ksB[k - ksplit]); scr[(2 * i + (lane >> 5)) * 33 + (lane & 31)] = x; }
;     LDS_WAIT(); asm volatile("" ::: "memory");
;     const int c = lane & 7;
; #pragma unroll
;     for (int j = 0; j < 4; ++j) { const int n = (lane >> 3) + 8 * j; const LAS float* s = scr + (8 * c) * 33 + n;
;         const unsigned long long o = (unsigned long long)pg8::pk4_fp8(s[0 * 33], s[1 * 33], s[2 * 33], s[3 * 33]) | ((unsigned long long)pg8::pk4_fp8(s[4 * 33], s[5 * 33], s[6 * 33], s[7 * 33]) << 32);
;         *(GAS unsigned long long*)(WT + (size_t)(n0 + n) * K + k0 + 8 * c) = o; }
	s_add_u32 s8, s38, 0x8000000
	s_addc_u32 s9, s39, 0
	global_load_dwordx4 v[144:147], v75, s[8:9]
	s_add_u32 s8, s8, 0x8000
	s_addc_u32 s9, s9, 0
	global_load_dwordx4 v[148:151], v75, s[8:9]
	s_add_u32 s8, s8, 0x8000
	s_addc_u32 s9, s9, 0
	global_load_dwordx4 v[152:155], v75, s[8:9]
	s_add_u32 s8, s8, 0x8000
	s_addc_u32 s9, s9, 0
	global_load_dwordx4 v[156:159], v75, s[8:9]
	s_add_u32 s8, s8, 0x8000
	s_addc_u32 s9, s9, 0
	global_load_dwordx4 v[160:163], v75, s[8:9]
	s_add_u32 s8, s8, 0x8000
	s_addc_u32 s9, s9, 0
	global_load_dwordx4 v[164:167], v75, s[8:9]
	s_add_u32 s8, s8, 0x8000
	s_addc_u32 s9, s9, 0
	global_load_dwordx4 v[168:171], v75, s[8:9]
	s_add_u32 s8, s8, 0x8000
	s_addc_u32 s9, s9, 0
	global_load_dwordx4 v[172:175], v75, s[8:9]
	s_add_u32 s6, s40, 0x2001000
	s_addc_u32 s7, s41, 0
	ds_read_b32 v226, v211
	ds_read_b32 v227, v211 offset:512
	ds_read_b32 v228, v211 offset:1024
	ds_read_b32 v229, v211 offset:1536
	ds_read_b32 v230, v211 offset:2048
	ds_read_b32 v231, v211 offset:2560
	ds_read_b32 v232, v211 offset:3072
	ds_read_b32 v233, v211 offset:3584
	ds_read_b32 v234, v211 offset:4096
	ds_read_b32 v235, v211 offset:4608
	ds_read_b32 v236, v211 offset:5120
	ds_read_b32 v237, v211 offset:5632
	ds_read_b32 v238, v211 offset:6144
	ds_read_b32 v239, v211 offset:6656
	ds_read_b32 v240, v211 offset:7168
	ds_read_b32 v241, v211 offset:7680
	s_waitcnt lgkmcnt(0)
	v_max_f32_e32 v226, v226, v226
	v_max_f32_e32 v227, v227, v227
	v_max_f32_e32 v228, v228, v228
	v_max_f32_e32 v229, v229, v229
	v_max_f32_e32 v230, v230, v230
	v_max_f32_e32 v231, v231, v231
	v_max_f32_e32 v232, v232, v232
	v_max_f32_e32 v233, v233, v233
	v_max_f32_e32 v234, v234, v234
	v_max_f32_e32 v235, v235, v235
	v_max_f32_e32 v236, v236, v236
	v_max_f32_e32 v237, v237, v237
	v_max_f32_e32 v238, v238, v238
	v_max_f32_e32 v239, v239, v239
	v_max_f32_e32 v240, v240, v240
	v_max_f32_e32 v241, v241, v241
	v_med3_f32 v226, v226, s62, v95
	v_med3_f32 v227, v227, s62, v95
	v_med3_f32 v228, v228, s62, v95
	v_med3_f32 v229, v229, s62, v95
	v_med3_f32 v230, v230, s62, v95
	v_med3_f32 v231, v231, s62, v95
	v_med3_f32 v232, v232, s62, v95
	v_med3_f32 v233, v233, s62, v95
	v_med3_f32 v234, v234, s62, v95
	v_med3_f32 v235, v235, s62, v95
	v_med3_f32 v236, v236, s62, v95
	v_med3_f32 v237, v237, s62, v95
	v_med3_f32 v238, v238, s62, v95
	v_med3_f32 v239, v239, s62, v95
	v_med3_f32 v240, v240, s62, v95
	v_med3_f32 v241, v241, s62, v95
	v_mov_b32_e32 v242, 0
	v_mov_b32_e32 v243, 0
	v_mov_b32_e32 v244, 0
	v_mov_b32_e32 v245, 0
	v_cvt_pk_fp8_f32 v242, v226, v227
	v_cvt_pk_fp8_f32 v243, v230, v231
	v_cvt_pk_fp8_f32 v244, v234, v235
	v_cvt_pk_fp8_f32 v245, v238, v239
	v_cvt_pk_fp8_f32 v242, v228, v229 op_sel:[0,0,1]
	v_cvt_pk_fp8_f32 v243, v232, v233 op_sel:[0,0,1]
	v_cvt_pk_fp8_f32 v244, v236, v237 op_sel:[0,0,1]
	v_cvt_pk_fp8_f32 v245, v240, v241 op_sel:[0,0,1]
	s_nop 0
	global_store_dwordx4 v79, v[242:245], s[6:7]
	ds_read_b32 v226, v213
	ds_read_b32 v227, v213 offset:512
	ds_read_b32 v228, v213 offset:1024
	ds_read_b32 v229, v213 offset:1536
	ds_read_b32 v230, v213 offset:2048
	ds_read_b32 v231, v213 offset:2560
	ds_read_b32 v232, v213 offset:3072
	ds_read_b32 v233, v213 offset:3584
	ds_read_b32 v234, v213 offset:4096
	ds_read_b32 v235, v213 offset:4608
	ds_read_b32 v236, v213 offset:5120
	ds_read_b32 v237, v213 offset:5632
	ds_read_b32 v238, v213 offset:6144
	ds_read_b32 v239, v213 offset:6656
	ds_read_b32 v240, v213 offset:7168
	ds_read_b32 v241, v213 offset:7680
	s_waitcnt lgkmcnt(0)
	v_max_f32_e32 v226, v226, v226
	v_max_f32_e32 v227, v227, v227
	v_max_f32_e32 v228, v228, v228
	v_max_f32_e32 v229, v229, v229
	v_max_f32_e32 v230, v230, v230
	v_max_f32_e32 v231, v231, v231
	v_max_f32_e32 v232, v232, v232
	v_max_f32_e32 v233, v233, v233
	v_max_f32_e32 v234, v234, v234
	v_max_f32_e32 v235, v235, v235
	v_max_f32_e32 v236, v236, v236
	v_max_f32_e32 v237, v237, v237
	v_max_f32_e32 v238, v238, v238
	v_max_f32_e32 v239, v239, v239
	v_max_f32_e32 v240, v240, v240
	v_max_f32_e32 v241, v241, v241
	v_med3_f32 v226, v226, s62, v95
	v_med3_f32 v227, v227, s62, v95
	v_med3_f32 v228, v228, s62, v95
	v_med3_f32 v229, v229, s62, v95
	v_med3_f32 v230, v230, s62, v95
	v_med3_f32 v231, v231, s62, v95
	v_med3_f32 v232, v232, s62, v95
	v_med3_f32 v233, v233, s62, v95
	v_med3_f32 v234, v234, s62, v95
	v_med3_f32 v235, v235, s62, v95
	v_med3_f32 v236, v236, s62, v95
	v_med3_f32 v237, v237, s62, v95
	v_med3_f32 v238, v238, s62, v95
	v_med3_f32 v239, v239, s62, v95
	v_med3_f32 v240, v240, s62, v95
	v_med3_f32 v241, v241, s62, v95
	v_mov_b32_e32 v242, 0
	v_mov_b32_e32 v243, 0
	v_mov_b32_e32 v244, 0
	v_mov_b32_e32 v245, 0
	v_cvt_pk_fp8_f32 v242, v226, v227
	v_cvt_pk_fp8_f32 v243, v230, v231
	v_cvt_pk_fp8_f32 v244, v234, v235
	v_cvt_pk_fp8_f32 v245, v238, v239
	v_cvt_pk_fp8_f32 v242, v228, v229 op_sel:[0,0,1]
	v_cvt_pk_fp8_f32 v243, v232, v233 op_sel:[0,0,1]
	v_cvt_pk_fp8_f32 v244, v236, v237 op_sel:[0,0,1]
	v_cvt_pk_fp8_f32 v245, v240, v241 op_sel:[0,0,1]
	s_nop 0
	global_store_dwordx4 v80, v[242:245], s[6:7]
	s_waitcnt vmcnt(12)
	v_mul_f32_e32 v176, 0x43000000, v176
	v_mul_f32_e32 v177, 0x43000000, v177
	v_mul_f32_e32 v178, 0x43000000, v178
	v_mul_f32_e32 v179, 0x43000000, v179
	ds_write_b128 v210, v[176:179]
	v_mul_f32_e32 v180, 0x43000000, v180
	v_mul_f32_e32 v181, 0x43000000, v181
	v_mul_f32_e32 v182, 0x43000000, v182
	v_mul_f32_e32 v183, 0x43000000, v183
	ds_write_b128 v210, v[180:183] offset:1024
	v_mul_f32_e32 v184, 0x43000000, v184
	v_mul_f32_e32 v185, 0x43000000, v185
	v_mul_f32_e32 v186, 0x43000000, v186
	v_mul_f32_e32 v187, 0x43000000, v187
	ds_write_b128 v210, v[184:187] offset:2048
	v_mul_f32_e32 v188, 0x43000000, v188
	v_mul_f32_e32 v189, 0x43000000, v189
	v_mul_f32_e32 v190, 0x43000000, v190
	v_mul_f32_e32 v191, 0x43000000, v191
	ds_write_b128 v210, v[188:191] offset:3072
	v_mul_f32_e32 v192, 0x43000000, v192
	v_mul_f32_e32 v193, 0x43000000, v193
	v_mul_f32_e32 v194, 0x43000000, v194
	v_mul_f32_e32 v195, 0x43000000, v195
	ds_write_b128 v210, v[192:195] offset:4096
	v_mul_f32_e32 v196, 0x43000000, v196
	v_mul_f32_e32 v197, 0x43000000, v197
	v_mul_f32_e32 v198, 0x43000000, v198
	v_mul_f32_e32 v199, 0x43000000, v199
	ds_write_b128 v210, v[196:199] offset:5120
	v_mul_f32_e32 v200, 0x43000000, v200
	v_mul_f32_e32 v201, 0x43000000, v201
	v_mul_f32_e32 v202, 0x43000000, v202
	v_mul_f32_e32 v203, 0x43000000, v203
	ds_write_b128 v210, v[200:203] offset:6144
	v_mul_f32_e32 v204, 0x43000000, v204
	v_mul_f32_e32 v205, 0x43000000, v205
	v_mul_f32_e32 v206, 0x43000000, v206
	v_mul_f32_e32 v207, 0x43000000, v207
	ds_write_b128 v210, v[204:207] offset:7168
	s_waitcnt lgkmcnt(0)
	s_barrier
; #define GAS __attribute__((address_space(1)))
; #define LAS __attribute__((address_space(3)))
; #define LDS_WAIT() asm volatile("s_waitcnt lgkmcnt(0)" ::: "memory")
; __device__ __forceinline__ unsigned pk4_fp8(float a, float b, float c, float d) {
;     a = fminf(fmaxf(a, -448.f), 448.f); b = fminf(fmaxf(b, -448.f), 448.f); c = fminf(fmaxf(c, -448.f), 448.f); d = fminf(fmaxf(d, -448.f), 448.f);
;     int w = __builtin_amdgcn_cvt_pk_fp8_f32(a, b, 0, false); w = __builtin_amdgcn_cvt_pk_fp8_f32(c, d, w, true); return (unsigned)w; }
;     ...
; #pragma unroll
;     for (int i = 0; i < 32; ++i) v[i] = sc >= 0 ? W[(size_t)(k0 + 2 * i + (lane >> 5)) * Nsrc + sc] : 0.f;
; #pragma unroll
;     for (int i = 0; i < 32; ++i) { const int k = k0 + 2 * i + (lane >> 5); float x = v[i] * wscale; if (KS) x *= (k < ksplit ? ksA[k] : ksB[k - ksplit]); scr[(2 * i + (lane >> 5)) * 33 + (lane & 31)] = x; }
;     LDS_WAIT(); asm volatile("" ::: "memory");
;     const int c = lane & 7;
; #pragma unroll
;     for (int j = 0; j < 4; ++j) { const int n = (lane >> 3) + 8 * j; const LAS float* s = scr + (8 * c) * 33 + n;
;         const unsigned long long o = (unsigned long long)pg8::pk4_fp8(s[0 * 33], s[1 * 33], s[2 * 33], s[3 * 33]) | ((unsigned long long)pg8::pk4_fp8(s[4 * 33], s[5 * 33], s[6 * 33], s[7 * 33]) << 32);
;         *(GAS unsigned long long*)(WT + (size_t)(n0 + n) * K + k0 + 8 * c) = o; }
	s_add_u32 s8, s38, 0x8001000
	s_addc_u32 s9, s39, 0
	global_load_dwordx4 v[176:179], v75, s[8:9]
	s_add_u32 s8, s8, 0x8000
	s_addc_u32 s9, s9, 0
	global_load_dwordx4 v[180:183], v75, s[8:9]
	s_add_u32 s8, s8, 0x8000
	s_addc_u32 s9, s9, 0
	global_load_dwordx4 v[184:187], v75, s[8:9]
	s_add_u32 s8, s8, 0x8000
	s_addc_u32 s9, s9, 0
	global_load_dwordx4 v[188:191], v75, s[8:9]
	s_add_u32 s8, s8, 0x8000
	s_addc_u32 s9, s9, 0
	global_load_dwordx4 v[192:195], v75, s[8:9]
	s_add_u32 s8, s8, 0x8000
	s_addc_u32 s9, s9, 0
	global_load_dwordx4 v[196:199], v75, s[8:9]
	s_add_u32 s8, s8, 0x8000
	s_addc_u32 s9, s9, 0
	global_load_dwordx4 v[200:203], v75, s[8:9]
	s_add_u32 s8, s8, 0x8000
	s_addc_u32 s9, s9, 0
	global_load_dwordx4 v[204:207], v75, s[8:9]
	s_add_u32 s6, s40, 0x3001000
	s_addc_u32 s7, s41, 0
	ds_read_b32 v226, v212
	ds_read_b32 v227, v212 offset:512
	ds_read_b32 v228, v212 offset:1024
	ds_read_b32 v229, v212 offset:1536
	ds_read_b32 v230, v212 offset:2048
	ds_read_b32 v231, v212 offset:2560
	ds_read_b32 v232, v212 offset:3072
	ds_read_b32 v233, v212 offset:3584
	ds_read_b32 v234, v212 offset:4096
	ds_read_b32 v235, v212 offset:4608
	ds_read_b32 v236, v212 offset:5120
	ds_read_b32 v237, v212 offset:5632
	ds_read_b32 v238, v212 offset:6144
	ds_read_b32 v239, v212 offset:6656
	ds_read_b32 v240, v212 offset:7168
	ds_read_b32 v241, v212 offset:7680
	s_waitcnt lgkmcnt(0)
	v_max_f32_e32 v226, v226, v226
	v_max_f32_e32 v227, v227, v227
	v_max_f32_e32 v228, v228, v228
	v_max_f32_e32 v229, v229, v229
	v_max_f32_e32 v230, v230, v230
	v_max_f32_e32 v231, v231, v231
	v_max_f32_e32 v232, v232, v232
	v_max_f32_e32 v233, v233, v233
	v_max_f32_e32 v234, v234, v234
	v_max_f32_e32 v235, v235, v235
	v_max_f32_e32 v236, v236, v236
	v_max_f32_e32 v237, v237, v237
	v_max_f32_e32 v238, v238, v238
	v_max_f32_e32 v239, v239, v239
	v_max_f32_e32 v240, v240, v240
	v_max_f32_e32 v241, v241, v241
	v_med3_f32 v226, v226, s62, v95
	v_med3_f32 v227, v227, s62, v95
	v_med3_f32 v228, v228, s62, v95
	v_med3_f32 v229, v229, s62, v95
	v_med3_f32 v230, v230, s62, v95
	v_med3_f32 v231, v231, s62, v95
	v_med3_f32 v232, v232, s62, v95
	v_med3_f32 v233, v233, s62, v95
	v_med3_f32 v234, v234, s62, v95
	v_med3_f32 v235, v235, s62, v95
	v_med3_f32 v236, v236, s62, v95
	v_med3_f32 v237, v237, s62, v95
	v_med3_f32 v238, v238, s62, v95
	v_med3_f32 v239, v239, s62, v95
	v_med3_f32 v240, v240, s62, v95
	v_med3_f32 v241, v241, s62, v95
	v_mov_b32_e32 v242, 0
	v_mov_b32_e32 v243, 0
	v_mov_b32_e32 v244, 0
	v_mov_b32_e32 v245, 0
	v_cvt_pk_fp8_f32 v242, v226, v227
	v_cvt_pk_fp8_f32 v243, v230, v231
	v_cvt_pk_fp8_f32 v244, v234, v235
	v_cvt_pk_fp8_f32 v245, v238, v239
	v_cvt_pk_fp8_f32 v242, v228, v229 op_sel:[0,0,1]
	v_cvt_pk_fp8_f32 v243, v232, v233 op_sel:[0,0,1]
	v_cvt_pk_fp8_f32 v244, v236, v237 op_sel:[0,0,1]
	v_cvt_pk_fp8_f32 v245, v240, v241 op_sel:[0,0,1]
	s_nop 0
	global_store_dwordx4 v79, v[242:245], s[6:7]
	ds_read_b32 v226, v214
	ds_read_b32 v227, v214 offset:512
	ds_read_b32 v228, v214 offset:1024
	ds_read_b32 v229, v214 offset:1536
	ds_read_b32 v230, v214 offset:2048
	ds_read_b32 v231, v214 offset:2560
	ds_read_b32 v232, v214 offset:3072
	ds_read_b32 v233, v214 offset:3584
	ds_read_b32 v234, v214 offset:4096
	ds_read_b32 v235, v214 offset:4608
	ds_read_b32 v236, v214 offset:5120
	ds_read_b32 v237, v214 offset:5632
	ds_read_b32 v238, v214 offset:6144
	ds_read_b32 v239, v214 offset:6656
	ds_read_b32 v240, v214 offset:7168
	ds_read_b32 v241, v214 offset:7680
	s_waitcnt lgkmcnt(0)
	v_max_f32_e32 v226, v226, v226
	v_max_f32_e32 v227, v227, v227
	v_max_f32_e32 v228, v228, v228
	v_max_f32_e32 v229, v229, v229
	v_max_f32_e32 v230, v230, v230
	v_max_f32_e32 v231, v231, v231
	v_max_f32_e32 v232, v232, v232
	v_max_f32_e32 v233, v233, v233
	v_max_f32_e32 v234, v234, v234
	v_max_f32_e32 v235, v235, v235
	v_max_f32_e32 v236, v236, v236
	v_max_f32_e32 v237, v237, v237
	v_max_f32_e32 v238, v238, v238
	v_max_f32_e32 v239, v239, v239
	v_max_f32_e32 v240, v240, v240
	v_max_f32_e32 v241, v241, v241
	v_med3_f32 v226, v226, s62, v95
	v_med3_f32 v227, v227, s62, v95
	v_med3_f32 v228, v228, s62, v95
	v_med3_f32 v229, v229, s62, v95
	v_med3_f32 v230, v230, s62, v95
	v_med3_f32 v231, v231, s62, v95
	v_med3_f32 v232, v232, s62, v95
	v_med3_f32 v233, v233, s62, v95
	v_med3_f32 v234, v234, s62, v95
	v_med3_f32 v235, v235, s62, v95
	v_med3_f32 v236, v236, s62, v95
	v_med3_f32 v237, v237, s62, v95
	v_med3_f32 v238, v238, s62, v95
	v_med3_f32 v239, v239, s62, v95
	v_med3_f32 v240, v240, s62, v95
	v_med3_f32 v241, v241, s62, v95
	v_mov_b32_e32 v242, 0
	v_mov_b32_e32 v243, 0
	v_mov_b32_e32 v244, 0
	v_mov_b32_e32 v245, 0
	v_cvt_pk_fp8_f32 v242, v226, v227
	v_cvt_pk_fp8_f32 v243, v230, v231
	v_cvt_pk_fp8_f32 v244, v234, v235
	v_cvt_pk_fp8_f32 v245, v238, v239
	v_cvt_pk_fp8_f32 v242, v228, v229 op_sel:[0,0,1]
	v_cvt_pk_fp8_f32 v243, v232, v233 op_sel:[0,0,1]
	v_cvt_pk_fp8_f32 v244, v236, v237 op_sel:[0,0,1]
	v_cvt_pk_fp8_f32 v245, v240, v241 op_sel:[0,0,1]
	s_nop 0
	global_store_dwordx4 v80, v[242:245], s[6:7]
	s_waitcnt vmcnt(12)
	v_mul_f32_e32 v144, 0x43000000, v144
	v_mul_f32_e32 v145, 0x43000000, v145
	v_mul_f32_e32 v146, 0x43000000, v146
	v_mul_f32_e32 v147, 0x43000000, v147
	ds_write_b128 v209, v[144:147]
	v_mul_f32_e32 v148, 0x43000000, v148
	v_mul_f32_e32 v149, 0x43000000, v149
	v_mul_f32_e32 v150, 0x43000000, v150
	v_mul_f32_e32 v151, 0x43000000, v151
	ds_write_b128 v209, v[148:151] offset:1024
	v_mul_f32_e32 v152, 0x43000000, v152
	v_mul_f32_e32 v153, 0x43000000, v153
	v_mul_f32_e32 v154, 0x43000000, v154
	v_mul_f32_e32 v155, 0x43000000, v155
	ds_write_b128 v209, v[152:155] offset:2048
	v_mul_f32_e32 v156, 0x43000000, v156
	v_mul_f32_e32 v157, 0x43000000, v157
	v_mul_f32_e32 v158, 0x43000000, v158
	v_mul_f32_e32 v159, 0x43000000, v159
	ds_write_b128 v209, v[156:159] offset:3072
	v_mul_f32_e32 v160, 0x43000000, v160
	v_mul_f32_e32 v161, 0x43000000, v161
	v_mul_f32_e32 v162, 0x43000000, v162
	v_mul_f32_e32 v163, 0x43000000, v163
	ds_write_b128 v209, v[160:163] offset:4096
	v_mul_f32_e32 v164, 0x43000000, v164
	v_mul_f32_e32 v165, 0x43000000, v165
	v_mul_f32_e32 v166, 0x43000000, v166
	v_mul_f32_e32 v167, 0x43000000, v167
	ds_write_b128 v209, v[164:167] offset:5120
	v_mul_f32_e32 v168, 0x43000000, v168
	v_mul_f32_e32 v169, 0x43000000, v169
	v_mul_f32_e32 v170, 0x43000000, v170
	v_mul_f32_e32 v171, 0x43000000, v171
	ds_write_b128 v209, v[168:171] offset:6144
	v_mul_f32_e32 v172, 0x43000000, v172
	v_mul_f32_e32 v173, 0x43000000, v173
	v_mul_f32_e32 v174, 0x43000000, v174
	v_mul_f32_e32 v175, 0x43000000, v175
	ds_write_b128 v209, v[172:175] offset:7168
	s_waitcnt lgkmcnt(0)
	s_barrier
; #define GAS __attribute__((address_space(1)))
; #define LAS __attribute__((address_space(3)))
; #define LDS_WAIT() asm volatile("s_waitcnt lgkmcnt(0)" ::: "memory")
; __device__ __forceinline__ unsigned pk4_fp8(float a, float b, float c, float d) {
;     a = fminf(fmaxf(a, -448.f), 448.f); b = fminf(fmaxf(b, -448.f), 448.f); c = fminf(fmaxf(c, -448.f), 448.f); d = fminf(fmaxf(d, -448.f), 448.f);
;     int w = __builtin_amdgcn_cvt_pk_fp8_f32(a, b, 0, false); w = __builtin_amdgcn_cvt_pk_fp8_f32(c, d, w, true); return (unsigned)w; }
;     ...
; #pragma unroll
;     for (int i = 0; i < 32; ++i) v[i] = sc >= 0 ? W[(size_t)(k0 + 2 * i + (lane >> 5)) * Nsrc + sc] : 0.f;
; #pragma unroll
;     for (int i = 0; i < 32; ++i) { const int k = k0 + 2 * i + (lane >> 5); float x = v[i] * wscale; if (KS) x *= (k < ksplit ? ksA[k] : ksB[k - ksplit]); scr[(2 * i + (lane >> 5)) * 33 + (lane & 31)] = x; }
;     LDS_WAIT(); asm volatile("" ::: "memory");
;     const int c = lane & 7;
; #pragma unroll
;     for (int j = 0; j < 4; ++j) { const int n = (lane >> 3) + 8 * j; const LAS float* s = scr + (8 * c) * 33 + n;
;         const unsigned long long o = (unsigned long long)pg8::pk4_fp8(s[0 * 33], s[1 * 33], s[2 * 33], s[3 * 33]) | ((unsigned long long)pg8::pk4_fp8(s[4 * 33], s[5 * 33], s[6 * 33], s[7 * 33]) << 32);
;         *(GAS unsigned long long*)(WT + (size_t)(n0 + n) * K + k0 + 8 * c) = o; }
	s_add_u32 s8, s38, 0x8002000
	s_addc_u32 s9, s39, 0
	global_load_dwordx4 v[144:147], v75, s[8:9]
	s_add_u32 s8, s8, 0x8000
	s_addc_u32 s9, s9, 0
	global_load_dwordx4 v[148:151], v75, s[8:9]
	s_add_u32 s8, s8, 0x8000
	s_addc_u32 s9, s9, 0
	global_load_dwordx4 v[152:155], v75, s[8:9]
	s_add_u32 s8, s8, 0x8000
	s_addc_u32 s9, s9, 0
	global_load_dwordx4 v[156:159], v75, s[8:9]
	s_add_u32 s8, s8, 0x8000
	s_addc_u32 s9, s9, 0
	global_load_dwordx4 v[160:163], v75, s[8:9]
	s_add_u32 s8, s8, 0x8000
	s_addc_u32 s9, s9, 0
	global_load_dwordx4 v[164:167], v75, s[8:9]
	s_add_u32 s8, s8, 0x8000
	s_addc_u32 s9, s9, 0
	global_load_dwordx4 v[168:171], v75, s[8:9]
	s_add_u32 s8, s8, 0x8000
	s_addc_u32 s9, s9, 0
	global_load_dwordx4 v[172:175], v75, s[8:9]
	s_add_u32 s6, s40, 0x2000
	s_addc_u32 s7, s41, 0
	ds_read_b32 v226, v211
	ds_read_b32 v227, v211 offset:512
	ds_read_b32 v228, v211 offset:1024
	ds_read_b32 v229, v211 offset:1536
	ds_read_b32 v230, v211 offset:2048
	ds_read_b32 v231, v211 offset:2560
	ds_read_b32 v232, v211 offset:3072
	ds_read_b32 v233, v211 offset:3584
	ds_read_b32 v234, v211 offset:4096
	ds_read_b32 v235, v211 offset:4608
	ds_read_b32 v236, v211 offset:5120
	ds_read_b32 v237, v211 offset:5632
	ds_read_b32 v238, v211 offset:6144
	ds_read_b32 v239, v211 offset:6656
	ds_read_b32 v240, v211 offset:7168
	ds_read_b32 v241, v211 offset:7680
	s_waitcnt lgkmcnt(0)
	v_max_f32_e32 v226, v226, v226
	v_max_f32_e32 v227, v227, v227
	v_max_f32_e32 v228, v228, v228
	v_max_f32_e32 v229, v229, v229
	v_max_f32_e32 v230, v230, v230
	v_max_f32_e32 v231, v231, v231
	v_max_f32_e32 v232, v232, v232
	v_max_f32_e32 v233, v233, v233
	v_max_f32_e32 v234, v234, v234
	v_max_f32_e32 v235, v235, v235
	v_max_f32_e32 v236, v236, v236
	v_max_f32_e32 v237, v237, v237
	v_max_f32_e32 v238, v238, v238
	v_max_f32_e32 v239, v239, v239
	v_max_f32_e32 v240, v240, v240
	v_max_f32_e32 v241, v241, v241
	v_med3_f32 v226, v226, s62, v95
	v_med3_f32 v227, v227, s62, v95
	v_med3_f32 v228, v228, s62, v95
	v_med3_f32 v229, v229, s62, v95
	v_med3_f32 v230, v230, s62, v95
	v_med3_f32 v231, v231, s62, v95
	v_med3_f32 v232, v232, s62, v95
	v_med3_f32 v233, v233, s62, v95
	v_med3_f32 v234, v234, s62, v95
	v_med3_f32 v235, v235, s62, v95
	v_med3_f32 v236, v236, s62, v95
	v_med3_f32 v237, v237, s62, v95
	v_med3_f32 v238, v238, s62, v95
	v_med3_f32 v239, v239, s62, v95
	v_med3_f32 v240, v240, s62, v95
	v_med3_f32 v241, v241, s62, v95
	v_mov_b32_e32 v242, 0
	v_mov_b32_e32 v243, 0
	v_mov_b32_e32 v244, 0
	v_mov_b32_e32 v245, 0
	v_cvt_pk_fp8_f32 v242, v226, v227
	v_cvt_pk_fp8_f32 v243, v230, v231
	v_cvt_pk_fp8_f32 v244, v234, v235
	v_cvt_pk_fp8_f32 v245, v238, v239
	v_cvt_pk_fp8_f32 v242, v228, v229 op_sel:[0,0,1]
	v_cvt_pk_fp8_f32 v243, v232, v233 op_sel:[0,0,1]
	v_cvt_pk_fp8_f32 v244, v236, v237 op_sel:[0,0,1]
	v_cvt_pk_fp8_f32 v245, v240, v241 op_sel:[0,0,1]
	s_nop 0
	global_store_dwordx4 v79, v[242:245], s[6:7]
	ds_read_b32 v226, v213
	ds_read_b32 v227, v213 offset:512
	ds_read_b32 v228, v213 offset:1024
	ds_read_b32 v229, v213 offset:1536
	ds_read_b32 v230, v213 offset:2048
	ds_read_b32 v231, v213 offset:2560
	ds_read_b32 v232, v213 offset:3072
	ds_read_b32 v233, v213 offset:3584
	ds_read_b32 v234, v213 offset:4096
	ds_read_b32 v235, v213 offset:4608
	ds_read_b32 v236, v213 offset:5120
	ds_read_b32 v237, v213 offset:5632
	ds_read_b32 v238, v213 offset:6144
	ds_read_b32 v239, v213 offset:6656
	ds_read_b32 v240, v213 offset:7168
	ds_read_b32 v241, v213 offset:7680
	s_waitcnt lgkmcnt(0)
	v_max_f32_e32 v226, v226, v226
	v_max_f32_e32 v227, v227, v227
	v_max_f32_e32 v228, v228, v228
	v_max_f32_e32 v229, v229, v229
	v_max_f32_e32 v230, v230, v230
	v_max_f32_e32 v231, v231, v231
	v_max_f32_e32 v232, v232, v232
	v_max_f32_e32 v233, v233, v233
	v_max_f32_e32 v234, v234, v234
	v_max_f32_e32 v235, v235, v235
	v_max_f32_e32 v236, v236, v236
	v_max_f32_e32 v237, v237, v237
	v_max_f32_e32 v238, v238, v238
	v_max_f32_e32 v239, v239, v239
	v_max_f32_e32 v240, v240, v240
	v_max_f32_e32 v241, v241, v241
	v_med3_f32 v226, v226, s62, v95
	v_med3_f32 v227, v227, s62, v95
	v_med3_f32 v228, v228, s62, v95
	v_med3_f32 v229, v229, s62, v95
	v_med3_f32 v230, v230, s62, v95
	v_med3_f32 v231, v231, s62, v95
	v_med3_f32 v232, v232, s62, v95
	v_med3_f32 v233, v233, s62, v95
	v_med3_f32 v234, v234, s62, v95
	v_med3_f32 v235, v235, s62, v95
	v_med3_f32 v236, v236, s62, v95
	v_med3_f32 v237, v237, s62, v95
	v_med3_f32 v238, v238, s62, v95
	v_med3_f32 v239, v239, s62, v95
	v_med3_f32 v240, v240, s62, v95
	v_med3_f32 v241, v241, s62, v95
	v_mov_b32_e32 v242, 0
	v_mov_b32_e32 v243, 0
	v_mov_b32_e32 v244, 0
	v_mov_b32_e32 v245, 0
	v_cvt_pk_fp8_f32 v242, v226, v227
	v_cvt_pk_fp8_f32 v243, v230, v231
	v_cvt_pk_fp8_f32 v244, v234, v235
	v_cvt_pk_fp8_f32 v245, v238, v239
	v_cvt_pk_fp8_f32 v242, v228, v229 op_sel:[0,0,1]
	v_cvt_pk_fp8_f32 v243, v232, v233 op_sel:[0,0,1]
	v_cvt_pk_fp8_f32 v244, v236, v237 op_sel:[0,0,1]
	v_cvt_pk_fp8_f32 v245, v240, v241 op_sel:[0,0,1]
	s_nop 0
	global_store_dwordx4 v80, v[242:245], s[6:7]
	s_waitcnt vmcnt(12)
	v_mul_f32_e32 v176, 0x43000000, v176
	v_mul_f32_e32 v177, 0x43000000, v177
	v_mul_f32_e32 v178, 0x43000000, v178
	v_mul_f32_e32 v179, 0x43000000, v179
	ds_write_b128 v210, v[176:179]
	v_mul_f32_e32 v180, 0x43000000, v180
	v_mul_f32_e32 v181, 0x43000000, v181
	v_mul_f32_e32 v182, 0x43000000, v182
	v_mul_f32_e32 v183, 0x43000000, v183
	ds_write_b128 v210, v[180:183] offset:1024
	v_mul_f32_e32 v184, 0x43000000, v184
	v_mul_f32_e32 v185, 0x43000000, v185
	v_mul_f32_e32 v186, 0x43000000, v186
	v_mul_f32_e32 v187, 0x43000000, v187
	ds_write_b128 v210, v[184:187] offset:2048
	v_mul_f32_e32 v188, 0x43000000, v188
	v_mul_f32_e32 v189, 0x43000000, v189
	v_mul_f32_e32 v190, 0x43000000, v190
	v_mul_f32_e32 v191, 0x43000000, v191
	ds_write_b128 v210, v[188:191] offset:3072
	v_mul_f32_e32 v192, 0x43000000, v192
	v_mul_f32_e32 v193, 0x43000000, v193
	v_mul_f32_e32 v194, 0x43000000, v194
	v_mul_f32_e32 v195, 0x43000000, v195
	ds_write_b128 v210, v[192:195] offset:4096
	v_mul_f32_e32 v196, 0x43000000, v196
	v_mul_f32_e32 v197, 0x43000000, v197
	v_mul_f32_e32 v198, 0x43000000, v198
	v_mul_f32_e32 v199, 0x43000000, v199
	ds_write_b128 v210, v[196:199] offset:5120
	v_mul_f32_e32 v200, 0x43000000, v200
	v_mul_f32_e32 v201, 0x43000000, v201
	v_mul_f32_e32 v202, 0x43000000, v202
	v_mul_f32_e32 v203, 0x43000000, v203
	ds_write_b128 v210, v[200:203] offset:6144
	v_mul_f32_e32 v204, 0x43000000, v204
	v_mul_f32_e32 v205, 0x43000000, v205
	v_mul_f32_e32 v206, 0x43000000, v206
	v_mul_f32_e32 v207, 0x43000000, v207
	ds_write_b128 v210, v[204:207] offset:7168
	s_waitcnt lgkmcnt(0)
	s_barrier
; #define GAS __attribute__((address_space(1)))
; #define LAS __attribute__((address_space(3)))
; #define LDS_WAIT() asm volatile("s_waitcnt lgkmcnt(0)" ::: "memory")
; __device__ __forceinline__ unsigned pk4_fp8(float a, float b, float c, float d) {
;     a = fminf(fmaxf(a, -448.f), 448.f); b = fminf(fmaxf(b, -448.f), 448.f); c = fminf(fmaxf(c, -448.f), 448.f); d = fminf(fmaxf(d, -448.f), 448.f);
;     int w = __builtin_amdgcn_cvt_pk_fp8_f32(a, b, 0, false); w = __builtin_amdgcn_cvt_pk_fp8_f32(c, d, w, true); return (unsigned)w; }
;     const int pr = item >> 1, kb = 2 * (pr / nblk) + (item & 1), nb = pr % nblk, k0 = 64 * kb, n0 = 32 * nb;
;     const int nr = n0 + (lane & 31); const int sc = MAP == 1 ? src_col_in(nr) : nr;
;     float v[32];
; #pragma unroll
;     for (int i = 0; i < 32; ++i) v[i] = sc >= 0 ? W[(size_t)(k0 + 2 * i + (lane >> 5)) * Nsrc + sc] : 0.f;
; #pragma unroll
;     for (int i = 0; i < 32; ++i) { const int k = k0 + 2 * i + (lane >> 5); float x = v[i] * wscale; if (KS) x *= (k < ksplit ? ksA[k] : ksB[k - ksplit]); scr[(2 * i + (lane >> 5)) * 33 + (lane & 31)] = x; }
;     LDS_WAIT(); asm volatile("" ::: "memory");
;     const int c = lane & 7;
; #pragma unroll
;     for (int j = 0; j < 4; ++j) { const int n = (lane >> 3) + 8 * j; const LAS float* s = scr + (8 * c) * 33 + n;
;         const unsigned long long o = (unsigned long long)pg8::pk4_fp8(s[0 * 33], s[1 * 33], s[2 * 33], s[3 * 33]) | ((unsigned long long)pg8::pk4_fp8(s[4 * 33], s[5 * 33], s[6 * 33], s[7 * 33]) << 32);
;         *(GAS unsigned long long*)(WT + (size_t)(n0 + n) * K + k0 + 8 * c) = o; }
;     LDS_WAIT(); asm volatile("" ::: "memory");
; }
	s_add_u32 s8, s38, 0x8003000
	s_addc_u32 s9, s39, 0
	global_load_dwordx4 v[176:179], v75, s[8:9]
	s_add_u32 s8, s8, 0x8000
	s_addc_u32 s9, s9, 0
	global_load_dwordx4 v[180:183], v75, s[8:9]
	s_add_u32 s8, s8, 0x8000
	s_addc_u32 s9, s9, 0
	global_load_dwordx4 v[184:187], v75, s[8:9]
	s_add_u32 s8, s8, 0x8000
	s_addc_u32 s9, s9, 0
	global_load_dwordx4 v[188:191], v75, s[8:9]
	s_add_u32 s8, s8, 0x8000
	s_addc_u32 s9, s9, 0
	global_load_dwordx4 v[192:195], v75, s[8:9]
	s_add_u32 s8, s8, 0x8000
	s_addc_u32 s9, s9, 0
	global_load_dwordx4 v[196:199], v75, s[8:9]
	s_add_u32 s8, s8, 0x8000
	s_addc_u32 s9, s9, 0
	global_load_dwordx4 v[200:203], v75, s[8:9]
	s_add_u32 s8, s8, 0x8000
	s_addc_u32 s9, s9, 0
	global_load_dwordx4 v[204:207], v75, s[8:9]
	s_add_u32 s6, s40, 0x1002000
	s_addc_u32 s7, s41, 0
	ds_read_b32 v226, v212
	ds_read_b32 v227, v212 offset:512
	ds_read_b32 v228, v212 offset:1024
	ds_read_b32 v229, v212 offset:1536
	ds_read_b32 v230, v212 offset:2048
	ds_read_b32 v231, v212 offset:2560
	ds_read_b32 v232, v212 offset:3072
	ds_read_b32 v233, v212 offset:3584
	ds_read_b32 v234, v212 offset:4096
	ds_read_b32 v235, v212 offset:4608
	ds_read_b32 v236, v212 offset:5120
	ds_read_b32 v237, v212 offset:5632
	ds_read_b32 v238, v212 offset:6144
	ds_read_b32 v239, v212 offset:6656
	ds_read_b32 v240, v212 offset:7168
	ds_read_b32 v241, v212 offset:7680
	s_waitcnt lgkmcnt(0)
	v_max_f32_e32 v226, v226, v226
	v_max_f32_e32 v227, v227, v227
	v_max_f32_e32 v228, v228, v228
	v_max_f32_e32 v229, v229, v229
	v_max_f32_e32 v230, v230, v230
	v_max_f32_e32 v231, v231, v231
	v_max_f32_e32 v232, v232, v232
	v_max_f32_e32 v233, v233, v233
	v_max_f32_e32 v234, v234, v234
	v_max_f32_e32 v235, v235, v235
	v_max_f32_e32 v236, v236, v236
	v_max_f32_e32 v237, v237, v237
	v_max_f32_e32 v238, v238, v238
	v_max_f32_e32 v239, v239, v239
	v_max_f32_e32 v240, v240, v240
	v_max_f32_e32 v241, v241, v241
	v_med3_f32 v226, v226, s62, v95
	v_med3_f32 v227, v227, s62, v95
	v_med3_f32 v228, v228, s62, v95
	v_med3_f32 v229, v229, s62, v95
	v_med3_f32 v230, v230, s62, v95
	v_med3_f32 v231, v231, s62, v95
	v_med3_f32 v232, v232, s62, v95
	v_med3_f32 v233, v233, s62, v95
	v_med3_f32 v234, v234, s62, v95
	v_med3_f32 v235, v235, s62, v95
	v_med3_f32 v236, v236, s62, v95
	v_med3_f32 v237, v237, s62, v95
	v_med3_f32 v238, v238, s62, v95
	v_med3_f32 v239, v239, s62, v95
	v_med3_f32 v240, v240, s62, v95
	v_med3_f32 v241, v241, s62, v95
	v_mov_b32_e32 v242, 0
	v_mov_b32_e32 v243, 0
	v_mov_b32_e32 v244, 0
	v_mov_b32_e32 v245, 0
	v_cvt_pk_fp8_f32 v242, v226, v227
	v_cvt_pk_fp8_f32 v243, v230, v231
	v_cvt_pk_fp8_f32 v244, v234, v235
	v_cvt_pk_fp8_f32 v245, v238, v239
	v_cvt_pk_fp8_f32 v242, v228, v229 op_sel:[0,0,1]
	v_cvt_pk_fp8_f32 v243, v232, v233 op_sel:[0,0,1]
	v_cvt_pk_fp8_f32 v244, v236, v237 op_sel:[0,0,1]
	v_cvt_pk_fp8_f32 v245, v240, v241 op_sel:[0,0,1]
	s_nop 0
	global_store_dwordx4 v79, v[242:245], s[6:7]
	ds_read_b32 v226, v214
	ds_read_b32 v227, v214 offset:512
	ds_read_b32 v228, v214 offset:1024
	ds_read_b32 v229, v214 offset:1536
	ds_read_b32 v230, v214 offset:2048
	ds_read_b32 v231, v214 offset:2560
	ds_read_b32 v232, v214 offset:3072
	ds_read_b32 v233, v214 offset:3584
	ds_read_b32 v234, v214 offset:4096
	ds_read_b32 v235, v214 offset:4608
	ds_read_b32 v236, v214 offset:5120
	ds_read_b32 v237, v214 offset:5632
	ds_read_b32 v238, v214 offset:6144
	ds_read_b32 v239, v214 offset:6656
	ds_read_b32 v240, v214 offset:7168
	ds_read_b32 v241, v214 offset:7680
	s_waitcnt lgkmcnt(0)
	v_max_f32_e32 v226, v226, v226
	v_max_f32_e32 v227, v227, v227
	v_max_f32_e32 v228, v228, v228
	v_max_f32_e32 v229, v229, v229
	v_max_f32_e32 v230, v230, v230
	v_max_f32_e32 v231, v231, v231
	v_max_f32_e32 v232, v232, v232
	v_max_f32_e32 v233, v233, v233
	v_max_f32_e32 v234, v234, v234
	v_max_f32_e32 v235, v235, v235
	v_max_f32_e32 v236, v236, v236
	v_max_f32_e32 v237, v237, v237
	v_max_f32_e32 v238, v238, v238
	v_max_f32_e32 v239, v239, v239
	v_max_f32_e32 v240, v240, v240
	v_max_f32_e32 v241, v241, v241
	v_med3_f32 v226, v226, s62, v95
	v_med3_f32 v227, v227, s62, v95
	v_med3_f32 v228, v228, s62, v95
	v_med3_f32 v229, v229, s62, v95
	v_med3_f32 v230, v230, s62, v95
	v_med3_f32 v231, v231, s62, v95
	v_med3_f32 v232, v232, s62, v95
	v_med3_f32 v233, v233, s62, v95
	v_med3_f32 v234, v234, s62, v95
	v_med3_f32 v235, v235, s62, v95
	v_med3_f32 v236, v236, s62, v95
	v_med3_f32 v237, v237, s62, v95
	v_med3_f32 v238, v238, s62, v95
	v_med3_f32 v239, v239, s62, v95
	v_med3_f32 v240, v240, s62, v95
	v_med3_f32 v241, v241, s62, v95
	v_mov_b32_e32 v242, 0
	v_mov_b32_e32 v243, 0
	v_mov_b32_e32 v244, 0
	v_mov_b32_e32 v245, 0
	v_cvt_pk_fp8_f32 v242, v226, v227
	v_cvt_pk_fp8_f32 v243, v230, v231
	v_cvt_pk_fp8_f32 v244, v234, v235
	v_cvt_pk_fp8_f32 v245, v238, v239
	v_cvt_pk_fp8_f32 v242, v228, v229 op_sel:[0,0,1]
	v_cvt_pk_fp8_f32 v243, v232, v233 op_sel:[0,0,1]
	v_cvt_pk_fp8_f32 v244, v236, v237 op_sel:[0,0,1]
	v_cvt_pk_fp8_f32 v245, v240, v241 op_sel:[0,0,1]
	s_nop 0
	global_store_dwordx4 v80, v[242:245], s[6:7]
	s_waitcnt vmcnt(12)
	v_mul_f32_e32 v144, 0x43000000, v144
	v_mul_f32_e32 v145, 0x43000000, v145
	v_mul_f32_e32 v146, 0x43000000, v146
	v_mul_f32_e32 v147, 0x43000000, v147
	ds_write_b128 v209, v[144:147]
	v_mul_f32_e32 v148, 0x43000000, v148
	v_mul_f32_e32 v149, 0x43000000, v149
	v_mul_f32_e32 v150, 0x43000000, v150
	v_mul_f32_e32 v151, 0x43000000, v151
	ds_write_b128 v209, v[148:151] offset:1024
	v_mul_f32_e32 v152, 0x43000000, v152
	v_mul_f32_e32 v153, 0x43000000, v153
	v_mul_f32_e32 v154, 0x43000000, v154
	v_mul_f32_e32 v155, 0x43000000, v155
	ds_write_b128 v209, v[152:155] offset:2048
	v_mul_f32_e32 v156, 0x43000000, v156
	v_mul_f32_e32 v157, 0x43000000, v157
	v_mul_f32_e32 v158, 0x43000000, v158
	v_mul_f32_e32 v159, 0x43000000, v159
	ds_write_b128 v209, v[156:159] offset:3072
	v_mul_f32_e32 v160, 0x43000000, v160
	v_mul_f32_e32 v161, 0x43000000, v161
	v_mul_f32_e32 v162, 0x43000000, v162
	v_mul_f32_e32 v163, 0x43000000, v163
	ds_write_b128 v209, v[160:163] offset:4096
	v_mul_f32_e32 v164, 0x43000000, v164
	v_mul_f32_e32 v165, 0x43000000, v165
	v_mul_f32_e32 v166, 0x43000000, v166
	v_mul_f32_e32 v167, 0x43000000, v167
	ds_write_b128 v209, v[164:167] offset:5120
	v_mul_f32_e32 v168, 0x43000000, v168
	v_mul_f32_e32 v169, 0x43000000, v169
	v_mul_f32_e32 v170, 0x43000000, v170
	v_mul_f32_e32 v171, 0x43000000, v171
	ds_write_b128 v209, v[168:171] offset:6144
	v_mul_f32_e32 v172, 0x43000000, v172
	v_mul_f32_e32 v173, 0x43000000, v173
	v_mul_f32_e32 v174, 0x43000000, v174
	v_mul_f32_e32 v175, 0x43000000, v175
	ds_write_b128 v209, v[172:175] offset:7168
	s_waitcnt lgkmcnt(0)
	s_barrier
; #define GAS __attribute__((address_space(1)))
; #define LAS __attribute__((address_space(3)))
; #define LDS_WAIT() asm volatile("s_waitcnt lgkmcnt(0)" ::: "memory")
; __device__ __forceinline__ unsigned pk4_fp8(float a, float b, float c, float d) {
;     a = fminf(fmaxf(a, -448.f), 448.f); b = fminf(fmaxf(b, -448.f), 448.f); c = fminf(fmaxf(c, -448.f), 448.f); d = fminf(fmaxf(d, -448.f), 448.f);
;     int w = __builtin_amdgcn_cvt_pk_fp8_f32(a, b, 0, false); w = __builtin_amdgcn_cvt_pk_fp8_f32(c, d, w, true); return (unsigned)w; }
;     const int pr = item >> 1, kb = 2 * (pr / nblk) + (item & 1), nb = pr % nblk, k0 = 64 * kb, n0 = 32 * nb;
;     const int nr = n0 + (lane & 31); const int sc = MAP == 1 ? src_col_in(nr) : nr;
;     float v[32];
; #pragma unroll
;     for (int i = 0; i < 32; ++i) v[i] = sc >= 0 ? W[(size_t)(k0 + 2 * i + (lane >> 5)) * Nsrc + sc] : 0.f;
; #pragma unroll
;     for (int i = 0; i < 32; ++i) { const int k = k0 + 2 * i + (lane >> 5); float x = v[i] * wscale; if (KS) x *= (k < ksplit ? ksA[k] : ksB[k - ksplit]); scr[(2 * i + (lane >> 5)) * 33 + (lane & 31)] = x; }
;     LDS_WAIT(); asm volatile("" ::: "memory");
;     const int c = lane & 7;
; #pragma unroll
;     for (int j = 0; j < 4; ++j) { const int n = (lane >> 3) + 8 * j; const LAS float* s = scr + (8 * c) * 33 + n;
;         const unsigned long long o = (unsigned long long)pg8::pk4_fp8(s[0 * 33], s[1 * 33], s[2 * 33], s[3 * 33]) | ((unsigned long long)pg8::pk4_fp8(s[4 * 33], s[5 * 33], s[6 * 33], s[7 * 33]) << 32);
;         *(GAS unsigned long long*)(WT + (size_t)(n0 + n) * K + k0 + 8 * c) = o; }
;     LDS_WAIT(); asm volatile("" ::: "memory");
; }
	s_add_u32 s8, s38, 0xc000000
	s_addc_u32 s9, s39, 0
	global_load_dwordx4 v[144:147], v75, s[8:9]
	s_add_u32 s8, s8, 0x8000
	s_addc_u32 s9, s9, 0
	global_load_dwordx4 v[148:151], v75, s[8:9]
	s_add_u32 s8, s8, 0x8000
	s_addc_u32 s9, s9, 0
	global_load_dwordx4 v[152:155], v75, s[8:9]
	s_add_u32 s8, s8, 0x8000
	s_addc_u32 s9, s9, 0
	global_load_dwordx4 v[156:159], v75, s[8:9]
	s_add_u32 s8, s8, 0x8000
	s_addc_u32 s9, s9, 0
	global_load_dwordx4 v[160:163], v75, s[8:9]
	s_add_u32 s8, s8, 0x8000
	s_addc_u32 s9, s9, 0
	global_load_dwordx4 v[164:167], v75, s[8:9]
	s_add_u32 s8, s8, 0x8000
	s_addc_u32 s9, s9, 0
	global_load_dwordx4 v[168:171], v75, s[8:9]
	s_add_u32 s8, s8, 0x8000
	s_addc_u32 s9, s9, 0
	global_load_dwordx4 v[172:175], v75, s[8:9]
	s_add_u32 s6, s40, 0x2002000
	s_addc_u32 s7, s41, 0
	ds_read_b32 v226, v211
	ds_read_b32 v227, v211 offset:512
	ds_read_b32 v228, v211 offset:1024
	ds_read_b32 v229, v211 offset:1536
	ds_read_b32 v230, v211 offset:2048
	ds_read_b32 v231, v211 offset:2560
	ds_read_b32 v232, v211 offset:3072
	ds_read_b32 v233, v211 offset:3584
	ds_read_b32 v234, v211 offset:4096
	ds_read_b32 v235, v211 offset:4608
	ds_read_b32 v236, v211 offset:5120
	ds_read_b32 v237, v211 offset:5632
	ds_read_b32 v238, v211 offset:6144
	ds_read_b32 v239, v211 offset:6656
	ds_read_b32 v240, v211 offset:7168
	ds_read_b32 v241, v211 offset:7680
	s_waitcnt lgkmcnt(0)
	v_max_f32_e32 v226, v226, v226
	v_max_f32_e32 v227, v227, v227
	v_max_f32_e32 v228, v228, v228
	v_max_f32_e32 v229, v229, v229
	v_max_f32_e32 v230, v230, v230
	v_max_f32_e32 v231, v231, v231
	v_max_f32_e32 v232, v232, v232
	v_max_f32_e32 v233, v233, v233
	v_max_f32_e32 v234, v234, v234
	v_max_f32_e32 v235, v235, v235
	v_max_f32_e32 v236, v236, v236
	v_max_f32_e32 v237, v237, v237
	v_max_f32_e32 v238, v238, v238
	v_max_f32_e32 v239, v239, v239
	v_max_f32_e32 v240, v240, v240
	v_max_f32_e32 v241, v241, v241
	v_med3_f32 v226, v226, s62, v95
	v_med3_f32 v227, v227, s62, v95
	v_med3_f32 v228, v228, s62, v95
	v_med3_f32 v229, v229, s62, v95
	v_med3_f32 v230, v230, s62, v95
	v_med3_f32 v231, v231, s62, v95
	v_med3_f32 v232, v232, s62, v95
	v_med3_f32 v233, v233, s62, v95
	v_med3_f32 v234, v234, s62, v95
	v_med3_f32 v235, v235, s62, v95
	v_med3_f32 v236, v236, s62, v95
	v_med3_f32 v237, v237, s62, v95
	v_med3_f32 v238, v238, s62, v95
	v_med3_f32 v239, v239, s62, v95
	v_med3_f32 v240, v240, s62, v95
	v_med3_f32 v241, v241, s62, v95
	v_mov_b32_e32 v242, 0
	v_mov_b32_e32 v243, 0
	v_mov_b32_e32 v244, 0
	v_mov_b32_e32 v245, 0
	v_cvt_pk_fp8_f32 v242, v226, v227
	v_cvt_pk_fp8_f32 v243, v230, v231
	v_cvt_pk_fp8_f32 v244, v234, v235
	v_cvt_pk_fp8_f32 v245, v238, v239
	v_cvt_pk_fp8_f32 v242, v228, v229 op_sel:[0,0,1]
	v_cvt_pk_fp8_f32 v243, v232, v233 op_sel:[0,0,1]
	v_cvt_pk_fp8_f32 v244, v236, v237 op_sel:[0,0,1]
	v_cvt_pk_fp8_f32 v245, v240, v241 op_sel:[0,0,1]
	s_nop 0
	global_store_dwordx4 v79, v[242:245], s[6:7]
	ds_read_b32 v226, v213
	ds_read_b32 v227, v213 offset:512
	ds_read_b32 v228, v213 offset:1024
	ds_read_b32 v229, v213 offset:1536
	ds_read_b32 v230, v213 offset:2048
	ds_read_b32 v231, v213 offset:2560
	ds_read_b32 v232, v213 offset:3072
	ds_read_b32 v233, v213 offset:3584
	ds_read_b32 v234, v213 offset:4096
	ds_read_b32 v235, v213 offset:4608
	ds_read_b32 v236, v213 offset:5120
	ds_read_b32 v237, v213 offset:5632
	ds_read_b32 v238, v213 offset:6144
	ds_read_b32 v239, v213 offset:6656
	ds_read_b32 v240, v213 offset:7168
	ds_read_b32 v241, v213 offset:7680
	s_waitcnt lgkmcnt(0)
	v_max_f32_e32 v226, v226, v226
	v_max_f32_e32 v227, v227, v227
	v_max_f32_e32 v228, v228, v228
	v_max_f32_e32 v229, v229, v229
	v_max_f32_e32 v230, v230, v230
	v_max_f32_e32 v231, v231, v231
	v_max_f32_e32 v232, v232, v232
	v_max_f32_e32 v233, v233, v233
	v_max_f32_e32 v234, v234, v234
	v_max_f32_e32 v235, v235, v235
	v_max_f32_e32 v236, v236, v236
	v_max_f32_e32 v237, v237, v237
	v_max_f32_e32 v238, v238, v238
	v_max_f32_e32 v239, v239, v239
	v_max_f32_e32 v240, v240, v240
	v_max_f32_e32 v241, v241, v241
	v_med3_f32 v226, v226, s62, v95
	v_med3_f32 v227, v227, s62, v95
	v_med3_f32 v228, v228, s62, v95
	v_med3_f32 v229, v229, s62, v95
	v_med3_f32 v230, v230, s62, v95
	v_med3_f32 v231, v231, s62, v95
	v_med3_f32 v232, v232, s62, v95
	v_med3_f32 v233, v233, s62, v95
	v_med3_f32 v234, v234, s62, v95
	v_med3_f32 v235, v235, s62, v95
	v_med3_f32 v236, v236, s62, v95
	v_med3_f32 v237, v237, s62, v95
	v_med3_f32 v238, v238, s62, v95
	v_med3_f32 v239, v239, s62, v95
	v_med3_f32 v240, v240, s62, v95
	v_med3_f32 v241, v241, s62, v95
	v_mov_b32_e32 v242, 0
	v_mov_b32_e32 v243, 0
	v_mov_b32_e32 v244, 0
	v_mov_b32_e32 v245, 0
	v_cvt_pk_fp8_f32 v242, v226, v227
	v_cvt_pk_fp8_f32 v243, v230, v231
	v_cvt_pk_fp8_f32 v244, v234, v235
	v_cvt_pk_fp8_f32 v245, v238, v239
	v_cvt_pk_fp8_f32 v242, v228, v229 op_sel:[0,0,1]
	v_cvt_pk_fp8_f32 v243, v232, v233 op_sel:[0,0,1]
	v_cvt_pk_fp8_f32 v244, v236, v237 op_sel:[0,0,1]
	v_cvt_pk_fp8_f32 v245, v240, v241 op_sel:[0,0,1]
	s_nop 0
	global_store_dwordx4 v80, v[242:245], s[6:7]
	s_waitcnt vmcnt(12)
	v_mul_f32_e32 v176, 0x43000000, v176
	v_mul_f32_e32 v177, 0x43000000, v177
	v_mul_f32_e32 v178, 0x43000000, v178
	v_mul_f32_e32 v179, 0x43000000, v179
	ds_write_b128 v210, v[176:179]
	v_mul_f32_e32 v180, 0x43000000, v180
	v_mul_f32_e32 v181, 0x43000000, v181
	v_mul_f32_e32 v182, 0x43000000, v182
	v_mul_f32_e32 v183, 0x43000000, v183
	ds_write_b128 v210, v[180:183] offset:1024
	v_mul_f32_e32 v184, 0x43000000, v184
	v_mul_f32_e32 v185, 0x43000000, v185
	v_mul_f32_e32 v186, 0x43000000, v186
	v_mul_f32_e32 v187, 0x43000000, v187
	ds_write_b128 v210, v[184:187] offset:2048
	v_mul_f32_e32 v188, 0x43000000, v188
	v_mul_f32_e32 v189, 0x43000000, v189
	v_mul_f32_e32 v190, 0x43000000, v190
	v_mul_f32_e32 v191, 0x43000000, v191
	ds_write_b128 v210, v[188:191] offset:3072
	v_mul_f32_e32 v192, 0x43000000, v192
	v_mul_f32_e32 v193, 0x43000000, v193
	v_mul_f32_e32 v194, 0x43000000, v194
	v_mul_f32_e32 v195, 0x43000000, v195
	ds_write_b128 v210, v[192:195] offset:4096
	v_mul_f32_e32 v196, 0x43000000, v196
	v_mul_f32_e32 v197, 0x43000000, v197
	v_mul_f32_e32 v198, 0x43000000, v198
	v_mul_f32_e32 v199, 0x43000000, v199
	ds_write_b128 v210, v[196:199] offset:5120
	v_mul_f32_e32 v200, 0x43000000, v200
	v_mul_f32_e32 v201, 0x43000000, v201
	v_mul_f32_e32 v202, 0x43000000, v202
	v_mul_f32_e32 v203, 0x43000000, v203
	ds_write_b128 v210, v[200:203] offset:6144
	v_mul_f32_e32 v204, 0x43000000, v204
	v_mul_f32_e32 v205, 0x43000000, v205
	v_mul_f32_e32 v206, 0x43000000, v206
	v_mul_f32_e32 v207, 0x43000000, v207
	ds_write_b128 v210, v[204:207] offset:7168
	s_waitcnt lgkmcnt(0)
	s_barrier
; #define GAS __attribute__((address_space(1)))
; #define LAS __attribute__((address_space(3)))
; #define LDS_WAIT() asm volatile("s_waitcnt lgkmcnt(0)" ::: "memory")
; __device__ __forceinline__ unsigned pk4_fp8(float a, float b, float c, float d) {
;     a = fminf(fmaxf(a, -448.f), 448.f); b = fminf(fmaxf(b, -448.f), 448.f); c = fminf(fmaxf(c, -448.f), 448.f); d = fminf(fmaxf(d, -448.f), 448.f);
;     int w = __builtin_amdgcn_cvt_pk_fp8_f32(a, b, 0, false); w = __builtin_amdgcn_cvt_pk_fp8_f32(c, d, w, true); return (unsigned)w; }
;     const int pr = item >> 1, kb = 2 * (pr / nblk) + (item & 1), nb = pr % nblk, k0 = 64 * kb, n0 = 32 * nb;
;     const int nr = n0 + (lane & 31); const int sc = MAP == 1 ? src_col_in(nr) : nr;
;     float v[32];
; #pragma unroll
;     for (int i = 0; i < 32; ++i) v[i] = sc >= 0 ? W[(size_t)(k0 + 2 * i + (lane >> 5)) * Nsrc + sc] : 0.f;
; #pragma unroll
;     for (int i = 0; i < 32; ++i) { const int k = k0 + 2 * i + (lane >> 5); float x = v[i] * wscale; if (KS) x *= (k < ksplit ? ksA[k] : ksB[k - ksplit]); scr[(2 * i + (lane >> 5)) * 33 + (lane & 31)] = x; }
;     LDS_WAIT(); asm volatile("" ::: "memory");
;     const int c = lane & 7;
; #pragma unroll
;     for (int j = 0; j < 4; ++j) { const int n = (lane >> 3) + 8 * j; const LAS float* s = scr + (8 * c) * 33 + n;
;         const unsigned long long o = (unsigned long long)pg8::pk4_fp8(s[0 * 33], s[1 * 33], s[2 * 33], s[3 * 33]) | ((unsigned long long)pg8::pk4_fp8(s[4 * 33], s[5 * 33], s[6 * 33], s[7 * 33]) << 32);
;         *(GAS unsigned long long*)(WT + (size_t)(n0 + n) * K + k0 + 8 * c) = o; }
;     LDS_WAIT(); asm volatile("" ::: "memory");
; }
	s_add_u32 s8, s38, 0xc001000
	s_addc_u32 s9, s39, 0
	global_load_dwordx4 v[176:179], v75, s[8:9]
	s_add_u32 s8, s8, 0x8000
	s_addc_u32 s9, s9, 0
	global_load_dwordx4 v[180:183], v75, s[8:9]
	s_add_u32 s8, s8, 0x8000
	s_addc_u32 s9, s9, 0
	global_load_dwordx4 v[184:187], v75, s[8:9]
	s_add_u32 s8, s8, 0x8000
	s_addc_u32 s9, s9, 0
	global_load_dwordx4 v[188:191], v75, s[8:9]
	s_add_u32 s8, s8, 0x8000
	s_addc_u32 s9, s9, 0
	global_load_dwordx4 v[192:195], v75, s[8:9]
	s_add_u32 s8, s8, 0x8000
	s_addc_u32 s9, s9, 0
	global_load_dwordx4 v[196:199], v75, s[8:9]
	s_add_u32 s8, s8, 0x8000
	s_addc_u32 s9, s9, 0
	global_load_dwordx4 v[200:203], v75, s[8:9]
	s_add_u32 s8, s8, 0x8000
	s_addc_u32 s9, s9, 0
	global_load_dwordx4 v[204:207], v75, s[8:9]
	s_add_u32 s6, s40, 0x3002000
	s_addc_u32 s7, s41, 0
	ds_read_b32 v226, v212
	ds_read_b32 v227, v212 offset:512
	ds_read_b32 v228, v212 offset:1024
	ds_read_b32 v229, v212 offset:1536
	ds_read_b32 v230, v212 offset:2048
	ds_read_b32 v231, v212 offset:2560
	ds_read_b32 v232, v212 offset:3072
	ds_read_b32 v233, v212 offset:3584
	ds_read_b32 v234, v212 offset:4096
	ds_read_b32 v235, v212 offset:4608
	ds_read_b32 v236, v212 offset:5120
	ds_read_b32 v237, v212 offset:5632
	ds_read_b32 v238, v212 offset:6144
	ds_read_b32 v239, v212 offset:6656
	ds_read_b32 v240, v212 offset:7168
	ds_read_b32 v241, v212 offset:7680
	s_waitcnt lgkmcnt(0)
	v_max_f32_e32 v226, v226, v226
	v_max_f32_e32 v227, v227, v227
	v_max_f32_e32 v228, v228, v228
	v_max_f32_e32 v229, v229, v229
	v_max_f32_e32 v230, v230, v230
	v_max_f32_e32 v231, v231, v231
	v_max_f32_e32 v232, v232, v232
	v_max_f32_e32 v233, v233, v233
	v_max_f32_e32 v234, v234, v234
	v_max_f32_e32 v235, v235, v235
	v_max_f32_e32 v236, v236, v236
	v_max_f32_e32 v237, v237, v237
	v_max_f32_e32 v238, v238, v238
	v_max_f32_e32 v239, v239, v239
	v_max_f32_e32 v240, v240, v240
	v_max_f32_e32 v241, v241, v241
	v_med3_f32 v226, v226, s62, v95
	v_med3_f32 v227, v227, s62, v95
	v_med3_f32 v228, v228, s62, v95
	v_med3_f32 v229, v229, s62, v95
	v_med3_f32 v230, v230, s62, v95
	v_med3_f32 v231, v231, s62, v95
	v_med3_f32 v232, v232, s62, v95
	v_med3_f32 v233, v233, s62, v95
	v_med3_f32 v234, v234, s62, v95
	v_med3_f32 v235, v235, s62, v95
	v_med3_f32 v236, v236, s62, v95
	v_med3_f32 v237, v237, s62, v95
	v_med3_f32 v238, v238, s62, v95
	v_med3_f32 v239, v239, s62, v95
	v_med3_f32 v240, v240, s62, v95
	v_med3_f32 v241, v241, s62, v95
	v_mov_b32_e32 v242, 0
	v_mov_b32_e32 v243, 0
	v_mov_b32_e32 v244, 0
	v_mov_b32_e32 v245, 0
	v_cvt_pk_fp8_f32 v242, v226, v227
	v_cvt_pk_fp8_f32 v243, v230, v231
	v_cvt_pk_fp8_f32 v244, v234, v235
	v_cvt_pk_fp8_f32 v245, v238, v239
	v_cvt_pk_fp8_f32 v242, v228, v229 op_sel:[0,0,1]
	v_cvt_pk_fp8_f32 v243, v232, v233 op_sel:[0,0,1]
	v_cvt_pk_fp8_f32 v244, v236, v237 op_sel:[0,0,1]
	v_cvt_pk_fp8_f32 v245, v240, v241 op_sel:[0,0,1]
	s_nop 0
	global_store_dwordx4 v79, v[242:245], s[6:7]
	ds_read_b32 v226, v214
	ds_read_b32 v227, v214 offset:512
	ds_read_b32 v228, v214 offset:1024
	ds_read_b32 v229, v214 offset:1536
	ds_read_b32 v230, v214 offset:2048
	ds_read_b32 v231, v214 offset:2560
	ds_read_b32 v232, v214 offset:3072
	ds_read_b32 v233, v214 offset:3584
	ds_read_b32 v234, v214 offset:4096
	ds_read_b32 v235, v214 offset:4608
	ds_read_b32 v236, v214 offset:5120
	ds_read_b32 v237, v214 offset:5632
	ds_read_b32 v238, v214 offset:6144
	ds_read_b32 v239, v214 offset:6656
	ds_read_b32 v240, v214 offset:7168
	ds_read_b32 v241, v214 offset:7680
	s_waitcnt lgkmcnt(0)
	v_max_f32_e32 v226, v226, v226
	v_max_f32_e32 v227, v227, v227
	v_max_f32_e32 v228, v228, v228
	v_max_f32_e32 v229, v229, v229
	v_max_f32_e32 v230, v230, v230
	v_max_f32_e32 v231, v231, v231
	v_max_f32_e32 v232, v232, v232
	v_max_f32_e32 v233, v233, v233
	v_max_f32_e32 v234, v234, v234
	v_max_f32_e32 v235, v235, v235
	v_max_f32_e32 v236, v236, v236
	v_max_f32_e32 v237, v237, v237
	v_max_f32_e32 v238, v238, v238
	v_max_f32_e32 v239, v239, v239
	v_max_f32_e32 v240, v240, v240
	v_max_f32_e32 v241, v241, v241
	v_med3_f32 v226, v226, s62, v95
	v_med3_f32 v227, v227, s62, v95
	v_med3_f32 v228, v228, s62, v95
	v_med3_f32 v229, v229, s62, v95
	v_med3_f32 v230, v230, s62, v95
	v_med3_f32 v231, v231, s62, v95
	v_med3_f32 v232, v232, s62, v95
	v_med3_f32 v233, v233, s62, v95
	v_med3_f32 v234, v234, s62, v95
	v_med3_f32 v235, v235, s62, v95
	v_med3_f32 v236, v236, s62, v95
	v_med3_f32 v237, v237, s62, v95
	v_med3_f32 v238, v238, s62, v95
	v_med3_f32 v239, v239, s62, v95
	v_med3_f32 v240, v240, s62, v95
	v_med3_f32 v241, v241, s62, v95
	v_mov_b32_e32 v242, 0
	v_mov_b32_e32 v243, 0
	v_mov_b32_e32 v244, 0
	v_mov_b32_e32 v245, 0
	v_cvt_pk_fp8_f32 v242, v226, v227
	v_cvt_pk_fp8_f32 v243, v230, v231
	v_cvt_pk_fp8_f32 v244, v234, v235
	v_cvt_pk_fp8_f32 v245, v238, v239
	v_cvt_pk_fp8_f32 v242, v228, v229 op_sel:[0,0,1]
	v_cvt_pk_fp8_f32 v243, v232, v233 op_sel:[0,0,1]
	v_cvt_pk_fp8_f32 v244, v236, v237 op_sel:[0,0,1]
	v_cvt_pk_fp8_f32 v245, v240, v241 op_sel:[0,0,1]
	s_nop 0
	global_store_dwordx4 v80, v[242:245], s[6:7]
	s_waitcnt vmcnt(12)
	v_mul_f32_e32 v144, 0x43000000, v144
	v_mul_f32_e32 v145, 0x43000000, v145
	v_mul_f32_e32 v146, 0x43000000, v146
	v_mul_f32_e32 v147, 0x43000000, v147
	ds_write_b128 v209, v[144:147]
	v_mul_f32_e32 v148, 0x43000000, v148
	v_mul_f32_e32 v149, 0x43000000, v149
	v_mul_f32_e32 v150, 0x43000000, v150
	v_mul_f32_e32 v151, 0x43000000, v151
	ds_write_b128 v209, v[148:151] offset:1024
	v_mul_f32_e32 v152, 0x43000000, v152
	v_mul_f32_e32 v153, 0x43000000, v153
	v_mul_f32_e32 v154, 0x43000000, v154
	v_mul_f32_e32 v155, 0x43000000, v155
	ds_write_b128 v209, v[152:155] offset:2048
	v_mul_f32_e32 v156, 0x43000000, v156
	v_mul_f32_e32 v157, 0x43000000, v157
	v_mul_f32_e32 v158, 0x43000000, v158
	v_mul_f32_e32 v159, 0x43000000, v159
	ds_write_b128 v209, v[156:159] offset:3072
	v_mul_f32_e32 v160, 0x43000000, v160
	v_mul_f32_e32 v161, 0x43000000, v161
	v_mul_f32_e32 v162, 0x43000000, v162
	v_mul_f32_e32 v163, 0x43000000, v163
	ds_write_b128 v209, v[160:163] offset:4096
	v_mul_f32_e32 v164, 0x43000000, v164
	v_mul_f32_e32 v165, 0x43000000, v165
	v_mul_f32_e32 v166, 0x43000000, v166
	v_mul_f32_e32 v167, 0x43000000, v167
	ds_write_b128 v209, v[164:167] offset:5120
	v_mul_f32_e32 v168, 0x43000000, v168
	v_mul_f32_e32 v169, 0x43000000, v169
	v_mul_f32_e32 v170, 0x43000000, v170
	v_mul_f32_e32 v171, 0x43000000, v171
	ds_write_b128 v209, v[168:171] offset:6144
	v_mul_f32_e32 v172, 0x43000000, v172
	v_mul_f32_e32 v173, 0x43000000, v173
	v_mul_f32_e32 v174, 0x43000000, v174
	v_mul_f32_e32 v175, 0x43000000, v175
	ds_write_b128 v209, v[172:175] offset:7168
	s_waitcnt lgkmcnt(0)
	s_barrier
; #define GAS __attribute__((address_space(1)))
; #define LAS __attribute__((address_space(3)))
; #define LDS_WAIT() asm volatile("s_waitcnt lgkmcnt(0)" ::: "memory")
; __device__ __forceinline__ unsigned pk4_fp8(float a, float b, float c, float d) {
;     a = fminf(fmaxf(a, -448.f), 448.f); b = fminf(fmaxf(b, -448.f), 448.f); c = fminf(fmaxf(c, -448.f), 448.f); d = fminf(fmaxf(d, -448.f), 448.f);
;     int w = __builtin_amdgcn_cvt_pk_fp8_f32(a, b, 0, false); w = __builtin_amdgcn_cvt_pk_fp8_f32(c, d, w, true); return (unsigned)w; }
;     const int pr = item >> 1, kb = 2 * (pr / nblk) + (item & 1), nb = pr % nblk, k0 = 64 * kb, n0 = 32 * nb;
;     const int nr = n0 + (lane & 31); const int sc = MAP == 1 ? src_col_in(nr) : nr;
;     float v[32];
; #pragma unroll
;     for (int i = 0; i < 32; ++i) v[i] = sc >= 0 ? W[(size_t)(k0 + 2 * i + (lane >> 5)) * Nsrc + sc] : 0.f;
; #pragma unroll
;     for (int i = 0; i < 32; ++i) { const int k = k0 + 2 * i + (lane >> 5); float x = v[i] * wscale; if (KS) x *= (k < ksplit ? ksA[k] : ksB[k - ksplit]); scr[(2 * i + (lane >> 5)) * 33 + (lane & 31)] = x; }
;     LDS_WAIT(); asm volatile("" ::: "memory");
;     const int c = lane & 7;
; #pragma unroll
;     for (int j = 0; j < 4; ++j) { const int n = (lane >> 3) + 8 * j; const LAS float* s = scr + (8 * c) * 33 + n;
;         const unsigned long long o = (unsigned long long)pg8::pk4_fp8(s[0 * 33], s[1 * 33], s[2 * 33], s[3 * 33]) | ((unsigned long long)pg8::pk4_fp8(s[4 * 33], s[5 * 33], s[6 * 33], s[7 * 33]) << 32);
;         *(GAS unsigned long long*)(WT + (size_t)(n0 + n) * K + k0 + 8 * c) = o; }
;     LDS_WAIT(); asm volatile("" ::: "memory");
; }
	s_add_u32 s8, s38, 0xc002000
	s_addc_u32 s9, s39, 0
	global_load_dwordx4 v[144:147], v75, s[8:9]
	s_add_u32 s8, s8, 0x8000
	s_addc_u32 s9, s9, 0
	global_load_dwordx4 v[148:151], v75, s[8:9]
	s_add_u32 s8, s8, 0x8000
	s_addc_u32 s9, s9, 0
	global_load_dwordx4 v[152:155], v75, s[8:9]
	s_add_u32 s8, s8, 0x8000
	s_addc_u32 s9, s9, 0
	global_load_dwordx4 v[156:159], v75, s[8:9]
	s_add_u32 s8, s8, 0x8000
	s_addc_u32 s9, s9, 0
	global_load_dwordx4 v[160:163], v75, s[8:9]
	s_add_u32 s8, s8, 0x8000
	s_addc_u32 s9, s9, 0
	global_load_dwordx4 v[164:167], v75, s[8:9]
	s_add_u32 s8, s8, 0x8000
	s_addc_u32 s9, s9, 0
	global_load_dwordx4 v[168:171], v75, s[8:9]
	s_add_u32 s8, s8, 0x8000
	s_addc_u32 s9, s9, 0
	global_load_dwordx4 v[172:175], v75, s[8:9]
	s_add_u32 s6, s40, 0x3000
	s_addc_u32 s7, s41, 0
	ds_read_b32 v226, v211
	ds_read_b32 v227, v211 offset:512
	ds_read_b32 v228, v211 offset:1024
	ds_read_b32 v229, v211 offset:1536
	ds_read_b32 v230, v211 offset:2048
	ds_read_b32 v231, v211 offset:2560
	ds_read_b32 v232, v211 offset:3072
	ds_read_b32 v233, v211 offset:3584
	ds_read_b32 v234, v211 offset:4096
	ds_read_b32 v235, v211 offset:4608
	ds_read_b32 v236, v211 offset:5120
	ds_read_b32 v237, v211 offset:5632
	ds_read_b32 v238, v211 offset:6144
	ds_read_b32 v239, v211 offset:6656
	ds_read_b32 v240, v211 offset:7168
	ds_read_b32 v241, v211 offset:7680
	s_waitcnt lgkmcnt(0)
	v_max_f32_e32 v226, v226, v226
	v_max_f32_e32 v227, v227, v227
	v_max_f32_e32 v228, v228, v228
	v_max_f32_e32 v229, v229, v229
	v_max_f32_e32 v230, v230, v230
	v_max_f32_e32 v231, v231, v231
	v_max_f32_e32 v232, v232, v232
	v_max_f32_e32 v233, v233, v233
	v_max_f32_e32 v234, v234, v234
	v_max_f32_e32 v235, v235, v235
	v_max_f32_e32 v236, v236, v236
	v_max_f32_e32 v237, v237, v237
	v_max_f32_e32 v238, v238, v238
	v_max_f32_e32 v239, v239, v239
	v_max_f32_e32 v240, v240, v240
	v_max_f32_e32 v241, v241, v241
	v_med3_f32 v226, v226, s62, v95
	v_med3_f32 v227, v227, s62, v95
	v_med3_f32 v228, v228, s62, v95
	v_med3_f32 v229, v229, s62, v95
	v_med3_f32 v230, v230, s62, v95
	v_med3_f32 v231, v231, s62, v95
	v_med3_f32 v232, v232, s62, v95
	v_med3_f32 v233, v233, s62, v95
	v_med3_f32 v234, v234, s62, v95
	v_med3_f32 v235, v235, s62, v95
	v_med3_f32 v236, v236, s62, v95
	v_med3_f32 v237, v237, s62, v95
	v_med3_f32 v238, v238, s62, v95
	v_med3_f32 v239, v239, s62, v95
	v_med3_f32 v240, v240, s62, v95
	v_med3_f32 v241, v241, s62, v95
	v_mov_b32_e32 v242, 0
	v_mov_b32_e32 v243, 0
	v_mov_b32_e32 v244, 0
	v_mov_b32_e32 v245, 0
	v_cvt_pk_fp8_f32 v242, v226, v227
	v_cvt_pk_fp8_f32 v243, v230, v231
	v_cvt_pk_fp8_f32 v244, v234, v235
	v_cvt_pk_fp8_f32 v245, v238, v239
	v_cvt_pk_fp8_f32 v242, v228, v229 op_sel:[0,0,1]
	v_cvt_pk_fp8_f32 v243, v232, v233 op_sel:[0,0,1]
	v_cvt_pk_fp8_f32 v244, v236, v237 op_sel:[0,0,1]
	v_cvt_pk_fp8_f32 v245, v240, v241 op_sel:[0,0,1]
	s_nop 0
	global_store_dwordx4 v79, v[242:245], s[6:7]
	ds_read_b32 v226, v213
	ds_read_b32 v227, v213 offset:512
	ds_read_b32 v228, v213 offset:1024
	ds_read_b32 v229, v213 offset:1536
	ds_read_b32 v230, v213 offset:2048
	ds_read_b32 v231, v213 offset:2560
	ds_read_b32 v232, v213 offset:3072
	ds_read_b32 v233, v213 offset:3584
	ds_read_b32 v234, v213 offset:4096
	ds_read_b32 v235, v213 offset:4608
	ds_read_b32 v236, v213 offset:5120
	ds_read_b32 v237, v213 offset:5632
	ds_read_b32 v238, v213 offset:6144
	ds_read_b32 v239, v213 offset:6656
	ds_read_b32 v240, v213 offset:7168
	ds_read_b32 v241, v213 offset:7680
	s_waitcnt lgkmcnt(0)
	v_max_f32_e32 v226, v226, v226
	v_max_f32_e32 v227, v227, v227
	v_max_f32_e32 v228, v228, v228
	v_max_f32_e32 v229, v229, v229
	v_max_f32_e32 v230, v230, v230
	v_max_f32_e32 v231, v231, v231
	v_max_f32_e32 v232, v232, v232
	v_max_f32_e32 v233, v233, v233
	v_max_f32_e32 v234, v234, v234
	v_max_f32_e32 v235, v235, v235
	v_max_f32_e32 v236, v236, v236
	v_max_f32_e32 v237, v237, v237
	v_max_f32_e32 v238, v238, v238
	v_max_f32_e32 v239, v239, v239
	v_max_f32_e32 v240, v240, v240
	v_max_f32_e32 v241, v241, v241
	v_med3_f32 v226, v226, s62, v95
	v_med3_f32 v227, v227, s62, v95
	v_med3_f32 v228, v228, s62, v95
	v_med3_f32 v229, v229, s62, v95
	v_med3_f32 v230, v230, s62, v95
	v_med3_f32 v231, v231, s62, v95
	v_med3_f32 v232, v232, s62, v95
	v_med3_f32 v233, v233, s62, v95
	v_med3_f32 v234, v234, s62, v95
	v_med3_f32 v235, v235, s62, v95
	v_med3_f32 v236, v236, s62, v95
	v_med3_f32 v237, v237, s62, v95
	v_med3_f32 v238, v238, s62, v95
	v_med3_f32 v239, v239, s62, v95
	v_med3_f32 v240, v240, s62, v95
	v_med3_f32 v241, v241, s62, v95
	v_mov_b32_e32 v242, 0
	v_mov_b32_e32 v243, 0
	v_mov_b32_e32 v244, 0
	v_mov_b32_e32 v245, 0
	v_cvt_pk_fp8_f32 v242, v226, v227
	v_cvt_pk_fp8_f32 v243, v230, v231
	v_cvt_pk_fp8_f32 v244, v234, v235
	v_cvt_pk_fp8_f32 v245, v238, v239
	v_cvt_pk_fp8_f32 v242, v228, v229 op_sel:[0,0,1]
	v_cvt_pk_fp8_f32 v243, v232, v233 op_sel:[0,0,1]
	v_cvt_pk_fp8_f32 v244, v236, v237 op_sel:[0,0,1]
	v_cvt_pk_fp8_f32 v245, v240, v241 op_sel:[0,0,1]
	s_nop 0
	global_store_dwordx4 v80, v[242:245], s[6:7]
	s_branch .Lco3_hop_skip

; #define GAS __attribute__((address_space(1)))
; #define LAS __attribute__((address_space(3)))
; #define LDS_WAIT() asm volatile("s_waitcnt lgkmcnt(0)" ::: "memory")
; __device__ __forceinline__ unsigned pk4_fp8(float a, float b, float c, float d) {
;     a = fminf(fmaxf(a, -448.f), 448.f); b = fminf(fmaxf(b, -448.f), 448.f); c = fminf(fmaxf(c, -448.f), 448.f); d = fminf(fmaxf(d, -448.f), 448.f);
;     int w = __builtin_amdgcn_cvt_pk_fp8_f32(a, b, 0, false); w = __builtin_amdgcn_cvt_pk_fp8_f32(c, d, w, true); return (unsigned)w; }
;     const int pr = item >> 1, kb = 2 * (pr / nblk) + (item & 1), nb = pr % nblk, k0 = 64 * kb, n0 = 32 * nb;
;     const int nr = n0 + (lane & 31); const int sc = MAP == 1 ? src_col_in(nr) : nr;
;     float v[32];
; #pragma unroll
;     for (int i = 0; i < 32; ++i) v[i] = sc >= 0 ? W[(size_t)(k0 + 2 * i + (lane >> 5)) * Nsrc + sc] : 0.f;
; #pragma unroll
;     for (int i = 0; i < 32; ++i) { const int k = k0 + 2 * i + (lane >> 5); float x = v[i] * wscale; if (KS) x *= (k < ksplit ? ksA[k] : ksB[k - ksplit]); scr[(2 * i + (lane >> 5)) * 33 + (lane & 31)] = x; }
;     LDS_WAIT(); asm volatile("" ::: "memory");
;     const int c = lane & 7;
; #pragma unroll
;     for (int j = 0; j < 4; ++j) { const int n = (lane >> 3) + 8 * j; const LAS float* s = scr + (8 * c) * 33 + n;
;         const unsigned long long o = (unsigned long long)pg8::pk4_fp8(s[0 * 33], s[1 * 33], s[2 * 33], s[3 * 33]) | ((unsigned long long)pg8::pk4_fp8(s[4 * 33], s[5 * 33], s[6 * 33], s[7 * 33]) << 32);
;         *(GAS unsigned long long*)(WT + (size_t)(n0 + n) * K + k0 + 8 * c) = o; }
;     LDS_WAIT(); asm volatile("" ::: "memory");
; }
.Lco3_hop_skip:
	s_waitcnt vmcnt(12)
	v_mul_f32_e32 v176, 0x43000000, v176
	v_mul_f32_e32 v177, 0x43000000, v177
	v_mul_f32_e32 v178, 0x43000000, v178
	v_mul_f32_e32 v179, 0x43000000, v179
	ds_write_b128 v210, v[176:179]
	v_mul_f32_e32 v180, 0x43000000, v180
	v_mul_f32_e32 v181, 0x43000000, v181
	v_mul_f32_e32 v182, 0x43000000, v182
	v_mul_f32_e32 v183, 0x43000000, v183
	ds_write_b128 v210, v[180:183] offset:1024
	v_mul_f32_e32 v184, 0x43000000, v184
	v_mul_f32_e32 v185, 0x43000000, v185
	v_mul_f32_e32 v186, 0x43000000, v186
	v_mul_f32_e32 v187, 0x43000000, v187
	ds_write_b128 v210, v[184:187] offset:2048
	v_mul_f32_e32 v188, 0x43000000, v188
	v_mul_f32_e32 v189, 0x43000000, v189
	v_mul_f32_e32 v190, 0x43000000, v190
	v_mul_f32_e32 v191, 0x43000000, v191
	ds_write_b128 v210, v[188:191] offset:3072
	v_mul_f32_e32 v192, 0x43000000, v192
	v_mul_f32_e32 v193, 0x43000000, v193
	v_mul_f32_e32 v194, 0x43000000, v194
	v_mul_f32_e32 v195, 0x43000000, v195
	ds_write_b128 v210, v[192:195] offset:4096
	v_mul_f32_e32 v196, 0x43000000, v196
	v_mul_f32_e32 v197, 0x43000000, v197
	v_mul_f32_e32 v198, 0x43000000, v198
	v_mul_f32_e32 v199, 0x43000000, v199
	ds_write_b128 v210, v[196:199] offset:5120
	v_mul_f32_e32 v200, 0x43000000, v200
	v_mul_f32_e32 v201, 0x43000000, v201
	v_mul_f32_e32 v202, 0x43000000, v202
	v_mul_f32_e32 v203, 0x43000000, v203
	ds_write_b128 v210, v[200:203] offset:6144
	v_mul_f32_e32 v204, 0x43000000, v204
	v_mul_f32_e32 v205, 0x43000000, v205
	v_mul_f32_e32 v206, 0x43000000, v206
	v_mul_f32_e32 v207, 0x43000000, v207
	ds_write_b128 v210, v[204:207] offset:7168
	s_waitcnt lgkmcnt(0)
	s_barrier
	s_add_u32 s8, s38, 0xc003000
	s_addc_u32 s9, s39, 0
	global_load_dwordx4 v[176:179], v75, s[8:9]
	s_add_u32 s8, s8, 0x8000
	s_addc_u32 s9, s9, 0
	global_load_dwordx4 v[180:183], v75, s[8:9]
	s_add_u32 s8, s8, 0x8000
	s_addc_u32 s9, s9, 0
	global_load_dwordx4 v[184:187], v75, s[8:9]
	s_add_u32 s8, s8, 0x8000
	s_addc_u32 s9, s9, 0
	global_load_dwordx4 v[188:191], v75, s[8:9]
	s_add_u32 s8, s8, 0x8000
	s_addc_u32 s9, s9, 0
	global_load_dwordx4 v[192:195], v75, s[8:9]
	s_add_u32 s8, s8, 0x8000
	s_addc_u32 s9, s9, 0
	global_load_dwordx4 v[196:199], v75, s[8:9]
	s_add_u32 s8, s8, 0x8000
	s_addc_u32 s9, s9, 0
	global_load_dwordx4 v[200:203], v75, s[8:9]
	s_add_u32 s8, s8, 0x8000
	s_addc_u32 s9, s9, 0
	global_load_dwordx4 v[204:207], v75, s[8:9]
	s_add_u32 s6, s40, 0x1003000
	s_addc_u32 s7, s41, 0
	ds_read_b32 v226, v212
	ds_read_b32 v227, v212 offset:512
	ds_read_b32 v228, v212 offset:1024
	ds_read_b32 v229, v212 offset:1536
	ds_read_b32 v230, v212 offset:2048
	ds_read_b32 v231, v212 offset:2560
	ds_read_b32 v232, v212 offset:3072
	ds_read_b32 v233, v212 offset:3584
	ds_read_b32 v234, v212 offset:4096
	ds_read_b32 v235, v212 offset:4608
	ds_read_b32 v236, v212 offset:5120
	ds_read_b32 v237, v212 offset:5632
	ds_read_b32 v238, v212 offset:6144
	ds_read_b32 v239, v212 offset:6656
	ds_read_b32 v240, v212 offset:7168
	ds_read_b32 v241, v212 offset:7680
	s_waitcnt lgkmcnt(0)
	v_max_f32_e32 v226, v226, v226
	v_max_f32_e32 v227, v227, v227
	v_max_f32_e32 v228, v228, v228
	v_max_f32_e32 v229, v229, v229
	v_max_f32_e32 v230, v230, v230
	v_max_f32_e32 v231, v231, v231
	v_max_f32_e32 v232, v232, v232
	v_max_f32_e32 v233, v233, v233
	v_max_f32_e32 v234, v234, v234
	v_max_f32_e32 v235, v235, v235
	v_max_f32_e32 v236, v236, v236
	v_max_f32_e32 v237, v237, v237
	v_max_f32_e32 v238, v238, v238
	v_max_f32_e32 v239, v239, v239
	v_max_f32_e32 v240, v240, v240
	v_max_f32_e32 v241, v241, v241
	v_med3_f32 v226, v226, s62, v95
	v_med3_f32 v227, v227, s62, v95
	v_med3_f32 v228, v228, s62, v95
	v_med3_f32 v229, v229, s62, v95
	v_med3_f32 v230, v230, s62, v95
	v_med3_f32 v231, v231, s62, v95
	v_med3_f32 v232, v232, s62, v95
	v_med3_f32 v233, v233, s62, v95
	v_med3_f32 v234, v234, s62, v95
	v_med3_f32 v235, v235, s62, v95
	v_med3_f32 v236, v236, s62, v95
	v_med3_f32 v237, v237, s62, v95
	v_med3_f32 v238, v238, s62, v95
	v_med3_f32 v239, v239, s62, v95
	v_med3_f32 v240, v240, s62, v95
	v_med3_f32 v241, v241, s62, v95
	v_mov_b32_e32 v242, 0
	v_mov_b32_e32 v243, 0
	v_mov_b32_e32 v244, 0
	v_mov_b32_e32 v245, 0
	v_cvt_pk_fp8_f32 v242, v226, v227
	v_cvt_pk_fp8_f32 v243, v230, v231
	v_cvt_pk_fp8_f32 v244, v234, v235
	v_cvt_pk_fp8_f32 v245, v238, v239
	v_cvt_pk_fp8_f32 v242, v228, v229 op_sel:[0,0,1]
	v_cvt_pk_fp8_f32 v243, v232, v233 op_sel:[0,0,1]
	v_cvt_pk_fp8_f32 v244, v236, v237 op_sel:[0,0,1]
	v_cvt_pk_fp8_f32 v245, v240, v241 op_sel:[0,0,1]
	s_nop 0
	global_store_dwordx4 v79, v[242:245], s[6:7]
	ds_read_b32 v226, v214
	ds_read_b32 v227, v214 offset:512
	ds_read_b32 v228, v214 offset:1024
	ds_read_b32 v229, v214 offset:1536
	ds_read_b32 v230, v214 offset:2048
	ds_read_b32 v231, v214 offset:2560
	ds_read_b32 v232, v214 offset:3072
	ds_read_b32 v233, v214 offset:3584
	ds_read_b32 v234, v214 offset:4096
	ds_read_b32 v235, v214 offset:4608
	ds_read_b32 v236, v214 offset:5120
	ds_read_b32 v237, v214 offset:5632
	ds_read_b32 v238, v214 offset:6144
	ds_read_b32 v239, v214 offset:6656
	ds_read_b32 v240, v214 offset:7168
	ds_read_b32 v241, v214 offset:7680
	s_waitcnt lgkmcnt(0)
; #define GAS __attribute__((address_space(1)))
; #define LAS __attribute__((address_space(3)))
; #define LDS_WAIT() asm volatile("s_waitcnt lgkmcnt(0)" ::: "memory")
; __device__ __forceinline__ unsigned pk4_fp8(float a, float b, float c, float d) {
;     a = fminf(fmaxf(a, -448.f), 448.f); b = fminf(fmaxf(b, -448.f), 448.f); c = fminf(fmaxf(c, -448.f), 448.f); d = fminf(fmaxf(d, -448.f), 448.f);
;     int w = __builtin_amdgcn_cvt_pk_fp8_f32(a, b, 0, false); w = __builtin_amdgcn_cvt_pk_fp8_f32(c, d, w, true); return (unsigned)w; }
;     const int pr = item >> 1, kb = 2 * (pr / nblk) + (item & 1), nb = pr % nblk, k0 = 64 * kb, n0 = 32 * nb;
;     const int nr = n0 + (lane & 31); const int sc = MAP == 1 ? src_col_in(nr) : nr;
;     float v[32];
; #pragma unroll
;     for (int i = 0; i < 32; ++i) v[i] = sc >= 0 ? W[(size_t)(k0 + 2 * i + (lane >> 5)) * Nsrc + sc] : 0.f;
; #pragma unroll
;     for (int i = 0; i < 32; ++i) { const int k = k0 + 2 * i + (lane >> 5); float x = v[i] * wscale; if (KS) x *= (k < ksplit ? ksA[k] : ksB[k - ksplit]); scr[(2 * i + (lane >> 5)) * 33 + (lane & 31)] = x; }
;     LDS_WAIT(); asm volatile("" ::: "memory");
;     const int c = lane & 7;
; #pragma unroll
;     for (int j = 0; j < 4; ++j) { const int n = (lane >> 3) + 8 * j; const LAS float* s = scr + (8 * c) * 33 + n;
;         const unsigned long long o = (unsigned long long)pg8::pk4_fp8(s[0 * 33], s[1 * 33], s[2 * 33], s[3 * 33]) | ((unsigned long long)pg8::pk4_fp8(s[4 * 33], s[5 * 33], s[6 * 33], s[7 * 33]) << 32);
;         *(GAS unsigned long long*)(WT + (size_t)(n0 + n) * K + k0 + 8 * c) = o; }
;     LDS_WAIT(); asm volatile("" ::: "memory");
; }
	v_max_f32_e32 v226, v226, v226
	v_max_f32_e32 v227, v227, v227
	v_max_f32_e32 v228, v228, v228
	v_max_f32_e32 v229, v229, v229
	v_max_f32_e32 v230, v230, v230
	v_max_f32_e32 v231, v231, v231
	v_max_f32_e32 v232, v232, v232
	v_max_f32_e32 v233, v233, v233
	v_max_f32_e32 v234, v234, v234
	v_max_f32_e32 v235, v235, v235
	v_max_f32_e32 v236, v236, v236
	v_max_f32_e32 v237, v237, v237
	v_max_f32_e32 v238, v238, v238
	v_max_f32_e32 v239, v239, v239
	v_max_f32_e32 v240, v240, v240
	v_max_f32_e32 v241, v241, v241
	v_med3_f32 v226, v226, s62, v95
	v_med3_f32 v227, v227, s62, v95
	v_med3_f32 v228, v228, s62, v95
	v_med3_f32 v229, v229, s62, v95
	v_med3_f32 v230, v230, s62, v95
	v_med3_f32 v231, v231, s62, v95
	v_med3_f32 v232, v232, s62, v95
	v_med3_f32 v233, v233, s62, v95
	v_med3_f32 v234, v234, s62, v95
	v_med3_f32 v235, v235, s62, v95
	v_med3_f32 v236, v236, s62, v95
	v_med3_f32 v237, v237, s62, v95
	v_med3_f32 v238, v238, s62, v95
	v_med3_f32 v239, v239, s62, v95
	v_med3_f32 v240, v240, s62, v95
	v_med3_f32 v241, v241, s62, v95
	v_mov_b32_e32 v242, 0
	v_mov_b32_e32 v243, 0
	v_mov_b32_e32 v244, 0
	v_mov_b32_e32 v245, 0
	v_cvt_pk_fp8_f32 v242, v226, v227
	v_cvt_pk_fp8_f32 v243, v230, v231
	v_cvt_pk_fp8_f32 v244, v234, v235
	v_cvt_pk_fp8_f32 v245, v238, v239
	v_cvt_pk_fp8_f32 v242, v228, v229 op_sel:[0,0,1]
	v_cvt_pk_fp8_f32 v243, v232, v233 op_sel:[0,0,1]
	v_cvt_pk_fp8_f32 v244, v236, v237 op_sel:[0,0,1]
	v_cvt_pk_fp8_f32 v245, v240, v241 op_sel:[0,0,1]
	s_nop 0
	global_store_dwordx4 v80, v[242:245], s[6:7]
	s_waitcnt vmcnt(12)
	v_mul_f32_e32 v144, 0x43000000, v144
	v_mul_f32_e32 v145, 0x43000000, v145
	v_mul_f32_e32 v146, 0x43000000, v146
	v_mul_f32_e32 v147, 0x43000000, v147
	ds_write_b128 v209, v[144:147]
	v_mul_f32_e32 v148, 0x43000000, v148
	v_mul_f32_e32 v149, 0x43000000, v149
	v_mul_f32_e32 v150, 0x43000000, v150
	v_mul_f32_e32 v151, 0x43000000, v151
	ds_write_b128 v209, v[148:151] offset:1024
	v_mul_f32_e32 v152, 0x43000000, v152
	v_mul_f32_e32 v153, 0x43000000, v153
	v_mul_f32_e32 v154, 0x43000000, v154
	v_mul_f32_e32 v155, 0x43000000, v155
	ds_write_b128 v209, v[152:155] offset:2048
	v_mul_f32_e32 v156, 0x43000000, v156
	v_mul_f32_e32 v157, 0x43000000, v157
	v_mul_f32_e32 v158, 0x43000000, v158
	v_mul_f32_e32 v159, 0x43000000, v159
	ds_write_b128 v209, v[156:159] offset:3072
	v_mul_f32_e32 v160, 0x43000000, v160
	v_mul_f32_e32 v161, 0x43000000, v161
	v_mul_f32_e32 v162, 0x43000000, v162
	v_mul_f32_e32 v163, 0x43000000, v163
	ds_write_b128 v209, v[160:163] offset:4096
	v_mul_f32_e32 v164, 0x43000000, v164
	v_mul_f32_e32 v165, 0x43000000, v165
	v_mul_f32_e32 v166, 0x43000000, v166
	v_mul_f32_e32 v167, 0x43000000, v167
	ds_write_b128 v209, v[164:167] offset:5120
	v_mul_f32_e32 v168, 0x43000000, v168
	v_mul_f32_e32 v169, 0x43000000, v169
	v_mul_f32_e32 v170, 0x43000000, v170
	v_mul_f32_e32 v171, 0x43000000, v171
	ds_write_b128 v209, v[168:171] offset:6144
	v_mul_f32_e32 v172, 0x43000000, v172
	v_mul_f32_e32 v173, 0x43000000, v173
	v_mul_f32_e32 v174, 0x43000000, v174
	v_mul_f32_e32 v175, 0x43000000, v175
	ds_write_b128 v209, v[172:175] offset:7168
	s_waitcnt lgkmcnt(0)
	s_barrier
	s_mov_b64 s[8:9], s[42:43]
	global_load_dwordx4 v[144:147], v75, s[8:9]
	s_add_u32 s8, s8, 0x8000
	s_addc_u32 s9, s9, 0
	global_load_dwordx4 v[148:151], v75, s[8:9]
	s_add_u32 s8, s8, 0x8000
	s_addc_u32 s9, s9, 0
	global_load_dwordx4 v[152:155], v75, s[8:9]
	s_add_u32 s8, s8, 0x8000
	s_addc_u32 s9, s9, 0
	global_load_dwordx4 v[156:159], v75, s[8:9]
	s_add_u32 s8, s8, 0x8000
	s_addc_u32 s9, s9, 0
	global_load_dwordx4 v[160:163], v75, s[8:9]
	s_add_u32 s8, s8, 0x8000
	s_addc_u32 s9, s9, 0
	global_load_dwordx4 v[164:167], v75, s[8:9]
	s_add_u32 s8, s8, 0x8000
	s_addc_u32 s9, s9, 0
	global_load_dwordx4 v[168:171], v75, s[8:9]
	s_add_u32 s8, s8, 0x8000
	s_addc_u32 s9, s9, 0
	global_load_dwordx4 v[172:175], v75, s[8:9]
	s_add_u32 s6, s40, 0x2003000
	s_addc_u32 s7, s41, 0
	ds_read_b32 v226, v211
	ds_read_b32 v227, v211 offset:512
	ds_read_b32 v228, v211 offset:1024
	ds_read_b32 v229, v211 offset:1536
	ds_read_b32 v230, v211 offset:2048
	ds_read_b32 v231, v211 offset:2560
	ds_read_b32 v232, v211 offset:3072
	ds_read_b32 v233, v211 offset:3584
	ds_read_b32 v234, v211 offset:4096
	ds_read_b32 v235, v211 offset:4608
	ds_read_b32 v236, v211 offset:5120
	ds_read_b32 v237, v211 offset:5632
	ds_read_b32 v238, v211 offset:6144
	ds_read_b32 v239, v211 offset:6656
	ds_read_b32 v240, v211 offset:7168
	ds_read_b32 v241, v211 offset:7680
	s_waitcnt lgkmcnt(0)
	v_max_f32_e32 v226, v226, v226
	v_max_f32_e32 v227, v227, v227
	v_max_f32_e32 v228, v228, v228
	v_max_f32_e32 v229, v229, v229
	v_max_f32_e32 v230, v230, v230
	v_max_f32_e32 v231, v231, v231
	v_max_f32_e32 v232, v232, v232
	v_max_f32_e32 v233, v233, v233
	v_max_f32_e32 v234, v234, v234
	v_max_f32_e32 v235, v235, v235
	v_max_f32_e32 v236, v236, v236
	v_max_f32_e32 v237, v237, v237
	v_max_f32_e32 v238, v238, v238
	v_max_f32_e32 v239, v239, v239
	v_max_f32_e32 v240, v240, v240
	v_max_f32_e32 v241, v241, v241
	v_med3_f32 v226, v226, s62, v95
	v_med3_f32 v227, v227, s62, v95
	v_med3_f32 v228, v228, s62, v95
	v_med3_f32 v229, v229, s62, v95
	v_med3_f32 v230, v230, s62, v95
	v_med3_f32 v231, v231, s62, v95
	v_med3_f32 v232, v232, s62, v95
	v_med3_f32 v233, v233, s62, v95
	v_med3_f32 v234, v234, s62, v95
	v_med3_f32 v235, v235, s62, v95
	v_med3_f32 v236, v236, s62, v95
	v_med3_f32 v237, v237, s62, v95
	v_med3_f32 v238, v238, s62, v95
	v_med3_f32 v239, v239, s62, v95
	v_med3_f32 v240, v240, s62, v95
	v_med3_f32 v241, v241, s62, v95
	v_mov_b32_e32 v242, 0
	v_mov_b32_e32 v243, 0
	v_mov_b32_e32 v244, 0
	v_mov_b32_e32 v245, 0
	v_cvt_pk_fp8_f32 v242, v226, v227
	v_cvt_pk_fp8_f32 v243, v230, v231
	v_cvt_pk_fp8_f32 v244, v234, v235
	v_cvt_pk_fp8_f32 v245, v238, v239
	v_cvt_pk_fp8_f32 v242, v228, v229 op_sel:[0,0,1]
	v_cvt_pk_fp8_f32 v243, v232, v233 op_sel:[0,0,1]
	v_cvt_pk_fp8_f32 v244, v236, v237 op_sel:[0,0,1]
	v_cvt_pk_fp8_f32 v245, v240, v241 op_sel:[0,0,1]
	s_nop 0
	global_store_dwordx4 v79, v[242:245], s[6:7]
	ds_read_b32 v226, v213
	ds_read_b32 v227, v213 offset:512
	ds_read_b32 v228, v213 offset:1024
	ds_read_b32 v229, v213 offset:1536
	ds_read_b32 v230, v213 offset:2048
	ds_read_b32 v231, v213 offset:2560
	ds_read_b32 v232, v213 offset:3072
	ds_read_b32 v233, v213 offset:3584
	ds_read_b32 v234, v213 offset:4096
	ds_read_b32 v235, v213 offset:4608
	ds_read_b32 v236, v213 offset:5120
	ds_read_b32 v237, v213 offset:5632
	ds_read_b32 v238, v213 offset:6144
	ds_read_b32 v239, v213 offset:6656
	ds_read_b32 v240, v213 offset:7168
	ds_read_b32 v241, v213 offset:7680
	s_waitcnt lgkmcnt(0)
; #define GAS __attribute__((address_space(1)))
; #define LAS __attribute__((address_space(3)))
; #define LDS_WAIT() asm volatile("s_waitcnt lgkmcnt(0)" ::: "memory")
; __device__ __forceinline__ unsigned pk4_fp8(float a, float b, float c, float d) {
;     a = fminf(fmaxf(a, -448.f), 448.f); b = fminf(fmaxf(b, -448.f), 448.f); c = fminf(fmaxf(c, -448.f), 448.f); d = fminf(fmaxf(d, -448.f), 448.f);
;     int w = __builtin_amdgcn_cvt_pk_fp8_f32(a, b, 0, false); w = __builtin_amdgcn_cvt_pk_fp8_f32(c, d, w, true); return (unsigned)w; }
;     const int pr = item >> 1, kb = 2 * (pr / nblk) + (item & 1), nb = pr % nblk, k0 = 64 * kb, n0 = 32 * nb;
;     const int nr = n0 + (lane & 31); const int sc = MAP == 1 ? src_col_in(nr) : nr;
;     float v[32];
; #pragma unroll
;     for (int i = 0; i < 32; ++i) v[i] = sc >= 0 ? W[(size_t)(k0 + 2 * i + (lane >> 5)) * Nsrc + sc] : 0.f;
; #pragma unroll
;     for (int i = 0; i < 32; ++i) { const int k = k0 + 2 * i + (lane >> 5); float x = v[i] * wscale; if (KS) x *= (k < ksplit ? ksA[k] : ksB[k - ksplit]); scr[(2 * i + (lane >> 5)) * 33 + (lane & 31)] = x; }
;     LDS_WAIT(); asm volatile("" ::: "memory");
;     const int c = lane & 7;
; #pragma unroll
;     for (int j = 0; j < 4; ++j) { const int n = (lane >> 3) + 8 * j; const LAS float* s = scr + (8 * c) * 33 + n;
;         const unsigned long long o = (unsigned long long)pg8::pk4_fp8(s[0 * 33], s[1 * 33], s[2 * 33], s[3 * 33]) | ((unsigned long long)pg8::pk4_fp8(s[4 * 33], s[5 * 33], s[6 * 33], s[7 * 33]) << 32);
;         *(GAS unsigned long long*)(WT + (size_t)(n0 + n) * K + k0 + 8 * c) = o; }
;     LDS_WAIT(); asm volatile("" ::: "memory");
; }
	v_max_f32_e32 v226, v226, v226
	v_max_f32_e32 v227, v227, v227
	v_max_f32_e32 v228, v228, v228
	v_max_f32_e32 v229, v229, v229
	v_max_f32_e32 v230, v230, v230
	v_max_f32_e32 v231, v231, v231
	v_max_f32_e32 v232, v232, v232
	v_max_f32_e32 v233, v233, v233
	v_max_f32_e32 v234, v234, v234
	v_max_f32_e32 v235, v235, v235
	v_max_f32_e32 v236, v236, v236
	v_max_f32_e32 v237, v237, v237
	v_max_f32_e32 v238, v238, v238
	v_max_f32_e32 v239, v239, v239
	v_max_f32_e32 v240, v240, v240
	v_max_f32_e32 v241, v241, v241
	v_med3_f32 v226, v226, s62, v95
	v_med3_f32 v227, v227, s62, v95
	v_med3_f32 v228, v228, s62, v95
	v_med3_f32 v229, v229, s62, v95
	v_med3_f32 v230, v230, s62, v95
	v_med3_f32 v231, v231, s62, v95
	v_med3_f32 v232, v232, s62, v95
	v_med3_f32 v233, v233, s62, v95
	v_med3_f32 v234, v234, s62, v95
	v_med3_f32 v235, v235, s62, v95
	v_med3_f32 v236, v236, s62, v95
	v_med3_f32 v237, v237, s62, v95
	v_med3_f32 v238, v238, s62, v95
	v_med3_f32 v239, v239, s62, v95
	v_med3_f32 v240, v240, s62, v95
	v_med3_f32 v241, v241, s62, v95
	v_mov_b32_e32 v242, 0
	v_mov_b32_e32 v243, 0
	v_mov_b32_e32 v244, 0
	v_mov_b32_e32 v245, 0
	v_cvt_pk_fp8_f32 v242, v226, v227
	v_cvt_pk_fp8_f32 v243, v230, v231
	v_cvt_pk_fp8_f32 v244, v234, v235
	v_cvt_pk_fp8_f32 v245, v238, v239
	v_cvt_pk_fp8_f32 v242, v228, v229 op_sel:[0,0,1]
	v_cvt_pk_fp8_f32 v243, v232, v233 op_sel:[0,0,1]
	v_cvt_pk_fp8_f32 v244, v236, v237 op_sel:[0,0,1]
	v_cvt_pk_fp8_f32 v245, v240, v241 op_sel:[0,0,1]
	s_nop 0
	global_store_dwordx4 v80, v[242:245], s[6:7]
	s_waitcnt vmcnt(12)
	v_mul_f32_e32 v176, 0x43000000, v176
	v_mul_f32_e32 v177, 0x43000000, v177
	v_mul_f32_e32 v178, 0x43000000, v178
	v_mul_f32_e32 v179, 0x43000000, v179
	ds_write_b128 v210, v[176:179]
	v_mul_f32_e32 v180, 0x43000000, v180
	v_mul_f32_e32 v181, 0x43000000, v181
	v_mul_f32_e32 v182, 0x43000000, v182
	v_mul_f32_e32 v183, 0x43000000, v183
	ds_write_b128 v210, v[180:183] offset:1024
	v_mul_f32_e32 v184, 0x43000000, v184
	v_mul_f32_e32 v185, 0x43000000, v185
	v_mul_f32_e32 v186, 0x43000000, v186
	v_mul_f32_e32 v187, 0x43000000, v187
	ds_write_b128 v210, v[184:187] offset:2048
	v_mul_f32_e32 v188, 0x43000000, v188
	v_mul_f32_e32 v189, 0x43000000, v189
	v_mul_f32_e32 v190, 0x43000000, v190
	v_mul_f32_e32 v191, 0x43000000, v191
	ds_write_b128 v210, v[188:191] offset:3072
	v_mul_f32_e32 v192, 0x43000000, v192
	v_mul_f32_e32 v193, 0x43000000, v193
	v_mul_f32_e32 v194, 0x43000000, v194
	v_mul_f32_e32 v195, 0x43000000, v195
	ds_write_b128 v210, v[192:195] offset:4096
	v_mul_f32_e32 v196, 0x43000000, v196
	v_mul_f32_e32 v197, 0x43000000, v197
	v_mul_f32_e32 v198, 0x43000000, v198
	v_mul_f32_e32 v199, 0x43000000, v199
	ds_write_b128 v210, v[196:199] offset:5120
	v_mul_f32_e32 v200, 0x43000000, v200
	v_mul_f32_e32 v201, 0x43000000, v201
	v_mul_f32_e32 v202, 0x43000000, v202
	v_mul_f32_e32 v203, 0x43000000, v203
	ds_write_b128 v210, v[200:203] offset:6144
	v_mul_f32_e32 v204, 0x43000000, v204
	v_mul_f32_e32 v205, 0x43000000, v205
	v_mul_f32_e32 v206, 0x43000000, v206
	v_mul_f32_e32 v207, 0x43000000, v207
	ds_write_b128 v210, v[204:207] offset:7168
	s_waitcnt lgkmcnt(0)
	s_barrier
	s_add_u32 s8, s42, 0x1000
	s_addc_u32 s9, s43, 0
	global_load_dwordx4 v[176:179], v75, s[8:9]
	s_add_u32 s8, s8, 0x8000
	s_addc_u32 s9, s9, 0
	global_load_dwordx4 v[180:183], v75, s[8:9]
	s_add_u32 s8, s8, 0x8000
	s_addc_u32 s9, s9, 0
	global_load_dwordx4 v[184:187], v75, s[8:9]
	s_add_u32 s8, s8, 0x8000
	s_addc_u32 s9, s9, 0
	global_load_dwordx4 v[188:191], v75, s[8:9]
	s_add_u32 s8, s8, 0x8000
	s_addc_u32 s9, s9, 0
	global_load_dwordx4 v[192:195], v75, s[8:9]
	s_add_u32 s8, s8, 0x8000
	s_addc_u32 s9, s9, 0
	global_load_dwordx4 v[196:199], v75, s[8:9]
	s_add_u32 s8, s8, 0x8000
	s_addc_u32 s9, s9, 0
	global_load_dwordx4 v[200:203], v75, s[8:9]
	s_add_u32 s8, s8, 0x8000
	s_addc_u32 s9, s9, 0
	global_load_dwordx4 v[204:207], v75, s[8:9]
	s_add_u32 s6, s40, 0x3003000
	s_addc_u32 s7, s41, 0
	ds_read_b32 v226, v212
	ds_read_b32 v227, v212 offset:512
	ds_read_b32 v228, v212 offset:1024
	ds_read_b32 v229, v212 offset:1536
	ds_read_b32 v230, v212 offset:2048
	ds_read_b32 v231, v212 offset:2560
	ds_read_b32 v232, v212 offset:3072
	ds_read_b32 v233, v212 offset:3584
	ds_read_b32 v234, v212 offset:4096
	ds_read_b32 v235, v212 offset:4608
	ds_read_b32 v236, v212 offset:5120
	ds_read_b32 v237, v212 offset:5632
	ds_read_b32 v238, v212 offset:6144
	ds_read_b32 v239, v212 offset:6656
	ds_read_b32 v240, v212 offset:7168
	ds_read_b32 v241, v212 offset:7680
	s_waitcnt lgkmcnt(0)
	v_max_f32_e32 v226, v226, v226
	v_max_f32_e32 v227, v227, v227
	v_max_f32_e32 v228, v228, v228
	v_max_f32_e32 v229, v229, v229
	v_max_f32_e32 v230, v230, v230
	v_max_f32_e32 v231, v231, v231
	v_max_f32_e32 v232, v232, v232
	v_max_f32_e32 v233, v233, v233
	v_max_f32_e32 v234, v234, v234
	v_max_f32_e32 v235, v235, v235
	v_max_f32_e32 v236, v236, v236
	v_max_f32_e32 v237, v237, v237
	v_max_f32_e32 v238, v238, v238
	v_max_f32_e32 v239, v239, v239
	v_max_f32_e32 v240, v240, v240
	v_max_f32_e32 v241, v241, v241
	v_med3_f32 v226, v226, s62, v95
	v_med3_f32 v227, v227, s62, v95
	v_med3_f32 v228, v228, s62, v95
	v_med3_f32 v229, v229, s62, v95
	v_med3_f32 v230, v230, s62, v95
	v_med3_f32 v231, v231, s62, v95
	v_med3_f32 v232, v232, s62, v95
	v_med3_f32 v233, v233, s62, v95
	v_med3_f32 v234, v234, s62, v95
	v_med3_f32 v235, v235, s62, v95
	v_med3_f32 v236, v236, s62, v95
	v_med3_f32 v237, v237, s62, v95
	v_med3_f32 v238, v238, s62, v95
	v_med3_f32 v239, v239, s62, v95
	v_med3_f32 v240, v240, s62, v95
	v_med3_f32 v241, v241, s62, v95
	v_mov_b32_e32 v242, 0
	v_mov_b32_e32 v243, 0
	v_mov_b32_e32 v244, 0
	v_mov_b32_e32 v245, 0
	v_cvt_pk_fp8_f32 v242, v226, v227
	v_cvt_pk_fp8_f32 v243, v230, v231
	v_cvt_pk_fp8_f32 v244, v234, v235
	v_cvt_pk_fp8_f32 v245, v238, v239
	v_cvt_pk_fp8_f32 v242, v228, v229 op_sel:[0,0,1]
	v_cvt_pk_fp8_f32 v243, v232, v233 op_sel:[0,0,1]
	v_cvt_pk_fp8_f32 v244, v236, v237 op_sel:[0,0,1]
	v_cvt_pk_fp8_f32 v245, v240, v241 op_sel:[0,0,1]
	s_nop 0
	global_store_dwordx4 v79, v[242:245], s[6:7]
	ds_read_b32 v226, v214
	ds_read_b32 v227, v214 offset:512
	ds_read_b32 v228, v214 offset:1024
	ds_read_b32 v229, v214 offset:1536
	ds_read_b32 v230, v214 offset:2048
	ds_read_b32 v231, v214 offset:2560
	ds_read_b32 v232, v214 offset:3072
	ds_read_b32 v233, v214 offset:3584
	ds_read_b32 v234, v214 offset:4096
	ds_read_b32 v235, v214 offset:4608
	ds_read_b32 v236, v214 offset:5120
	ds_read_b32 v237, v214 offset:5632
	ds_read_b32 v238, v214 offset:6144
	ds_read_b32 v239, v214 offset:6656
	ds_read_b32 v240, v214 offset:7168
	ds_read_b32 v241, v214 offset:7680
	s_waitcnt lgkmcnt(0)
; #define GAS __attribute__((address_space(1)))
; #define LAS __attribute__((address_space(3)))
; #define LDS_WAIT() asm volatile("s_waitcnt lgkmcnt(0)" ::: "memory")
; __device__ __forceinline__ unsigned pk4_fp8(float a, float b, float c, float d) {
;     a = fminf(fmaxf(a, -448.f), 448.f); b = fminf(fmaxf(b, -448.f), 448.f); c = fminf(fmaxf(c, -448.f), 448.f); d = fminf(fmaxf(d, -448.f), 448.f);
;     int w = __builtin_amdgcn_cvt_pk_fp8_f32(a, b, 0, false); w = __builtin_amdgcn_cvt_pk_fp8_f32(c, d, w, true); return (unsigned)w; }
;     const int pr = item >> 1, kb = 2 * (pr / nblk) + (item & 1), nb = pr % nblk, k0 = 64 * kb, n0 = 32 * nb;
;     const int nr = n0 + (lane & 31); const int sc = MAP == 1 ? src_col_in(nr) : nr;
;     float v[32];
; #pragma unroll
;     for (int i = 0; i < 32; ++i) v[i] = sc >= 0 ? W[(size_t)(k0 + 2 * i + (lane >> 5)) * Nsrc + sc] : 0.f;
; #pragma unroll
;     for (int i = 0; i < 32; ++i) { const int k = k0 + 2 * i + (lane >> 5); float x = v[i] * wscale; if (KS) x *= (k < ksplit ? ksA[k] : ksB[k - ksplit]); scr[(2 * i + (lane >> 5)) * 33 + (lane & 31)] = x; }
;     LDS_WAIT(); asm volatile("" ::: "memory");
;     const int c = lane & 7;
; #pragma unroll
;     for (int j = 0; j < 4; ++j) { const int n = (lane >> 3) + 8 * j; const LAS float* s = scr + (8 * c) * 33 + n;
;         const unsigned long long o = (unsigned long long)pg8::pk4_fp8(s[0 * 33], s[1 * 33], s[2 * 33], s[3 * 33]) | ((unsigned long long)pg8::pk4_fp8(s[4 * 33], s[5 * 33], s[6 * 33], s[7 * 33]) << 32);
;         *(GAS unsigned long long*)(WT + (size_t)(n0 + n) * K + k0 + 8 * c) = o; }
;     LDS_WAIT(); asm volatile("" ::: "memory");
; }
	v_max_f32_e32 v226, v226, v226
	v_max_f32_e32 v227, v227, v227
	v_max_f32_e32 v228, v228, v228
	v_max_f32_e32 v229, v229, v229
	v_max_f32_e32 v230, v230, v230
	v_max_f32_e32 v231, v231, v231
	v_max_f32_e32 v232, v232, v232
	v_max_f32_e32 v233, v233, v233
	v_max_f32_e32 v234, v234, v234
	v_max_f32_e32 v235, v235, v235
	v_max_f32_e32 v236, v236, v236
	v_max_f32_e32 v237, v237, v237
	v_max_f32_e32 v238, v238, v238
	v_max_f32_e32 v239, v239, v239
	v_max_f32_e32 v240, v240, v240
	v_max_f32_e32 v241, v241, v241
	v_med3_f32 v226, v226, s62, v95
	v_med3_f32 v227, v227, s62, v95
	v_med3_f32 v228, v228, s62, v95
	v_med3_f32 v229, v229, s62, v95
	v_med3_f32 v230, v230, s62, v95
	v_med3_f32 v231, v231, s62, v95
	v_med3_f32 v232, v232, s62, v95
	v_med3_f32 v233, v233, s62, v95
	v_med3_f32 v234, v234, s62, v95
	v_med3_f32 v235, v235, s62, v95
	v_med3_f32 v236, v236, s62, v95
	v_med3_f32 v237, v237, s62, v95
	v_med3_f32 v238, v238, s62, v95
	v_med3_f32 v239, v239, s62, v95
	v_med3_f32 v240, v240, s62, v95
	v_med3_f32 v241, v241, s62, v95
	v_mov_b32_e32 v242, 0
	v_mov_b32_e32 v243, 0
	v_mov_b32_e32 v244, 0
	v_mov_b32_e32 v245, 0
	v_cvt_pk_fp8_f32 v242, v226, v227
	v_cvt_pk_fp8_f32 v243, v230, v231
	v_cvt_pk_fp8_f32 v244, v234, v235
	v_cvt_pk_fp8_f32 v245, v238, v239
	v_cvt_pk_fp8_f32 v242, v228, v229 op_sel:[0,0,1]
	v_cvt_pk_fp8_f32 v243, v232, v233 op_sel:[0,0,1]
	v_cvt_pk_fp8_f32 v244, v236, v237 op_sel:[0,0,1]
	v_cvt_pk_fp8_f32 v245, v240, v241 op_sel:[0,0,1]
	s_nop 0
	global_store_dwordx4 v80, v[242:245], s[6:7]
	s_waitcnt vmcnt(12)
	v_mul_f32_e32 v144, 0x43000000, v144
	v_mul_f32_e32 v145, 0x43000000, v145
	v_mul_f32_e32 v146, 0x43000000, v146
	v_mul_f32_e32 v147, 0x43000000, v147
	ds_write_b128 v209, v[144:147]
	v_mul_f32_e32 v148, 0x43000000, v148
	v_mul_f32_e32 v149, 0x43000000, v149
	v_mul_f32_e32 v150, 0x43000000, v150
	v_mul_f32_e32 v151, 0x43000000, v151
	ds_write_b128 v209, v[148:151] offset:1024
	v_mul_f32_e32 v152, 0x43000000, v152
	v_mul_f32_e32 v153, 0x43000000, v153
	v_mul_f32_e32 v154, 0x43000000, v154
	v_mul_f32_e32 v155, 0x43000000, v155
	ds_write_b128 v209, v[152:155] offset:2048
	v_mul_f32_e32 v156, 0x43000000, v156
	v_mul_f32_e32 v157, 0x43000000, v157
	v_mul_f32_e32 v158, 0x43000000, v158
	v_mul_f32_e32 v159, 0x43000000, v159
	ds_write_b128 v209, v[156:159] offset:3072
	v_mul_f32_e32 v160, 0x43000000, v160
	v_mul_f32_e32 v161, 0x43000000, v161
	v_mul_f32_e32 v162, 0x43000000, v162
	v_mul_f32_e32 v163, 0x43000000, v163
	ds_write_b128 v209, v[160:163] offset:4096
	v_mul_f32_e32 v164, 0x43000000, v164
	v_mul_f32_e32 v165, 0x43000000, v165
	v_mul_f32_e32 v166, 0x43000000, v166
	v_mul_f32_e32 v167, 0x43000000, v167
	ds_write_b128 v209, v[164:167] offset:5120
	v_mul_f32_e32 v168, 0x43000000, v168
	v_mul_f32_e32 v169, 0x43000000, v169
	v_mul_f32_e32 v170, 0x43000000, v170
	v_mul_f32_e32 v171, 0x43000000, v171
	ds_write_b128 v209, v[168:171] offset:6144
	v_mul_f32_e32 v172, 0x43000000, v172
	v_mul_f32_e32 v173, 0x43000000, v173
	v_mul_f32_e32 v174, 0x43000000, v174
	v_mul_f32_e32 v175, 0x43000000, v175
	ds_write_b128 v209, v[172:175] offset:7168
	s_waitcnt lgkmcnt(0)
	s_barrier
	s_add_u32 s8, s42, 0x2000
	s_addc_u32 s9, s43, 0
	global_load_dwordx4 v[144:147], v75, s[8:9]
	s_add_u32 s8, s8, 0x8000
	s_addc_u32 s9, s9, 0
	global_load_dwordx4 v[148:151], v75, s[8:9]
	s_add_u32 s8, s8, 0x8000
	s_addc_u32 s9, s9, 0
	global_load_dwordx4 v[152:155], v75, s[8:9]
	s_add_u32 s8, s8, 0x8000
	s_addc_u32 s9, s9, 0
	global_load_dwordx4 v[156:159], v75, s[8:9]
	s_add_u32 s8, s8, 0x8000
	s_addc_u32 s9, s9, 0
	global_load_dwordx4 v[160:163], v75, s[8:9]
	s_add_u32 s8, s8, 0x8000
	s_addc_u32 s9, s9, 0
	global_load_dwordx4 v[164:167], v75, s[8:9]
	s_add_u32 s8, s8, 0x8000
	s_addc_u32 s9, s9, 0
	global_load_dwordx4 v[168:171], v75, s[8:9]
	s_add_u32 s8, s8, 0x8000
	s_addc_u32 s9, s9, 0
	global_load_dwordx4 v[172:175], v75, s[8:9]
	s_mov_b64 s[6:7], s[44:45]
	ds_read_b32 v226, v211
	ds_read_b32 v227, v211 offset:512
	ds_read_b32 v228, v211 offset:1024
	ds_read_b32 v229, v211 offset:1536
	ds_read_b32 v230, v211 offset:2048
	ds_read_b32 v231, v211 offset:2560
	ds_read_b32 v232, v211 offset:3072
	ds_read_b32 v233, v211 offset:3584
	ds_read_b32 v234, v211 offset:4096
	ds_read_b32 v235, v211 offset:4608
	ds_read_b32 v236, v211 offset:5120
	ds_read_b32 v237, v211 offset:5632
	ds_read_b32 v238, v211 offset:6144
	ds_read_b32 v239, v211 offset:6656
	ds_read_b32 v240, v211 offset:7168
	ds_read_b32 v241, v211 offset:7680
	s_waitcnt lgkmcnt(0)
	v_max_f32_e32 v226, v226, v226
	v_max_f32_e32 v227, v227, v227
	v_max_f32_e32 v228, v228, v228
	v_max_f32_e32 v229, v229, v229
	v_max_f32_e32 v230, v230, v230
	v_max_f32_e32 v231, v231, v231
	v_max_f32_e32 v232, v232, v232
	v_max_f32_e32 v233, v233, v233
	v_max_f32_e32 v234, v234, v234
	v_max_f32_e32 v235, v235, v235
	v_max_f32_e32 v236, v236, v236
	v_max_f32_e32 v237, v237, v237
	v_max_f32_e32 v238, v238, v238
	v_max_f32_e32 v239, v239, v239
	v_max_f32_e32 v240, v240, v240
	v_max_f32_e32 v241, v241, v241
	v_med3_f32 v226, v226, s62, v95
	v_med3_f32 v227, v227, s62, v95
	v_med3_f32 v228, v228, s62, v95
	v_med3_f32 v229, v229, s62, v95
	v_med3_f32 v230, v230, s62, v95
	v_med3_f32 v231, v231, s62, v95
	v_med3_f32 v232, v232, s62, v95
	v_med3_f32 v233, v233, s62, v95
	v_med3_f32 v234, v234, s62, v95
	v_med3_f32 v235, v235, s62, v95
	v_med3_f32 v236, v236, s62, v95
	v_med3_f32 v237, v237, s62, v95
	v_med3_f32 v238, v238, s62, v95
	v_med3_f32 v239, v239, s62, v95
	v_med3_f32 v240, v240, s62, v95
	v_med3_f32 v241, v241, s62, v95
	v_mov_b32_e32 v242, 0
	v_mov_b32_e32 v243, 0
	v_mov_b32_e32 v244, 0
	v_mov_b32_e32 v245, 0
	v_cvt_pk_fp8_f32 v242, v226, v227
	v_cvt_pk_fp8_f32 v243, v230, v231
	v_cvt_pk_fp8_f32 v244, v234, v235
	v_cvt_pk_fp8_f32 v245, v238, v239
	v_cvt_pk_fp8_f32 v242, v228, v229 op_sel:[0,0,1]
	v_cvt_pk_fp8_f32 v243, v232, v233 op_sel:[0,0,1]
	v_cvt_pk_fp8_f32 v244, v236, v237 op_sel:[0,0,1]
	v_cvt_pk_fp8_f32 v245, v240, v241 op_sel:[0,0,1]
	s_nop 0
	global_store_dwordx4 v79, v[242:245], s[6:7]
	ds_read_b32 v226, v213
	ds_read_b32 v227, v213 offset:512
	ds_read_b32 v228, v213 offset:1024
	ds_read_b32 v229, v213 offset:1536
	ds_read_b32 v230, v213 offset:2048
	ds_read_b32 v231, v213 offset:2560
	ds_read_b32 v232, v213 offset:3072
	ds_read_b32 v233, v213 offset:3584
	ds_read_b32 v234, v213 offset:4096
	ds_read_b32 v235, v213 offset:4608
	ds_read_b32 v236, v213 offset:5120
	ds_read_b32 v237, v213 offset:5632
	ds_read_b32 v238, v213 offset:6144
	ds_read_b32 v239, v213 offset:6656
	ds_read_b32 v240, v213 offset:7168
	ds_read_b32 v241, v213 offset:7680
	s_waitcnt lgkmcnt(0)
; #define GAS __attribute__((address_space(1)))
; #define LAS __attribute__((address_space(3)))
; #define LDS_WAIT() asm volatile("s_waitcnt lgkmcnt(0)" ::: "memory")
; __device__ __forceinline__ unsigned pk4_fp8(float a, float b, float c, float d) {
;     a = fminf(fmaxf(a, -448.f), 448.f); b = fminf(fmaxf(b, -448.f), 448.f); c = fminf(fmaxf(c, -448.f), 448.f); d = fminf(fmaxf(d, -448.f), 448.f);
;     int w = __builtin_amdgcn_cvt_pk_fp8_f32(a, b, 0, false); w = __builtin_amdgcn_cvt_pk_fp8_f32(c, d, w, true); return (unsigned)w; }
;     const int pr = item >> 1, kb = 2 * (pr / nblk) + (item & 1), nb = pr % nblk, k0 = 64 * kb, n0 = 32 * nb;
;     const int nr = n0 + (lane & 31); const int sc = MAP == 1 ? src_col_in(nr) : nr;
;     float v[32];
; #pragma unroll
;     for (int i = 0; i < 32; ++i) v[i] = sc >= 0 ? W[(size_t)(k0 + 2 * i + (lane >> 5)) * Nsrc + sc] : 0.f;
; #pragma unroll
;     for (int i = 0; i < 32; ++i) { const int k = k0 + 2 * i + (lane >> 5); float x = v[i] * wscale; if (KS) x *= (k < ksplit ? ksA[k] : ksB[k - ksplit]); scr[(2 * i + (lane >> 5)) * 33 + (lane & 31)] = x; }
;     LDS_WAIT(); asm volatile("" ::: "memory");
;     const int c = lane & 7;
; #pragma unroll
;     for (int j = 0; j < 4; ++j) { const int n = (lane >> 3) + 8 * j; const LAS float* s = scr + (8 * c) * 33 + n;
;         const unsigned long long o = (unsigned long long)pg8::pk4_fp8(s[0 * 33], s[1 * 33], s[2 * 33], s[3 * 33]) | ((unsigned long long)pg8::pk4_fp8(s[4 * 33], s[5 * 33], s[6 * 33], s[7 * 33]) << 32);
;         *(GAS unsigned long long*)(WT + (size_t)(n0 + n) * K + k0 + 8 * c) = o; }
;     LDS_WAIT(); asm volatile("" ::: "memory");
; }
	v_max_f32_e32 v226, v226, v226
	v_max_f32_e32 v227, v227, v227
	v_max_f32_e32 v228, v228, v228
	v_max_f32_e32 v229, v229, v229
	v_max_f32_e32 v230, v230, v230
	v_max_f32_e32 v231, v231, v231
	v_max_f32_e32 v232, v232, v232
	v_max_f32_e32 v233, v233, v233
	v_max_f32_e32 v234, v234, v234
	v_max_f32_e32 v235, v235, v235
	v_max_f32_e32 v236, v236, v236
	v_max_f32_e32 v237, v237, v237
	v_max_f32_e32 v238, v238, v238
	v_max_f32_e32 v239, v239, v239
	v_max_f32_e32 v240, v240, v240
	v_max_f32_e32 v241, v241, v241
	v_med3_f32 v226, v226, s62, v95
	v_med3_f32 v227, v227, s62, v95
	v_med3_f32 v228, v228, s62, v95
	v_med3_f32 v229, v229, s62, v95
	v_med3_f32 v230, v230, s62, v95
	v_med3_f32 v231, v231, s62, v95
	v_med3_f32 v232, v232, s62, v95
	v_med3_f32 v233, v233, s62, v95
	v_med3_f32 v234, v234, s62, v95
	v_med3_f32 v235, v235, s62, v95
	v_med3_f32 v236, v236, s62, v95
	v_med3_f32 v237, v237, s62, v95
	v_med3_f32 v238, v238, s62, v95
	v_med3_f32 v239, v239, s62, v95
	v_med3_f32 v240, v240, s62, v95
	v_med3_f32 v241, v241, s62, v95
	v_mov_b32_e32 v242, 0
	v_mov_b32_e32 v243, 0
	v_mov_b32_e32 v244, 0
	v_mov_b32_e32 v245, 0
	v_cvt_pk_fp8_f32 v242, v226, v227
	v_cvt_pk_fp8_f32 v243, v230, v231
	v_cvt_pk_fp8_f32 v244, v234, v235
	v_cvt_pk_fp8_f32 v245, v238, v239
	v_cvt_pk_fp8_f32 v242, v228, v229 op_sel:[0,0,1]
	v_cvt_pk_fp8_f32 v243, v232, v233 op_sel:[0,0,1]
	v_cvt_pk_fp8_f32 v244, v236, v237 op_sel:[0,0,1]
	v_cvt_pk_fp8_f32 v245, v240, v241 op_sel:[0,0,1]
	s_nop 0
	global_store_dwordx4 v80, v[242:245], s[6:7]
	s_waitcnt vmcnt(12)
	v_mul_f32_e32 v176, 0x43000000, v176
	v_mul_f32_e32 v177, 0x43000000, v177
	v_mul_f32_e32 v178, 0x43000000, v178
	v_mul_f32_e32 v179, 0x43000000, v179
	ds_write_b128 v210, v[176:179]
	v_mul_f32_e32 v180, 0x43000000, v180
	v_mul_f32_e32 v181, 0x43000000, v181
	v_mul_f32_e32 v182, 0x43000000, v182
	v_mul_f32_e32 v183, 0x43000000, v183
	ds_write_b128 v210, v[180:183] offset:1024
	v_mul_f32_e32 v184, 0x43000000, v184
	v_mul_f32_e32 v185, 0x43000000, v185
	v_mul_f32_e32 v186, 0x43000000, v186
	v_mul_f32_e32 v187, 0x43000000, v187
	ds_write_b128 v210, v[184:187] offset:2048
	v_mul_f32_e32 v188, 0x43000000, v188
	v_mul_f32_e32 v189, 0x43000000, v189
	v_mul_f32_e32 v190, 0x43000000, v190
	v_mul_f32_e32 v191, 0x43000000, v191
	ds_write_b128 v210, v[188:191] offset:3072
	v_mul_f32_e32 v192, 0x43000000, v192
	v_mul_f32_e32 v193, 0x43000000, v193
	v_mul_f32_e32 v194, 0x43000000, v194
	v_mul_f32_e32 v195, 0x43000000, v195
	ds_write_b128 v210, v[192:195] offset:4096
	v_mul_f32_e32 v196, 0x43000000, v196
	v_mul_f32_e32 v197, 0x43000000, v197
	v_mul_f32_e32 v198, 0x43000000, v198
	v_mul_f32_e32 v199, 0x43000000, v199
	ds_write_b128 v210, v[196:199] offset:5120
	v_mul_f32_e32 v200, 0x43000000, v200
	v_mul_f32_e32 v201, 0x43000000, v201
	v_mul_f32_e32 v202, 0x43000000, v202
	v_mul_f32_e32 v203, 0x43000000, v203
	ds_write_b128 v210, v[200:203] offset:6144
	v_mul_f32_e32 v204, 0x43000000, v204
	v_mul_f32_e32 v205, 0x43000000, v205
	v_mul_f32_e32 v206, 0x43000000, v206
	v_mul_f32_e32 v207, 0x43000000, v207
	ds_write_b128 v210, v[204:207] offset:7168
	s_waitcnt lgkmcnt(0)
	s_barrier
	s_add_u32 s8, s42, 0x3000
	s_addc_u32 s9, s43, 0
	global_load_dwordx4 v[176:179], v75, s[8:9]
	s_add_u32 s8, s8, 0x8000
	s_addc_u32 s9, s9, 0
	global_load_dwordx4 v[180:183], v75, s[8:9]
	s_add_u32 s8, s8, 0x8000
	s_addc_u32 s9, s9, 0
	global_load_dwordx4 v[184:187], v75, s[8:9]
	s_add_u32 s8, s8, 0x8000
	s_addc_u32 s9, s9, 0
	global_load_dwordx4 v[188:191], v75, s[8:9]
	s_add_u32 s8, s8, 0x8000
	s_addc_u32 s9, s9, 0
	global_load_dwordx4 v[192:195], v75, s[8:9]
	s_add_u32 s8, s8, 0x8000
	s_addc_u32 s9, s9, 0
	global_load_dwordx4 v[196:199], v75, s[8:9]
	s_add_u32 s8, s8, 0x8000
	s_addc_u32 s9, s9, 0
	global_load_dwordx4 v[200:203], v75, s[8:9]
	s_add_u32 s8, s8, 0x8000
	s_addc_u32 s9, s9, 0
	global_load_dwordx4 v[204:207], v75, s[8:9]
	s_add_u32 s6, s44, 0x1000000
	s_addc_u32 s7, s45, 0
	ds_read_b32 v226, v212
	ds_read_b32 v227, v212 offset:512
	ds_read_b32 v228, v212 offset:1024
	ds_read_b32 v229, v212 offset:1536
	ds_read_b32 v230, v212 offset:2048
	ds_read_b32 v231, v212 offset:2560
	ds_read_b32 v232, v212 offset:3072
	ds_read_b32 v233, v212 offset:3584
	ds_read_b32 v234, v212 offset:4096
	ds_read_b32 v235, v212 offset:4608
	ds_read_b32 v236, v212 offset:5120
	ds_read_b32 v237, v212 offset:5632
	ds_read_b32 v238, v212 offset:6144
	ds_read_b32 v239, v212 offset:6656
	ds_read_b32 v240, v212 offset:7168
	ds_read_b32 v241, v212 offset:7680
	s_waitcnt lgkmcnt(0)
	v_max_f32_e32 v226, v226, v226
	v_max_f32_e32 v227, v227, v227
	v_max_f32_e32 v228, v228, v228
	v_max_f32_e32 v229, v229, v229
	v_max_f32_e32 v230, v230, v230
	v_max_f32_e32 v231, v231, v231
	v_max_f32_e32 v232, v232, v232
	v_max_f32_e32 v233, v233, v233
	v_max_f32_e32 v234, v234, v234
	v_max_f32_e32 v235, v235, v235
	v_max_f32_e32 v236, v236, v236
	v_max_f32_e32 v237, v237, v237
	v_max_f32_e32 v238, v238, v238
	v_max_f32_e32 v239, v239, v239
	v_max_f32_e32 v240, v240, v240
	v_max_f32_e32 v241, v241, v241
	v_med3_f32 v226, v226, s62, v95
	v_med3_f32 v227, v227, s62, v95
	v_med3_f32 v228, v228, s62, v95
	v_med3_f32 v229, v229, s62, v95
	v_med3_f32 v230, v230, s62, v95
	v_med3_f32 v231, v231, s62, v95
	v_med3_f32 v232, v232, s62, v95
	v_med3_f32 v233, v233, s62, v95
	v_med3_f32 v234, v234, s62, v95
	v_med3_f32 v235, v235, s62, v95
	v_med3_f32 v236, v236, s62, v95
	v_med3_f32 v237, v237, s62, v95
	v_med3_f32 v238, v238, s62, v95
	v_med3_f32 v239, v239, s62, v95
	v_med3_f32 v240, v240, s62, v95
	v_med3_f32 v241, v241, s62, v95
	v_mov_b32_e32 v242, 0
	v_mov_b32_e32 v243, 0
	v_mov_b32_e32 v244, 0
	v_mov_b32_e32 v245, 0
	v_cvt_pk_fp8_f32 v242, v226, v227
	v_cvt_pk_fp8_f32 v243, v230, v231
	v_cvt_pk_fp8_f32 v244, v234, v235
	v_cvt_pk_fp8_f32 v245, v238, v239
	v_cvt_pk_fp8_f32 v242, v228, v229 op_sel:[0,0,1]
	v_cvt_pk_fp8_f32 v243, v232, v233 op_sel:[0,0,1]
	v_cvt_pk_fp8_f32 v244, v236, v237 op_sel:[0,0,1]
	v_cvt_pk_fp8_f32 v245, v240, v241 op_sel:[0,0,1]
	s_nop 0
	global_store_dwordx4 v79, v[242:245], s[6:7]
	ds_read_b32 v226, v214
	ds_read_b32 v227, v214 offset:512
	ds_read_b32 v228, v214 offset:1024
	ds_read_b32 v229, v214 offset:1536
	ds_read_b32 v230, v214 offset:2048
	ds_read_b32 v231, v214 offset:2560
	ds_read_b32 v232, v214 offset:3072
	ds_read_b32 v233, v214 offset:3584
	ds_read_b32 v234, v214 offset:4096
	ds_read_b32 v235, v214 offset:4608
	ds_read_b32 v236, v214 offset:5120
	ds_read_b32 v237, v214 offset:5632
	ds_read_b32 v238, v214 offset:6144
	ds_read_b32 v239, v214 offset:6656
	ds_read_b32 v240, v214 offset:7168
	ds_read_b32 v241, v214 offset:7680
	s_waitcnt lgkmcnt(0)
; #define GAS __attribute__((address_space(1)))
; #define LAS __attribute__((address_space(3)))
; #define LDS_WAIT() asm volatile("s_waitcnt lgkmcnt(0)" ::: "memory")
; __device__ __forceinline__ unsigned pk4_fp8(float a, float b, float c, float d) {
;     a = fminf(fmaxf(a, -448.f), 448.f); b = fminf(fmaxf(b, -448.f), 448.f); c = fminf(fmaxf(c, -448.f), 448.f); d = fminf(fmaxf(d, -448.f), 448.f);
;     int w = __builtin_amdgcn_cvt_pk_fp8_f32(a, b, 0, false); w = __builtin_amdgcn_cvt_pk_fp8_f32(c, d, w, true); return (unsigned)w; }
;     const int pr = item >> 1, kb = 2 * (pr / nblk) + (item & 1), nb = pr % nblk, k0 = 64 * kb, n0 = 32 * nb;
;     const int nr = n0 + (lane & 31); const int sc = MAP == 1 ? src_col_in(nr) : nr;
;     float v[32];
; #pragma unroll
;     for (int i = 0; i < 32; ++i) v[i] = sc >= 0 ? W[(size_t)(k0 + 2 * i + (lane >> 5)) * Nsrc + sc] : 0.f;
; #pragma unroll
;     for (int i = 0; i < 32; ++i) { const int k = k0 + 2 * i + (lane >> 5); float x = v[i] * wscale; if (KS) x *= (k < ksplit ? ksA[k] : ksB[k - ksplit]); scr[(2 * i + (lane >> 5)) * 33 + (lane & 31)] = x; }
;     LDS_WAIT(); asm volatile("" ::: "memory");
;     const int c = lane & 7;
; #pragma unroll
;     for (int j = 0; j < 4; ++j) { const int n = (lane >> 3) + 8 * j; const LAS float* s = scr + (8 * c) * 33 + n;
;         const unsigned long long o = (unsigned long long)pg8::pk4_fp8(s[0 * 33], s[1 * 33], s[2 * 33], s[3 * 33]) | ((unsigned long long)pg8::pk4_fp8(s[4 * 33], s[5 * 33], s[6 * 33], s[7 * 33]) << 32);
;         *(GAS unsigned long long*)(WT + (size_t)(n0 + n) * K + k0 + 8 * c) = o; }
;     LDS_WAIT(); asm volatile("" ::: "memory");
; }
	v_max_f32_e32 v226, v226, v226
	v_max_f32_e32 v227, v227, v227
	v_max_f32_e32 v228, v228, v228
	v_max_f32_e32 v229, v229, v229
	v_max_f32_e32 v230, v230, v230
	v_max_f32_e32 v231, v231, v231
	v_max_f32_e32 v232, v232, v232
	v_max_f32_e32 v233, v233, v233
	v_max_f32_e32 v234, v234, v234
	v_max_f32_e32 v235, v235, v235
	v_max_f32_e32 v236, v236, v236
	v_max_f32_e32 v237, v237, v237
	v_max_f32_e32 v238, v238, v238
	v_max_f32_e32 v239, v239, v239
	v_max_f32_e32 v240, v240, v240
	v_max_f32_e32 v241, v241, v241
	v_med3_f32 v226, v226, s62, v95
	v_med3_f32 v227, v227, s62, v95
	v_med3_f32 v228, v228, s62, v95
	v_med3_f32 v229, v229, s62, v95
	v_med3_f32 v230, v230, s62, v95
	v_med3_f32 v231, v231, s62, v95
	v_med3_f32 v232, v232, s62, v95
	v_med3_f32 v233, v233, s62, v95
	v_med3_f32 v234, v234, s62, v95
	v_med3_f32 v235, v235, s62, v95
	v_med3_f32 v236, v236, s62, v95
	v_med3_f32 v237, v237, s62, v95
	v_med3_f32 v238, v238, s62, v95
	v_med3_f32 v239, v239, s62, v95
	v_med3_f32 v240, v240, s62, v95
	v_med3_f32 v241, v241, s62, v95
	v_mov_b32_e32 v242, 0
	v_mov_b32_e32 v243, 0
	v_mov_b32_e32 v244, 0
	v_mov_b32_e32 v245, 0
	v_cvt_pk_fp8_f32 v242, v226, v227
	v_cvt_pk_fp8_f32 v243, v230, v231
	v_cvt_pk_fp8_f32 v244, v234, v235
	v_cvt_pk_fp8_f32 v245, v238, v239
	v_cvt_pk_fp8_f32 v242, v228, v229 op_sel:[0,0,1]
	v_cvt_pk_fp8_f32 v243, v232, v233 op_sel:[0,0,1]
	v_cvt_pk_fp8_f32 v244, v236, v237 op_sel:[0,0,1]
	v_cvt_pk_fp8_f32 v245, v240, v241 op_sel:[0,0,1]
	s_nop 0
	global_store_dwordx4 v80, v[242:245], s[6:7]
	s_waitcnt vmcnt(12)
	v_mul_f32_e32 v144, 0x43000000, v144
	v_mul_f32_e32 v145, 0x43000000, v145
	v_mul_f32_e32 v146, 0x43000000, v146
	v_mul_f32_e32 v147, 0x43000000, v147
	ds_write_b128 v209, v[144:147]
	v_mul_f32_e32 v148, 0x43000000, v148
	v_mul_f32_e32 v149, 0x43000000, v149
	v_mul_f32_e32 v150, 0x43000000, v150
	v_mul_f32_e32 v151, 0x43000000, v151
	ds_write_b128 v209, v[148:151] offset:1024
	v_mul_f32_e32 v152, 0x43000000, v152
	v_mul_f32_e32 v153, 0x43000000, v153
	v_mul_f32_e32 v154, 0x43000000, v154
	v_mul_f32_e32 v155, 0x43000000, v155
	ds_write_b128 v209, v[152:155] offset:2048
	v_mul_f32_e32 v156, 0x43000000, v156
	v_mul_f32_e32 v157, 0x43000000, v157
	v_mul_f32_e32 v158, 0x43000000, v158
	v_mul_f32_e32 v159, 0x43000000, v159
	ds_write_b128 v209, v[156:159] offset:3072
	v_mul_f32_e32 v160, 0x43000000, v160
	v_mul_f32_e32 v161, 0x43000000, v161
	v_mul_f32_e32 v162, 0x43000000, v162
	v_mul_f32_e32 v163, 0x43000000, v163
	ds_write_b128 v209, v[160:163] offset:4096
	v_mul_f32_e32 v164, 0x43000000, v164
	v_mul_f32_e32 v165, 0x43000000, v165
	v_mul_f32_e32 v166, 0x43000000, v166
	v_mul_f32_e32 v167, 0x43000000, v167
	ds_write_b128 v209, v[164:167] offset:5120
	v_mul_f32_e32 v168, 0x43000000, v168
	v_mul_f32_e32 v169, 0x43000000, v169
	v_mul_f32_e32 v170, 0x43000000, v170
	v_mul_f32_e32 v171, 0x43000000, v171
	ds_write_b128 v209, v[168:171] offset:6144
	v_mul_f32_e32 v172, 0x43000000, v172
	v_mul_f32_e32 v173, 0x43000000, v173
	v_mul_f32_e32 v174, 0x43000000, v174
	v_mul_f32_e32 v175, 0x43000000, v175
	ds_write_b128 v209, v[172:175] offset:7168
	s_waitcnt lgkmcnt(0)
	s_barrier
	s_add_u32 s8, s42, 0x4000000
	s_addc_u32 s9, s43, 0
	global_load_dwordx4 v[144:147], v75, s[8:9]
	s_add_u32 s8, s8, 0x8000
	s_addc_u32 s9, s9, 0
	global_load_dwordx4 v[148:151], v75, s[8:9]
	s_add_u32 s8, s8, 0x8000
	s_addc_u32 s9, s9, 0
	global_load_dwordx4 v[152:155], v75, s[8:9]
	s_add_u32 s8, s8, 0x8000
	s_addc_u32 s9, s9, 0
	global_load_dwordx4 v[156:159], v75, s[8:9]
	s_add_u32 s8, s8, 0x8000
	s_addc_u32 s9, s9, 0
	global_load_dwordx4 v[160:163], v75, s[8:9]
	s_add_u32 s8, s8, 0x8000
	s_addc_u32 s9, s9, 0
	global_load_dwordx4 v[164:167], v75, s[8:9]
	s_add_u32 s8, s8, 0x8000
	s_addc_u32 s9, s9, 0
	global_load_dwordx4 v[168:171], v75, s[8:9]
	s_add_u32 s8, s8, 0x8000
	s_addc_u32 s9, s9, 0
	global_load_dwordx4 v[172:175], v75, s[8:9]
	s_add_u32 s6, s44, 0x2000000
	s_addc_u32 s7, s45, 0
	ds_read_b32 v226, v211
	ds_read_b32 v227, v211 offset:512
	ds_read_b32 v228, v211 offset:1024
	ds_read_b32 v229, v211 offset:1536
	ds_read_b32 v230, v211 offset:2048
	ds_read_b32 v231, v211 offset:2560
	ds_read_b32 v232, v211 offset:3072
	ds_read_b32 v233, v211 offset:3584
	ds_read_b32 v234, v211 offset:4096
	ds_read_b32 v235, v211 offset:4608
	ds_read_b32 v236, v211 offset:5120
	ds_read_b32 v237, v211 offset:5632
	ds_read_b32 v238, v211 offset:6144
	ds_read_b32 v239, v211 offset:6656
	ds_read_b32 v240, v211 offset:7168
	ds_read_b32 v241, v211 offset:7680
	s_waitcnt lgkmcnt(0)
	v_max_f32_e32 v226, v226, v226
	v_max_f32_e32 v227, v227, v227
	v_max_f32_e32 v228, v228, v228
	v_max_f32_e32 v229, v229, v229
	v_max_f32_e32 v230, v230, v230
	v_max_f32_e32 v231, v231, v231
	v_max_f32_e32 v232, v232, v232
	v_max_f32_e32 v233, v233, v233
	v_max_f32_e32 v234, v234, v234
	v_max_f32_e32 v235, v235, v235
	v_max_f32_e32 v236, v236, v236
	v_max_f32_e32 v237, v237, v237
	v_max_f32_e32 v238, v238, v238
	v_max_f32_e32 v239, v239, v239
	v_max_f32_e32 v240, v240, v240
	v_max_f32_e32 v241, v241, v241
	v_med3_f32 v226, v226, s62, v95
	v_med3_f32 v227, v227, s62, v95
	v_med3_f32 v228, v228, s62, v95
	v_med3_f32 v229, v229, s62, v95
	v_med3_f32 v230, v230, s62, v95
	v_med3_f32 v231, v231, s62, v95
	v_med3_f32 v232, v232, s62, v95
	v_med3_f32 v233, v233, s62, v95
	v_med3_f32 v234, v234, s62, v95
	v_med3_f32 v235, v235, s62, v95
	v_med3_f32 v236, v236, s62, v95
	v_med3_f32 v237, v237, s62, v95
	v_med3_f32 v238, v238, s62, v95
	v_med3_f32 v239, v239, s62, v95
	v_med3_f32 v240, v240, s62, v95
	v_med3_f32 v241, v241, s62, v95
	v_mov_b32_e32 v242, 0
	v_mov_b32_e32 v243, 0
	v_mov_b32_e32 v244, 0
	v_mov_b32_e32 v245, 0
	v_cvt_pk_fp8_f32 v242, v226, v227
	v_cvt_pk_fp8_f32 v243, v230, v231
	v_cvt_pk_fp8_f32 v244, v234, v235
	v_cvt_pk_fp8_f32 v245, v238, v239
	v_cvt_pk_fp8_f32 v242, v228, v229 op_sel:[0,0,1]
	v_cvt_pk_fp8_f32 v243, v232, v233 op_sel:[0,0,1]
	v_cvt_pk_fp8_f32 v244, v236, v237 op_sel:[0,0,1]
	v_cvt_pk_fp8_f32 v245, v240, v241 op_sel:[0,0,1]
	s_nop 0
	global_store_dwordx4 v79, v[242:245], s[6:7]
	ds_read_b32 v226, v213
	ds_read_b32 v227, v213 offset:512
	ds_read_b32 v228, v213 offset:1024
	ds_read_b32 v229, v213 offset:1536
	ds_read_b32 v230, v213 offset:2048
	ds_read_b32 v231, v213 offset:2560
	ds_read_b32 v232, v213 offset:3072
	ds_read_b32 v233, v213 offset:3584
	ds_read_b32 v234, v213 offset:4096
	ds_read_b32 v235, v213 offset:4608
	ds_read_b32 v236, v213 offset:5120
	ds_read_b32 v237, v213 offset:5632
	ds_read_b32 v238, v213 offset:6144
	ds_read_b32 v239, v213 offset:6656
	ds_read_b32 v240, v213 offset:7168
	ds_read_b32 v241, v213 offset:7680
	s_waitcnt lgkmcnt(0)
; #define GAS __attribute__((address_space(1)))
; #define LAS __attribute__((address_space(3)))
; #define LDS_WAIT() asm volatile("s_waitcnt lgkmcnt(0)" ::: "memory")
; __device__ __forceinline__ unsigned pk4_fp8(float a, float b, float c, float d) {
;     a = fminf(fmaxf(a, -448.f), 448.f); b = fminf(fmaxf(b, -448.f), 448.f); c = fminf(fmaxf(c, -448.f), 448.f); d = fminf(fmaxf(d, -448.f), 448.f);
;     int w = __builtin_amdgcn_cvt_pk_fp8_f32(a, b, 0, false); w = __builtin_amdgcn_cvt_pk_fp8_f32(c, d, w, true); return (unsigned)w; }
;     const int pr = item >> 1, kb = 2 * (pr / nblk) + (item & 1), nb = pr % nblk, k0 = 64 * kb, n0 = 32 * nb;
;     const int nr = n0 + (lane & 31); const int sc = MAP == 1 ? src_col_in(nr) : nr;
;     float v[32];
; #pragma unroll
;     for (int i = 0; i < 32; ++i) v[i] = sc >= 0 ? W[(size_t)(k0 + 2 * i + (lane >> 5)) * Nsrc + sc] : 0.f;
; #pragma unroll
;     for (int i = 0; i < 32; ++i) { const int k = k0 + 2 * i + (lane >> 5); float x = v[i] * wscale; if (KS) x *= (k < ksplit ? ksA[k] : ksB[k - ksplit]); scr[(2 * i + (lane >> 5)) * 33 + (lane & 31)] = x; }
;     LDS_WAIT(); asm volatile("" ::: "memory");
;     const int c = lane & 7;
; #pragma unroll
;     for (int j = 0; j < 4; ++j) { const int n = (lane >> 3) + 8 * j; const LAS float* s = scr + (8 * c) * 33 + n;
;         const unsigned long long o = (unsigned long long)pg8::pk4_fp8(s[0 * 33], s[1 * 33], s[2 * 33], s[3 * 33]) | ((unsigned long long)pg8::pk4_fp8(s[4 * 33], s[5 * 33], s[6 * 33], s[7 * 33]) << 32);
;         *(GAS unsigned long long*)(WT + (size_t)(n0 + n) * K + k0 + 8 * c) = o; }
;     LDS_WAIT(); asm volatile("" ::: "memory");
; }
	v_max_f32_e32 v226, v226, v226
	v_max_f32_e32 v227, v227, v227
	v_max_f32_e32 v228, v228, v228
	v_max_f32_e32 v229, v229, v229
	v_max_f32_e32 v230, v230, v230
	v_max_f32_e32 v231, v231, v231
	v_max_f32_e32 v232, v232, v232
	v_max_f32_e32 v233, v233, v233
	v_max_f32_e32 v234, v234, v234
	v_max_f32_e32 v235, v235, v235
	v_max_f32_e32 v236, v236, v236
	v_max_f32_e32 v237, v237, v237
	v_max_f32_e32 v238, v238, v238
	v_max_f32_e32 v239, v239, v239
	v_max_f32_e32 v240, v240, v240
	v_max_f32_e32 v241, v241, v241
	v_med3_f32 v226, v226, s62, v95
	v_med3_f32 v227, v227, s62, v95
	v_med3_f32 v228, v228, s62, v95
	v_med3_f32 v229, v229, s62, v95
	v_med3_f32 v230, v230, s62, v95
	v_med3_f32 v231, v231, s62, v95
	v_med3_f32 v232, v232, s62, v95
	v_med3_f32 v233, v233, s62, v95
	v_med3_f32 v234, v234, s62, v95
	v_med3_f32 v235, v235, s62, v95
	v_med3_f32 v236, v236, s62, v95
	v_med3_f32 v237, v237, s62, v95
	v_med3_f32 v238, v238, s62, v95
	v_med3_f32 v239, v239, s62, v95
	v_med3_f32 v240, v240, s62, v95
	v_med3_f32 v241, v241, s62, v95
	v_mov_b32_e32 v242, 0
	v_mov_b32_e32 v243, 0
	v_mov_b32_e32 v244, 0
	v_mov_b32_e32 v245, 0
	v_cvt_pk_fp8_f32 v242, v226, v227
	v_cvt_pk_fp8_f32 v243, v230, v231
	v_cvt_pk_fp8_f32 v244, v234, v235
	v_cvt_pk_fp8_f32 v245, v238, v239
	v_cvt_pk_fp8_f32 v242, v228, v229 op_sel:[0,0,1]
	v_cvt_pk_fp8_f32 v243, v232, v233 op_sel:[0,0,1]
	v_cvt_pk_fp8_f32 v244, v236, v237 op_sel:[0,0,1]
	v_cvt_pk_fp8_f32 v245, v240, v241 op_sel:[0,0,1]
	s_nop 0
	global_store_dwordx4 v80, v[242:245], s[6:7]
	s_waitcnt vmcnt(12)
	v_mul_f32_e32 v176, 0x43000000, v176
	v_mul_f32_e32 v177, 0x43000000, v177
	v_mul_f32_e32 v178, 0x43000000, v178
	v_mul_f32_e32 v179, 0x43000000, v179
	ds_write_b128 v210, v[176:179]
	v_mul_f32_e32 v180, 0x43000000, v180
	v_mul_f32_e32 v181, 0x43000000, v181
	v_mul_f32_e32 v182, 0x43000000, v182
	v_mul_f32_e32 v183, 0x43000000, v183
	ds_write_b128 v210, v[180:183] offset:1024
	v_mul_f32_e32 v184, 0x43000000, v184
	v_mul_f32_e32 v185, 0x43000000, v185
	v_mul_f32_e32 v186, 0x43000000, v186
	v_mul_f32_e32 v187, 0x43000000, v187
	ds_write_b128 v210, v[184:187] offset:2048
	v_mul_f32_e32 v188, 0x43000000, v188
	v_mul_f32_e32 v189, 0x43000000, v189
	v_mul_f32_e32 v190, 0x43000000, v190
	v_mul_f32_e32 v191, 0x43000000, v191
	ds_write_b128 v210, v[188:191] offset:3072
	v_mul_f32_e32 v192, 0x43000000, v192
	v_mul_f32_e32 v193, 0x43000000, v193
	v_mul_f32_e32 v194, 0x43000000, v194
	v_mul_f32_e32 v195, 0x43000000, v195
	ds_write_b128 v210, v[192:195] offset:4096
	v_mul_f32_e32 v196, 0x43000000, v196
	v_mul_f32_e32 v197, 0x43000000, v197
	v_mul_f32_e32 v198, 0x43000000, v198
	v_mul_f32_e32 v199, 0x43000000, v199
	ds_write_b128 v210, v[196:199] offset:5120
	v_mul_f32_e32 v200, 0x43000000, v200
	v_mul_f32_e32 v201, 0x43000000, v201
	v_mul_f32_e32 v202, 0x43000000, v202
	v_mul_f32_e32 v203, 0x43000000, v203
	ds_write_b128 v210, v[200:203] offset:6144
	v_mul_f32_e32 v204, 0x43000000, v204
	v_mul_f32_e32 v205, 0x43000000, v205
	v_mul_f32_e32 v206, 0x43000000, v206
	v_mul_f32_e32 v207, 0x43000000, v207
	ds_write_b128 v210, v[204:207] offset:7168
	s_waitcnt lgkmcnt(0)
	s_barrier
	s_add_u32 s8, s42, 0x4001000
	s_addc_u32 s9, s43, 0
	global_load_dwordx4 v[176:179], v75, s[8:9]
	s_add_u32 s8, s8, 0x8000
	s_addc_u32 s9, s9, 0
	global_load_dwordx4 v[180:183], v75, s[8:9]
	s_add_u32 s8, s8, 0x8000
	s_addc_u32 s9, s9, 0
	global_load_dwordx4 v[184:187], v75, s[8:9]
	s_add_u32 s8, s8, 0x8000
	s_addc_u32 s9, s9, 0
	global_load_dwordx4 v[188:191], v75, s[8:9]
	s_add_u32 s8, s8, 0x8000
	s_addc_u32 s9, s9, 0
	global_load_dwordx4 v[192:195], v75, s[8:9]
	s_add_u32 s8, s8, 0x8000
	s_addc_u32 s9, s9, 0
	global_load_dwordx4 v[196:199], v75, s[8:9]
	s_add_u32 s8, s8, 0x8000
	s_addc_u32 s9, s9, 0
	global_load_dwordx4 v[200:203], v75, s[8:9]
	s_add_u32 s8, s8, 0x8000
	s_addc_u32 s9, s9, 0
	global_load_dwordx4 v[204:207], v75, s[8:9]
	s_add_u32 s6, s44, 0x3000000
	s_addc_u32 s7, s45, 0
	ds_read_b32 v226, v212
	ds_read_b32 v227, v212 offset:512
	ds_read_b32 v228, v212 offset:1024
	ds_read_b32 v229, v212 offset:1536
	ds_read_b32 v230, v212 offset:2048
	ds_read_b32 v231, v212 offset:2560
	ds_read_b32 v232, v212 offset:3072
	ds_read_b32 v233, v212 offset:3584
	ds_read_b32 v234, v212 offset:4096
	ds_read_b32 v235, v212 offset:4608
	ds_read_b32 v236, v212 offset:5120
	ds_read_b32 v237, v212 offset:5632
	ds_read_b32 v238, v212 offset:6144
	ds_read_b32 v239, v212 offset:6656
	ds_read_b32 v240, v212 offset:7168
	ds_read_b32 v241, v212 offset:7680
	s_waitcnt lgkmcnt(0)
	v_max_f32_e32 v226, v226, v226
	v_max_f32_e32 v227, v227, v227
	v_max_f32_e32 v228, v228, v228
	v_max_f32_e32 v229, v229, v229
	v_max_f32_e32 v230, v230, v230
	v_max_f32_e32 v231, v231, v231
	v_max_f32_e32 v232, v232, v232
	v_max_f32_e32 v233, v233, v233
	v_max_f32_e32 v234, v234, v234
	v_max_f32_e32 v235, v235, v235
	v_max_f32_e32 v236, v236, v236
	v_max_f32_e32 v237, v237, v237
	v_max_f32_e32 v238, v238, v238
	v_max_f32_e32 v239, v239, v239
	v_max_f32_e32 v240, v240, v240
	v_max_f32_e32 v241, v241, v241
	v_med3_f32 v226, v226, s62, v95
	v_med3_f32 v227, v227, s62, v95
	v_med3_f32 v228, v228, s62, v95
	v_med3_f32 v229, v229, s62, v95
	v_med3_f32 v230, v230, s62, v95
	v_med3_f32 v231, v231, s62, v95
	v_med3_f32 v232, v232, s62, v95
	v_med3_f32 v233, v233, s62, v95
	v_med3_f32 v234, v234, s62, v95
	v_med3_f32 v235, v235, s62, v95
	v_med3_f32 v236, v236, s62, v95
	v_med3_f32 v237, v237, s62, v95
	v_med3_f32 v238, v238, s62, v95
	v_med3_f32 v239, v239, s62, v95
	v_med3_f32 v240, v240, s62, v95
	v_med3_f32 v241, v241, s62, v95
	v_mov_b32_e32 v242, 0
	v_mov_b32_e32 v243, 0
	v_mov_b32_e32 v244, 0
	v_mov_b32_e32 v245, 0
	v_cvt_pk_fp8_f32 v242, v226, v227
	v_cvt_pk_fp8_f32 v243, v230, v231
	v_cvt_pk_fp8_f32 v244, v234, v235
	v_cvt_pk_fp8_f32 v245, v238, v239
	v_cvt_pk_fp8_f32 v242, v228, v229 op_sel:[0,0,1]
	v_cvt_pk_fp8_f32 v243, v232, v233 op_sel:[0,0,1]
	v_cvt_pk_fp8_f32 v244, v236, v237 op_sel:[0,0,1]
	v_cvt_pk_fp8_f32 v245, v240, v241 op_sel:[0,0,1]
	s_nop 0
	global_store_dwordx4 v79, v[242:245], s[6:7]
	ds_read_b32 v226, v214
	ds_read_b32 v227, v214 offset:512
	ds_read_b32 v228, v214 offset:1024
	ds_read_b32 v229, v214 offset:1536
	ds_read_b32 v230, v214 offset:2048
	ds_read_b32 v231, v214 offset:2560
	ds_read_b32 v232, v214 offset:3072
	ds_read_b32 v233, v214 offset:3584
	ds_read_b32 v234, v214 offset:4096
	ds_read_b32 v235, v214 offset:4608
	ds_read_b32 v236, v214 offset:5120
	ds_read_b32 v237, v214 offset:5632
	ds_read_b32 v238, v214 offset:6144
	ds_read_b32 v239, v214 offset:6656
	ds_read_b32 v240, v214 offset:7168
	ds_read_b32 v241, v214 offset:7680
	s_waitcnt lgkmcnt(0)
; #define GAS __attribute__((address_space(1)))
; #define LAS __attribute__((address_space(3)))
; #define LDS_WAIT() asm volatile("s_waitcnt lgkmcnt(0)" ::: "memory")
; __device__ __forceinline__ unsigned pk4_fp8(float a, float b, float c, float d) {
;     a = fminf(fmaxf(a, -448.f), 448.f); b = fminf(fmaxf(b, -448.f), 448.f); c = fminf(fmaxf(c, -448.f), 448.f); d = fminf(fmaxf(d, -448.f), 448.f);
;     int w = __builtin_amdgcn_cvt_pk_fp8_f32(a, b, 0, false); w = __builtin_amdgcn_cvt_pk_fp8_f32(c, d, w, true); return (unsigned)w; }
;     const int pr = item >> 1, kb = 2 * (pr / nblk) + (item & 1), nb = pr % nblk, k0 = 64 * kb, n0 = 32 * nb;
;     const int nr = n0 + (lane & 31); const int sc = MAP == 1 ? src_col_in(nr) : nr;
;     float v[32];
; #pragma unroll
;     for (int i = 0; i < 32; ++i) v[i] = sc >= 0 ? W[(size_t)(k0 + 2 * i + (lane >> 5)) * Nsrc + sc] : 0.f;
; #pragma unroll
;     for (int i = 0; i < 32; ++i) { const int k = k0 + 2 * i + (lane >> 5); float x = v[i] * wscale; if (KS) x *= (k < ksplit ? ksA[k] : ksB[k - ksplit]); scr[(2 * i + (lane >> 5)) * 33 + (lane & 31)] = x; }
;     LDS_WAIT(); asm volatile("" ::: "memory");
;     const int c = lane & 7;
; #pragma unroll
;     for (int j = 0; j < 4; ++j) { const int n = (lane >> 3) + 8 * j; const LAS float* s = scr + (8 * c) * 33 + n;
;         const unsigned long long o = (unsigned long long)pg8::pk4_fp8(s[0 * 33], s[1 * 33], s[2 * 33], s[3 * 33]) | ((unsigned long long)pg8::pk4_fp8(s[4 * 33], s[5 * 33], s[6 * 33], s[7 * 33]) << 32);
;         *(GAS unsigned long long*)(WT + (size_t)(n0 + n) * K + k0 + 8 * c) = o; }
;     LDS_WAIT(); asm volatile("" ::: "memory");
; }
	v_max_f32_e32 v226, v226, v226
	v_max_f32_e32 v227, v227, v227
	v_max_f32_e32 v228, v228, v228
	v_max_f32_e32 v229, v229, v229
	v_max_f32_e32 v230, v230, v230
	v_max_f32_e32 v231, v231, v231
	v_max_f32_e32 v232, v232, v232
	v_max_f32_e32 v233, v233, v233
	v_max_f32_e32 v234, v234, v234
	v_max_f32_e32 v235, v235, v235
	v_max_f32_e32 v236, v236, v236
	v_max_f32_e32 v237, v237, v237
	v_max_f32_e32 v238, v238, v238
	v_max_f32_e32 v239, v239, v239
	v_max_f32_e32 v240, v240, v240
	v_max_f32_e32 v241, v241, v241
	v_med3_f32 v226, v226, s62, v95
	v_med3_f32 v227, v227, s62, v95
	v_med3_f32 v228, v228, s62, v95
	v_med3_f32 v229, v229, s62, v95
	v_med3_f32 v230, v230, s62, v95
	v_med3_f32 v231, v231, s62, v95
	v_med3_f32 v232, v232, s62, v95
	v_med3_f32 v233, v233, s62, v95
	v_med3_f32 v234, v234, s62, v95
	v_med3_f32 v235, v235, s62, v95
	v_med3_f32 v236, v236, s62, v95
	v_med3_f32 v237, v237, s62, v95
	v_med3_f32 v238, v238, s62, v95
	v_med3_f32 v239, v239, s62, v95
	v_med3_f32 v240, v240, s62, v95
	v_med3_f32 v241, v241, s62, v95
	v_mov_b32_e32 v242, 0
	v_mov_b32_e32 v243, 0
	v_mov_b32_e32 v244, 0
	v_mov_b32_e32 v245, 0
	v_cvt_pk_fp8_f32 v242, v226, v227
	v_cvt_pk_fp8_f32 v243, v230, v231
	v_cvt_pk_fp8_f32 v244, v234, v235
	v_cvt_pk_fp8_f32 v245, v238, v239
	v_cvt_pk_fp8_f32 v242, v228, v229 op_sel:[0,0,1]
	v_cvt_pk_fp8_f32 v243, v232, v233 op_sel:[0,0,1]
	v_cvt_pk_fp8_f32 v244, v236, v237 op_sel:[0,0,1]
	v_cvt_pk_fp8_f32 v245, v240, v241 op_sel:[0,0,1]
	s_nop 0
	global_store_dwordx4 v80, v[242:245], s[6:7]
	s_waitcnt vmcnt(12)
	v_mul_f32_e32 v144, 0x43000000, v144
	v_mul_f32_e32 v145, 0x43000000, v145
	v_mul_f32_e32 v146, 0x43000000, v146
	v_mul_f32_e32 v147, 0x43000000, v147
	ds_write_b128 v209, v[144:147]
	v_mul_f32_e32 v148, 0x43000000, v148
	v_mul_f32_e32 v149, 0x43000000, v149
	v_mul_f32_e32 v150, 0x43000000, v150
	v_mul_f32_e32 v151, 0x43000000, v151
	ds_write_b128 v209, v[148:151] offset:1024
	v_mul_f32_e32 v152, 0x43000000, v152
	v_mul_f32_e32 v153, 0x43000000, v153
	v_mul_f32_e32 v154, 0x43000000, v154
	v_mul_f32_e32 v155, 0x43000000, v155
	ds_write_b128 v209, v[152:155] offset:2048
	v_mul_f32_e32 v156, 0x43000000, v156
	v_mul_f32_e32 v157, 0x43000000, v157
	v_mul_f32_e32 v158, 0x43000000, v158
	v_mul_f32_e32 v159, 0x43000000, v159
	ds_write_b128 v209, v[156:159] offset:3072
	v_mul_f32_e32 v160, 0x43000000, v160
	v_mul_f32_e32 v161, 0x43000000, v161
	v_mul_f32_e32 v162, 0x43000000, v162
	v_mul_f32_e32 v163, 0x43000000, v163
	ds_write_b128 v209, v[160:163] offset:4096
	v_mul_f32_e32 v164, 0x43000000, v164
	v_mul_f32_e32 v165, 0x43000000, v165
	v_mul_f32_e32 v166, 0x43000000, v166
	v_mul_f32_e32 v167, 0x43000000, v167
	ds_write_b128 v209, v[164:167] offset:5120
	v_mul_f32_e32 v168, 0x43000000, v168
	v_mul_f32_e32 v169, 0x43000000, v169
	v_mul_f32_e32 v170, 0x43000000, v170
	v_mul_f32_e32 v171, 0x43000000, v171
	ds_write_b128 v209, v[168:171] offset:6144
	v_mul_f32_e32 v172, 0x43000000, v172
	v_mul_f32_e32 v173, 0x43000000, v173
	v_mul_f32_e32 v174, 0x43000000, v174
	v_mul_f32_e32 v175, 0x43000000, v175
	ds_write_b128 v209, v[172:175] offset:7168
	s_waitcnt lgkmcnt(0)
	s_barrier
	s_add_u32 s8, s42, 0x4002000
	s_addc_u32 s9, s43, 0
	global_load_dwordx4 v[144:147], v75, s[8:9]
	s_add_u32 s8, s8, 0x8000
	s_addc_u32 s9, s9, 0
	global_load_dwordx4 v[148:151], v75, s[8:9]
	s_add_u32 s8, s8, 0x8000
	s_addc_u32 s9, s9, 0
	global_load_dwordx4 v[152:155], v75, s[8:9]
	s_add_u32 s8, s8, 0x8000
	s_addc_u32 s9, s9, 0
	global_load_dwordx4 v[156:159], v75, s[8:9]
	s_add_u32 s8, s8, 0x8000
	s_addc_u32 s9, s9, 0
	global_load_dwordx4 v[160:163], v75, s[8:9]
	s_add_u32 s8, s8, 0x8000
	s_addc_u32 s9, s9, 0
	global_load_dwordx4 v[164:167], v75, s[8:9]
	s_add_u32 s8, s8, 0x8000
	s_addc_u32 s9, s9, 0
	global_load_dwordx4 v[168:171], v75, s[8:9]
	s_add_u32 s8, s8, 0x8000
	s_addc_u32 s9, s9, 0
	global_load_dwordx4 v[172:175], v75, s[8:9]
	s_add_u32 s6, s44, 0x1000
	s_addc_u32 s7, s45, 0
	ds_read_b32 v226, v211
	ds_read_b32 v227, v211 offset:512
	ds_read_b32 v228, v211 offset:1024
	ds_read_b32 v229, v211 offset:1536
	ds_read_b32 v230, v211 offset:2048
	ds_read_b32 v231, v211 offset:2560
	ds_read_b32 v232, v211 offset:3072
	ds_read_b32 v233, v211 offset:3584
	ds_read_b32 v234, v211 offset:4096
	ds_read_b32 v235, v211 offset:4608
	ds_read_b32 v236, v211 offset:5120
	ds_read_b32 v237, v211 offset:5632
	ds_read_b32 v238, v211 offset:6144
	ds_read_b32 v239, v211 offset:6656
	ds_read_b32 v240, v211 offset:7168
	ds_read_b32 v241, v211 offset:7680
	s_waitcnt lgkmcnt(0)
	v_max_f32_e32 v226, v226, v226
	v_max_f32_e32 v227, v227, v227
	v_max_f32_e32 v228, v228, v228
	v_max_f32_e32 v229, v229, v229
	v_max_f32_e32 v230, v230, v230
	v_max_f32_e32 v231, v231, v231
	v_max_f32_e32 v232, v232, v232
	v_max_f32_e32 v233, v233, v233
	v_max_f32_e32 v234, v234, v234
	v_max_f32_e32 v235, v235, v235
	v_max_f32_e32 v236, v236, v236
	v_max_f32_e32 v237, v237, v237
	v_max_f32_e32 v238, v238, v238
	v_max_f32_e32 v239, v239, v239
	v_max_f32_e32 v240, v240, v240
	v_max_f32_e32 v241, v241, v241
	v_med3_f32 v226, v226, s62, v95
	v_med3_f32 v227, v227, s62, v95
	v_med3_f32 v228, v228, s62, v95
	v_med3_f32 v229, v229, s62, v95
	v_med3_f32 v230, v230, s62, v95
	v_med3_f32 v231, v231, s62, v95
	v_med3_f32 v232, v232, s62, v95
	v_med3_f32 v233, v233, s62, v95
	v_med3_f32 v234, v234, s62, v95
	v_med3_f32 v235, v235, s62, v95
	v_med3_f32 v236, v236, s62, v95
	v_med3_f32 v237, v237, s62, v95
	v_med3_f32 v238, v238, s62, v95
	v_med3_f32 v239, v239, s62, v95
	v_med3_f32 v240, v240, s62, v95
	v_med3_f32 v241, v241, s62, v95
	v_mov_b32_e32 v242, 0
	v_mov_b32_e32 v243, 0
	v_mov_b32_e32 v244, 0
	v_mov_b32_e32 v245, 0
	v_cvt_pk_fp8_f32 v242, v226, v227
	v_cvt_pk_fp8_f32 v243, v230, v231
	v_cvt_pk_fp8_f32 v244, v234, v235
	v_cvt_pk_fp8_f32 v245, v238, v239
	v_cvt_pk_fp8_f32 v242, v228, v229 op_sel:[0,0,1]
	v_cvt_pk_fp8_f32 v243, v232, v233 op_sel:[0,0,1]
	v_cvt_pk_fp8_f32 v244, v236, v237 op_sel:[0,0,1]
	v_cvt_pk_fp8_f32 v245, v240, v241 op_sel:[0,0,1]
	s_nop 0
	global_store_dwordx4 v79, v[242:245], s[6:7]
	ds_read_b32 v226, v213
	ds_read_b32 v227, v213 offset:512
	ds_read_b32 v228, v213 offset:1024
	ds_read_b32 v229, v213 offset:1536
	ds_read_b32 v230, v213 offset:2048
	ds_read_b32 v231, v213 offset:2560
	ds_read_b32 v232, v213 offset:3072
	ds_read_b32 v233, v213 offset:3584
	ds_read_b32 v234, v213 offset:4096
	ds_read_b32 v235, v213 offset:4608
	ds_read_b32 v236, v213 offset:5120
	ds_read_b32 v237, v213 offset:5632
	ds_read_b32 v238, v213 offset:6144
	ds_read_b32 v239, v213 offset:6656
	ds_read_b32 v240, v213 offset:7168
	ds_read_b32 v241, v213 offset:7680
	s_waitcnt lgkmcnt(0)
; #define GAS __attribute__((address_space(1)))
; #define LAS __attribute__((address_space(3)))
; #define LDS_WAIT() asm volatile("s_waitcnt lgkmcnt(0)" ::: "memory")
; __device__ __forceinline__ unsigned pk4_fp8(float a, float b, float c, float d) {
;     a = fminf(fmaxf(a, -448.f), 448.f); b = fminf(fmaxf(b, -448.f), 448.f); c = fminf(fmaxf(c, -448.f), 448.f); d = fminf(fmaxf(d, -448.f), 448.f);
;     int w = __builtin_amdgcn_cvt_pk_fp8_f32(a, b, 0, false); w = __builtin_amdgcn_cvt_pk_fp8_f32(c, d, w, true); return (unsigned)w; }
;     const int pr = item >> 1, kb = 2 * (pr / nblk) + (item & 1), nb = pr % nblk, k0 = 64 * kb, n0 = 32 * nb;
;     const int nr = n0 + (lane & 31); const int sc = MAP == 1 ? src_col_in(nr) : nr;
;     float v[32];
; #pragma unroll
;     for (int i = 0; i < 32; ++i) v[i] = sc >= 0 ? W[(size_t)(k0 + 2 * i + (lane >> 5)) * Nsrc + sc] : 0.f;
; #pragma unroll
;     for (int i = 0; i < 32; ++i) { const int k = k0 + 2 * i + (lane >> 5); float x = v[i] * wscale; if (KS) x *= (k < ksplit ? ksA[k] : ksB[k - ksplit]); scr[(2 * i + (lane >> 5)) * 33 + (lane & 31)] = x; }
;     LDS_WAIT(); asm volatile("" ::: "memory");
;     const int c = lane & 7;
; #pragma unroll
;     for (int j = 0; j < 4; ++j) { const int n = (lane >> 3) + 8 * j; const LAS float* s = scr + (8 * c) * 33 + n;
;         const unsigned long long o = (unsigned long long)pg8::pk4_fp8(s[0 * 33], s[1 * 33], s[2 * 33], s[3 * 33]) | ((unsigned long long)pg8::pk4_fp8(s[4 * 33], s[5 * 33], s[6 * 33], s[7 * 33]) << 32);
;         *(GAS unsigned long long*)(WT + (size_t)(n0 + n) * K + k0 + 8 * c) = o; }
;     LDS_WAIT(); asm volatile("" ::: "memory");
; }
	v_max_f32_e32 v226, v226, v226
	v_max_f32_e32 v227, v227, v227
	v_max_f32_e32 v228, v228, v228
	v_max_f32_e32 v229, v229, v229
	v_max_f32_e32 v230, v230, v230
	v_max_f32_e32 v231, v231, v231
	v_max_f32_e32 v232, v232, v232
	v_max_f32_e32 v233, v233, v233
	v_max_f32_e32 v234, v234, v234
	v_max_f32_e32 v235, v235, v235
	v_max_f32_e32 v236, v236, v236
	v_max_f32_e32 v237, v237, v237
	v_max_f32_e32 v238, v238, v238
	v_max_f32_e32 v239, v239, v239
	v_max_f32_e32 v240, v240, v240
	v_max_f32_e32 v241, v241, v241
	v_med3_f32 v226, v226, s62, v95
	v_med3_f32 v227, v227, s62, v95
	v_med3_f32 v228, v228, s62, v95
	v_med3_f32 v229, v229, s62, v95
	v_med3_f32 v230, v230, s62, v95
	v_med3_f32 v231, v231, s62, v95
	v_med3_f32 v232, v232, s62, v95
	v_med3_f32 v233, v233, s62, v95
	v_med3_f32 v234, v234, s62, v95
	v_med3_f32 v235, v235, s62, v95
	v_med3_f32 v236, v236, s62, v95
	v_med3_f32 v237, v237, s62, v95
	v_med3_f32 v238, v238, s62, v95
	v_med3_f32 v239, v239, s62, v95
	v_med3_f32 v240, v240, s62, v95
	v_med3_f32 v241, v241, s62, v95
	v_mov_b32_e32 v242, 0
	v_mov_b32_e32 v243, 0
	v_mov_b32_e32 v244, 0
	v_mov_b32_e32 v245, 0
	v_cvt_pk_fp8_f32 v242, v226, v227
	v_cvt_pk_fp8_f32 v243, v230, v231
	v_cvt_pk_fp8_f32 v244, v234, v235
	v_cvt_pk_fp8_f32 v245, v238, v239
	v_cvt_pk_fp8_f32 v242, v228, v229 op_sel:[0,0,1]
	v_cvt_pk_fp8_f32 v243, v232, v233 op_sel:[0,0,1]
	v_cvt_pk_fp8_f32 v244, v236, v237 op_sel:[0,0,1]
	v_cvt_pk_fp8_f32 v245, v240, v241 op_sel:[0,0,1]
	s_nop 0
	global_store_dwordx4 v80, v[242:245], s[6:7]
	s_waitcnt vmcnt(12)
	v_mul_f32_e32 v176, 0x43000000, v176
	v_mul_f32_e32 v177, 0x43000000, v177
	v_mul_f32_e32 v178, 0x43000000, v178
	v_mul_f32_e32 v179, 0x43000000, v179
	ds_write_b128 v210, v[176:179]
	v_mul_f32_e32 v180, 0x43000000, v180
	v_mul_f32_e32 v181, 0x43000000, v181
	v_mul_f32_e32 v182, 0x43000000, v182
	v_mul_f32_e32 v183, 0x43000000, v183
	ds_write_b128 v210, v[180:183] offset:1024
	v_mul_f32_e32 v184, 0x43000000, v184
	v_mul_f32_e32 v185, 0x43000000, v185
	v_mul_f32_e32 v186, 0x43000000, v186
	v_mul_f32_e32 v187, 0x43000000, v187
	ds_write_b128 v210, v[184:187] offset:2048
	v_mul_f32_e32 v188, 0x43000000, v188
	v_mul_f32_e32 v189, 0x43000000, v189
	v_mul_f32_e32 v190, 0x43000000, v190
	v_mul_f32_e32 v191, 0x43000000, v191
	ds_write_b128 v210, v[188:191] offset:3072
	v_mul_f32_e32 v192, 0x43000000, v192
	v_mul_f32_e32 v193, 0x43000000, v193
	v_mul_f32_e32 v194, 0x43000000, v194
	v_mul_f32_e32 v195, 0x43000000, v195
	ds_write_b128 v210, v[192:195] offset:4096
	v_mul_f32_e32 v196, 0x43000000, v196
	v_mul_f32_e32 v197, 0x43000000, v197
	v_mul_f32_e32 v198, 0x43000000, v198
	v_mul_f32_e32 v199, 0x43000000, v199
	ds_write_b128 v210, v[196:199] offset:5120
	v_mul_f32_e32 v200, 0x43000000, v200
	v_mul_f32_e32 v201, 0x43000000, v201
	v_mul_f32_e32 v202, 0x43000000, v202
	v_mul_f32_e32 v203, 0x43000000, v203
	ds_write_b128 v210, v[200:203] offset:6144
	v_mul_f32_e32 v204, 0x43000000, v204
	v_mul_f32_e32 v205, 0x43000000, v205
	v_mul_f32_e32 v206, 0x43000000, v206
	v_mul_f32_e32 v207, 0x43000000, v207
	ds_write_b128 v210, v[204:207] offset:7168
	s_waitcnt lgkmcnt(0)
	s_barrier
	s_add_u32 s8, s42, 0x4003000
	s_addc_u32 s9, s43, 0
	global_load_dwordx4 v[176:179], v75, s[8:9]
	s_add_u32 s8, s8, 0x8000
	s_addc_u32 s9, s9, 0
	global_load_dwordx4 v[180:183], v75, s[8:9]
	s_add_u32 s8, s8, 0x8000
	s_addc_u32 s9, s9, 0
	global_load_dwordx4 v[184:187], v75, s[8:9]
	s_add_u32 s8, s8, 0x8000
	s_addc_u32 s9, s9, 0
	global_load_dwordx4 v[188:191], v75, s[8:9]
	s_add_u32 s8, s8, 0x8000
	s_addc_u32 s9, s9, 0
	global_load_dwordx4 v[192:195], v75, s[8:9]
	s_add_u32 s8, s8, 0x8000
	s_addc_u32 s9, s9, 0
	global_load_dwordx4 v[196:199], v75, s[8:9]
	s_add_u32 s8, s8, 0x8000
	s_addc_u32 s9, s9, 0
	global_load_dwordx4 v[200:203], v75, s[8:9]
	s_add_u32 s8, s8, 0x8000
	s_addc_u32 s9, s9, 0
	global_load_dwordx4 v[204:207], v75, s[8:9]
	s_add_u32 s6, s44, 0x1001000
	s_addc_u32 s7, s45, 0
	ds_read_b32 v226, v212
	ds_read_b32 v227, v212 offset:512
	ds_read_b32 v228, v212 offset:1024
	ds_read_b32 v229, v212 offset:1536
	ds_read_b32 v230, v212 offset:2048
	ds_read_b32 v231, v212 offset:2560
	ds_read_b32 v232, v212 offset:3072
	ds_read_b32 v233, v212 offset:3584
	ds_read_b32 v234, v212 offset:4096
	ds_read_b32 v235, v212 offset:4608
	ds_read_b32 v236, v212 offset:5120
	ds_read_b32 v237, v212 offset:5632
	ds_read_b32 v238, v212 offset:6144
	ds_read_b32 v239, v212 offset:6656
	ds_read_b32 v240, v212 offset:7168
	ds_read_b32 v241, v212 offset:7680
	s_waitcnt lgkmcnt(0)
	v_max_f32_e32 v226, v226, v226
	v_max_f32_e32 v227, v227, v227
	v_max_f32_e32 v228, v228, v228
	v_max_f32_e32 v229, v229, v229
	v_max_f32_e32 v230, v230, v230
	v_max_f32_e32 v231, v231, v231
	v_max_f32_e32 v232, v232, v232
	v_max_f32_e32 v233, v233, v233
	v_max_f32_e32 v234, v234, v234
	v_max_f32_e32 v235, v235, v235
	v_max_f32_e32 v236, v236, v236
	v_max_f32_e32 v237, v237, v237
	v_max_f32_e32 v238, v238, v238
	v_max_f32_e32 v239, v239, v239
	v_max_f32_e32 v240, v240, v240
	v_max_f32_e32 v241, v241, v241
	v_med3_f32 v226, v226, s62, v95
	v_med3_f32 v227, v227, s62, v95
	v_med3_f32 v228, v228, s62, v95
	v_med3_f32 v229, v229, s62, v95
	v_med3_f32 v230, v230, s62, v95
	v_med3_f32 v231, v231, s62, v95
	v_med3_f32 v232, v232, s62, v95
	v_med3_f32 v233, v233, s62, v95
	v_med3_f32 v234, v234, s62, v95
	v_med3_f32 v235, v235, s62, v95
	v_med3_f32 v236, v236, s62, v95
	v_med3_f32 v237, v237, s62, v95
	v_med3_f32 v238, v238, s62, v95
	v_med3_f32 v239, v239, s62, v95
	v_med3_f32 v240, v240, s62, v95
	v_med3_f32 v241, v241, s62, v95
	v_mov_b32_e32 v242, 0
	v_mov_b32_e32 v243, 0
	v_mov_b32_e32 v244, 0
	v_mov_b32_e32 v245, 0
	v_cvt_pk_fp8_f32 v242, v226, v227
	v_cvt_pk_fp8_f32 v243, v230, v231
	v_cvt_pk_fp8_f32 v244, v234, v235
	v_cvt_pk_fp8_f32 v245, v238, v239
	v_cvt_pk_fp8_f32 v242, v228, v229 op_sel:[0,0,1]
	v_cvt_pk_fp8_f32 v243, v232, v233 op_sel:[0,0,1]
	v_cvt_pk_fp8_f32 v244, v236, v237 op_sel:[0,0,1]
	v_cvt_pk_fp8_f32 v245, v240, v241 op_sel:[0,0,1]
	s_nop 0
	global_store_dwordx4 v79, v[242:245], s[6:7]
	ds_read_b32 v226, v214
	ds_read_b32 v227, v214 offset:512
	ds_read_b32 v228, v214 offset:1024
	ds_read_b32 v229, v214 offset:1536
	ds_read_b32 v230, v214 offset:2048
	ds_read_b32 v231, v214 offset:2560
	ds_read_b32 v232, v214 offset:3072
	ds_read_b32 v233, v214 offset:3584
	ds_read_b32 v234, v214 offset:4096
	ds_read_b32 v235, v214 offset:4608
	ds_read_b32 v236, v214 offset:5120
	ds_read_b32 v237, v214 offset:5632
	ds_read_b32 v238, v214 offset:6144
	ds_read_b32 v239, v214 offset:6656
	ds_read_b32 v240, v214 offset:7168
	ds_read_b32 v241, v214 offset:7680
	s_waitcnt lgkmcnt(0)
; #define GAS __attribute__((address_space(1)))
; #define LAS __attribute__((address_space(3)))
; #define LDS_WAIT() asm volatile("s_waitcnt lgkmcnt(0)" ::: "memory")
; __device__ __forceinline__ unsigned pk4_fp8(float a, float b, float c, float d) {
;     a = fminf(fmaxf(a, -448.f), 448.f); b = fminf(fmaxf(b, -448.f), 448.f); c = fminf(fmaxf(c, -448.f), 448.f); d = fminf(fmaxf(d, -448.f), 448.f);
;     int w = __builtin_amdgcn_cvt_pk_fp8_f32(a, b, 0, false); w = __builtin_amdgcn_cvt_pk_fp8_f32(c, d, w, true); return (unsigned)w; }
;     const int pr = item >> 1, kb = 2 * (pr / nblk) + (item & 1), nb = pr % nblk, k0 = 64 * kb, n0 = 32 * nb;
;     const int nr = n0 + (lane & 31); const int sc = MAP == 1 ? src_col_in(nr) : nr;
;     float v[32];
; #pragma unroll
;     for (int i = 0; i < 32; ++i) v[i] = sc >= 0 ? W[(size_t)(k0 + 2 * i + (lane >> 5)) * Nsrc + sc] : 0.f;
; #pragma unroll
;     for (int i = 0; i < 32; ++i) { const int k = k0 + 2 * i + (lane >> 5); float x = v[i] * wscale; if (KS) x *= (k < ksplit ? ksA[k] : ksB[k - ksplit]); scr[(2 * i + (lane >> 5)) * 33 + (lane & 31)] = x; }
;     LDS_WAIT(); asm volatile("" ::: "memory");
;     const int c = lane & 7;
; #pragma unroll
;     for (int j = 0; j < 4; ++j) { const int n = (lane >> 3) + 8 * j; const LAS float* s = scr + (8 * c) * 33 + n;
;         const unsigned long long o = (unsigned long long)pg8::pk4_fp8(s[0 * 33], s[1 * 33], s[2 * 33], s[3 * 33]) | ((unsigned long long)pg8::pk4_fp8(s[4 * 33], s[5 * 33], s[6 * 33], s[7 * 33]) << 32);
;         *(GAS unsigned long long*)(WT + (size_t)(n0 + n) * K + k0 + 8 * c) = o; }
;     LDS_WAIT(); asm volatile("" ::: "memory");
; }
	v_max_f32_e32 v226, v226, v226
	v_max_f32_e32 v227, v227, v227
	v_max_f32_e32 v228, v228, v228
	v_max_f32_e32 v229, v229, v229
	v_max_f32_e32 v230, v230, v230
	v_max_f32_e32 v231, v231, v231
	v_max_f32_e32 v232, v232, v232
	v_max_f32_e32 v233, v233, v233
	v_max_f32_e32 v234, v234, v234
	v_max_f32_e32 v235, v235, v235
	v_max_f32_e32 v236, v236, v236
	v_max_f32_e32 v237, v237, v237
	v_max_f32_e32 v238, v238, v238
	v_max_f32_e32 v239, v239, v239
	v_max_f32_e32 v240, v240, v240
	v_max_f32_e32 v241, v241, v241
	v_med3_f32 v226, v226, s62, v95
	v_med3_f32 v227, v227, s62, v95
	v_med3_f32 v228, v228, s62, v95
	v_med3_f32 v229, v229, s62, v95
	v_med3_f32 v230, v230, s62, v95
	v_med3_f32 v231, v231, s62, v95
	v_med3_f32 v232, v232, s62, v95
	v_med3_f32 v233, v233, s62, v95
	v_med3_f32 v234, v234, s62, v95
	v_med3_f32 v235, v235, s62, v95
	v_med3_f32 v236, v236, s62, v95
	v_med3_f32 v237, v237, s62, v95
	v_med3_f32 v238, v238, s62, v95
	v_med3_f32 v239, v239, s62, v95
	v_med3_f32 v240, v240, s62, v95
	v_med3_f32 v241, v241, s62, v95
	v_mov_b32_e32 v242, 0
	v_mov_b32_e32 v243, 0
	v_mov_b32_e32 v244, 0
	v_mov_b32_e32 v245, 0
	v_cvt_pk_fp8_f32 v242, v226, v227
	v_cvt_pk_fp8_f32 v243, v230, v231
	v_cvt_pk_fp8_f32 v244, v234, v235
	v_cvt_pk_fp8_f32 v245, v238, v239
	v_cvt_pk_fp8_f32 v242, v228, v229 op_sel:[0,0,1]
	v_cvt_pk_fp8_f32 v243, v232, v233 op_sel:[0,0,1]
	v_cvt_pk_fp8_f32 v244, v236, v237 op_sel:[0,0,1]
	v_cvt_pk_fp8_f32 v245, v240, v241 op_sel:[0,0,1]
	s_nop 0
	global_store_dwordx4 v80, v[242:245], s[6:7]
	s_waitcnt vmcnt(12)
	v_mul_f32_e32 v144, 0x43000000, v144
	v_mul_f32_e32 v145, 0x43000000, v145
	v_mul_f32_e32 v146, 0x43000000, v146
	v_mul_f32_e32 v147, 0x43000000, v147
	ds_write_b128 v209, v[144:147]
	v_mul_f32_e32 v148, 0x43000000, v148
	v_mul_f32_e32 v149, 0x43000000, v149
	v_mul_f32_e32 v150, 0x43000000, v150
	v_mul_f32_e32 v151, 0x43000000, v151
	ds_write_b128 v209, v[148:151] offset:1024
	v_mul_f32_e32 v152, 0x43000000, v152
	v_mul_f32_e32 v153, 0x43000000, v153
	v_mul_f32_e32 v154, 0x43000000, v154
	v_mul_f32_e32 v155, 0x43000000, v155
	ds_write_b128 v209, v[152:155] offset:2048
	v_mul_f32_e32 v156, 0x43000000, v156
	v_mul_f32_e32 v157, 0x43000000, v157
	v_mul_f32_e32 v158, 0x43000000, v158
	v_mul_f32_e32 v159, 0x43000000, v159
	ds_write_b128 v209, v[156:159] offset:3072
	v_mul_f32_e32 v160, 0x43000000, v160
	v_mul_f32_e32 v161, 0x43000000, v161
	v_mul_f32_e32 v162, 0x43000000, v162
	v_mul_f32_e32 v163, 0x43000000, v163
	ds_write_b128 v209, v[160:163] offset:4096
	v_mul_f32_e32 v164, 0x43000000, v164
	v_mul_f32_e32 v165, 0x43000000, v165
	v_mul_f32_e32 v166, 0x43000000, v166
	v_mul_f32_e32 v167, 0x43000000, v167
	ds_write_b128 v209, v[164:167] offset:5120
	v_mul_f32_e32 v168, 0x43000000, v168
	v_mul_f32_e32 v169, 0x43000000, v169
	v_mul_f32_e32 v170, 0x43000000, v170
	v_mul_f32_e32 v171, 0x43000000, v171
	ds_write_b128 v209, v[168:171] offset:6144
	v_mul_f32_e32 v172, 0x43000000, v172
	v_mul_f32_e32 v173, 0x43000000, v173
	v_mul_f32_e32 v174, 0x43000000, v174
	v_mul_f32_e32 v175, 0x43000000, v175
	ds_write_b128 v209, v[172:175] offset:7168
	s_waitcnt lgkmcnt(0)
	s_barrier
	s_add_u32 s8, s42, 0x8000000
	s_addc_u32 s9, s43, 0
	global_load_dwordx4 v[144:147], v75, s[8:9]
	s_add_u32 s8, s8, 0x8000
	s_addc_u32 s9, s9, 0
	global_load_dwordx4 v[148:151], v75, s[8:9]
	s_add_u32 s8, s8, 0x8000
	s_addc_u32 s9, s9, 0
	global_load_dwordx4 v[152:155], v75, s[8:9]
	s_add_u32 s8, s8, 0x8000
	s_addc_u32 s9, s9, 0
	global_load_dwordx4 v[156:159], v75, s[8:9]
	s_add_u32 s8, s8, 0x8000
	s_addc_u32 s9, s9, 0
	global_load_dwordx4 v[160:163], v75, s[8:9]
	s_add_u32 s8, s8, 0x8000
	s_addc_u32 s9, s9, 0
	global_load_dwordx4 v[164:167], v75, s[8:9]
	s_add_u32 s8, s8, 0x8000
	s_addc_u32 s9, s9, 0
	global_load_dwordx4 v[168:171], v75, s[8:9]
	s_add_u32 s8, s8, 0x8000
	s_addc_u32 s9, s9, 0
	global_load_dwordx4 v[172:175], v75, s[8:9]
	s_add_u32 s6, s44, 0x2001000
	s_addc_u32 s7, s45, 0
	ds_read_b32 v226, v211
	ds_read_b32 v227, v211 offset:512
	ds_read_b32 v228, v211 offset:1024
	ds_read_b32 v229, v211 offset:1536
	ds_read_b32 v230, v211 offset:2048
	ds_read_b32 v231, v211 offset:2560
	ds_read_b32 v232, v211 offset:3072
	ds_read_b32 v233, v211 offset:3584
	ds_read_b32 v234, v211 offset:4096
	ds_read_b32 v235, v211 offset:4608
	ds_read_b32 v236, v211 offset:5120
	ds_read_b32 v237, v211 offset:5632
	ds_read_b32 v238, v211 offset:6144
	ds_read_b32 v239, v211 offset:6656
	ds_read_b32 v240, v211 offset:7168
	ds_read_b32 v241, v211 offset:7680
	s_waitcnt lgkmcnt(0)
	v_max_f32_e32 v226, v226, v226
	v_max_f32_e32 v227, v227, v227
	v_max_f32_e32 v228, v228, v228
	v_max_f32_e32 v229, v229, v229
	v_max_f32_e32 v230, v230, v230
	v_max_f32_e32 v231, v231, v231
	v_max_f32_e32 v232, v232, v232
	v_max_f32_e32 v233, v233, v233
	v_max_f32_e32 v234, v234, v234
	v_max_f32_e32 v235, v235, v235
	v_max_f32_e32 v236, v236, v236
	v_max_f32_e32 v237, v237, v237
	v_max_f32_e32 v238, v238, v238
	v_max_f32_e32 v239, v239, v239
	v_max_f32_e32 v240, v240, v240
	v_max_f32_e32 v241, v241, v241
	v_med3_f32 v226, v226, s62, v95
	v_med3_f32 v227, v227, s62, v95
	v_med3_f32 v228, v228, s62, v95
	v_med3_f32 v229, v229, s62, v95
	v_med3_f32 v230, v230, s62, v95
	v_med3_f32 v231, v231, s62, v95
	v_med3_f32 v232, v232, s62, v95
	v_med3_f32 v233, v233, s62, v95
	v_med3_f32 v234, v234, s62, v95
	v_med3_f32 v235, v235, s62, v95
	v_med3_f32 v236, v236, s62, v95
	v_med3_f32 v237, v237, s62, v95
	v_med3_f32 v238, v238, s62, v95
	v_med3_f32 v239, v239, s62, v95
	v_med3_f32 v240, v240, s62, v95
	v_med3_f32 v241, v241, s62, v95
	v_mov_b32_e32 v242, 0
	v_mov_b32_e32 v243, 0
	v_mov_b32_e32 v244, 0
	v_mov_b32_e32 v245, 0
	v_cvt_pk_fp8_f32 v242, v226, v227
	v_cvt_pk_fp8_f32 v243, v230, v231
	v_cvt_pk_fp8_f32 v244, v234, v235
	v_cvt_pk_fp8_f32 v245, v238, v239
	v_cvt_pk_fp8_f32 v242, v228, v229 op_sel:[0,0,1]
	v_cvt_pk_fp8_f32 v243, v232, v233 op_sel:[0,0,1]
	v_cvt_pk_fp8_f32 v244, v236, v237 op_sel:[0,0,1]
	v_cvt_pk_fp8_f32 v245, v240, v241 op_sel:[0,0,1]
	s_nop 0
	global_store_dwordx4 v79, v[242:245], s[6:7]
	ds_read_b32 v226, v213
	ds_read_b32 v227, v213 offset:512
	ds_read_b32 v228, v213 offset:1024
	ds_read_b32 v229, v213 offset:1536
	ds_read_b32 v230, v213 offset:2048
	ds_read_b32 v231, v213 offset:2560
	ds_read_b32 v232, v213 offset:3072
	ds_read_b32 v233, v213 offset:3584
	ds_read_b32 v234, v213 offset:4096
	ds_read_b32 v235, v213 offset:4608
	ds_read_b32 v236, v213 offset:5120
	ds_read_b32 v237, v213 offset:5632
	ds_read_b32 v238, v213 offset:6144
	ds_read_b32 v239, v213 offset:6656
	ds_read_b32 v240, v213 offset:7168
	ds_read_b32 v241, v213 offset:7680
	s_waitcnt lgkmcnt(0)
; #define GAS __attribute__((address_space(1)))
; #define LAS __attribute__((address_space(3)))
; #define LDS_WAIT() asm volatile("s_waitcnt lgkmcnt(0)" ::: "memory")
; __device__ __forceinline__ unsigned pk4_fp8(float a, float b, float c, float d) {
;     a = fminf(fmaxf(a, -448.f), 448.f); b = fminf(fmaxf(b, -448.f), 448.f); c = fminf(fmaxf(c, -448.f), 448.f); d = fminf(fmaxf(d, -448.f), 448.f);
;     int w = __builtin_amdgcn_cvt_pk_fp8_f32(a, b, 0, false); w = __builtin_amdgcn_cvt_pk_fp8_f32(c, d, w, true); return (unsigned)w; }
;     const int pr = item >> 1, kb = 2 * (pr / nblk) + (item & 1), nb = pr % nblk, k0 = 64 * kb, n0 = 32 * nb;
;     const int nr = n0 + (lane & 31); const int sc = MAP == 1 ? src_col_in(nr) : nr;
;     float v[32];
; #pragma unroll
;     for (int i = 0; i < 32; ++i) v[i] = sc >= 0 ? W[(size_t)(k0 + 2 * i + (lane >> 5)) * Nsrc + sc] : 0.f;
; #pragma unroll
;     for (int i = 0; i < 32; ++i) { const int k = k0 + 2 * i + (lane >> 5); float x = v[i] * wscale; if (KS) x *= (k < ksplit ? ksA[k] : ksB[k - ksplit]); scr[(2 * i + (lane >> 5)) * 33 + (lane & 31)] = x; }
;     LDS_WAIT(); asm volatile("" ::: "memory");
;     const int c = lane & 7;
; #pragma unroll
;     for (int j = 0; j < 4; ++j) { const int n = (lane >> 3) + 8 * j; const LAS float* s = scr + (8 * c) * 33 + n;
;         const unsigned long long o = (unsigned long long)pg8::pk4_fp8(s[0 * 33], s[1 * 33], s[2 * 33], s[3 * 33]) | ((unsigned long long)pg8::pk4_fp8(s[4 * 33], s[5 * 33], s[6 * 33], s[7 * 33]) << 32);
;         *(GAS unsigned long long*)(WT + (size_t)(n0 + n) * K + k0 + 8 * c) = o; }
;     LDS_WAIT(); asm volatile("" ::: "memory");
; }
	v_max_f32_e32 v226, v226, v226
	v_max_f32_e32 v227, v227, v227
	v_max_f32_e32 v228, v228, v228
	v_max_f32_e32 v229, v229, v229
	v_max_f32_e32 v230, v230, v230
	v_max_f32_e32 v231, v231, v231
	v_max_f32_e32 v232, v232, v232
	v_max_f32_e32 v233, v233, v233
	v_max_f32_e32 v234, v234, v234
	v_max_f32_e32 v235, v235, v235
	v_max_f32_e32 v236, v236, v236
	v_max_f32_e32 v237, v237, v237
	v_max_f32_e32 v238, v238, v238
	v_max_f32_e32 v239, v239, v239
	v_max_f32_e32 v240, v240, v240
	v_max_f32_e32 v241, v241, v241
	v_med3_f32 v226, v226, s62, v95
	v_med3_f32 v227, v227, s62, v95
	v_med3_f32 v228, v228, s62, v95
	v_med3_f32 v229, v229, s62, v95
	v_med3_f32 v230, v230, s62, v95
	v_med3_f32 v231, v231, s62, v95
	v_med3_f32 v232, v232, s62, v95
	v_med3_f32 v233, v233, s62, v95
	v_med3_f32 v234, v234, s62, v95
	v_med3_f32 v235, v235, s62, v95
	v_med3_f32 v236, v236, s62, v95
	v_med3_f32 v237, v237, s62, v95
	v_med3_f32 v238, v238, s62, v95
	v_med3_f32 v239, v239, s62, v95
	v_med3_f32 v240, v240, s62, v95
	v_med3_f32 v241, v241, s62, v95
	v_mov_b32_e32 v242, 0
	v_mov_b32_e32 v243, 0
	v_mov_b32_e32 v244, 0
	v_mov_b32_e32 v245, 0
	v_cvt_pk_fp8_f32 v242, v226, v227
	v_cvt_pk_fp8_f32 v243, v230, v231
	v_cvt_pk_fp8_f32 v244, v234, v235
	v_cvt_pk_fp8_f32 v245, v238, v239
	v_cvt_pk_fp8_f32 v242, v228, v229 op_sel:[0,0,1]
	v_cvt_pk_fp8_f32 v243, v232, v233 op_sel:[0,0,1]
	v_cvt_pk_fp8_f32 v244, v236, v237 op_sel:[0,0,1]
	v_cvt_pk_fp8_f32 v245, v240, v241 op_sel:[0,0,1]
	s_nop 0
	global_store_dwordx4 v80, v[242:245], s[6:7]
	s_waitcnt vmcnt(12)
	v_mul_f32_e32 v176, 0x43000000, v176
	v_mul_f32_e32 v177, 0x43000000, v177
	v_mul_f32_e32 v178, 0x43000000, v178
	v_mul_f32_e32 v179, 0x43000000, v179
	ds_write_b128 v210, v[176:179]
	v_mul_f32_e32 v180, 0x43000000, v180
	v_mul_f32_e32 v181, 0x43000000, v181
	v_mul_f32_e32 v182, 0x43000000, v182
	v_mul_f32_e32 v183, 0x43000000, v183
	ds_write_b128 v210, v[180:183] offset:1024
	v_mul_f32_e32 v184, 0x43000000, v184
	v_mul_f32_e32 v185, 0x43000000, v185
	v_mul_f32_e32 v186, 0x43000000, v186
	v_mul_f32_e32 v187, 0x43000000, v187
	ds_write_b128 v210, v[184:187] offset:2048
	v_mul_f32_e32 v188, 0x43000000, v188
	v_mul_f32_e32 v189, 0x43000000, v189
	v_mul_f32_e32 v190, 0x43000000, v190
	v_mul_f32_e32 v191, 0x43000000, v191
	ds_write_b128 v210, v[188:191] offset:3072
	v_mul_f32_e32 v192, 0x43000000, v192
	v_mul_f32_e32 v193, 0x43000000, v193
	v_mul_f32_e32 v194, 0x43000000, v194
	v_mul_f32_e32 v195, 0x43000000, v195
	ds_write_b128 v210, v[192:195] offset:4096
	v_mul_f32_e32 v196, 0x43000000, v196
	v_mul_f32_e32 v197, 0x43000000, v197
	v_mul_f32_e32 v198, 0x43000000, v198
	v_mul_f32_e32 v199, 0x43000000, v199
	ds_write_b128 v210, v[196:199] offset:5120
	v_mul_f32_e32 v200, 0x43000000, v200
	v_mul_f32_e32 v201, 0x43000000, v201
	v_mul_f32_e32 v202, 0x43000000, v202
	v_mul_f32_e32 v203, 0x43000000, v203
	ds_write_b128 v210, v[200:203] offset:6144
	v_mul_f32_e32 v204, 0x43000000, v204
	v_mul_f32_e32 v205, 0x43000000, v205
	v_mul_f32_e32 v206, 0x43000000, v206
	v_mul_f32_e32 v207, 0x43000000, v207
	ds_write_b128 v210, v[204:207] offset:7168
	s_waitcnt lgkmcnt(0)
	s_barrier
	s_add_u32 s8, s42, 0x8001000
	s_addc_u32 s9, s43, 0
	global_load_dwordx4 v[176:179], v75, s[8:9]
	s_add_u32 s8, s8, 0x8000
	s_addc_u32 s9, s9, 0
	global_load_dwordx4 v[180:183], v75, s[8:9]
	s_add_u32 s8, s8, 0x8000
	s_addc_u32 s9, s9, 0
	global_load_dwordx4 v[184:187], v75, s[8:9]
	s_add_u32 s8, s8, 0x8000
	s_addc_u32 s9, s9, 0
	global_load_dwordx4 v[188:191], v75, s[8:9]
	s_add_u32 s8, s8, 0x8000
	s_addc_u32 s9, s9, 0
	global_load_dwordx4 v[192:195], v75, s[8:9]
	s_add_u32 s8, s8, 0x8000
	s_addc_u32 s9, s9, 0
	global_load_dwordx4 v[196:199], v75, s[8:9]
	s_add_u32 s8, s8, 0x8000
	s_addc_u32 s9, s9, 0
	global_load_dwordx4 v[200:203], v75, s[8:9]
	s_add_u32 s8, s8, 0x8000
	s_addc_u32 s9, s9, 0
	global_load_dwordx4 v[204:207], v75, s[8:9]
	s_add_u32 s6, s44, 0x3001000
	s_addc_u32 s7, s45, 0
	ds_read_b32 v226, v212
	ds_read_b32 v227, v212 offset:512
	ds_read_b32 v228, v212 offset:1024
	ds_read_b32 v229, v212 offset:1536
	ds_read_b32 v230, v212 offset:2048
	ds_read_b32 v231, v212 offset:2560
	ds_read_b32 v232, v212 offset:3072
	ds_read_b32 v233, v212 offset:3584
	ds_read_b32 v234, v212 offset:4096
	ds_read_b32 v235, v212 offset:4608
	ds_read_b32 v236, v212 offset:5120
	ds_read_b32 v237, v212 offset:5632
	ds_read_b32 v238, v212 offset:6144
	ds_read_b32 v239, v212 offset:6656
	ds_read_b32 v240, v212 offset:7168
	ds_read_b32 v241, v212 offset:7680
	s_waitcnt lgkmcnt(0)
	v_max_f32_e32 v226, v226, v226
	v_max_f32_e32 v227, v227, v227
	v_max_f32_e32 v228, v228, v228
	v_max_f32_e32 v229, v229, v229
	v_max_f32_e32 v230, v230, v230
	v_max_f32_e32 v231, v231, v231
	v_max_f32_e32 v232, v232, v232
	v_max_f32_e32 v233, v233, v233
	v_max_f32_e32 v234, v234, v234
	v_max_f32_e32 v235, v235, v235
	v_max_f32_e32 v236, v236, v236
	v_max_f32_e32 v237, v237, v237
	v_max_f32_e32 v238, v238, v238
	v_max_f32_e32 v239, v239, v239
	v_max_f32_e32 v240, v240, v240
	v_max_f32_e32 v241, v241, v241
	v_med3_f32 v226, v226, s62, v95
	v_med3_f32 v227, v227, s62, v95
	v_med3_f32 v228, v228, s62, v95
	v_med3_f32 v229, v229, s62, v95
	v_med3_f32 v230, v230, s62, v95
	v_med3_f32 v231, v231, s62, v95
	v_med3_f32 v232, v232, s62, v95
	v_med3_f32 v233, v233, s62, v95
	v_med3_f32 v234, v234, s62, v95
	v_med3_f32 v235, v235, s62, v95
	v_med3_f32 v236, v236, s62, v95
	v_med3_f32 v237, v237, s62, v95
	v_med3_f32 v238, v238, s62, v95
	v_med3_f32 v239, v239, s62, v95
	v_med3_f32 v240, v240, s62, v95
	v_med3_f32 v241, v241, s62, v95
	v_mov_b32_e32 v242, 0
	v_mov_b32_e32 v243, 0
	v_mov_b32_e32 v244, 0
	v_mov_b32_e32 v245, 0
	v_cvt_pk_fp8_f32 v242, v226, v227
	v_cvt_pk_fp8_f32 v243, v230, v231
	v_cvt_pk_fp8_f32 v244, v234, v235
	v_cvt_pk_fp8_f32 v245, v238, v239
	v_cvt_pk_fp8_f32 v242, v228, v229 op_sel:[0,0,1]
	v_cvt_pk_fp8_f32 v243, v232, v233 op_sel:[0,0,1]
	v_cvt_pk_fp8_f32 v244, v236, v237 op_sel:[0,0,1]
	v_cvt_pk_fp8_f32 v245, v240, v241 op_sel:[0,0,1]
	s_nop 0
	global_store_dwordx4 v79, v[242:245], s[6:7]
	ds_read_b32 v226, v214
	ds_read_b32 v227, v214 offset:512
	ds_read_b32 v228, v214 offset:1024
	ds_read_b32 v229, v214 offset:1536
	ds_read_b32 v230, v214 offset:2048
	ds_read_b32 v231, v214 offset:2560
	ds_read_b32 v232, v214 offset:3072
	ds_read_b32 v233, v214 offset:3584
	ds_read_b32 v234, v214 offset:4096
	ds_read_b32 v235, v214 offset:4608
	ds_read_b32 v236, v214 offset:5120
	ds_read_b32 v237, v214 offset:5632
	ds_read_b32 v238, v214 offset:6144
	ds_read_b32 v239, v214 offset:6656
	ds_read_b32 v240, v214 offset:7168
	ds_read_b32 v241, v214 offset:7680
	s_waitcnt lgkmcnt(0)
; #define GAS __attribute__((address_space(1)))
; #define LAS __attribute__((address_space(3)))
; #define LDS_WAIT() asm volatile("s_waitcnt lgkmcnt(0)" ::: "memory")
; __device__ __forceinline__ unsigned pk4_fp8(float a, float b, float c, float d) {
;     a = fminf(fmaxf(a, -448.f), 448.f); b = fminf(fmaxf(b, -448.f), 448.f); c = fminf(fmaxf(c, -448.f), 448.f); d = fminf(fmaxf(d, -448.f), 448.f);
;     int w = __builtin_amdgcn_cvt_pk_fp8_f32(a, b, 0, false); w = __builtin_amdgcn_cvt_pk_fp8_f32(c, d, w, true); return (unsigned)w; }
;     const int pr = item >> 1, kb = 2 * (pr / nblk) + (item & 1), nb = pr % nblk, k0 = 64 * kb, n0 = 32 * nb;
;     const int nr = n0 + (lane & 31); const int sc = MAP == 1 ? src_col_in(nr) : nr;
;     float v[32];
; #pragma unroll
;     for (int i = 0; i < 32; ++i) v[i] = sc >= 0 ? W[(size_t)(k0 + 2 * i + (lane >> 5)) * Nsrc + sc] : 0.f;
; #pragma unroll
;     for (int i = 0; i < 32; ++i) { const int k = k0 + 2 * i + (lane >> 5); float x = v[i] * wscale; if (KS) x *= (k < ksplit ? ksA[k] : ksB[k - ksplit]); scr[(2 * i + (lane >> 5)) * 33 + (lane & 31)] = x; }
;     LDS_WAIT(); asm volatile("" ::: "memory");
;     const int c = lane & 7;
; #pragma unroll
;     for (int j = 0; j < 4; ++j) { const int n = (lane >> 3) + 8 * j; const LAS float* s = scr + (8 * c) * 33 + n;
;         const unsigned long long o = (unsigned long long)pg8::pk4_fp8(s[0 * 33], s[1 * 33], s[2 * 33], s[3 * 33]) | ((unsigned long long)pg8::pk4_fp8(s[4 * 33], s[5 * 33], s[6 * 33], s[7 * 33]) << 32);
;         *(GAS unsigned long long*)(WT + (size_t)(n0 + n) * K + k0 + 8 * c) = o; }
;     LDS_WAIT(); asm volatile("" ::: "memory");
; }
	v_max_f32_e32 v226, v226, v226
	v_max_f32_e32 v227, v227, v227
	v_max_f32_e32 v228, v228, v228
	v_max_f32_e32 v229, v229, v229
	v_max_f32_e32 v230, v230, v230
	v_max_f32_e32 v231, v231, v231
	v_max_f32_e32 v232, v232, v232
	v_max_f32_e32 v233, v233, v233
	v_max_f32_e32 v234, v234, v234
	v_max_f32_e32 v235, v235, v235
	v_max_f32_e32 v236, v236, v236
	v_max_f32_e32 v237, v237, v237
	v_max_f32_e32 v238, v238, v238
	v_max_f32_e32 v239, v239, v239
	v_max_f32_e32 v240, v240, v240
	v_max_f32_e32 v241, v241, v241
	v_med3_f32 v226, v226, s62, v95
	v_med3_f32 v227, v227, s62, v95
	v_med3_f32 v228, v228, s62, v95
	v_med3_f32 v229, v229, s62, v95
	v_med3_f32 v230, v230, s62, v95
	v_med3_f32 v231, v231, s62, v95
	v_med3_f32 v232, v232, s62, v95
	v_med3_f32 v233, v233, s62, v95
	v_med3_f32 v234, v234, s62, v95
	v_med3_f32 v235, v235, s62, v95
	v_med3_f32 v236, v236, s62, v95
	v_med3_f32 v237, v237, s62, v95
	v_med3_f32 v238, v238, s62, v95
	v_med3_f32 v239, v239, s62, v95
	v_med3_f32 v240, v240, s62, v95
	v_med3_f32 v241, v241, s62, v95
	v_mov_b32_e32 v242, 0
	v_mov_b32_e32 v243, 0
	v_mov_b32_e32 v244, 0
	v_mov_b32_e32 v245, 0
	v_cvt_pk_fp8_f32 v242, v226, v227
	v_cvt_pk_fp8_f32 v243, v230, v231
	v_cvt_pk_fp8_f32 v244, v234, v235
	v_cvt_pk_fp8_f32 v245, v238, v239
	v_cvt_pk_fp8_f32 v242, v228, v229 op_sel:[0,0,1]
	v_cvt_pk_fp8_f32 v243, v232, v233 op_sel:[0,0,1]
	v_cvt_pk_fp8_f32 v244, v236, v237 op_sel:[0,0,1]
	v_cvt_pk_fp8_f32 v245, v240, v241 op_sel:[0,0,1]
	s_nop 0
	global_store_dwordx4 v80, v[242:245], s[6:7]
	s_waitcnt vmcnt(12)
	v_mul_f32_e32 v144, 0x43000000, v144
	v_mul_f32_e32 v145, 0x43000000, v145
	v_mul_f32_e32 v146, 0x43000000, v146
	v_mul_f32_e32 v147, 0x43000000, v147
	ds_write_b128 v209, v[144:147]
	v_mul_f32_e32 v148, 0x43000000, v148
	v_mul_f32_e32 v149, 0x43000000, v149
	v_mul_f32_e32 v150, 0x43000000, v150
	v_mul_f32_e32 v151, 0x43000000, v151
	ds_write_b128 v209, v[148:151] offset:1024
	v_mul_f32_e32 v152, 0x43000000, v152
	v_mul_f32_e32 v153, 0x43000000, v153
	v_mul_f32_e32 v154, 0x43000000, v154
	v_mul_f32_e32 v155, 0x43000000, v155
	ds_write_b128 v209, v[152:155] offset:2048
	v_mul_f32_e32 v156, 0x43000000, v156
	v_mul_f32_e32 v157, 0x43000000, v157
	v_mul_f32_e32 v158, 0x43000000, v158
	v_mul_f32_e32 v159, 0x43000000, v159
	ds_write_b128 v209, v[156:159] offset:3072
	v_mul_f32_e32 v160, 0x43000000, v160
	v_mul_f32_e32 v161, 0x43000000, v161
	v_mul_f32_e32 v162, 0x43000000, v162
	v_mul_f32_e32 v163, 0x43000000, v163
	ds_write_b128 v209, v[160:163] offset:4096
	v_mul_f32_e32 v164, 0x43000000, v164
	v_mul_f32_e32 v165, 0x43000000, v165
	v_mul_f32_e32 v166, 0x43000000, v166
	v_mul_f32_e32 v167, 0x43000000, v167
	ds_write_b128 v209, v[164:167] offset:5120
	v_mul_f32_e32 v168, 0x43000000, v168
	v_mul_f32_e32 v169, 0x43000000, v169
	v_mul_f32_e32 v170, 0x43000000, v170
	v_mul_f32_e32 v171, 0x43000000, v171
	ds_write_b128 v209, v[168:171] offset:6144
	v_mul_f32_e32 v172, 0x43000000, v172
	v_mul_f32_e32 v173, 0x43000000, v173
	v_mul_f32_e32 v174, 0x43000000, v174
	v_mul_f32_e32 v175, 0x43000000, v175
	ds_write_b128 v209, v[172:175] offset:7168
	s_waitcnt lgkmcnt(0)
	s_barrier
	s_add_u32 s8, s42, 0x8002000
	s_addc_u32 s9, s43, 0
	global_load_dwordx4 v[144:147], v75, s[8:9]
	s_add_u32 s8, s8, 0x8000
	s_addc_u32 s9, s9, 0
	global_load_dwordx4 v[148:151], v75, s[8:9]
	s_add_u32 s8, s8, 0x8000
	s_addc_u32 s9, s9, 0
	global_load_dwordx4 v[152:155], v75, s[8:9]
	s_add_u32 s8, s8, 0x8000
	s_addc_u32 s9, s9, 0
	global_load_dwordx4 v[156:159], v75, s[8:9]
	s_add_u32 s8, s8, 0x8000
	s_addc_u32 s9, s9, 0
	global_load_dwordx4 v[160:163], v75, s[8:9]
	s_add_u32 s8, s8, 0x8000
	s_addc_u32 s9, s9, 0
	global_load_dwordx4 v[164:167], v75, s[8:9]
	s_add_u32 s8, s8, 0x8000
	s_addc_u32 s9, s9, 0
	global_load_dwordx4 v[168:171], v75, s[8:9]
	s_add_u32 s8, s8, 0x8000
	s_addc_u32 s9, s9, 0
	global_load_dwordx4 v[172:175], v75, s[8:9]
	s_add_u32 s6, s44, 0x2000
	s_addc_u32 s7, s45, 0
	ds_read_b32 v226, v211
	ds_read_b32 v227, v211 offset:512
	ds_read_b32 v228, v211 offset:1024
	ds_read_b32 v229, v211 offset:1536
	ds_read_b32 v230, v211 offset:2048
	ds_read_b32 v231, v211 offset:2560
	ds_read_b32 v232, v211 offset:3072
	ds_read_b32 v233, v211 offset:3584
	ds_read_b32 v234, v211 offset:4096
	ds_read_b32 v235, v211 offset:4608
	ds_read_b32 v236, v211 offset:5120
	ds_read_b32 v237, v211 offset:5632
	ds_read_b32 v238, v211 offset:6144
	ds_read_b32 v239, v211 offset:6656
	ds_read_b32 v240, v211 offset:7168
	ds_read_b32 v241, v211 offset:7680
	s_waitcnt lgkmcnt(0)
	v_max_f32_e32 v226, v226, v226
	v_max_f32_e32 v227, v227, v227
	v_max_f32_e32 v228, v228, v228
	v_max_f32_e32 v229, v229, v229
	v_max_f32_e32 v230, v230, v230
	v_max_f32_e32 v231, v231, v231
	v_max_f32_e32 v232, v232, v232
	v_max_f32_e32 v233, v233, v233
	v_max_f32_e32 v234, v234, v234
	v_max_f32_e32 v235, v235, v235
	v_max_f32_e32 v236, v236, v236
	v_max_f32_e32 v237, v237, v237
	v_max_f32_e32 v238, v238, v238
	v_max_f32_e32 v239, v239, v239
	v_max_f32_e32 v240, v240, v240
	v_max_f32_e32 v241, v241, v241
	v_med3_f32 v226, v226, s62, v95
	v_med3_f32 v227, v227, s62, v95
	v_med3_f32 v228, v228, s62, v95
	v_med3_f32 v229, v229, s62, v95
	v_med3_f32 v230, v230, s62, v95
	v_med3_f32 v231, v231, s62, v95
	v_med3_f32 v232, v232, s62, v95
	v_med3_f32 v233, v233, s62, v95
	v_med3_f32 v234, v234, s62, v95
	v_med3_f32 v235, v235, s62, v95
	v_med3_f32 v236, v236, s62, v95
	v_med3_f32 v237, v237, s62, v95
	v_med3_f32 v238, v238, s62, v95
	v_med3_f32 v239, v239, s62, v95
	v_med3_f32 v240, v240, s62, v95
	v_med3_f32 v241, v241, s62, v95
	v_mov_b32_e32 v242, 0
	v_mov_b32_e32 v243, 0
	v_mov_b32_e32 v244, 0
	v_mov_b32_e32 v245, 0
	v_cvt_pk_fp8_f32 v242, v226, v227
	v_cvt_pk_fp8_f32 v243, v230, v231
	v_cvt_pk_fp8_f32 v244, v234, v235
	v_cvt_pk_fp8_f32 v245, v238, v239
	v_cvt_pk_fp8_f32 v242, v228, v229 op_sel:[0,0,1]
	v_cvt_pk_fp8_f32 v243, v232, v233 op_sel:[0,0,1]
	v_cvt_pk_fp8_f32 v244, v236, v237 op_sel:[0,0,1]
	v_cvt_pk_fp8_f32 v245, v240, v241 op_sel:[0,0,1]
	s_nop 0
	global_store_dwordx4 v79, v[242:245], s[6:7]
	ds_read_b32 v226, v213
	ds_read_b32 v227, v213 offset:512
	ds_read_b32 v228, v213 offset:1024
	ds_read_b32 v229, v213 offset:1536
	ds_read_b32 v230, v213 offset:2048
	ds_read_b32 v231, v213 offset:2560
	ds_read_b32 v232, v213 offset:3072
	ds_read_b32 v233, v213 offset:3584
	ds_read_b32 v234, v213 offset:4096
	ds_read_b32 v235, v213 offset:4608
	ds_read_b32 v236, v213 offset:5120
	ds_read_b32 v237, v213 offset:5632
	ds_read_b32 v238, v213 offset:6144
	ds_read_b32 v239, v213 offset:6656
	ds_read_b32 v240, v213 offset:7168
	ds_read_b32 v241, v213 offset:7680
	s_waitcnt lgkmcnt(0)
; #define GAS __attribute__((address_space(1)))
; #define LAS __attribute__((address_space(3)))
; #define LDS_WAIT() asm volatile("s_waitcnt lgkmcnt(0)" ::: "memory")
; __device__ __forceinline__ unsigned pk4_fp8(float a, float b, float c, float d) {
;     a = fminf(fmaxf(a, -448.f), 448.f); b = fminf(fmaxf(b, -448.f), 448.f); c = fminf(fmaxf(c, -448.f), 448.f); d = fminf(fmaxf(d, -448.f), 448.f);
;     int w = __builtin_amdgcn_cvt_pk_fp8_f32(a, b, 0, false); w = __builtin_amdgcn_cvt_pk_fp8_f32(c, d, w, true); return (unsigned)w; }
;     const int pr = item >> 1, kb = 2 * (pr / nblk) + (item & 1), nb = pr % nblk, k0 = 64 * kb, n0 = 32 * nb;
;     const int nr = n0 + (lane & 31); const int sc = MAP == 1 ? src_col_in(nr) : nr;
;     float v[32];
; #pragma unroll
;     for (int i = 0; i < 32; ++i) v[i] = sc >= 0 ? W[(size_t)(k0 + 2 * i + (lane >> 5)) * Nsrc + sc] : 0.f;
; #pragma unroll
;     for (int i = 0; i < 32; ++i) { const int k = k0 + 2 * i + (lane >> 5); float x = v[i] * wscale; if (KS) x *= (k < ksplit ? ksA[k] : ksB[k - ksplit]); scr[(2 * i + (lane >> 5)) * 33 + (lane & 31)] = x; }
;     LDS_WAIT(); asm volatile("" ::: "memory");
;     const int c = lane & 7;
; #pragma unroll
;     for (int j = 0; j < 4; ++j) { const int n = (lane >> 3) + 8 * j; const LAS float* s = scr + (8 * c) * 33 + n;
;         const unsigned long long o = (unsigned long long)pg8::pk4_fp8(s[0 * 33], s[1 * 33], s[2 * 33], s[3 * 33]) | ((unsigned long long)pg8::pk4_fp8(s[4 * 33], s[5 * 33], s[6 * 33], s[7 * 33]) << 32);
;         *(GAS unsigned long long*)(WT + (size_t)(n0 + n) * K + k0 + 8 * c) = o; }
;     LDS_WAIT(); asm volatile("" ::: "memory");
; }
	v_max_f32_e32 v226, v226, v226
	v_max_f32_e32 v227, v227, v227
	v_max_f32_e32 v228, v228, v228
	v_max_f32_e32 v229, v229, v229
	v_max_f32_e32 v230, v230, v230
	v_max_f32_e32 v231, v231, v231
	v_max_f32_e32 v232, v232, v232
	v_max_f32_e32 v233, v233, v233
	v_max_f32_e32 v234, v234, v234
	v_max_f32_e32 v235, v235, v235
	v_max_f32_e32 v236, v236, v236
	v_max_f32_e32 v237, v237, v237
	v_max_f32_e32 v238, v238, v238
	v_max_f32_e32 v239, v239, v239
	v_max_f32_e32 v240, v240, v240
	v_max_f32_e32 v241, v241, v241
	v_med3_f32 v226, v226, s62, v95
	v_med3_f32 v227, v227, s62, v95
	v_med3_f32 v228, v228, s62, v95
	v_med3_f32 v229, v229, s62, v95
	v_med3_f32 v230, v230, s62, v95
	v_med3_f32 v231, v231, s62, v95
	v_med3_f32 v232, v232, s62, v95
	v_med3_f32 v233, v233, s62, v95
	v_med3_f32 v234, v234, s62, v95
	v_med3_f32 v235, v235, s62, v95
	v_med3_f32 v236, v236, s62, v95
	v_med3_f32 v237, v237, s62, v95
	v_med3_f32 v238, v238, s62, v95
	v_med3_f32 v239, v239, s62, v95
	v_med3_f32 v240, v240, s62, v95
	v_med3_f32 v241, v241, s62, v95
	v_mov_b32_e32 v242, 0
	v_mov_b32_e32 v243, 0
	v_mov_b32_e32 v244, 0
	v_mov_b32_e32 v245, 0
	v_cvt_pk_fp8_f32 v242, v226, v227
	v_cvt_pk_fp8_f32 v243, v230, v231
	v_cvt_pk_fp8_f32 v244, v234, v235
	v_cvt_pk_fp8_f32 v245, v238, v239
	v_cvt_pk_fp8_f32 v242, v228, v229 op_sel:[0,0,1]
	v_cvt_pk_fp8_f32 v243, v232, v233 op_sel:[0,0,1]
	v_cvt_pk_fp8_f32 v244, v236, v237 op_sel:[0,0,1]
	v_cvt_pk_fp8_f32 v245, v240, v241 op_sel:[0,0,1]
	s_nop 0
	global_store_dwordx4 v80, v[242:245], s[6:7]
	s_waitcnt vmcnt(12)
	v_mul_f32_e32 v176, 0x43000000, v176
	v_mul_f32_e32 v177, 0x43000000, v177
	v_mul_f32_e32 v178, 0x43000000, v178
	v_mul_f32_e32 v179, 0x43000000, v179
	ds_write_b128 v210, v[176:179]
	v_mul_f32_e32 v180, 0x43000000, v180
	v_mul_f32_e32 v181, 0x43000000, v181
	v_mul_f32_e32 v182, 0x43000000, v182
	v_mul_f32_e32 v183, 0x43000000, v183
	ds_write_b128 v210, v[180:183] offset:1024
	v_mul_f32_e32 v184, 0x43000000, v184
	v_mul_f32_e32 v185, 0x43000000, v185
	v_mul_f32_e32 v186, 0x43000000, v186
	v_mul_f32_e32 v187, 0x43000000, v187
	ds_write_b128 v210, v[184:187] offset:2048
	v_mul_f32_e32 v188, 0x43000000, v188
	v_mul_f32_e32 v189, 0x43000000, v189
	v_mul_f32_e32 v190, 0x43000000, v190
	v_mul_f32_e32 v191, 0x43000000, v191
	ds_write_b128 v210, v[188:191] offset:3072
	v_mul_f32_e32 v192, 0x43000000, v192
	v_mul_f32_e32 v193, 0x43000000, v193
	v_mul_f32_e32 v194, 0x43000000, v194
	v_mul_f32_e32 v195, 0x43000000, v195
	ds_write_b128 v210, v[192:195] offset:4096
	v_mul_f32_e32 v196, 0x43000000, v196
	v_mul_f32_e32 v197, 0x43000000, v197
	v_mul_f32_e32 v198, 0x43000000, v198
	v_mul_f32_e32 v199, 0x43000000, v199
	ds_write_b128 v210, v[196:199] offset:5120
	v_mul_f32_e32 v200, 0x43000000, v200
	v_mul_f32_e32 v201, 0x43000000, v201
	v_mul_f32_e32 v202, 0x43000000, v202
	v_mul_f32_e32 v203, 0x43000000, v203
	ds_write_b128 v210, v[200:203] offset:6144
	v_mul_f32_e32 v204, 0x43000000, v204
	v_mul_f32_e32 v205, 0x43000000, v205
	v_mul_f32_e32 v206, 0x43000000, v206
	v_mul_f32_e32 v207, 0x43000000, v207
	ds_write_b128 v210, v[204:207] offset:7168
	s_waitcnt lgkmcnt(0)
	s_barrier
	s_add_u32 s8, s42, 0x8003000
	s_addc_u32 s9, s43, 0
	global_load_dwordx4 v[176:179], v75, s[8:9]
	s_add_u32 s8, s8, 0x8000
	s_addc_u32 s9, s9, 0
	global_load_dwordx4 v[180:183], v75, s[8:9]
	s_add_u32 s8, s8, 0x8000
	s_addc_u32 s9, s9, 0
	global_load_dwordx4 v[184:187], v75, s[8:9]
	s_add_u32 s8, s8, 0x8000
	s_addc_u32 s9, s9, 0
	global_load_dwordx4 v[188:191], v75, s[8:9]
	s_add_u32 s8, s8, 0x8000
	s_addc_u32 s9, s9, 0
	global_load_dwordx4 v[192:195], v75, s[8:9]
	s_add_u32 s8, s8, 0x8000
	s_addc_u32 s9, s9, 0
	global_load_dwordx4 v[196:199], v75, s[8:9]
	s_add_u32 s8, s8, 0x8000
	s_addc_u32 s9, s9, 0
	global_load_dwordx4 v[200:203], v75, s[8:9]
	s_add_u32 s8, s8, 0x8000
	s_addc_u32 s9, s9, 0
	global_load_dwordx4 v[204:207], v75, s[8:9]
	s_add_u32 s6, s44, 0x1002000
	s_addc_u32 s7, s45, 0
	ds_read_b32 v226, v212
	ds_read_b32 v227, v212 offset:512
	ds_read_b32 v228, v212 offset:1024
	ds_read_b32 v229, v212 offset:1536
	ds_read_b32 v230, v212 offset:2048
	ds_read_b32 v231, v212 offset:2560
	ds_read_b32 v232, v212 offset:3072
	ds_read_b32 v233, v212 offset:3584
	ds_read_b32 v234, v212 offset:4096
	ds_read_b32 v235, v212 offset:4608
	ds_read_b32 v236, v212 offset:5120
	ds_read_b32 v237, v212 offset:5632
	ds_read_b32 v238, v212 offset:6144
	ds_read_b32 v239, v212 offset:6656
	ds_read_b32 v240, v212 offset:7168
	ds_read_b32 v241, v212 offset:7680
	s_waitcnt lgkmcnt(0)
	v_max_f32_e32 v226, v226, v226
	v_max_f32_e32 v227, v227, v227
	v_max_f32_e32 v228, v228, v228
	v_max_f32_e32 v229, v229, v229
	v_max_f32_e32 v230, v230, v230
	v_max_f32_e32 v231, v231, v231
	v_max_f32_e32 v232, v232, v232
	v_max_f32_e32 v233, v233, v233
	v_max_f32_e32 v234, v234, v234
	v_max_f32_e32 v235, v235, v235
	v_max_f32_e32 v236, v236, v236
	v_max_f32_e32 v237, v237, v237
	v_max_f32_e32 v238, v238, v238
	v_max_f32_e32 v239, v239, v239
	v_max_f32_e32 v240, v240, v240
	v_max_f32_e32 v241, v241, v241
	v_med3_f32 v226, v226, s62, v95
	v_med3_f32 v227, v227, s62, v95
	v_med3_f32 v228, v228, s62, v95
	v_med3_f32 v229, v229, s62, v95
	v_med3_f32 v230, v230, s62, v95
	v_med3_f32 v231, v231, s62, v95
	v_med3_f32 v232, v232, s62, v95
	v_med3_f32 v233, v233, s62, v95
	v_med3_f32 v234, v234, s62, v95
	v_med3_f32 v235, v235, s62, v95
	v_med3_f32 v236, v236, s62, v95
	v_med3_f32 v237, v237, s62, v95
	v_med3_f32 v238, v238, s62, v95
	v_med3_f32 v239, v239, s62, v95
	v_med3_f32 v240, v240, s62, v95
	v_med3_f32 v241, v241, s62, v95
	v_mov_b32_e32 v242, 0
	v_mov_b32_e32 v243, 0
	v_mov_b32_e32 v244, 0
	v_mov_b32_e32 v245, 0
	v_cvt_pk_fp8_f32 v242, v226, v227
	v_cvt_pk_fp8_f32 v243, v230, v231
	v_cvt_pk_fp8_f32 v244, v234, v235
	v_cvt_pk_fp8_f32 v245, v238, v239
	v_cvt_pk_fp8_f32 v242, v228, v229 op_sel:[0,0,1]
	v_cvt_pk_fp8_f32 v243, v232, v233 op_sel:[0,0,1]
	v_cvt_pk_fp8_f32 v244, v236, v237 op_sel:[0,0,1]
	v_cvt_pk_fp8_f32 v245, v240, v241 op_sel:[0,0,1]
	s_nop 0
	global_store_dwordx4 v79, v[242:245], s[6:7]
	ds_read_b32 v226, v214
	ds_read_b32 v227, v214 offset:512
	ds_read_b32 v228, v214 offset:1024
	ds_read_b32 v229, v214 offset:1536
	ds_read_b32 v230, v214 offset:2048
	ds_read_b32 v231, v214 offset:2560
	ds_read_b32 v232, v214 offset:3072
	ds_read_b32 v233, v214 offset:3584
	ds_read_b32 v234, v214 offset:4096
	ds_read_b32 v235, v214 offset:4608
	ds_read_b32 v236, v214 offset:5120
	ds_read_b32 v237, v214 offset:5632
	ds_read_b32 v238, v214 offset:6144
	ds_read_b32 v239, v214 offset:6656
	ds_read_b32 v240, v214 offset:7168
	ds_read_b32 v241, v214 offset:7680
	s_waitcnt lgkmcnt(0)
; #define GAS __attribute__((address_space(1)))
; #define LAS __attribute__((address_space(3)))
; #define LDS_WAIT() asm volatile("s_waitcnt lgkmcnt(0)" ::: "memory")
; __device__ __forceinline__ int src_col_in(int c) {
;     if (c < 5120) { const int blk = c >> 7, p = c & 127; const bool rope = blk < 16 || ((((blk - 16) >> 2) & 1) == 0); const int d = rope ? (p >> 1) + 64 * (p & 1) : p; return blk * 128 + d; }
;     if (c < OFF_Z) return c + 2096;
;     if (c < OFF_G) return c - 4048;
;     if (c < OFF_DT) return 5120 + (c - OFF_G);
;     if (c < NSRC) return c;
;     return -1;
; }
;     const int pr = item >> 1, kb = 2 * (pr / nblk) + (item & 1), nb = pr % nblk, k0 = 64 * kb, n0 = 32 * nb;
;     const int nr = n0 + (lane & 31); const int sc = MAP == 1 ? src_col_in(nr) : nr;
;     float v[32];
; #pragma unroll
;     for (int i = 0; i < 32; ++i) v[i] = sc >= 0 ? W[(size_t)(k0 + 2 * i + (lane >> 5)) * Nsrc + sc] : 0.f;
; #pragma unroll
;     for (int i = 0; i < 32; ++i) { const int k = k0 + 2 * i + (lane >> 5); float x = v[i] * wscale; if (KS) x *= (k < ksplit ? ksA[k] : ksB[k - ksplit]); scr[(2 * i + (lane >> 5)) * 33 + (lane & 31)] = x; }
;     LDS_WAIT(); asm volatile("" ::: "memory");
;     const int c = lane & 7;
; #pragma unroll
;     for (int j = 0; j < 4; ++j) { const int n = (lane >> 3) + 8 * j; const LAS float* s = scr + (8 * c) * 33 + n;
;         const unsigned long long o = (unsigned long long)pg8::pk4_fp8(s[0 * 33], s[1 * 33], s[2 * 33], s[3 * 33]) | ((unsigned long long)pg8::pk4_fp8(s[4 * 33], s[5 * 33], s[6 * 33], s[7 * 33]) << 32);
;         *(GAS unsigned long long*)(WT + (size_t)(n0 + n) * K + k0 + 8 * c) = o; }
;     LDS_WAIT(); asm volatile("" ::: "memory");
; }
	v_max_f32_e32 v226, v226, v226
	v_max_f32_e32 v227, v227, v227
	v_max_f32_e32 v228, v228, v228
	v_max_f32_e32 v229, v229, v229
	v_max_f32_e32 v230, v230, v230
	v_max_f32_e32 v231, v231, v231
	v_max_f32_e32 v232, v232, v232
	v_max_f32_e32 v233, v233, v233
	v_max_f32_e32 v234, v234, v234
	v_max_f32_e32 v235, v235, v235
	v_max_f32_e32 v236, v236, v236
	v_max_f32_e32 v237, v237, v237
	v_max_f32_e32 v238, v238, v238
	v_max_f32_e32 v239, v239, v239
	v_max_f32_e32 v240, v240, v240
	v_max_f32_e32 v241, v241, v241
	v_med3_f32 v226, v226, s62, v95
	v_med3_f32 v227, v227, s62, v95
	v_med3_f32 v228, v228, s62, v95
	v_med3_f32 v229, v229, s62, v95
	v_med3_f32 v230, v230, s62, v95
	v_med3_f32 v231, v231, s62, v95
	v_med3_f32 v232, v232, s62, v95
	v_med3_f32 v233, v233, s62, v95
	v_med3_f32 v234, v234, s62, v95
	v_med3_f32 v235, v235, s62, v95
	v_med3_f32 v236, v236, s62, v95
	v_med3_f32 v237, v237, s62, v95
	v_med3_f32 v238, v238, s62, v95
	v_med3_f32 v239, v239, s62, v95
	v_med3_f32 v240, v240, s62, v95
	v_med3_f32 v241, v241, s62, v95
	v_mov_b32_e32 v242, 0
	v_mov_b32_e32 v243, 0
	v_mov_b32_e32 v244, 0
	v_mov_b32_e32 v245, 0
	v_cvt_pk_fp8_f32 v242, v226, v227
	v_cvt_pk_fp8_f32 v243, v230, v231
	v_cvt_pk_fp8_f32 v244, v234, v235
	v_cvt_pk_fp8_f32 v245, v238, v239
	v_cvt_pk_fp8_f32 v242, v228, v229 op_sel:[0,0,1]
	v_cvt_pk_fp8_f32 v243, v232, v233 op_sel:[0,0,1]
	v_cvt_pk_fp8_f32 v244, v236, v237 op_sel:[0,0,1]
	v_cvt_pk_fp8_f32 v245, v240, v241 op_sel:[0,0,1]
	s_nop 0
	global_store_dwordx4 v80, v[242:245], s[6:7]
	s_waitcnt vmcnt(12)
	v_mul_f32_e32 v144, 0x43000000, v144
	v_mul_f32_e32 v145, 0x43000000, v145
	v_mul_f32_e32 v146, 0x43000000, v146
	v_mul_f32_e32 v147, 0x43000000, v147
	ds_write_b128 v209, v[144:147]
	v_mul_f32_e32 v148, 0x43000000, v148
	v_mul_f32_e32 v149, 0x43000000, v149
	v_mul_f32_e32 v150, 0x43000000, v150
	v_mul_f32_e32 v151, 0x43000000, v151
	ds_write_b128 v209, v[148:151] offset:1024
	v_mul_f32_e32 v152, 0x43000000, v152
	v_mul_f32_e32 v153, 0x43000000, v153
	v_mul_f32_e32 v154, 0x43000000, v154
	v_mul_f32_e32 v155, 0x43000000, v155
	ds_write_b128 v209, v[152:155] offset:2048
	v_mul_f32_e32 v156, 0x43000000, v156
	v_mul_f32_e32 v157, 0x43000000, v157
	v_mul_f32_e32 v158, 0x43000000, v158
	v_mul_f32_e32 v159, 0x43000000, v159
	ds_write_b128 v209, v[156:159] offset:3072
	v_mul_f32_e32 v160, 0x43000000, v160
	v_mul_f32_e32 v161, 0x43000000, v161
	v_mul_f32_e32 v162, 0x43000000, v162
	v_mul_f32_e32 v163, 0x43000000, v163
	ds_write_b128 v209, v[160:163] offset:4096
	v_mul_f32_e32 v164, 0x43000000, v164
	v_mul_f32_e32 v165, 0x43000000, v165
	v_mul_f32_e32 v166, 0x43000000, v166
	v_mul_f32_e32 v167, 0x43000000, v167
	ds_write_b128 v209, v[164:167] offset:5120
	v_mul_f32_e32 v168, 0x43000000, v168
	v_mul_f32_e32 v169, 0x43000000, v169
	v_mul_f32_e32 v170, 0x43000000, v170
	v_mul_f32_e32 v171, 0x43000000, v171
	ds_write_b128 v209, v[168:171] offset:6144
	v_mul_f32_e32 v172, 0x43000000, v172
	v_mul_f32_e32 v173, 0x43000000, v173
	v_mul_f32_e32 v174, 0x43000000, v174
	v_mul_f32_e32 v175, 0x43000000, v175
	ds_write_b128 v209, v[172:175] offset:7168
	s_waitcnt lgkmcnt(0)
	s_barrier
	s_add_i32 s24, s23, 0
	s_lshl_b32 s20, s24, 7
	s_cmp_lt_u32 s24, 40
	s_cselect_b32 s21, 0, 0x830
	s_cmp_lt_u32 s24, 72
	s_cselect_b32 s21, s21, 0xfffff030
	s_add_i32 s20, s20, s21
	s_lshl_b32 s20, s20, 2
	s_add_u32 s8, s46, s20
	s_addc_u32 s9, s47, 0
	global_load_dwordx4 v[144:147], v76, s[8:9]
	s_add_u32 s8, s8, 0x16280
	s_addc_u32 s9, s9, 0
	global_load_dwordx4 v[148:151], v76, s[8:9]
	s_add_u32 s8, s8, 0x16280
	s_addc_u32 s9, s9, 0
	global_load_dwordx4 v[152:155], v76, s[8:9]
	s_add_u32 s8, s8, 0x16280
	s_addc_u32 s9, s9, 0
	global_load_dwordx4 v[156:159], v76, s[8:9]
	s_add_u32 s8, s8, 0x16280
	s_addc_u32 s9, s9, 0
	global_load_dwordx4 v[160:163], v76, s[8:9]
	s_add_u32 s8, s8, 0x16280
	s_addc_u32 s9, s9, 0
	global_load_dwordx4 v[164:167], v76, s[8:9]
	s_add_u32 s8, s8, 0x16280
	s_addc_u32 s9, s9, 0
	global_load_dwordx4 v[168:171], v76, s[8:9]
	s_add_u32 s8, s8, 0x16280
	s_addc_u32 s9, s9, 0
	global_load_dwordx4 v[172:175], v76, s[8:9]
	s_add_u32 s6, s44, 0x2002000
	s_addc_u32 s7, s45, 0
	ds_read_b32 v226, v211
	ds_read_b32 v227, v211 offset:512
	ds_read_b32 v228, v211 offset:1024
	ds_read_b32 v229, v211 offset:1536
	ds_read_b32 v230, v211 offset:2048
	ds_read_b32 v231, v211 offset:2560
	ds_read_b32 v232, v211 offset:3072
	ds_read_b32 v233, v211 offset:3584
	ds_read_b32 v234, v211 offset:4096
	ds_read_b32 v235, v211 offset:4608
	ds_read_b32 v236, v211 offset:5120
	ds_read_b32 v237, v211 offset:5632
	ds_read_b32 v238, v211 offset:6144
	ds_read_b32 v239, v211 offset:6656
	ds_read_b32 v240, v211 offset:7168
	ds_read_b32 v241, v211 offset:7680
	s_waitcnt lgkmcnt(0)
; #define GAS __attribute__((address_space(1)))
; #define LAS __attribute__((address_space(3)))
; #define LDS_WAIT() asm volatile("s_waitcnt lgkmcnt(0)" ::: "memory")
; __device__ __forceinline__ unsigned pk4_fp8(float a, float b, float c, float d) {
;     a = fminf(fmaxf(a, -448.f), 448.f); b = fminf(fmaxf(b, -448.f), 448.f); c = fminf(fmaxf(c, -448.f), 448.f); d = fminf(fmaxf(d, -448.f), 448.f);
;     int w = __builtin_amdgcn_cvt_pk_fp8_f32(a, b, 0, false); w = __builtin_amdgcn_cvt_pk_fp8_f32(c, d, w, true); return (unsigned)w; }
;     const int pr = item >> 1, kb = 2 * (pr / nblk) + (item & 1), nb = pr % nblk, k0 = 64 * kb, n0 = 32 * nb;
;     const int nr = n0 + (lane & 31); const int sc = MAP == 1 ? src_col_in(nr) : nr;
;     float v[32];
; #pragma unroll
;     for (int i = 0; i < 32; ++i) v[i] = sc >= 0 ? W[(size_t)(k0 + 2 * i + (lane >> 5)) * Nsrc + sc] : 0.f;
; #pragma unroll
;     for (int i = 0; i < 32; ++i) { const int k = k0 + 2 * i + (lane >> 5); float x = v[i] * wscale; if (KS) x *= (k < ksplit ? ksA[k] : ksB[k - ksplit]); scr[(2 * i + (lane >> 5)) * 33 + (lane & 31)] = x; }
;     LDS_WAIT(); asm volatile("" ::: "memory");
;     const int c = lane & 7;
; #pragma unroll
;     for (int j = 0; j < 4; ++j) { const int n = (lane >> 3) + 8 * j; const LAS float* s = scr + (8 * c) * 33 + n;
;         const unsigned long long o = (unsigned long long)pg8::pk4_fp8(s[0 * 33], s[1 * 33], s[2 * 33], s[3 * 33]) | ((unsigned long long)pg8::pk4_fp8(s[4 * 33], s[5 * 33], s[6 * 33], s[7 * 33]) << 32);
;         *(GAS unsigned long long*)(WT + (size_t)(n0 + n) * K + k0 + 8 * c) = o; }
;     LDS_WAIT(); asm volatile("" ::: "memory");
; }
	v_max_f32_e32 v226, v226, v226
	v_max_f32_e32 v227, v227, v227
	v_max_f32_e32 v228, v228, v228
	v_max_f32_e32 v229, v229, v229
	v_max_f32_e32 v230, v230, v230
	v_max_f32_e32 v231, v231, v231
	v_max_f32_e32 v232, v232, v232
	v_max_f32_e32 v233, v233, v233
	v_max_f32_e32 v234, v234, v234
	v_max_f32_e32 v235, v235, v235
	v_max_f32_e32 v236, v236, v236
	v_max_f32_e32 v237, v237, v237
	v_max_f32_e32 v238, v238, v238
	v_max_f32_e32 v239, v239, v239
	v_max_f32_e32 v240, v240, v240
	v_max_f32_e32 v241, v241, v241
	v_med3_f32 v226, v226, s62, v95
	v_med3_f32 v227, v227, s62, v95
	v_med3_f32 v228, v228, s62, v95
	v_med3_f32 v229, v229, s62, v95
	v_med3_f32 v230, v230, s62, v95
	v_med3_f32 v231, v231, s62, v95
	v_med3_f32 v232, v232, s62, v95
	v_med3_f32 v233, v233, s62, v95
	v_med3_f32 v234, v234, s62, v95
	v_med3_f32 v235, v235, s62, v95
	v_med3_f32 v236, v236, s62, v95
	v_med3_f32 v237, v237, s62, v95
	v_med3_f32 v238, v238, s62, v95
	v_med3_f32 v239, v239, s62, v95
	v_med3_f32 v240, v240, s62, v95
	v_med3_f32 v241, v241, s62, v95
	v_mov_b32_e32 v242, 0
	v_mov_b32_e32 v243, 0
	v_mov_b32_e32 v244, 0
	v_mov_b32_e32 v245, 0
	v_cvt_pk_fp8_f32 v242, v226, v227
	v_cvt_pk_fp8_f32 v243, v230, v231
	v_cvt_pk_fp8_f32 v244, v234, v235
	v_cvt_pk_fp8_f32 v245, v238, v239
	v_cvt_pk_fp8_f32 v242, v228, v229 op_sel:[0,0,1]
	v_cvt_pk_fp8_f32 v243, v232, v233 op_sel:[0,0,1]
	v_cvt_pk_fp8_f32 v244, v236, v237 op_sel:[0,0,1]
	v_cvt_pk_fp8_f32 v245, v240, v241 op_sel:[0,0,1]
	s_nop 0
	global_store_dwordx4 v79, v[242:245], s[6:7]
	ds_read_b32 v226, v213
	ds_read_b32 v227, v213 offset:512
	ds_read_b32 v228, v213 offset:1024
	ds_read_b32 v229, v213 offset:1536
	ds_read_b32 v230, v213 offset:2048
	ds_read_b32 v231, v213 offset:2560
	ds_read_b32 v232, v213 offset:3072
	ds_read_b32 v233, v213 offset:3584
	ds_read_b32 v234, v213 offset:4096
	ds_read_b32 v235, v213 offset:4608
	ds_read_b32 v236, v213 offset:5120
	ds_read_b32 v237, v213 offset:5632
	ds_read_b32 v238, v213 offset:6144
	ds_read_b32 v239, v213 offset:6656
	ds_read_b32 v240, v213 offset:7168
	ds_read_b32 v241, v213 offset:7680
	s_waitcnt lgkmcnt(0)
	v_max_f32_e32 v226, v226, v226
	v_max_f32_e32 v227, v227, v227
	v_max_f32_e32 v228, v228, v228
	v_max_f32_e32 v229, v229, v229
	v_max_f32_e32 v230, v230, v230
	v_max_f32_e32 v231, v231, v231
	v_max_f32_e32 v232, v232, v232
	v_max_f32_e32 v233, v233, v233
	v_max_f32_e32 v234, v234, v234
	v_max_f32_e32 v235, v235, v235
	v_max_f32_e32 v236, v236, v236
	v_max_f32_e32 v237, v237, v237
	v_max_f32_e32 v238, v238, v238
	v_max_f32_e32 v239, v239, v239
	v_max_f32_e32 v240, v240, v240
	v_max_f32_e32 v241, v241, v241
	v_med3_f32 v226, v226, s62, v95
	v_med3_f32 v227, v227, s62, v95
	v_med3_f32 v228, v228, s62, v95
	v_med3_f32 v229, v229, s62, v95
	v_med3_f32 v230, v230, s62, v95
	v_med3_f32 v231, v231, s62, v95
	v_med3_f32 v232, v232, s62, v95
	v_med3_f32 v233, v233, s62, v95
	v_med3_f32 v234, v234, s62, v95
	v_med3_f32 v235, v235, s62, v95
	v_med3_f32 v236, v236, s62, v95
	v_med3_f32 v237, v237, s62, v95
	v_med3_f32 v238, v238, s62, v95
	v_med3_f32 v239, v239, s62, v95
	v_med3_f32 v240, v240, s62, v95
	v_med3_f32 v241, v241, s62, v95
	v_mov_b32_e32 v242, 0
	v_mov_b32_e32 v243, 0
	v_mov_b32_e32 v244, 0
	v_mov_b32_e32 v245, 0
	v_cvt_pk_fp8_f32 v242, v226, v227
	v_cvt_pk_fp8_f32 v243, v230, v231
	v_cvt_pk_fp8_f32 v244, v234, v235
	v_cvt_pk_fp8_f32 v245, v238, v239
	v_cvt_pk_fp8_f32 v242, v228, v229 op_sel:[0,0,1]
	v_cvt_pk_fp8_f32 v243, v232, v233 op_sel:[0,0,1]
	v_cvt_pk_fp8_f32 v244, v236, v237 op_sel:[0,0,1]
	v_cvt_pk_fp8_f32 v245, v240, v241 op_sel:[0,0,1]
	s_nop 0
	global_store_dwordx4 v80, v[242:245], s[6:7]
	s_waitcnt vmcnt(12)
	v_mul_f32_e32 v176, 0x43000000, v176
	v_mul_f32_e32 v177, 0x43000000, v177
	v_mul_f32_e32 v178, 0x43000000, v178
	v_mul_f32_e32 v179, 0x43000000, v179
	ds_write_b128 v210, v[176:179]
	v_mul_f32_e32 v180, 0x43000000, v180
	v_mul_f32_e32 v181, 0x43000000, v181
	v_mul_f32_e32 v182, 0x43000000, v182
	v_mul_f32_e32 v183, 0x43000000, v183
	ds_write_b128 v210, v[180:183] offset:1024
	v_mul_f32_e32 v184, 0x43000000, v184
	v_mul_f32_e32 v185, 0x43000000, v185
	v_mul_f32_e32 v186, 0x43000000, v186
	v_mul_f32_e32 v187, 0x43000000, v187
	ds_write_b128 v210, v[184:187] offset:2048
	v_mul_f32_e32 v188, 0x43000000, v188
	v_mul_f32_e32 v189, 0x43000000, v189
	v_mul_f32_e32 v190, 0x43000000, v190
	v_mul_f32_e32 v191, 0x43000000, v191
	ds_write_b128 v210, v[188:191] offset:3072
	v_mul_f32_e32 v192, 0x43000000, v192
	v_mul_f32_e32 v193, 0x43000000, v193
	v_mul_f32_e32 v194, 0x43000000, v194
	v_mul_f32_e32 v195, 0x43000000, v195
	ds_write_b128 v210, v[192:195] offset:4096
	v_mul_f32_e32 v196, 0x43000000, v196
	v_mul_f32_e32 v197, 0x43000000, v197
	v_mul_f32_e32 v198, 0x43000000, v198
	v_mul_f32_e32 v199, 0x43000000, v199
	ds_write_b128 v210, v[196:199] offset:5120
	v_mul_f32_e32 v200, 0x43000000, v200
	v_mul_f32_e32 v201, 0x43000000, v201
	v_mul_f32_e32 v202, 0x43000000, v202
	v_mul_f32_e32 v203, 0x43000000, v203
	ds_write_b128 v210, v[200:203] offset:6144
	v_mul_f32_e32 v204, 0x43000000, v204
	v_mul_f32_e32 v205, 0x43000000, v205
	v_mul_f32_e32 v206, 0x43000000, v206
	v_mul_f32_e32 v207, 0x43000000, v207
	ds_write_b128 v210, v[204:207] offset:7168
	s_waitcnt lgkmcnt(0)
	s_barrier
; #define GAS __attribute__((address_space(1)))
; #define LAS __attribute__((address_space(3)))
; #define LDS_WAIT() asm volatile("s_waitcnt lgkmcnt(0)" ::: "memory")
; __device__ __forceinline__ int nat_dim(int p) { return (p >> 1) + 64 * (p & 1); }
; template <int MAP, bool KS, bool KPERM = false>
; __device__ __forceinline__ void p0_transpose_item(const float* W, int K, int Nsrc, int nblk, bf16* WT, const float* ksA, const float* ksB, int ksplit, LAS float* scr, int item, int lane) {
;     const int kb = item / nblk, nb = item % nblk, k0 = 64 * kb, n0 = 32 * nb;
;     const int nr = n0 + (lane & 31); const int sc = MAP == 1 ? src_col_in(nr) : (MAP == 2 ? nat_dim(nr) : nr);
;     float v[32];
; #pragma unroll
;     for (int i = 0; i < 32; ++i) { const int k = k0 + 2 * i + (lane >> 5); const int ksrc = KPERM ? ((k & ~127) + nat_dim(k & 127)) : k;
;         v[i] = sc >= 0 ? W[(size_t)ksrc * Nsrc + sc] : 0.f; }
; #pragma unroll
;     for (int i = 0; i < 32; ++i) { const int kk = 2 * i + (lane >> 5); const int k = k0 + kk;
;         if (KS) v[i] *= (k < ksplit ? ksA[k] : ksB[k - ksplit]);
;         scr[kk * 33 + (lane & 31)] = v[i]; }
;     LDS_WAIT(); asm volatile("" ::: "memory");
;     const int pr = item >> 1, kb = 2 * (pr / nblk) + (item & 1), nb = pr % nblk, k0 = 64 * kb, n0 = 32 * nb;
;     const int nr = n0 + (lane & 31); const int sc = MAP == 1 ? src_col_in(nr) : nr;
;     float v[32];
; #pragma unroll
;     for (int i = 0; i < 32; ++i) v[i] = sc >= 0 ? W[(size_t)(k0 + 2 * i + (lane >> 5)) * Nsrc + sc] : 0.f;
; #pragma unroll
;     for (int i = 0; i < 32; ++i) { const int k = k0 + 2 * i + (lane >> 5); float x = v[i] * wscale; if (KS) x *= (k < ksplit ? ksA[k] : ksB[k - ksplit]); scr[(2 * i + (lane >> 5)) * 33 + (lane & 31)] = x; }
;     LDS_WAIT(); asm volatile("" ::: "memory");
;     const int c = lane & 7;
; #pragma unroll
;     for (int j = 0; j < 4; ++j) { const int n = (lane >> 3) + 8 * j; const LAS float* s = scr + (8 * c) * 33 + n;
;         const unsigned long long o = (unsigned long long)pg8::pk4_fp8(s[0 * 33], s[1 * 33], s[2 * 33], s[3 * 33]) | ((unsigned long long)pg8::pk4_fp8(s[4 * 33], s[5 * 33], s[6 * 33], s[7 * 33]) << 32);
;         *(GAS unsigned long long*)(WT + (size_t)(n0 + n) * K + k0 + 8 * c) = o; }
;     LDS_WAIT(); asm volatile("" ::: "memory");
	s_add_i32 s24, s23, 8
	s_lshl_b32 s20, s24, 7
	s_cmp_lt_u32 s24, 40
	s_cselect_b32 s21, 0, 0x830
	s_cmp_lt_u32 s24, 72
	s_cselect_b32 s21, s21, 0xfffff030
	s_add_i32 s20, s20, s21
	s_lshl_b32 s20, s20, 2
	s_add_u32 s8, s46, s20
	s_addc_u32 s9, s47, 0
	global_load_dwordx4 v[176:179], v76, s[8:9]
	s_add_u32 s8, s8, 0x16280
	s_addc_u32 s9, s9, 0
	global_load_dwordx4 v[180:183], v76, s[8:9]
	s_add_u32 s8, s8, 0x16280
	s_addc_u32 s9, s9, 0
	global_load_dwordx4 v[184:187], v76, s[8:9]
	s_add_u32 s8, s8, 0x16280
	s_addc_u32 s9, s9, 0
	global_load_dwordx4 v[188:191], v76, s[8:9]
	s_add_u32 s8, s8, 0x16280
	s_addc_u32 s9, s9, 0
	global_load_dwordx4 v[192:195], v76, s[8:9]
	s_add_u32 s8, s8, 0x16280
	s_addc_u32 s9, s9, 0
	global_load_dwordx4 v[196:199], v76, s[8:9]
	s_add_u32 s8, s8, 0x16280
	s_addc_u32 s9, s9, 0
	global_load_dwordx4 v[200:203], v76, s[8:9]
	s_add_u32 s8, s8, 0x16280
	s_addc_u32 s9, s9, 0
	global_load_dwordx4 v[204:207], v76, s[8:9]
	s_add_u32 s6, s44, 0x3002000
	s_addc_u32 s7, s45, 0
	ds_read_b32 v226, v212
	ds_read_b32 v227, v212 offset:512
	ds_read_b32 v228, v212 offset:1024
	ds_read_b32 v229, v212 offset:1536
	ds_read_b32 v230, v212 offset:2048
	ds_read_b32 v231, v212 offset:2560
	ds_read_b32 v232, v212 offset:3072
	ds_read_b32 v233, v212 offset:3584
	ds_read_b32 v234, v212 offset:4096
	ds_read_b32 v235, v212 offset:4608
	ds_read_b32 v236, v212 offset:5120
	ds_read_b32 v237, v212 offset:5632
	ds_read_b32 v238, v212 offset:6144
	ds_read_b32 v239, v212 offset:6656
	ds_read_b32 v240, v212 offset:7168
	ds_read_b32 v241, v212 offset:7680
	s_waitcnt lgkmcnt(0)
	v_max_f32_e32 v226, v226, v226
	v_max_f32_e32 v227, v227, v227
	v_max_f32_e32 v228, v228, v228
	v_max_f32_e32 v229, v229, v229
	v_max_f32_e32 v230, v230, v230
	v_max_f32_e32 v231, v231, v231
	v_max_f32_e32 v232, v232, v232
	v_max_f32_e32 v233, v233, v233
	v_max_f32_e32 v234, v234, v234
	v_max_f32_e32 v235, v235, v235
	v_max_f32_e32 v236, v236, v236
	v_max_f32_e32 v237, v237, v237
	v_max_f32_e32 v238, v238, v238
	v_max_f32_e32 v239, v239, v239
	v_max_f32_e32 v240, v240, v240
	v_max_f32_e32 v241, v241, v241
	v_med3_f32 v226, v226, s62, v95
	v_med3_f32 v227, v227, s62, v95
	v_med3_f32 v228, v228, s62, v95
	v_med3_f32 v229, v229, s62, v95
	v_med3_f32 v230, v230, s62, v95
	v_med3_f32 v231, v231, s62, v95
	v_med3_f32 v232, v232, s62, v95
	v_med3_f32 v233, v233, s62, v95
	v_med3_f32 v234, v234, s62, v95
	v_med3_f32 v235, v235, s62, v95
	v_med3_f32 v236, v236, s62, v95
	v_med3_f32 v237, v237, s62, v95
	v_med3_f32 v238, v238, s62, v95
	v_med3_f32 v239, v239, s62, v95
	v_med3_f32 v240, v240, s62, v95
	v_med3_f32 v241, v241, s62, v95
	v_mov_b32_e32 v242, 0
	v_mov_b32_e32 v243, 0
	v_mov_b32_e32 v244, 0
	v_mov_b32_e32 v245, 0
	v_cvt_pk_fp8_f32 v242, v226, v227
	v_cvt_pk_fp8_f32 v243, v230, v231
	v_cvt_pk_fp8_f32 v244, v234, v235
	v_cvt_pk_fp8_f32 v245, v238, v239
	v_cvt_pk_fp8_f32 v242, v228, v229 op_sel:[0,0,1]
	v_cvt_pk_fp8_f32 v243, v232, v233 op_sel:[0,0,1]
	v_cvt_pk_fp8_f32 v244, v236, v237 op_sel:[0,0,1]
	v_cvt_pk_fp8_f32 v245, v240, v241 op_sel:[0,0,1]
	s_nop 0
	global_store_dwordx4 v79, v[242:245], s[6:7]
	ds_read_b32 v226, v214
	ds_read_b32 v227, v214 offset:512
	ds_read_b32 v228, v214 offset:1024
	ds_read_b32 v229, v214 offset:1536
	ds_read_b32 v230, v214 offset:2048
	ds_read_b32 v231, v214 offset:2560
	ds_read_b32 v232, v214 offset:3072
	ds_read_b32 v233, v214 offset:3584
	ds_read_b32 v234, v214 offset:4096
	ds_read_b32 v235, v214 offset:4608
	ds_read_b32 v236, v214 offset:5120
	ds_read_b32 v237, v214 offset:5632
	ds_read_b32 v238, v214 offset:6144
	ds_read_b32 v239, v214 offset:6656
	ds_read_b32 v240, v214 offset:7168
	ds_read_b32 v241, v214 offset:7680
	s_waitcnt lgkmcnt(0)
	v_max_f32_e32 v226, v226, v226
	v_max_f32_e32 v227, v227, v227
	v_max_f32_e32 v228, v228, v228
	v_max_f32_e32 v229, v229, v229
	v_max_f32_e32 v230, v230, v230
	v_max_f32_e32 v231, v231, v231
	v_max_f32_e32 v232, v232, v232
	v_max_f32_e32 v233, v233, v233
	v_max_f32_e32 v234, v234, v234
	v_max_f32_e32 v235, v235, v235
	v_max_f32_e32 v236, v236, v236
	v_max_f32_e32 v237, v237, v237
	v_max_f32_e32 v238, v238, v238
	v_max_f32_e32 v239, v239, v239
	v_max_f32_e32 v240, v240, v240
	v_max_f32_e32 v241, v241, v241
	v_med3_f32 v226, v226, s62, v95
	v_med3_f32 v227, v227, s62, v95
	v_med3_f32 v228, v228, s62, v95
	v_med3_f32 v229, v229, s62, v95
	v_med3_f32 v230, v230, s62, v95
	v_med3_f32 v231, v231, s62, v95
	v_med3_f32 v232, v232, s62, v95
	v_med3_f32 v233, v233, s62, v95
	v_med3_f32 v234, v234, s62, v95
	v_med3_f32 v235, v235, s62, v95
	v_med3_f32 v236, v236, s62, v95
	v_med3_f32 v237, v237, s62, v95
	v_med3_f32 v238, v238, s62, v95
	v_med3_f32 v239, v239, s62, v95
	v_med3_f32 v240, v240, s62, v95
	v_med3_f32 v241, v241, s62, v95
	v_mov_b32_e32 v242, 0
	v_mov_b32_e32 v243, 0
	v_mov_b32_e32 v244, 0
	v_mov_b32_e32 v245, 0
	v_cvt_pk_fp8_f32 v242, v226, v227
	v_cvt_pk_fp8_f32 v243, v230, v231
	v_cvt_pk_fp8_f32 v244, v234, v235
	v_cvt_pk_fp8_f32 v245, v238, v239
	v_cvt_pk_fp8_f32 v242, v228, v229 op_sel:[0,0,1]
	v_cvt_pk_fp8_f32 v243, v232, v233 op_sel:[0,0,1]
	v_cvt_pk_fp8_f32 v244, v236, v237 op_sel:[0,0,1]
	v_cvt_pk_fp8_f32 v245, v240, v241 op_sel:[0,0,1]
	s_nop 0
	global_store_dwordx4 v80, v[242:245], s[6:7]
	s_waitcnt vmcnt(12)
	v_mul_f32_e32 v144, v42, v144
	v_mul_f32_e32 v145, v42, v145
	v_mul_f32_e32 v146, v42, v146
	v_mul_f32_e32 v147, v42, v147
	ds_write_b128 v209, v[144:147]
	v_mul_f32_e32 v148, v43, v148
	v_mul_f32_e32 v149, v43, v149
	v_mul_f32_e32 v150, v43, v150
	v_mul_f32_e32 v151, v43, v151
	ds_write_b128 v209, v[148:151] offset:1024
	v_mul_f32_e32 v152, v44, v152
	v_mul_f32_e32 v153, v44, v153
	v_mul_f32_e32 v154, v44, v154
	v_mul_f32_e32 v155, v44, v155
	ds_write_b128 v209, v[152:155] offset:2048
	v_mul_f32_e32 v156, v45, v156
	v_mul_f32_e32 v157, v45, v157
	v_mul_f32_e32 v158, v45, v158
	v_mul_f32_e32 v159, v45, v159
	ds_write_b128 v209, v[156:159] offset:3072
	v_mul_f32_e32 v160, v46, v160
	v_mul_f32_e32 v161, v46, v161
	v_mul_f32_e32 v162, v46, v162
	v_mul_f32_e32 v163, v46, v163
	ds_write_b128 v209, v[160:163] offset:4096
	v_mul_f32_e32 v164, v47, v164
	v_mul_f32_e32 v165, v47, v165
	v_mul_f32_e32 v166, v47, v166
	v_mul_f32_e32 v167, v47, v167
	ds_write_b128 v209, v[164:167] offset:5120
	v_mul_f32_e32 v168, v48, v168
	v_mul_f32_e32 v169, v48, v169
	v_mul_f32_e32 v170, v48, v170
	v_mul_f32_e32 v171, v48, v171
	ds_write_b128 v209, v[168:171] offset:6144
	v_mul_f32_e32 v172, v49, v172
	v_mul_f32_e32 v173, v49, v173
	v_mul_f32_e32 v174, v49, v174
	v_mul_f32_e32 v175, v49, v175
	ds_write_b128 v209, v[172:175] offset:7168
	s_waitcnt lgkmcnt(0)
	s_barrier
; #define GAS __attribute__((address_space(1)))
; #define LAS __attribute__((address_space(3)))
; #define LDS_WAIT() asm volatile("s_waitcnt lgkmcnt(0)" ::: "memory")
; __device__ __forceinline__ unsigned pk2(float lo, float hi) { return f2bf(lo) | (f2bf(hi) << 16); }
; __device__ __forceinline__ int nat_dim(int p) { return (p >> 1) + 64 * (p & 1); }
; __device__ __forceinline__ int src_col_in(int c) {
;     if (c < 5120) { const int blk = c >> 7, p = c & 127; const bool rope = blk < 16 || ((((blk - 16) >> 2) & 1) == 0); const int d = rope ? (p >> 1) + 64 * (p & 1) : p; return blk * 128 + d; }
;     if (c < OFF_Z) return c + 2096;
;     if (c < OFF_G) return c - 4048;
;     if (c < OFF_DT) return 5120 + (c - OFF_G);
;     if (c < NSRC) return c;
; template <int MAP, bool KS, bool KPERM = false>
; __device__ __forceinline__ void p0_transpose_item(const float* W, int K, int Nsrc, int nblk, bf16* WT, const float* ksA, const float* ksB, int ksplit, LAS float* scr, int item, int lane) {
;     const int kb = item / nblk, nb = item % nblk, k0 = 64 * kb, n0 = 32 * nb;
;     const int nr = n0 + (lane & 31); const int sc = MAP == 1 ? src_col_in(nr) : (MAP == 2 ? nat_dim(nr) : nr);
;     float v[32];
; #pragma unroll
;     for (int i = 0; i < 32; ++i) { const int k = k0 + 2 * i + (lane >> 5); const int ksrc = KPERM ? ((k & ~127) + nat_dim(k & 127)) : k;
;         v[i] = sc >= 0 ? W[(size_t)ksrc * Nsrc + sc] : 0.f; }
; #pragma unroll
;     for (int i = 0; i < 32; ++i) { const int kk = 2 * i + (lane >> 5); const int k = k0 + kk;
;         if (KS) v[i] *= (k < ksplit ? ksA[k] : ksB[k - ksplit]);
;         scr[kk * 33 + (lane & 31)] = v[i]; }
;     LDS_WAIT(); asm volatile("" ::: "memory");
;     const int c = lane & 7;
; #pragma unroll
;     for (int j = 0; j < 4; ++j) { const int n = (lane >> 3) + 8 * j; const LAS float* s = scr + (8 * c) * 33 + n;
;         v4u o; o.x = pk2(s[0 * 33], s[1 * 33]); o.y = pk2(s[2 * 33], s[3 * 33]); o.z = pk2(s[4 * 33], s[5 * 33]); o.w = pk2(s[6 * 33], s[7 * 33]);
;         *(GAS v4u*)(WT + (size_t)(n0 + n) * K + k0 + 8 * c) = o; }
	s_add_i32 s24, s23, 16
	s_lshl_b32 s20, s24, 7
	s_cmp_lt_u32 s24, 40
	s_cselect_b32 s21, 0, 0x830
	s_cmp_lt_u32 s24, 72
	s_cselect_b32 s21, s21, 0xfffff030
	s_add_i32 s20, s20, s21
	s_lshl_b32 s20, s20, 2
	s_add_u32 s8, s46, s20
	s_addc_u32 s9, s47, 0
	global_load_dwordx4 v[144:147], v76, s[8:9]
	s_add_u32 s8, s8, 0x16280
	s_addc_u32 s9, s9, 0
	global_load_dwordx4 v[148:151], v76, s[8:9]
	s_add_u32 s8, s8, 0x16280
	s_addc_u32 s9, s9, 0
	global_load_dwordx4 v[152:155], v76, s[8:9]
	s_add_u32 s8, s8, 0x16280
	s_addc_u32 s9, s9, 0
	global_load_dwordx4 v[156:159], v76, s[8:9]
	s_add_u32 s8, s8, 0x16280
	s_addc_u32 s9, s9, 0
	global_load_dwordx4 v[160:163], v76, s[8:9]
	s_add_u32 s8, s8, 0x16280
	s_addc_u32 s9, s9, 0
	global_load_dwordx4 v[164:167], v76, s[8:9]
	s_add_u32 s8, s8, 0x16280
	s_addc_u32 s9, s9, 0
	global_load_dwordx4 v[168:171], v76, s[8:9]
	s_add_u32 s8, s8, 0x16280
	s_addc_u32 s9, s9, 0
	global_load_dwordx4 v[172:175], v76, s[8:9]
	s_add_i32 s24, s23, 0
	s_mul_i32 s20, s24, 0x100000
	s_add_u32 s6, s48, s20
	s_addc_u32 s7, s49, 0
	s_cmp_lt_u32 s24, 16
	s_cselect_b32 s20, 1, 0
	s_sub_i32 s21, s24, 16
	s_bitcmp0_b32 s21, 2
	s_cselect_b32 s21, 1, 0
	s_cmp_lt_u32 s24, 40
	s_cselect_b32 s21, s21, 0
	s_or_b32 s20, s20, s21
	s_cmp_lg_u32 s20, 0
	s_cselect_b64 s[20:21], -1, 0
	v_cndmask_b32_e64 v91, v83, v87, s[20:21]
	v_cndmask_b32_e64 v92, v84, v88, s[20:21]
	v_cndmask_b32_e64 v93, v85, v89, s[20:21]
	v_cndmask_b32_e64 v94, v86, v90, s[20:21]
	ds_read_b32 v226, v112
	ds_read_b32 v227, v112 offset:512
	ds_read_b32 v228, v112 offset:1024
	ds_read_b32 v229, v112 offset:1536
	ds_read_b32 v230, v112 offset:2048
	ds_read_b32 v231, v112 offset:2560
	ds_read_b32 v232, v112 offset:3072
	ds_read_b32 v233, v112 offset:3584
	s_waitcnt lgkmcnt(0)
	v_bfe_u32 v120, v226, 16, 1
	v_bfe_u32 v121, v227, 16, 1
	v_bfe_u32 v122, v228, 16, 1
	v_bfe_u32 v123, v229, 16, 1
	v_bfe_u32 v124, v230, 16, 1
	v_bfe_u32 v125, v231, 16, 1
	v_bfe_u32 v126, v232, 16, 1
	v_bfe_u32 v127, v233, 16, 1
	v_add3_u32 v226, v226, v120, s63
	v_add3_u32 v227, v227, v121, s63
	v_add3_u32 v228, v228, v122, s63
	v_add3_u32 v229, v229, v123, s63
	v_add3_u32 v230, v230, v124, s63
	v_add3_u32 v231, v231, v125, s63
	v_add3_u32 v232, v232, v126, s63
	v_add3_u32 v233, v233, v127, s63
	v_perm_b32 v242, v227, v226, s64
	v_perm_b32 v243, v229, v228, s64
	v_perm_b32 v244, v231, v230, s64
	v_perm_b32 v245, v233, v232, s64
	s_nop 0
	global_store_dwordx4 v91, v[242:245], s[6:7]
	ds_read_b32 v226, v114
	ds_read_b32 v227, v114 offset:512
	ds_read_b32 v228, v114 offset:1024
	ds_read_b32 v229, v114 offset:1536
	ds_read_b32 v230, v114 offset:2048
	ds_read_b32 v231, v114 offset:2560
	ds_read_b32 v232, v114 offset:3072
	ds_read_b32 v233, v114 offset:3584
	s_waitcnt lgkmcnt(0)
	v_bfe_u32 v120, v226, 16, 1
	v_bfe_u32 v121, v227, 16, 1
	v_bfe_u32 v122, v228, 16, 1
	v_bfe_u32 v123, v229, 16, 1
	v_bfe_u32 v124, v230, 16, 1
	v_bfe_u32 v125, v231, 16, 1
	v_bfe_u32 v126, v232, 16, 1
	v_bfe_u32 v127, v233, 16, 1
	v_add3_u32 v226, v226, v120, s63
	v_add3_u32 v227, v227, v121, s63
	v_add3_u32 v228, v228, v122, s63
	v_add3_u32 v229, v229, v123, s63
	v_add3_u32 v230, v230, v124, s63
	v_add3_u32 v231, v231, v125, s63
	v_add3_u32 v232, v232, v126, s63
	v_add3_u32 v233, v233, v127, s63
	v_perm_b32 v242, v227, v226, s64
	v_perm_b32 v243, v229, v228, s64
	v_perm_b32 v244, v231, v230, s64
	v_perm_b32 v245, v233, v232, s64
	s_nop 0
	global_store_dwordx4 v92, v[242:245], s[6:7]
	ds_read_b32 v226, v116
	ds_read_b32 v227, v116 offset:512
	ds_read_b32 v228, v116 offset:1024
	ds_read_b32 v229, v116 offset:1536
	ds_read_b32 v230, v116 offset:2048
	ds_read_b32 v231, v116 offset:2560
	ds_read_b32 v232, v116 offset:3072
	ds_read_b32 v233, v116 offset:3584
	s_waitcnt lgkmcnt(0)
	v_bfe_u32 v120, v226, 16, 1
	v_bfe_u32 v121, v227, 16, 1
	v_bfe_u32 v122, v228, 16, 1
	v_bfe_u32 v123, v229, 16, 1
	v_bfe_u32 v124, v230, 16, 1
	v_bfe_u32 v125, v231, 16, 1
	v_bfe_u32 v126, v232, 16, 1
	v_bfe_u32 v127, v233, 16, 1
	v_add3_u32 v226, v226, v120, s63
	v_add3_u32 v227, v227, v121, s63
	v_add3_u32 v228, v228, v122, s63
	v_add3_u32 v229, v229, v123, s63
	v_add3_u32 v230, v230, v124, s63
	v_add3_u32 v231, v231, v125, s63
	v_add3_u32 v232, v232, v126, s63
	v_add3_u32 v233, v233, v127, s63
	v_perm_b32 v242, v227, v226, s64
	v_perm_b32 v243, v229, v228, s64
	v_perm_b32 v244, v231, v230, s64
	v_perm_b32 v245, v233, v232, s64
	s_nop 0
	global_store_dwordx4 v93, v[242:245], s[6:7]
	ds_read_b32 v226, v118
	ds_read_b32 v227, v118 offset:512
	ds_read_b32 v228, v118 offset:1024
	ds_read_b32 v229, v118 offset:1536
	ds_read_b32 v230, v118 offset:2048
	ds_read_b32 v231, v118 offset:2560
	ds_read_b32 v232, v118 offset:3072
	ds_read_b32 v233, v118 offset:3584
	s_waitcnt lgkmcnt(0)
	v_bfe_u32 v120, v226, 16, 1
	v_bfe_u32 v121, v227, 16, 1
	v_bfe_u32 v122, v228, 16, 1
	v_bfe_u32 v123, v229, 16, 1
	v_bfe_u32 v124, v230, 16, 1
	v_bfe_u32 v125, v231, 16, 1
	v_bfe_u32 v126, v232, 16, 1
	v_bfe_u32 v127, v233, 16, 1
	v_add3_u32 v226, v226, v120, s63
	v_add3_u32 v227, v227, v121, s63
	v_add3_u32 v228, v228, v122, s63
	v_add3_u32 v229, v229, v123, s63
	v_add3_u32 v230, v230, v124, s63
	v_add3_u32 v231, v231, v125, s63
	v_add3_u32 v232, v232, v126, s63
	v_add3_u32 v233, v233, v127, s63
	v_perm_b32 v242, v227, v226, s64
	v_perm_b32 v243, v229, v228, s64
	v_perm_b32 v244, v231, v230, s64
	v_perm_b32 v245, v233, v232, s64
	s_nop 0
	global_store_dwordx4 v94, v[242:245], s[6:7]
	s_waitcnt vmcnt(14)
	v_mul_f32_e32 v176, v42, v176
	v_mul_f32_e32 v177, v42, v177
	v_mul_f32_e32 v178, v42, v178
	v_mul_f32_e32 v179, v42, v179
	ds_write_b128 v210, v[176:179]
	v_mul_f32_e32 v180, v43, v180
	v_mul_f32_e32 v181, v43, v181
	v_mul_f32_e32 v182, v43, v182
	v_mul_f32_e32 v183, v43, v183
	ds_write_b128 v210, v[180:183] offset:1024
	v_mul_f32_e32 v184, v44, v184
	v_mul_f32_e32 v185, v44, v185
	v_mul_f32_e32 v186, v44, v186
	v_mul_f32_e32 v187, v44, v187
	ds_write_b128 v210, v[184:187] offset:2048
	v_mul_f32_e32 v188, v45, v188
	v_mul_f32_e32 v189, v45, v189
	v_mul_f32_e32 v190, v45, v190
	v_mul_f32_e32 v191, v45, v191
	ds_write_b128 v210, v[188:191] offset:3072
	v_mul_f32_e32 v192, v46, v192
	v_mul_f32_e32 v193, v46, v193
	v_mul_f32_e32 v194, v46, v194
	v_mul_f32_e32 v195, v46, v195
	ds_write_b128 v210, v[192:195] offset:4096
	v_mul_f32_e32 v196, v47, v196
	v_mul_f32_e32 v197, v47, v197
	v_mul_f32_e32 v198, v47, v198
	v_mul_f32_e32 v199, v47, v199
	ds_write_b128 v210, v[196:199] offset:5120
	v_mul_f32_e32 v200, v48, v200
	v_mul_f32_e32 v201, v48, v201
	v_mul_f32_e32 v202, v48, v202
	v_mul_f32_e32 v203, v48, v203
	ds_write_b128 v210, v[200:203] offset:6144
	v_mul_f32_e32 v204, v49, v204
	v_mul_f32_e32 v205, v49, v205
	v_mul_f32_e32 v206, v49, v206
	v_mul_f32_e32 v207, v49, v207
	ds_write_b128 v210, v[204:207] offset:7168
	s_waitcnt lgkmcnt(0)
	s_barrier
; #define GAS __attribute__((address_space(1)))
; #define LAS __attribute__((address_space(3)))
; #define LDS_WAIT() asm volatile("s_waitcnt lgkmcnt(0)" ::: "memory")
; __device__ __forceinline__ unsigned pk2(float lo, float hi) { return f2bf(lo) | (f2bf(hi) << 16); }
; __device__ __forceinline__ int nat_dim(int p) { return (p >> 1) + 64 * (p & 1); }
; __device__ __forceinline__ int src_col_in(int c) {
;     if (c < 5120) { const int blk = c >> 7, p = c & 127; const bool rope = blk < 16 || ((((blk - 16) >> 2) & 1) == 0); const int d = rope ? (p >> 1) + 64 * (p & 1) : p; return blk * 128 + d; }
;     if (c < OFF_Z) return c + 2096;
;     if (c < OFF_G) return c - 4048;
;     if (c < OFF_DT) return 5120 + (c - OFF_G);
;     if (c < NSRC) return c;
; template <int MAP, bool KS, bool KPERM = false>
; __device__ __forceinline__ void p0_transpose_item(const float* W, int K, int Nsrc, int nblk, bf16* WT, const float* ksA, const float* ksB, int ksplit, LAS float* scr, int item, int lane) {
;     const int kb = item / nblk, nb = item % nblk, k0 = 64 * kb, n0 = 32 * nb;
;     const int nr = n0 + (lane & 31); const int sc = MAP == 1 ? src_col_in(nr) : (MAP == 2 ? nat_dim(nr) : nr);
;     float v[32];
; #pragma unroll
;     for (int i = 0; i < 32; ++i) { const int k = k0 + 2 * i + (lane >> 5); const int ksrc = KPERM ? ((k & ~127) + nat_dim(k & 127)) : k;
;         v[i] = sc >= 0 ? W[(size_t)ksrc * Nsrc + sc] : 0.f; }
; #pragma unroll
;     for (int i = 0; i < 32; ++i) { const int kk = 2 * i + (lane >> 5); const int k = k0 + kk;
;         if (KS) v[i] *= (k < ksplit ? ksA[k] : ksB[k - ksplit]);
;         scr[kk * 33 + (lane & 31)] = v[i]; }
;     LDS_WAIT(); asm volatile("" ::: "memory");
;     const int c = lane & 7;
; #pragma unroll
;     for (int j = 0; j < 4; ++j) { const int n = (lane >> 3) + 8 * j; const LAS float* s = scr + (8 * c) * 33 + n;
;         v4u o; o.x = pk2(s[0 * 33], s[1 * 33]); o.y = pk2(s[2 * 33], s[3 * 33]); o.z = pk2(s[4 * 33], s[5 * 33]); o.w = pk2(s[6 * 33], s[7 * 33]);
;         *(GAS v4u*)(WT + (size_t)(n0 + n) * K + k0 + 8 * c) = o; }
	s_add_i32 s24, s23, 24
	s_lshl_b32 s20, s24, 7
	s_cmp_lt_u32 s24, 40
	s_cselect_b32 s21, 0, 0x830
	s_cmp_lt_u32 s24, 72
	s_cselect_b32 s21, s21, 0xfffff030
	s_add_i32 s20, s20, s21
	s_lshl_b32 s20, s20, 2
	s_add_u32 s8, s46, s20
	s_addc_u32 s9, s47, 0
	global_load_dwordx4 v[176:179], v76, s[8:9]
	s_add_u32 s8, s8, 0x16280
	s_addc_u32 s9, s9, 0
	global_load_dwordx4 v[180:183], v76, s[8:9]
	s_add_u32 s8, s8, 0x16280
	s_addc_u32 s9, s9, 0
	global_load_dwordx4 v[184:187], v76, s[8:9]
	s_add_u32 s8, s8, 0x16280
	s_addc_u32 s9, s9, 0
	global_load_dwordx4 v[188:191], v76, s[8:9]
	s_add_u32 s8, s8, 0x16280
	s_addc_u32 s9, s9, 0
	global_load_dwordx4 v[192:195], v76, s[8:9]
	s_add_u32 s8, s8, 0x16280
	s_addc_u32 s9, s9, 0
	global_load_dwordx4 v[196:199], v76, s[8:9]
	s_add_u32 s8, s8, 0x16280
	s_addc_u32 s9, s9, 0
	global_load_dwordx4 v[200:203], v76, s[8:9]
	s_add_u32 s8, s8, 0x16280
	s_addc_u32 s9, s9, 0
	global_load_dwordx4 v[204:207], v76, s[8:9]
	s_add_i32 s24, s23, 8
	s_mul_i32 s20, s24, 0x100000
	s_add_u32 s6, s48, s20
	s_addc_u32 s7, s49, 0
	s_cmp_lt_u32 s24, 16
	s_cselect_b32 s20, 1, 0
	s_sub_i32 s21, s24, 16
	s_bitcmp0_b32 s21, 2
	s_cselect_b32 s21, 1, 0
	s_cmp_lt_u32 s24, 40
	s_cselect_b32 s21, s21, 0
	s_or_b32 s20, s20, s21
	s_cmp_lg_u32 s20, 0
	s_cselect_b64 s[20:21], -1, 0
	v_cndmask_b32_e64 v91, v83, v87, s[20:21]
	v_cndmask_b32_e64 v92, v84, v88, s[20:21]
	v_cndmask_b32_e64 v93, v85, v89, s[20:21]
	v_cndmask_b32_e64 v94, v86, v90, s[20:21]
	ds_read_b32 v226, v113
	ds_read_b32 v227, v113 offset:512
	ds_read_b32 v228, v113 offset:1024
	ds_read_b32 v229, v113 offset:1536
	ds_read_b32 v230, v113 offset:2048
	ds_read_b32 v231, v113 offset:2560
	ds_read_b32 v232, v113 offset:3072
	ds_read_b32 v233, v113 offset:3584
	s_waitcnt lgkmcnt(0)
	v_bfe_u32 v120, v226, 16, 1
	v_bfe_u32 v121, v227, 16, 1
	v_bfe_u32 v122, v228, 16, 1
	v_bfe_u32 v123, v229, 16, 1
	v_bfe_u32 v124, v230, 16, 1
	v_bfe_u32 v125, v231, 16, 1
	v_bfe_u32 v126, v232, 16, 1
	v_bfe_u32 v127, v233, 16, 1
	v_add3_u32 v226, v226, v120, s63
	v_add3_u32 v227, v227, v121, s63
	v_add3_u32 v228, v228, v122, s63
	v_add3_u32 v229, v229, v123, s63
	v_add3_u32 v230, v230, v124, s63
	v_add3_u32 v231, v231, v125, s63
	v_add3_u32 v232, v232, v126, s63
	v_add3_u32 v233, v233, v127, s63
	v_perm_b32 v242, v227, v226, s64
	v_perm_b32 v243, v229, v228, s64
	v_perm_b32 v244, v231, v230, s64
	v_perm_b32 v245, v233, v232, s64
	s_nop 0
	global_store_dwordx4 v91, v[242:245], s[6:7]
	ds_read_b32 v226, v115
	ds_read_b32 v227, v115 offset:512
	ds_read_b32 v228, v115 offset:1024
	ds_read_b32 v229, v115 offset:1536
	ds_read_b32 v230, v115 offset:2048
	ds_read_b32 v231, v115 offset:2560
	ds_read_b32 v232, v115 offset:3072
	ds_read_b32 v233, v115 offset:3584
	s_waitcnt lgkmcnt(0)
	v_bfe_u32 v120, v226, 16, 1
	v_bfe_u32 v121, v227, 16, 1
	v_bfe_u32 v122, v228, 16, 1
	v_bfe_u32 v123, v229, 16, 1
	v_bfe_u32 v124, v230, 16, 1
	v_bfe_u32 v125, v231, 16, 1
	v_bfe_u32 v126, v232, 16, 1
	v_bfe_u32 v127, v233, 16, 1
	v_add3_u32 v226, v226, v120, s63
	v_add3_u32 v227, v227, v121, s63
	v_add3_u32 v228, v228, v122, s63
	v_add3_u32 v229, v229, v123, s63
	v_add3_u32 v230, v230, v124, s63
	v_add3_u32 v231, v231, v125, s63
	v_add3_u32 v232, v232, v126, s63
	v_add3_u32 v233, v233, v127, s63
	v_perm_b32 v242, v227, v226, s64
	v_perm_b32 v243, v229, v228, s64
	v_perm_b32 v244, v231, v230, s64
	v_perm_b32 v245, v233, v232, s64
	s_nop 0
	global_store_dwordx4 v92, v[242:245], s[6:7]
	ds_read_b32 v226, v117
	ds_read_b32 v227, v117 offset:512
	ds_read_b32 v228, v117 offset:1024
	ds_read_b32 v229, v117 offset:1536
	ds_read_b32 v230, v117 offset:2048
	ds_read_b32 v231, v117 offset:2560
	ds_read_b32 v232, v117 offset:3072
	ds_read_b32 v233, v117 offset:3584
	s_waitcnt lgkmcnt(0)
	v_bfe_u32 v120, v226, 16, 1
	v_bfe_u32 v121, v227, 16, 1
	v_bfe_u32 v122, v228, 16, 1
	v_bfe_u32 v123, v229, 16, 1
	v_bfe_u32 v124, v230, 16, 1
	v_bfe_u32 v125, v231, 16, 1
	v_bfe_u32 v126, v232, 16, 1
	v_bfe_u32 v127, v233, 16, 1
	v_add3_u32 v226, v226, v120, s63
	v_add3_u32 v227, v227, v121, s63
	v_add3_u32 v228, v228, v122, s63
	v_add3_u32 v229, v229, v123, s63
	v_add3_u32 v230, v230, v124, s63
	v_add3_u32 v231, v231, v125, s63
	v_add3_u32 v232, v232, v126, s63
	v_add3_u32 v233, v233, v127, s63
	v_perm_b32 v242, v227, v226, s64
	v_perm_b32 v243, v229, v228, s64
	v_perm_b32 v244, v231, v230, s64
	v_perm_b32 v245, v233, v232, s64
	s_nop 0
	global_store_dwordx4 v93, v[242:245], s[6:7]
	ds_read_b32 v226, v119
	ds_read_b32 v227, v119 offset:512
	ds_read_b32 v228, v119 offset:1024
	ds_read_b32 v229, v119 offset:1536
	ds_read_b32 v230, v119 offset:2048
	ds_read_b32 v231, v119 offset:2560
	ds_read_b32 v232, v119 offset:3072
	ds_read_b32 v233, v119 offset:3584
	s_waitcnt lgkmcnt(0)
	v_bfe_u32 v120, v226, 16, 1
	v_bfe_u32 v121, v227, 16, 1
	v_bfe_u32 v122, v228, 16, 1
	v_bfe_u32 v123, v229, 16, 1
	v_bfe_u32 v124, v230, 16, 1
	v_bfe_u32 v125, v231, 16, 1
	v_bfe_u32 v126, v232, 16, 1
	v_bfe_u32 v127, v233, 16, 1
	v_add3_u32 v226, v226, v120, s63
	v_add3_u32 v227, v227, v121, s63
	v_add3_u32 v228, v228, v122, s63
	v_add3_u32 v229, v229, v123, s63
	v_add3_u32 v230, v230, v124, s63
	v_add3_u32 v231, v231, v125, s63
	v_add3_u32 v232, v232, v126, s63
	v_add3_u32 v233, v233, v127, s63
	v_perm_b32 v242, v227, v226, s64
	v_perm_b32 v243, v229, v228, s64
	v_perm_b32 v244, v231, v230, s64
	v_perm_b32 v245, v233, v232, s64
	s_nop 0
	global_store_dwordx4 v94, v[242:245], s[6:7]
	s_waitcnt vmcnt(16)
	v_mul_f32_e32 v144, v42, v144
	v_mul_f32_e32 v145, v42, v145
	v_mul_f32_e32 v146, v42, v146
	v_mul_f32_e32 v147, v42, v147
	ds_write_b128 v209, v[144:147]
	v_mul_f32_e32 v148, v43, v148
	v_mul_f32_e32 v149, v43, v149
	v_mul_f32_e32 v150, v43, v150
	v_mul_f32_e32 v151, v43, v151
	ds_write_b128 v209, v[148:151] offset:1024
	v_mul_f32_e32 v152, v44, v152
	v_mul_f32_e32 v153, v44, v153
	v_mul_f32_e32 v154, v44, v154
	v_mul_f32_e32 v155, v44, v155
	ds_write_b128 v209, v[152:155] offset:2048
	v_mul_f32_e32 v156, v45, v156
	v_mul_f32_e32 v157, v45, v157
	v_mul_f32_e32 v158, v45, v158
	v_mul_f32_e32 v159, v45, v159
	ds_write_b128 v209, v[156:159] offset:3072
	v_mul_f32_e32 v160, v46, v160
	v_mul_f32_e32 v161, v46, v161
	v_mul_f32_e32 v162, v46, v162
	v_mul_f32_e32 v163, v46, v163
	ds_write_b128 v209, v[160:163] offset:4096
	v_mul_f32_e32 v164, v47, v164
	v_mul_f32_e32 v165, v47, v165
	v_mul_f32_e32 v166, v47, v166
	v_mul_f32_e32 v167, v47, v167
	ds_write_b128 v209, v[164:167] offset:5120
	v_mul_f32_e32 v168, v48, v168
	v_mul_f32_e32 v169, v48, v169
	v_mul_f32_e32 v170, v48, v170
	v_mul_f32_e32 v171, v48, v171
	ds_write_b128 v209, v[168:171] offset:6144
	v_mul_f32_e32 v172, v49, v172
	v_mul_f32_e32 v173, v49, v173
	v_mul_f32_e32 v174, v49, v174
	v_mul_f32_e32 v175, v49, v175
	ds_write_b128 v209, v[172:175] offset:7168
	s_waitcnt lgkmcnt(0)
	s_barrier
; #define GAS __attribute__((address_space(1)))
; #define LAS __attribute__((address_space(3)))
; #define LDS_WAIT() asm volatile("s_waitcnt lgkmcnt(0)" ::: "memory")
; __device__ __forceinline__ unsigned pk2(float lo, float hi) { return f2bf(lo) | (f2bf(hi) << 16); }
; __device__ __forceinline__ int nat_dim(int p) { return (p >> 1) + 64 * (p & 1); }
; __device__ __forceinline__ int src_col_in(int c) {
;     if (c < 5120) { const int blk = c >> 7, p = c & 127; const bool rope = blk < 16 || ((((blk - 16) >> 2) & 1) == 0); const int d = rope ? (p >> 1) + 64 * (p & 1) : p; return blk * 128 + d; }
;     if (c < OFF_Z) return c + 2096;
;     if (c < OFF_G) return c - 4048;
;     if (c < OFF_DT) return 5120 + (c - OFF_G);
;     if (c < NSRC) return c;
; template <int MAP, bool KS, bool KPERM = false>
; __device__ __forceinline__ void p0_transpose_item(const float* W, int K, int Nsrc, int nblk, bf16* WT, const float* ksA, const float* ksB, int ksplit, LAS float* scr, int item, int lane) {
;     const int kb = item / nblk, nb = item % nblk, k0 = 64 * kb, n0 = 32 * nb;
;     const int nr = n0 + (lane & 31); const int sc = MAP == 1 ? src_col_in(nr) : (MAP == 2 ? nat_dim(nr) : nr);
;     float v[32];
; #pragma unroll
;     for (int i = 0; i < 32; ++i) { const int k = k0 + 2 * i + (lane >> 5); const int ksrc = KPERM ? ((k & ~127) + nat_dim(k & 127)) : k;
;         v[i] = sc >= 0 ? W[(size_t)ksrc * Nsrc + sc] : 0.f; }
; #pragma unroll
;     for (int i = 0; i < 32; ++i) { const int kk = 2 * i + (lane >> 5); const int k = k0 + kk;
;         if (KS) v[i] *= (k < ksplit ? ksA[k] : ksB[k - ksplit]);
;         scr[kk * 33 + (lane & 31)] = v[i]; }
;     LDS_WAIT(); asm volatile("" ::: "memory");
;     const int c = lane & 7;
; #pragma unroll
;     for (int j = 0; j < 4; ++j) { const int n = (lane >> 3) + 8 * j; const LAS float* s = scr + (8 * c) * 33 + n;
;         v4u o; o.x = pk2(s[0 * 33], s[1 * 33]); o.y = pk2(s[2 * 33], s[3 * 33]); o.z = pk2(s[4 * 33], s[5 * 33]); o.w = pk2(s[6 * 33], s[7 * 33]);
;         *(GAS v4u*)(WT + (size_t)(n0 + n) * K + k0 + 8 * c) = o; }
	s_add_i32 s24, s23, 32
	s_lshl_b32 s20, s24, 7
	s_cmp_lt_u32 s24, 40
	s_cselect_b32 s21, 0, 0x830
	s_cmp_lt_u32 s24, 72
	s_cselect_b32 s21, s21, 0xfffff030
	s_add_i32 s20, s20, s21
	s_lshl_b32 s20, s20, 2
	s_add_u32 s8, s46, s20
	s_addc_u32 s9, s47, 0
	global_load_dwordx4 v[144:147], v76, s[8:9]
	s_add_u32 s8, s8, 0x16280
	s_addc_u32 s9, s9, 0
	global_load_dwordx4 v[148:151], v76, s[8:9]
	s_add_u32 s8, s8, 0x16280
	s_addc_u32 s9, s9, 0
	global_load_dwordx4 v[152:155], v76, s[8:9]
	s_add_u32 s8, s8, 0x16280
	s_addc_u32 s9, s9, 0
	global_load_dwordx4 v[156:159], v76, s[8:9]
	s_add_u32 s8, s8, 0x16280
	s_addc_u32 s9, s9, 0
	global_load_dwordx4 v[160:163], v76, s[8:9]
	s_add_u32 s8, s8, 0x16280
	s_addc_u32 s9, s9, 0
	global_load_dwordx4 v[164:167], v76, s[8:9]
	s_add_u32 s8, s8, 0x16280
	s_addc_u32 s9, s9, 0
	global_load_dwordx4 v[168:171], v76, s[8:9]
	s_add_u32 s8, s8, 0x16280
	s_addc_u32 s9, s9, 0
	global_load_dwordx4 v[172:175], v76, s[8:9]
	s_add_i32 s24, s23, 16
	s_mul_i32 s20, s24, 0x100000
	s_add_u32 s6, s48, s20
	s_addc_u32 s7, s49, 0
	s_cmp_lt_u32 s24, 16
	s_cselect_b32 s20, 1, 0
	s_sub_i32 s21, s24, 16
	s_bitcmp0_b32 s21, 2
	s_cselect_b32 s21, 1, 0
	s_cmp_lt_u32 s24, 40
	s_cselect_b32 s21, s21, 0
	s_or_b32 s20, s20, s21
	s_cmp_lg_u32 s20, 0
	s_cselect_b64 s[20:21], -1, 0
	v_cndmask_b32_e64 v91, v83, v87, s[20:21]
	v_cndmask_b32_e64 v92, v84, v88, s[20:21]
	v_cndmask_b32_e64 v93, v85, v89, s[20:21]
	v_cndmask_b32_e64 v94, v86, v90, s[20:21]
	ds_read_b32 v226, v112
	ds_read_b32 v227, v112 offset:512
	ds_read_b32 v228, v112 offset:1024
	ds_read_b32 v229, v112 offset:1536
	ds_read_b32 v230, v112 offset:2048
	ds_read_b32 v231, v112 offset:2560
	ds_read_b32 v232, v112 offset:3072
	ds_read_b32 v233, v112 offset:3584
	s_waitcnt lgkmcnt(0)
	v_bfe_u32 v120, v226, 16, 1
	v_bfe_u32 v121, v227, 16, 1
	v_bfe_u32 v122, v228, 16, 1
	v_bfe_u32 v123, v229, 16, 1
	v_bfe_u32 v124, v230, 16, 1
	v_bfe_u32 v125, v231, 16, 1
	v_bfe_u32 v126, v232, 16, 1
	v_bfe_u32 v127, v233, 16, 1
	v_add3_u32 v226, v226, v120, s63
	v_add3_u32 v227, v227, v121, s63
	v_add3_u32 v228, v228, v122, s63
	v_add3_u32 v229, v229, v123, s63
	v_add3_u32 v230, v230, v124, s63
	v_add3_u32 v231, v231, v125, s63
	v_add3_u32 v232, v232, v126, s63
	v_add3_u32 v233, v233, v127, s63
	v_perm_b32 v242, v227, v226, s64
	v_perm_b32 v243, v229, v228, s64
	v_perm_b32 v244, v231, v230, s64
	v_perm_b32 v245, v233, v232, s64
	s_nop 0
	global_store_dwordx4 v91, v[242:245], s[6:7]
	ds_read_b32 v226, v114
	ds_read_b32 v227, v114 offset:512
	ds_read_b32 v228, v114 offset:1024
	ds_read_b32 v229, v114 offset:1536
	ds_read_b32 v230, v114 offset:2048
	ds_read_b32 v231, v114 offset:2560
	ds_read_b32 v232, v114 offset:3072
	ds_read_b32 v233, v114 offset:3584
	s_waitcnt lgkmcnt(0)
	v_bfe_u32 v120, v226, 16, 1
	v_bfe_u32 v121, v227, 16, 1
	v_bfe_u32 v122, v228, 16, 1
	v_bfe_u32 v123, v229, 16, 1
	v_bfe_u32 v124, v230, 16, 1
	v_bfe_u32 v125, v231, 16, 1
	v_bfe_u32 v126, v232, 16, 1
	v_bfe_u32 v127, v233, 16, 1
	v_add3_u32 v226, v226, v120, s63
	v_add3_u32 v227, v227, v121, s63
	v_add3_u32 v228, v228, v122, s63
	v_add3_u32 v229, v229, v123, s63
	v_add3_u32 v230, v230, v124, s63
	v_add3_u32 v231, v231, v125, s63
	v_add3_u32 v232, v232, v126, s63
	v_add3_u32 v233, v233, v127, s63
	v_perm_b32 v242, v227, v226, s64
	v_perm_b32 v243, v229, v228, s64
	v_perm_b32 v244, v231, v230, s64
	v_perm_b32 v245, v233, v232, s64
	s_nop 0
	global_store_dwordx4 v92, v[242:245], s[6:7]
	ds_read_b32 v226, v116
	ds_read_b32 v227, v116 offset:512
	ds_read_b32 v228, v116 offset:1024
	ds_read_b32 v229, v116 offset:1536
	ds_read_b32 v230, v116 offset:2048
	ds_read_b32 v231, v116 offset:2560
	ds_read_b32 v232, v116 offset:3072
	ds_read_b32 v233, v116 offset:3584
	s_waitcnt lgkmcnt(0)
	v_bfe_u32 v120, v226, 16, 1
	v_bfe_u32 v121, v227, 16, 1
	v_bfe_u32 v122, v228, 16, 1
	v_bfe_u32 v123, v229, 16, 1
	v_bfe_u32 v124, v230, 16, 1
	v_bfe_u32 v125, v231, 16, 1
	v_bfe_u32 v126, v232, 16, 1
	v_bfe_u32 v127, v233, 16, 1
	v_add3_u32 v226, v226, v120, s63
	v_add3_u32 v227, v227, v121, s63
	v_add3_u32 v228, v228, v122, s63
	v_add3_u32 v229, v229, v123, s63
	v_add3_u32 v230, v230, v124, s63
	v_add3_u32 v231, v231, v125, s63
	v_add3_u32 v232, v232, v126, s63
	v_add3_u32 v233, v233, v127, s63
	v_perm_b32 v242, v227, v226, s64
	v_perm_b32 v243, v229, v228, s64
	v_perm_b32 v244, v231, v230, s64
	v_perm_b32 v245, v233, v232, s64
	s_nop 0
	global_store_dwordx4 v93, v[242:245], s[6:7]
	ds_read_b32 v226, v118
	ds_read_b32 v227, v118 offset:512
	ds_read_b32 v228, v118 offset:1024
	ds_read_b32 v229, v118 offset:1536
	ds_read_b32 v230, v118 offset:2048
	ds_read_b32 v231, v118 offset:2560
	ds_read_b32 v232, v118 offset:3072
	ds_read_b32 v233, v118 offset:3584
	s_waitcnt lgkmcnt(0)
	v_bfe_u32 v120, v226, 16, 1
	v_bfe_u32 v121, v227, 16, 1
	v_bfe_u32 v122, v228, 16, 1
	v_bfe_u32 v123, v229, 16, 1
	v_bfe_u32 v124, v230, 16, 1
	v_bfe_u32 v125, v231, 16, 1
	v_bfe_u32 v126, v232, 16, 1
	v_bfe_u32 v127, v233, 16, 1
	v_add3_u32 v226, v226, v120, s63
	v_add3_u32 v227, v227, v121, s63
	v_add3_u32 v228, v228, v122, s63
	v_add3_u32 v229, v229, v123, s63
	v_add3_u32 v230, v230, v124, s63
	v_add3_u32 v231, v231, v125, s63
	v_add3_u32 v232, v232, v126, s63
	v_add3_u32 v233, v233, v127, s63
	v_perm_b32 v242, v227, v226, s64
	v_perm_b32 v243, v229, v228, s64
	v_perm_b32 v244, v231, v230, s64
	v_perm_b32 v245, v233, v232, s64
	s_nop 0
	global_store_dwordx4 v94, v[242:245], s[6:7]
	s_waitcnt vmcnt(16)
	v_mul_f32_e32 v176, v42, v176
	v_mul_f32_e32 v177, v42, v177
	v_mul_f32_e32 v178, v42, v178
	v_mul_f32_e32 v179, v42, v179
	ds_write_b128 v210, v[176:179]
	v_mul_f32_e32 v180, v43, v180
	v_mul_f32_e32 v181, v43, v181
	v_mul_f32_e32 v182, v43, v182
	v_mul_f32_e32 v183, v43, v183
	ds_write_b128 v210, v[180:183] offset:1024
	v_mul_f32_e32 v184, v44, v184
	v_mul_f32_e32 v185, v44, v185
	v_mul_f32_e32 v186, v44, v186
	v_mul_f32_e32 v187, v44, v187
	ds_write_b128 v210, v[184:187] offset:2048
	v_mul_f32_e32 v188, v45, v188
	v_mul_f32_e32 v189, v45, v189
	v_mul_f32_e32 v190, v45, v190
	v_mul_f32_e32 v191, v45, v191
	ds_write_b128 v210, v[188:191] offset:3072
	v_mul_f32_e32 v192, v46, v192
	v_mul_f32_e32 v193, v46, v193
	v_mul_f32_e32 v194, v46, v194
	v_mul_f32_e32 v195, v46, v195
	ds_write_b128 v210, v[192:195] offset:4096
	v_mul_f32_e32 v196, v47, v196
	v_mul_f32_e32 v197, v47, v197
	v_mul_f32_e32 v198, v47, v198
	v_mul_f32_e32 v199, v47, v199
	ds_write_b128 v210, v[196:199] offset:5120
	v_mul_f32_e32 v200, v48, v200
	v_mul_f32_e32 v201, v48, v201
	v_mul_f32_e32 v202, v48, v202
	v_mul_f32_e32 v203, v48, v203
	ds_write_b128 v210, v[200:203] offset:6144
	v_mul_f32_e32 v204, v49, v204
	v_mul_f32_e32 v205, v49, v205
	v_mul_f32_e32 v206, v49, v206
	v_mul_f32_e32 v207, v49, v207
	ds_write_b128 v210, v[204:207] offset:7168
	s_waitcnt lgkmcnt(0)
	s_barrier
; #define GAS __attribute__((address_space(1)))
; #define LAS __attribute__((address_space(3)))
; #define LDS_WAIT() asm volatile("s_waitcnt lgkmcnt(0)" ::: "memory")
; __device__ __forceinline__ unsigned pk2(float lo, float hi) { return f2bf(lo) | (f2bf(hi) << 16); }
; __device__ __forceinline__ int nat_dim(int p) { return (p >> 1) + 64 * (p & 1); }
; __device__ __forceinline__ int src_col_in(int c) {
;     if (c < 5120) { const int blk = c >> 7, p = c & 127; const bool rope = blk < 16 || ((((blk - 16) >> 2) & 1) == 0); const int d = rope ? (p >> 1) + 64 * (p & 1) : p; return blk * 128 + d; }
;     if (c < OFF_Z) return c + 2096;
;     if (c < OFF_G) return c - 4048;
;     if (c < OFF_DT) return 5120 + (c - OFF_G);
;     if (c < NSRC) return c;
; template <int MAP, bool KS, bool KPERM = false>
; __device__ __forceinline__ void p0_transpose_item(const float* W, int K, int Nsrc, int nblk, bf16* WT, const float* ksA, const float* ksB, int ksplit, LAS float* scr, int item, int lane) {
;     const int kb = item / nblk, nb = item % nblk, k0 = 64 * kb, n0 = 32 * nb;
;     const int nr = n0 + (lane & 31); const int sc = MAP == 1 ? src_col_in(nr) : (MAP == 2 ? nat_dim(nr) : nr);
;     float v[32];
; #pragma unroll
;     for (int i = 0; i < 32; ++i) { const int k = k0 + 2 * i + (lane >> 5); const int ksrc = KPERM ? ((k & ~127) + nat_dim(k & 127)) : k;
;         v[i] = sc >= 0 ? W[(size_t)ksrc * Nsrc + sc] : 0.f; }
; #pragma unroll
;     for (int i = 0; i < 32; ++i) { const int kk = 2 * i + (lane >> 5); const int k = k0 + kk;
;         if (KS) v[i] *= (k < ksplit ? ksA[k] : ksB[k - ksplit]);
;         scr[kk * 33 + (lane & 31)] = v[i]; }
;     LDS_WAIT(); asm volatile("" ::: "memory");
;     const int c = lane & 7;
; #pragma unroll
;     for (int j = 0; j < 4; ++j) { const int n = (lane >> 3) + 8 * j; const LAS float* s = scr + (8 * c) * 33 + n;
;         v4u o; o.x = pk2(s[0 * 33], s[1 * 33]); o.y = pk2(s[2 * 33], s[3 * 33]); o.z = pk2(s[4 * 33], s[5 * 33]); o.w = pk2(s[6 * 33], s[7 * 33]);
;         *(GAS v4u*)(WT + (size_t)(n0 + n) * K + k0 + 8 * c) = o; }
	s_add_i32 s24, s23, 40
	s_lshl_b32 s20, s24, 7
	s_cmp_lt_u32 s24, 40
	s_cselect_b32 s21, 0, 0x830
	s_cmp_lt_u32 s24, 72
	s_cselect_b32 s21, s21, 0xfffff030
	s_add_i32 s20, s20, s21
	s_lshl_b32 s20, s20, 2
	s_add_u32 s8, s46, s20
	s_addc_u32 s9, s47, 0
	global_load_dwordx4 v[176:179], v76, s[8:9]
	s_add_u32 s8, s8, 0x16280
	s_addc_u32 s9, s9, 0
	global_load_dwordx4 v[180:183], v76, s[8:9]
	s_add_u32 s8, s8, 0x16280
	s_addc_u32 s9, s9, 0
	global_load_dwordx4 v[184:187], v76, s[8:9]
	s_add_u32 s8, s8, 0x16280
	s_addc_u32 s9, s9, 0
	global_load_dwordx4 v[188:191], v76, s[8:9]
	s_add_u32 s8, s8, 0x16280
	s_addc_u32 s9, s9, 0
	global_load_dwordx4 v[192:195], v76, s[8:9]
	s_add_u32 s8, s8, 0x16280
	s_addc_u32 s9, s9, 0
	global_load_dwordx4 v[196:199], v76, s[8:9]
	s_add_u32 s8, s8, 0x16280
	s_addc_u32 s9, s9, 0
	global_load_dwordx4 v[200:203], v76, s[8:9]
	s_add_u32 s8, s8, 0x16280
	s_addc_u32 s9, s9, 0
	global_load_dwordx4 v[204:207], v76, s[8:9]
	s_add_i32 s24, s23, 24
	s_mul_i32 s20, s24, 0x100000
	s_add_u32 s6, s48, s20
	s_addc_u32 s7, s49, 0
	s_cmp_lt_u32 s24, 16
	s_cselect_b32 s20, 1, 0
	s_sub_i32 s21, s24, 16
	s_bitcmp0_b32 s21, 2
	s_cselect_b32 s21, 1, 0
	s_cmp_lt_u32 s24, 40
	s_cselect_b32 s21, s21, 0
	s_or_b32 s20, s20, s21
	s_cmp_lg_u32 s20, 0
	s_cselect_b64 s[20:21], -1, 0
	v_cndmask_b32_e64 v91, v83, v87, s[20:21]
	v_cndmask_b32_e64 v92, v84, v88, s[20:21]
	v_cndmask_b32_e64 v93, v85, v89, s[20:21]
	v_cndmask_b32_e64 v94, v86, v90, s[20:21]
	ds_read_b32 v226, v113
	ds_read_b32 v227, v113 offset:512
	ds_read_b32 v228, v113 offset:1024
	ds_read_b32 v229, v113 offset:1536
	ds_read_b32 v230, v113 offset:2048
	ds_read_b32 v231, v113 offset:2560
	ds_read_b32 v232, v113 offset:3072
	ds_read_b32 v233, v113 offset:3584
	s_waitcnt lgkmcnt(0)
	v_bfe_u32 v120, v226, 16, 1
	v_bfe_u32 v121, v227, 16, 1
	v_bfe_u32 v122, v228, 16, 1
	v_bfe_u32 v123, v229, 16, 1
	v_bfe_u32 v124, v230, 16, 1
	v_bfe_u32 v125, v231, 16, 1
	v_bfe_u32 v126, v232, 16, 1
	v_bfe_u32 v127, v233, 16, 1
	v_add3_u32 v226, v226, v120, s63
	v_add3_u32 v227, v227, v121, s63
	v_add3_u32 v228, v228, v122, s63
	v_add3_u32 v229, v229, v123, s63
	v_add3_u32 v230, v230, v124, s63
	v_add3_u32 v231, v231, v125, s63
	v_add3_u32 v232, v232, v126, s63
	v_add3_u32 v233, v233, v127, s63
	v_perm_b32 v242, v227, v226, s64
	v_perm_b32 v243, v229, v228, s64
	v_perm_b32 v244, v231, v230, s64
	v_perm_b32 v245, v233, v232, s64
	s_nop 0
	global_store_dwordx4 v91, v[242:245], s[6:7]
	ds_read_b32 v226, v115
	ds_read_b32 v227, v115 offset:512
	ds_read_b32 v228, v115 offset:1024
	ds_read_b32 v229, v115 offset:1536
	ds_read_b32 v230, v115 offset:2048
	ds_read_b32 v231, v115 offset:2560
	ds_read_b32 v232, v115 offset:3072
	ds_read_b32 v233, v115 offset:3584
	s_waitcnt lgkmcnt(0)
	v_bfe_u32 v120, v226, 16, 1
	v_bfe_u32 v121, v227, 16, 1
	v_bfe_u32 v122, v228, 16, 1
	v_bfe_u32 v123, v229, 16, 1
	v_bfe_u32 v124, v230, 16, 1
	v_bfe_u32 v125, v231, 16, 1
	v_bfe_u32 v126, v232, 16, 1
	v_bfe_u32 v127, v233, 16, 1
	v_add3_u32 v226, v226, v120, s63
	v_add3_u32 v227, v227, v121, s63
	v_add3_u32 v228, v228, v122, s63
	v_add3_u32 v229, v229, v123, s63
	v_add3_u32 v230, v230, v124, s63
	v_add3_u32 v231, v231, v125, s63
	v_add3_u32 v232, v232, v126, s63
	v_add3_u32 v233, v233, v127, s63
	v_perm_b32 v242, v227, v226, s64
	v_perm_b32 v243, v229, v228, s64
	v_perm_b32 v244, v231, v230, s64
	v_perm_b32 v245, v233, v232, s64
	s_nop 0
	global_store_dwordx4 v92, v[242:245], s[6:7]
	ds_read_b32 v226, v117
	ds_read_b32 v227, v117 offset:512
	ds_read_b32 v228, v117 offset:1024
	ds_read_b32 v229, v117 offset:1536
	ds_read_b32 v230, v117 offset:2048
	ds_read_b32 v231, v117 offset:2560
	ds_read_b32 v232, v117 offset:3072
	ds_read_b32 v233, v117 offset:3584
	s_waitcnt lgkmcnt(0)
	v_bfe_u32 v120, v226, 16, 1
	v_bfe_u32 v121, v227, 16, 1
	v_bfe_u32 v122, v228, 16, 1
	v_bfe_u32 v123, v229, 16, 1
	v_bfe_u32 v124, v230, 16, 1
	v_bfe_u32 v125, v231, 16, 1
	v_bfe_u32 v126, v232, 16, 1
	v_bfe_u32 v127, v233, 16, 1
	v_add3_u32 v226, v226, v120, s63
	v_add3_u32 v227, v227, v121, s63
	v_add3_u32 v228, v228, v122, s63
	v_add3_u32 v229, v229, v123, s63
	v_add3_u32 v230, v230, v124, s63
	v_add3_u32 v231, v231, v125, s63
	v_add3_u32 v232, v232, v126, s63
	v_add3_u32 v233, v233, v127, s63
	v_perm_b32 v242, v227, v226, s64
	v_perm_b32 v243, v229, v228, s64
	v_perm_b32 v244, v231, v230, s64
	v_perm_b32 v245, v233, v232, s64
	s_nop 0
	global_store_dwordx4 v93, v[242:245], s[6:7]
	ds_read_b32 v226, v119
	ds_read_b32 v227, v119 offset:512
	ds_read_b32 v228, v119 offset:1024
	ds_read_b32 v229, v119 offset:1536
	ds_read_b32 v230, v119 offset:2048
	ds_read_b32 v231, v119 offset:2560
	ds_read_b32 v232, v119 offset:3072
	ds_read_b32 v233, v119 offset:3584
	s_waitcnt lgkmcnt(0)
	v_bfe_u32 v120, v226, 16, 1
	v_bfe_u32 v121, v227, 16, 1
	v_bfe_u32 v122, v228, 16, 1
	v_bfe_u32 v123, v229, 16, 1
	v_bfe_u32 v124, v230, 16, 1
	v_bfe_u32 v125, v231, 16, 1
	v_bfe_u32 v126, v232, 16, 1
	v_bfe_u32 v127, v233, 16, 1
	v_add3_u32 v226, v226, v120, s63
	v_add3_u32 v227, v227, v121, s63
	v_add3_u32 v228, v228, v122, s63
	v_add3_u32 v229, v229, v123, s63
	v_add3_u32 v230, v230, v124, s63
	v_add3_u32 v231, v231, v125, s63
	v_add3_u32 v232, v232, v126, s63
	v_add3_u32 v233, v233, v127, s63
	v_perm_b32 v242, v227, v226, s64
	v_perm_b32 v243, v229, v228, s64
	v_perm_b32 v244, v231, v230, s64
	v_perm_b32 v245, v233, v232, s64
	s_nop 0
	global_store_dwordx4 v94, v[242:245], s[6:7]
	s_waitcnt vmcnt(16)
	v_mul_f32_e32 v144, v42, v144
	v_mul_f32_e32 v145, v42, v145
	v_mul_f32_e32 v146, v42, v146
	v_mul_f32_e32 v147, v42, v147
	ds_write_b128 v209, v[144:147]
	v_mul_f32_e32 v148, v43, v148
	v_mul_f32_e32 v149, v43, v149
	v_mul_f32_e32 v150, v43, v150
	v_mul_f32_e32 v151, v43, v151
	ds_write_b128 v209, v[148:151] offset:1024
	v_mul_f32_e32 v152, v44, v152
	v_mul_f32_e32 v153, v44, v153
	v_mul_f32_e32 v154, v44, v154
	v_mul_f32_e32 v155, v44, v155
	ds_write_b128 v209, v[152:155] offset:2048
	v_mul_f32_e32 v156, v45, v156
	v_mul_f32_e32 v157, v45, v157
	v_mul_f32_e32 v158, v45, v158
	v_mul_f32_e32 v159, v45, v159
	ds_write_b128 v209, v[156:159] offset:3072
	v_mul_f32_e32 v160, v46, v160
	v_mul_f32_e32 v161, v46, v161
	v_mul_f32_e32 v162, v46, v162
	v_mul_f32_e32 v163, v46, v163
	ds_write_b128 v209, v[160:163] offset:4096
	v_mul_f32_e32 v164, v47, v164
	v_mul_f32_e32 v165, v47, v165
	v_mul_f32_e32 v166, v47, v166
	v_mul_f32_e32 v167, v47, v167
	ds_write_b128 v209, v[164:167] offset:5120
	v_mul_f32_e32 v168, v48, v168
	v_mul_f32_e32 v169, v48, v169
	v_mul_f32_e32 v170, v48, v170
	v_mul_f32_e32 v171, v48, v171
	ds_write_b128 v209, v[168:171] offset:6144
	v_mul_f32_e32 v172, v49, v172
	v_mul_f32_e32 v173, v49, v173
	v_mul_f32_e32 v174, v49, v174
	v_mul_f32_e32 v175, v49, v175
	ds_write_b128 v209, v[172:175] offset:7168
	s_waitcnt lgkmcnt(0)
	s_barrier
; #define GAS __attribute__((address_space(1)))
; #define LAS __attribute__((address_space(3)))
; #define LDS_WAIT() asm volatile("s_waitcnt lgkmcnt(0)" ::: "memory")
; __device__ __forceinline__ unsigned pk2(float lo, float hi) { return f2bf(lo) | (f2bf(hi) << 16); }
; __device__ __forceinline__ int nat_dim(int p) { return (p >> 1) + 64 * (p & 1); }
; __device__ __forceinline__ int src_col_in(int c) {
;     if (c < 5120) { const int blk = c >> 7, p = c & 127; const bool rope = blk < 16 || ((((blk - 16) >> 2) & 1) == 0); const int d = rope ? (p >> 1) + 64 * (p & 1) : p; return blk * 128 + d; }
;     if (c < OFF_Z) return c + 2096;
;     if (c < OFF_G) return c - 4048;
;     if (c < OFF_DT) return 5120 + (c - OFF_G);
;     if (c < NSRC) return c;
; template <int MAP, bool KS, bool KPERM = false>
; __device__ __forceinline__ void p0_transpose_item(const float* W, int K, int Nsrc, int nblk, bf16* WT, const float* ksA, const float* ksB, int ksplit, LAS float* scr, int item, int lane) {
;     const int kb = item / nblk, nb = item % nblk, k0 = 64 * kb, n0 = 32 * nb;
;     const int nr = n0 + (lane & 31); const int sc = MAP == 1 ? src_col_in(nr) : (MAP == 2 ? nat_dim(nr) : nr);
;     float v[32];
; #pragma unroll
;     for (int i = 0; i < 32; ++i) { const int k = k0 + 2 * i + (lane >> 5); const int ksrc = KPERM ? ((k & ~127) + nat_dim(k & 127)) : k;
;         v[i] = sc >= 0 ? W[(size_t)ksrc * Nsrc + sc] : 0.f; }
; #pragma unroll
;     for (int i = 0; i < 32; ++i) { const int kk = 2 * i + (lane >> 5); const int k = k0 + kk;
;         if (KS) v[i] *= (k < ksplit ? ksA[k] : ksB[k - ksplit]);
;         scr[kk * 33 + (lane & 31)] = v[i]; }
;     LDS_WAIT(); asm volatile("" ::: "memory");
;     const int c = lane & 7;
; #pragma unroll
;     for (int j = 0; j < 4; ++j) { const int n = (lane >> 3) + 8 * j; const LAS float* s = scr + (8 * c) * 33 + n;
;         v4u o; o.x = pk2(s[0 * 33], s[1 * 33]); o.y = pk2(s[2 * 33], s[3 * 33]); o.z = pk2(s[4 * 33], s[5 * 33]); o.w = pk2(s[6 * 33], s[7 * 33]);
;         *(GAS v4u*)(WT + (size_t)(n0 + n) * K + k0 + 8 * c) = o; }
	s_add_i32 s24, s23, 48
	s_lshl_b32 s20, s24, 7
	s_cmp_lt_u32 s24, 40
	s_cselect_b32 s21, 0, 0x830
	s_cmp_lt_u32 s24, 72
	s_cselect_b32 s21, s21, 0xfffff030
	s_add_i32 s20, s20, s21
	s_lshl_b32 s20, s20, 2
	s_add_u32 s8, s46, s20
	s_addc_u32 s9, s47, 0
	global_load_dwordx4 v[144:147], v76, s[8:9]
	s_add_u32 s8, s8, 0x16280
	s_addc_u32 s9, s9, 0
	global_load_dwordx4 v[148:151], v76, s[8:9]
	s_add_u32 s8, s8, 0x16280
	s_addc_u32 s9, s9, 0
	global_load_dwordx4 v[152:155], v76, s[8:9]
	s_add_u32 s8, s8, 0x16280
	s_addc_u32 s9, s9, 0
	global_load_dwordx4 v[156:159], v76, s[8:9]
	s_add_u32 s8, s8, 0x16280
	s_addc_u32 s9, s9, 0
	global_load_dwordx4 v[160:163], v76, s[8:9]
	s_add_u32 s8, s8, 0x16280
	s_addc_u32 s9, s9, 0
	global_load_dwordx4 v[164:167], v76, s[8:9]
	s_add_u32 s8, s8, 0x16280
	s_addc_u32 s9, s9, 0
	global_load_dwordx4 v[168:171], v76, s[8:9]
	s_add_u32 s8, s8, 0x16280
	s_addc_u32 s9, s9, 0
	global_load_dwordx4 v[172:175], v76, s[8:9]
	s_add_i32 s24, s23, 32
	s_mul_i32 s20, s24, 0x100000
	s_add_u32 s6, s48, s20
	s_addc_u32 s7, s49, 0
	s_cmp_lt_u32 s24, 16
	s_cselect_b32 s20, 1, 0
	s_sub_i32 s21, s24, 16
	s_bitcmp0_b32 s21, 2
	s_cselect_b32 s21, 1, 0
	s_cmp_lt_u32 s24, 40
	s_cselect_b32 s21, s21, 0
	s_or_b32 s20, s20, s21
	s_cmp_lg_u32 s20, 0
	s_cselect_b64 s[20:21], -1, 0
	v_cndmask_b32_e64 v91, v83, v87, s[20:21]
	v_cndmask_b32_e64 v92, v84, v88, s[20:21]
	v_cndmask_b32_e64 v93, v85, v89, s[20:21]
	v_cndmask_b32_e64 v94, v86, v90, s[20:21]
	ds_read_b32 v226, v112
	ds_read_b32 v227, v112 offset:512
	ds_read_b32 v228, v112 offset:1024
	ds_read_b32 v229, v112 offset:1536
	ds_read_b32 v230, v112 offset:2048
	ds_read_b32 v231, v112 offset:2560
	ds_read_b32 v232, v112 offset:3072
	ds_read_b32 v233, v112 offset:3584
	s_waitcnt lgkmcnt(0)
	v_bfe_u32 v120, v226, 16, 1
	v_bfe_u32 v121, v227, 16, 1
	v_bfe_u32 v122, v228, 16, 1
	v_bfe_u32 v123, v229, 16, 1
	v_bfe_u32 v124, v230, 16, 1
	v_bfe_u32 v125, v231, 16, 1
	v_bfe_u32 v126, v232, 16, 1
	v_bfe_u32 v127, v233, 16, 1
	v_add3_u32 v226, v226, v120, s63
	v_add3_u32 v227, v227, v121, s63
	v_add3_u32 v228, v228, v122, s63
	v_add3_u32 v229, v229, v123, s63
	v_add3_u32 v230, v230, v124, s63
	v_add3_u32 v231, v231, v125, s63
	v_add3_u32 v232, v232, v126, s63
	v_add3_u32 v233, v233, v127, s63
	v_perm_b32 v242, v227, v226, s64
	v_perm_b32 v243, v229, v228, s64
	v_perm_b32 v244, v231, v230, s64
	v_perm_b32 v245, v233, v232, s64
	s_nop 0
	global_store_dwordx4 v91, v[242:245], s[6:7]
	ds_read_b32 v226, v114
	ds_read_b32 v227, v114 offset:512
	ds_read_b32 v228, v114 offset:1024
	ds_read_b32 v229, v114 offset:1536
	ds_read_b32 v230, v114 offset:2048
	ds_read_b32 v231, v114 offset:2560
	ds_read_b32 v232, v114 offset:3072
	ds_read_b32 v233, v114 offset:3584
	s_waitcnt lgkmcnt(0)
	v_bfe_u32 v120, v226, 16, 1
	v_bfe_u32 v121, v227, 16, 1
	v_bfe_u32 v122, v228, 16, 1
	v_bfe_u32 v123, v229, 16, 1
	v_bfe_u32 v124, v230, 16, 1
	v_bfe_u32 v125, v231, 16, 1
	v_bfe_u32 v126, v232, 16, 1
	v_bfe_u32 v127, v233, 16, 1
	v_add3_u32 v226, v226, v120, s63
	v_add3_u32 v227, v227, v121, s63
	v_add3_u32 v228, v228, v122, s63
	v_add3_u32 v229, v229, v123, s63
	v_add3_u32 v230, v230, v124, s63
	v_add3_u32 v231, v231, v125, s63
	v_add3_u32 v232, v232, v126, s63
	v_add3_u32 v233, v233, v127, s63
	v_perm_b32 v242, v227, v226, s64
	v_perm_b32 v243, v229, v228, s64
	v_perm_b32 v244, v231, v230, s64
	v_perm_b32 v245, v233, v232, s64
	s_nop 0
	global_store_dwordx4 v92, v[242:245], s[6:7]
	ds_read_b32 v226, v116
	ds_read_b32 v227, v116 offset:512
	ds_read_b32 v228, v116 offset:1024
	ds_read_b32 v229, v116 offset:1536
	ds_read_b32 v230, v116 offset:2048
	ds_read_b32 v231, v116 offset:2560
	ds_read_b32 v232, v116 offset:3072
	ds_read_b32 v233, v116 offset:3584
	s_waitcnt lgkmcnt(0)
	v_bfe_u32 v120, v226, 16, 1
	v_bfe_u32 v121, v227, 16, 1
	v_bfe_u32 v122, v228, 16, 1
	v_bfe_u32 v123, v229, 16, 1
	v_bfe_u32 v124, v230, 16, 1
	v_bfe_u32 v125, v231, 16, 1
	v_bfe_u32 v126, v232, 16, 1
	v_bfe_u32 v127, v233, 16, 1
	v_add3_u32 v226, v226, v120, s63
	v_add3_u32 v227, v227, v121, s63
	v_add3_u32 v228, v228, v122, s63
	v_add3_u32 v229, v229, v123, s63
	v_add3_u32 v230, v230, v124, s63
	v_add3_u32 v231, v231, v125, s63
	v_add3_u32 v232, v232, v126, s63
	v_add3_u32 v233, v233, v127, s63
	v_perm_b32 v242, v227, v226, s64
	v_perm_b32 v243, v229, v228, s64
	v_perm_b32 v244, v231, v230, s64
	v_perm_b32 v245, v233, v232, s64
	s_nop 0
	global_store_dwordx4 v93, v[242:245], s[6:7]
	ds_read_b32 v226, v118
	ds_read_b32 v227, v118 offset:512
	ds_read_b32 v228, v118 offset:1024
	ds_read_b32 v229, v118 offset:1536
	ds_read_b32 v230, v118 offset:2048
	ds_read_b32 v231, v118 offset:2560
	ds_read_b32 v232, v118 offset:3072
	ds_read_b32 v233, v118 offset:3584
	s_waitcnt lgkmcnt(0)
	v_bfe_u32 v120, v226, 16, 1
	v_bfe_u32 v121, v227, 16, 1
	v_bfe_u32 v122, v228, 16, 1
	v_bfe_u32 v123, v229, 16, 1
	v_bfe_u32 v124, v230, 16, 1
	v_bfe_u32 v125, v231, 16, 1
	v_bfe_u32 v126, v232, 16, 1
	v_bfe_u32 v127, v233, 16, 1
	v_add3_u32 v226, v226, v120, s63
	v_add3_u32 v227, v227, v121, s63
	v_add3_u32 v228, v228, v122, s63
	v_add3_u32 v229, v229, v123, s63
	v_add3_u32 v230, v230, v124, s63
	v_add3_u32 v231, v231, v125, s63
	v_add3_u32 v232, v232, v126, s63
	v_add3_u32 v233, v233, v127, s63
	v_perm_b32 v242, v227, v226, s64
	v_perm_b32 v243, v229, v228, s64
	v_perm_b32 v244, v231, v230, s64
	v_perm_b32 v245, v233, v232, s64
	s_nop 0
	global_store_dwordx4 v94, v[242:245], s[6:7]
	s_waitcnt vmcnt(16)
	v_mul_f32_e32 v176, v42, v176
	v_mul_f32_e32 v177, v42, v177
	v_mul_f32_e32 v178, v42, v178
	v_mul_f32_e32 v179, v42, v179
	ds_write_b128 v210, v[176:179]
	v_mul_f32_e32 v180, v43, v180
	v_mul_f32_e32 v181, v43, v181
	v_mul_f32_e32 v182, v43, v182
	v_mul_f32_e32 v183, v43, v183
	ds_write_b128 v210, v[180:183] offset:1024
	v_mul_f32_e32 v184, v44, v184
	v_mul_f32_e32 v185, v44, v185
	v_mul_f32_e32 v186, v44, v186
	v_mul_f32_e32 v187, v44, v187
	ds_write_b128 v210, v[184:187] offset:2048
	v_mul_f32_e32 v188, v45, v188
	v_mul_f32_e32 v189, v45, v189
	v_mul_f32_e32 v190, v45, v190
	v_mul_f32_e32 v191, v45, v191
	ds_write_b128 v210, v[188:191] offset:3072
	v_mul_f32_e32 v192, v46, v192
	v_mul_f32_e32 v193, v46, v193
	v_mul_f32_e32 v194, v46, v194
	v_mul_f32_e32 v195, v46, v195
	ds_write_b128 v210, v[192:195] offset:4096
	v_mul_f32_e32 v196, v47, v196
	v_mul_f32_e32 v197, v47, v197
	v_mul_f32_e32 v198, v47, v198
	v_mul_f32_e32 v199, v47, v199
	ds_write_b128 v210, v[196:199] offset:5120
	v_mul_f32_e32 v200, v48, v200
	v_mul_f32_e32 v201, v48, v201
	v_mul_f32_e32 v202, v48, v202
	v_mul_f32_e32 v203, v48, v203
	ds_write_b128 v210, v[200:203] offset:6144
	v_mul_f32_e32 v204, v49, v204
	v_mul_f32_e32 v205, v49, v205
	v_mul_f32_e32 v206, v49, v206
	v_mul_f32_e32 v207, v49, v207
	ds_write_b128 v210, v[204:207] offset:7168
	s_waitcnt lgkmcnt(0)
	s_barrier
; #define GAS __attribute__((address_space(1)))
; #define LAS __attribute__((address_space(3)))
; #define LDS_WAIT() asm volatile("s_waitcnt lgkmcnt(0)" ::: "memory")
; __device__ __forceinline__ unsigned pk2(float lo, float hi) { return f2bf(lo) | (f2bf(hi) << 16); }
; __device__ __forceinline__ int nat_dim(int p) { return (p >> 1) + 64 * (p & 1); }
; __device__ __forceinline__ int src_col_in(int c) {
;     if (c < 5120) { const int blk = c >> 7, p = c & 127; const bool rope = blk < 16 || ((((blk - 16) >> 2) & 1) == 0); const int d = rope ? (p >> 1) + 64 * (p & 1) : p; return blk * 128 + d; }
;     if (c < OFF_Z) return c + 2096;
;     if (c < OFF_G) return c - 4048;
;     if (c < OFF_DT) return 5120 + (c - OFF_G);
;     if (c < NSRC) return c;
; template <int MAP, bool KS, bool KPERM = false>
; __device__ __forceinline__ void p0_transpose_item(const float* W, int K, int Nsrc, int nblk, bf16* WT, const float* ksA, const float* ksB, int ksplit, LAS float* scr, int item, int lane) {
;     const int kb = item / nblk, nb = item % nblk, k0 = 64 * kb, n0 = 32 * nb;
;     const int nr = n0 + (lane & 31); const int sc = MAP == 1 ? src_col_in(nr) : (MAP == 2 ? nat_dim(nr) : nr);
;     float v[32];
; #pragma unroll
;     for (int i = 0; i < 32; ++i) { const int k = k0 + 2 * i + (lane >> 5); const int ksrc = KPERM ? ((k & ~127) + nat_dim(k & 127)) : k;
;         v[i] = sc >= 0 ? W[(size_t)ksrc * Nsrc + sc] : 0.f; }
; #pragma unroll
;     for (int i = 0; i < 32; ++i) { const int kk = 2 * i + (lane >> 5); const int k = k0 + kk;
;         if (KS) v[i] *= (k < ksplit ? ksA[k] : ksB[k - ksplit]);
;         scr[kk * 33 + (lane & 31)] = v[i]; }
;     LDS_WAIT(); asm volatile("" ::: "memory");
;     const int c = lane & 7;
; #pragma unroll
;     for (int j = 0; j < 4; ++j) { const int n = (lane >> 3) + 8 * j; const LAS float* s = scr + (8 * c) * 33 + n;
;         v4u o; o.x = pk2(s[0 * 33], s[1 * 33]); o.y = pk2(s[2 * 33], s[3 * 33]); o.z = pk2(s[4 * 33], s[5 * 33]); o.w = pk2(s[6 * 33], s[7 * 33]);
;         *(GAS v4u*)(WT + (size_t)(n0 + n) * K + k0 + 8 * c) = o; }
	s_add_i32 s24, s23, 56
	s_lshl_b32 s20, s24, 7
	s_cmp_lt_u32 s24, 40
	s_cselect_b32 s21, 0, 0x830
	s_cmp_lt_u32 s24, 72
	s_cselect_b32 s21, s21, 0xfffff030
	s_add_i32 s20, s20, s21
	s_lshl_b32 s20, s20, 2
	s_add_u32 s8, s46, s20
	s_addc_u32 s9, s47, 0
	global_load_dwordx4 v[176:179], v76, s[8:9]
	s_add_u32 s8, s8, 0x16280
	s_addc_u32 s9, s9, 0
	global_load_dwordx4 v[180:183], v76, s[8:9]
	s_add_u32 s8, s8, 0x16280
	s_addc_u32 s9, s9, 0
	global_load_dwordx4 v[184:187], v76, s[8:9]
	s_add_u32 s8, s8, 0x16280
	s_addc_u32 s9, s9, 0
	global_load_dwordx4 v[188:191], v76, s[8:9]
	s_add_u32 s8, s8, 0x16280
	s_addc_u32 s9, s9, 0
	global_load_dwordx4 v[192:195], v76, s[8:9]
	s_add_u32 s8, s8, 0x16280
	s_addc_u32 s9, s9, 0
	global_load_dwordx4 v[196:199], v76, s[8:9]
	s_add_u32 s8, s8, 0x16280
	s_addc_u32 s9, s9, 0
	global_load_dwordx4 v[200:203], v76, s[8:9]
	s_add_u32 s8, s8, 0x16280
	s_addc_u32 s9, s9, 0
	global_load_dwordx4 v[204:207], v76, s[8:9]
	s_add_i32 s24, s23, 40
	s_mul_i32 s20, s24, 0x100000
	s_add_u32 s6, s48, s20
	s_addc_u32 s7, s49, 0
	s_cmp_lt_u32 s24, 16
	s_cselect_b32 s20, 1, 0
	s_sub_i32 s21, s24, 16
	s_bitcmp0_b32 s21, 2
	s_cselect_b32 s21, 1, 0
	s_cmp_lt_u32 s24, 40
	s_cselect_b32 s21, s21, 0
	s_or_b32 s20, s20, s21
	s_cmp_lg_u32 s20, 0
	s_cselect_b64 s[20:21], -1, 0
	v_cndmask_b32_e64 v91, v83, v87, s[20:21]
	v_cndmask_b32_e64 v92, v84, v88, s[20:21]
	v_cndmask_b32_e64 v93, v85, v89, s[20:21]
	v_cndmask_b32_e64 v94, v86, v90, s[20:21]
	ds_read_b32 v226, v113
	ds_read_b32 v227, v113 offset:512
	ds_read_b32 v228, v113 offset:1024
	ds_read_b32 v229, v113 offset:1536
	ds_read_b32 v230, v113 offset:2048
	ds_read_b32 v231, v113 offset:2560
	ds_read_b32 v232, v113 offset:3072
	ds_read_b32 v233, v113 offset:3584
	s_waitcnt lgkmcnt(0)
	v_bfe_u32 v120, v226, 16, 1
	v_bfe_u32 v121, v227, 16, 1
	v_bfe_u32 v122, v228, 16, 1
	v_bfe_u32 v123, v229, 16, 1
	v_bfe_u32 v124, v230, 16, 1
	v_bfe_u32 v125, v231, 16, 1
	v_bfe_u32 v126, v232, 16, 1
	v_bfe_u32 v127, v233, 16, 1
	v_add3_u32 v226, v226, v120, s63
	v_add3_u32 v227, v227, v121, s63
	v_add3_u32 v228, v228, v122, s63
	v_add3_u32 v229, v229, v123, s63
	v_add3_u32 v230, v230, v124, s63
	v_add3_u32 v231, v231, v125, s63
	v_add3_u32 v232, v232, v126, s63
	v_add3_u32 v233, v233, v127, s63
	v_perm_b32 v242, v227, v226, s64
	v_perm_b32 v243, v229, v228, s64
	v_perm_b32 v244, v231, v230, s64
	v_perm_b32 v245, v233, v232, s64
	s_nop 0
	global_store_dwordx4 v91, v[242:245], s[6:7]
	ds_read_b32 v226, v115
	ds_read_b32 v227, v115 offset:512
	ds_read_b32 v228, v115 offset:1024
	ds_read_b32 v229, v115 offset:1536
	ds_read_b32 v230, v115 offset:2048
	ds_read_b32 v231, v115 offset:2560
	ds_read_b32 v232, v115 offset:3072
	ds_read_b32 v233, v115 offset:3584
	s_waitcnt lgkmcnt(0)
	v_bfe_u32 v120, v226, 16, 1
	v_bfe_u32 v121, v227, 16, 1
	v_bfe_u32 v122, v228, 16, 1
	v_bfe_u32 v123, v229, 16, 1
	v_bfe_u32 v124, v230, 16, 1
	v_bfe_u32 v125, v231, 16, 1
	v_bfe_u32 v126, v232, 16, 1
	v_bfe_u32 v127, v233, 16, 1
	v_add3_u32 v226, v226, v120, s63
	v_add3_u32 v227, v227, v121, s63
	v_add3_u32 v228, v228, v122, s63
	v_add3_u32 v229, v229, v123, s63
	v_add3_u32 v230, v230, v124, s63
	v_add3_u32 v231, v231, v125, s63
	v_add3_u32 v232, v232, v126, s63
	v_add3_u32 v233, v233, v127, s63
	v_perm_b32 v242, v227, v226, s64
	v_perm_b32 v243, v229, v228, s64
	v_perm_b32 v244, v231, v230, s64
	v_perm_b32 v245, v233, v232, s64
	s_nop 0
	global_store_dwordx4 v92, v[242:245], s[6:7]
	ds_read_b32 v226, v117
	ds_read_b32 v227, v117 offset:512
	ds_read_b32 v228, v117 offset:1024
	ds_read_b32 v229, v117 offset:1536
	ds_read_b32 v230, v117 offset:2048
	ds_read_b32 v231, v117 offset:2560
	ds_read_b32 v232, v117 offset:3072
	ds_read_b32 v233, v117 offset:3584
	s_waitcnt lgkmcnt(0)
	v_bfe_u32 v120, v226, 16, 1
	v_bfe_u32 v121, v227, 16, 1
	v_bfe_u32 v122, v228, 16, 1
	v_bfe_u32 v123, v229, 16, 1
	v_bfe_u32 v124, v230, 16, 1
	v_bfe_u32 v125, v231, 16, 1
	v_bfe_u32 v126, v232, 16, 1
	v_bfe_u32 v127, v233, 16, 1
	v_add3_u32 v226, v226, v120, s63
	v_add3_u32 v227, v227, v121, s63
	v_add3_u32 v228, v228, v122, s63
	v_add3_u32 v229, v229, v123, s63
	v_add3_u32 v230, v230, v124, s63
	v_add3_u32 v231, v231, v125, s63
	v_add3_u32 v232, v232, v126, s63
	v_add3_u32 v233, v233, v127, s63
	v_perm_b32 v242, v227, v226, s64
	v_perm_b32 v243, v229, v228, s64
	v_perm_b32 v244, v231, v230, s64
	v_perm_b32 v245, v233, v232, s64
	s_nop 0
	global_store_dwordx4 v93, v[242:245], s[6:7]
	ds_read_b32 v226, v119
	ds_read_b32 v227, v119 offset:512
	ds_read_b32 v228, v119 offset:1024
	ds_read_b32 v229, v119 offset:1536
	ds_read_b32 v230, v119 offset:2048
	ds_read_b32 v231, v119 offset:2560
	ds_read_b32 v232, v119 offset:3072
	ds_read_b32 v233, v119 offset:3584
	s_waitcnt lgkmcnt(0)
	v_bfe_u32 v120, v226, 16, 1
	v_bfe_u32 v121, v227, 16, 1
	v_bfe_u32 v122, v228, 16, 1
	v_bfe_u32 v123, v229, 16, 1
	v_bfe_u32 v124, v230, 16, 1
	v_bfe_u32 v125, v231, 16, 1
	v_bfe_u32 v126, v232, 16, 1
	v_bfe_u32 v127, v233, 16, 1
	v_add3_u32 v226, v226, v120, s63
	v_add3_u32 v227, v227, v121, s63
	v_add3_u32 v228, v228, v122, s63
	v_add3_u32 v229, v229, v123, s63
	v_add3_u32 v230, v230, v124, s63
	v_add3_u32 v231, v231, v125, s63
	v_add3_u32 v232, v232, v126, s63
	v_add3_u32 v233, v233, v127, s63
	v_perm_b32 v242, v227, v226, s64
	v_perm_b32 v243, v229, v228, s64
	v_perm_b32 v244, v231, v230, s64
	v_perm_b32 v245, v233, v232, s64
	s_nop 0
	global_store_dwordx4 v94, v[242:245], s[6:7]
	s_waitcnt vmcnt(16)
	v_mul_f32_e32 v144, v42, v144
	v_mul_f32_e32 v145, v42, v145
	v_mul_f32_e32 v146, v42, v146
	v_mul_f32_e32 v147, v42, v147
	ds_write_b128 v209, v[144:147]
	v_mul_f32_e32 v148, v43, v148
	v_mul_f32_e32 v149, v43, v149
	v_mul_f32_e32 v150, v43, v150
	v_mul_f32_e32 v151, v43, v151
	ds_write_b128 v209, v[148:151] offset:1024
	v_mul_f32_e32 v152, v44, v152
	v_mul_f32_e32 v153, v44, v153
	v_mul_f32_e32 v154, v44, v154
	v_mul_f32_e32 v155, v44, v155
	ds_write_b128 v209, v[152:155] offset:2048
	v_mul_f32_e32 v156, v45, v156
	v_mul_f32_e32 v157, v45, v157
	v_mul_f32_e32 v158, v45, v158
	v_mul_f32_e32 v159, v45, v159
	ds_write_b128 v209, v[156:159] offset:3072
	v_mul_f32_e32 v160, v46, v160
	v_mul_f32_e32 v161, v46, v161
	v_mul_f32_e32 v162, v46, v162
	v_mul_f32_e32 v163, v46, v163
	ds_write_b128 v209, v[160:163] offset:4096
	v_mul_f32_e32 v164, v47, v164
	v_mul_f32_e32 v165, v47, v165
	v_mul_f32_e32 v166, v47, v166
	v_mul_f32_e32 v167, v47, v167
	ds_write_b128 v209, v[164:167] offset:5120
	v_mul_f32_e32 v168, v48, v168
	v_mul_f32_e32 v169, v48, v169
	v_mul_f32_e32 v170, v48, v170
	v_mul_f32_e32 v171, v48, v171
	ds_write_b128 v209, v[168:171] offset:6144
	v_mul_f32_e32 v172, v49, v172
	v_mul_f32_e32 v173, v49, v173
	v_mul_f32_e32 v174, v49, v174
	v_mul_f32_e32 v175, v49, v175
	ds_write_b128 v209, v[172:175] offset:7168
	s_waitcnt lgkmcnt(0)
	s_barrier
; #define GAS __attribute__((address_space(1)))
; #define LAS __attribute__((address_space(3)))
; #define LDS_WAIT() asm volatile("s_waitcnt lgkmcnt(0)" ::: "memory")
; __device__ __forceinline__ unsigned pk2(float lo, float hi) { return f2bf(lo) | (f2bf(hi) << 16); }
; __device__ __forceinline__ int nat_dim(int p) { return (p >> 1) + 64 * (p & 1); }
; __device__ __forceinline__ int src_col_in(int c) {
;     if (c < 5120) { const int blk = c >> 7, p = c & 127; const bool rope = blk < 16 || ((((blk - 16) >> 2) & 1) == 0); const int d = rope ? (p >> 1) + 64 * (p & 1) : p; return blk * 128 + d; }
;     if (c < OFF_Z) return c + 2096;
;     if (c < OFF_G) return c - 4048;
;     if (c < OFF_DT) return 5120 + (c - OFF_G);
;     if (c < NSRC) return c;
; template <int MAP, bool KS, bool KPERM = false>
; __device__ __forceinline__ void p0_transpose_item(const float* W, int K, int Nsrc, int nblk, bf16* WT, const float* ksA, const float* ksB, int ksplit, LAS float* scr, int item, int lane) {
;     const int kb = item / nblk, nb = item % nblk, k0 = 64 * kb, n0 = 32 * nb;
;     const int nr = n0 + (lane & 31); const int sc = MAP == 1 ? src_col_in(nr) : (MAP == 2 ? nat_dim(nr) : nr);
;     float v[32];
; #pragma unroll
;     for (int i = 0; i < 32; ++i) { const int k = k0 + 2 * i + (lane >> 5); const int ksrc = KPERM ? ((k & ~127) + nat_dim(k & 127)) : k;
;         v[i] = sc >= 0 ? W[(size_t)ksrc * Nsrc + sc] : 0.f; }
; #pragma unroll
;     for (int i = 0; i < 32; ++i) { const int kk = 2 * i + (lane >> 5); const int k = k0 + kk;
;         if (KS) v[i] *= (k < ksplit ? ksA[k] : ksB[k - ksplit]);
;         scr[kk * 33 + (lane & 31)] = v[i]; }
;     LDS_WAIT(); asm volatile("" ::: "memory");
;     const int c = lane & 7;
; #pragma unroll
;     for (int j = 0; j < 4; ++j) { const int n = (lane >> 3) + 8 * j; const LAS float* s = scr + (8 * c) * 33 + n;
;         v4u o; o.x = pk2(s[0 * 33], s[1 * 33]); o.y = pk2(s[2 * 33], s[3 * 33]); o.z = pk2(s[4 * 33], s[5 * 33]); o.w = pk2(s[6 * 33], s[7 * 33]);
;         *(GAS v4u*)(WT + (size_t)(n0 + n) * K + k0 + 8 * c) = o; }
	s_add_i32 s24, s23, 64
	s_lshl_b32 s20, s24, 7
	s_cmp_lt_u32 s24, 40
	s_cselect_b32 s21, 0, 0x830
	s_cmp_lt_u32 s24, 72
	s_cselect_b32 s21, s21, 0xfffff030
	s_add_i32 s20, s20, s21
	s_lshl_b32 s20, s20, 2
	s_add_u32 s8, s46, s20
	s_addc_u32 s9, s47, 0
	global_load_dwordx4 v[144:147], v76, s[8:9]
	s_add_u32 s8, s8, 0x16280
	s_addc_u32 s9, s9, 0
	global_load_dwordx4 v[148:151], v76, s[8:9]
	s_add_u32 s8, s8, 0x16280
	s_addc_u32 s9, s9, 0
	global_load_dwordx4 v[152:155], v76, s[8:9]
	s_add_u32 s8, s8, 0x16280
	s_addc_u32 s9, s9, 0
	global_load_dwordx4 v[156:159], v76, s[8:9]
	s_add_u32 s8, s8, 0x16280
	s_addc_u32 s9, s9, 0
	global_load_dwordx4 v[160:163], v76, s[8:9]
	s_add_u32 s8, s8, 0x16280
	s_addc_u32 s9, s9, 0
	global_load_dwordx4 v[164:167], v76, s[8:9]
	s_add_u32 s8, s8, 0x16280
	s_addc_u32 s9, s9, 0
	global_load_dwordx4 v[168:171], v76, s[8:9]
	s_add_u32 s8, s8, 0x16280
	s_addc_u32 s9, s9, 0
	global_load_dwordx4 v[172:175], v76, s[8:9]
	s_add_i32 s24, s23, 48
	s_mul_i32 s20, s24, 0x100000
	s_add_u32 s6, s48, s20
	s_addc_u32 s7, s49, 0
	s_cmp_lt_u32 s24, 16
	s_cselect_b32 s20, 1, 0
	s_sub_i32 s21, s24, 16
	s_bitcmp0_b32 s21, 2
	s_cselect_b32 s21, 1, 0
	s_cmp_lt_u32 s24, 40
	s_cselect_b32 s21, s21, 0
	s_or_b32 s20, s20, s21
	s_cmp_lg_u32 s20, 0
	s_cselect_b64 s[20:21], -1, 0
	v_cndmask_b32_e64 v91, v83, v87, s[20:21]
	v_cndmask_b32_e64 v92, v84, v88, s[20:21]
	v_cndmask_b32_e64 v93, v85, v89, s[20:21]
	v_cndmask_b32_e64 v94, v86, v90, s[20:21]
	ds_read_b32 v226, v112
	ds_read_b32 v227, v112 offset:512
	ds_read_b32 v228, v112 offset:1024
	ds_read_b32 v229, v112 offset:1536
	ds_read_b32 v230, v112 offset:2048
	ds_read_b32 v231, v112 offset:2560
	ds_read_b32 v232, v112 offset:3072
	ds_read_b32 v233, v112 offset:3584
	s_waitcnt lgkmcnt(0)
	v_bfe_u32 v120, v226, 16, 1
	v_bfe_u32 v121, v227, 16, 1
	v_bfe_u32 v122, v228, 16, 1
	v_bfe_u32 v123, v229, 16, 1
	v_bfe_u32 v124, v230, 16, 1
	v_bfe_u32 v125, v231, 16, 1
	v_bfe_u32 v126, v232, 16, 1
	v_bfe_u32 v127, v233, 16, 1
	v_add3_u32 v226, v226, v120, s63
	v_add3_u32 v227, v227, v121, s63
	v_add3_u32 v228, v228, v122, s63
	v_add3_u32 v229, v229, v123, s63
	v_add3_u32 v230, v230, v124, s63
	v_add3_u32 v231, v231, v125, s63
	v_add3_u32 v232, v232, v126, s63
	v_add3_u32 v233, v233, v127, s63
	v_perm_b32 v242, v227, v226, s64
	v_perm_b32 v243, v229, v228, s64
	v_perm_b32 v244, v231, v230, s64
	v_perm_b32 v245, v233, v232, s64
	s_nop 0
	global_store_dwordx4 v91, v[242:245], s[6:7]
	ds_read_b32 v226, v114
	ds_read_b32 v227, v114 offset:512
	ds_read_b32 v228, v114 offset:1024
	ds_read_b32 v229, v114 offset:1536
	ds_read_b32 v230, v114 offset:2048
	ds_read_b32 v231, v114 offset:2560
	ds_read_b32 v232, v114 offset:3072
	ds_read_b32 v233, v114 offset:3584
	s_waitcnt lgkmcnt(0)
	v_bfe_u32 v120, v226, 16, 1
	v_bfe_u32 v121, v227, 16, 1
	v_bfe_u32 v122, v228, 16, 1
	v_bfe_u32 v123, v229, 16, 1
	v_bfe_u32 v124, v230, 16, 1
	v_bfe_u32 v125, v231, 16, 1
	v_bfe_u32 v126, v232, 16, 1
	v_bfe_u32 v127, v233, 16, 1
	v_add3_u32 v226, v226, v120, s63
	v_add3_u32 v227, v227, v121, s63
	v_add3_u32 v228, v228, v122, s63
	v_add3_u32 v229, v229, v123, s63
	v_add3_u32 v230, v230, v124, s63
	v_add3_u32 v231, v231, v125, s63
	v_add3_u32 v232, v232, v126, s63
	v_add3_u32 v233, v233, v127, s63
	v_perm_b32 v242, v227, v226, s64
	v_perm_b32 v243, v229, v228, s64
	v_perm_b32 v244, v231, v230, s64
	v_perm_b32 v245, v233, v232, s64
	s_nop 0
	global_store_dwordx4 v92, v[242:245], s[6:7]
	ds_read_b32 v226, v116
	ds_read_b32 v227, v116 offset:512
	ds_read_b32 v228, v116 offset:1024
	ds_read_b32 v229, v116 offset:1536
	ds_read_b32 v230, v116 offset:2048
	ds_read_b32 v231, v116 offset:2560
	ds_read_b32 v232, v116 offset:3072
	ds_read_b32 v233, v116 offset:3584
	s_waitcnt lgkmcnt(0)
	v_bfe_u32 v120, v226, 16, 1
	v_bfe_u32 v121, v227, 16, 1
	v_bfe_u32 v122, v228, 16, 1
	v_bfe_u32 v123, v229, 16, 1
	v_bfe_u32 v124, v230, 16, 1
	v_bfe_u32 v125, v231, 16, 1
	v_bfe_u32 v126, v232, 16, 1
	v_bfe_u32 v127, v233, 16, 1
	v_add3_u32 v226, v226, v120, s63
	v_add3_u32 v227, v227, v121, s63
	v_add3_u32 v228, v228, v122, s63
	v_add3_u32 v229, v229, v123, s63
	v_add3_u32 v230, v230, v124, s63
	v_add3_u32 v231, v231, v125, s63
	v_add3_u32 v232, v232, v126, s63
	v_add3_u32 v233, v233, v127, s63
	v_perm_b32 v242, v227, v226, s64
	v_perm_b32 v243, v229, v228, s64
	v_perm_b32 v244, v231, v230, s64
	v_perm_b32 v245, v233, v232, s64
	s_nop 0
	global_store_dwordx4 v93, v[242:245], s[6:7]
	ds_read_b32 v226, v118
	ds_read_b32 v227, v118 offset:512
	ds_read_b32 v228, v118 offset:1024
	ds_read_b32 v229, v118 offset:1536
	ds_read_b32 v230, v118 offset:2048
	ds_read_b32 v231, v118 offset:2560
	ds_read_b32 v232, v118 offset:3072
	ds_read_b32 v233, v118 offset:3584
	s_waitcnt lgkmcnt(0)
	v_bfe_u32 v120, v226, 16, 1
	v_bfe_u32 v121, v227, 16, 1
	v_bfe_u32 v122, v228, 16, 1
	v_bfe_u32 v123, v229, 16, 1
	v_bfe_u32 v124, v230, 16, 1
	v_bfe_u32 v125, v231, 16, 1
	v_bfe_u32 v126, v232, 16, 1
	v_bfe_u32 v127, v233, 16, 1
	v_add3_u32 v226, v226, v120, s63
	v_add3_u32 v227, v227, v121, s63
	v_add3_u32 v228, v228, v122, s63
	v_add3_u32 v229, v229, v123, s63
	v_add3_u32 v230, v230, v124, s63
	v_add3_u32 v231, v231, v125, s63
	v_add3_u32 v232, v232, v126, s63
	v_add3_u32 v233, v233, v127, s63
	v_perm_b32 v242, v227, v226, s64
	v_perm_b32 v243, v229, v228, s64
	v_perm_b32 v244, v231, v230, s64
	v_perm_b32 v245, v233, v232, s64
	s_nop 0
	global_store_dwordx4 v94, v[242:245], s[6:7]
	s_waitcnt vmcnt(16)
	v_mul_f32_e32 v176, v42, v176
	v_mul_f32_e32 v177, v42, v177
	v_mul_f32_e32 v178, v42, v178
	v_mul_f32_e32 v179, v42, v179
	ds_write_b128 v210, v[176:179]
	v_mul_f32_e32 v180, v43, v180
	v_mul_f32_e32 v181, v43, v181
	v_mul_f32_e32 v182, v43, v182
	v_mul_f32_e32 v183, v43, v183
	ds_write_b128 v210, v[180:183] offset:1024
	v_mul_f32_e32 v184, v44, v184
	v_mul_f32_e32 v185, v44, v185
	v_mul_f32_e32 v186, v44, v186
	v_mul_f32_e32 v187, v44, v187
	ds_write_b128 v210, v[184:187] offset:2048
	v_mul_f32_e32 v188, v45, v188
	v_mul_f32_e32 v189, v45, v189
	v_mul_f32_e32 v190, v45, v190
	v_mul_f32_e32 v191, v45, v191
	ds_write_b128 v210, v[188:191] offset:3072
	v_mul_f32_e32 v192, v46, v192
	v_mul_f32_e32 v193, v46, v193
	v_mul_f32_e32 v194, v46, v194
	v_mul_f32_e32 v195, v46, v195
	ds_write_b128 v210, v[192:195] offset:4096
	v_mul_f32_e32 v196, v47, v196
	v_mul_f32_e32 v197, v47, v197
	v_mul_f32_e32 v198, v47, v198
	v_mul_f32_e32 v199, v47, v199
	ds_write_b128 v210, v[196:199] offset:5120
	v_mul_f32_e32 v200, v48, v200
	v_mul_f32_e32 v201, v48, v201
	v_mul_f32_e32 v202, v48, v202
	v_mul_f32_e32 v203, v48, v203
	ds_write_b128 v210, v[200:203] offset:6144
	v_mul_f32_e32 v204, v49, v204
	v_mul_f32_e32 v205, v49, v205
	v_mul_f32_e32 v206, v49, v206
	v_mul_f32_e32 v207, v49, v207
	ds_write_b128 v210, v[204:207] offset:7168
	s_waitcnt lgkmcnt(0)
	s_barrier
; #define GAS __attribute__((address_space(1)))
; #define LAS __attribute__((address_space(3)))
; #define LDS_WAIT() asm volatile("s_waitcnt lgkmcnt(0)" ::: "memory")
; __device__ __forceinline__ unsigned pk2(float lo, float hi) { return f2bf(lo) | (f2bf(hi) << 16); }
; __device__ __forceinline__ int nat_dim(int p) { return (p >> 1) + 64 * (p & 1); }
; __device__ __forceinline__ int src_col_in(int c) {
;     if (c < 5120) { const int blk = c >> 7, p = c & 127; const bool rope = blk < 16 || ((((blk - 16) >> 2) & 1) == 0); const int d = rope ? (p >> 1) + 64 * (p & 1) : p; return blk * 128 + d; }
;     if (c < OFF_Z) return c + 2096;
;     if (c < OFF_G) return c - 4048;
;     if (c < OFF_DT) return 5120 + (c - OFF_G);
;     if (c < NSRC) return c;
; template <int MAP, bool KS, bool KPERM = false>
; __device__ __forceinline__ void p0_transpose_item(const float* W, int K, int Nsrc, int nblk, bf16* WT, const float* ksA, const float* ksB, int ksplit, LAS float* scr, int item, int lane) {
;     const int kb = item / nblk, nb = item % nblk, k0 = 64 * kb, n0 = 32 * nb;
;     const int nr = n0 + (lane & 31); const int sc = MAP == 1 ? src_col_in(nr) : (MAP == 2 ? nat_dim(nr) : nr);
;     float v[32];
; #pragma unroll
;     for (int i = 0; i < 32; ++i) { const int k = k0 + 2 * i + (lane >> 5); const int ksrc = KPERM ? ((k & ~127) + nat_dim(k & 127)) : k;
;         v[i] = sc >= 0 ? W[(size_t)ksrc * Nsrc + sc] : 0.f; }
; #pragma unroll
;     for (int i = 0; i < 32; ++i) { const int kk = 2 * i + (lane >> 5); const int k = k0 + kk;
;         if (KS) v[i] *= (k < ksplit ? ksA[k] : ksB[k - ksplit]);
;         scr[kk * 33 + (lane & 31)] = v[i]; }
;     LDS_WAIT(); asm volatile("" ::: "memory");
;     const int c = lane & 7;
; #pragma unroll
;     for (int j = 0; j < 4; ++j) { const int n = (lane >> 3) + 8 * j; const LAS float* s = scr + (8 * c) * 33 + n;
;         v4u o; o.x = pk2(s[0 * 33], s[1 * 33]); o.y = pk2(s[2 * 33], s[3 * 33]); o.z = pk2(s[4 * 33], s[5 * 33]); o.w = pk2(s[6 * 33], s[7 * 33]);
;         *(GAS v4u*)(WT + (size_t)(n0 + n) * K + k0 + 8 * c) = o; }
	s_add_i32 s24, s23, 72
	s_lshl_b32 s20, s24, 7
	s_cmp_lt_u32 s24, 40
	s_cselect_b32 s21, 0, 0x830
	s_cmp_lt_u32 s24, 72
	s_cselect_b32 s21, s21, 0xfffff030
	s_add_i32 s20, s20, s21
	s_lshl_b32 s20, s20, 2
	s_add_u32 s8, s46, s20
	s_addc_u32 s9, s47, 0
	global_load_dwordx4 v[176:179], v76, s[8:9]
	s_add_u32 s8, s8, 0x16280
	s_addc_u32 s9, s9, 0
	global_load_dwordx4 v[180:183], v76, s[8:9]
	s_add_u32 s8, s8, 0x16280
	s_addc_u32 s9, s9, 0
	global_load_dwordx4 v[184:187], v76, s[8:9]
	s_add_u32 s8, s8, 0x16280
	s_addc_u32 s9, s9, 0
	global_load_dwordx4 v[188:191], v76, s[8:9]
	s_add_u32 s8, s8, 0x16280
	s_addc_u32 s9, s9, 0
	global_load_dwordx4 v[192:195], v76, s[8:9]
	s_add_u32 s8, s8, 0x16280
	s_addc_u32 s9, s9, 0
	global_load_dwordx4 v[196:199], v76, s[8:9]
	s_add_u32 s8, s8, 0x16280
	s_addc_u32 s9, s9, 0
	global_load_dwordx4 v[200:203], v76, s[8:9]
	s_add_u32 s8, s8, 0x16280
	s_addc_u32 s9, s9, 0
	global_load_dwordx4 v[204:207], v76, s[8:9]
	s_add_i32 s24, s23, 56
	s_mul_i32 s20, s24, 0x100000
	s_add_u32 s6, s48, s20
	s_addc_u32 s7, s49, 0
	s_cmp_lt_u32 s24, 16
	s_cselect_b32 s20, 1, 0
	s_sub_i32 s21, s24, 16
	s_bitcmp0_b32 s21, 2
	s_cselect_b32 s21, 1, 0
	s_cmp_lt_u32 s24, 40
	s_cselect_b32 s21, s21, 0
	s_or_b32 s20, s20, s21
	s_cmp_lg_u32 s20, 0
	s_cselect_b64 s[20:21], -1, 0
	v_cndmask_b32_e64 v91, v83, v87, s[20:21]
	v_cndmask_b32_e64 v92, v84, v88, s[20:21]
	v_cndmask_b32_e64 v93, v85, v89, s[20:21]
	v_cndmask_b32_e64 v94, v86, v90, s[20:21]
	ds_read_b32 v226, v113
	ds_read_b32 v227, v113 offset:512
	ds_read_b32 v228, v113 offset:1024
	ds_read_b32 v229, v113 offset:1536
	ds_read_b32 v230, v113 offset:2048
	ds_read_b32 v231, v113 offset:2560
	ds_read_b32 v232, v113 offset:3072
	ds_read_b32 v233, v113 offset:3584
	s_waitcnt lgkmcnt(0)
	v_bfe_u32 v120, v226, 16, 1
	v_bfe_u32 v121, v227, 16, 1
	v_bfe_u32 v122, v228, 16, 1
	v_bfe_u32 v123, v229, 16, 1
	v_bfe_u32 v124, v230, 16, 1
	v_bfe_u32 v125, v231, 16, 1
	v_bfe_u32 v126, v232, 16, 1
	v_bfe_u32 v127, v233, 16, 1
	v_add3_u32 v226, v226, v120, s63
	v_add3_u32 v227, v227, v121, s63
	v_add3_u32 v228, v228, v122, s63
	v_add3_u32 v229, v229, v123, s63
	v_add3_u32 v230, v230, v124, s63
	v_add3_u32 v231, v231, v125, s63
	v_add3_u32 v232, v232, v126, s63
	v_add3_u32 v233, v233, v127, s63
	v_perm_b32 v242, v227, v226, s64
	v_perm_b32 v243, v229, v228, s64
	v_perm_b32 v244, v231, v230, s64
	v_perm_b32 v245, v233, v232, s64
	s_nop 0
	global_store_dwordx4 v91, v[242:245], s[6:7]
	ds_read_b32 v226, v115
	ds_read_b32 v227, v115 offset:512
	ds_read_b32 v228, v115 offset:1024
	ds_read_b32 v229, v115 offset:1536
	ds_read_b32 v230, v115 offset:2048
	ds_read_b32 v231, v115 offset:2560
	ds_read_b32 v232, v115 offset:3072
	ds_read_b32 v233, v115 offset:3584
	s_waitcnt lgkmcnt(0)
	v_bfe_u32 v120, v226, 16, 1
	v_bfe_u32 v121, v227, 16, 1
	v_bfe_u32 v122, v228, 16, 1
	v_bfe_u32 v123, v229, 16, 1
	v_bfe_u32 v124, v230, 16, 1
	v_bfe_u32 v125, v231, 16, 1
	v_bfe_u32 v126, v232, 16, 1
	v_bfe_u32 v127, v233, 16, 1
	v_add3_u32 v226, v226, v120, s63
	v_add3_u32 v227, v227, v121, s63
	v_add3_u32 v228, v228, v122, s63
	v_add3_u32 v229, v229, v123, s63
	v_add3_u32 v230, v230, v124, s63
	v_add3_u32 v231, v231, v125, s63
	v_add3_u32 v232, v232, v126, s63
	v_add3_u32 v233, v233, v127, s63
	v_perm_b32 v242, v227, v226, s64
	v_perm_b32 v243, v229, v228, s64
	v_perm_b32 v244, v231, v230, s64
	v_perm_b32 v245, v233, v232, s64
	s_nop 0
	global_store_dwordx4 v92, v[242:245], s[6:7]
	ds_read_b32 v226, v117
	ds_read_b32 v227, v117 offset:512
	ds_read_b32 v228, v117 offset:1024
	ds_read_b32 v229, v117 offset:1536
	ds_read_b32 v230, v117 offset:2048
	ds_read_b32 v231, v117 offset:2560
	ds_read_b32 v232, v117 offset:3072
	ds_read_b32 v233, v117 offset:3584
	s_waitcnt lgkmcnt(0)
	v_bfe_u32 v120, v226, 16, 1
	v_bfe_u32 v121, v227, 16, 1
	v_bfe_u32 v122, v228, 16, 1
	v_bfe_u32 v123, v229, 16, 1
	v_bfe_u32 v124, v230, 16, 1
	v_bfe_u32 v125, v231, 16, 1
	v_bfe_u32 v126, v232, 16, 1
	v_bfe_u32 v127, v233, 16, 1
	v_add3_u32 v226, v226, v120, s63
	v_add3_u32 v227, v227, v121, s63
	v_add3_u32 v228, v228, v122, s63
	v_add3_u32 v229, v229, v123, s63
	v_add3_u32 v230, v230, v124, s63
	v_add3_u32 v231, v231, v125, s63
	v_add3_u32 v232, v232, v126, s63
	v_add3_u32 v233, v233, v127, s63
	v_perm_b32 v242, v227, v226, s64
	v_perm_b32 v243, v229, v228, s64
	v_perm_b32 v244, v231, v230, s64
	v_perm_b32 v245, v233, v232, s64
	s_nop 0
	global_store_dwordx4 v93, v[242:245], s[6:7]
	ds_read_b32 v226, v119
	ds_read_b32 v227, v119 offset:512
	ds_read_b32 v228, v119 offset:1024
	ds_read_b32 v229, v119 offset:1536
	ds_read_b32 v230, v119 offset:2048
	ds_read_b32 v231, v119 offset:2560
	ds_read_b32 v232, v119 offset:3072
	ds_read_b32 v233, v119 offset:3584
	s_waitcnt lgkmcnt(0)
	v_bfe_u32 v120, v226, 16, 1
	v_bfe_u32 v121, v227, 16, 1
	v_bfe_u32 v122, v228, 16, 1
	v_bfe_u32 v123, v229, 16, 1
	v_bfe_u32 v124, v230, 16, 1
	v_bfe_u32 v125, v231, 16, 1
	v_bfe_u32 v126, v232, 16, 1
	v_bfe_u32 v127, v233, 16, 1
	v_add3_u32 v226, v226, v120, s63
	v_add3_u32 v227, v227, v121, s63
	v_add3_u32 v228, v228, v122, s63
	v_add3_u32 v229, v229, v123, s63
	v_add3_u32 v230, v230, v124, s63
	v_add3_u32 v231, v231, v125, s63
	v_add3_u32 v232, v232, v126, s63
	v_add3_u32 v233, v233, v127, s63
	v_perm_b32 v242, v227, v226, s64
	v_perm_b32 v243, v229, v228, s64
	v_perm_b32 v244, v231, v230, s64
	v_perm_b32 v245, v233, v232, s64
	s_nop 0
	global_store_dwordx4 v94, v[242:245], s[6:7]
	s_waitcnt vmcnt(16)
	v_mul_f32_e32 v144, v42, v144
	v_mul_f32_e32 v145, v42, v145
	v_mul_f32_e32 v146, v42, v146
	v_mul_f32_e32 v147, v42, v147
	ds_write_b128 v209, v[144:147]
	v_mul_f32_e32 v148, v43, v148
	v_mul_f32_e32 v149, v43, v149
	v_mul_f32_e32 v150, v43, v150
	v_mul_f32_e32 v151, v43, v151
	ds_write_b128 v209, v[148:151] offset:1024
	v_mul_f32_e32 v152, v44, v152
	v_mul_f32_e32 v153, v44, v153
	v_mul_f32_e32 v154, v44, v154
	v_mul_f32_e32 v155, v44, v155
	ds_write_b128 v209, v[152:155] offset:2048
	v_mul_f32_e32 v156, v45, v156
	v_mul_f32_e32 v157, v45, v157
	v_mul_f32_e32 v158, v45, v158
	v_mul_f32_e32 v159, v45, v159
	ds_write_b128 v209, v[156:159] offset:3072
	v_mul_f32_e32 v160, v46, v160
	v_mul_f32_e32 v161, v46, v161
	v_mul_f32_e32 v162, v46, v162
	v_mul_f32_e32 v163, v46, v163
	ds_write_b128 v209, v[160:163] offset:4096
	v_mul_f32_e32 v164, v47, v164
	v_mul_f32_e32 v165, v47, v165
	v_mul_f32_e32 v166, v47, v166
	v_mul_f32_e32 v167, v47, v167
	ds_write_b128 v209, v[164:167] offset:5120
	v_mul_f32_e32 v168, v48, v168
	v_mul_f32_e32 v169, v48, v169
	v_mul_f32_e32 v170, v48, v170
	v_mul_f32_e32 v171, v48, v171
	ds_write_b128 v209, v[168:171] offset:6144
	v_mul_f32_e32 v172, v49, v172
	v_mul_f32_e32 v173, v49, v173
	v_mul_f32_e32 v174, v49, v174
	v_mul_f32_e32 v175, v49, v175
	ds_write_b128 v209, v[172:175] offset:7168
	s_waitcnt lgkmcnt(0)
	s_barrier
; #define GAS __attribute__((address_space(1)))
; #define LAS __attribute__((address_space(3)))
; #define LDS_WAIT() asm volatile("s_waitcnt lgkmcnt(0)" ::: "memory")
; __device__ __forceinline__ unsigned pk2(float lo, float hi) { return f2bf(lo) | (f2bf(hi) << 16); }
; __device__ __forceinline__ int nat_dim(int p) { return (p >> 1) + 64 * (p & 1); }
; __device__ __forceinline__ int src_col_in(int c) {
;     if (c < 5120) { const int blk = c >> 7, p = c & 127; const bool rope = blk < 16 || ((((blk - 16) >> 2) & 1) == 0); const int d = rope ? (p >> 1) + 64 * (p & 1) : p; return blk * 128 + d; }
;     if (c < OFF_Z) return c + 2096;
;     if (c < OFF_G) return c - 4048;
;     if (c < OFF_DT) return 5120 + (c - OFF_G);
;     if (c < NSRC) return c;
; template <int MAP, bool KS, bool KPERM = false>
; __device__ __forceinline__ void p0_transpose_item(const float* W, int K, int Nsrc, int nblk, bf16* WT, const float* ksA, const float* ksB, int ksplit, LAS float* scr, int item, int lane) {
;     const int kb = item / nblk, nb = item % nblk, k0 = 64 * kb, n0 = 32 * nb;
;     const int nr = n0 + (lane & 31); const int sc = MAP == 1 ? src_col_in(nr) : (MAP == 2 ? nat_dim(nr) : nr);
;     float v[32];
; #pragma unroll
;     for (int i = 0; i < 32; ++i) { const int k = k0 + 2 * i + (lane >> 5); const int ksrc = KPERM ? ((k & ~127) + nat_dim(k & 127)) : k;
;         v[i] = sc >= 0 ? W[(size_t)ksrc * Nsrc + sc] : 0.f; }
; #pragma unroll
;     for (int i = 0; i < 32; ++i) { const int kk = 2 * i + (lane >> 5); const int k = k0 + kk;
;         if (KS) v[i] *= (k < ksplit ? ksA[k] : ksB[k - ksplit]);
;         scr[kk * 33 + (lane & 31)] = v[i]; }
;     LDS_WAIT(); asm volatile("" ::: "memory");
;     const int c = lane & 7;
; #pragma unroll
;     for (int j = 0; j < 4; ++j) { const int n = (lane >> 3) + 8 * j; const LAS float* s = scr + (8 * c) * 33 + n;
;         v4u o; o.x = pk2(s[0 * 33], s[1 * 33]); o.y = pk2(s[2 * 33], s[3 * 33]); o.z = pk2(s[4 * 33], s[5 * 33]); o.w = pk2(s[6 * 33], s[7 * 33]);
;         *(GAS v4u*)(WT + (size_t)(n0 + n) * K + k0 + 8 * c) = o; }
	s_add_i32 s24, s23, 80
	s_lshl_b32 s20, s24, 7
	s_cmp_lt_u32 s24, 40
	s_cselect_b32 s21, 0, 0x830
	s_cmp_lt_u32 s24, 72
	s_cselect_b32 s21, s21, 0xfffff030
	s_add_i32 s20, s20, s21
	s_lshl_b32 s20, s20, 2
	s_add_u32 s8, s46, s20
	s_addc_u32 s9, s47, 0
	global_load_dwordx4 v[144:147], v76, s[8:9]
	s_add_u32 s8, s8, 0x16280
	s_addc_u32 s9, s9, 0
	global_load_dwordx4 v[148:151], v76, s[8:9]
	s_add_u32 s8, s8, 0x16280
	s_addc_u32 s9, s9, 0
	global_load_dwordx4 v[152:155], v76, s[8:9]
	s_add_u32 s8, s8, 0x16280
	s_addc_u32 s9, s9, 0
	global_load_dwordx4 v[156:159], v76, s[8:9]
	s_add_u32 s8, s8, 0x16280
	s_addc_u32 s9, s9, 0
	global_load_dwordx4 v[160:163], v76, s[8:9]
	s_add_u32 s8, s8, 0x16280
	s_addc_u32 s9, s9, 0
	global_load_dwordx4 v[164:167], v76, s[8:9]
	s_add_u32 s8, s8, 0x16280
	s_addc_u32 s9, s9, 0
	global_load_dwordx4 v[168:171], v76, s[8:9]
	s_add_u32 s8, s8, 0x16280
	s_addc_u32 s9, s9, 0
	global_load_dwordx4 v[172:175], v76, s[8:9]
	s_add_i32 s24, s23, 64
	s_mul_i32 s20, s24, 0x100000
	s_add_u32 s6, s48, s20
	s_addc_u32 s7, s49, 0
	s_cmp_lt_u32 s24, 16
	s_cselect_b32 s20, 1, 0
	s_sub_i32 s21, s24, 16
	s_bitcmp0_b32 s21, 2
	s_cselect_b32 s21, 1, 0
	s_cmp_lt_u32 s24, 40
	s_cselect_b32 s21, s21, 0
	s_or_b32 s20, s20, s21
	s_cmp_lg_u32 s20, 0
	s_cselect_b64 s[20:21], -1, 0
	v_cndmask_b32_e64 v91, v83, v87, s[20:21]
	v_cndmask_b32_e64 v92, v84, v88, s[20:21]
	v_cndmask_b32_e64 v93, v85, v89, s[20:21]
	v_cndmask_b32_e64 v94, v86, v90, s[20:21]
	ds_read_b32 v226, v112
	ds_read_b32 v227, v112 offset:512
	ds_read_b32 v228, v112 offset:1024
	ds_read_b32 v229, v112 offset:1536
	ds_read_b32 v230, v112 offset:2048
	ds_read_b32 v231, v112 offset:2560
	ds_read_b32 v232, v112 offset:3072
	ds_read_b32 v233, v112 offset:3584
	s_waitcnt lgkmcnt(0)
	v_bfe_u32 v120, v226, 16, 1
	v_bfe_u32 v121, v227, 16, 1
	v_bfe_u32 v122, v228, 16, 1
	v_bfe_u32 v123, v229, 16, 1
	v_bfe_u32 v124, v230, 16, 1
	v_bfe_u32 v125, v231, 16, 1
	v_bfe_u32 v126, v232, 16, 1
	v_bfe_u32 v127, v233, 16, 1
	v_add3_u32 v226, v226, v120, s63
	v_add3_u32 v227, v227, v121, s63
	v_add3_u32 v228, v228, v122, s63
	v_add3_u32 v229, v229, v123, s63
	v_add3_u32 v230, v230, v124, s63
	v_add3_u32 v231, v231, v125, s63
	v_add3_u32 v232, v232, v126, s63
	v_add3_u32 v233, v233, v127, s63
	v_perm_b32 v242, v227, v226, s64
	v_perm_b32 v243, v229, v228, s64
	v_perm_b32 v244, v231, v230, s64
	v_perm_b32 v245, v233, v232, s64
	s_nop 0
	global_store_dwordx4 v91, v[242:245], s[6:7]
	ds_read_b32 v226, v114
	ds_read_b32 v227, v114 offset:512
	ds_read_b32 v228, v114 offset:1024
	ds_read_b32 v229, v114 offset:1536
	ds_read_b32 v230, v114 offset:2048
	ds_read_b32 v231, v114 offset:2560
	ds_read_b32 v232, v114 offset:3072
	ds_read_b32 v233, v114 offset:3584
	s_waitcnt lgkmcnt(0)
	v_bfe_u32 v120, v226, 16, 1
	v_bfe_u32 v121, v227, 16, 1
	v_bfe_u32 v122, v228, 16, 1
	v_bfe_u32 v123, v229, 16, 1
	v_bfe_u32 v124, v230, 16, 1
	v_bfe_u32 v125, v231, 16, 1
	v_bfe_u32 v126, v232, 16, 1
	v_bfe_u32 v127, v233, 16, 1
	v_add3_u32 v226, v226, v120, s63
	v_add3_u32 v227, v227, v121, s63
	v_add3_u32 v228, v228, v122, s63
	v_add3_u32 v229, v229, v123, s63
	v_add3_u32 v230, v230, v124, s63
	v_add3_u32 v231, v231, v125, s63
	v_add3_u32 v232, v232, v126, s63
	v_add3_u32 v233, v233, v127, s63
	v_perm_b32 v242, v227, v226, s64
	v_perm_b32 v243, v229, v228, s64
	v_perm_b32 v244, v231, v230, s64
	v_perm_b32 v245, v233, v232, s64
	s_nop 0
	global_store_dwordx4 v92, v[242:245], s[6:7]
	ds_read_b32 v226, v116
	ds_read_b32 v227, v116 offset:512
	ds_read_b32 v228, v116 offset:1024
	ds_read_b32 v229, v116 offset:1536
	ds_read_b32 v230, v116 offset:2048
	ds_read_b32 v231, v116 offset:2560
	ds_read_b32 v232, v116 offset:3072
	ds_read_b32 v233, v116 offset:3584
	s_waitcnt lgkmcnt(0)
	v_bfe_u32 v120, v226, 16, 1
	v_bfe_u32 v121, v227, 16, 1
	v_bfe_u32 v122, v228, 16, 1
	v_bfe_u32 v123, v229, 16, 1
	v_bfe_u32 v124, v230, 16, 1
	v_bfe_u32 v125, v231, 16, 1
	v_bfe_u32 v126, v232, 16, 1
	v_bfe_u32 v127, v233, 16, 1
	v_add3_u32 v226, v226, v120, s63
	v_add3_u32 v227, v227, v121, s63
	v_add3_u32 v228, v228, v122, s63
	v_add3_u32 v229, v229, v123, s63
	v_add3_u32 v230, v230, v124, s63
	v_add3_u32 v231, v231, v125, s63
	v_add3_u32 v232, v232, v126, s63
	v_add3_u32 v233, v233, v127, s63
	v_perm_b32 v242, v227, v226, s64
	v_perm_b32 v243, v229, v228, s64
	v_perm_b32 v244, v231, v230, s64
	v_perm_b32 v245, v233, v232, s64
	s_nop 0
	global_store_dwordx4 v93, v[242:245], s[6:7]
	ds_read_b32 v226, v118
	ds_read_b32 v227, v118 offset:512
	ds_read_b32 v228, v118 offset:1024
	ds_read_b32 v229, v118 offset:1536
	ds_read_b32 v230, v118 offset:2048
	ds_read_b32 v231, v118 offset:2560
	ds_read_b32 v232, v118 offset:3072
	ds_read_b32 v233, v118 offset:3584
	s_waitcnt lgkmcnt(0)
	v_bfe_u32 v120, v226, 16, 1
	v_bfe_u32 v121, v227, 16, 1
	v_bfe_u32 v122, v228, 16, 1
	v_bfe_u32 v123, v229, 16, 1
	v_bfe_u32 v124, v230, 16, 1
	v_bfe_u32 v125, v231, 16, 1
	v_bfe_u32 v126, v232, 16, 1
	v_bfe_u32 v127, v233, 16, 1
	v_add3_u32 v226, v226, v120, s63
	v_add3_u32 v227, v227, v121, s63
	v_add3_u32 v228, v228, v122, s63
	v_add3_u32 v229, v229, v123, s63
	v_add3_u32 v230, v230, v124, s63
	v_add3_u32 v231, v231, v125, s63
	v_add3_u32 v232, v232, v126, s63
	v_add3_u32 v233, v233, v127, s63
	v_perm_b32 v242, v227, v226, s64
	v_perm_b32 v243, v229, v228, s64
	v_perm_b32 v244, v231, v230, s64
	v_perm_b32 v245, v233, v232, s64
	s_nop 0
	global_store_dwordx4 v94, v[242:245], s[6:7]
	s_waitcnt vmcnt(16)
	v_mul_f32_e32 v176, v42, v176
	v_mul_f32_e32 v177, v42, v177
	v_mul_f32_e32 v178, v42, v178
	v_mul_f32_e32 v179, v42, v179
	ds_write_b128 v210, v[176:179]
	v_mul_f32_e32 v180, v43, v180
	v_mul_f32_e32 v181, v43, v181
	v_mul_f32_e32 v182, v43, v182
	v_mul_f32_e32 v183, v43, v183
	ds_write_b128 v210, v[180:183] offset:1024
	v_mul_f32_e32 v184, v44, v184
	v_mul_f32_e32 v185, v44, v185
	v_mul_f32_e32 v186, v44, v186
	v_mul_f32_e32 v187, v44, v187
	ds_write_b128 v210, v[184:187] offset:2048
	v_mul_f32_e32 v188, v45, v188
	v_mul_f32_e32 v189, v45, v189
	v_mul_f32_e32 v190, v45, v190
	v_mul_f32_e32 v191, v45, v191
	ds_write_b128 v210, v[188:191] offset:3072
	v_mul_f32_e32 v192, v46, v192
	v_mul_f32_e32 v193, v46, v193
	v_mul_f32_e32 v194, v46, v194
	v_mul_f32_e32 v195, v46, v195
	ds_write_b128 v210, v[192:195] offset:4096
	v_mul_f32_e32 v196, v47, v196
	v_mul_f32_e32 v197, v47, v197
	v_mul_f32_e32 v198, v47, v198
	v_mul_f32_e32 v199, v47, v199
	ds_write_b128 v210, v[196:199] offset:5120
	v_mul_f32_e32 v200, v48, v200
	v_mul_f32_e32 v201, v48, v201
	v_mul_f32_e32 v202, v48, v202
	v_mul_f32_e32 v203, v48, v203
	ds_write_b128 v210, v[200:203] offset:6144
	v_mul_f32_e32 v204, v49, v204
	v_mul_f32_e32 v205, v49, v205
	v_mul_f32_e32 v206, v49, v206
	v_mul_f32_e32 v207, v49, v207
	ds_write_b128 v210, v[204:207] offset:7168
	s_waitcnt lgkmcnt(0)
	s_barrier
; #define GAS __attribute__((address_space(1)))
; #define LAS __attribute__((address_space(3)))
; #define LDS_WAIT() asm volatile("s_waitcnt lgkmcnt(0)" ::: "memory")
; __device__ __forceinline__ unsigned pk2(float lo, float hi) { return f2bf(lo) | (f2bf(hi) << 16); }
; __device__ __forceinline__ int nat_dim(int p) { return (p >> 1) + 64 * (p & 1); }
; __device__ __forceinline__ int src_col_in(int c) {
;     if (c < 5120) { const int blk = c >> 7, p = c & 127; const bool rope = blk < 16 || ((((blk - 16) >> 2) & 1) == 0); const int d = rope ? (p >> 1) + 64 * (p & 1) : p; return blk * 128 + d; }
;     if (c < OFF_Z) return c + 2096;
;     if (c < OFF_G) return c - 4048;
;     if (c < OFF_DT) return 5120 + (c - OFF_G);
;     if (c < NSRC) return c;
; template <int MAP, bool KS, bool KPERM = false>
; __device__ __forceinline__ void p0_transpose_item(const float* W, int K, int Nsrc, int nblk, bf16* WT, const float* ksA, const float* ksB, int ksplit, LAS float* scr, int item, int lane) {
;     const int kb = item / nblk, nb = item % nblk, k0 = 64 * kb, n0 = 32 * nb;
;     const int nr = n0 + (lane & 31); const int sc = MAP == 1 ? src_col_in(nr) : (MAP == 2 ? nat_dim(nr) : nr);
;     float v[32];
; #pragma unroll
;     for (int i = 0; i < 32; ++i) { const int k = k0 + 2 * i + (lane >> 5); const int ksrc = KPERM ? ((k & ~127) + nat_dim(k & 127)) : k;
;         v[i] = sc >= 0 ? W[(size_t)ksrc * Nsrc + sc] : 0.f; }
; #pragma unroll
;     for (int i = 0; i < 32; ++i) { const int kk = 2 * i + (lane >> 5); const int k = k0 + kk;
;         if (KS) v[i] *= (k < ksplit ? ksA[k] : ksB[k - ksplit]);
;         scr[kk * 33 + (lane & 31)] = v[i]; }
;     LDS_WAIT(); asm volatile("" ::: "memory");
;     const int c = lane & 7;
; #pragma unroll
;     for (int j = 0; j < 4; ++j) { const int n = (lane >> 3) + 8 * j; const LAS float* s = scr + (8 * c) * 33 + n;
;         v4u o; o.x = pk2(s[0 * 33], s[1 * 33]); o.y = pk2(s[2 * 33], s[3 * 33]); o.z = pk2(s[4 * 33], s[5 * 33]); o.w = pk2(s[6 * 33], s[7 * 33]);
;         *(GAS v4u*)(WT + (size_t)(n0 + n) * K + k0 + 8 * c) = o; }
	s_add_i32 s24, s23, 0
	s_lshl_b32 s20, s24, 7
	s_cmp_lt_u32 s24, 40
	s_cselect_b32 s21, 0, 0x830
	s_cmp_lt_u32 s24, 72
	s_cselect_b32 s21, s21, 0xfffff030
	s_add_i32 s20, s20, s21
	s_lshl_b32 s20, s20, 2
	s_add_u32 s8, s50, s20
	s_addc_u32 s9, s51, 0
	global_load_dwordx4 v[176:179], v76, s[8:9]
	s_add_u32 s8, s8, 0x16280
	s_addc_u32 s9, s9, 0
	global_load_dwordx4 v[180:183], v76, s[8:9]
	s_add_u32 s8, s8, 0x16280
	s_addc_u32 s9, s9, 0
	global_load_dwordx4 v[184:187], v76, s[8:9]
	s_add_u32 s8, s8, 0x16280
	s_addc_u32 s9, s9, 0
	global_load_dwordx4 v[188:191], v76, s[8:9]
	s_add_u32 s8, s8, 0x16280
	s_addc_u32 s9, s9, 0
	global_load_dwordx4 v[192:195], v76, s[8:9]
	s_add_u32 s8, s8, 0x16280
	s_addc_u32 s9, s9, 0
	global_load_dwordx4 v[196:199], v76, s[8:9]
	s_add_u32 s8, s8, 0x16280
	s_addc_u32 s9, s9, 0
	global_load_dwordx4 v[200:203], v76, s[8:9]
	s_add_u32 s8, s8, 0x16280
	s_addc_u32 s9, s9, 0
	global_load_dwordx4 v[204:207], v76, s[8:9]
	s_add_i32 s24, s23, 72
	s_mul_i32 s20, s24, 0x100000
	s_add_u32 s6, s48, s20
	s_addc_u32 s7, s49, 0
	s_cmp_lt_u32 s24, 16
	s_cselect_b32 s20, 1, 0
	s_sub_i32 s21, s24, 16
	s_bitcmp0_b32 s21, 2
	s_cselect_b32 s21, 1, 0
	s_cmp_lt_u32 s24, 40
	s_cselect_b32 s21, s21, 0
	s_or_b32 s20, s20, s21
	s_cmp_lg_u32 s20, 0
	s_cselect_b64 s[20:21], -1, 0
	v_cndmask_b32_e64 v91, v83, v87, s[20:21]
	v_cndmask_b32_e64 v92, v84, v88, s[20:21]
	v_cndmask_b32_e64 v93, v85, v89, s[20:21]
	v_cndmask_b32_e64 v94, v86, v90, s[20:21]
	ds_read_b32 v226, v113
	ds_read_b32 v227, v113 offset:512
	ds_read_b32 v228, v113 offset:1024
	ds_read_b32 v229, v113 offset:1536
	ds_read_b32 v230, v113 offset:2048
	ds_read_b32 v231, v113 offset:2560
	ds_read_b32 v232, v113 offset:3072
	ds_read_b32 v233, v113 offset:3584
	s_waitcnt lgkmcnt(0)
	v_bfe_u32 v120, v226, 16, 1
	v_bfe_u32 v121, v227, 16, 1
	v_bfe_u32 v122, v228, 16, 1
	v_bfe_u32 v123, v229, 16, 1
	v_bfe_u32 v124, v230, 16, 1
	v_bfe_u32 v125, v231, 16, 1
	v_bfe_u32 v126, v232, 16, 1
	v_bfe_u32 v127, v233, 16, 1
	v_add3_u32 v226, v226, v120, s63
	v_add3_u32 v227, v227, v121, s63
	v_add3_u32 v228, v228, v122, s63
	v_add3_u32 v229, v229, v123, s63
	v_add3_u32 v230, v230, v124, s63
	v_add3_u32 v231, v231, v125, s63
	v_add3_u32 v232, v232, v126, s63
	v_add3_u32 v233, v233, v127, s63
	v_perm_b32 v242, v227, v226, s64
	v_perm_b32 v243, v229, v228, s64
	v_perm_b32 v244, v231, v230, s64
	v_perm_b32 v245, v233, v232, s64
	s_nop 0
	global_store_dwordx4 v91, v[242:245], s[6:7]
	ds_read_b32 v226, v115
	ds_read_b32 v227, v115 offset:512
	ds_read_b32 v228, v115 offset:1024
	ds_read_b32 v229, v115 offset:1536
	ds_read_b32 v230, v115 offset:2048
	ds_read_b32 v231, v115 offset:2560
	ds_read_b32 v232, v115 offset:3072
	ds_read_b32 v233, v115 offset:3584
	s_waitcnt lgkmcnt(0)
	v_bfe_u32 v120, v226, 16, 1
	v_bfe_u32 v121, v227, 16, 1
	v_bfe_u32 v122, v228, 16, 1
	v_bfe_u32 v123, v229, 16, 1
	v_bfe_u32 v124, v230, 16, 1
	v_bfe_u32 v125, v231, 16, 1
	v_bfe_u32 v126, v232, 16, 1
	v_bfe_u32 v127, v233, 16, 1
	v_add3_u32 v226, v226, v120, s63
	v_add3_u32 v227, v227, v121, s63
	v_add3_u32 v228, v228, v122, s63
	v_add3_u32 v229, v229, v123, s63
	v_add3_u32 v230, v230, v124, s63
	v_add3_u32 v231, v231, v125, s63
	v_add3_u32 v232, v232, v126, s63
	v_add3_u32 v233, v233, v127, s63
	v_perm_b32 v242, v227, v226, s64
	v_perm_b32 v243, v229, v228, s64
	v_perm_b32 v244, v231, v230, s64
	v_perm_b32 v245, v233, v232, s64
	s_nop 0
	global_store_dwordx4 v92, v[242:245], s[6:7]
	ds_read_b32 v226, v117
	ds_read_b32 v227, v117 offset:512
	ds_read_b32 v228, v117 offset:1024
	ds_read_b32 v229, v117 offset:1536
	ds_read_b32 v230, v117 offset:2048
	ds_read_b32 v231, v117 offset:2560
	ds_read_b32 v232, v117 offset:3072
	ds_read_b32 v233, v117 offset:3584
	s_waitcnt lgkmcnt(0)
	v_bfe_u32 v120, v226, 16, 1
	v_bfe_u32 v121, v227, 16, 1
	v_bfe_u32 v122, v228, 16, 1
	v_bfe_u32 v123, v229, 16, 1
	v_bfe_u32 v124, v230, 16, 1
	v_bfe_u32 v125, v231, 16, 1
	v_bfe_u32 v126, v232, 16, 1
	v_bfe_u32 v127, v233, 16, 1
	v_add3_u32 v226, v226, v120, s63
	v_add3_u32 v227, v227, v121, s63
	v_add3_u32 v228, v228, v122, s63
	v_add3_u32 v229, v229, v123, s63
	v_add3_u32 v230, v230, v124, s63
	v_add3_u32 v231, v231, v125, s63
	v_add3_u32 v232, v232, v126, s63
	v_add3_u32 v233, v233, v127, s63
	v_perm_b32 v242, v227, v226, s64
	v_perm_b32 v243, v229, v228, s64
	v_perm_b32 v244, v231, v230, s64
	v_perm_b32 v245, v233, v232, s64
	s_nop 0
	global_store_dwordx4 v93, v[242:245], s[6:7]
	ds_read_b32 v226, v119
	ds_read_b32 v227, v119 offset:512
	ds_read_b32 v228, v119 offset:1024
	ds_read_b32 v229, v119 offset:1536
	ds_read_b32 v230, v119 offset:2048
	ds_read_b32 v231, v119 offset:2560
	ds_read_b32 v232, v119 offset:3072
	ds_read_b32 v233, v119 offset:3584
	s_waitcnt lgkmcnt(0)
	v_bfe_u32 v120, v226, 16, 1
	v_bfe_u32 v121, v227, 16, 1
	v_bfe_u32 v122, v228, 16, 1
	v_bfe_u32 v123, v229, 16, 1
	v_bfe_u32 v124, v230, 16, 1
	v_bfe_u32 v125, v231, 16, 1
	v_bfe_u32 v126, v232, 16, 1
	v_bfe_u32 v127, v233, 16, 1
	v_add3_u32 v226, v226, v120, s63
	v_add3_u32 v227, v227, v121, s63
	v_add3_u32 v228, v228, v122, s63
	v_add3_u32 v229, v229, v123, s63
	v_add3_u32 v230, v230, v124, s63
	v_add3_u32 v231, v231, v125, s63
	v_add3_u32 v232, v232, v126, s63
	v_add3_u32 v233, v233, v127, s63
	v_perm_b32 v242, v227, v226, s64
	v_perm_b32 v243, v229, v228, s64
	v_perm_b32 v244, v231, v230, s64
	v_perm_b32 v245, v233, v232, s64
	s_nop 0
	global_store_dwordx4 v94, v[242:245], s[6:7]
	s_waitcnt vmcnt(16)
	v_mul_f32_e32 v144, v42, v144
	v_mul_f32_e32 v145, v42, v145
	v_mul_f32_e32 v146, v42, v146
	v_mul_f32_e32 v147, v42, v147
	ds_write_b128 v209, v[144:147]
	v_mul_f32_e32 v148, v43, v148
	v_mul_f32_e32 v149, v43, v149
	v_mul_f32_e32 v150, v43, v150
	v_mul_f32_e32 v151, v43, v151
	ds_write_b128 v209, v[148:151] offset:1024
	v_mul_f32_e32 v152, v44, v152
	v_mul_f32_e32 v153, v44, v153
	v_mul_f32_e32 v154, v44, v154
	v_mul_f32_e32 v155, v44, v155
	ds_write_b128 v209, v[152:155] offset:2048
	v_mul_f32_e32 v156, v45, v156
	v_mul_f32_e32 v157, v45, v157
	v_mul_f32_e32 v158, v45, v158
	v_mul_f32_e32 v159, v45, v159
	ds_write_b128 v209, v[156:159] offset:3072
	v_mul_f32_e32 v160, v46, v160
	v_mul_f32_e32 v161, v46, v161
	v_mul_f32_e32 v162, v46, v162
	v_mul_f32_e32 v163, v46, v163
	ds_write_b128 v209, v[160:163] offset:4096
	v_mul_f32_e32 v164, v47, v164
	v_mul_f32_e32 v165, v47, v165
	v_mul_f32_e32 v166, v47, v166
	v_mul_f32_e32 v167, v47, v167
	ds_write_b128 v209, v[164:167] offset:5120
	v_mul_f32_e32 v168, v48, v168
	v_mul_f32_e32 v169, v48, v169
	v_mul_f32_e32 v170, v48, v170
	v_mul_f32_e32 v171, v48, v171
	ds_write_b128 v209, v[168:171] offset:6144
	v_mul_f32_e32 v172, v49, v172
	v_mul_f32_e32 v173, v49, v173
	v_mul_f32_e32 v174, v49, v174
	v_mul_f32_e32 v175, v49, v175
	ds_write_b128 v209, v[172:175] offset:7168
	s_waitcnt lgkmcnt(0)
	s_barrier
; #define GAS __attribute__((address_space(1)))
; #define LAS __attribute__((address_space(3)))
; #define LDS_WAIT() asm volatile("s_waitcnt lgkmcnt(0)" ::: "memory")
; __device__ __forceinline__ unsigned pk2(float lo, float hi) { return f2bf(lo) | (f2bf(hi) << 16); }
; __device__ __forceinline__ int nat_dim(int p) { return (p >> 1) + 64 * (p & 1); }
; __device__ __forceinline__ int src_col_in(int c) {
;     if (c < 5120) { const int blk = c >> 7, p = c & 127; const bool rope = blk < 16 || ((((blk - 16) >> 2) & 1) == 0); const int d = rope ? (p >> 1) + 64 * (p & 1) : p; return blk * 128 + d; }
;     if (c < OFF_Z) return c + 2096;
;     if (c < OFF_G) return c - 4048;
;     if (c < OFF_DT) return 5120 + (c - OFF_G);
;     if (c < NSRC) return c;
; template <int MAP, bool KS, bool KPERM = false>
; __device__ __forceinline__ void p0_transpose_item(const float* W, int K, int Nsrc, int nblk, bf16* WT, const float* ksA, const float* ksB, int ksplit, LAS float* scr, int item, int lane) {
;     const int kb = item / nblk, nb = item % nblk, k0 = 64 * kb, n0 = 32 * nb;
;     const int nr = n0 + (lane & 31); const int sc = MAP == 1 ? src_col_in(nr) : (MAP == 2 ? nat_dim(nr) : nr);
;     float v[32];
; #pragma unroll
;     for (int i = 0; i < 32; ++i) { const int k = k0 + 2 * i + (lane >> 5); const int ksrc = KPERM ? ((k & ~127) + nat_dim(k & 127)) : k;
;         v[i] = sc >= 0 ? W[(size_t)ksrc * Nsrc + sc] : 0.f; }
; #pragma unroll
;     for (int i = 0; i < 32; ++i) { const int kk = 2 * i + (lane >> 5); const int k = k0 + kk;
;         if (KS) v[i] *= (k < ksplit ? ksA[k] : ksB[k - ksplit]);
;         scr[kk * 33 + (lane & 31)] = v[i]; }
;     LDS_WAIT(); asm volatile("" ::: "memory");
;     const int c = lane & 7;
; #pragma unroll
;     for (int j = 0; j < 4; ++j) { const int n = (lane >> 3) + 8 * j; const LAS float* s = scr + (8 * c) * 33 + n;
;         v4u o; o.x = pk2(s[0 * 33], s[1 * 33]); o.y = pk2(s[2 * 33], s[3 * 33]); o.z = pk2(s[4 * 33], s[5 * 33]); o.w = pk2(s[6 * 33], s[7 * 33]);
;         *(GAS v4u*)(WT + (size_t)(n0 + n) * K + k0 + 8 * c) = o; }
	s_add_i32 s24, s23, 8
	s_lshl_b32 s20, s24, 7
	s_cmp_lt_u32 s24, 40
	s_cselect_b32 s21, 0, 0x830
	s_cmp_lt_u32 s24, 72
	s_cselect_b32 s21, s21, 0xfffff030
	s_add_i32 s20, s20, s21
	s_lshl_b32 s20, s20, 2
	s_add_u32 s8, s50, s20
	s_addc_u32 s9, s51, 0
	global_load_dwordx4 v[144:147], v76, s[8:9]
	s_add_u32 s8, s8, 0x16280
	s_addc_u32 s9, s9, 0
	global_load_dwordx4 v[148:151], v76, s[8:9]
	s_add_u32 s8, s8, 0x16280
	s_addc_u32 s9, s9, 0
	global_load_dwordx4 v[152:155], v76, s[8:9]
	s_add_u32 s8, s8, 0x16280
	s_addc_u32 s9, s9, 0
	global_load_dwordx4 v[156:159], v76, s[8:9]
	s_add_u32 s8, s8, 0x16280
	s_addc_u32 s9, s9, 0
	global_load_dwordx4 v[160:163], v76, s[8:9]
	s_add_u32 s8, s8, 0x16280
	s_addc_u32 s9, s9, 0
	global_load_dwordx4 v[164:167], v76, s[8:9]
	s_add_u32 s8, s8, 0x16280
	s_addc_u32 s9, s9, 0
	global_load_dwordx4 v[168:171], v76, s[8:9]
	s_add_u32 s8, s8, 0x16280
	s_addc_u32 s9, s9, 0
	global_load_dwordx4 v[172:175], v76, s[8:9]
	s_add_i32 s24, s23, 80
	s_mul_i32 s20, s24, 0x100000
	s_add_u32 s6, s48, s20
	s_addc_u32 s7, s49, 0
	s_cmp_lt_u32 s24, 16
	s_cselect_b32 s20, 1, 0
	s_sub_i32 s21, s24, 16
	s_bitcmp0_b32 s21, 2
	s_cselect_b32 s21, 1, 0
	s_cmp_lt_u32 s24, 40
	s_cselect_b32 s21, s21, 0
	s_or_b32 s20, s20, s21
	s_cmp_lg_u32 s20, 0
	s_cselect_b64 s[20:21], -1, 0
	v_cndmask_b32_e64 v91, v83, v87, s[20:21]
	v_cndmask_b32_e64 v92, v84, v88, s[20:21]
	v_cndmask_b32_e64 v93, v85, v89, s[20:21]
	v_cndmask_b32_e64 v94, v86, v90, s[20:21]
	ds_read_b32 v226, v112
	ds_read_b32 v227, v112 offset:512
	ds_read_b32 v228, v112 offset:1024
	ds_read_b32 v229, v112 offset:1536
	ds_read_b32 v230, v112 offset:2048
	ds_read_b32 v231, v112 offset:2560
	ds_read_b32 v232, v112 offset:3072
	ds_read_b32 v233, v112 offset:3584
	s_waitcnt lgkmcnt(0)
	v_bfe_u32 v120, v226, 16, 1
	v_bfe_u32 v121, v227, 16, 1
	v_bfe_u32 v122, v228, 16, 1
	v_bfe_u32 v123, v229, 16, 1
	v_bfe_u32 v124, v230, 16, 1
	v_bfe_u32 v125, v231, 16, 1
	v_bfe_u32 v126, v232, 16, 1
	v_bfe_u32 v127, v233, 16, 1
	v_add3_u32 v226, v226, v120, s63
	v_add3_u32 v227, v227, v121, s63
	v_add3_u32 v228, v228, v122, s63
	v_add3_u32 v229, v229, v123, s63
	v_add3_u32 v230, v230, v124, s63
	v_add3_u32 v231, v231, v125, s63
	v_add3_u32 v232, v232, v126, s63
	v_add3_u32 v233, v233, v127, s63
	v_perm_b32 v242, v227, v226, s64
	v_perm_b32 v243, v229, v228, s64
	v_perm_b32 v244, v231, v230, s64
	v_perm_b32 v245, v233, v232, s64
	s_nop 0
	global_store_dwordx4 v91, v[242:245], s[6:7]
	ds_read_b32 v226, v114
	ds_read_b32 v227, v114 offset:512
	ds_read_b32 v228, v114 offset:1024
	ds_read_b32 v229, v114 offset:1536
	ds_read_b32 v230, v114 offset:2048
	ds_read_b32 v231, v114 offset:2560
	ds_read_b32 v232, v114 offset:3072
	ds_read_b32 v233, v114 offset:3584
	s_waitcnt lgkmcnt(0)
	v_bfe_u32 v120, v226, 16, 1
	v_bfe_u32 v121, v227, 16, 1
	v_bfe_u32 v122, v228, 16, 1
	v_bfe_u32 v123, v229, 16, 1
	v_bfe_u32 v124, v230, 16, 1
	v_bfe_u32 v125, v231, 16, 1
	v_bfe_u32 v126, v232, 16, 1
	v_bfe_u32 v127, v233, 16, 1
	v_add3_u32 v226, v226, v120, s63
	v_add3_u32 v227, v227, v121, s63
	v_add3_u32 v228, v228, v122, s63
	v_add3_u32 v229, v229, v123, s63
	v_add3_u32 v230, v230, v124, s63
	v_add3_u32 v231, v231, v125, s63
	v_add3_u32 v232, v232, v126, s63
	v_add3_u32 v233, v233, v127, s63
	v_perm_b32 v242, v227, v226, s64
	v_perm_b32 v243, v229, v228, s64
	v_perm_b32 v244, v231, v230, s64
	v_perm_b32 v245, v233, v232, s64
	s_nop 0
	global_store_dwordx4 v92, v[242:245], s[6:7]
	ds_read_b32 v226, v116
	ds_read_b32 v227, v116 offset:512
	ds_read_b32 v228, v116 offset:1024
	ds_read_b32 v229, v116 offset:1536
	ds_read_b32 v230, v116 offset:2048
	ds_read_b32 v231, v116 offset:2560
	ds_read_b32 v232, v116 offset:3072
	ds_read_b32 v233, v116 offset:3584
	s_waitcnt lgkmcnt(0)
	v_bfe_u32 v120, v226, 16, 1
	v_bfe_u32 v121, v227, 16, 1
	v_bfe_u32 v122, v228, 16, 1
	v_bfe_u32 v123, v229, 16, 1
	v_bfe_u32 v124, v230, 16, 1
	v_bfe_u32 v125, v231, 16, 1
	v_bfe_u32 v126, v232, 16, 1
	v_bfe_u32 v127, v233, 16, 1
	v_add3_u32 v226, v226, v120, s63
	v_add3_u32 v227, v227, v121, s63
	v_add3_u32 v228, v228, v122, s63
	v_add3_u32 v229, v229, v123, s63
	v_add3_u32 v230, v230, v124, s63
	v_add3_u32 v231, v231, v125, s63
	v_add3_u32 v232, v232, v126, s63
	v_add3_u32 v233, v233, v127, s63
	v_perm_b32 v242, v227, v226, s64
	v_perm_b32 v243, v229, v228, s64
	v_perm_b32 v244, v231, v230, s64
	v_perm_b32 v245, v233, v232, s64
	s_nop 0
	global_store_dwordx4 v93, v[242:245], s[6:7]
	ds_read_b32 v226, v118
	ds_read_b32 v227, v118 offset:512
	ds_read_b32 v228, v118 offset:1024
	ds_read_b32 v229, v118 offset:1536
	ds_read_b32 v230, v118 offset:2048
	ds_read_b32 v231, v118 offset:2560
	ds_read_b32 v232, v118 offset:3072
	ds_read_b32 v233, v118 offset:3584
	s_waitcnt lgkmcnt(0)
	v_bfe_u32 v120, v226, 16, 1
	v_bfe_u32 v121, v227, 16, 1
	v_bfe_u32 v122, v228, 16, 1
	v_bfe_u32 v123, v229, 16, 1
	v_bfe_u32 v124, v230, 16, 1
	v_bfe_u32 v125, v231, 16, 1
	v_bfe_u32 v126, v232, 16, 1
	v_bfe_u32 v127, v233, 16, 1
	v_add3_u32 v226, v226, v120, s63
	v_add3_u32 v227, v227, v121, s63
	v_add3_u32 v228, v228, v122, s63
	v_add3_u32 v229, v229, v123, s63
	v_add3_u32 v230, v230, v124, s63
	v_add3_u32 v231, v231, v125, s63
	v_add3_u32 v232, v232, v126, s63
	v_add3_u32 v233, v233, v127, s63
	v_perm_b32 v242, v227, v226, s64
	v_perm_b32 v243, v229, v228, s64
	v_perm_b32 v244, v231, v230, s64
	v_perm_b32 v245, v233, v232, s64
	s_nop 0
	global_store_dwordx4 v94, v[242:245], s[6:7]
	s_waitcnt vmcnt(16)
	v_mul_f32_e32 v176, v50, v176
	v_mul_f32_e32 v177, v50, v177
	v_mul_f32_e32 v178, v50, v178
	v_mul_f32_e32 v179, v50, v179
	ds_write_b128 v210, v[176:179]
	v_mul_f32_e32 v180, v51, v180
	v_mul_f32_e32 v181, v51, v181
	v_mul_f32_e32 v182, v51, v182
	v_mul_f32_e32 v183, v51, v183
	ds_write_b128 v210, v[180:183] offset:1024
	v_mul_f32_e32 v184, v52, v184
	v_mul_f32_e32 v185, v52, v185
	v_mul_f32_e32 v186, v52, v186
	v_mul_f32_e32 v187, v52, v187
	ds_write_b128 v210, v[184:187] offset:2048
	v_mul_f32_e32 v188, v53, v188
	v_mul_f32_e32 v189, v53, v189
	v_mul_f32_e32 v190, v53, v190
	v_mul_f32_e32 v191, v53, v191
	ds_write_b128 v210, v[188:191] offset:3072
	v_mul_f32_e32 v192, v54, v192
	v_mul_f32_e32 v193, v54, v193
	v_mul_f32_e32 v194, v54, v194
	v_mul_f32_e32 v195, v54, v195
	ds_write_b128 v210, v[192:195] offset:4096
	v_mul_f32_e32 v196, v55, v196
	v_mul_f32_e32 v197, v55, v197
	v_mul_f32_e32 v198, v55, v198
	v_mul_f32_e32 v199, v55, v199
	ds_write_b128 v210, v[196:199] offset:5120
	v_mul_f32_e32 v200, v56, v200
	v_mul_f32_e32 v201, v56, v201
	v_mul_f32_e32 v202, v56, v202
	v_mul_f32_e32 v203, v56, v203
	ds_write_b128 v210, v[200:203] offset:6144
	v_mul_f32_e32 v204, v57, v204
	v_mul_f32_e32 v205, v57, v205
	v_mul_f32_e32 v206, v57, v206
	v_mul_f32_e32 v207, v57, v207
	ds_write_b128 v210, v[204:207] offset:7168
	s_waitcnt lgkmcnt(0)
	s_barrier
; #define GAS __attribute__((address_space(1)))
; #define LAS __attribute__((address_space(3)))
; #define LDS_WAIT() asm volatile("s_waitcnt lgkmcnt(0)" ::: "memory")
; __device__ __forceinline__ int nat_dim(int p) { return (p >> 1) + 64 * (p & 1); }
; template <int MAP, bool KS, bool KPERM = false>
; __device__ __forceinline__ void p0_transpose_item(const float* W, int K, int Nsrc, int nblk, bf16* WT, const float* ksA, const float* ksB, int ksplit, LAS float* scr, int item, int lane) {
;     const int kb = item / nblk, nb = item % nblk, k0 = 64 * kb, n0 = 32 * nb;
;     const int nr = n0 + (lane & 31); const int sc = MAP == 1 ? src_col_in(nr) : (MAP == 2 ? nat_dim(nr) : nr);
;     float v[32];
; #pragma unroll
;     for (int i = 0; i < 32; ++i) { const int k = k0 + 2 * i + (lane >> 5); const int ksrc = KPERM ? ((k & ~127) + nat_dim(k & 127)) : k;
;         v[i] = sc >= 0 ? W[(size_t)ksrc * Nsrc + sc] : 0.f; }
; #pragma unroll
;     for (int i = 0; i < 32; ++i) { const int kk = 2 * i + (lane >> 5); const int k = k0 + kk;
;         if (KS) v[i] *= (k < ksplit ? ksA[k] : ksB[k - ksplit]);
;         scr[kk * 33 + (lane & 31)] = v[i]; }
;     LDS_WAIT(); asm volatile("" ::: "memory");
;     const int pr = item >> 1, kb = 2 * (pr / nblk) + (item & 1), nb = pr % nblk, k0 = 64 * kb, n0 = 32 * nb;
;     const int nr = n0 + (lane & 31); const int sc = MAP == 1 ? src_col_in(nr) : nr;
;     float v[32];
; #pragma unroll
;     for (int i = 0; i < 32; ++i) v[i] = sc >= 0 ? W[(size_t)(k0 + 2 * i + (lane >> 5)) * Nsrc + sc] : 0.f;
; #pragma unroll
;     for (int i = 0; i < 32; ++i) { const int k = k0 + 2 * i + (lane >> 5); float x = v[i] * wscale; if (KS) x *= (k < ksplit ? ksA[k] : ksB[k - ksplit]); scr[(2 * i + (lane >> 5)) * 33 + (lane & 31)] = x; }
;     LDS_WAIT(); asm volatile("" ::: "memory");
;     const int c = lane & 7;
; #pragma unroll
;     for (int j = 0; j < 4; ++j) { const int n = (lane >> 3) + 8 * j; const LAS float* s = scr + (8 * c) * 33 + n;
;         const unsigned long long o = (unsigned long long)pg8::pk4_fp8(s[0 * 33], s[1 * 33], s[2 * 33], s[3 * 33]) | ((unsigned long long)pg8::pk4_fp8(s[4 * 33], s[5 * 33], s[6 * 33], s[7 * 33]) << 32);
;         *(GAS unsigned long long*)(WT + (size_t)(n0 + n) * K + k0 + 8 * c) = o; }
;     LDS_WAIT(); asm volatile("" ::: "memory");
	s_add_i32 s24, s23, 16
	s_lshl_b32 s20, s24, 7
	s_cmp_lt_u32 s24, 40
	s_cselect_b32 s21, 0, 0x830
	s_cmp_lt_u32 s24, 72
	s_cselect_b32 s21, s21, 0xfffff030
	s_add_i32 s20, s20, s21
	s_lshl_b32 s20, s20, 2
	s_add_u32 s8, s50, s20
	s_addc_u32 s9, s51, 0
	global_load_dwordx4 v[176:179], v76, s[8:9]
	s_add_u32 s8, s8, 0x16280
	s_addc_u32 s9, s9, 0
	global_load_dwordx4 v[180:183], v76, s[8:9]
	s_add_u32 s8, s8, 0x16280
	s_addc_u32 s9, s9, 0
	global_load_dwordx4 v[184:187], v76, s[8:9]
	s_add_u32 s8, s8, 0x16280
	s_addc_u32 s9, s9, 0
	global_load_dwordx4 v[188:191], v76, s[8:9]
	s_add_u32 s8, s8, 0x16280
	s_addc_u32 s9, s9, 0
	global_load_dwordx4 v[192:195], v76, s[8:9]
	s_add_u32 s8, s8, 0x16280
	s_addc_u32 s9, s9, 0
	global_load_dwordx4 v[196:199], v76, s[8:9]
	s_add_u32 s8, s8, 0x16280
	s_addc_u32 s9, s9, 0
	global_load_dwordx4 v[200:203], v76, s[8:9]
	s_add_u32 s8, s8, 0x16280
	s_addc_u32 s9, s9, 0
	global_load_dwordx4 v[204:207], v76, s[8:9]
	s_add_i32 s24, s23, 0
	s_mul_i32 s20, s24, 0x80000
	s_add_u32 s6, s52, s20
	s_addc_u32 s7, s53, 0
	s_cmp_lt_u32 s24, 16
	s_cselect_b32 s20, 1, 0
	s_sub_i32 s21, s24, 16
	s_bitcmp0_b32 s21, 2
	s_cselect_b32 s21, 1, 0
	s_cmp_lt_u32 s24, 40
	s_cselect_b32 s21, s21, 0
	s_or_b32 s20, s20, s21
	s_cmp_lg_u32 s20, 0
	s_cselect_b64 s[20:21], -1, 0
	v_cndmask_b32_e64 v91, v77, v81, s[20:21]
	v_cndmask_b32_e64 v92, v78, v82, s[20:21]
	ds_read_b32 v226, v212
	ds_read_b32 v227, v212 offset:512
	ds_read_b32 v228, v212 offset:1024
	ds_read_b32 v229, v212 offset:1536
	ds_read_b32 v230, v212 offset:2048
	ds_read_b32 v231, v212 offset:2560
	ds_read_b32 v232, v212 offset:3072
	ds_read_b32 v233, v212 offset:3584
	ds_read_b32 v234, v212 offset:4096
	ds_read_b32 v235, v212 offset:4608
	ds_read_b32 v236, v212 offset:5120
	ds_read_b32 v237, v212 offset:5632
	ds_read_b32 v238, v212 offset:6144
	ds_read_b32 v239, v212 offset:6656
	ds_read_b32 v240, v212 offset:7168
	ds_read_b32 v241, v212 offset:7680
	s_waitcnt lgkmcnt(0)
	v_max_f32_e32 v226, v226, v226
	v_max_f32_e32 v227, v227, v227
	v_max_f32_e32 v228, v228, v228
	v_max_f32_e32 v229, v229, v229
	v_max_f32_e32 v230, v230, v230
	v_max_f32_e32 v231, v231, v231
	v_max_f32_e32 v232, v232, v232
	v_max_f32_e32 v233, v233, v233
	v_max_f32_e32 v234, v234, v234
	v_max_f32_e32 v235, v235, v235
	v_max_f32_e32 v236, v236, v236
	v_max_f32_e32 v237, v237, v237
	v_max_f32_e32 v238, v238, v238
	v_max_f32_e32 v239, v239, v239
	v_max_f32_e32 v240, v240, v240
	v_max_f32_e32 v241, v241, v241
	v_med3_f32 v226, v226, s62, v95
	v_med3_f32 v227, v227, s62, v95
	v_med3_f32 v228, v228, s62, v95
	v_med3_f32 v229, v229, s62, v95
	v_med3_f32 v230, v230, s62, v95
	v_med3_f32 v231, v231, s62, v95
	v_med3_f32 v232, v232, s62, v95
	v_med3_f32 v233, v233, s62, v95
	v_med3_f32 v234, v234, s62, v95
	v_med3_f32 v235, v235, s62, v95
	v_med3_f32 v236, v236, s62, v95
	v_med3_f32 v237, v237, s62, v95
	v_med3_f32 v238, v238, s62, v95
	v_med3_f32 v239, v239, s62, v95
	v_med3_f32 v240, v240, s62, v95
	v_med3_f32 v241, v241, s62, v95
	v_mov_b32_e32 v242, 0
	v_mov_b32_e32 v243, 0
	v_mov_b32_e32 v244, 0
	v_mov_b32_e32 v245, 0
	v_cvt_pk_fp8_f32 v242, v226, v227
	v_cvt_pk_fp8_f32 v243, v230, v231
	v_cvt_pk_fp8_f32 v244, v234, v235
	v_cvt_pk_fp8_f32 v245, v238, v239
	v_cvt_pk_fp8_f32 v242, v228, v229 op_sel:[0,0,1]
	v_cvt_pk_fp8_f32 v243, v232, v233 op_sel:[0,0,1]
	v_cvt_pk_fp8_f32 v244, v236, v237 op_sel:[0,0,1]
	v_cvt_pk_fp8_f32 v245, v240, v241 op_sel:[0,0,1]
	s_nop 0
	global_store_dwordx4 v91, v[242:245], s[6:7]
	ds_read_b32 v226, v214
	ds_read_b32 v227, v214 offset:512
	ds_read_b32 v228, v214 offset:1024
	ds_read_b32 v229, v214 offset:1536
	ds_read_b32 v230, v214 offset:2048
	ds_read_b32 v231, v214 offset:2560
	ds_read_b32 v232, v214 offset:3072
	ds_read_b32 v233, v214 offset:3584
	ds_read_b32 v234, v214 offset:4096
	ds_read_b32 v235, v214 offset:4608
	ds_read_b32 v236, v214 offset:5120
	ds_read_b32 v237, v214 offset:5632
	ds_read_b32 v238, v214 offset:6144
	ds_read_b32 v239, v214 offset:6656
	ds_read_b32 v240, v214 offset:7168
	ds_read_b32 v241, v214 offset:7680
	s_waitcnt lgkmcnt(0)
	v_max_f32_e32 v226, v226, v226
	v_max_f32_e32 v227, v227, v227
	v_max_f32_e32 v228, v228, v228
	v_max_f32_e32 v229, v229, v229
	v_max_f32_e32 v230, v230, v230
	v_max_f32_e32 v231, v231, v231
	v_max_f32_e32 v232, v232, v232
	v_max_f32_e32 v233, v233, v233
	v_max_f32_e32 v234, v234, v234
	v_max_f32_e32 v235, v235, v235
	v_max_f32_e32 v236, v236, v236
	v_max_f32_e32 v237, v237, v237
	v_max_f32_e32 v238, v238, v238
	v_max_f32_e32 v239, v239, v239
	v_max_f32_e32 v240, v240, v240
	v_max_f32_e32 v241, v241, v241
	v_med3_f32 v226, v226, s62, v95
	v_med3_f32 v227, v227, s62, v95
	v_med3_f32 v228, v228, s62, v95
	v_med3_f32 v229, v229, s62, v95
	v_med3_f32 v230, v230, s62, v95
	v_med3_f32 v231, v231, s62, v95
	v_med3_f32 v232, v232, s62, v95
	v_med3_f32 v233, v233, s62, v95
	v_med3_f32 v234, v234, s62, v95
	v_med3_f32 v235, v235, s62, v95
	v_med3_f32 v236, v236, s62, v95
	v_med3_f32 v237, v237, s62, v95
	v_med3_f32 v238, v238, s62, v95
	v_med3_f32 v239, v239, s62, v95
	v_med3_f32 v240, v240, s62, v95
	v_med3_f32 v241, v241, s62, v95
	v_mov_b32_e32 v242, 0
	v_mov_b32_e32 v243, 0
	v_mov_b32_e32 v244, 0
	v_mov_b32_e32 v245, 0
	v_cvt_pk_fp8_f32 v242, v226, v227
	v_cvt_pk_fp8_f32 v243, v230, v231
	v_cvt_pk_fp8_f32 v244, v234, v235
	v_cvt_pk_fp8_f32 v245, v238, v239
	v_cvt_pk_fp8_f32 v242, v228, v229 op_sel:[0,0,1]
	v_cvt_pk_fp8_f32 v243, v232, v233 op_sel:[0,0,1]
	v_cvt_pk_fp8_f32 v244, v236, v237 op_sel:[0,0,1]
	v_cvt_pk_fp8_f32 v245, v240, v241 op_sel:[0,0,1]
	s_nop 0
	global_store_dwordx4 v92, v[242:245], s[6:7]
	s_waitcnt vmcnt(14)
	v_mul_f32_e32 v144, v50, v144
	v_mul_f32_e32 v145, v50, v145
	v_mul_f32_e32 v146, v50, v146
	v_mul_f32_e32 v147, v50, v147
	ds_write_b128 v209, v[144:147]
	v_mul_f32_e32 v148, v51, v148
	v_mul_f32_e32 v149, v51, v149
	v_mul_f32_e32 v150, v51, v150
	v_mul_f32_e32 v151, v51, v151
	ds_write_b128 v209, v[148:151] offset:1024
	v_mul_f32_e32 v152, v52, v152
	v_mul_f32_e32 v153, v52, v153
	v_mul_f32_e32 v154, v52, v154
	v_mul_f32_e32 v155, v52, v155
	ds_write_b128 v209, v[152:155] offset:2048
	v_mul_f32_e32 v156, v53, v156
	v_mul_f32_e32 v157, v53, v157
	v_mul_f32_e32 v158, v53, v158
	v_mul_f32_e32 v159, v53, v159
	ds_write_b128 v209, v[156:159] offset:3072
	v_mul_f32_e32 v160, v54, v160
	v_mul_f32_e32 v161, v54, v161
	v_mul_f32_e32 v162, v54, v162
	v_mul_f32_e32 v163, v54, v163
	ds_write_b128 v209, v[160:163] offset:4096
	v_mul_f32_e32 v164, v55, v164
	v_mul_f32_e32 v165, v55, v165
	v_mul_f32_e32 v166, v55, v166
	v_mul_f32_e32 v167, v55, v167
	ds_write_b128 v209, v[164:167] offset:5120
	v_mul_f32_e32 v168, v56, v168
	v_mul_f32_e32 v169, v56, v169
	v_mul_f32_e32 v170, v56, v170
	v_mul_f32_e32 v171, v56, v171
	ds_write_b128 v209, v[168:171] offset:6144
	v_mul_f32_e32 v172, v57, v172
	v_mul_f32_e32 v173, v57, v173
	v_mul_f32_e32 v174, v57, v174
	v_mul_f32_e32 v175, v57, v175
	ds_write_b128 v209, v[172:175] offset:7168
	s_waitcnt lgkmcnt(0)
	s_barrier
; #define GAS __attribute__((address_space(1)))
; #define LAS __attribute__((address_space(3)))
; #define LDS_WAIT() asm volatile("s_waitcnt lgkmcnt(0)" ::: "memory")
; __device__ __forceinline__ int nat_dim(int p) { return (p >> 1) + 64 * (p & 1); }
; template <int MAP, bool KS, bool KPERM = false>
; __device__ __forceinline__ void p0_transpose_item(const float* W, int K, int Nsrc, int nblk, bf16* WT, const float* ksA, const float* ksB, int ksplit, LAS float* scr, int item, int lane) {
;     const int kb = item / nblk, nb = item % nblk, k0 = 64 * kb, n0 = 32 * nb;
;     const int nr = n0 + (lane & 31); const int sc = MAP == 1 ? src_col_in(nr) : (MAP == 2 ? nat_dim(nr) : nr);
;     float v[32];
; #pragma unroll
;     for (int i = 0; i < 32; ++i) { const int k = k0 + 2 * i + (lane >> 5); const int ksrc = KPERM ? ((k & ~127) + nat_dim(k & 127)) : k;
;         v[i] = sc >= 0 ? W[(size_t)ksrc * Nsrc + sc] : 0.f; }
; #pragma unroll
;     for (int i = 0; i < 32; ++i) { const int kk = 2 * i + (lane >> 5); const int k = k0 + kk;
;         if (KS) v[i] *= (k < ksplit ? ksA[k] : ksB[k - ksplit]);
;         scr[kk * 33 + (lane & 31)] = v[i]; }
;     LDS_WAIT(); asm volatile("" ::: "memory");
;     const int pr = item >> 1, kb = 2 * (pr / nblk) + (item & 1), nb = pr % nblk, k0 = 64 * kb, n0 = 32 * nb;
;     const int nr = n0 + (lane & 31); const int sc = MAP == 1 ? src_col_in(nr) : nr;
;     float v[32];
; #pragma unroll
;     for (int i = 0; i < 32; ++i) v[i] = sc >= 0 ? W[(size_t)(k0 + 2 * i + (lane >> 5)) * Nsrc + sc] : 0.f;
; #pragma unroll
;     for (int i = 0; i < 32; ++i) { const int k = k0 + 2 * i + (lane >> 5); float x = v[i] * wscale; if (KS) x *= (k < ksplit ? ksA[k] : ksB[k - ksplit]); scr[(2 * i + (lane >> 5)) * 33 + (lane & 31)] = x; }
;     LDS_WAIT(); asm volatile("" ::: "memory");
;     const int c = lane & 7;
; #pragma unroll
;     for (int j = 0; j < 4; ++j) { const int n = (lane >> 3) + 8 * j; const LAS float* s = scr + (8 * c) * 33 + n;
;         const unsigned long long o = (unsigned long long)pg8::pk4_fp8(s[0 * 33], s[1 * 33], s[2 * 33], s[3 * 33]) | ((unsigned long long)pg8::pk4_fp8(s[4 * 33], s[5 * 33], s[6 * 33], s[7 * 33]) << 32);
;         *(GAS unsigned long long*)(WT + (size_t)(n0 + n) * K + k0 + 8 * c) = o; }
;     LDS_WAIT(); asm volatile("" ::: "memory");
	s_add_i32 s24, s23, 24
	s_lshl_b32 s20, s24, 7
	s_cmp_lt_u32 s24, 40
	s_cselect_b32 s21, 0, 0x830
	s_cmp_lt_u32 s24, 72
	s_cselect_b32 s21, s21, 0xfffff030
	s_add_i32 s20, s20, s21
	s_lshl_b32 s20, s20, 2
	s_add_u32 s8, s50, s20
	s_addc_u32 s9, s51, 0
	global_load_dwordx4 v[144:147], v76, s[8:9]
	s_add_u32 s8, s8, 0x16280
	s_addc_u32 s9, s9, 0
	global_load_dwordx4 v[148:151], v76, s[8:9]
	s_add_u32 s8, s8, 0x16280
	s_addc_u32 s9, s9, 0
	global_load_dwordx4 v[152:155], v76, s[8:9]
	s_add_u32 s8, s8, 0x16280
	s_addc_u32 s9, s9, 0
	global_load_dwordx4 v[156:159], v76, s[8:9]
	s_add_u32 s8, s8, 0x16280
	s_addc_u32 s9, s9, 0
	global_load_dwordx4 v[160:163], v76, s[8:9]
	s_add_u32 s8, s8, 0x16280
	s_addc_u32 s9, s9, 0
	global_load_dwordx4 v[164:167], v76, s[8:9]
	s_add_u32 s8, s8, 0x16280
	s_addc_u32 s9, s9, 0
	global_load_dwordx4 v[168:171], v76, s[8:9]
	s_add_u32 s8, s8, 0x16280
	s_addc_u32 s9, s9, 0
	global_load_dwordx4 v[172:175], v76, s[8:9]
	s_add_i32 s24, s23, 8
	s_mul_i32 s20, s24, 0x80000
	s_add_u32 s6, s52, s20
	s_addc_u32 s7, s53, 0
	s_cmp_lt_u32 s24, 16
	s_cselect_b32 s20, 1, 0
	s_sub_i32 s21, s24, 16
	s_bitcmp0_b32 s21, 2
	s_cselect_b32 s21, 1, 0
	s_cmp_lt_u32 s24, 40
	s_cselect_b32 s21, s21, 0
	s_or_b32 s20, s20, s21
	s_cmp_lg_u32 s20, 0
	s_cselect_b64 s[20:21], -1, 0
	v_cndmask_b32_e64 v91, v77, v81, s[20:21]
	v_cndmask_b32_e64 v92, v78, v82, s[20:21]
	ds_read_b32 v226, v211
	ds_read_b32 v227, v211 offset:512
	ds_read_b32 v228, v211 offset:1024
	ds_read_b32 v229, v211 offset:1536
	ds_read_b32 v230, v211 offset:2048
	ds_read_b32 v231, v211 offset:2560
	ds_read_b32 v232, v211 offset:3072
	ds_read_b32 v233, v211 offset:3584
	ds_read_b32 v234, v211 offset:4096
	ds_read_b32 v235, v211 offset:4608
	ds_read_b32 v236, v211 offset:5120
	ds_read_b32 v237, v211 offset:5632
	ds_read_b32 v238, v211 offset:6144
	ds_read_b32 v239, v211 offset:6656
	ds_read_b32 v240, v211 offset:7168
	ds_read_b32 v241, v211 offset:7680
	s_waitcnt lgkmcnt(0)
	v_max_f32_e32 v226, v226, v226
	v_max_f32_e32 v227, v227, v227
	v_max_f32_e32 v228, v228, v228
	v_max_f32_e32 v229, v229, v229
	v_max_f32_e32 v230, v230, v230
	v_max_f32_e32 v231, v231, v231
	v_max_f32_e32 v232, v232, v232
	v_max_f32_e32 v233, v233, v233
	v_max_f32_e32 v234, v234, v234
	v_max_f32_e32 v235, v235, v235
	v_max_f32_e32 v236, v236, v236
	v_max_f32_e32 v237, v237, v237
	v_max_f32_e32 v238, v238, v238
	v_max_f32_e32 v239, v239, v239
	v_max_f32_e32 v240, v240, v240
	v_max_f32_e32 v241, v241, v241
	v_med3_f32 v226, v226, s62, v95
	v_med3_f32 v227, v227, s62, v95
	v_med3_f32 v228, v228, s62, v95
	v_med3_f32 v229, v229, s62, v95
	v_med3_f32 v230, v230, s62, v95
	v_med3_f32 v231, v231, s62, v95
	v_med3_f32 v232, v232, s62, v95
	v_med3_f32 v233, v233, s62, v95
	v_med3_f32 v234, v234, s62, v95
	v_med3_f32 v235, v235, s62, v95
	v_med3_f32 v236, v236, s62, v95
	v_med3_f32 v237, v237, s62, v95
	v_med3_f32 v238, v238, s62, v95
	v_med3_f32 v239, v239, s62, v95
	v_med3_f32 v240, v240, s62, v95
	v_med3_f32 v241, v241, s62, v95
	v_mov_b32_e32 v242, 0
	v_mov_b32_e32 v243, 0
	v_mov_b32_e32 v244, 0
	v_mov_b32_e32 v245, 0
	v_cvt_pk_fp8_f32 v242, v226, v227
	v_cvt_pk_fp8_f32 v243, v230, v231
	v_cvt_pk_fp8_f32 v244, v234, v235
	v_cvt_pk_fp8_f32 v245, v238, v239
	v_cvt_pk_fp8_f32 v242, v228, v229 op_sel:[0,0,1]
	v_cvt_pk_fp8_f32 v243, v232, v233 op_sel:[0,0,1]
	v_cvt_pk_fp8_f32 v244, v236, v237 op_sel:[0,0,1]
	v_cvt_pk_fp8_f32 v245, v240, v241 op_sel:[0,0,1]
	s_nop 0
	global_store_dwordx4 v91, v[242:245], s[6:7]
	ds_read_b32 v226, v213
	ds_read_b32 v227, v213 offset:512
	ds_read_b32 v228, v213 offset:1024
	ds_read_b32 v229, v213 offset:1536
	ds_read_b32 v230, v213 offset:2048
	ds_read_b32 v231, v213 offset:2560
	ds_read_b32 v232, v213 offset:3072
	ds_read_b32 v233, v213 offset:3584
	ds_read_b32 v234, v213 offset:4096
	ds_read_b32 v235, v213 offset:4608
	ds_read_b32 v236, v213 offset:5120
	ds_read_b32 v237, v213 offset:5632
	ds_read_b32 v238, v213 offset:6144
	ds_read_b32 v239, v213 offset:6656
	ds_read_b32 v240, v213 offset:7168
	ds_read_b32 v241, v213 offset:7680
	s_waitcnt lgkmcnt(0)
	v_max_f32_e32 v226, v226, v226
	v_max_f32_e32 v227, v227, v227
	v_max_f32_e32 v228, v228, v228
	v_max_f32_e32 v229, v229, v229
	v_max_f32_e32 v230, v230, v230
	v_max_f32_e32 v231, v231, v231
	v_max_f32_e32 v232, v232, v232
	v_max_f32_e32 v233, v233, v233
	v_max_f32_e32 v234, v234, v234
	v_max_f32_e32 v235, v235, v235
	v_max_f32_e32 v236, v236, v236
	v_max_f32_e32 v237, v237, v237
	v_max_f32_e32 v238, v238, v238
	v_max_f32_e32 v239, v239, v239
	v_max_f32_e32 v240, v240, v240
	v_max_f32_e32 v241, v241, v241
	v_med3_f32 v226, v226, s62, v95
	v_med3_f32 v227, v227, s62, v95
	v_med3_f32 v228, v228, s62, v95
	v_med3_f32 v229, v229, s62, v95
	v_med3_f32 v230, v230, s62, v95
	v_med3_f32 v231, v231, s62, v95
	v_med3_f32 v232, v232, s62, v95
	v_med3_f32 v233, v233, s62, v95
	v_med3_f32 v234, v234, s62, v95
	v_med3_f32 v235, v235, s62, v95
	v_med3_f32 v236, v236, s62, v95
	v_med3_f32 v237, v237, s62, v95
	v_med3_f32 v238, v238, s62, v95
	v_med3_f32 v239, v239, s62, v95
	v_med3_f32 v240, v240, s62, v95
	v_med3_f32 v241, v241, s62, v95
	v_mov_b32_e32 v242, 0
	v_mov_b32_e32 v243, 0
	v_mov_b32_e32 v244, 0
	v_mov_b32_e32 v245, 0
	v_cvt_pk_fp8_f32 v242, v226, v227
	v_cvt_pk_fp8_f32 v243, v230, v231
	v_cvt_pk_fp8_f32 v244, v234, v235
	v_cvt_pk_fp8_f32 v245, v238, v239
	v_cvt_pk_fp8_f32 v242, v228, v229 op_sel:[0,0,1]
	v_cvt_pk_fp8_f32 v243, v232, v233 op_sel:[0,0,1]
	v_cvt_pk_fp8_f32 v244, v236, v237 op_sel:[0,0,1]
	v_cvt_pk_fp8_f32 v245, v240, v241 op_sel:[0,0,1]
	s_nop 0
	global_store_dwordx4 v92, v[242:245], s[6:7]
	s_waitcnt vmcnt(12)
	v_mul_f32_e32 v176, v50, v176
	v_mul_f32_e32 v177, v50, v177
	v_mul_f32_e32 v178, v50, v178
	v_mul_f32_e32 v179, v50, v179
	ds_write_b128 v210, v[176:179]
	v_mul_f32_e32 v180, v51, v180
	v_mul_f32_e32 v181, v51, v181
	v_mul_f32_e32 v182, v51, v182
	v_mul_f32_e32 v183, v51, v183
	ds_write_b128 v210, v[180:183] offset:1024
	v_mul_f32_e32 v184, v52, v184
	v_mul_f32_e32 v185, v52, v185
	v_mul_f32_e32 v186, v52, v186
	v_mul_f32_e32 v187, v52, v187
	ds_write_b128 v210, v[184:187] offset:2048
	v_mul_f32_e32 v188, v53, v188
	v_mul_f32_e32 v189, v53, v189
	v_mul_f32_e32 v190, v53, v190
	v_mul_f32_e32 v191, v53, v191
	ds_write_b128 v210, v[188:191] offset:3072
	v_mul_f32_e32 v192, v54, v192
	v_mul_f32_e32 v193, v54, v193
	v_mul_f32_e32 v194, v54, v194
	v_mul_f32_e32 v195, v54, v195
	ds_write_b128 v210, v[192:195] offset:4096
	v_mul_f32_e32 v196, v55, v196
	v_mul_f32_e32 v197, v55, v197
	v_mul_f32_e32 v198, v55, v198
	v_mul_f32_e32 v199, v55, v199
	ds_write_b128 v210, v[196:199] offset:5120
	v_mul_f32_e32 v200, v56, v200
	v_mul_f32_e32 v201, v56, v201
	v_mul_f32_e32 v202, v56, v202
	v_mul_f32_e32 v203, v56, v203
	ds_write_b128 v210, v[200:203] offset:6144
	v_mul_f32_e32 v204, v57, v204
	v_mul_f32_e32 v205, v57, v205
	v_mul_f32_e32 v206, v57, v206
	v_mul_f32_e32 v207, v57, v207
	ds_write_b128 v210, v[204:207] offset:7168
	s_waitcnt lgkmcnt(0)
	s_barrier
; #define GAS __attribute__((address_space(1)))
; #define LAS __attribute__((address_space(3)))
; #define LDS_WAIT() asm volatile("s_waitcnt lgkmcnt(0)" ::: "memory")
; __device__ __forceinline__ int nat_dim(int p) { return (p >> 1) + 64 * (p & 1); }
; template <int MAP, bool KS, bool KPERM = false>
; __device__ __forceinline__ void p0_transpose_item(const float* W, int K, int Nsrc, int nblk, bf16* WT, const float* ksA, const float* ksB, int ksplit, LAS float* scr, int item, int lane) {
;     const int kb = item / nblk, nb = item % nblk, k0 = 64 * kb, n0 = 32 * nb;
;     const int nr = n0 + (lane & 31); const int sc = MAP == 1 ? src_col_in(nr) : (MAP == 2 ? nat_dim(nr) : nr);
;     float v[32];
; #pragma unroll
;     for (int i = 0; i < 32; ++i) { const int k = k0 + 2 * i + (lane >> 5); const int ksrc = KPERM ? ((k & ~127) + nat_dim(k & 127)) : k;
;         v[i] = sc >= 0 ? W[(size_t)ksrc * Nsrc + sc] : 0.f; }
; #pragma unroll
;     for (int i = 0; i < 32; ++i) { const int kk = 2 * i + (lane >> 5); const int k = k0 + kk;
;         if (KS) v[i] *= (k < ksplit ? ksA[k] : ksB[k - ksplit]);
;         scr[kk * 33 + (lane & 31)] = v[i]; }
;     LDS_WAIT(); asm volatile("" ::: "memory");
;     const int pr = item >> 1, kb = 2 * (pr / nblk) + (item & 1), nb = pr % nblk, k0 = 64 * kb, n0 = 32 * nb;
;     const int nr = n0 + (lane & 31); const int sc = MAP == 1 ? src_col_in(nr) : nr;
;     float v[32];
; #pragma unroll
;     for (int i = 0; i < 32; ++i) v[i] = sc >= 0 ? W[(size_t)(k0 + 2 * i + (lane >> 5)) * Nsrc + sc] : 0.f;
; #pragma unroll
;     for (int i = 0; i < 32; ++i) { const int k = k0 + 2 * i + (lane >> 5); float x = v[i] * wscale; if (KS) x *= (k < ksplit ? ksA[k] : ksB[k - ksplit]); scr[(2 * i + (lane >> 5)) * 33 + (lane & 31)] = x; }
;     LDS_WAIT(); asm volatile("" ::: "memory");
;     const int c = lane & 7;
; #pragma unroll
;     for (int j = 0; j < 4; ++j) { const int n = (lane >> 3) + 8 * j; const LAS float* s = scr + (8 * c) * 33 + n;
;         const unsigned long long o = (unsigned long long)pg8::pk4_fp8(s[0 * 33], s[1 * 33], s[2 * 33], s[3 * 33]) | ((unsigned long long)pg8::pk4_fp8(s[4 * 33], s[5 * 33], s[6 * 33], s[7 * 33]) << 32);
;         *(GAS unsigned long long*)(WT + (size_t)(n0 + n) * K + k0 + 8 * c) = o; }
;     LDS_WAIT(); asm volatile("" ::: "memory");
	s_add_i32 s24, s23, 32
	s_lshl_b32 s20, s24, 7
	s_cmp_lt_u32 s24, 40
	s_cselect_b32 s21, 0, 0x830
	s_cmp_lt_u32 s24, 72
	s_cselect_b32 s21, s21, 0xfffff030
	s_add_i32 s20, s20, s21
	s_lshl_b32 s20, s20, 2
	s_add_u32 s8, s50, s20
	s_addc_u32 s9, s51, 0
	global_load_dwordx4 v[176:179], v76, s[8:9]
	s_add_u32 s8, s8, 0x16280
	s_addc_u32 s9, s9, 0
	global_load_dwordx4 v[180:183], v76, s[8:9]
	s_add_u32 s8, s8, 0x16280
	s_addc_u32 s9, s9, 0
	global_load_dwordx4 v[184:187], v76, s[8:9]
	s_add_u32 s8, s8, 0x16280
	s_addc_u32 s9, s9, 0
	global_load_dwordx4 v[188:191], v76, s[8:9]
	s_add_u32 s8, s8, 0x16280
	s_addc_u32 s9, s9, 0
	global_load_dwordx4 v[192:195], v76, s[8:9]
	s_add_u32 s8, s8, 0x16280
	s_addc_u32 s9, s9, 0
	global_load_dwordx4 v[196:199], v76, s[8:9]
	s_add_u32 s8, s8, 0x16280
	s_addc_u32 s9, s9, 0
	global_load_dwordx4 v[200:203], v76, s[8:9]
	s_add_u32 s8, s8, 0x16280
	s_addc_u32 s9, s9, 0
	global_load_dwordx4 v[204:207], v76, s[8:9]
	s_add_i32 s24, s23, 16
	s_mul_i32 s20, s24, 0x80000
	s_add_u32 s6, s52, s20
	s_addc_u32 s7, s53, 0
	s_cmp_lt_u32 s24, 16
	s_cselect_b32 s20, 1, 0
	s_sub_i32 s21, s24, 16
	s_bitcmp0_b32 s21, 2
	s_cselect_b32 s21, 1, 0
	s_cmp_lt_u32 s24, 40
	s_cselect_b32 s21, s21, 0
	s_or_b32 s20, s20, s21
	s_cmp_lg_u32 s20, 0
	s_cselect_b64 s[20:21], -1, 0
	v_cndmask_b32_e64 v91, v77, v81, s[20:21]
	v_cndmask_b32_e64 v92, v78, v82, s[20:21]
	ds_read_b32 v226, v212
	ds_read_b32 v227, v212 offset:512
	ds_read_b32 v228, v212 offset:1024
	ds_read_b32 v229, v212 offset:1536
	ds_read_b32 v230, v212 offset:2048
	ds_read_b32 v231, v212 offset:2560
	ds_read_b32 v232, v212 offset:3072
	ds_read_b32 v233, v212 offset:3584
	ds_read_b32 v234, v212 offset:4096
	ds_read_b32 v235, v212 offset:4608
	ds_read_b32 v236, v212 offset:5120
	ds_read_b32 v237, v212 offset:5632
	ds_read_b32 v238, v212 offset:6144
	ds_read_b32 v239, v212 offset:6656
	ds_read_b32 v240, v212 offset:7168
	ds_read_b32 v241, v212 offset:7680
	s_waitcnt lgkmcnt(0)
	v_max_f32_e32 v226, v226, v226
	v_max_f32_e32 v227, v227, v227
	v_max_f32_e32 v228, v228, v228
	v_max_f32_e32 v229, v229, v229
	v_max_f32_e32 v230, v230, v230
	v_max_f32_e32 v231, v231, v231
	v_max_f32_e32 v232, v232, v232
	v_max_f32_e32 v233, v233, v233
	v_max_f32_e32 v234, v234, v234
	v_max_f32_e32 v235, v235, v235
	v_max_f32_e32 v236, v236, v236
	v_max_f32_e32 v237, v237, v237
	v_max_f32_e32 v238, v238, v238
	v_max_f32_e32 v239, v239, v239
	v_max_f32_e32 v240, v240, v240
	v_max_f32_e32 v241, v241, v241
	v_med3_f32 v226, v226, s62, v95
	v_med3_f32 v227, v227, s62, v95
	v_med3_f32 v228, v228, s62, v95
	v_med3_f32 v229, v229, s62, v95
	v_med3_f32 v230, v230, s62, v95
	v_med3_f32 v231, v231, s62, v95
	v_med3_f32 v232, v232, s62, v95
	v_med3_f32 v233, v233, s62, v95
	v_med3_f32 v234, v234, s62, v95
	v_med3_f32 v235, v235, s62, v95
	v_med3_f32 v236, v236, s62, v95
	v_med3_f32 v237, v237, s62, v95
	v_med3_f32 v238, v238, s62, v95
	v_med3_f32 v239, v239, s62, v95
	v_med3_f32 v240, v240, s62, v95
	v_med3_f32 v241, v241, s62, v95
	v_mov_b32_e32 v242, 0
	v_mov_b32_e32 v243, 0
	v_mov_b32_e32 v244, 0
	v_mov_b32_e32 v245, 0
	v_cvt_pk_fp8_f32 v242, v226, v227
	v_cvt_pk_fp8_f32 v243, v230, v231
	v_cvt_pk_fp8_f32 v244, v234, v235
	v_cvt_pk_fp8_f32 v245, v238, v239
	v_cvt_pk_fp8_f32 v242, v228, v229 op_sel:[0,0,1]
	v_cvt_pk_fp8_f32 v243, v232, v233 op_sel:[0,0,1]
	v_cvt_pk_fp8_f32 v244, v236, v237 op_sel:[0,0,1]
	v_cvt_pk_fp8_f32 v245, v240, v241 op_sel:[0,0,1]
	s_nop 0
	global_store_dwordx4 v91, v[242:245], s[6:7]
	ds_read_b32 v226, v214
	ds_read_b32 v227, v214 offset:512
	ds_read_b32 v228, v214 offset:1024
	ds_read_b32 v229, v214 offset:1536
	ds_read_b32 v230, v214 offset:2048
	ds_read_b32 v231, v214 offset:2560
	ds_read_b32 v232, v214 offset:3072
	ds_read_b32 v233, v214 offset:3584
	ds_read_b32 v234, v214 offset:4096
	ds_read_b32 v235, v214 offset:4608
	ds_read_b32 v236, v214 offset:5120
	ds_read_b32 v237, v214 offset:5632
	ds_read_b32 v238, v214 offset:6144
	ds_read_b32 v239, v214 offset:6656
	ds_read_b32 v240, v214 offset:7168
	ds_read_b32 v241, v214 offset:7680
	s_waitcnt lgkmcnt(0)
	v_max_f32_e32 v226, v226, v226
	v_max_f32_e32 v227, v227, v227
	v_max_f32_e32 v228, v228, v228
	v_max_f32_e32 v229, v229, v229
	v_max_f32_e32 v230, v230, v230
	v_max_f32_e32 v231, v231, v231
	v_max_f32_e32 v232, v232, v232
	v_max_f32_e32 v233, v233, v233
	v_max_f32_e32 v234, v234, v234
	v_max_f32_e32 v235, v235, v235
	v_max_f32_e32 v236, v236, v236
	v_max_f32_e32 v237, v237, v237
	v_max_f32_e32 v238, v238, v238
	v_max_f32_e32 v239, v239, v239
	v_max_f32_e32 v240, v240, v240
	v_max_f32_e32 v241, v241, v241
	v_med3_f32 v226, v226, s62, v95
	v_med3_f32 v227, v227, s62, v95
	v_med3_f32 v228, v228, s62, v95
	v_med3_f32 v229, v229, s62, v95
	v_med3_f32 v230, v230, s62, v95
	v_med3_f32 v231, v231, s62, v95
	v_med3_f32 v232, v232, s62, v95
	v_med3_f32 v233, v233, s62, v95
	v_med3_f32 v234, v234, s62, v95
	v_med3_f32 v235, v235, s62, v95
	v_med3_f32 v236, v236, s62, v95
	v_med3_f32 v237, v237, s62, v95
	v_med3_f32 v238, v238, s62, v95
	v_med3_f32 v239, v239, s62, v95
	v_med3_f32 v240, v240, s62, v95
	v_med3_f32 v241, v241, s62, v95
	v_mov_b32_e32 v242, 0
	v_mov_b32_e32 v243, 0
	v_mov_b32_e32 v244, 0
	v_mov_b32_e32 v245, 0
	v_cvt_pk_fp8_f32 v242, v226, v227
	v_cvt_pk_fp8_f32 v243, v230, v231
	v_cvt_pk_fp8_f32 v244, v234, v235
	v_cvt_pk_fp8_f32 v245, v238, v239
	v_cvt_pk_fp8_f32 v242, v228, v229 op_sel:[0,0,1]
	v_cvt_pk_fp8_f32 v243, v232, v233 op_sel:[0,0,1]
	v_cvt_pk_fp8_f32 v244, v236, v237 op_sel:[0,0,1]
	v_cvt_pk_fp8_f32 v245, v240, v241 op_sel:[0,0,1]
	s_nop 0
	global_store_dwordx4 v92, v[242:245], s[6:7]
	s_waitcnt vmcnt(12)
	v_mul_f32_e32 v144, v50, v144
	v_mul_f32_e32 v145, v50, v145
	v_mul_f32_e32 v146, v50, v146
	v_mul_f32_e32 v147, v50, v147
	ds_write_b128 v209, v[144:147]
	v_mul_f32_e32 v148, v51, v148
	v_mul_f32_e32 v149, v51, v149
	v_mul_f32_e32 v150, v51, v150
	v_mul_f32_e32 v151, v51, v151
	ds_write_b128 v209, v[148:151] offset:1024
	v_mul_f32_e32 v152, v52, v152
	v_mul_f32_e32 v153, v52, v153
	v_mul_f32_e32 v154, v52, v154
	v_mul_f32_e32 v155, v52, v155
	ds_write_b128 v209, v[152:155] offset:2048
	v_mul_f32_e32 v156, v53, v156
	v_mul_f32_e32 v157, v53, v157
	v_mul_f32_e32 v158, v53, v158
	v_mul_f32_e32 v159, v53, v159
	ds_write_b128 v209, v[156:159] offset:3072
	v_mul_f32_e32 v160, v54, v160
	v_mul_f32_e32 v161, v54, v161
	v_mul_f32_e32 v162, v54, v162
	v_mul_f32_e32 v163, v54, v163
	ds_write_b128 v209, v[160:163] offset:4096
	v_mul_f32_e32 v164, v55, v164
	v_mul_f32_e32 v165, v55, v165
	v_mul_f32_e32 v166, v55, v166
	v_mul_f32_e32 v167, v55, v167
	ds_write_b128 v209, v[164:167] offset:5120
	v_mul_f32_e32 v168, v56, v168
	v_mul_f32_e32 v169, v56, v169
	v_mul_f32_e32 v170, v56, v170
	v_mul_f32_e32 v171, v56, v171
	ds_write_b128 v209, v[168:171] offset:6144
	v_mul_f32_e32 v172, v57, v172
	v_mul_f32_e32 v173, v57, v173
	v_mul_f32_e32 v174, v57, v174
	v_mul_f32_e32 v175, v57, v175
	ds_write_b128 v209, v[172:175] offset:7168
	s_waitcnt lgkmcnt(0)
	s_barrier
; #define GAS __attribute__((address_space(1)))
; #define LAS __attribute__((address_space(3)))
; #define LDS_WAIT() asm volatile("s_waitcnt lgkmcnt(0)" ::: "memory")
; __device__ __forceinline__ int nat_dim(int p) { return (p >> 1) + 64 * (p & 1); }
; template <int MAP, bool KS, bool KPERM = false>
; __device__ __forceinline__ void p0_transpose_item(const float* W, int K, int Nsrc, int nblk, bf16* WT, const float* ksA, const float* ksB, int ksplit, LAS float* scr, int item, int lane) {
;     const int kb = item / nblk, nb = item % nblk, k0 = 64 * kb, n0 = 32 * nb;
;     const int nr = n0 + (lane & 31); const int sc = MAP == 1 ? src_col_in(nr) : (MAP == 2 ? nat_dim(nr) : nr);
;     float v[32];
; #pragma unroll
;     for (int i = 0; i < 32; ++i) { const int k = k0 + 2 * i + (lane >> 5); const int ksrc = KPERM ? ((k & ~127) + nat_dim(k & 127)) : k;
;         v[i] = sc >= 0 ? W[(size_t)ksrc * Nsrc + sc] : 0.f; }
; #pragma unroll
;     for (int i = 0; i < 32; ++i) { const int kk = 2 * i + (lane >> 5); const int k = k0 + kk;
;         if (KS) v[i] *= (k < ksplit ? ksA[k] : ksB[k - ksplit]);
;         scr[kk * 33 + (lane & 31)] = v[i]; }
;     LDS_WAIT(); asm volatile("" ::: "memory");
;     const int pr = item >> 1, kb = 2 * (pr / nblk) + (item & 1), nb = pr % nblk, k0 = 64 * kb, n0 = 32 * nb;
;     const int nr = n0 + (lane & 31); const int sc = MAP == 1 ? src_col_in(nr) : nr;
;     float v[32];
; #pragma unroll
;     for (int i = 0; i < 32; ++i) v[i] = sc >= 0 ? W[(size_t)(k0 + 2 * i + (lane >> 5)) * Nsrc + sc] : 0.f;
; #pragma unroll
;     for (int i = 0; i < 32; ++i) { const int k = k0 + 2 * i + (lane >> 5); float x = v[i] * wscale; if (KS) x *= (k < ksplit ? ksA[k] : ksB[k - ksplit]); scr[(2 * i + (lane >> 5)) * 33 + (lane & 31)] = x; }
;     LDS_WAIT(); asm volatile("" ::: "memory");
;     const int c = lane & 7;
; #pragma unroll
;     for (int j = 0; j < 4; ++j) { const int n = (lane >> 3) + 8 * j; const LAS float* s = scr + (8 * c) * 33 + n;
;         const unsigned long long o = (unsigned long long)pg8::pk4_fp8(s[0 * 33], s[1 * 33], s[2 * 33], s[3 * 33]) | ((unsigned long long)pg8::pk4_fp8(s[4 * 33], s[5 * 33], s[6 * 33], s[7 * 33]) << 32);
;         *(GAS unsigned long long*)(WT + (size_t)(n0 + n) * K + k0 + 8 * c) = o; }
;     LDS_WAIT(); asm volatile("" ::: "memory");
	s_add_i32 s24, s23, 40
	s_lshl_b32 s20, s24, 7
	s_cmp_lt_u32 s24, 40
	s_cselect_b32 s21, 0, 0x830
	s_cmp_lt_u32 s24, 72
	s_cselect_b32 s21, s21, 0xfffff030
	s_add_i32 s20, s20, s21
	s_lshl_b32 s20, s20, 2
	s_add_u32 s8, s50, s20
	s_addc_u32 s9, s51, 0
	global_load_dwordx4 v[144:147], v76, s[8:9]
	s_add_u32 s8, s8, 0x16280
	s_addc_u32 s9, s9, 0
	global_load_dwordx4 v[148:151], v76, s[8:9]
	s_add_u32 s8, s8, 0x16280
	s_addc_u32 s9, s9, 0
	global_load_dwordx4 v[152:155], v76, s[8:9]
	s_add_u32 s8, s8, 0x16280
	s_addc_u32 s9, s9, 0
	global_load_dwordx4 v[156:159], v76, s[8:9]
	s_add_u32 s8, s8, 0x16280
	s_addc_u32 s9, s9, 0
	global_load_dwordx4 v[160:163], v76, s[8:9]
	s_add_u32 s8, s8, 0x16280
	s_addc_u32 s9, s9, 0
	global_load_dwordx4 v[164:167], v76, s[8:9]
	s_add_u32 s8, s8, 0x16280
	s_addc_u32 s9, s9, 0
	global_load_dwordx4 v[168:171], v76, s[8:9]
	s_add_u32 s8, s8, 0x16280
	s_addc_u32 s9, s9, 0
	global_load_dwordx4 v[172:175], v76, s[8:9]
	s_add_i32 s24, s23, 24
	s_mul_i32 s20, s24, 0x80000
	s_add_u32 s6, s52, s20
	s_addc_u32 s7, s53, 0
	s_cmp_lt_u32 s24, 16
	s_cselect_b32 s20, 1, 0
	s_sub_i32 s21, s24, 16
	s_bitcmp0_b32 s21, 2
	s_cselect_b32 s21, 1, 0
	s_cmp_lt_u32 s24, 40
	s_cselect_b32 s21, s21, 0
	s_or_b32 s20, s20, s21
	s_cmp_lg_u32 s20, 0
	s_cselect_b64 s[20:21], -1, 0
	v_cndmask_b32_e64 v91, v77, v81, s[20:21]
	v_cndmask_b32_e64 v92, v78, v82, s[20:21]
	ds_read_b32 v226, v211
	ds_read_b32 v227, v211 offset:512
	ds_read_b32 v228, v211 offset:1024
	ds_read_b32 v229, v211 offset:1536
	ds_read_b32 v230, v211 offset:2048
	ds_read_b32 v231, v211 offset:2560
	ds_read_b32 v232, v211 offset:3072
	ds_read_b32 v233, v211 offset:3584
	ds_read_b32 v234, v211 offset:4096
	ds_read_b32 v235, v211 offset:4608
	ds_read_b32 v236, v211 offset:5120
	ds_read_b32 v237, v211 offset:5632
	ds_read_b32 v238, v211 offset:6144
	ds_read_b32 v239, v211 offset:6656
	ds_read_b32 v240, v211 offset:7168
	ds_read_b32 v241, v211 offset:7680
	s_waitcnt lgkmcnt(0)
	v_max_f32_e32 v226, v226, v226
	v_max_f32_e32 v227, v227, v227
	v_max_f32_e32 v228, v228, v228
	v_max_f32_e32 v229, v229, v229
	v_max_f32_e32 v230, v230, v230
	v_max_f32_e32 v231, v231, v231
	v_max_f32_e32 v232, v232, v232
	v_max_f32_e32 v233, v233, v233
	v_max_f32_e32 v234, v234, v234
	v_max_f32_e32 v235, v235, v235
	v_max_f32_e32 v236, v236, v236
	v_max_f32_e32 v237, v237, v237
	v_max_f32_e32 v238, v238, v238
	v_max_f32_e32 v239, v239, v239
	v_max_f32_e32 v240, v240, v240
	v_max_f32_e32 v241, v241, v241
	v_med3_f32 v226, v226, s62, v95
	v_med3_f32 v227, v227, s62, v95
	v_med3_f32 v228, v228, s62, v95
	v_med3_f32 v229, v229, s62, v95
	v_med3_f32 v230, v230, s62, v95
	v_med3_f32 v231, v231, s62, v95
	v_med3_f32 v232, v232, s62, v95
	v_med3_f32 v233, v233, s62, v95
	v_med3_f32 v234, v234, s62, v95
	v_med3_f32 v235, v235, s62, v95
	v_med3_f32 v236, v236, s62, v95
	v_med3_f32 v237, v237, s62, v95
	v_med3_f32 v238, v238, s62, v95
	v_med3_f32 v239, v239, s62, v95
	v_med3_f32 v240, v240, s62, v95
	v_med3_f32 v241, v241, s62, v95
	v_mov_b32_e32 v242, 0
	v_mov_b32_e32 v243, 0
	v_mov_b32_e32 v244, 0
	v_mov_b32_e32 v245, 0
	v_cvt_pk_fp8_f32 v242, v226, v227
	v_cvt_pk_fp8_f32 v243, v230, v231
	v_cvt_pk_fp8_f32 v244, v234, v235
	v_cvt_pk_fp8_f32 v245, v238, v239
	v_cvt_pk_fp8_f32 v242, v228, v229 op_sel:[0,0,1]
	v_cvt_pk_fp8_f32 v243, v232, v233 op_sel:[0,0,1]
	v_cvt_pk_fp8_f32 v244, v236, v237 op_sel:[0,0,1]
	v_cvt_pk_fp8_f32 v245, v240, v241 op_sel:[0,0,1]
	s_nop 0
	global_store_dwordx4 v91, v[242:245], s[6:7]
	ds_read_b32 v226, v213
	ds_read_b32 v227, v213 offset:512
	ds_read_b32 v228, v213 offset:1024
	ds_read_b32 v229, v213 offset:1536
	ds_read_b32 v230, v213 offset:2048
	ds_read_b32 v231, v213 offset:2560
	ds_read_b32 v232, v213 offset:3072
	ds_read_b32 v233, v213 offset:3584
	ds_read_b32 v234, v213 offset:4096
	ds_read_b32 v235, v213 offset:4608
	ds_read_b32 v236, v213 offset:5120
	ds_read_b32 v237, v213 offset:5632
	ds_read_b32 v238, v213 offset:6144
	ds_read_b32 v239, v213 offset:6656
	ds_read_b32 v240, v213 offset:7168
	ds_read_b32 v241, v213 offset:7680
	s_waitcnt lgkmcnt(0)
	v_max_f32_e32 v226, v226, v226
	v_max_f32_e32 v227, v227, v227
	v_max_f32_e32 v228, v228, v228
	v_max_f32_e32 v229, v229, v229
	v_max_f32_e32 v230, v230, v230
	v_max_f32_e32 v231, v231, v231
	v_max_f32_e32 v232, v232, v232
	v_max_f32_e32 v233, v233, v233
	v_max_f32_e32 v234, v234, v234
	v_max_f32_e32 v235, v235, v235
	v_max_f32_e32 v236, v236, v236
	v_max_f32_e32 v237, v237, v237
	v_max_f32_e32 v238, v238, v238
	v_max_f32_e32 v239, v239, v239
	v_max_f32_e32 v240, v240, v240
	v_max_f32_e32 v241, v241, v241
	v_med3_f32 v226, v226, s62, v95
	v_med3_f32 v227, v227, s62, v95
	v_med3_f32 v228, v228, s62, v95
	v_med3_f32 v229, v229, s62, v95
	v_med3_f32 v230, v230, s62, v95
	v_med3_f32 v231, v231, s62, v95
	v_med3_f32 v232, v232, s62, v95
	v_med3_f32 v233, v233, s62, v95
	v_med3_f32 v234, v234, s62, v95
	v_med3_f32 v235, v235, s62, v95
	v_med3_f32 v236, v236, s62, v95
	v_med3_f32 v237, v237, s62, v95
	v_med3_f32 v238, v238, s62, v95
	v_med3_f32 v239, v239, s62, v95
	v_med3_f32 v240, v240, s62, v95
	v_med3_f32 v241, v241, s62, v95
	v_mov_b32_e32 v242, 0
	v_mov_b32_e32 v243, 0
	v_mov_b32_e32 v244, 0
	v_mov_b32_e32 v245, 0
	v_cvt_pk_fp8_f32 v242, v226, v227
	v_cvt_pk_fp8_f32 v243, v230, v231
	v_cvt_pk_fp8_f32 v244, v234, v235
	v_cvt_pk_fp8_f32 v245, v238, v239
	v_cvt_pk_fp8_f32 v242, v228, v229 op_sel:[0,0,1]
	v_cvt_pk_fp8_f32 v243, v232, v233 op_sel:[0,0,1]
	v_cvt_pk_fp8_f32 v244, v236, v237 op_sel:[0,0,1]
	v_cvt_pk_fp8_f32 v245, v240, v241 op_sel:[0,0,1]
	s_nop 0
	global_store_dwordx4 v92, v[242:245], s[6:7]
	s_waitcnt vmcnt(12)
	v_mul_f32_e32 v176, v50, v176
	v_mul_f32_e32 v177, v50, v177
	v_mul_f32_e32 v178, v50, v178
	v_mul_f32_e32 v179, v50, v179
	ds_write_b128 v210, v[176:179]
	v_mul_f32_e32 v180, v51, v180
	v_mul_f32_e32 v181, v51, v181
	v_mul_f32_e32 v182, v51, v182
	v_mul_f32_e32 v183, v51, v183
	ds_write_b128 v210, v[180:183] offset:1024
	v_mul_f32_e32 v184, v52, v184
	v_mul_f32_e32 v185, v52, v185
	v_mul_f32_e32 v186, v52, v186
	v_mul_f32_e32 v187, v52, v187
	ds_write_b128 v210, v[184:187] offset:2048
	v_mul_f32_e32 v188, v53, v188
	v_mul_f32_e32 v189, v53, v189
	v_mul_f32_e32 v190, v53, v190
	v_mul_f32_e32 v191, v53, v191
	ds_write_b128 v210, v[188:191] offset:3072
	v_mul_f32_e32 v192, v54, v192
	v_mul_f32_e32 v193, v54, v193
	v_mul_f32_e32 v194, v54, v194
	v_mul_f32_e32 v195, v54, v195
	ds_write_b128 v210, v[192:195] offset:4096
	v_mul_f32_e32 v196, v55, v196
	v_mul_f32_e32 v197, v55, v197
	v_mul_f32_e32 v198, v55, v198
	v_mul_f32_e32 v199, v55, v199
	ds_write_b128 v210, v[196:199] offset:5120
	v_mul_f32_e32 v200, v56, v200
	v_mul_f32_e32 v201, v56, v201
	v_mul_f32_e32 v202, v56, v202
	v_mul_f32_e32 v203, v56, v203
	ds_write_b128 v210, v[200:203] offset:6144
	v_mul_f32_e32 v204, v57, v204
	v_mul_f32_e32 v205, v57, v205
	v_mul_f32_e32 v206, v57, v206
	v_mul_f32_e32 v207, v57, v207
	ds_write_b128 v210, v[204:207] offset:7168
	s_waitcnt lgkmcnt(0)
	s_barrier
; #define GAS __attribute__((address_space(1)))
; #define LAS __attribute__((address_space(3)))
; #define LDS_WAIT() asm volatile("s_waitcnt lgkmcnt(0)" ::: "memory")
; __device__ __forceinline__ int nat_dim(int p) { return (p >> 1) + 64 * (p & 1); }
; template <int MAP, bool KS, bool KPERM = false>
; __device__ __forceinline__ void p0_transpose_item(const float* W, int K, int Nsrc, int nblk, bf16* WT, const float* ksA, const float* ksB, int ksplit, LAS float* scr, int item, int lane) {
;     const int kb = item / nblk, nb = item % nblk, k0 = 64 * kb, n0 = 32 * nb;
;     const int nr = n0 + (lane & 31); const int sc = MAP == 1 ? src_col_in(nr) : (MAP == 2 ? nat_dim(nr) : nr);
;     float v[32];
; #pragma unroll
;     for (int i = 0; i < 32; ++i) { const int k = k0 + 2 * i + (lane >> 5); const int ksrc = KPERM ? ((k & ~127) + nat_dim(k & 127)) : k;
;         v[i] = sc >= 0 ? W[(size_t)ksrc * Nsrc + sc] : 0.f; }
; #pragma unroll
;     for (int i = 0; i < 32; ++i) { const int kk = 2 * i + (lane >> 5); const int k = k0 + kk;
;         if (KS) v[i] *= (k < ksplit ? ksA[k] : ksB[k - ksplit]);
;         scr[kk * 33 + (lane & 31)] = v[i]; }
;     LDS_WAIT(); asm volatile("" ::: "memory");
;     const int pr = item >> 1, kb = 2 * (pr / nblk) + (item & 1), nb = pr % nblk, k0 = 64 * kb, n0 = 32 * nb;
;     const int nr = n0 + (lane & 31); const int sc = MAP == 1 ? src_col_in(nr) : nr;
;     float v[32];
; #pragma unroll
;     for (int i = 0; i < 32; ++i) v[i] = sc >= 0 ? W[(size_t)(k0 + 2 * i + (lane >> 5)) * Nsrc + sc] : 0.f;
; #pragma unroll
;     for (int i = 0; i < 32; ++i) { const int k = k0 + 2 * i + (lane >> 5); float x = v[i] * wscale; if (KS) x *= (k < ksplit ? ksA[k] : ksB[k - ksplit]); scr[(2 * i + (lane >> 5)) * 33 + (lane & 31)] = x; }
;     LDS_WAIT(); asm volatile("" ::: "memory");
;     const int c = lane & 7;
; #pragma unroll
;     for (int j = 0; j < 4; ++j) { const int n = (lane >> 3) + 8 * j; const LAS float* s = scr + (8 * c) * 33 + n;
;         const unsigned long long o = (unsigned long long)pg8::pk4_fp8(s[0 * 33], s[1 * 33], s[2 * 33], s[3 * 33]) | ((unsigned long long)pg8::pk4_fp8(s[4 * 33], s[5 * 33], s[6 * 33], s[7 * 33]) << 32);
;         *(GAS unsigned long long*)(WT + (size_t)(n0 + n) * K + k0 + 8 * c) = o; }
;     LDS_WAIT(); asm volatile("" ::: "memory");
	s_add_i32 s24, s23, 48
	s_lshl_b32 s20, s24, 7
	s_cmp_lt_u32 s24, 40
	s_cselect_b32 s21, 0, 0x830
	s_cmp_lt_u32 s24, 72
	s_cselect_b32 s21, s21, 0xfffff030
	s_add_i32 s20, s20, s21
	s_lshl_b32 s20, s20, 2
	s_add_u32 s8, s50, s20
	s_addc_u32 s9, s51, 0
	global_load_dwordx4 v[176:179], v76, s[8:9]
	s_add_u32 s8, s8, 0x16280
	s_addc_u32 s9, s9, 0
	global_load_dwordx4 v[180:183], v76, s[8:9]
	s_add_u32 s8, s8, 0x16280
	s_addc_u32 s9, s9, 0
	global_load_dwordx4 v[184:187], v76, s[8:9]
	s_add_u32 s8, s8, 0x16280
	s_addc_u32 s9, s9, 0
	global_load_dwordx4 v[188:191], v76, s[8:9]
	s_add_u32 s8, s8, 0x16280
	s_addc_u32 s9, s9, 0
	global_load_dwordx4 v[192:195], v76, s[8:9]
	s_add_u32 s8, s8, 0x16280
	s_addc_u32 s9, s9, 0
	global_load_dwordx4 v[196:199], v76, s[8:9]
	s_add_u32 s8, s8, 0x16280
	s_addc_u32 s9, s9, 0
	global_load_dwordx4 v[200:203], v76, s[8:9]
	s_add_u32 s8, s8, 0x16280
	s_addc_u32 s9, s9, 0
	global_load_dwordx4 v[204:207], v76, s[8:9]
	s_add_i32 s24, s23, 32
	s_mul_i32 s20, s24, 0x80000
	s_add_u32 s6, s52, s20
	s_addc_u32 s7, s53, 0
	s_cmp_lt_u32 s24, 16
	s_cselect_b32 s20, 1, 0
	s_sub_i32 s21, s24, 16
	s_bitcmp0_b32 s21, 2
	s_cselect_b32 s21, 1, 0
	s_cmp_lt_u32 s24, 40
	s_cselect_b32 s21, s21, 0
	s_or_b32 s20, s20, s21
	s_cmp_lg_u32 s20, 0
	s_cselect_b64 s[20:21], -1, 0
	v_cndmask_b32_e64 v91, v77, v81, s[20:21]
	v_cndmask_b32_e64 v92, v78, v82, s[20:21]
	ds_read_b32 v226, v212
	ds_read_b32 v227, v212 offset:512
	ds_read_b32 v228, v212 offset:1024
	ds_read_b32 v229, v212 offset:1536
	ds_read_b32 v230, v212 offset:2048
	ds_read_b32 v231, v212 offset:2560
	ds_read_b32 v232, v212 offset:3072
	ds_read_b32 v233, v212 offset:3584
	ds_read_b32 v234, v212 offset:4096
	ds_read_b32 v235, v212 offset:4608
	ds_read_b32 v236, v212 offset:5120
	ds_read_b32 v237, v212 offset:5632
	ds_read_b32 v238, v212 offset:6144
	ds_read_b32 v239, v212 offset:6656
	ds_read_b32 v240, v212 offset:7168
	ds_read_b32 v241, v212 offset:7680
	s_waitcnt lgkmcnt(0)
	v_max_f32_e32 v226, v226, v226
	v_max_f32_e32 v227, v227, v227
	v_max_f32_e32 v228, v228, v228
	v_max_f32_e32 v229, v229, v229
	v_max_f32_e32 v230, v230, v230
	v_max_f32_e32 v231, v231, v231
	v_max_f32_e32 v232, v232, v232
	v_max_f32_e32 v233, v233, v233
	v_max_f32_e32 v234, v234, v234
	v_max_f32_e32 v235, v235, v235
	v_max_f32_e32 v236, v236, v236
	v_max_f32_e32 v237, v237, v237
	v_max_f32_e32 v238, v238, v238
	v_max_f32_e32 v239, v239, v239
	v_max_f32_e32 v240, v240, v240
	v_max_f32_e32 v241, v241, v241
	v_med3_f32 v226, v226, s62, v95
	v_med3_f32 v227, v227, s62, v95
	v_med3_f32 v228, v228, s62, v95
	v_med3_f32 v229, v229, s62, v95
	v_med3_f32 v230, v230, s62, v95
	v_med3_f32 v231, v231, s62, v95
	v_med3_f32 v232, v232, s62, v95
	v_med3_f32 v233, v233, s62, v95
	v_med3_f32 v234, v234, s62, v95
	v_med3_f32 v235, v235, s62, v95
	v_med3_f32 v236, v236, s62, v95
	v_med3_f32 v237, v237, s62, v95
	v_med3_f32 v238, v238, s62, v95
	v_med3_f32 v239, v239, s62, v95
	v_med3_f32 v240, v240, s62, v95
	v_med3_f32 v241, v241, s62, v95
	v_mov_b32_e32 v242, 0
	v_mov_b32_e32 v243, 0
	v_mov_b32_e32 v244, 0
	v_mov_b32_e32 v245, 0
	v_cvt_pk_fp8_f32 v242, v226, v227
	v_cvt_pk_fp8_f32 v243, v230, v231
	v_cvt_pk_fp8_f32 v244, v234, v235
	v_cvt_pk_fp8_f32 v245, v238, v239
	v_cvt_pk_fp8_f32 v242, v228, v229 op_sel:[0,0,1]
	v_cvt_pk_fp8_f32 v243, v232, v233 op_sel:[0,0,1]
	v_cvt_pk_fp8_f32 v244, v236, v237 op_sel:[0,0,1]
	v_cvt_pk_fp8_f32 v245, v240, v241 op_sel:[0,0,1]
	s_nop 0
	global_store_dwordx4 v91, v[242:245], s[6:7]
	ds_read_b32 v226, v214
	ds_read_b32 v227, v214 offset:512
	ds_read_b32 v228, v214 offset:1024
	ds_read_b32 v229, v214 offset:1536
	ds_read_b32 v230, v214 offset:2048
	ds_read_b32 v231, v214 offset:2560
	ds_read_b32 v232, v214 offset:3072
	ds_read_b32 v233, v214 offset:3584
	ds_read_b32 v234, v214 offset:4096
	ds_read_b32 v235, v214 offset:4608
	ds_read_b32 v236, v214 offset:5120
	ds_read_b32 v237, v214 offset:5632
	ds_read_b32 v238, v214 offset:6144
	ds_read_b32 v239, v214 offset:6656
	ds_read_b32 v240, v214 offset:7168
	ds_read_b32 v241, v214 offset:7680
	s_waitcnt lgkmcnt(0)
	v_max_f32_e32 v226, v226, v226
	v_max_f32_e32 v227, v227, v227
	v_max_f32_e32 v228, v228, v228
	v_max_f32_e32 v229, v229, v229
	v_max_f32_e32 v230, v230, v230
	v_max_f32_e32 v231, v231, v231
	v_max_f32_e32 v232, v232, v232
	v_max_f32_e32 v233, v233, v233
	v_max_f32_e32 v234, v234, v234
	v_max_f32_e32 v235, v235, v235
	v_max_f32_e32 v236, v236, v236
	v_max_f32_e32 v237, v237, v237
	v_max_f32_e32 v238, v238, v238
	v_max_f32_e32 v239, v239, v239
	v_max_f32_e32 v240, v240, v240
	v_max_f32_e32 v241, v241, v241
	v_med3_f32 v226, v226, s62, v95
	v_med3_f32 v227, v227, s62, v95
	v_med3_f32 v228, v228, s62, v95
	v_med3_f32 v229, v229, s62, v95
	v_med3_f32 v230, v230, s62, v95
	v_med3_f32 v231, v231, s62, v95
	v_med3_f32 v232, v232, s62, v95
	v_med3_f32 v233, v233, s62, v95
	v_med3_f32 v234, v234, s62, v95
	v_med3_f32 v235, v235, s62, v95
	v_med3_f32 v236, v236, s62, v95
	v_med3_f32 v237, v237, s62, v95
	v_med3_f32 v238, v238, s62, v95
	v_med3_f32 v239, v239, s62, v95
	v_med3_f32 v240, v240, s62, v95
	v_med3_f32 v241, v241, s62, v95
	v_mov_b32_e32 v242, 0
	v_mov_b32_e32 v243, 0
	v_mov_b32_e32 v244, 0
	v_mov_b32_e32 v245, 0
	v_cvt_pk_fp8_f32 v242, v226, v227
	v_cvt_pk_fp8_f32 v243, v230, v231
	v_cvt_pk_fp8_f32 v244, v234, v235
	v_cvt_pk_fp8_f32 v245, v238, v239
	v_cvt_pk_fp8_f32 v242, v228, v229 op_sel:[0,0,1]
	v_cvt_pk_fp8_f32 v243, v232, v233 op_sel:[0,0,1]
	v_cvt_pk_fp8_f32 v244, v236, v237 op_sel:[0,0,1]
	v_cvt_pk_fp8_f32 v245, v240, v241 op_sel:[0,0,1]
	s_nop 0
	global_store_dwordx4 v92, v[242:245], s[6:7]
	s_waitcnt vmcnt(12)
	v_mul_f32_e32 v144, v50, v144
	v_mul_f32_e32 v145, v50, v145
	v_mul_f32_e32 v146, v50, v146
	v_mul_f32_e32 v147, v50, v147
	ds_write_b128 v209, v[144:147]
	v_mul_f32_e32 v148, v51, v148
	v_mul_f32_e32 v149, v51, v149
	v_mul_f32_e32 v150, v51, v150
	v_mul_f32_e32 v151, v51, v151
	ds_write_b128 v209, v[148:151] offset:1024
	v_mul_f32_e32 v152, v52, v152
	v_mul_f32_e32 v153, v52, v153
	v_mul_f32_e32 v154, v52, v154
	v_mul_f32_e32 v155, v52, v155
	ds_write_b128 v209, v[152:155] offset:2048
	v_mul_f32_e32 v156, v53, v156
	v_mul_f32_e32 v157, v53, v157
	v_mul_f32_e32 v158, v53, v158
	v_mul_f32_e32 v159, v53, v159
	ds_write_b128 v209, v[156:159] offset:3072
	v_mul_f32_e32 v160, v54, v160
	v_mul_f32_e32 v161, v54, v161
	v_mul_f32_e32 v162, v54, v162
	v_mul_f32_e32 v163, v54, v163
	ds_write_b128 v209, v[160:163] offset:4096
	v_mul_f32_e32 v164, v55, v164
	v_mul_f32_e32 v165, v55, v165
	v_mul_f32_e32 v166, v55, v166
	v_mul_f32_e32 v167, v55, v167
	ds_write_b128 v209, v[164:167] offset:5120
	v_mul_f32_e32 v168, v56, v168
	v_mul_f32_e32 v169, v56, v169
	v_mul_f32_e32 v170, v56, v170
	v_mul_f32_e32 v171, v56, v171
	ds_write_b128 v209, v[168:171] offset:6144
	v_mul_f32_e32 v172, v57, v172
	v_mul_f32_e32 v173, v57, v173
	v_mul_f32_e32 v174, v57, v174
	v_mul_f32_e32 v175, v57, v175
	ds_write_b128 v209, v[172:175] offset:7168
	s_waitcnt lgkmcnt(0)
	s_barrier
; #define GAS __attribute__((address_space(1)))
; #define LAS __attribute__((address_space(3)))
; #define LDS_WAIT() asm volatile("s_waitcnt lgkmcnt(0)" ::: "memory")
; __device__ __forceinline__ int src_col_in(int c) {
;     if (c < 5120) { const int blk = c >> 7, p = c & 127; const bool rope = blk < 16 || ((((blk - 16) >> 2) & 1) == 0); const int d = rope ? (p >> 1) + 64 * (p & 1) : p; return blk * 128 + d; }
;     if (c < OFF_Z) return c + 2096;
;     if (c < OFF_G) return c - 4048;
;     if (c < OFF_DT) return 5120 + (c - OFF_G);
;     if (c < NSRC) return c;
;     return -1;
; }
;     const int pr = item >> 1, kb = 2 * (pr / nblk) + (item & 1), nb = pr % nblk, k0 = 64 * kb, n0 = 32 * nb;
;     const int nr = n0 + (lane & 31); const int sc = MAP == 1 ? src_col_in(nr) : nr;
;     float v[32];
; #pragma unroll
;     for (int i = 0; i < 32; ++i) v[i] = sc >= 0 ? W[(size_t)(k0 + 2 * i + (lane >> 5)) * Nsrc + sc] : 0.f;
; #pragma unroll
;     for (int i = 0; i < 32; ++i) { const int k = k0 + 2 * i + (lane >> 5); float x = v[i] * wscale; if (KS) x *= (k < ksplit ? ksA[k] : ksB[k - ksplit]); scr[(2 * i + (lane >> 5)) * 33 + (lane & 31)] = x; }
;     LDS_WAIT(); asm volatile("" ::: "memory");
;     const int c = lane & 7;
; #pragma unroll
;     for (int j = 0; j < 4; ++j) { const int n = (lane >> 3) + 8 * j; const LAS float* s = scr + (8 * c) * 33 + n;
;         const unsigned long long o = (unsigned long long)pg8::pk4_fp8(s[0 * 33], s[1 * 33], s[2 * 33], s[3 * 33]) | ((unsigned long long)pg8::pk4_fp8(s[4 * 33], s[5 * 33], s[6 * 33], s[7 * 33]) << 32);
;         *(GAS unsigned long long*)(WT + (size_t)(n0 + n) * K + k0 + 8 * c) = o; }
;     LDS_WAIT(); asm volatile("" ::: "memory");
; }
	s_add_i32 s24, s23, 56
	s_lshl_b32 s20, s24, 7
	s_cmp_lt_u32 s24, 40
	s_cselect_b32 s21, 0, 0x830
	s_cmp_lt_u32 s24, 72
	s_cselect_b32 s21, s21, 0xfffff030
	s_add_i32 s20, s20, s21
	s_lshl_b32 s20, s20, 2
	s_add_u32 s8, s50, s20
	s_addc_u32 s9, s51, 0
	global_load_dwordx4 v[144:147], v76, s[8:9]
	s_add_u32 s8, s8, 0x16280
	s_addc_u32 s9, s9, 0
	global_load_dwordx4 v[148:151], v76, s[8:9]
	s_add_u32 s8, s8, 0x16280
	s_addc_u32 s9, s9, 0
	global_load_dwordx4 v[152:155], v76, s[8:9]
	s_add_u32 s8, s8, 0x16280
	s_addc_u32 s9, s9, 0
	global_load_dwordx4 v[156:159], v76, s[8:9]
	s_add_u32 s8, s8, 0x16280
	s_addc_u32 s9, s9, 0
	global_load_dwordx4 v[160:163], v76, s[8:9]
	s_add_u32 s8, s8, 0x16280
	s_addc_u32 s9, s9, 0
	global_load_dwordx4 v[164:167], v76, s[8:9]
	s_add_u32 s8, s8, 0x16280
	s_addc_u32 s9, s9, 0
	global_load_dwordx4 v[168:171], v76, s[8:9]
	s_add_u32 s8, s8, 0x16280
	s_addc_u32 s9, s9, 0
	global_load_dwordx4 v[172:175], v76, s[8:9]
	s_add_i32 s24, s23, 40
	s_mul_i32 s20, s24, 0x80000
	s_add_u32 s6, s52, s20
	s_addc_u32 s7, s53, 0
	s_cmp_lt_u32 s24, 16
	s_cselect_b32 s20, 1, 0
	s_sub_i32 s21, s24, 16
	s_bitcmp0_b32 s21, 2
	s_cselect_b32 s21, 1, 0
	s_cmp_lt_u32 s24, 40
	s_cselect_b32 s21, s21, 0
	s_or_b32 s20, s20, s21
	s_cmp_lg_u32 s20, 0
	s_cselect_b64 s[20:21], -1, 0
	v_cndmask_b32_e64 v91, v77, v81, s[20:21]
	v_cndmask_b32_e64 v92, v78, v82, s[20:21]
	ds_read_b32 v226, v211
	ds_read_b32 v227, v211 offset:512
	ds_read_b32 v228, v211 offset:1024
	ds_read_b32 v229, v211 offset:1536
	ds_read_b32 v230, v211 offset:2048
	ds_read_b32 v231, v211 offset:2560
	ds_read_b32 v232, v211 offset:3072
	ds_read_b32 v233, v211 offset:3584
	ds_read_b32 v234, v211 offset:4096
	ds_read_b32 v235, v211 offset:4608
	ds_read_b32 v236, v211 offset:5120
	ds_read_b32 v237, v211 offset:5632
	ds_read_b32 v238, v211 offset:6144
	ds_read_b32 v239, v211 offset:6656
	ds_read_b32 v240, v211 offset:7168
	ds_read_b32 v241, v211 offset:7680
	s_waitcnt lgkmcnt(0)
	v_max_f32_e32 v226, v226, v226
	v_max_f32_e32 v227, v227, v227
	v_max_f32_e32 v228, v228, v228
	v_max_f32_e32 v229, v229, v229
	v_max_f32_e32 v230, v230, v230
	v_max_f32_e32 v231, v231, v231
	v_max_f32_e32 v232, v232, v232
	v_max_f32_e32 v233, v233, v233
	v_max_f32_e32 v234, v234, v234
	v_max_f32_e32 v235, v235, v235
	v_max_f32_e32 v236, v236, v236
	v_max_f32_e32 v237, v237, v237
	v_max_f32_e32 v238, v238, v238
	v_max_f32_e32 v239, v239, v239
	v_max_f32_e32 v240, v240, v240
	v_max_f32_e32 v241, v241, v241
	v_med3_f32 v226, v226, s62, v95
	v_med3_f32 v227, v227, s62, v95
	v_med3_f32 v228, v228, s62, v95
	v_med3_f32 v229, v229, s62, v95
	v_med3_f32 v230, v230, s62, v95
	v_med3_f32 v231, v231, s62, v95
	v_med3_f32 v232, v232, s62, v95
	v_med3_f32 v233, v233, s62, v95
	v_med3_f32 v234, v234, s62, v95
	v_med3_f32 v235, v235, s62, v95
	v_med3_f32 v236, v236, s62, v95
	v_med3_f32 v237, v237, s62, v95
	v_med3_f32 v238, v238, s62, v95
	v_med3_f32 v239, v239, s62, v95
	v_med3_f32 v240, v240, s62, v95
	v_med3_f32 v241, v241, s62, v95
	v_mov_b32_e32 v242, 0
	v_mov_b32_e32 v243, 0
	v_mov_b32_e32 v244, 0
	v_mov_b32_e32 v245, 0
	v_cvt_pk_fp8_f32 v242, v226, v227
	v_cvt_pk_fp8_f32 v243, v230, v231
	v_cvt_pk_fp8_f32 v244, v234, v235
	v_cvt_pk_fp8_f32 v245, v238, v239
	v_cvt_pk_fp8_f32 v242, v228, v229 op_sel:[0,0,1]
	v_cvt_pk_fp8_f32 v243, v232, v233 op_sel:[0,0,1]
	v_cvt_pk_fp8_f32 v244, v236, v237 op_sel:[0,0,1]
	v_cvt_pk_fp8_f32 v245, v240, v241 op_sel:[0,0,1]
	s_nop 0
	global_store_dwordx4 v91, v[242:245], s[6:7]
	ds_read_b32 v226, v213
	ds_read_b32 v227, v213 offset:512
	ds_read_b32 v228, v213 offset:1024
	ds_read_b32 v229, v213 offset:1536
	ds_read_b32 v230, v213 offset:2048
	ds_read_b32 v231, v213 offset:2560
	ds_read_b32 v232, v213 offset:3072
	ds_read_b32 v233, v213 offset:3584
	ds_read_b32 v234, v213 offset:4096
	ds_read_b32 v235, v213 offset:4608
	ds_read_b32 v236, v213 offset:5120
	ds_read_b32 v237, v213 offset:5632
	ds_read_b32 v238, v213 offset:6144
	ds_read_b32 v239, v213 offset:6656
	ds_read_b32 v240, v213 offset:7168
	ds_read_b32 v241, v213 offset:7680
	s_waitcnt lgkmcnt(0)
	v_max_f32_e32 v226, v226, v226
	v_max_f32_e32 v227, v227, v227
	v_max_f32_e32 v228, v228, v228
	v_max_f32_e32 v229, v229, v229
	v_max_f32_e32 v230, v230, v230
	v_max_f32_e32 v231, v231, v231
	v_max_f32_e32 v232, v232, v232
	v_max_f32_e32 v233, v233, v233
	v_max_f32_e32 v234, v234, v234
	v_max_f32_e32 v235, v235, v235
	v_max_f32_e32 v236, v236, v236
	v_max_f32_e32 v237, v237, v237
	v_max_f32_e32 v238, v238, v238
	v_max_f32_e32 v239, v239, v239
	v_max_f32_e32 v240, v240, v240
	v_max_f32_e32 v241, v241, v241
	v_med3_f32 v226, v226, s62, v95
	v_med3_f32 v227, v227, s62, v95
	v_med3_f32 v228, v228, s62, v95
	v_med3_f32 v229, v229, s62, v95
	v_med3_f32 v230, v230, s62, v95
	v_med3_f32 v231, v231, s62, v95
	v_med3_f32 v232, v232, s62, v95
	v_med3_f32 v233, v233, s62, v95
	v_med3_f32 v234, v234, s62, v95
	v_med3_f32 v235, v235, s62, v95
	v_med3_f32 v236, v236, s62, v95
	v_med3_f32 v237, v237, s62, v95
	v_med3_f32 v238, v238, s62, v95
	v_med3_f32 v239, v239, s62, v95
	v_med3_f32 v240, v240, s62, v95
	v_med3_f32 v241, v241, s62, v95
	v_mov_b32_e32 v242, 0
	v_mov_b32_e32 v243, 0
	v_mov_b32_e32 v244, 0
	v_mov_b32_e32 v245, 0
	v_cvt_pk_fp8_f32 v242, v226, v227
	v_cvt_pk_fp8_f32 v243, v230, v231
	v_cvt_pk_fp8_f32 v244, v234, v235
	v_cvt_pk_fp8_f32 v245, v238, v239
	v_cvt_pk_fp8_f32 v242, v228, v229 op_sel:[0,0,1]
	v_cvt_pk_fp8_f32 v243, v232, v233 op_sel:[0,0,1]
	v_cvt_pk_fp8_f32 v244, v236, v237 op_sel:[0,0,1]
	v_cvt_pk_fp8_f32 v245, v240, v241 op_sel:[0,0,1]
	s_nop 0
	global_store_dwordx4 v92, v[242:245], s[6:7]
	s_waitcnt vmcnt(12)
	v_mul_f32_e32 v176, v50, v176
	v_mul_f32_e32 v177, v50, v177
	v_mul_f32_e32 v178, v50, v178
	v_mul_f32_e32 v179, v50, v179
	ds_write_b128 v210, v[176:179]
	v_mul_f32_e32 v180, v51, v180
	v_mul_f32_e32 v181, v51, v181
	v_mul_f32_e32 v182, v51, v182
	v_mul_f32_e32 v183, v51, v183
	ds_write_b128 v210, v[180:183] offset:1024
	v_mul_f32_e32 v184, v52, v184
	v_mul_f32_e32 v185, v52, v185
	v_mul_f32_e32 v186, v52, v186
	v_mul_f32_e32 v187, v52, v187
	ds_write_b128 v210, v[184:187] offset:2048
	v_mul_f32_e32 v188, v53, v188
	v_mul_f32_e32 v189, v53, v189
	v_mul_f32_e32 v190, v53, v190
	v_mul_f32_e32 v191, v53, v191
	ds_write_b128 v210, v[188:191] offset:3072
	v_mul_f32_e32 v192, v54, v192
	v_mul_f32_e32 v193, v54, v193
	v_mul_f32_e32 v194, v54, v194
	v_mul_f32_e32 v195, v54, v195
	ds_write_b128 v210, v[192:195] offset:4096
	v_mul_f32_e32 v196, v55, v196
	v_mul_f32_e32 v197, v55, v197
	v_mul_f32_e32 v198, v55, v198
	v_mul_f32_e32 v199, v55, v199
	ds_write_b128 v210, v[196:199] offset:5120
	v_mul_f32_e32 v200, v56, v200
	v_mul_f32_e32 v201, v56, v201
	v_mul_f32_e32 v202, v56, v202
	v_mul_f32_e32 v203, v56, v203
	ds_write_b128 v210, v[200:203] offset:6144
	v_mul_f32_e32 v204, v57, v204
	v_mul_f32_e32 v205, v57, v205
	v_mul_f32_e32 v206, v57, v206
	v_mul_f32_e32 v207, v57, v207
	ds_write_b128 v210, v[204:207] offset:7168
	s_waitcnt lgkmcnt(0)
	s_barrier
; #define GAS __attribute__((address_space(1)))
; #define LAS __attribute__((address_space(3)))
; #define LDS_WAIT() asm volatile("s_waitcnt lgkmcnt(0)" ::: "memory")
; __device__ __forceinline__ int src_col_in(int c) {
;     if (c < 5120) { const int blk = c >> 7, p = c & 127; const bool rope = blk < 16 || ((((blk - 16) >> 2) & 1) == 0); const int d = rope ? (p >> 1) + 64 * (p & 1) : p; return blk * 128 + d; }
;     if (c < OFF_Z) return c + 2096;
;     if (c < OFF_G) return c - 4048;
;     if (c < OFF_DT) return 5120 + (c - OFF_G);
;     if (c < NSRC) return c;
;     return -1;
; }
;     const int pr = item >> 1, kb = 2 * (pr / nblk) + (item & 1), nb = pr % nblk, k0 = 64 * kb, n0 = 32 * nb;
;     const int nr = n0 + (lane & 31); const int sc = MAP == 1 ? src_col_in(nr) : nr;
;     float v[32];
; #pragma unroll
;     for (int i = 0; i < 32; ++i) v[i] = sc >= 0 ? W[(size_t)(k0 + 2 * i + (lane >> 5)) * Nsrc + sc] : 0.f;
; #pragma unroll
;     for (int i = 0; i < 32; ++i) { const int k = k0 + 2 * i + (lane >> 5); float x = v[i] * wscale; if (KS) x *= (k < ksplit ? ksA[k] : ksB[k - ksplit]); scr[(2 * i + (lane >> 5)) * 33 + (lane & 31)] = x; }
;     LDS_WAIT(); asm volatile("" ::: "memory");
;     const int c = lane & 7;
; #pragma unroll
;     for (int j = 0; j < 4; ++j) { const int n = (lane >> 3) + 8 * j; const LAS float* s = scr + (8 * c) * 33 + n;
;         const unsigned long long o = (unsigned long long)pg8::pk4_fp8(s[0 * 33], s[1 * 33], s[2 * 33], s[3 * 33]) | ((unsigned long long)pg8::pk4_fp8(s[4 * 33], s[5 * 33], s[6 * 33], s[7 * 33]) << 32);
;         *(GAS unsigned long long*)(WT + (size_t)(n0 + n) * K + k0 + 8 * c) = o; }
;     LDS_WAIT(); asm volatile("" ::: "memory");
; }
	s_add_i32 s24, s23, 64
	s_lshl_b32 s20, s24, 7
	s_cmp_lt_u32 s24, 40
	s_cselect_b32 s21, 0, 0x830
	s_cmp_lt_u32 s24, 72
	s_cselect_b32 s21, s21, 0xfffff030
	s_add_i32 s20, s20, s21
	s_lshl_b32 s20, s20, 2
	s_add_u32 s8, s50, s20
	s_addc_u32 s9, s51, 0
	global_load_dwordx4 v[176:179], v76, s[8:9]
	s_add_u32 s8, s8, 0x16280
	s_addc_u32 s9, s9, 0
	global_load_dwordx4 v[180:183], v76, s[8:9]
	s_add_u32 s8, s8, 0x16280
	s_addc_u32 s9, s9, 0
	global_load_dwordx4 v[184:187], v76, s[8:9]
	s_add_u32 s8, s8, 0x16280
	s_addc_u32 s9, s9, 0
	global_load_dwordx4 v[188:191], v76, s[8:9]
	s_add_u32 s8, s8, 0x16280
	s_addc_u32 s9, s9, 0
	global_load_dwordx4 v[192:195], v76, s[8:9]
	s_add_u32 s8, s8, 0x16280
	s_addc_u32 s9, s9, 0
	global_load_dwordx4 v[196:199], v76, s[8:9]
	s_add_u32 s8, s8, 0x16280
	s_addc_u32 s9, s9, 0
	global_load_dwordx4 v[200:203], v76, s[8:9]
	s_add_u32 s8, s8, 0x16280
	s_addc_u32 s9, s9, 0
	global_load_dwordx4 v[204:207], v76, s[8:9]
	s_add_i32 s24, s23, 48
	s_mul_i32 s20, s24, 0x80000
	s_add_u32 s6, s52, s20
	s_addc_u32 s7, s53, 0
	s_cmp_lt_u32 s24, 16
	s_cselect_b32 s20, 1, 0
	s_sub_i32 s21, s24, 16
	s_bitcmp0_b32 s21, 2
	s_cselect_b32 s21, 1, 0
	s_cmp_lt_u32 s24, 40
	s_cselect_b32 s21, s21, 0
	s_or_b32 s20, s20, s21
	s_cmp_lg_u32 s20, 0
	s_cselect_b64 s[20:21], -1, 0
	v_cndmask_b32_e64 v91, v77, v81, s[20:21]
	v_cndmask_b32_e64 v92, v78, v82, s[20:21]
	ds_read_b32 v226, v212
	ds_read_b32 v227, v212 offset:512
	ds_read_b32 v228, v212 offset:1024
	ds_read_b32 v229, v212 offset:1536
	ds_read_b32 v230, v212 offset:2048
	ds_read_b32 v231, v212 offset:2560
	ds_read_b32 v232, v212 offset:3072
	ds_read_b32 v233, v212 offset:3584
	ds_read_b32 v234, v212 offset:4096
	ds_read_b32 v235, v212 offset:4608
	ds_read_b32 v236, v212 offset:5120
	ds_read_b32 v237, v212 offset:5632
	ds_read_b32 v238, v212 offset:6144
	ds_read_b32 v239, v212 offset:6656
	ds_read_b32 v240, v212 offset:7168
	ds_read_b32 v241, v212 offset:7680
	s_waitcnt lgkmcnt(0)
	v_max_f32_e32 v226, v226, v226
	v_max_f32_e32 v227, v227, v227
	v_max_f32_e32 v228, v228, v228
	v_max_f32_e32 v229, v229, v229
	v_max_f32_e32 v230, v230, v230
	v_max_f32_e32 v231, v231, v231
	v_max_f32_e32 v232, v232, v232
	v_max_f32_e32 v233, v233, v233
	v_max_f32_e32 v234, v234, v234
	v_max_f32_e32 v235, v235, v235
	v_max_f32_e32 v236, v236, v236
	v_max_f32_e32 v237, v237, v237
	v_max_f32_e32 v238, v238, v238
	v_max_f32_e32 v239, v239, v239
	v_max_f32_e32 v240, v240, v240
	v_max_f32_e32 v241, v241, v241
	v_med3_f32 v226, v226, s62, v95
	v_med3_f32 v227, v227, s62, v95
	v_med3_f32 v228, v228, s62, v95
	v_med3_f32 v229, v229, s62, v95
	v_med3_f32 v230, v230, s62, v95
	v_med3_f32 v231, v231, s62, v95
	v_med3_f32 v232, v232, s62, v95
	v_med3_f32 v233, v233, s62, v95
	v_med3_f32 v234, v234, s62, v95
	v_med3_f32 v235, v235, s62, v95
	v_med3_f32 v236, v236, s62, v95
	v_med3_f32 v237, v237, s62, v95
	v_med3_f32 v238, v238, s62, v95
	v_med3_f32 v239, v239, s62, v95
	v_med3_f32 v240, v240, s62, v95
	v_med3_f32 v241, v241, s62, v95
	v_mov_b32_e32 v242, 0
	v_mov_b32_e32 v243, 0
	v_mov_b32_e32 v244, 0
	v_mov_b32_e32 v245, 0
	v_cvt_pk_fp8_f32 v242, v226, v227
	v_cvt_pk_fp8_f32 v243, v230, v231
	v_cvt_pk_fp8_f32 v244, v234, v235
	v_cvt_pk_fp8_f32 v245, v238, v239
	v_cvt_pk_fp8_f32 v242, v228, v229 op_sel:[0,0,1]
	v_cvt_pk_fp8_f32 v243, v232, v233 op_sel:[0,0,1]
	v_cvt_pk_fp8_f32 v244, v236, v237 op_sel:[0,0,1]
	v_cvt_pk_fp8_f32 v245, v240, v241 op_sel:[0,0,1]
	s_nop 0
	global_store_dwordx4 v91, v[242:245], s[6:7]
	ds_read_b32 v226, v214
	ds_read_b32 v227, v214 offset:512
	ds_read_b32 v228, v214 offset:1024
	ds_read_b32 v229, v214 offset:1536
	ds_read_b32 v230, v214 offset:2048
	ds_read_b32 v231, v214 offset:2560
	ds_read_b32 v232, v214 offset:3072
	ds_read_b32 v233, v214 offset:3584
	ds_read_b32 v234, v214 offset:4096
	ds_read_b32 v235, v214 offset:4608
	ds_read_b32 v236, v214 offset:5120
	ds_read_b32 v237, v214 offset:5632
	ds_read_b32 v238, v214 offset:6144
	ds_read_b32 v239, v214 offset:6656
	ds_read_b32 v240, v214 offset:7168
	ds_read_b32 v241, v214 offset:7680
	s_waitcnt lgkmcnt(0)
	v_max_f32_e32 v226, v226, v226
	v_max_f32_e32 v227, v227, v227
	v_max_f32_e32 v228, v228, v228
	v_max_f32_e32 v229, v229, v229
	v_max_f32_e32 v230, v230, v230
	v_max_f32_e32 v231, v231, v231
	v_max_f32_e32 v232, v232, v232
	v_max_f32_e32 v233, v233, v233
	v_max_f32_e32 v234, v234, v234
	v_max_f32_e32 v235, v235, v235
	v_max_f32_e32 v236, v236, v236
	v_max_f32_e32 v237, v237, v237
	v_max_f32_e32 v238, v238, v238
	v_max_f32_e32 v239, v239, v239
	v_max_f32_e32 v240, v240, v240
	v_max_f32_e32 v241, v241, v241
	v_med3_f32 v226, v226, s62, v95
	v_med3_f32 v227, v227, s62, v95
	v_med3_f32 v228, v228, s62, v95
	v_med3_f32 v229, v229, s62, v95
	v_med3_f32 v230, v230, s62, v95
	v_med3_f32 v231, v231, s62, v95
	v_med3_f32 v232, v232, s62, v95
	v_med3_f32 v233, v233, s62, v95
	v_med3_f32 v234, v234, s62, v95
	v_med3_f32 v235, v235, s62, v95
	v_med3_f32 v236, v236, s62, v95
	v_med3_f32 v237, v237, s62, v95
	v_med3_f32 v238, v238, s62, v95
	v_med3_f32 v239, v239, s62, v95
	v_med3_f32 v240, v240, s62, v95
	v_med3_f32 v241, v241, s62, v95
	v_mov_b32_e32 v242, 0
	v_mov_b32_e32 v243, 0
	v_mov_b32_e32 v244, 0
	v_mov_b32_e32 v245, 0
	v_cvt_pk_fp8_f32 v242, v226, v227
	v_cvt_pk_fp8_f32 v243, v230, v231
	v_cvt_pk_fp8_f32 v244, v234, v235
	v_cvt_pk_fp8_f32 v245, v238, v239
	v_cvt_pk_fp8_f32 v242, v228, v229 op_sel:[0,0,1]
	v_cvt_pk_fp8_f32 v243, v232, v233 op_sel:[0,0,1]
	v_cvt_pk_fp8_f32 v244, v236, v237 op_sel:[0,0,1]
	v_cvt_pk_fp8_f32 v245, v240, v241 op_sel:[0,0,1]
	s_nop 0
	global_store_dwordx4 v92, v[242:245], s[6:7]
	s_waitcnt vmcnt(12)
	v_mul_f32_e32 v144, v50, v144
	v_mul_f32_e32 v145, v50, v145
	v_mul_f32_e32 v146, v50, v146
	v_mul_f32_e32 v147, v50, v147
	ds_write_b128 v209, v[144:147]
	v_mul_f32_e32 v148, v51, v148
	v_mul_f32_e32 v149, v51, v149
	v_mul_f32_e32 v150, v51, v150
	v_mul_f32_e32 v151, v51, v151
	ds_write_b128 v209, v[148:151] offset:1024
	v_mul_f32_e32 v152, v52, v152
	v_mul_f32_e32 v153, v52, v153
	v_mul_f32_e32 v154, v52, v154
	v_mul_f32_e32 v155, v52, v155
	ds_write_b128 v209, v[152:155] offset:2048
	v_mul_f32_e32 v156, v53, v156
	v_mul_f32_e32 v157, v53, v157
	v_mul_f32_e32 v158, v53, v158
	v_mul_f32_e32 v159, v53, v159
	ds_write_b128 v209, v[156:159] offset:3072
	v_mul_f32_e32 v160, v54, v160
	v_mul_f32_e32 v161, v54, v161
	v_mul_f32_e32 v162, v54, v162
	v_mul_f32_e32 v163, v54, v163
	ds_write_b128 v209, v[160:163] offset:4096
	v_mul_f32_e32 v164, v55, v164
	v_mul_f32_e32 v165, v55, v165
	v_mul_f32_e32 v166, v55, v166
	v_mul_f32_e32 v167, v55, v167
	ds_write_b128 v209, v[164:167] offset:5120
	v_mul_f32_e32 v168, v56, v168
	v_mul_f32_e32 v169, v56, v169
	v_mul_f32_e32 v170, v56, v170
	v_mul_f32_e32 v171, v56, v171
	ds_write_b128 v209, v[168:171] offset:6144
	v_mul_f32_e32 v172, v57, v172
	v_mul_f32_e32 v173, v57, v173
	v_mul_f32_e32 v174, v57, v174
	v_mul_f32_e32 v175, v57, v175
	ds_write_b128 v209, v[172:175] offset:7168
	s_waitcnt lgkmcnt(0)
	s_barrier
; #define GAS __attribute__((address_space(1)))
; #define LAS __attribute__((address_space(3)))
; #define LDS_WAIT() asm volatile("s_waitcnt lgkmcnt(0)" ::: "memory")
; __device__ __forceinline__ int src_col_in(int c) {
;     if (c < 5120) { const int blk = c >> 7, p = c & 127; const bool rope = blk < 16 || ((((blk - 16) >> 2) & 1) == 0); const int d = rope ? (p >> 1) + 64 * (p & 1) : p; return blk * 128 + d; }
;     if (c < OFF_Z) return c + 2096;
;     if (c < OFF_G) return c - 4048;
;     if (c < OFF_DT) return 5120 + (c - OFF_G);
;     if (c < NSRC) return c;
;     return -1;
; }
;     const int pr = item >> 1, kb = 2 * (pr / nblk) + (item & 1), nb = pr % nblk, k0 = 64 * kb, n0 = 32 * nb;
;     const int nr = n0 + (lane & 31); const int sc = MAP == 1 ? src_col_in(nr) : nr;
;     float v[32];
; #pragma unroll
;     for (int i = 0; i < 32; ++i) v[i] = sc >= 0 ? W[(size_t)(k0 + 2 * i + (lane >> 5)) * Nsrc + sc] : 0.f;
; #pragma unroll
;     for (int i = 0; i < 32; ++i) { const int k = k0 + 2 * i + (lane >> 5); float x = v[i] * wscale; if (KS) x *= (k < ksplit ? ksA[k] : ksB[k - ksplit]); scr[(2 * i + (lane >> 5)) * 33 + (lane & 31)] = x; }
;     LDS_WAIT(); asm volatile("" ::: "memory");
;     const int c = lane & 7;
; #pragma unroll
;     for (int j = 0; j < 4; ++j) { const int n = (lane >> 3) + 8 * j; const LAS float* s = scr + (8 * c) * 33 + n;
;         const unsigned long long o = (unsigned long long)pg8::pk4_fp8(s[0 * 33], s[1 * 33], s[2 * 33], s[3 * 33]) | ((unsigned long long)pg8::pk4_fp8(s[4 * 33], s[5 * 33], s[6 * 33], s[7 * 33]) << 32);
;         *(GAS unsigned long long*)(WT + (size_t)(n0 + n) * K + k0 + 8 * c) = o; }
;     LDS_WAIT(); asm volatile("" ::: "memory");
; }
	s_add_i32 s24, s23, 72
	s_lshl_b32 s20, s24, 7
	s_cmp_lt_u32 s24, 40
	s_cselect_b32 s21, 0, 0x830
	s_cmp_lt_u32 s24, 72
	s_cselect_b32 s21, s21, 0xfffff030
	s_add_i32 s20, s20, s21
	s_lshl_b32 s20, s20, 2
	s_add_u32 s8, s50, s20
	s_addc_u32 s9, s51, 0
	global_load_dwordx4 v[144:147], v76, s[8:9]
	s_add_u32 s8, s8, 0x16280
	s_addc_u32 s9, s9, 0
	global_load_dwordx4 v[148:151], v76, s[8:9]
	s_add_u32 s8, s8, 0x16280
	s_addc_u32 s9, s9, 0
	global_load_dwordx4 v[152:155], v76, s[8:9]
	s_add_u32 s8, s8, 0x16280
	s_addc_u32 s9, s9, 0
	global_load_dwordx4 v[156:159], v76, s[8:9]
	s_add_u32 s8, s8, 0x16280
	s_addc_u32 s9, s9, 0
	global_load_dwordx4 v[160:163], v76, s[8:9]
	s_add_u32 s8, s8, 0x16280
	s_addc_u32 s9, s9, 0
	global_load_dwordx4 v[164:167], v76, s[8:9]
	s_add_u32 s8, s8, 0x16280
	s_addc_u32 s9, s9, 0
	global_load_dwordx4 v[168:171], v76, s[8:9]
	s_add_u32 s8, s8, 0x16280
	s_addc_u32 s9, s9, 0
	global_load_dwordx4 v[172:175], v76, s[8:9]
	s_add_i32 s24, s23, 56
	s_mul_i32 s20, s24, 0x80000
	s_add_u32 s6, s52, s20
	s_addc_u32 s7, s53, 0
	s_cmp_lt_u32 s24, 16
	s_cselect_b32 s20, 1, 0
	s_sub_i32 s21, s24, 16
	s_bitcmp0_b32 s21, 2
	s_cselect_b32 s21, 1, 0
	s_cmp_lt_u32 s24, 40
	s_cselect_b32 s21, s21, 0
	s_or_b32 s20, s20, s21
	s_cmp_lg_u32 s20, 0
	s_cselect_b64 s[20:21], -1, 0
	v_cndmask_b32_e64 v91, v77, v81, s[20:21]
	v_cndmask_b32_e64 v92, v78, v82, s[20:21]
	ds_read_b32 v226, v211
	ds_read_b32 v227, v211 offset:512
	ds_read_b32 v228, v211 offset:1024
	ds_read_b32 v229, v211 offset:1536
	ds_read_b32 v230, v211 offset:2048
	ds_read_b32 v231, v211 offset:2560
	ds_read_b32 v232, v211 offset:3072
	ds_read_b32 v233, v211 offset:3584
	ds_read_b32 v234, v211 offset:4096
	ds_read_b32 v235, v211 offset:4608
	ds_read_b32 v236, v211 offset:5120
	ds_read_b32 v237, v211 offset:5632
	ds_read_b32 v238, v211 offset:6144
	ds_read_b32 v239, v211 offset:6656
	ds_read_b32 v240, v211 offset:7168
	ds_read_b32 v241, v211 offset:7680
	s_waitcnt lgkmcnt(0)
	v_max_f32_e32 v226, v226, v226
	v_max_f32_e32 v227, v227, v227
	v_max_f32_e32 v228, v228, v228
	v_max_f32_e32 v229, v229, v229
	v_max_f32_e32 v230, v230, v230
	v_max_f32_e32 v231, v231, v231
	v_max_f32_e32 v232, v232, v232
	v_max_f32_e32 v233, v233, v233
	v_max_f32_e32 v234, v234, v234
	v_max_f32_e32 v235, v235, v235
	v_max_f32_e32 v236, v236, v236
	v_max_f32_e32 v237, v237, v237
	v_max_f32_e32 v238, v238, v238
	v_max_f32_e32 v239, v239, v239
	v_max_f32_e32 v240, v240, v240
	v_max_f32_e32 v241, v241, v241
	v_med3_f32 v226, v226, s62, v95
	v_med3_f32 v227, v227, s62, v95
	v_med3_f32 v228, v228, s62, v95
	v_med3_f32 v229, v229, s62, v95
	v_med3_f32 v230, v230, s62, v95
	v_med3_f32 v231, v231, s62, v95
	v_med3_f32 v232, v232, s62, v95
	v_med3_f32 v233, v233, s62, v95
	v_med3_f32 v234, v234, s62, v95
	v_med3_f32 v235, v235, s62, v95
	v_med3_f32 v236, v236, s62, v95
	v_med3_f32 v237, v237, s62, v95
	v_med3_f32 v238, v238, s62, v95
	v_med3_f32 v239, v239, s62, v95
	v_med3_f32 v240, v240, s62, v95
	v_med3_f32 v241, v241, s62, v95
	v_mov_b32_e32 v242, 0
	v_mov_b32_e32 v243, 0
	v_mov_b32_e32 v244, 0
	v_mov_b32_e32 v245, 0
	v_cvt_pk_fp8_f32 v242, v226, v227
	v_cvt_pk_fp8_f32 v243, v230, v231
	v_cvt_pk_fp8_f32 v244, v234, v235
	v_cvt_pk_fp8_f32 v245, v238, v239
	v_cvt_pk_fp8_f32 v242, v228, v229 op_sel:[0,0,1]
	v_cvt_pk_fp8_f32 v243, v232, v233 op_sel:[0,0,1]
	v_cvt_pk_fp8_f32 v244, v236, v237 op_sel:[0,0,1]
	v_cvt_pk_fp8_f32 v245, v240, v241 op_sel:[0,0,1]
	s_nop 0
	global_store_dwordx4 v91, v[242:245], s[6:7]
	ds_read_b32 v226, v213
	ds_read_b32 v227, v213 offset:512
	ds_read_b32 v228, v213 offset:1024
	ds_read_b32 v229, v213 offset:1536
	ds_read_b32 v230, v213 offset:2048
	ds_read_b32 v231, v213 offset:2560
	ds_read_b32 v232, v213 offset:3072
	ds_read_b32 v233, v213 offset:3584
	ds_read_b32 v234, v213 offset:4096
	ds_read_b32 v235, v213 offset:4608
	ds_read_b32 v236, v213 offset:5120
	ds_read_b32 v237, v213 offset:5632
	ds_read_b32 v238, v213 offset:6144
	ds_read_b32 v239, v213 offset:6656
	ds_read_b32 v240, v213 offset:7168
	ds_read_b32 v241, v213 offset:7680
	s_waitcnt lgkmcnt(0)
	v_max_f32_e32 v226, v226, v226
	v_max_f32_e32 v227, v227, v227
	v_max_f32_e32 v228, v228, v228
	v_max_f32_e32 v229, v229, v229
	v_max_f32_e32 v230, v230, v230
	v_max_f32_e32 v231, v231, v231
	v_max_f32_e32 v232, v232, v232
	v_max_f32_e32 v233, v233, v233
	v_max_f32_e32 v234, v234, v234
	v_max_f32_e32 v235, v235, v235
	v_max_f32_e32 v236, v236, v236
	v_max_f32_e32 v237, v237, v237
	v_max_f32_e32 v238, v238, v238
	v_max_f32_e32 v239, v239, v239
	v_max_f32_e32 v240, v240, v240
	v_max_f32_e32 v241, v241, v241
	v_med3_f32 v226, v226, s62, v95
	v_med3_f32 v227, v227, s62, v95
	v_med3_f32 v228, v228, s62, v95
	v_med3_f32 v229, v229, s62, v95
	v_med3_f32 v230, v230, s62, v95
	v_med3_f32 v231, v231, s62, v95
	v_med3_f32 v232, v232, s62, v95
	v_med3_f32 v233, v233, s62, v95
	v_med3_f32 v234, v234, s62, v95
	v_med3_f32 v235, v235, s62, v95
	v_med3_f32 v236, v236, s62, v95
	v_med3_f32 v237, v237, s62, v95
	v_med3_f32 v238, v238, s62, v95
	v_med3_f32 v239, v239, s62, v95
	v_med3_f32 v240, v240, s62, v95
	v_med3_f32 v241, v241, s62, v95
	v_mov_b32_e32 v242, 0
	v_mov_b32_e32 v243, 0
	v_mov_b32_e32 v244, 0
	v_mov_b32_e32 v245, 0
	v_cvt_pk_fp8_f32 v242, v226, v227
	v_cvt_pk_fp8_f32 v243, v230, v231
	v_cvt_pk_fp8_f32 v244, v234, v235
	v_cvt_pk_fp8_f32 v245, v238, v239
	v_cvt_pk_fp8_f32 v242, v228, v229 op_sel:[0,0,1]
	v_cvt_pk_fp8_f32 v243, v232, v233 op_sel:[0,0,1]
	v_cvt_pk_fp8_f32 v244, v236, v237 op_sel:[0,0,1]
	v_cvt_pk_fp8_f32 v245, v240, v241 op_sel:[0,0,1]
	s_nop 0
	global_store_dwordx4 v92, v[242:245], s[6:7]
	s_waitcnt vmcnt(12)
	v_mul_f32_e32 v176, v50, v176
	v_mul_f32_e32 v177, v50, v177
	v_mul_f32_e32 v178, v50, v178
	v_mul_f32_e32 v179, v50, v179
	ds_write_b128 v210, v[176:179]
	v_mul_f32_e32 v180, v51, v180
	v_mul_f32_e32 v181, v51, v181
	v_mul_f32_e32 v182, v51, v182
	v_mul_f32_e32 v183, v51, v183
	ds_write_b128 v210, v[180:183] offset:1024
	v_mul_f32_e32 v184, v52, v184
	v_mul_f32_e32 v185, v52, v185
	v_mul_f32_e32 v186, v52, v186
	v_mul_f32_e32 v187, v52, v187
	ds_write_b128 v210, v[184:187] offset:2048
	v_mul_f32_e32 v188, v53, v188
	v_mul_f32_e32 v189, v53, v189
	v_mul_f32_e32 v190, v53, v190
	v_mul_f32_e32 v191, v53, v191
	ds_write_b128 v210, v[188:191] offset:3072
	v_mul_f32_e32 v192, v54, v192
	v_mul_f32_e32 v193, v54, v193
	v_mul_f32_e32 v194, v54, v194
	v_mul_f32_e32 v195, v54, v195
	ds_write_b128 v210, v[192:195] offset:4096
	v_mul_f32_e32 v196, v55, v196
	v_mul_f32_e32 v197, v55, v197
	v_mul_f32_e32 v198, v55, v198
	v_mul_f32_e32 v199, v55, v199
	ds_write_b128 v210, v[196:199] offset:5120
	v_mul_f32_e32 v200, v56, v200
	v_mul_f32_e32 v201, v56, v201
	v_mul_f32_e32 v202, v56, v202
	v_mul_f32_e32 v203, v56, v203
	ds_write_b128 v210, v[200:203] offset:6144
	v_mul_f32_e32 v204, v57, v204
	v_mul_f32_e32 v205, v57, v205
	v_mul_f32_e32 v206, v57, v206
	v_mul_f32_e32 v207, v57, v207
	ds_write_b128 v210, v[204:207] offset:7168
	s_waitcnt lgkmcnt(0)
	s_barrier
; #define GAS __attribute__((address_space(1)))
; #define LAS __attribute__((address_space(3)))
; #define LDS_WAIT() asm volatile("s_waitcnt lgkmcnt(0)" ::: "memory")
; __device__ __forceinline__ int src_col_in(int c) {
;     if (c < 5120) { const int blk = c >> 7, p = c & 127; const bool rope = blk < 16 || ((((blk - 16) >> 2) & 1) == 0); const int d = rope ? (p >> 1) + 64 * (p & 1) : p; return blk * 128 + d; }
;     if (c < OFF_Z) return c + 2096;
;     if (c < OFF_G) return c - 4048;
;     if (c < OFF_DT) return 5120 + (c - OFF_G);
;     if (c < NSRC) return c;
;     return -1;
; }
;     const int pr = item >> 1, kb = 2 * (pr / nblk) + (item & 1), nb = pr % nblk, k0 = 64 * kb, n0 = 32 * nb;
;     const int nr = n0 + (lane & 31); const int sc = MAP == 1 ? src_col_in(nr) : nr;
;     float v[32];
; #pragma unroll
;     for (int i = 0; i < 32; ++i) v[i] = sc >= 0 ? W[(size_t)(k0 + 2 * i + (lane >> 5)) * Nsrc + sc] : 0.f;
; #pragma unroll
;     for (int i = 0; i < 32; ++i) { const int k = k0 + 2 * i + (lane >> 5); float x = v[i] * wscale; if (KS) x *= (k < ksplit ? ksA[k] : ksB[k - ksplit]); scr[(2 * i + (lane >> 5)) * 33 + (lane & 31)] = x; }
;     LDS_WAIT(); asm volatile("" ::: "memory");
;     const int c = lane & 7;
; #pragma unroll
;     for (int j = 0; j < 4; ++j) { const int n = (lane >> 3) + 8 * j; const LAS float* s = scr + (8 * c) * 33 + n;
;         const unsigned long long o = (unsigned long long)pg8::pk4_fp8(s[0 * 33], s[1 * 33], s[2 * 33], s[3 * 33]) | ((unsigned long long)pg8::pk4_fp8(s[4 * 33], s[5 * 33], s[6 * 33], s[7 * 33]) << 32);
;         *(GAS unsigned long long*)(WT + (size_t)(n0 + n) * K + k0 + 8 * c) = o; }
;     LDS_WAIT(); asm volatile("" ::: "memory");
; }
	s_add_i32 s24, s23, 80
	s_lshl_b32 s20, s24, 7
	s_cmp_lt_u32 s24, 40
	s_cselect_b32 s21, 0, 0x830
	s_cmp_lt_u32 s24, 72
	s_cselect_b32 s21, s21, 0xfffff030
	s_add_i32 s20, s20, s21
	s_lshl_b32 s20, s20, 2
	s_add_u32 s8, s50, s20
	s_addc_u32 s9, s51, 0
	global_load_dwordx4 v[176:179], v76, s[8:9]
	s_add_u32 s8, s8, 0x16280
	s_addc_u32 s9, s9, 0
	global_load_dwordx4 v[180:183], v76, s[8:9]
	s_add_u32 s8, s8, 0x16280
	s_addc_u32 s9, s9, 0
	global_load_dwordx4 v[184:187], v76, s[8:9]
	s_add_u32 s8, s8, 0x16280
	s_addc_u32 s9, s9, 0
	global_load_dwordx4 v[188:191], v76, s[8:9]
	s_add_u32 s8, s8, 0x16280
	s_addc_u32 s9, s9, 0
	global_load_dwordx4 v[192:195], v76, s[8:9]
	s_add_u32 s8, s8, 0x16280
	s_addc_u32 s9, s9, 0
	global_load_dwordx4 v[196:199], v76, s[8:9]
	s_add_u32 s8, s8, 0x16280
	s_addc_u32 s9, s9, 0
	global_load_dwordx4 v[200:203], v76, s[8:9]
	s_add_u32 s8, s8, 0x16280
	s_addc_u32 s9, s9, 0
	global_load_dwordx4 v[204:207], v76, s[8:9]
	s_add_i32 s24, s23, 64
	s_mul_i32 s20, s24, 0x80000
	s_add_u32 s6, s52, s20
	s_addc_u32 s7, s53, 0
	s_cmp_lt_u32 s24, 16
	s_cselect_b32 s20, 1, 0
	s_sub_i32 s21, s24, 16
	s_bitcmp0_b32 s21, 2
	s_cselect_b32 s21, 1, 0
	s_cmp_lt_u32 s24, 40
	s_cselect_b32 s21, s21, 0
	s_or_b32 s20, s20, s21
	s_cmp_lg_u32 s20, 0
	s_cselect_b64 s[20:21], -1, 0
	v_cndmask_b32_e64 v91, v77, v81, s[20:21]
	v_cndmask_b32_e64 v92, v78, v82, s[20:21]
	ds_read_b32 v226, v212
	ds_read_b32 v227, v212 offset:512
	ds_read_b32 v228, v212 offset:1024
	ds_read_b32 v229, v212 offset:1536
	ds_read_b32 v230, v212 offset:2048
	ds_read_b32 v231, v212 offset:2560
	ds_read_b32 v232, v212 offset:3072
	ds_read_b32 v233, v212 offset:3584
	ds_read_b32 v234, v212 offset:4096
	ds_read_b32 v235, v212 offset:4608
	ds_read_b32 v236, v212 offset:5120
	ds_read_b32 v237, v212 offset:5632
	ds_read_b32 v238, v212 offset:6144
	ds_read_b32 v239, v212 offset:6656
	ds_read_b32 v240, v212 offset:7168
	ds_read_b32 v241, v212 offset:7680
	s_waitcnt lgkmcnt(0)
	v_max_f32_e32 v226, v226, v226
	v_max_f32_e32 v227, v227, v227
	v_max_f32_e32 v228, v228, v228
	v_max_f32_e32 v229, v229, v229
	v_max_f32_e32 v230, v230, v230
	v_max_f32_e32 v231, v231, v231
	v_max_f32_e32 v232, v232, v232
	v_max_f32_e32 v233, v233, v233
	v_max_f32_e32 v234, v234, v234
	v_max_f32_e32 v235, v235, v235
	v_max_f32_e32 v236, v236, v236
	v_max_f32_e32 v237, v237, v237
	v_max_f32_e32 v238, v238, v238
	v_max_f32_e32 v239, v239, v239
	v_max_f32_e32 v240, v240, v240
	v_max_f32_e32 v241, v241, v241
	v_med3_f32 v226, v226, s62, v95
	v_med3_f32 v227, v227, s62, v95
	v_med3_f32 v228, v228, s62, v95
	v_med3_f32 v229, v229, s62, v95
	v_med3_f32 v230, v230, s62, v95
	v_med3_f32 v231, v231, s62, v95
	v_med3_f32 v232, v232, s62, v95
	v_med3_f32 v233, v233, s62, v95
	v_med3_f32 v234, v234, s62, v95
	v_med3_f32 v235, v235, s62, v95
	v_med3_f32 v236, v236, s62, v95
	v_med3_f32 v237, v237, s62, v95
	v_med3_f32 v238, v238, s62, v95
	v_med3_f32 v239, v239, s62, v95
	v_med3_f32 v240, v240, s62, v95
	v_med3_f32 v241, v241, s62, v95
	v_mov_b32_e32 v242, 0
	v_mov_b32_e32 v243, 0
	v_mov_b32_e32 v244, 0
	v_mov_b32_e32 v245, 0
	v_cvt_pk_fp8_f32 v242, v226, v227
	v_cvt_pk_fp8_f32 v243, v230, v231
	v_cvt_pk_fp8_f32 v244, v234, v235
	v_cvt_pk_fp8_f32 v245, v238, v239
	v_cvt_pk_fp8_f32 v242, v228, v229 op_sel:[0,0,1]
	v_cvt_pk_fp8_f32 v243, v232, v233 op_sel:[0,0,1]
	v_cvt_pk_fp8_f32 v244, v236, v237 op_sel:[0,0,1]
	v_cvt_pk_fp8_f32 v245, v240, v241 op_sel:[0,0,1]
	s_nop 0
	global_store_dwordx4 v91, v[242:245], s[6:7]
	ds_read_b32 v226, v214
	ds_read_b32 v227, v214 offset:512
	ds_read_b32 v228, v214 offset:1024
	ds_read_b32 v229, v214 offset:1536
	ds_read_b32 v230, v214 offset:2048
	ds_read_b32 v231, v214 offset:2560
	ds_read_b32 v232, v214 offset:3072
	ds_read_b32 v233, v214 offset:3584
	ds_read_b32 v234, v214 offset:4096
	ds_read_b32 v235, v214 offset:4608
	ds_read_b32 v236, v214 offset:5120
	ds_read_b32 v237, v214 offset:5632
	ds_read_b32 v238, v214 offset:6144
	ds_read_b32 v239, v214 offset:6656
	ds_read_b32 v240, v214 offset:7168
	ds_read_b32 v241, v214 offset:7680
	s_waitcnt lgkmcnt(0)
	v_max_f32_e32 v226, v226, v226
	v_max_f32_e32 v227, v227, v227
	v_max_f32_e32 v228, v228, v228
	v_max_f32_e32 v229, v229, v229
	v_max_f32_e32 v230, v230, v230
	v_max_f32_e32 v231, v231, v231
	v_max_f32_e32 v232, v232, v232
	v_max_f32_e32 v233, v233, v233
	v_max_f32_e32 v234, v234, v234
	v_max_f32_e32 v235, v235, v235
	v_max_f32_e32 v236, v236, v236
	v_max_f32_e32 v237, v237, v237
	v_max_f32_e32 v238, v238, v238
	v_max_f32_e32 v239, v239, v239
	v_max_f32_e32 v240, v240, v240
	v_max_f32_e32 v241, v241, v241
	v_med3_f32 v226, v226, s62, v95
	v_med3_f32 v227, v227, s62, v95
	v_med3_f32 v228, v228, s62, v95
	v_med3_f32 v229, v229, s62, v95
	v_med3_f32 v230, v230, s62, v95
	v_med3_f32 v231, v231, s62, v95
	v_med3_f32 v232, v232, s62, v95
	v_med3_f32 v233, v233, s62, v95
	v_med3_f32 v234, v234, s62, v95
	v_med3_f32 v235, v235, s62, v95
	v_med3_f32 v236, v236, s62, v95
	v_med3_f32 v237, v237, s62, v95
	v_med3_f32 v238, v238, s62, v95
	v_med3_f32 v239, v239, s62, v95
	v_med3_f32 v240, v240, s62, v95
	v_med3_f32 v241, v241, s62, v95
	v_mov_b32_e32 v242, 0
	v_mov_b32_e32 v243, 0
	v_mov_b32_e32 v244, 0
	v_mov_b32_e32 v245, 0
	v_cvt_pk_fp8_f32 v242, v226, v227
	v_cvt_pk_fp8_f32 v243, v230, v231
	v_cvt_pk_fp8_f32 v244, v234, v235
	v_cvt_pk_fp8_f32 v245, v238, v239
	v_cvt_pk_fp8_f32 v242, v228, v229 op_sel:[0,0,1]
	v_cvt_pk_fp8_f32 v243, v232, v233 op_sel:[0,0,1]
	v_cvt_pk_fp8_f32 v244, v236, v237 op_sel:[0,0,1]
	v_cvt_pk_fp8_f32 v245, v240, v241 op_sel:[0,0,1]
	s_nop 0
	global_store_dwordx4 v92, v[242:245], s[6:7]
	s_waitcnt vmcnt(12)
	v_mul_f32_e32 v144, v50, v144
	v_mul_f32_e32 v145, v50, v145
	v_mul_f32_e32 v146, v50, v146
	v_mul_f32_e32 v147, v50, v147
	ds_write_b128 v209, v[144:147]
	v_mul_f32_e32 v148, v51, v148
	v_mul_f32_e32 v149, v51, v149
	v_mul_f32_e32 v150, v51, v150
	v_mul_f32_e32 v151, v51, v151
	ds_write_b128 v209, v[148:151] offset:1024
	v_mul_f32_e32 v152, v52, v152
	v_mul_f32_e32 v153, v52, v153
	v_mul_f32_e32 v154, v52, v154
	v_mul_f32_e32 v155, v52, v155
	ds_write_b128 v209, v[152:155] offset:2048
	v_mul_f32_e32 v156, v53, v156
	v_mul_f32_e32 v157, v53, v157
	v_mul_f32_e32 v158, v53, v158
	v_mul_f32_e32 v159, v53, v159
	ds_write_b128 v209, v[156:159] offset:3072
	v_mul_f32_e32 v160, v54, v160
	v_mul_f32_e32 v161, v54, v161
	v_mul_f32_e32 v162, v54, v162
	v_mul_f32_e32 v163, v54, v163
	ds_write_b128 v209, v[160:163] offset:4096
	v_mul_f32_e32 v164, v55, v164
	v_mul_f32_e32 v165, v55, v165
	v_mul_f32_e32 v166, v55, v166
	v_mul_f32_e32 v167, v55, v167
	ds_write_b128 v209, v[164:167] offset:5120
	v_mul_f32_e32 v168, v56, v168
	v_mul_f32_e32 v169, v56, v169
	v_mul_f32_e32 v170, v56, v170
	v_mul_f32_e32 v171, v56, v171
	ds_write_b128 v209, v[168:171] offset:6144
	v_mul_f32_e32 v172, v57, v172
	v_mul_f32_e32 v173, v57, v173
	v_mul_f32_e32 v174, v57, v174
	v_mul_f32_e32 v175, v57, v175
	ds_write_b128 v209, v[172:175] offset:7168
	s_waitcnt lgkmcnt(0)
	s_barrier
; template <int MAP, bool KS, bool KPERM = false>
; __device__ __forceinline__ void p0_transpose_item(const float* W, int K, int Nsrc, int nblk, bf16* WT, const float* ksA, const float* ksB, int ksplit, LAS float* scr, int item, int lane) {
;     const int kb = item / nblk, nb = item % nblk, k0 = 64 * kb, n0 = 32 * nb;
;     const int nr = n0 + (lane & 31); const int sc = MAP == 1 ? src_col_in(nr) : (MAP == 2 ? nat_dim(nr) : nr);
;     float v[32];
; #pragma unroll
;     for (int i = 0; i < 32; ++i) { const int k = k0 + 2 * i + (lane >> 5); const int ksrc = KPERM ? ((k & ~127) + nat_dim(k & 127)) : k;
;         v[i] = sc >= 0 ? W[(size_t)ksrc * Nsrc + sc] : 0.f; }
; #pragma unroll
;     for (int i = 0; i < 32; ++i) { const int kk = 2 * i + (lane >> 5); const int k = k0 + kk;
;         if (KS) v[i] *= (k < ksplit ? ksA[k] : ksB[k - ksplit]);
;         scr[kk * 33 + (lane & 31)] = v[i]; }
;     LDS_WAIT(); asm volatile("" ::: "memory");
;     const int c = lane & 7;
; #pragma unroll
;     for (int j = 0; j < 4; ++j) { const int n = (lane >> 3) + 8 * j; const LAS float* s = scr + (8 * c) * 33 + n;
;         v4u o; o.x = pk2(s[0 * 33], s[1 * 33]); o.y = pk2(s[2 * 33], s[3 * 33]); o.z = pk2(s[4 * 33], s[5 * 33]); o.w = pk2(s[6 * 33], s[7 * 33]);
;     const int pr = item >> 1, kb = 2 * (pr / nblk) + (item & 1), nb = pr % nblk, k0 = 64 * kb, n0 = 32 * nb;
;     const int nr = n0 + (lane & 31); const int sc = MAP == 1 ? src_col_in(nr) : nr;
;     float v[32];
; #pragma unroll
;     for (int i = 0; i < 32; ++i) v[i] = sc >= 0 ? W[(size_t)(k0 + 2 * i + (lane >> 5)) * Nsrc + sc] : 0.f;
; #pragma unroll
;     for (int i = 0; i < 32; ++i) { const int k = k0 + 2 * i + (lane >> 5); float x = v[i] * wscale; if (KS) x *= (k < ksplit ? ksA[k] : ksB[k - ksplit]); scr[(2 * i + (lane >> 5)) * 33 + (lane & 31)] = x; }
;     LDS_WAIT(); asm volatile("" ::: "memory");
;     const int c = lane & 7;
; #pragma unroll
;     for (int j = 0; j < 4; ++j) { const int n = (lane >> 3) + 8 * j; const LAS float* s = scr + (8 * c) * 33 + n;
;         const unsigned long long o = (unsigned long long)pg8::pk4_fp8(s[0 * 33], s[1 * 33], s[2 * 33], s[3 * 33]) | ((unsigned long long)pg8::pk4_fp8(s[4 * 33], s[5 * 33], s[6 * 33], s[7 * 33]) << 32);
;         *(GAS unsigned long long*)(WT + (size_t)(n0 + n) * K + k0 + 8 * c) = o; }
;     LDS_WAIT(); asm volatile("" ::: "memory");
; }
	s_mov_b64 s[8:9], s[54:55]
	global_load_dwordx4 v[144:147], v75, s[8:9]
	s_add_u32 s8, s8, 0x8000
	s_addc_u32 s9, s9, 0
	global_load_dwordx4 v[148:151], v75, s[8:9]
	s_add_u32 s8, s8, 0x8000
	s_addc_u32 s9, s9, 0
	global_load_dwordx4 v[152:155], v75, s[8:9]
	s_add_u32 s8, s8, 0x8000
	s_addc_u32 s9, s9, 0
	global_load_dwordx4 v[156:159], v75, s[8:9]
	s_add_u32 s8, s8, 0x8000
	s_addc_u32 s9, s9, 0
	global_load_dwordx4 v[160:163], v75, s[8:9]
	s_add_u32 s8, s8, 0x8000
	s_addc_u32 s9, s9, 0
	global_load_dwordx4 v[164:167], v75, s[8:9]
	s_add_u32 s8, s8, 0x8000
	s_addc_u32 s9, s9, 0
	global_load_dwordx4 v[168:171], v75, s[8:9]
	s_add_u32 s8, s8, 0x8000
	s_addc_u32 s9, s9, 0
	global_load_dwordx4 v[172:175], v75, s[8:9]
	s_add_i32 s24, s23, 72
	s_mul_i32 s20, s24, 0x80000
	s_add_u32 s6, s52, s20
	s_addc_u32 s7, s53, 0
	s_cmp_lt_u32 s24, 16
	s_cselect_b32 s20, 1, 0
	s_sub_i32 s21, s24, 16
	s_bitcmp0_b32 s21, 2
	s_cselect_b32 s21, 1, 0
	s_cmp_lt_u32 s24, 40
	s_cselect_b32 s21, s21, 0
	s_or_b32 s20, s20, s21
	s_cmp_lg_u32 s20, 0
	s_cselect_b64 s[20:21], -1, 0
	v_cndmask_b32_e64 v91, v77, v81, s[20:21]
	v_cndmask_b32_e64 v92, v78, v82, s[20:21]
	ds_read_b32 v226, v211
	ds_read_b32 v227, v211 offset:512
	ds_read_b32 v228, v211 offset:1024
	ds_read_b32 v229, v211 offset:1536
	ds_read_b32 v230, v211 offset:2048
	ds_read_b32 v231, v211 offset:2560
	ds_read_b32 v232, v211 offset:3072
	ds_read_b32 v233, v211 offset:3584
	ds_read_b32 v234, v211 offset:4096
	ds_read_b32 v235, v211 offset:4608
	ds_read_b32 v236, v211 offset:5120
	ds_read_b32 v237, v211 offset:5632
	ds_read_b32 v238, v211 offset:6144
	ds_read_b32 v239, v211 offset:6656
	ds_read_b32 v240, v211 offset:7168
	ds_read_b32 v241, v211 offset:7680
	s_waitcnt lgkmcnt(0)
	v_max_f32_e32 v226, v226, v226
	v_max_f32_e32 v227, v227, v227
	v_max_f32_e32 v228, v228, v228
	v_max_f32_e32 v229, v229, v229
	v_max_f32_e32 v230, v230, v230
	v_max_f32_e32 v231, v231, v231
	v_max_f32_e32 v232, v232, v232
	v_max_f32_e32 v233, v233, v233
	v_max_f32_e32 v234, v234, v234
	v_max_f32_e32 v235, v235, v235
	v_max_f32_e32 v236, v236, v236
	v_max_f32_e32 v237, v237, v237
	v_max_f32_e32 v238, v238, v238
	v_max_f32_e32 v239, v239, v239
	v_max_f32_e32 v240, v240, v240
	v_max_f32_e32 v241, v241, v241
	v_med3_f32 v226, v226, s62, v95
	v_med3_f32 v227, v227, s62, v95
	v_med3_f32 v228, v228, s62, v95
	v_med3_f32 v229, v229, s62, v95
	v_med3_f32 v230, v230, s62, v95
	v_med3_f32 v231, v231, s62, v95
	v_med3_f32 v232, v232, s62, v95
	v_med3_f32 v233, v233, s62, v95
	v_med3_f32 v234, v234, s62, v95
	v_med3_f32 v235, v235, s62, v95
	v_med3_f32 v236, v236, s62, v95
	v_med3_f32 v237, v237, s62, v95
	v_med3_f32 v238, v238, s62, v95
	v_med3_f32 v239, v239, s62, v95
	v_med3_f32 v240, v240, s62, v95
	v_med3_f32 v241, v241, s62, v95
	v_mov_b32_e32 v242, 0
	v_mov_b32_e32 v243, 0
	v_mov_b32_e32 v244, 0
	v_mov_b32_e32 v245, 0
	v_cvt_pk_fp8_f32 v242, v226, v227
	v_cvt_pk_fp8_f32 v243, v230, v231
	v_cvt_pk_fp8_f32 v244, v234, v235
	v_cvt_pk_fp8_f32 v245, v238, v239
	v_cvt_pk_fp8_f32 v242, v228, v229 op_sel:[0,0,1]
	v_cvt_pk_fp8_f32 v243, v232, v233 op_sel:[0,0,1]
	v_cvt_pk_fp8_f32 v244, v236, v237 op_sel:[0,0,1]
	v_cvt_pk_fp8_f32 v245, v240, v241 op_sel:[0,0,1]
	s_nop 0
	global_store_dwordx4 v91, v[242:245], s[6:7]
	ds_read_b32 v226, v213
	ds_read_b32 v227, v213 offset:512
	ds_read_b32 v228, v213 offset:1024
	ds_read_b32 v229, v213 offset:1536
	ds_read_b32 v230, v213 offset:2048
	ds_read_b32 v231, v213 offset:2560
	ds_read_b32 v232, v213 offset:3072
	ds_read_b32 v233, v213 offset:3584
	ds_read_b32 v234, v213 offset:4096
	ds_read_b32 v235, v213 offset:4608
	ds_read_b32 v236, v213 offset:5120
	ds_read_b32 v237, v213 offset:5632
	ds_read_b32 v238, v213 offset:6144
	ds_read_b32 v239, v213 offset:6656
	ds_read_b32 v240, v213 offset:7168
	ds_read_b32 v241, v213 offset:7680
	s_waitcnt lgkmcnt(0)
	v_max_f32_e32 v226, v226, v226
	v_max_f32_e32 v227, v227, v227
	v_max_f32_e32 v228, v228, v228
	v_max_f32_e32 v229, v229, v229
	v_max_f32_e32 v230, v230, v230
	v_max_f32_e32 v231, v231, v231
	v_max_f32_e32 v232, v232, v232
	v_max_f32_e32 v233, v233, v233
	v_max_f32_e32 v234, v234, v234
	v_max_f32_e32 v235, v235, v235
	v_max_f32_e32 v236, v236, v236
	v_max_f32_e32 v237, v237, v237
	v_max_f32_e32 v238, v238, v238
	v_max_f32_e32 v239, v239, v239
	v_max_f32_e32 v240, v240, v240
	v_max_f32_e32 v241, v241, v241
	v_med3_f32 v226, v226, s62, v95
	v_med3_f32 v227, v227, s62, v95
	v_med3_f32 v228, v228, s62, v95
	v_med3_f32 v229, v229, s62, v95
	v_med3_f32 v230, v230, s62, v95
	v_med3_f32 v231, v231, s62, v95
	v_med3_f32 v232, v232, s62, v95
	v_med3_f32 v233, v233, s62, v95
	v_med3_f32 v234, v234, s62, v95
	v_med3_f32 v235, v235, s62, v95
	v_med3_f32 v236, v236, s62, v95
	v_med3_f32 v237, v237, s62, v95
	v_med3_f32 v238, v238, s62, v95
	v_med3_f32 v239, v239, s62, v95
	v_med3_f32 v240, v240, s62, v95
	v_med3_f32 v241, v241, s62, v95
	v_mov_b32_e32 v242, 0
	v_mov_b32_e32 v243, 0
	v_mov_b32_e32 v244, 0
	v_mov_b32_e32 v245, 0
	v_cvt_pk_fp8_f32 v242, v226, v227
	v_cvt_pk_fp8_f32 v243, v230, v231
	v_cvt_pk_fp8_f32 v244, v234, v235
	v_cvt_pk_fp8_f32 v245, v238, v239
	v_cvt_pk_fp8_f32 v242, v228, v229 op_sel:[0,0,1]
	v_cvt_pk_fp8_f32 v243, v232, v233 op_sel:[0,0,1]
	v_cvt_pk_fp8_f32 v244, v236, v237 op_sel:[0,0,1]
	v_cvt_pk_fp8_f32 v245, v240, v241 op_sel:[0,0,1]
	s_nop 0
	global_store_dwordx4 v92, v[242:245], s[6:7]
	s_waitcnt vmcnt(12)
	v_mul_f32_e32 v176, v50, v176
	v_mul_f32_e32 v177, v50, v177
	v_mul_f32_e32 v178, v50, v178
	v_mul_f32_e32 v179, v50, v179
	ds_write_b128 v210, v[176:179]
	v_mul_f32_e32 v180, v51, v180
	v_mul_f32_e32 v181, v51, v181
	v_mul_f32_e32 v182, v51, v182
	v_mul_f32_e32 v183, v51, v183
	ds_write_b128 v210, v[180:183] offset:1024
	v_mul_f32_e32 v184, v52, v184
	v_mul_f32_e32 v185, v52, v185
	v_mul_f32_e32 v186, v52, v186
	v_mul_f32_e32 v187, v52, v187
	ds_write_b128 v210, v[184:187] offset:2048
	v_mul_f32_e32 v188, v53, v188
	v_mul_f32_e32 v189, v53, v189
	v_mul_f32_e32 v190, v53, v190
	v_mul_f32_e32 v191, v53, v191
	ds_write_b128 v210, v[188:191] offset:3072
	v_mul_f32_e32 v192, v54, v192
	v_mul_f32_e32 v193, v54, v193
	v_mul_f32_e32 v194, v54, v194
	v_mul_f32_e32 v195, v54, v195
	ds_write_b128 v210, v[192:195] offset:4096
	v_mul_f32_e32 v196, v55, v196
	v_mul_f32_e32 v197, v55, v197
	v_mul_f32_e32 v198, v55, v198
	v_mul_f32_e32 v199, v55, v199
	ds_write_b128 v210, v[196:199] offset:5120
	v_mul_f32_e32 v200, v56, v200
	v_mul_f32_e32 v201, v56, v201
	v_mul_f32_e32 v202, v56, v202
	v_mul_f32_e32 v203, v56, v203
	ds_write_b128 v210, v[200:203] offset:6144
	v_mul_f32_e32 v204, v57, v204
	v_mul_f32_e32 v205, v57, v205
	v_mul_f32_e32 v206, v57, v206
	v_mul_f32_e32 v207, v57, v207
	ds_write_b128 v210, v[204:207] offset:7168
	s_waitcnt lgkmcnt(0)
	s_barrier
; template <int MAP, bool KS, bool KPERM = false>
; __device__ __forceinline__ void p0_transpose_item(const float* W, int K, int Nsrc, int nblk, bf16* WT, const float* ksA, const float* ksB, int ksplit, LAS float* scr, int item, int lane) {
;     const int kb = item / nblk, nb = item % nblk, k0 = 64 * kb, n0 = 32 * nb;
;     const int nr = n0 + (lane & 31); const int sc = MAP == 1 ? src_col_in(nr) : (MAP == 2 ? nat_dim(nr) : nr);
;     float v[32];
; #pragma unroll
;     for (int i = 0; i < 32; ++i) { const int k = k0 + 2 * i + (lane >> 5); const int ksrc = KPERM ? ((k & ~127) + nat_dim(k & 127)) : k;
;         v[i] = sc >= 0 ? W[(size_t)ksrc * Nsrc + sc] : 0.f; }
; #pragma unroll
;     for (int i = 0; i < 32; ++i) { const int kk = 2 * i + (lane >> 5); const int k = k0 + kk;
;         if (KS) v[i] *= (k < ksplit ? ksA[k] : ksB[k - ksplit]);
;         scr[kk * 33 + (lane & 31)] = v[i]; }
;     LDS_WAIT(); asm volatile("" ::: "memory");
;     const int c = lane & 7;
; #pragma unroll
;     for (int j = 0; j < 4; ++j) { const int n = (lane >> 3) + 8 * j; const LAS float* s = scr + (8 * c) * 33 + n;
;         v4u o; o.x = pk2(s[0 * 33], s[1 * 33]); o.y = pk2(s[2 * 33], s[3 * 33]); o.z = pk2(s[4 * 33], s[5 * 33]); o.w = pk2(s[6 * 33], s[7 * 33]);
;     const int pr = item >> 1, kb = 2 * (pr / nblk) + (item & 1), nb = pr % nblk, k0 = 64 * kb, n0 = 32 * nb;
;     const int nr = n0 + (lane & 31); const int sc = MAP == 1 ? src_col_in(nr) : nr;
;     float v[32];
; #pragma unroll
;     for (int i = 0; i < 32; ++i) v[i] = sc >= 0 ? W[(size_t)(k0 + 2 * i + (lane >> 5)) * Nsrc + sc] : 0.f;
; #pragma unroll
;     for (int i = 0; i < 32; ++i) { const int k = k0 + 2 * i + (lane >> 5); float x = v[i] * wscale; if (KS) x *= (k < ksplit ? ksA[k] : ksB[k - ksplit]); scr[(2 * i + (lane >> 5)) * 33 + (lane & 31)] = x; }
;     LDS_WAIT(); asm volatile("" ::: "memory");
;     const int c = lane & 7;
; #pragma unroll
;     for (int j = 0; j < 4; ++j) { const int n = (lane >> 3) + 8 * j; const LAS float* s = scr + (8 * c) * 33 + n;
;         const unsigned long long o = (unsigned long long)pg8::pk4_fp8(s[0 * 33], s[1 * 33], s[2 * 33], s[3 * 33]) | ((unsigned long long)pg8::pk4_fp8(s[4 * 33], s[5 * 33], s[6 * 33], s[7 * 33]) << 32);
;         *(GAS unsigned long long*)(WT + (size_t)(n0 + n) * K + k0 + 8 * c) = o; }
;     LDS_WAIT(); asm volatile("" ::: "memory");
; }
	s_add_u32 s8, s54, 0x1000
	s_addc_u32 s9, s55, 0
	global_load_dwordx4 v[176:179], v75, s[8:9]
	s_add_u32 s8, s8, 0x8000
	s_addc_u32 s9, s9, 0
	global_load_dwordx4 v[180:183], v75, s[8:9]
	s_add_u32 s8, s8, 0x8000
	s_addc_u32 s9, s9, 0
	global_load_dwordx4 v[184:187], v75, s[8:9]
	s_add_u32 s8, s8, 0x8000
	s_addc_u32 s9, s9, 0
	global_load_dwordx4 v[188:191], v75, s[8:9]
	s_add_u32 s8, s8, 0x8000
	s_addc_u32 s9, s9, 0
	global_load_dwordx4 v[192:195], v75, s[8:9]
	s_add_u32 s8, s8, 0x8000
	s_addc_u32 s9, s9, 0
	global_load_dwordx4 v[196:199], v75, s[8:9]
	s_add_u32 s8, s8, 0x8000
	s_addc_u32 s9, s9, 0
	global_load_dwordx4 v[200:203], v75, s[8:9]
	s_add_u32 s8, s8, 0x8000
	s_addc_u32 s9, s9, 0
	global_load_dwordx4 v[204:207], v75, s[8:9]
	s_add_i32 s24, s23, 80
	s_mul_i32 s20, s24, 0x80000
	s_add_u32 s6, s52, s20
	s_addc_u32 s7, s53, 0
	s_cmp_lt_u32 s24, 16
	s_cselect_b32 s20, 1, 0
	s_sub_i32 s21, s24, 16
	s_bitcmp0_b32 s21, 2
	s_cselect_b32 s21, 1, 0
	s_cmp_lt_u32 s24, 40
	s_cselect_b32 s21, s21, 0
	s_or_b32 s20, s20, s21
	s_cmp_lg_u32 s20, 0
	s_cselect_b64 s[20:21], -1, 0
	v_cndmask_b32_e64 v91, v77, v81, s[20:21]
	v_cndmask_b32_e64 v92, v78, v82, s[20:21]
	ds_read_b32 v226, v212
	ds_read_b32 v227, v212 offset:512
	ds_read_b32 v228, v212 offset:1024
	ds_read_b32 v229, v212 offset:1536
	ds_read_b32 v230, v212 offset:2048
	ds_read_b32 v231, v212 offset:2560
	ds_read_b32 v232, v212 offset:3072
	ds_read_b32 v233, v212 offset:3584
	ds_read_b32 v234, v212 offset:4096
	ds_read_b32 v235, v212 offset:4608
	ds_read_b32 v236, v212 offset:5120
	ds_read_b32 v237, v212 offset:5632
	ds_read_b32 v238, v212 offset:6144
	ds_read_b32 v239, v212 offset:6656
	ds_read_b32 v240, v212 offset:7168
	ds_read_b32 v241, v212 offset:7680
	s_waitcnt lgkmcnt(0)
	v_max_f32_e32 v226, v226, v226
	v_max_f32_e32 v227, v227, v227
	v_max_f32_e32 v228, v228, v228
	v_max_f32_e32 v229, v229, v229
	v_max_f32_e32 v230, v230, v230
	v_max_f32_e32 v231, v231, v231
	v_max_f32_e32 v232, v232, v232
	v_max_f32_e32 v233, v233, v233
	v_max_f32_e32 v234, v234, v234
	v_max_f32_e32 v235, v235, v235
	v_max_f32_e32 v236, v236, v236
	v_max_f32_e32 v237, v237, v237
	v_max_f32_e32 v238, v238, v238
	v_max_f32_e32 v239, v239, v239
	v_max_f32_e32 v240, v240, v240
	v_max_f32_e32 v241, v241, v241
	v_med3_f32 v226, v226, s62, v95
	v_med3_f32 v227, v227, s62, v95
	v_med3_f32 v228, v228, s62, v95
	v_med3_f32 v229, v229, s62, v95
	v_med3_f32 v230, v230, s62, v95
	v_med3_f32 v231, v231, s62, v95
	v_med3_f32 v232, v232, s62, v95
	v_med3_f32 v233, v233, s62, v95
	v_med3_f32 v234, v234, s62, v95
	v_med3_f32 v235, v235, s62, v95
	v_med3_f32 v236, v236, s62, v95
	v_med3_f32 v237, v237, s62, v95
	v_med3_f32 v238, v238, s62, v95
	v_med3_f32 v239, v239, s62, v95
	v_med3_f32 v240, v240, s62, v95
	v_med3_f32 v241, v241, s62, v95
	v_mov_b32_e32 v242, 0
	v_mov_b32_e32 v243, 0
	v_mov_b32_e32 v244, 0
	v_mov_b32_e32 v245, 0
	v_cvt_pk_fp8_f32 v242, v226, v227
	v_cvt_pk_fp8_f32 v243, v230, v231
	v_cvt_pk_fp8_f32 v244, v234, v235
	v_cvt_pk_fp8_f32 v245, v238, v239
	v_cvt_pk_fp8_f32 v242, v228, v229 op_sel:[0,0,1]
	v_cvt_pk_fp8_f32 v243, v232, v233 op_sel:[0,0,1]
	v_cvt_pk_fp8_f32 v244, v236, v237 op_sel:[0,0,1]
	v_cvt_pk_fp8_f32 v245, v240, v241 op_sel:[0,0,1]
	s_nop 0
	global_store_dwordx4 v91, v[242:245], s[6:7]
	ds_read_b32 v226, v214
	ds_read_b32 v227, v214 offset:512
	ds_read_b32 v228, v214 offset:1024
	ds_read_b32 v229, v214 offset:1536
	ds_read_b32 v230, v214 offset:2048
	ds_read_b32 v231, v214 offset:2560
	ds_read_b32 v232, v214 offset:3072
	ds_read_b32 v233, v214 offset:3584
	ds_read_b32 v234, v214 offset:4096
	ds_read_b32 v235, v214 offset:4608
	ds_read_b32 v236, v214 offset:5120
	ds_read_b32 v237, v214 offset:5632
	ds_read_b32 v238, v214 offset:6144
	ds_read_b32 v239, v214 offset:6656
	ds_read_b32 v240, v214 offset:7168
	ds_read_b32 v241, v214 offset:7680
	s_waitcnt lgkmcnt(0)
	v_max_f32_e32 v226, v226, v226
	v_max_f32_e32 v227, v227, v227
	v_max_f32_e32 v228, v228, v228
	v_max_f32_e32 v229, v229, v229
	v_max_f32_e32 v230, v230, v230
	v_max_f32_e32 v231, v231, v231
	v_max_f32_e32 v232, v232, v232
	v_max_f32_e32 v233, v233, v233
	v_max_f32_e32 v234, v234, v234
	v_max_f32_e32 v235, v235, v235
	v_max_f32_e32 v236, v236, v236
	v_max_f32_e32 v237, v237, v237
	v_max_f32_e32 v238, v238, v238
	v_max_f32_e32 v239, v239, v239
	v_max_f32_e32 v240, v240, v240
	v_max_f32_e32 v241, v241, v241
	v_med3_f32 v226, v226, s62, v95
	v_med3_f32 v227, v227, s62, v95
	v_med3_f32 v228, v228, s62, v95
	v_med3_f32 v229, v229, s62, v95
	v_med3_f32 v230, v230, s62, v95
	v_med3_f32 v231, v231, s62, v95
	v_med3_f32 v232, v232, s62, v95
	v_med3_f32 v233, v233, s62, v95
	v_med3_f32 v234, v234, s62, v95
	v_med3_f32 v235, v235, s62, v95
	v_med3_f32 v236, v236, s62, v95
	v_med3_f32 v237, v237, s62, v95
	v_med3_f32 v238, v238, s62, v95
	v_med3_f32 v239, v239, s62, v95
	v_med3_f32 v240, v240, s62, v95
	v_med3_f32 v241, v241, s62, v95
	v_mov_b32_e32 v242, 0
	v_mov_b32_e32 v243, 0
	v_mov_b32_e32 v244, 0
	v_mov_b32_e32 v245, 0
	v_cvt_pk_fp8_f32 v242, v226, v227
	v_cvt_pk_fp8_f32 v243, v230, v231
	v_cvt_pk_fp8_f32 v244, v234, v235
	v_cvt_pk_fp8_f32 v245, v238, v239
	v_cvt_pk_fp8_f32 v242, v228, v229 op_sel:[0,0,1]
	v_cvt_pk_fp8_f32 v243, v232, v233 op_sel:[0,0,1]
	v_cvt_pk_fp8_f32 v244, v236, v237 op_sel:[0,0,1]
	v_cvt_pk_fp8_f32 v245, v240, v241 op_sel:[0,0,1]
	s_nop 0
	global_store_dwordx4 v92, v[242:245], s[6:7]
	s_waitcnt vmcnt(12)
	v_mul_f32_e32 v144, v58, v144
	v_mul_f32_e32 v145, v58, v145
	v_mul_f32_e32 v146, v58, v146
	v_mul_f32_e32 v147, v58, v147
	ds_write_b128 v209, v[144:147]
	v_mul_f32_e32 v148, v59, v148
	v_mul_f32_e32 v149, v59, v149
	v_mul_f32_e32 v150, v59, v150
	v_mul_f32_e32 v151, v59, v151
	ds_write_b128 v209, v[148:151] offset:1024
	v_mul_f32_e32 v152, v60, v152
	v_mul_f32_e32 v153, v60, v153
	v_mul_f32_e32 v154, v60, v154
	v_mul_f32_e32 v155, v60, v155
	ds_write_b128 v209, v[152:155] offset:2048
	v_mul_f32_e32 v156, v61, v156
	v_mul_f32_e32 v157, v61, v157
	v_mul_f32_e32 v158, v61, v158
	v_mul_f32_e32 v159, v61, v159
	ds_write_b128 v209, v[156:159] offset:3072
	v_mul_f32_e32 v160, v62, v160
	v_mul_f32_e32 v161, v62, v161
	v_mul_f32_e32 v162, v62, v162
	v_mul_f32_e32 v163, v62, v163
	ds_write_b128 v209, v[160:163] offset:4096
	v_mul_f32_e32 v164, v63, v164
	v_mul_f32_e32 v165, v63, v165
	v_mul_f32_e32 v166, v63, v166
	v_mul_f32_e32 v167, v63, v167
	ds_write_b128 v209, v[164:167] offset:5120
	v_mul_f32_e32 v168, v64, v168
	v_mul_f32_e32 v169, v64, v169
	v_mul_f32_e32 v170, v64, v170
	v_mul_f32_e32 v171, v64, v171
	ds_write_b128 v209, v[168:171] offset:6144
	v_mul_f32_e32 v172, v65, v172
	v_mul_f32_e32 v173, v65, v173
	v_mul_f32_e32 v174, v65, v174
	v_mul_f32_e32 v175, v65, v175
	ds_write_b128 v209, v[172:175] offset:7168
	s_waitcnt lgkmcnt(0)
	s_barrier
; #define GAS __attribute__((address_space(1)))
; #define LAS __attribute__((address_space(3)))
; #define LDS_WAIT() asm volatile("s_waitcnt lgkmcnt(0)" ::: "memory")
; __device__ __forceinline__ int nat_dim(int p) { return (p >> 1) + 64 * (p & 1); }
; __device__ __forceinline__ unsigned f2bf(float f) { unsigned u = __builtin_bit_cast(unsigned, f); return (u + 0x7fffu + ((u >> 16) & 1u)) >> 16; }
; __device__ __forceinline__ unsigned pk2(float lo, float hi) { return f2bf(lo) | (f2bf(hi) << 16); }
; template <int MAP, bool KS, bool KPERM = false>
; __device__ __forceinline__ void p0_transpose_item(const float* W, int K, int Nsrc, int nblk, bf16* WT, const float* ksA, const float* ksB, int ksplit, LAS float* scr, int item, int lane) {
;     const int kb = item / nblk, nb = item % nblk, k0 = 64 * kb, n0 = 32 * nb;
;     const int nr = n0 + (lane & 31); const int sc = MAP == 1 ? src_col_in(nr) : (MAP == 2 ? nat_dim(nr) : nr);
;     float v[32];
; #pragma unroll
;     for (int i = 0; i < 32; ++i) { const int k = k0 + 2 * i + (lane >> 5); const int ksrc = KPERM ? ((k & ~127) + nat_dim(k & 127)) : k;
;         v[i] = sc >= 0 ? W[(size_t)ksrc * Nsrc + sc] : 0.f; }
; #pragma unroll
;     for (int i = 0; i < 32; ++i) { const int kk = 2 * i + (lane >> 5); const int k = k0 + kk;
;         if (KS) v[i] *= (k < ksplit ? ksA[k] : ksB[k - ksplit]);
;         scr[kk * 33 + (lane & 31)] = v[i]; }
;     LDS_WAIT(); asm volatile("" ::: "memory");
;     const int c = lane & 7;
; #pragma unroll
;     for (int j = 0; j < 4; ++j) { const int n = (lane >> 3) + 8 * j; const LAS float* s = scr + (8 * c) * 33 + n;
;         v4u o; o.x = pk2(s[0 * 33], s[1 * 33]); o.y = pk2(s[2 * 33], s[3 * 33]); o.z = pk2(s[4 * 33], s[5 * 33]); o.w = pk2(s[6 * 33], s[7 * 33]);
;         *(GAS v4u*)(WT + (size_t)(n0 + n) * K + k0 + 8 * c) = o; }
;     LDS_WAIT(); asm volatile("" ::: "memory");
; }
	s_add_u32 s8, s54, 0x2000
	s_addc_u32 s9, s55, 0
	global_load_dwordx4 v[144:147], v75, s[8:9]
	s_add_u32 s8, s8, 0x8000
	s_addc_u32 s9, s9, 0
	global_load_dwordx4 v[148:151], v75, s[8:9]
	s_add_u32 s8, s8, 0x8000
	s_addc_u32 s9, s9, 0
	global_load_dwordx4 v[152:155], v75, s[8:9]
	s_add_u32 s8, s8, 0x8000
	s_addc_u32 s9, s9, 0
	global_load_dwordx4 v[156:159], v75, s[8:9]
	s_add_u32 s8, s8, 0x8000
	s_addc_u32 s9, s9, 0
	global_load_dwordx4 v[160:163], v75, s[8:9]
	s_add_u32 s8, s8, 0x8000
	s_addc_u32 s9, s9, 0
	global_load_dwordx4 v[164:167], v75, s[8:9]
	s_add_u32 s8, s8, 0x8000
	s_addc_u32 s9, s9, 0
	global_load_dwordx4 v[168:171], v75, s[8:9]
	s_add_u32 s8, s8, 0x8000
	s_addc_u32 s9, s9, 0
	global_load_dwordx4 v[172:175], v75, s[8:9]
	s_mov_b64 s[6:7], s[56:57]
	ds_read_b32 v226, v112
	ds_read_b32 v227, v112 offset:512
	ds_read_b32 v228, v112 offset:1024
	ds_read_b32 v229, v112 offset:1536
	ds_read_b32 v230, v112 offset:2048
	ds_read_b32 v231, v112 offset:2560
	ds_read_b32 v232, v112 offset:3072
	ds_read_b32 v233, v112 offset:3584
	s_waitcnt lgkmcnt(0)
	v_bfe_u32 v120, v226, 16, 1
	v_bfe_u32 v121, v227, 16, 1
	v_bfe_u32 v122, v228, 16, 1
	v_bfe_u32 v123, v229, 16, 1
	v_bfe_u32 v124, v230, 16, 1
	v_bfe_u32 v125, v231, 16, 1
	v_bfe_u32 v126, v232, 16, 1
	v_bfe_u32 v127, v233, 16, 1
	v_add3_u32 v226, v226, v120, s63
	v_add3_u32 v227, v227, v121, s63
	v_add3_u32 v228, v228, v122, s63
	v_add3_u32 v229, v229, v123, s63
	v_add3_u32 v230, v230, v124, s63
	v_add3_u32 v231, v231, v125, s63
	v_add3_u32 v232, v232, v126, s63
	v_add3_u32 v233, v233, v127, s63
	v_perm_b32 v242, v227, v226, s64
	v_perm_b32 v243, v229, v228, s64
	v_perm_b32 v244, v231, v230, s64
	v_perm_b32 v245, v233, v232, s64
	s_nop 0
	global_store_dwordx4 v83, v[242:245], s[6:7]
	ds_read_b32 v226, v114
	ds_read_b32 v227, v114 offset:512
	ds_read_b32 v228, v114 offset:1024
	ds_read_b32 v229, v114 offset:1536
	ds_read_b32 v230, v114 offset:2048
	ds_read_b32 v231, v114 offset:2560
	ds_read_b32 v232, v114 offset:3072
	ds_read_b32 v233, v114 offset:3584
	s_waitcnt lgkmcnt(0)
	v_bfe_u32 v120, v226, 16, 1
	v_bfe_u32 v121, v227, 16, 1
	v_bfe_u32 v122, v228, 16, 1
	v_bfe_u32 v123, v229, 16, 1
	v_bfe_u32 v124, v230, 16, 1
	v_bfe_u32 v125, v231, 16, 1
	v_bfe_u32 v126, v232, 16, 1
	v_bfe_u32 v127, v233, 16, 1
	v_add3_u32 v226, v226, v120, s63
	v_add3_u32 v227, v227, v121, s63
	v_add3_u32 v228, v228, v122, s63
	v_add3_u32 v229, v229, v123, s63
	v_add3_u32 v230, v230, v124, s63
	v_add3_u32 v231, v231, v125, s63
	v_add3_u32 v232, v232, v126, s63
	v_add3_u32 v233, v233, v127, s63
	v_perm_b32 v242, v227, v226, s64
	v_perm_b32 v243, v229, v228, s64
	v_perm_b32 v244, v231, v230, s64
	v_perm_b32 v245, v233, v232, s64
	s_nop 0
	global_store_dwordx4 v84, v[242:245], s[6:7]
	ds_read_b32 v226, v116
	ds_read_b32 v227, v116 offset:512
	ds_read_b32 v228, v116 offset:1024
	ds_read_b32 v229, v116 offset:1536
	ds_read_b32 v230, v116 offset:2048
	ds_read_b32 v231, v116 offset:2560
	ds_read_b32 v232, v116 offset:3072
	ds_read_b32 v233, v116 offset:3584
	s_waitcnt lgkmcnt(0)
	v_bfe_u32 v120, v226, 16, 1
	v_bfe_u32 v121, v227, 16, 1
	v_bfe_u32 v122, v228, 16, 1
	v_bfe_u32 v123, v229, 16, 1
	v_bfe_u32 v124, v230, 16, 1
	v_bfe_u32 v125, v231, 16, 1
	v_bfe_u32 v126, v232, 16, 1
	v_bfe_u32 v127, v233, 16, 1
	v_add3_u32 v226, v226, v120, s63
	v_add3_u32 v227, v227, v121, s63
	v_add3_u32 v228, v228, v122, s63
	v_add3_u32 v229, v229, v123, s63
	v_add3_u32 v230, v230, v124, s63
	v_add3_u32 v231, v231, v125, s63
	v_add3_u32 v232, v232, v126, s63
	v_add3_u32 v233, v233, v127, s63
	v_perm_b32 v242, v227, v226, s64
	v_perm_b32 v243, v229, v228, s64
	v_perm_b32 v244, v231, v230, s64
	v_perm_b32 v245, v233, v232, s64
	s_nop 0
	global_store_dwordx4 v85, v[242:245], s[6:7]
	ds_read_b32 v226, v118
	ds_read_b32 v227, v118 offset:512
	ds_read_b32 v228, v118 offset:1024
	ds_read_b32 v229, v118 offset:1536
	ds_read_b32 v230, v118 offset:2048
	ds_read_b32 v231, v118 offset:2560
	ds_read_b32 v232, v118 offset:3072
	ds_read_b32 v233, v118 offset:3584
	s_waitcnt lgkmcnt(0)
	v_bfe_u32 v120, v226, 16, 1
	v_bfe_u32 v121, v227, 16, 1
	v_bfe_u32 v122, v228, 16, 1
	v_bfe_u32 v123, v229, 16, 1
	v_bfe_u32 v124, v230, 16, 1
	v_bfe_u32 v125, v231, 16, 1
	v_bfe_u32 v126, v232, 16, 1
	v_bfe_u32 v127, v233, 16, 1
	v_add3_u32 v226, v226, v120, s63
	v_add3_u32 v227, v227, v121, s63
	v_add3_u32 v228, v228, v122, s63
	v_add3_u32 v229, v229, v123, s63
	v_add3_u32 v230, v230, v124, s63
	v_add3_u32 v231, v231, v125, s63
	v_add3_u32 v232, v232, v126, s63
	v_add3_u32 v233, v233, v127, s63
	v_perm_b32 v242, v227, v226, s64
	v_perm_b32 v243, v229, v228, s64
	v_perm_b32 v244, v231, v230, s64
	v_perm_b32 v245, v233, v232, s64
	s_nop 0
	global_store_dwordx4 v86, v[242:245], s[6:7]
	s_waitcnt vmcnt(14)
	v_mul_f32_e32 v176, v58, v176
	v_mul_f32_e32 v177, v58, v177
	v_mul_f32_e32 v178, v58, v178
	v_mul_f32_e32 v179, v58, v179
	ds_write_b128 v210, v[176:179]
	v_mul_f32_e32 v180, v59, v180
	v_mul_f32_e32 v181, v59, v181
	v_mul_f32_e32 v182, v59, v182
	v_mul_f32_e32 v183, v59, v183
	ds_write_b128 v210, v[180:183] offset:1024
	v_mul_f32_e32 v184, v60, v184
	v_mul_f32_e32 v185, v60, v185
	v_mul_f32_e32 v186, v60, v186
	v_mul_f32_e32 v187, v60, v187
	ds_write_b128 v210, v[184:187] offset:2048
	v_mul_f32_e32 v188, v61, v188
	v_mul_f32_e32 v189, v61, v189
	v_mul_f32_e32 v190, v61, v190
	v_mul_f32_e32 v191, v61, v191
	ds_write_b128 v210, v[188:191] offset:3072
	v_mul_f32_e32 v192, v62, v192
	v_mul_f32_e32 v193, v62, v193
	v_mul_f32_e32 v194, v62, v194
	v_mul_f32_e32 v195, v62, v195
	ds_write_b128 v210, v[192:195] offset:4096
	v_mul_f32_e32 v196, v63, v196
	v_mul_f32_e32 v197, v63, v197
	v_mul_f32_e32 v198, v63, v198
	v_mul_f32_e32 v199, v63, v199
	ds_write_b128 v210, v[196:199] offset:5120
	v_mul_f32_e32 v200, v64, v200
	v_mul_f32_e32 v201, v64, v201
	v_mul_f32_e32 v202, v64, v202
	v_mul_f32_e32 v203, v64, v203
	ds_write_b128 v210, v[200:203] offset:6144
	v_mul_f32_e32 v204, v65, v204
	v_mul_f32_e32 v205, v65, v205
	v_mul_f32_e32 v206, v65, v206
	v_mul_f32_e32 v207, v65, v207
	ds_write_b128 v210, v[204:207] offset:7168
	s_waitcnt lgkmcnt(0)
	s_barrier
; #define GAS __attribute__((address_space(1)))
; #define LAS __attribute__((address_space(3)))
; #define LDS_WAIT() asm volatile("s_waitcnt lgkmcnt(0)" ::: "memory")
; __device__ __forceinline__ unsigned pk2(float lo, float hi) { return f2bf(lo) | (f2bf(hi) << 16); }
; __device__ __forceinline__ int nat_dim(int p) { return (p >> 1) + 64 * (p & 1); }
; template <int MAP, bool KS, bool KPERM = false>
; __device__ __forceinline__ void p0_transpose_item(const float* W, int K, int Nsrc, int nblk, bf16* WT, const float* ksA, const float* ksB, int ksplit, LAS float* scr, int item, int lane) {
;     const int kb = item / nblk, nb = item % nblk, k0 = 64 * kb, n0 = 32 * nb;
;     const int nr = n0 + (lane & 31); const int sc = MAP == 1 ? src_col_in(nr) : (MAP == 2 ? nat_dim(nr) : nr);
;     float v[32];
; #pragma unroll
;     for (int i = 0; i < 32; ++i) { const int k = k0 + 2 * i + (lane >> 5); const int ksrc = KPERM ? ((k & ~127) + nat_dim(k & 127)) : k;
;         v[i] = sc >= 0 ? W[(size_t)ksrc * Nsrc + sc] : 0.f; }
; #pragma unroll
;     for (int i = 0; i < 32; ++i) { const int kk = 2 * i + (lane >> 5); const int k = k0 + kk;
;         if (KS) v[i] *= (k < ksplit ? ksA[k] : ksB[k - ksplit]);
;         scr[kk * 33 + (lane & 31)] = v[i]; }
;     LDS_WAIT(); asm volatile("" ::: "memory");
;     const int c = lane & 7;
; #pragma unroll
;     for (int j = 0; j < 4; ++j) { const int n = (lane >> 3) + 8 * j; const LAS float* s = scr + (8 * c) * 33 + n;
;         v4u o; o.x = pk2(s[0 * 33], s[1 * 33]); o.y = pk2(s[2 * 33], s[3 * 33]); o.z = pk2(s[4 * 33], s[5 * 33]); o.w = pk2(s[6 * 33], s[7 * 33]);
;         *(GAS v4u*)(WT + (size_t)(n0 + n) * K + k0 + 8 * c) = o; }
;     LDS_WAIT(); asm volatile("" ::: "memory");
; }
	s_add_u32 s8, s54, 0x3000
	s_addc_u32 s9, s55, 0
	global_load_dwordx4 v[176:179], v75, s[8:9]
	s_add_u32 s8, s8, 0x8000
	s_addc_u32 s9, s9, 0
	global_load_dwordx4 v[180:183], v75, s[8:9]
	s_add_u32 s8, s8, 0x8000
	s_addc_u32 s9, s9, 0
	global_load_dwordx4 v[184:187], v75, s[8:9]
	s_add_u32 s8, s8, 0x8000
	s_addc_u32 s9, s9, 0
	global_load_dwordx4 v[188:191], v75, s[8:9]
	s_add_u32 s8, s8, 0x8000
	s_addc_u32 s9, s9, 0
	global_load_dwordx4 v[192:195], v75, s[8:9]
	s_add_u32 s8, s8, 0x8000
	s_addc_u32 s9, s9, 0
	global_load_dwordx4 v[196:199], v75, s[8:9]
	s_add_u32 s8, s8, 0x8000
	s_addc_u32 s9, s9, 0
	global_load_dwordx4 v[200:203], v75, s[8:9]
	s_add_u32 s8, s8, 0x8000
	s_addc_u32 s9, s9, 0
	global_load_dwordx4 v[204:207], v75, s[8:9]
	s_add_u32 s6, s56, 0x800000
	s_addc_u32 s7, s57, 0
	ds_read_b32 v226, v113
	ds_read_b32 v227, v113 offset:512
	ds_read_b32 v228, v113 offset:1024
	ds_read_b32 v229, v113 offset:1536
	ds_read_b32 v230, v113 offset:2048
	ds_read_b32 v231, v113 offset:2560
	ds_read_b32 v232, v113 offset:3072
	ds_read_b32 v233, v113 offset:3584
	s_waitcnt lgkmcnt(0)
	v_bfe_u32 v120, v226, 16, 1
	v_bfe_u32 v121, v227, 16, 1
	v_bfe_u32 v122, v228, 16, 1
	v_bfe_u32 v123, v229, 16, 1
	v_bfe_u32 v124, v230, 16, 1
	v_bfe_u32 v125, v231, 16, 1
	v_bfe_u32 v126, v232, 16, 1
	v_bfe_u32 v127, v233, 16, 1
	v_add3_u32 v226, v226, v120, s63
	v_add3_u32 v227, v227, v121, s63
	v_add3_u32 v228, v228, v122, s63
	v_add3_u32 v229, v229, v123, s63
	v_add3_u32 v230, v230, v124, s63
	v_add3_u32 v231, v231, v125, s63
	v_add3_u32 v232, v232, v126, s63
	v_add3_u32 v233, v233, v127, s63
	v_perm_b32 v242, v227, v226, s64
	v_perm_b32 v243, v229, v228, s64
	v_perm_b32 v244, v231, v230, s64
	v_perm_b32 v245, v233, v232, s64
	s_nop 0
	global_store_dwordx4 v83, v[242:245], s[6:7]
	ds_read_b32 v226, v115
	ds_read_b32 v227, v115 offset:512
	ds_read_b32 v228, v115 offset:1024
	ds_read_b32 v229, v115 offset:1536
	ds_read_b32 v230, v115 offset:2048
	ds_read_b32 v231, v115 offset:2560
	ds_read_b32 v232, v115 offset:3072
	ds_read_b32 v233, v115 offset:3584
	s_waitcnt lgkmcnt(0)
	v_bfe_u32 v120, v226, 16, 1
	v_bfe_u32 v121, v227, 16, 1
	v_bfe_u32 v122, v228, 16, 1
	v_bfe_u32 v123, v229, 16, 1
	v_bfe_u32 v124, v230, 16, 1
	v_bfe_u32 v125, v231, 16, 1
	v_bfe_u32 v126, v232, 16, 1
	v_bfe_u32 v127, v233, 16, 1
	v_add3_u32 v226, v226, v120, s63
	v_add3_u32 v227, v227, v121, s63
	v_add3_u32 v228, v228, v122, s63
	v_add3_u32 v229, v229, v123, s63
	v_add3_u32 v230, v230, v124, s63
	v_add3_u32 v231, v231, v125, s63
	v_add3_u32 v232, v232, v126, s63
	v_add3_u32 v233, v233, v127, s63
	v_perm_b32 v242, v227, v226, s64
	v_perm_b32 v243, v229, v228, s64
	v_perm_b32 v244, v231, v230, s64
	v_perm_b32 v245, v233, v232, s64
	s_nop 0
	global_store_dwordx4 v84, v[242:245], s[6:7]
	ds_read_b32 v226, v117
	ds_read_b32 v227, v117 offset:512
	ds_read_b32 v228, v117 offset:1024
	ds_read_b32 v229, v117 offset:1536
	ds_read_b32 v230, v117 offset:2048
	ds_read_b32 v231, v117 offset:2560
	ds_read_b32 v232, v117 offset:3072
	ds_read_b32 v233, v117 offset:3584
	s_waitcnt lgkmcnt(0)
	v_bfe_u32 v120, v226, 16, 1
	v_bfe_u32 v121, v227, 16, 1
	v_bfe_u32 v122, v228, 16, 1
	v_bfe_u32 v123, v229, 16, 1
	v_bfe_u32 v124, v230, 16, 1
	v_bfe_u32 v125, v231, 16, 1
	v_bfe_u32 v126, v232, 16, 1
	v_bfe_u32 v127, v233, 16, 1
	v_add3_u32 v226, v226, v120, s63
	v_add3_u32 v227, v227, v121, s63
	v_add3_u32 v228, v228, v122, s63
	v_add3_u32 v229, v229, v123, s63
	v_add3_u32 v230, v230, v124, s63
	v_add3_u32 v231, v231, v125, s63
	v_add3_u32 v232, v232, v126, s63
	v_add3_u32 v233, v233, v127, s63
	v_perm_b32 v242, v227, v226, s64
	v_perm_b32 v243, v229, v228, s64
	v_perm_b32 v244, v231, v230, s64
	v_perm_b32 v245, v233, v232, s64
	s_nop 0
	global_store_dwordx4 v85, v[242:245], s[6:7]
	ds_read_b32 v226, v119
	ds_read_b32 v227, v119 offset:512
	ds_read_b32 v228, v119 offset:1024
	ds_read_b32 v229, v119 offset:1536
	ds_read_b32 v230, v119 offset:2048
	ds_read_b32 v231, v119 offset:2560
	ds_read_b32 v232, v119 offset:3072
	ds_read_b32 v233, v119 offset:3584
	s_waitcnt lgkmcnt(0)
	v_bfe_u32 v120, v226, 16, 1
	v_bfe_u32 v121, v227, 16, 1
	v_bfe_u32 v122, v228, 16, 1
	v_bfe_u32 v123, v229, 16, 1
	v_bfe_u32 v124, v230, 16, 1
	v_bfe_u32 v125, v231, 16, 1
	v_bfe_u32 v126, v232, 16, 1
	v_bfe_u32 v127, v233, 16, 1
	v_add3_u32 v226, v226, v120, s63
	v_add3_u32 v227, v227, v121, s63
	v_add3_u32 v228, v228, v122, s63
	v_add3_u32 v229, v229, v123, s63
	v_add3_u32 v230, v230, v124, s63
	v_add3_u32 v231, v231, v125, s63
	v_add3_u32 v232, v232, v126, s63
	v_add3_u32 v233, v233, v127, s63
	v_perm_b32 v242, v227, v226, s64
	v_perm_b32 v243, v229, v228, s64
	v_perm_b32 v244, v231, v230, s64
	v_perm_b32 v245, v233, v232, s64
	s_nop 0
	global_store_dwordx4 v86, v[242:245], s[6:7]
	s_waitcnt vmcnt(16)
	v_mul_f32_e32 v144, v58, v144
	v_mul_f32_e32 v145, v58, v145
	v_mul_f32_e32 v146, v58, v146
	v_mul_f32_e32 v147, v58, v147
	ds_write_b128 v209, v[144:147]
	v_mul_f32_e32 v148, v59, v148
	v_mul_f32_e32 v149, v59, v149
	v_mul_f32_e32 v150, v59, v150
	v_mul_f32_e32 v151, v59, v151
	ds_write_b128 v209, v[148:151] offset:1024
	v_mul_f32_e32 v152, v60, v152
	v_mul_f32_e32 v153, v60, v153
	v_mul_f32_e32 v154, v60, v154
	v_mul_f32_e32 v155, v60, v155
	ds_write_b128 v209, v[152:155] offset:2048
	v_mul_f32_e32 v156, v61, v156
	v_mul_f32_e32 v157, v61, v157
	v_mul_f32_e32 v158, v61, v158
	v_mul_f32_e32 v159, v61, v159
	ds_write_b128 v209, v[156:159] offset:3072
	v_mul_f32_e32 v160, v62, v160
	v_mul_f32_e32 v161, v62, v161
	v_mul_f32_e32 v162, v62, v162
	v_mul_f32_e32 v163, v62, v163
	ds_write_b128 v209, v[160:163] offset:4096
	v_mul_f32_e32 v164, v63, v164
	v_mul_f32_e32 v165, v63, v165
	v_mul_f32_e32 v166, v63, v166
	v_mul_f32_e32 v167, v63, v167
	ds_write_b128 v209, v[164:167] offset:5120
	v_mul_f32_e32 v168, v64, v168
	v_mul_f32_e32 v169, v64, v169
	v_mul_f32_e32 v170, v64, v170
	v_mul_f32_e32 v171, v64, v171
	ds_write_b128 v209, v[168:171] offset:6144
	v_mul_f32_e32 v172, v65, v172
	v_mul_f32_e32 v173, v65, v173
	v_mul_f32_e32 v174, v65, v174
	v_mul_f32_e32 v175, v65, v175
	ds_write_b128 v209, v[172:175] offset:7168
	s_waitcnt lgkmcnt(0)
	s_barrier
; template <int MAP, bool KS, bool KPERM = false>
; __device__ __forceinline__ void p0_transpose_item(const float* W, int K, int Nsrc, int nblk, bf16* WT, const float* ksA, const float* ksB, int ksplit, LAS float* scr, int item, int lane) {
;     const int kb = item / nblk, nb = item % nblk, k0 = 64 * kb, n0 = 32 * nb;
;     const int nr = n0 + (lane & 31); const int sc = MAP == 1 ? src_col_in(nr) : (MAP == 2 ? nat_dim(nr) : nr);
;     float v[32];
; #pragma unroll
;     for (int i = 0; i < 32; ++i) { const int k = k0 + 2 * i + (lane >> 5); const int ksrc = KPERM ? ((k & ~127) + nat_dim(k & 127)) : k;
;         v[i] = sc >= 0 ? W[(size_t)ksrc * Nsrc + sc] : 0.f; }
; #pragma unroll
;     for (int i = 0; i < 32; ++i) { const int kk = 2 * i + (lane >> 5); const int k = k0 + kk;
;         if (KS) v[i] *= (k < ksplit ? ksA[k] : ksB[k - ksplit]);
;         scr[kk * 33 + (lane & 31)] = v[i]; }
;     LDS_WAIT(); asm volatile("" ::: "memory");
;     const int c = lane & 7;
; #pragma unroll
;     for (int j = 0; j < 4; ++j) { const int n = (lane >> 3) + 8 * j; const LAS float* s = scr + (8 * c) * 33 + n;
;         v4u o; o.x = pk2(s[0 * 33], s[1 * 33]); o.y = pk2(s[2 * 33], s[3 * 33]); o.z = pk2(s[4 * 33], s[5 * 33]); o.w = pk2(s[6 * 33], s[7 * 33]);
;         *(GAS v4u*)(WT + (size_t)(n0 + n) * K + k0 + 8 * c) = o; }
;     LDS_WAIT(); asm volatile("" ::: "memory");
; }
;     const int pr = item >> 1, kb = 2 * (pr / nblk) + (item & 1), nb = pr % nblk, k0 = 64 * kb, n0 = 32 * nb;
;     const int nr = n0 + (lane & 31); const int sc = MAP == 1 ? src_col_in(nr) : nr;
;     float v[32];
; #pragma unroll
;     for (int i = 0; i < 32; ++i) v[i] = sc >= 0 ? W[(size_t)(k0 + 2 * i + (lane >> 5)) * Nsrc + sc] : 0.f;
; #pragma unroll
;     for (int i = 0; i < 32; ++i) { const int k = k0 + 2 * i + (lane >> 5); float x = v[i] * wscale; if (KS) x *= (k < ksplit ? ksA[k] : ksB[k - ksplit]); scr[(2 * i + (lane >> 5)) * 33 + (lane & 31)] = x; }
;     LDS_WAIT(); asm volatile("" ::: "memory");
;     const int c = lane & 7;
; #pragma unroll
;     for (int j = 0; j < 4; ++j) { const int n = (lane >> 3) + 8 * j; const LAS float* s = scr + (8 * c) * 33 + n;
;         const unsigned long long o = (unsigned long long)pg8::pk4_fp8(s[0 * 33], s[1 * 33], s[2 * 33], s[3 * 33]) | ((unsigned long long)pg8::pk4_fp8(s[4 * 33], s[5 * 33], s[6 * 33], s[7 * 33]) << 32);
	s_mov_b64 s[8:9], s[58:59]
	global_load_dwordx4 v[144:147], v75, s[8:9]
	s_add_u32 s8, s8, 0x8000
	s_addc_u32 s9, s9, 0
	global_load_dwordx4 v[148:151], v75, s[8:9]
	s_add_u32 s8, s8, 0x8000
	s_addc_u32 s9, s9, 0
	global_load_dwordx4 v[152:155], v75, s[8:9]
	s_add_u32 s8, s8, 0x8000
	s_addc_u32 s9, s9, 0
	global_load_dwordx4 v[156:159], v75, s[8:9]
	s_add_u32 s8, s8, 0x8000
	s_addc_u32 s9, s9, 0
	global_load_dwordx4 v[160:163], v75, s[8:9]
	s_add_u32 s8, s8, 0x8000
	s_addc_u32 s9, s9, 0
	global_load_dwordx4 v[164:167], v75, s[8:9]
	s_add_u32 s8, s8, 0x8000
	s_addc_u32 s9, s9, 0
	global_load_dwordx4 v[168:171], v75, s[8:9]
	s_add_u32 s8, s8, 0x8000
	s_addc_u32 s9, s9, 0
	global_load_dwordx4 v[172:175], v75, s[8:9]
	s_add_u32 s6, s56, 0x1000000
	s_addc_u32 s7, s57, 0
	ds_read_b32 v226, v112
	ds_read_b32 v227, v112 offset:512
	ds_read_b32 v228, v112 offset:1024
	ds_read_b32 v229, v112 offset:1536
	ds_read_b32 v230, v112 offset:2048
	ds_read_b32 v231, v112 offset:2560
	ds_read_b32 v232, v112 offset:3072
	ds_read_b32 v233, v112 offset:3584
	s_waitcnt lgkmcnt(0)
	v_bfe_u32 v120, v226, 16, 1
	v_bfe_u32 v121, v227, 16, 1
	v_bfe_u32 v122, v228, 16, 1
	v_bfe_u32 v123, v229, 16, 1
	v_bfe_u32 v124, v230, 16, 1
	v_bfe_u32 v125, v231, 16, 1
	v_bfe_u32 v126, v232, 16, 1
	v_bfe_u32 v127, v233, 16, 1
	v_add3_u32 v226, v226, v120, s63
	v_add3_u32 v227, v227, v121, s63
	v_add3_u32 v228, v228, v122, s63
	v_add3_u32 v229, v229, v123, s63
	v_add3_u32 v230, v230, v124, s63
	v_add3_u32 v231, v231, v125, s63
	v_add3_u32 v232, v232, v126, s63
	v_add3_u32 v233, v233, v127, s63
	v_perm_b32 v242, v227, v226, s64
	v_perm_b32 v243, v229, v228, s64
	v_perm_b32 v244, v231, v230, s64
	v_perm_b32 v245, v233, v232, s64
	s_nop 0
	global_store_dwordx4 v83, v[242:245], s[6:7]
	ds_read_b32 v226, v114
	ds_read_b32 v227, v114 offset:512
	ds_read_b32 v228, v114 offset:1024
	ds_read_b32 v229, v114 offset:1536
	ds_read_b32 v230, v114 offset:2048
	ds_read_b32 v231, v114 offset:2560
	ds_read_b32 v232, v114 offset:3072
	ds_read_b32 v233, v114 offset:3584
	s_waitcnt lgkmcnt(0)
	v_bfe_u32 v120, v226, 16, 1
	v_bfe_u32 v121, v227, 16, 1
	v_bfe_u32 v122, v228, 16, 1
	v_bfe_u32 v123, v229, 16, 1
	v_bfe_u32 v124, v230, 16, 1
	v_bfe_u32 v125, v231, 16, 1
	v_bfe_u32 v126, v232, 16, 1
	v_bfe_u32 v127, v233, 16, 1
	v_add3_u32 v226, v226, v120, s63
	v_add3_u32 v227, v227, v121, s63
	v_add3_u32 v228, v228, v122, s63
	v_add3_u32 v229, v229, v123, s63
	v_add3_u32 v230, v230, v124, s63
	v_add3_u32 v231, v231, v125, s63
	v_add3_u32 v232, v232, v126, s63
	v_add3_u32 v233, v233, v127, s63
	v_perm_b32 v242, v227, v226, s64
	v_perm_b32 v243, v229, v228, s64
	v_perm_b32 v244, v231, v230, s64
	v_perm_b32 v245, v233, v232, s64
	s_nop 0
	global_store_dwordx4 v84, v[242:245], s[6:7]
	ds_read_b32 v226, v116
	ds_read_b32 v227, v116 offset:512
	ds_read_b32 v228, v116 offset:1024
	ds_read_b32 v229, v116 offset:1536
	ds_read_b32 v230, v116 offset:2048
	ds_read_b32 v231, v116 offset:2560
	ds_read_b32 v232, v116 offset:3072
	ds_read_b32 v233, v116 offset:3584
	s_waitcnt lgkmcnt(0)
	v_bfe_u32 v120, v226, 16, 1
	v_bfe_u32 v121, v227, 16, 1
	v_bfe_u32 v122, v228, 16, 1
	v_bfe_u32 v123, v229, 16, 1
	v_bfe_u32 v124, v230, 16, 1
	v_bfe_u32 v125, v231, 16, 1
	v_bfe_u32 v126, v232, 16, 1
	v_bfe_u32 v127, v233, 16, 1
	v_add3_u32 v226, v226, v120, s63
	v_add3_u32 v227, v227, v121, s63
	v_add3_u32 v228, v228, v122, s63
	v_add3_u32 v229, v229, v123, s63
	v_add3_u32 v230, v230, v124, s63
	v_add3_u32 v231, v231, v125, s63
	v_add3_u32 v232, v232, v126, s63
	v_add3_u32 v233, v233, v127, s63
	v_perm_b32 v242, v227, v226, s64
	v_perm_b32 v243, v229, v228, s64
	v_perm_b32 v244, v231, v230, s64
	v_perm_b32 v245, v233, v232, s64
	s_nop 0
	global_store_dwordx4 v85, v[242:245], s[6:7]
	ds_read_b32 v226, v118
	ds_read_b32 v227, v118 offset:512
	ds_read_b32 v228, v118 offset:1024
	ds_read_b32 v229, v118 offset:1536
	ds_read_b32 v230, v118 offset:2048
	ds_read_b32 v231, v118 offset:2560
	ds_read_b32 v232, v118 offset:3072
	ds_read_b32 v233, v118 offset:3584
	s_waitcnt lgkmcnt(0)
	v_bfe_u32 v120, v226, 16, 1
	v_bfe_u32 v121, v227, 16, 1
	v_bfe_u32 v122, v228, 16, 1
	v_bfe_u32 v123, v229, 16, 1
	v_bfe_u32 v124, v230, 16, 1
	v_bfe_u32 v125, v231, 16, 1
	v_bfe_u32 v126, v232, 16, 1
	v_bfe_u32 v127, v233, 16, 1
	v_add3_u32 v226, v226, v120, s63
	v_add3_u32 v227, v227, v121, s63
	v_add3_u32 v228, v228, v122, s63
	v_add3_u32 v229, v229, v123, s63
	v_add3_u32 v230, v230, v124, s63
	v_add3_u32 v231, v231, v125, s63
	v_add3_u32 v232, v232, v126, s63
	v_add3_u32 v233, v233, v127, s63
	v_perm_b32 v242, v227, v226, s64
	v_perm_b32 v243, v229, v228, s64
	v_perm_b32 v244, v231, v230, s64
	v_perm_b32 v245, v233, v232, s64
	s_nop 0
	global_store_dwordx4 v86, v[242:245], s[6:7]
	s_waitcnt vmcnt(16)
	v_mul_f32_e32 v176, v58, v176
	v_mul_f32_e32 v177, v58, v177
	v_mul_f32_e32 v178, v58, v178
	v_mul_f32_e32 v179, v58, v179
	ds_write_b128 v210, v[176:179]
	v_mul_f32_e32 v180, v59, v180
	v_mul_f32_e32 v181, v59, v181
	v_mul_f32_e32 v182, v59, v182
	v_mul_f32_e32 v183, v59, v183
	ds_write_b128 v210, v[180:183] offset:1024
	v_mul_f32_e32 v184, v60, v184
	v_mul_f32_e32 v185, v60, v185
	v_mul_f32_e32 v186, v60, v186
	v_mul_f32_e32 v187, v60, v187
	ds_write_b128 v210, v[184:187] offset:2048
	v_mul_f32_e32 v188, v61, v188
	v_mul_f32_e32 v189, v61, v189
	v_mul_f32_e32 v190, v61, v190
	v_mul_f32_e32 v191, v61, v191
	ds_write_b128 v210, v[188:191] offset:3072
	v_mul_f32_e32 v192, v62, v192
	v_mul_f32_e32 v193, v62, v193
	v_mul_f32_e32 v194, v62, v194
	v_mul_f32_e32 v195, v62, v195
	ds_write_b128 v210, v[192:195] offset:4096
	v_mul_f32_e32 v196, v63, v196
	v_mul_f32_e32 v197, v63, v197
	v_mul_f32_e32 v198, v63, v198
	v_mul_f32_e32 v199, v63, v199
	ds_write_b128 v210, v[196:199] offset:5120
	v_mul_f32_e32 v200, v64, v200
	v_mul_f32_e32 v201, v64, v201
	v_mul_f32_e32 v202, v64, v202
	v_mul_f32_e32 v203, v64, v203
	ds_write_b128 v210, v[200:203] offset:6144
	v_mul_f32_e32 v204, v65, v204
	v_mul_f32_e32 v205, v65, v205
	v_mul_f32_e32 v206, v65, v206
	v_mul_f32_e32 v207, v65, v207
	ds_write_b128 v210, v[204:207] offset:7168
	s_waitcnt lgkmcnt(0)
	s_barrier
; template <int MAP, bool KS, bool KPERM = false>
; __device__ __forceinline__ void p0_transpose_item(const float* W, int K, int Nsrc, int nblk, bf16* WT, const float* ksA, const float* ksB, int ksplit, LAS float* scr, int item, int lane) {
;     const int kb = item / nblk, nb = item % nblk, k0 = 64 * kb, n0 = 32 * nb;
;     const int nr = n0 + (lane & 31); const int sc = MAP == 1 ? src_col_in(nr) : (MAP == 2 ? nat_dim(nr) : nr);
;     float v[32];
; #pragma unroll
;     for (int i = 0; i < 32; ++i) { const int k = k0 + 2 * i + (lane >> 5); const int ksrc = KPERM ? ((k & ~127) + nat_dim(k & 127)) : k;
;         v[i] = sc >= 0 ? W[(size_t)ksrc * Nsrc + sc] : 0.f; }
; #pragma unroll
;     for (int i = 0; i < 32; ++i) { const int kk = 2 * i + (lane >> 5); const int k = k0 + kk;
;         if (KS) v[i] *= (k < ksplit ? ksA[k] : ksB[k - ksplit]);
;         scr[kk * 33 + (lane & 31)] = v[i]; }
;     LDS_WAIT(); asm volatile("" ::: "memory");
;     const int c = lane & 7;
; #pragma unroll
;     for (int j = 0; j < 4; ++j) { const int n = (lane >> 3) + 8 * j; const LAS float* s = scr + (8 * c) * 33 + n;
;         v4u o; o.x = pk2(s[0 * 33], s[1 * 33]); o.y = pk2(s[2 * 33], s[3 * 33]); o.z = pk2(s[4 * 33], s[5 * 33]); o.w = pk2(s[6 * 33], s[7 * 33]);
;         *(GAS v4u*)(WT + (size_t)(n0 + n) * K + k0 + 8 * c) = o; }
;     LDS_WAIT(); asm volatile("" ::: "memory");
; }
;     const int pr = item >> 1, kb = 2 * (pr / nblk) + (item & 1), nb = pr % nblk, k0 = 64 * kb, n0 = 32 * nb;
;     const int nr = n0 + (lane & 31); const int sc = MAP == 1 ? src_col_in(nr) : nr;
;     float v[32];
; #pragma unroll
;     for (int i = 0; i < 32; ++i) v[i] = sc >= 0 ? W[(size_t)(k0 + 2 * i + (lane >> 5)) * Nsrc + sc] : 0.f;
; #pragma unroll
;     for (int i = 0; i < 32; ++i) { const int k = k0 + 2 * i + (lane >> 5); float x = v[i] * wscale; if (KS) x *= (k < ksplit ? ksA[k] : ksB[k - ksplit]); scr[(2 * i + (lane >> 5)) * 33 + (lane & 31)] = x; }
;     LDS_WAIT(); asm volatile("" ::: "memory");
;     const int c = lane & 7;
; #pragma unroll
;     for (int j = 0; j < 4; ++j) { const int n = (lane >> 3) + 8 * j; const LAS float* s = scr + (8 * c) * 33 + n;
;         const unsigned long long o = (unsigned long long)pg8::pk4_fp8(s[0 * 33], s[1 * 33], s[2 * 33], s[3 * 33]) | ((unsigned long long)pg8::pk4_fp8(s[4 * 33], s[5 * 33], s[6 * 33], s[7 * 33]) << 32);
	s_add_u32 s8, s58, 0x1000
	s_addc_u32 s9, s59, 0
	global_load_dwordx4 v[176:179], v75, s[8:9]
	s_add_u32 s8, s8, 0x8000
	s_addc_u32 s9, s9, 0
	global_load_dwordx4 v[180:183], v75, s[8:9]
	s_add_u32 s8, s8, 0x8000
	s_addc_u32 s9, s9, 0
	global_load_dwordx4 v[184:187], v75, s[8:9]
	s_add_u32 s8, s8, 0x8000
	s_addc_u32 s9, s9, 0
	global_load_dwordx4 v[188:191], v75, s[8:9]
	s_add_u32 s8, s8, 0x8000
	s_addc_u32 s9, s9, 0
	global_load_dwordx4 v[192:195], v75, s[8:9]
	s_add_u32 s8, s8, 0x8000
	s_addc_u32 s9, s9, 0
	global_load_dwordx4 v[196:199], v75, s[8:9]
	s_add_u32 s8, s8, 0x8000
	s_addc_u32 s9, s9, 0
	global_load_dwordx4 v[200:203], v75, s[8:9]
	s_add_u32 s8, s8, 0x8000
	s_addc_u32 s9, s9, 0
	global_load_dwordx4 v[204:207], v75, s[8:9]
	s_add_u32 s6, s56, 0x1800000
	s_addc_u32 s7, s57, 0
	ds_read_b32 v226, v113
	ds_read_b32 v227, v113 offset:512
	ds_read_b32 v228, v113 offset:1024
	ds_read_b32 v229, v113 offset:1536
	ds_read_b32 v230, v113 offset:2048
	ds_read_b32 v231, v113 offset:2560
	ds_read_b32 v232, v113 offset:3072
	ds_read_b32 v233, v113 offset:3584
	s_waitcnt lgkmcnt(0)
	v_bfe_u32 v120, v226, 16, 1
	v_bfe_u32 v121, v227, 16, 1
	v_bfe_u32 v122, v228, 16, 1
	v_bfe_u32 v123, v229, 16, 1
	v_bfe_u32 v124, v230, 16, 1
	v_bfe_u32 v125, v231, 16, 1
	v_bfe_u32 v126, v232, 16, 1
	v_bfe_u32 v127, v233, 16, 1
	v_add3_u32 v226, v226, v120, s63
	v_add3_u32 v227, v227, v121, s63
	v_add3_u32 v228, v228, v122, s63
	v_add3_u32 v229, v229, v123, s63
	v_add3_u32 v230, v230, v124, s63
	v_add3_u32 v231, v231, v125, s63
	v_add3_u32 v232, v232, v126, s63
	v_add3_u32 v233, v233, v127, s63
	v_perm_b32 v242, v227, v226, s64
	v_perm_b32 v243, v229, v228, s64
	v_perm_b32 v244, v231, v230, s64
	v_perm_b32 v245, v233, v232, s64
	s_nop 0
	global_store_dwordx4 v83, v[242:245], s[6:7]
	ds_read_b32 v226, v115
	ds_read_b32 v227, v115 offset:512
	ds_read_b32 v228, v115 offset:1024
	ds_read_b32 v229, v115 offset:1536
	ds_read_b32 v230, v115 offset:2048
	ds_read_b32 v231, v115 offset:2560
	ds_read_b32 v232, v115 offset:3072
	ds_read_b32 v233, v115 offset:3584
	s_waitcnt lgkmcnt(0)
	v_bfe_u32 v120, v226, 16, 1
	v_bfe_u32 v121, v227, 16, 1
	v_bfe_u32 v122, v228, 16, 1
	v_bfe_u32 v123, v229, 16, 1
	v_bfe_u32 v124, v230, 16, 1
	v_bfe_u32 v125, v231, 16, 1
	v_bfe_u32 v126, v232, 16, 1
	v_bfe_u32 v127, v233, 16, 1
	v_add3_u32 v226, v226, v120, s63
	v_add3_u32 v227, v227, v121, s63
	v_add3_u32 v228, v228, v122, s63
	v_add3_u32 v229, v229, v123, s63
	v_add3_u32 v230, v230, v124, s63
	v_add3_u32 v231, v231, v125, s63
	v_add3_u32 v232, v232, v126, s63
	v_add3_u32 v233, v233, v127, s63
	v_perm_b32 v242, v227, v226, s64
	v_perm_b32 v243, v229, v228, s64
	v_perm_b32 v244, v231, v230, s64
	v_perm_b32 v245, v233, v232, s64
	s_nop 0
	global_store_dwordx4 v84, v[242:245], s[6:7]
	ds_read_b32 v226, v117
	ds_read_b32 v227, v117 offset:512
	ds_read_b32 v228, v117 offset:1024
	ds_read_b32 v229, v117 offset:1536
	ds_read_b32 v230, v117 offset:2048
	ds_read_b32 v231, v117 offset:2560
	ds_read_b32 v232, v117 offset:3072
	ds_read_b32 v233, v117 offset:3584
	s_waitcnt lgkmcnt(0)
	v_bfe_u32 v120, v226, 16, 1
	v_bfe_u32 v121, v227, 16, 1
	v_bfe_u32 v122, v228, 16, 1
	v_bfe_u32 v123, v229, 16, 1
	v_bfe_u32 v124, v230, 16, 1
	v_bfe_u32 v125, v231, 16, 1
	v_bfe_u32 v126, v232, 16, 1
	v_bfe_u32 v127, v233, 16, 1
	v_add3_u32 v226, v226, v120, s63
	v_add3_u32 v227, v227, v121, s63
	v_add3_u32 v228, v228, v122, s63
	v_add3_u32 v229, v229, v123, s63
	v_add3_u32 v230, v230, v124, s63
	v_add3_u32 v231, v231, v125, s63
	v_add3_u32 v232, v232, v126, s63
	v_add3_u32 v233, v233, v127, s63
	v_perm_b32 v242, v227, v226, s64
	v_perm_b32 v243, v229, v228, s64
	v_perm_b32 v244, v231, v230, s64
	v_perm_b32 v245, v233, v232, s64
	s_nop 0
	global_store_dwordx4 v85, v[242:245], s[6:7]
	ds_read_b32 v226, v119
	ds_read_b32 v227, v119 offset:512
	ds_read_b32 v228, v119 offset:1024
	ds_read_b32 v229, v119 offset:1536
	ds_read_b32 v230, v119 offset:2048
	ds_read_b32 v231, v119 offset:2560
	ds_read_b32 v232, v119 offset:3072
	ds_read_b32 v233, v119 offset:3584
	s_waitcnt lgkmcnt(0)
	v_bfe_u32 v120, v226, 16, 1
	v_bfe_u32 v121, v227, 16, 1
	v_bfe_u32 v122, v228, 16, 1
	v_bfe_u32 v123, v229, 16, 1
	v_bfe_u32 v124, v230, 16, 1
	v_bfe_u32 v125, v231, 16, 1
	v_bfe_u32 v126, v232, 16, 1
	v_bfe_u32 v127, v233, 16, 1
	v_add3_u32 v226, v226, v120, s63
	v_add3_u32 v227, v227, v121, s63
	v_add3_u32 v228, v228, v122, s63
	v_add3_u32 v229, v229, v123, s63
	v_add3_u32 v230, v230, v124, s63
	v_add3_u32 v231, v231, v125, s63
	v_add3_u32 v232, v232, v126, s63
	v_add3_u32 v233, v233, v127, s63
	v_perm_b32 v242, v227, v226, s64
	v_perm_b32 v243, v229, v228, s64
	v_perm_b32 v244, v231, v230, s64
	v_perm_b32 v245, v233, v232, s64
	s_nop 0
	global_store_dwordx4 v86, v[242:245], s[6:7]
	s_waitcnt vmcnt(16)
	v_mul_f32_e32 v144, v66, v144
	v_mul_f32_e32 v145, v66, v145
	v_mul_f32_e32 v146, v66, v146
	v_mul_f32_e32 v147, v66, v147
	ds_write_b128 v209, v[144:147]
	v_mul_f32_e32 v148, v67, v148
	v_mul_f32_e32 v149, v67, v149
	v_mul_f32_e32 v150, v67, v150
	v_mul_f32_e32 v151, v67, v151
	ds_write_b128 v209, v[148:151] offset:1024
	v_mul_f32_e32 v152, v68, v152
	v_mul_f32_e32 v153, v68, v153
	v_mul_f32_e32 v154, v68, v154
	v_mul_f32_e32 v155, v68, v155
	ds_write_b128 v209, v[152:155] offset:2048
	v_mul_f32_e32 v156, v69, v156
	v_mul_f32_e32 v157, v69, v157
	v_mul_f32_e32 v158, v69, v158
	v_mul_f32_e32 v159, v69, v159
	ds_write_b128 v209, v[156:159] offset:3072
	v_mul_f32_e32 v160, v70, v160
	v_mul_f32_e32 v161, v70, v161
	v_mul_f32_e32 v162, v70, v162
	v_mul_f32_e32 v163, v70, v163
	ds_write_b128 v209, v[160:163] offset:4096
	v_mul_f32_e32 v164, v71, v164
	v_mul_f32_e32 v165, v71, v165
	v_mul_f32_e32 v166, v71, v166
	v_mul_f32_e32 v167, v71, v167
	ds_write_b128 v209, v[164:167] offset:5120
	v_mul_f32_e32 v168, v72, v168
	v_mul_f32_e32 v169, v72, v169
	v_mul_f32_e32 v170, v72, v170
	v_mul_f32_e32 v171, v72, v171
	ds_write_b128 v209, v[168:171] offset:6144
	v_mul_f32_e32 v172, v73, v172
	v_mul_f32_e32 v173, v73, v173
	v_mul_f32_e32 v174, v73, v174
	v_mul_f32_e32 v175, v73, v175
	ds_write_b128 v209, v[172:175] offset:7168
	s_waitcnt lgkmcnt(0)
	s_barrier
; #define GAS __attribute__((address_space(1)))
; #define LAS __attribute__((address_space(3)))
; #define LDS_WAIT() asm volatile("s_waitcnt lgkmcnt(0)" ::: "memory")
;     const int pr = item >> 1, kb = 2 * (pr / nblk) + (item & 1), nb = pr % nblk, k0 = 64 * kb, n0 = 32 * nb;
;     const int nr = n0 + (lane & 31); const int sc = MAP == 1 ? src_col_in(nr) : nr;
;     float v[32];
; #pragma unroll
;     for (int i = 0; i < 32; ++i) v[i] = sc >= 0 ? W[(size_t)(k0 + 2 * i + (lane >> 5)) * Nsrc + sc] : 0.f;
; #pragma unroll
;     for (int i = 0; i < 32; ++i) { const int k = k0 + 2 * i + (lane >> 5); float x = v[i] * wscale; if (KS) x *= (k < ksplit ? ksA[k] : ksB[k - ksplit]); scr[(2 * i + (lane >> 5)) * 33 + (lane & 31)] = x; }
;     LDS_WAIT(); asm volatile("" ::: "memory");
;     const int c = lane & 7;
; #pragma unroll
;     for (int j = 0; j < 4; ++j) { const int n = (lane >> 3) + 8 * j; const LAS float* s = scr + (8 * c) * 33 + n;
;         const unsigned long long o = (unsigned long long)pg8::pk4_fp8(s[0 * 33], s[1 * 33], s[2 * 33], s[3 * 33]) | ((unsigned long long)pg8::pk4_fp8(s[4 * 33], s[5 * 33], s[6 * 33], s[7 * 33]) << 32);
;         *(GAS unsigned long long*)(WT + (size_t)(n0 + n) * K + k0 + 8 * c) = o; }
;     LDS_WAIT(); asm volatile("" ::: "memory");
; }
	s_add_u32 s8, s58, 0x2000
	s_addc_u32 s9, s59, 0
	global_load_dwordx4 v[144:147], v75, s[8:9]
	s_add_u32 s8, s8, 0x8000
	s_addc_u32 s9, s9, 0
	global_load_dwordx4 v[148:151], v75, s[8:9]
	s_add_u32 s8, s8, 0x8000
	s_addc_u32 s9, s9, 0
	global_load_dwordx4 v[152:155], v75, s[8:9]
	s_add_u32 s8, s8, 0x8000
	s_addc_u32 s9, s9, 0
	global_load_dwordx4 v[156:159], v75, s[8:9]
	s_add_u32 s8, s8, 0x8000
	s_addc_u32 s9, s9, 0
	global_load_dwordx4 v[160:163], v75, s[8:9]
	s_add_u32 s8, s8, 0x8000
	s_addc_u32 s9, s9, 0
	global_load_dwordx4 v[164:167], v75, s[8:9]
	s_add_u32 s8, s8, 0x8000
	s_addc_u32 s9, s9, 0
	global_load_dwordx4 v[168:171], v75, s[8:9]
	s_add_u32 s8, s8, 0x8000
	s_addc_u32 s9, s9, 0
	global_load_dwordx4 v[172:175], v75, s[8:9]
	s_mov_b64 s[6:7], s[60:61]
	ds_read_b32 v226, v211
	ds_read_b32 v227, v211 offset:512
	ds_read_b32 v228, v211 offset:1024
	ds_read_b32 v229, v211 offset:1536
	ds_read_b32 v230, v211 offset:2048
	ds_read_b32 v231, v211 offset:2560
	ds_read_b32 v232, v211 offset:3072
	ds_read_b32 v233, v211 offset:3584
	ds_read_b32 v234, v211 offset:4096
	ds_read_b32 v235, v211 offset:4608
	ds_read_b32 v236, v211 offset:5120
	ds_read_b32 v237, v211 offset:5632
	ds_read_b32 v238, v211 offset:6144
	ds_read_b32 v239, v211 offset:6656
	ds_read_b32 v240, v211 offset:7168
	ds_read_b32 v241, v211 offset:7680
	s_waitcnt lgkmcnt(0)
	v_max_f32_e32 v226, v226, v226
	v_max_f32_e32 v227, v227, v227
	v_max_f32_e32 v228, v228, v228
	v_max_f32_e32 v229, v229, v229
	v_max_f32_e32 v230, v230, v230
	v_max_f32_e32 v231, v231, v231
	v_max_f32_e32 v232, v232, v232
	v_max_f32_e32 v233, v233, v233
	v_max_f32_e32 v234, v234, v234
	v_max_f32_e32 v235, v235, v235
	v_max_f32_e32 v236, v236, v236
	v_max_f32_e32 v237, v237, v237
	v_max_f32_e32 v238, v238, v238
	v_max_f32_e32 v239, v239, v239
	v_max_f32_e32 v240, v240, v240
	v_max_f32_e32 v241, v241, v241
	v_med3_f32 v226, v226, s62, v95
	v_med3_f32 v227, v227, s62, v95
	v_med3_f32 v228, v228, s62, v95
	v_med3_f32 v229, v229, s62, v95
	v_med3_f32 v230, v230, s62, v95
	v_med3_f32 v231, v231, s62, v95
	v_med3_f32 v232, v232, s62, v95
	v_med3_f32 v233, v233, s62, v95
	v_med3_f32 v234, v234, s62, v95
	v_med3_f32 v235, v235, s62, v95
	v_med3_f32 v236, v236, s62, v95
	v_med3_f32 v237, v237, s62, v95
	v_med3_f32 v238, v238, s62, v95
	v_med3_f32 v239, v239, s62, v95
	v_med3_f32 v240, v240, s62, v95
	v_med3_f32 v241, v241, s62, v95
	v_mov_b32_e32 v242, 0
	v_mov_b32_e32 v243, 0
	v_mov_b32_e32 v244, 0
	v_mov_b32_e32 v245, 0
	v_cvt_pk_fp8_f32 v242, v226, v227
	v_cvt_pk_fp8_f32 v243, v230, v231
	v_cvt_pk_fp8_f32 v244, v234, v235
	v_cvt_pk_fp8_f32 v245, v238, v239
	v_cvt_pk_fp8_f32 v242, v228, v229 op_sel:[0,0,1]
	v_cvt_pk_fp8_f32 v243, v232, v233 op_sel:[0,0,1]
	v_cvt_pk_fp8_f32 v244, v236, v237 op_sel:[0,0,1]
	v_cvt_pk_fp8_f32 v245, v240, v241 op_sel:[0,0,1]
	s_nop 0
	global_store_dwordx4 v77, v[242:245], s[6:7]
	ds_read_b32 v226, v213
	ds_read_b32 v227, v213 offset:512
	ds_read_b32 v228, v213 offset:1024
	ds_read_b32 v229, v213 offset:1536
	ds_read_b32 v230, v213 offset:2048
	ds_read_b32 v231, v213 offset:2560
	ds_read_b32 v232, v213 offset:3072
	ds_read_b32 v233, v213 offset:3584
	ds_read_b32 v234, v213 offset:4096
	ds_read_b32 v235, v213 offset:4608
	ds_read_b32 v236, v213 offset:5120
	ds_read_b32 v237, v213 offset:5632
	ds_read_b32 v238, v213 offset:6144
	ds_read_b32 v239, v213 offset:6656
	ds_read_b32 v240, v213 offset:7168
	ds_read_b32 v241, v213 offset:7680
	s_waitcnt lgkmcnt(0)
	v_max_f32_e32 v226, v226, v226
	v_max_f32_e32 v227, v227, v227
	v_max_f32_e32 v228, v228, v228
	v_max_f32_e32 v229, v229, v229
	v_max_f32_e32 v230, v230, v230
	v_max_f32_e32 v231, v231, v231
	v_max_f32_e32 v232, v232, v232
	v_max_f32_e32 v233, v233, v233
	v_max_f32_e32 v234, v234, v234
	v_max_f32_e32 v235, v235, v235
	v_max_f32_e32 v236, v236, v236
	v_max_f32_e32 v237, v237, v237
	v_max_f32_e32 v238, v238, v238
	v_max_f32_e32 v239, v239, v239
	v_max_f32_e32 v240, v240, v240
	v_max_f32_e32 v241, v241, v241
	v_med3_f32 v226, v226, s62, v95
	v_med3_f32 v227, v227, s62, v95
	v_med3_f32 v228, v228, s62, v95
	v_med3_f32 v229, v229, s62, v95
	v_med3_f32 v230, v230, s62, v95
	v_med3_f32 v231, v231, s62, v95
	v_med3_f32 v232, v232, s62, v95
	v_med3_f32 v233, v233, s62, v95
	v_med3_f32 v234, v234, s62, v95
	v_med3_f32 v235, v235, s62, v95
	v_med3_f32 v236, v236, s62, v95
	v_med3_f32 v237, v237, s62, v95
	v_med3_f32 v238, v238, s62, v95
	v_med3_f32 v239, v239, s62, v95
	v_med3_f32 v240, v240, s62, v95
	v_med3_f32 v241, v241, s62, v95
	v_mov_b32_e32 v242, 0
	v_mov_b32_e32 v243, 0
	v_mov_b32_e32 v244, 0
	v_mov_b32_e32 v245, 0
	v_cvt_pk_fp8_f32 v242, v226, v227
	v_cvt_pk_fp8_f32 v243, v230, v231
	v_cvt_pk_fp8_f32 v244, v234, v235
	v_cvt_pk_fp8_f32 v245, v238, v239
	v_cvt_pk_fp8_f32 v242, v228, v229 op_sel:[0,0,1]
	v_cvt_pk_fp8_f32 v243, v232, v233 op_sel:[0,0,1]
	v_cvt_pk_fp8_f32 v244, v236, v237 op_sel:[0,0,1]
	v_cvt_pk_fp8_f32 v245, v240, v241 op_sel:[0,0,1]
	s_nop 0
	global_store_dwordx4 v78, v[242:245], s[6:7]
	s_waitcnt vmcnt(14)
	v_mul_f32_e32 v176, v66, v176
	v_mul_f32_e32 v177, v66, v177
	v_mul_f32_e32 v178, v66, v178
	v_mul_f32_e32 v179, v66, v179
	ds_write_b128 v210, v[176:179]
	v_mul_f32_e32 v180, v67, v180
	v_mul_f32_e32 v181, v67, v181
	v_mul_f32_e32 v182, v67, v182
	v_mul_f32_e32 v183, v67, v183
	ds_write_b128 v210, v[180:183] offset:1024
	v_mul_f32_e32 v184, v68, v184
	v_mul_f32_e32 v185, v68, v185
	v_mul_f32_e32 v186, v68, v186
	v_mul_f32_e32 v187, v68, v187
	ds_write_b128 v210, v[184:187] offset:2048
	v_mul_f32_e32 v188, v69, v188
	v_mul_f32_e32 v189, v69, v189
	v_mul_f32_e32 v190, v69, v190
	v_mul_f32_e32 v191, v69, v191
	ds_write_b128 v210, v[188:191] offset:3072
	v_mul_f32_e32 v192, v70, v192
	v_mul_f32_e32 v193, v70, v193
	v_mul_f32_e32 v194, v70, v194
	v_mul_f32_e32 v195, v70, v195
	ds_write_b128 v210, v[192:195] offset:4096
	v_mul_f32_e32 v196, v71, v196
	v_mul_f32_e32 v197, v71, v197
	v_mul_f32_e32 v198, v71, v198
	v_mul_f32_e32 v199, v71, v199
	ds_write_b128 v210, v[196:199] offset:5120
	v_mul_f32_e32 v200, v72, v200
	v_mul_f32_e32 v201, v72, v201
	v_mul_f32_e32 v202, v72, v202
	v_mul_f32_e32 v203, v72, v203
	ds_write_b128 v210, v[200:203] offset:6144
	v_mul_f32_e32 v204, v73, v204
	v_mul_f32_e32 v205, v73, v205
	v_mul_f32_e32 v206, v73, v206
	v_mul_f32_e32 v207, v73, v207
	ds_write_b128 v210, v[204:207] offset:7168
	s_waitcnt lgkmcnt(0)
	s_barrier
; #define GAS __attribute__((address_space(1)))
; #define LAS __attribute__((address_space(3)))
; #define LDS_WAIT() asm volatile("s_waitcnt lgkmcnt(0)" ::: "memory")
;     const int pr = item >> 1, kb = 2 * (pr / nblk) + (item & 1), nb = pr % nblk, k0 = 64 * kb, n0 = 32 * nb;
;     const int nr = n0 + (lane & 31); const int sc = MAP == 1 ? src_col_in(nr) : nr;
;     float v[32];
; #pragma unroll
;     for (int i = 0; i < 32; ++i) v[i] = sc >= 0 ? W[(size_t)(k0 + 2 * i + (lane >> 5)) * Nsrc + sc] : 0.f;
; #pragma unroll
;     for (int i = 0; i < 32; ++i) { const int k = k0 + 2 * i + (lane >> 5); float x = v[i] * wscale; if (KS) x *= (k < ksplit ? ksA[k] : ksB[k - ksplit]); scr[(2 * i + (lane >> 5)) * 33 + (lane & 31)] = x; }
;     LDS_WAIT(); asm volatile("" ::: "memory");
;     const int c = lane & 7;
; #pragma unroll
;     for (int j = 0; j < 4; ++j) { const int n = (lane >> 3) + 8 * j; const LAS float* s = scr + (8 * c) * 33 + n;
;         const unsigned long long o = (unsigned long long)pg8::pk4_fp8(s[0 * 33], s[1 * 33], s[2 * 33], s[3 * 33]) | ((unsigned long long)pg8::pk4_fp8(s[4 * 33], s[5 * 33], s[6 * 33], s[7 * 33]) << 32);
;         *(GAS unsigned long long*)(WT + (size_t)(n0 + n) * K + k0 + 8 * c) = o; }
;     LDS_WAIT(); asm volatile("" ::: "memory");
; }
	s_add_u32 s8, s58, 0x3000
	s_addc_u32 s9, s59, 0
	global_load_dwordx4 v[176:179], v75, s[8:9]
	s_add_u32 s8, s8, 0x8000
	s_addc_u32 s9, s9, 0
	global_load_dwordx4 v[180:183], v75, s[8:9]
	s_add_u32 s8, s8, 0x8000
	s_addc_u32 s9, s9, 0
	global_load_dwordx4 v[184:187], v75, s[8:9]
	s_add_u32 s8, s8, 0x8000
	s_addc_u32 s9, s9, 0
	global_load_dwordx4 v[188:191], v75, s[8:9]
	s_add_u32 s8, s8, 0x8000
	s_addc_u32 s9, s9, 0
	global_load_dwordx4 v[192:195], v75, s[8:9]
	s_add_u32 s8, s8, 0x8000
	s_addc_u32 s9, s9, 0
	global_load_dwordx4 v[196:199], v75, s[8:9]
	s_add_u32 s8, s8, 0x8000
	s_addc_u32 s9, s9, 0
	global_load_dwordx4 v[200:203], v75, s[8:9]
	s_add_u32 s8, s8, 0x8000
	s_addc_u32 s9, s9, 0
	global_load_dwordx4 v[204:207], v75, s[8:9]
	s_add_u32 s6, s60, 0x400000
	s_addc_u32 s7, s61, 0
	ds_read_b32 v226, v212
	ds_read_b32 v227, v212 offset:512
	ds_read_b32 v228, v212 offset:1024
	ds_read_b32 v229, v212 offset:1536
	ds_read_b32 v230, v212 offset:2048
	ds_read_b32 v231, v212 offset:2560
	ds_read_b32 v232, v212 offset:3072
	ds_read_b32 v233, v212 offset:3584
	ds_read_b32 v234, v212 offset:4096
	ds_read_b32 v235, v212 offset:4608
	ds_read_b32 v236, v212 offset:5120
	ds_read_b32 v237, v212 offset:5632
	ds_read_b32 v238, v212 offset:6144
	ds_read_b32 v239, v212 offset:6656
	ds_read_b32 v240, v212 offset:7168
	ds_read_b32 v241, v212 offset:7680
	s_waitcnt lgkmcnt(0)
	v_max_f32_e32 v226, v226, v226
	v_max_f32_e32 v227, v227, v227
	v_max_f32_e32 v228, v228, v228
	v_max_f32_e32 v229, v229, v229
	v_max_f32_e32 v230, v230, v230
	v_max_f32_e32 v231, v231, v231
	v_max_f32_e32 v232, v232, v232
	v_max_f32_e32 v233, v233, v233
	v_max_f32_e32 v234, v234, v234
	v_max_f32_e32 v235, v235, v235
	v_max_f32_e32 v236, v236, v236
	v_max_f32_e32 v237, v237, v237
	v_max_f32_e32 v238, v238, v238
	v_max_f32_e32 v239, v239, v239
	v_max_f32_e32 v240, v240, v240
	v_max_f32_e32 v241, v241, v241
	v_med3_f32 v226, v226, s62, v95
	v_med3_f32 v227, v227, s62, v95
	v_med3_f32 v228, v228, s62, v95
	v_med3_f32 v229, v229, s62, v95
	v_med3_f32 v230, v230, s62, v95
	v_med3_f32 v231, v231, s62, v95
	v_med3_f32 v232, v232, s62, v95
	v_med3_f32 v233, v233, s62, v95
	v_med3_f32 v234, v234, s62, v95
	v_med3_f32 v235, v235, s62, v95
	v_med3_f32 v236, v236, s62, v95
	v_med3_f32 v237, v237, s62, v95
	v_med3_f32 v238, v238, s62, v95
	v_med3_f32 v239, v239, s62, v95
	v_med3_f32 v240, v240, s62, v95
	v_med3_f32 v241, v241, s62, v95
	v_mov_b32_e32 v242, 0
	v_mov_b32_e32 v243, 0
	v_mov_b32_e32 v244, 0
	v_mov_b32_e32 v245, 0
	v_cvt_pk_fp8_f32 v242, v226, v227
	v_cvt_pk_fp8_f32 v243, v230, v231
	v_cvt_pk_fp8_f32 v244, v234, v235
	v_cvt_pk_fp8_f32 v245, v238, v239
	v_cvt_pk_fp8_f32 v242, v228, v229 op_sel:[0,0,1]
	v_cvt_pk_fp8_f32 v243, v232, v233 op_sel:[0,0,1]
	v_cvt_pk_fp8_f32 v244, v236, v237 op_sel:[0,0,1]
	v_cvt_pk_fp8_f32 v245, v240, v241 op_sel:[0,0,1]
	s_nop 0
	global_store_dwordx4 v77, v[242:245], s[6:7]
	ds_read_b32 v226, v214
	ds_read_b32 v227, v214 offset:512
	ds_read_b32 v228, v214 offset:1024
	ds_read_b32 v229, v214 offset:1536
	ds_read_b32 v230, v214 offset:2048
	ds_read_b32 v231, v214 offset:2560
	ds_read_b32 v232, v214 offset:3072
	ds_read_b32 v233, v214 offset:3584
	ds_read_b32 v234, v214 offset:4096
	ds_read_b32 v235, v214 offset:4608
	ds_read_b32 v236, v214 offset:5120
	ds_read_b32 v237, v214 offset:5632
	ds_read_b32 v238, v214 offset:6144
	ds_read_b32 v239, v214 offset:6656
	ds_read_b32 v240, v214 offset:7168
	ds_read_b32 v241, v214 offset:7680
	s_waitcnt lgkmcnt(0)
	v_max_f32_e32 v226, v226, v226
	v_max_f32_e32 v227, v227, v227
	v_max_f32_e32 v228, v228, v228
	v_max_f32_e32 v229, v229, v229
	v_max_f32_e32 v230, v230, v230
	v_max_f32_e32 v231, v231, v231
	v_max_f32_e32 v232, v232, v232
	v_max_f32_e32 v233, v233, v233
	v_max_f32_e32 v234, v234, v234
	v_max_f32_e32 v235, v235, v235
	v_max_f32_e32 v236, v236, v236
	v_max_f32_e32 v237, v237, v237
	v_max_f32_e32 v238, v238, v238
	v_max_f32_e32 v239, v239, v239
	v_max_f32_e32 v240, v240, v240
	v_max_f32_e32 v241, v241, v241
	v_med3_f32 v226, v226, s62, v95
	v_med3_f32 v227, v227, s62, v95
	v_med3_f32 v228, v228, s62, v95
	v_med3_f32 v229, v229, s62, v95
	v_med3_f32 v230, v230, s62, v95
	v_med3_f32 v231, v231, s62, v95
	v_med3_f32 v232, v232, s62, v95
	v_med3_f32 v233, v233, s62, v95
	v_med3_f32 v234, v234, s62, v95
	v_med3_f32 v235, v235, s62, v95
	v_med3_f32 v236, v236, s62, v95
	v_med3_f32 v237, v237, s62, v95
	v_med3_f32 v238, v238, s62, v95
	v_med3_f32 v239, v239, s62, v95
	v_med3_f32 v240, v240, s62, v95
	v_med3_f32 v241, v241, s62, v95
	v_mov_b32_e32 v242, 0
	v_mov_b32_e32 v243, 0
	v_mov_b32_e32 v244, 0
	v_mov_b32_e32 v245, 0
	v_cvt_pk_fp8_f32 v242, v226, v227
	v_cvt_pk_fp8_f32 v243, v230, v231
	v_cvt_pk_fp8_f32 v244, v234, v235
	v_cvt_pk_fp8_f32 v245, v238, v239
	v_cvt_pk_fp8_f32 v242, v228, v229 op_sel:[0,0,1]
	v_cvt_pk_fp8_f32 v243, v232, v233 op_sel:[0,0,1]
	v_cvt_pk_fp8_f32 v244, v236, v237 op_sel:[0,0,1]
	v_cvt_pk_fp8_f32 v245, v240, v241 op_sel:[0,0,1]
	s_nop 0
	global_store_dwordx4 v78, v[242:245], s[6:7]
	s_waitcnt vmcnt(12)
	v_mul_f32_e32 v144, v66, v144
	v_mul_f32_e32 v145, v66, v145
	v_mul_f32_e32 v146, v66, v146
	v_mul_f32_e32 v147, v66, v147
	ds_write_b128 v209, v[144:147]
	v_mul_f32_e32 v148, v67, v148
	v_mul_f32_e32 v149, v67, v149
	v_mul_f32_e32 v150, v67, v150
	v_mul_f32_e32 v151, v67, v151
	ds_write_b128 v209, v[148:151] offset:1024
	v_mul_f32_e32 v152, v68, v152
	v_mul_f32_e32 v153, v68, v153
	v_mul_f32_e32 v154, v68, v154
	v_mul_f32_e32 v155, v68, v155
	ds_write_b128 v209, v[152:155] offset:2048
	v_mul_f32_e32 v156, v69, v156
	v_mul_f32_e32 v157, v69, v157
	v_mul_f32_e32 v158, v69, v158
	v_mul_f32_e32 v159, v69, v159
	ds_write_b128 v209, v[156:159] offset:3072
	v_mul_f32_e32 v160, v70, v160
	v_mul_f32_e32 v161, v70, v161
	v_mul_f32_e32 v162, v70, v162
	v_mul_f32_e32 v163, v70, v163
	ds_write_b128 v209, v[160:163] offset:4096
	v_mul_f32_e32 v164, v71, v164
	v_mul_f32_e32 v165, v71, v165
	v_mul_f32_e32 v166, v71, v166
	v_mul_f32_e32 v167, v71, v167
	ds_write_b128 v209, v[164:167] offset:5120
	v_mul_f32_e32 v168, v72, v168
	v_mul_f32_e32 v169, v72, v169
	v_mul_f32_e32 v170, v72, v170
	v_mul_f32_e32 v171, v72, v171
	ds_write_b128 v209, v[168:171] offset:6144
	v_mul_f32_e32 v172, v73, v172
	v_mul_f32_e32 v173, v73, v173
	v_mul_f32_e32 v174, v73, v174
	v_mul_f32_e32 v175, v73, v175
	ds_write_b128 v209, v[172:175] offset:7168
	s_waitcnt lgkmcnt(0)
	s_barrier
; #define GAS __attribute__((address_space(1)))
; #define LAS __attribute__((address_space(3)))
; #define LDS_WAIT() asm volatile("s_waitcnt lgkmcnt(0)" ::: "memory")
;     const int pr = item >> 1, kb = 2 * (pr / nblk) + (item & 1), nb = pr % nblk, k0 = 64 * kb, n0 = 32 * nb;
;     const int nr = n0 + (lane & 31); const int sc = MAP == 1 ? src_col_in(nr) : nr;
;     float v[32];
; #pragma unroll
;     for (int i = 0; i < 32; ++i) v[i] = sc >= 0 ? W[(size_t)(k0 + 2 * i + (lane >> 5)) * Nsrc + sc] : 0.f;
; #pragma unroll
;     for (int i = 0; i < 32; ++i) { const int k = k0 + 2 * i + (lane >> 5); float x = v[i] * wscale; if (KS) x *= (k < ksplit ? ksA[k] : ksB[k - ksplit]); scr[(2 * i + (lane >> 5)) * 33 + (lane & 31)] = x; }
;     LDS_WAIT(); asm volatile("" ::: "memory");
;     const int c = lane & 7;
; #pragma unroll
;     for (int j = 0; j < 4; ++j) { const int n = (lane >> 3) + 8 * j; const LAS float* s = scr + (8 * c) * 33 + n;
;         const unsigned long long o = (unsigned long long)pg8::pk4_fp8(s[0 * 33], s[1 * 33], s[2 * 33], s[3 * 33]) | ((unsigned long long)pg8::pk4_fp8(s[4 * 33], s[5 * 33], s[6 * 33], s[7 * 33]) << 32);
;         *(GAS unsigned long long*)(WT + (size_t)(n0 + n) * K + k0 + 8 * c) = o; }
;     LDS_WAIT(); asm volatile("" ::: "memory");
; }
	s_add_u32 s6, s60, 0x800000
	s_addc_u32 s7, s61, 0
	ds_read_b32 v226, v211
	ds_read_b32 v227, v211 offset:512
	ds_read_b32 v228, v211 offset:1024
	ds_read_b32 v229, v211 offset:1536
	ds_read_b32 v230, v211 offset:2048
	ds_read_b32 v231, v211 offset:2560
	ds_read_b32 v232, v211 offset:3072
	ds_read_b32 v233, v211 offset:3584
	ds_read_b32 v234, v211 offset:4096
	ds_read_b32 v235, v211 offset:4608
	ds_read_b32 v236, v211 offset:5120
	ds_read_b32 v237, v211 offset:5632
	ds_read_b32 v238, v211 offset:6144
	ds_read_b32 v239, v211 offset:6656
	ds_read_b32 v240, v211 offset:7168
	ds_read_b32 v241, v211 offset:7680
	s_waitcnt lgkmcnt(0)
	v_max_f32_e32 v226, v226, v226
	v_max_f32_e32 v227, v227, v227
	v_max_f32_e32 v228, v228, v228
	v_max_f32_e32 v229, v229, v229
	v_max_f32_e32 v230, v230, v230
	v_max_f32_e32 v231, v231, v231
	v_max_f32_e32 v232, v232, v232
	v_max_f32_e32 v233, v233, v233
	v_max_f32_e32 v234, v234, v234
	v_max_f32_e32 v235, v235, v235
	v_max_f32_e32 v236, v236, v236
	v_max_f32_e32 v237, v237, v237
	v_max_f32_e32 v238, v238, v238
	v_max_f32_e32 v239, v239, v239
	v_max_f32_e32 v240, v240, v240
	v_max_f32_e32 v241, v241, v241
	v_med3_f32 v226, v226, s62, v95
	v_med3_f32 v227, v227, s62, v95
	v_med3_f32 v228, v228, s62, v95
	v_med3_f32 v229, v229, s62, v95
	v_med3_f32 v230, v230, s62, v95
	v_med3_f32 v231, v231, s62, v95
	v_med3_f32 v232, v232, s62, v95
	v_med3_f32 v233, v233, s62, v95
	v_med3_f32 v234, v234, s62, v95
	v_med3_f32 v235, v235, s62, v95
	v_med3_f32 v236, v236, s62, v95
	v_med3_f32 v237, v237, s62, v95
	v_med3_f32 v238, v238, s62, v95
	v_med3_f32 v239, v239, s62, v95
	v_med3_f32 v240, v240, s62, v95
	v_med3_f32 v241, v241, s62, v95
	v_mov_b32_e32 v242, 0
	v_mov_b32_e32 v243, 0
	v_mov_b32_e32 v244, 0
	v_mov_b32_e32 v245, 0
	v_cvt_pk_fp8_f32 v242, v226, v227
	v_cvt_pk_fp8_f32 v243, v230, v231
	v_cvt_pk_fp8_f32 v244, v234, v235
	v_cvt_pk_fp8_f32 v245, v238, v239
	v_cvt_pk_fp8_f32 v242, v228, v229 op_sel:[0,0,1]
	v_cvt_pk_fp8_f32 v243, v232, v233 op_sel:[0,0,1]
	v_cvt_pk_fp8_f32 v244, v236, v237 op_sel:[0,0,1]
	v_cvt_pk_fp8_f32 v245, v240, v241 op_sel:[0,0,1]
	s_nop 0
	global_store_dwordx4 v77, v[242:245], s[6:7]
	ds_read_b32 v226, v213
	ds_read_b32 v227, v213 offset:512
	ds_read_b32 v228, v213 offset:1024
	ds_read_b32 v229, v213 offset:1536
	ds_read_b32 v230, v213 offset:2048
	ds_read_b32 v231, v213 offset:2560
	ds_read_b32 v232, v213 offset:3072
	ds_read_b32 v233, v213 offset:3584
	ds_read_b32 v234, v213 offset:4096
	ds_read_b32 v235, v213 offset:4608
	ds_read_b32 v236, v213 offset:5120
	ds_read_b32 v237, v213 offset:5632
	ds_read_b32 v238, v213 offset:6144
	ds_read_b32 v239, v213 offset:6656
	ds_read_b32 v240, v213 offset:7168
	ds_read_b32 v241, v213 offset:7680
	s_waitcnt lgkmcnt(0)
	v_max_f32_e32 v226, v226, v226
	v_max_f32_e32 v227, v227, v227
	v_max_f32_e32 v228, v228, v228
	v_max_f32_e32 v229, v229, v229
	v_max_f32_e32 v230, v230, v230
	v_max_f32_e32 v231, v231, v231
	v_max_f32_e32 v232, v232, v232
	v_max_f32_e32 v233, v233, v233
	v_max_f32_e32 v234, v234, v234
	v_max_f32_e32 v235, v235, v235
	v_max_f32_e32 v236, v236, v236
	v_max_f32_e32 v237, v237, v237
	v_max_f32_e32 v238, v238, v238
	v_max_f32_e32 v239, v239, v239
	v_max_f32_e32 v240, v240, v240
	v_max_f32_e32 v241, v241, v241
	v_med3_f32 v226, v226, s62, v95
	v_med3_f32 v227, v227, s62, v95
	v_med3_f32 v228, v228, s62, v95
	v_med3_f32 v229, v229, s62, v95
	v_med3_f32 v230, v230, s62, v95
	v_med3_f32 v231, v231, s62, v95
	v_med3_f32 v232, v232, s62, v95
	v_med3_f32 v233, v233, s62, v95
	v_med3_f32 v234, v234, s62, v95
	v_med3_f32 v235, v235, s62, v95
	v_med3_f32 v236, v236, s62, v95
	v_med3_f32 v237, v237, s62, v95
	v_med3_f32 v238, v238, s62, v95
	v_med3_f32 v239, v239, s62, v95
	v_med3_f32 v240, v240, s62, v95
	v_med3_f32 v241, v241, s62, v95
	v_mov_b32_e32 v242, 0
	v_mov_b32_e32 v243, 0
	v_mov_b32_e32 v244, 0
	v_mov_b32_e32 v245, 0
	v_cvt_pk_fp8_f32 v242, v226, v227
	v_cvt_pk_fp8_f32 v243, v230, v231
	v_cvt_pk_fp8_f32 v244, v234, v235
	v_cvt_pk_fp8_f32 v245, v238, v239
	v_cvt_pk_fp8_f32 v242, v228, v229 op_sel:[0,0,1]
	v_cvt_pk_fp8_f32 v243, v232, v233 op_sel:[0,0,1]
	v_cvt_pk_fp8_f32 v244, v236, v237 op_sel:[0,0,1]
	v_cvt_pk_fp8_f32 v245, v240, v241 op_sel:[0,0,1]
	s_nop 0
	global_store_dwordx4 v78, v[242:245], s[6:7]
	s_waitcnt vmcnt(4)
	v_mul_f32_e32 v176, v66, v176
	v_mul_f32_e32 v177, v66, v177
	v_mul_f32_e32 v178, v66, v178
	v_mul_f32_e32 v179, v66, v179
	ds_write_b128 v210, v[176:179]
	v_mul_f32_e32 v180, v67, v180
	v_mul_f32_e32 v181, v67, v181
	v_mul_f32_e32 v182, v67, v182
	v_mul_f32_e32 v183, v67, v183
	ds_write_b128 v210, v[180:183] offset:1024
	v_mul_f32_e32 v184, v68, v184
	v_mul_f32_e32 v185, v68, v185
	v_mul_f32_e32 v186, v68, v186
	v_mul_f32_e32 v187, v68, v187
	ds_write_b128 v210, v[184:187] offset:2048
	v_mul_f32_e32 v188, v69, v188
	v_mul_f32_e32 v189, v69, v189
	v_mul_f32_e32 v190, v69, v190
	v_mul_f32_e32 v191, v69, v191
	ds_write_b128 v210, v[188:191] offset:3072
	v_mul_f32_e32 v192, v70, v192
	v_mul_f32_e32 v193, v70, v193
	v_mul_f32_e32 v194, v70, v194
	v_mul_f32_e32 v195, v70, v195
	ds_write_b128 v210, v[192:195] offset:4096
	v_mul_f32_e32 v196, v71, v196
	v_mul_f32_e32 v197, v71, v197
	v_mul_f32_e32 v198, v71, v198
	v_mul_f32_e32 v199, v71, v199
	ds_write_b128 v210, v[196:199] offset:5120
	v_mul_f32_e32 v200, v72, v200
	v_mul_f32_e32 v201, v72, v201
	v_mul_f32_e32 v202, v72, v202
	v_mul_f32_e32 v203, v72, v203
	ds_write_b128 v210, v[200:203] offset:6144
	v_mul_f32_e32 v204, v73, v204
	v_mul_f32_e32 v205, v73, v205
	v_mul_f32_e32 v206, v73, v206
	v_mul_f32_e32 v207, v73, v207
	ds_write_b128 v210, v[204:207] offset:7168
	s_waitcnt lgkmcnt(0)
	s_barrier
; #define GAS __attribute__((address_space(1)))
; #define LAS __attribute__((address_space(3)))
; #define LDS_WAIT() asm volatile("s_waitcnt lgkmcnt(0)" ::: "memory")
;     const int pr = item >> 1, kb = 2 * (pr / nblk) + (item & 1), nb = pr % nblk, k0 = 64 * kb, n0 = 32 * nb;
;     const int nr = n0 + (lane & 31); const int sc = MAP == 1 ? src_col_in(nr) : nr;
;     float v[32];
; #pragma unroll
;     for (int i = 0; i < 32; ++i) v[i] = sc >= 0 ? W[(size_t)(k0 + 2 * i + (lane >> 5)) * Nsrc + sc] : 0.f;
; #pragma unroll
;     for (int i = 0; i < 32; ++i) { const int k = k0 + 2 * i + (lane >> 5); float x = v[i] * wscale; if (KS) x *= (k < ksplit ? ksA[k] : ksB[k - ksplit]); scr[(2 * i + (lane >> 5)) * 33 + (lane & 31)] = x; }
;     LDS_WAIT(); asm volatile("" ::: "memory");
;     const int c = lane & 7;
; #pragma unroll
;     for (int j = 0; j < 4; ++j) { const int n = (lane >> 3) + 8 * j; const LAS float* s = scr + (8 * c) * 33 + n;
;         const unsigned long long o = (unsigned long long)pg8::pk4_fp8(s[0 * 33], s[1 * 33], s[2 * 33], s[3 * 33]) | ((unsigned long long)pg8::pk4_fp8(s[4 * 33], s[5 * 33], s[6 * 33], s[7 * 33]) << 32);
;         *(GAS unsigned long long*)(WT + (size_t)(n0 + n) * K + k0 + 8 * c) = o; }
;     LDS_WAIT(); asm volatile("" ::: "memory");
; }
	s_add_u32 s6, s60, 0xc00000
	s_addc_u32 s7, s61, 0
	ds_read_b32 v226, v212
	ds_read_b32 v227, v212 offset:512
	ds_read_b32 v228, v212 offset:1024
	ds_read_b32 v229, v212 offset:1536
	ds_read_b32 v230, v212 offset:2048
	ds_read_b32 v231, v212 offset:2560
	ds_read_b32 v232, v212 offset:3072
	ds_read_b32 v233, v212 offset:3584
	ds_read_b32 v234, v212 offset:4096
	ds_read_b32 v235, v212 offset:4608
	ds_read_b32 v236, v212 offset:5120
	ds_read_b32 v237, v212 offset:5632
	ds_read_b32 v238, v212 offset:6144
	ds_read_b32 v239, v212 offset:6656
	ds_read_b32 v240, v212 offset:7168
	ds_read_b32 v241, v212 offset:7680
	s_waitcnt lgkmcnt(0)
	v_max_f32_e32 v226, v226, v226
	v_max_f32_e32 v227, v227, v227
	v_max_f32_e32 v228, v228, v228
	v_max_f32_e32 v229, v229, v229
	v_max_f32_e32 v230, v230, v230
	v_max_f32_e32 v231, v231, v231
	v_max_f32_e32 v232, v232, v232
	v_max_f32_e32 v233, v233, v233
	v_max_f32_e32 v234, v234, v234
	v_max_f32_e32 v235, v235, v235
	v_max_f32_e32 v236, v236, v236
	v_max_f32_e32 v237, v237, v237
	v_max_f32_e32 v238, v238, v238
	v_max_f32_e32 v239, v239, v239
	v_max_f32_e32 v240, v240, v240
	v_max_f32_e32 v241, v241, v241
	v_med3_f32 v226, v226, s62, v95
	v_med3_f32 v227, v227, s62, v95
	v_med3_f32 v228, v228, s62, v95
	v_med3_f32 v229, v229, s62, v95
	v_med3_f32 v230, v230, s62, v95
	v_med3_f32 v231, v231, s62, v95
	v_med3_f32 v232, v232, s62, v95
	v_med3_f32 v233, v233, s62, v95
	v_med3_f32 v234, v234, s62, v95
	v_med3_f32 v235, v235, s62, v95
	v_med3_f32 v236, v236, s62, v95
	v_med3_f32 v237, v237, s62, v95
	v_med3_f32 v238, v238, s62, v95
	v_med3_f32 v239, v239, s62, v95
	v_med3_f32 v240, v240, s62, v95
	v_med3_f32 v241, v241, s62, v95
	v_mov_b32_e32 v242, 0
	v_mov_b32_e32 v243, 0
	v_mov_b32_e32 v244, 0
	v_mov_b32_e32 v245, 0
	v_cvt_pk_fp8_f32 v242, v226, v227
	v_cvt_pk_fp8_f32 v243, v230, v231
	v_cvt_pk_fp8_f32 v244, v234, v235
	v_cvt_pk_fp8_f32 v245, v238, v239
	v_cvt_pk_fp8_f32 v242, v228, v229 op_sel:[0,0,1]
	v_cvt_pk_fp8_f32 v243, v232, v233 op_sel:[0,0,1]
	v_cvt_pk_fp8_f32 v244, v236, v237 op_sel:[0,0,1]
	v_cvt_pk_fp8_f32 v245, v240, v241 op_sel:[0,0,1]
	s_nop 0
	global_store_dwordx4 v77, v[242:245], s[6:7]
	ds_read_b32 v226, v214
	ds_read_b32 v227, v214 offset:512
	ds_read_b32 v228, v214 offset:1024
	ds_read_b32 v229, v214 offset:1536
	ds_read_b32 v230, v214 offset:2048
	ds_read_b32 v231, v214 offset:2560
	ds_read_b32 v232, v214 offset:3072
	ds_read_b32 v233, v214 offset:3584
	ds_read_b32 v234, v214 offset:4096
	ds_read_b32 v235, v214 offset:4608
	ds_read_b32 v236, v214 offset:5120
	ds_read_b32 v237, v214 offset:5632
	ds_read_b32 v238, v214 offset:6144
	ds_read_b32 v239, v214 offset:6656
	ds_read_b32 v240, v214 offset:7168
	ds_read_b32 v241, v214 offset:7680
	s_waitcnt lgkmcnt(0)
	v_max_f32_e32 v226, v226, v226
	v_max_f32_e32 v227, v227, v227
	v_max_f32_e32 v228, v228, v228
	v_max_f32_e32 v229, v229, v229
	v_max_f32_e32 v230, v230, v230
	v_max_f32_e32 v231, v231, v231
	v_max_f32_e32 v232, v232, v232
	v_max_f32_e32 v233, v233, v233
	v_max_f32_e32 v234, v234, v234
	v_max_f32_e32 v235, v235, v235
	v_max_f32_e32 v236, v236, v236
	v_max_f32_e32 v237, v237, v237
	v_max_f32_e32 v238, v238, v238
	v_max_f32_e32 v239, v239, v239
	v_max_f32_e32 v240, v240, v240
	v_max_f32_e32 v241, v241, v241
	v_med3_f32 v226, v226, s62, v95
	v_med3_f32 v227, v227, s62, v95
	v_med3_f32 v228, v228, s62, v95
	v_med3_f32 v229, v229, s62, v95
	v_med3_f32 v230, v230, s62, v95
	v_med3_f32 v231, v231, s62, v95
	v_med3_f32 v232, v232, s62, v95
	v_med3_f32 v233, v233, s62, v95
	v_med3_f32 v234, v234, s62, v95
	v_med3_f32 v235, v235, s62, v95
	v_med3_f32 v236, v236, s62, v95
	v_med3_f32 v237, v237, s62, v95
	v_med3_f32 v238, v238, s62, v95
	v_med3_f32 v239, v239, s62, v95
	v_med3_f32 v240, v240, s62, v95
	v_med3_f32 v241, v241, s62, v95
	v_mov_b32_e32 v242, 0
	v_mov_b32_e32 v243, 0
	v_mov_b32_e32 v244, 0
	v_mov_b32_e32 v245, 0
	v_cvt_pk_fp8_f32 v242, v226, v227
	v_cvt_pk_fp8_f32 v243, v230, v231
	v_cvt_pk_fp8_f32 v244, v234, v235
	v_cvt_pk_fp8_f32 v245, v238, v239
	v_cvt_pk_fp8_f32 v242, v228, v229 op_sel:[0,0,1]
	v_cvt_pk_fp8_f32 v243, v232, v233 op_sel:[0,0,1]
	v_cvt_pk_fp8_f32 v244, v236, v237 op_sel:[0,0,1]
	v_cvt_pk_fp8_f32 v245, v240, v241 op_sel:[0,0,1]
	s_nop 0
	global_store_dwordx4 v78, v[242:245], s[6:7]
	s_waitcnt lgkmcnt(0)
	s_barrier
; __global__ void __launch_bounds__(NWAVES * 64, 2) hybrid_fwd(Args args) {
;     ...
;     for (int L = 0; L < DEPTH; ++L) {
;         { unsigned long long wz = 0; asm volatile("" : "+s"(wz)); ws = args.ws + wz; }
;         bf16* Hres = (bf16*)(ws + WS_H);     static_assert(DEPTH == 2 && WO_F8_FROM == 1 && PROJ_F8_FROM == 1, "the phase instantiations below are written for this precision plan");
;         bf16* XN = (bf16*)(ws + WS_XN); bf16* PROJ = (bf16*)(ws + WS_PROJ); bf16* ACT = (bf16*)(ws + WS_ACT); unsigned char* CAT = (unsigned char*)(ws + WS_CAT);     const bool wo_f8 = L >= WO_F8_FROM;
;         float* ATT = (float*)(ws + WS_ATT); bf16* XBC = (bf16*)(ws + WS_XBC); bf16* Y = (bf16*)(ws + WS_Y);
;         bf16* KC = (bf16*)(ws + WS_KC); bf16* VC = (bf16*)(ws + WS_VC); float* DT = (float*)(ws + WS_DT); float* ADT = (float*)(ws + WS_ADT);
;         float* COS = (float*)(ws + WS_COS); float* SIN = (float*)(ws + WS_SIN); unsigned* BMP = (unsigned*)(ws + WS_BMP);
;         bf16* AO = (bf16*)(ws + WS_ACT);     float* STT = (float*)(ws + WS_ST); bf16* PREVB = (bf16*)(ws + WS_PREV);     float* ACSG = (float*)(ws + WS_ACSG); float* DEC = (float*)(ws + WS_DEC);
;         {
;             const bool split = (L < PROJ_F8_FROM) && (F.G == 256);
;             if (L >= PROJ_F8_FROM) { pg8::StaticOrder So; So.init(S, NPROJ, F.G, (int)blockIdx.x); pg8::Gemm g{XN, (const bf16*)(ws + WS_WIN + L * SZ_WIN), S, NPROJ, DM / 2};
;                 pg8::EpiProj E{PROJ, NPROJ, COS, SIN, QSCALE, 1.f / (XN8_SCALE * WUP8_SCALE), 0};
;                 pg8::gemm_phase<pg8::EpiProj, pg8::StaticOrder, true, true, true>(F.lds + RING_OFF, g, So, E); }
	v_readlane_b32 s12, v253, 35
	v_readlane_b32 s18, v253, 41
	v_readlane_b32 s19, v253, 42
	s_add_u32 s81, s18, 0x1f600000
	s_addc_u32 s94, s19, 0
	s_add_u32 s24, s18, 0xf600000
	v_or_b32_e32 v2, 2, v6
	v_mov_b32_e32 v3, 0x630
	v_readlane_b32 s13, v253, 36
	v_readlane_b32 s14, v253, 37
	v_readlane_b32 s15, v253, 38
	s_addc_u32 s25, s19, 0
	v_mad_u32_u24 v58, v2, s0, v3
	v_mov_b32_e32 v3, 0xc60
	s_add_u32 s26, s18, 0xb600000
	v_mad_u32_u24 v59, v2, s0, v3
	v_readlane_b32 s0, v253, 19
	s_addc_u32 s27, s19, 0
	v_readlane_b32 s2, v253, 21
	v_readlane_b32 s10, v253, 29
	v_readlane_b32 s3, v253, 22
	v_readlane_b32 s11, v253, 30
	s_add_u32 s2, s10, 0x4000000
	v_readlane_b32 s40, v253, 3
	s_addc_u32 s3, s11, 0
	v_readlane_b32 s52, v253, 15
	v_readlane_b32 s53, v253, 16
	s_add_u32 s22, s52, 0x2000
	v_readlane_b32 s8, v253, 27
	s_addc_u32 s23, s53, 0
	v_readlane_b32 s9, v253, 28
	s_add_u32 s84, s8, 0x2000
	s_addc_u32 s85, s9, 0
	s_add_u32 s33, s18, 0x200000
	v_readlane_b32 s44, v253, 7
	s_addc_u32 s38, s19, 0
	v_mov_b32_e32 v9, v11
	v_readlane_b32 s1, v253, 20
	v_readlane_b32 s45, v253, 8
	s_add_u32 s86, s44, 0xb140000
	v_mul_u32_u24_e32 v57, 0x84, v2
	v_readlane_b32 s42, v253, 5
	v_lshl_add_u64 v[2:3], s[18:19], 0, v[8:9]
	s_mov_b64 s[0:1], 0xd600000
	s_addc_u32 s87, s45, 0
	v_readlane_b32 s12, v253, 31
	v_readlane_b32 s13, v253, 32
	v_readlane_b32 s14, v253, 33
	v_readlane_b32 s15, v253, 34
	v_readlane_b32 s43, v253, 6
	v_readlane_b32 s54, v253, 17
	v_readlane_b32 s55, v253, 18
	v_lshl_add_u64 v[12:13], v[2:3], 0, s[0:1]
	s_add_u32 s88, s42, 0x4000
	s_mov_b64 s[0:1], 0x5c00000
	v_readlane_b32 s41, v253, 4
	v_readlane_b32 s46, v253, 9
	v_readlane_b32 s47, v253, 10
	v_readlane_b32 s48, v253, 11
	v_readlane_b32 s49, v253, 12
	v_readlane_b32 s50, v253, 13
	s_addc_u32 s89, s43, 0
	v_lshlrev_b32_e32 v4, 6, v18
	v_lshl_add_u64 v[14:15], v[2:3], 0, s[0:1]
	s_lshl_b32 s0, s80, 5
	s_movk_i32 s12, 0xe000
	s_movk_i32 s14, 0xe008
	s_movk_i32 s18, 0xe010
	s_movk_i32 s78, 0xe018
	s_movk_i32 s92, 0xe0d0
	s_movk_i32 s28, 0xe0d8
	s_movk_i32 s34, 0xe0e0
	s_movk_i32 s52, 0xe0e8
	s_movk_i32 s54, 0xe0f0
	s_movk_i32 s56, 0xe0f8
	v_or_b32_e32 v26, 0x2000, v18
	v_or_b32_e32 v27, 0x4000, v18
	v_or_b32_e32 v28, 0x6000, v18
	v_or_b32_e32 v29, 0x8000, v18
	v_or_b32_e32 v30, 0xa000, v18
	v_or_b32_e32 v31, 0xc000, v18
	v_or_b32_e32 v32, 0xe000, v18
	v_or_b32_e32 v33, 0x10000, v18
	v_or_b32_e32 v34, 0x12000, v18
	v_or_b32_e32 v35, 0x14000, v18
	v_or_b32_e32 v36, 0x16000, v18
	v_or_b32_e32 v37, 0x18000, v18
	v_or_b32_e32 v38, 0x1a000, v18
	v_or_b32_e32 v39, 0x1c000, v18
	v_or_b32_e32 v40, 0x1e000, v18
	v_or_b32_e32 v41, 0x20000, v18
	v_or_b32_e32 v42, 0x22000, v18
	v_or_b32_e32 v43, 0x24000, v18
	v_or_b32_e32 v44, 0x26000, v18
	v_or_b32_e32 v45, 0x28000, v18
	v_or_b32_e32 v46, 0x2a000, v18
	v_or_b32_e32 v47, 0x2c000, v18
	v_or_b32_e32 v48, 0x2e000, v18
	v_or_b32_e32 v49, 0x30000, v18
	v_or_b32_e32 v50, 0x32000, v18
	v_or_b32_e32 v51, 0x34000, v18
	v_or_b32_e32 v52, 0x36000, v18
	v_or_b32_e32 v53, 0x38000, v18
	v_or_b32_e32 v54, 0x3a000, v18
	v_or_b32_e32 v55, 0x3c000, v18
	v_or_b32_e32 v56, 0x3e000, v18
	v_and_b32_e32 v60, 64, v4
	v_mov_b32_e32 v7, v11
	s_lshl_b32 s39, s80, 6
	s_add_i32 s40, s0, 0xfff4c000
	s_lshl_b32 s41, s83, 8
	s_lshl_b32 s42, s80, 4
	s_lshl_b32 s43, s83, 7
	s_mov_b32 s91, 0
	s_mov_b32 s44, 0xc3e00000
	s_movk_i32 s45, 0x7fff
	s_mov_b32 s46, 0xffff0000
	s_movk_i32 s47, 0x2c2f
	s_movk_i32 s48, 0x2c50
	s_mov_b32 s49, 0xb140
	v_add_u32_e32 v61, 0x400, v19
	v_add_u32_e32 v62, 0x800, v19
	v_add_u32_e32 v63, 0xc00, v19
	v_mov_b32_e32 v64, 0x43e00000
	s_mov_b32 s50, s80
	s_mov_b32 s13, -1
	s_mov_b32 s15, -1
	s_mov_b32 s19, -1
	s_mov_b32 s79, -1
	s_mov_b32 s93, -1
	s_mov_b32 s29, -1
	s_mov_b32 s35, -1
	s_mov_b32 s53, -1
	s_mov_b32 s55, -1
	s_mov_b32 s57, -1
	v_readlane_b32 s16, v253, 39
	v_readlane_b32 s17, v253, 40
	v_readlane_b32 s4, v253, 23
	v_readlane_b32 s5, v253, 24
	v_readlane_b32 s6, v253, 25
	v_readlane_b32 s7, v253, 26
	v_readlane_b32 s51, v253, 14
	s_branch .LBB0_15

; #define LDS_WAIT() asm volatile("s_waitcnt lgkmcnt(0)" ::: "memory")
;     const int pr = item >> 1, kb = 2 * (pr / nblk) + (item & 1), nb = pr % nblk, k0 = 64 * kb, n0 = 32 * nb;
;     const int nr = n0 + (lane & 31); const int sc = MAP == 1 ? src_col_in(nr) : nr;
;     float v[32];
; #pragma unroll
;     for (int i = 0; i < 32; ++i) v[i] = sc >= 0 ? W[(size_t)(k0 + 2 * i + (lane >> 5)) * Nsrc + sc] : 0.f;
; #pragma unroll
;     for (int i = 0; i < 32; ++i) { const int k = k0 + 2 * i + (lane >> 5); float x = v[i] * wscale; if (KS) x *= (k < ksplit ? ksA[k] : ksB[k - ksplit]); scr[(2 * i + (lane >> 5)) * 33 + (lane & 31)] = x; }
;     LDS_WAIT(); asm volatile("" ::: "memory");
; __global__ void __launch_bounds__(NWAVES * 64, 2) hybrid_fwd(Args args) {
;     ...
;         for (int it = gw; it < DEPTH * I_L; it += NGW) {
;             const int l = it / I_L; int r = it % I_L;
;             if (r < I_IN) { if (l >= PROJ_F8_FROM) p0_transpose_item_f8<true, 1>(args.in[2] + (size_t)l * DM * NSRC, DM, NSRC, NPROJ / 32, (unsigned char*)(ws + WS_WIN + l * SZ_WIN), WUP8_SCALE, args.in[1] + l * DM, args.in[1] + l * DM, DM, scr, r, lane);
;                 else p0_transpose_item<1, true>(args.in[2] + (size_t)l * DM * NSRC, DM, NSRC, NPROJ / 32, (bf16*)(ws + WS_WIN + l * SZ_WIN), args.in[1] + l * DM, args.in[1] + l * DM, DM, scr, r, lane); continue; } r -= I_IN;
;             if (r < I_O) { if (l >= WO_F8_FROM) p0_transpose_item_f8<true>(args.in[13] + (size_t)l * DM * DM, DM, DM, DM / 32, (unsigned char*)(ws + WS_WO + l * SZ_WO), 64.f, args.in[6] + l * 2048, args.in[12] + l * 2048, 2048, scr, r, lane);
;                 else p0_transpose_item<0, true>(args.in[13] + (size_t)l * DM * DM, DM, DM, DM / 32, (bf16*)(ws + WS_WO + l * SZ_WO), args.in[6] + l * 2048, args.in[12] + l * 2048, 2048, scr, r, lane); continue; } r -= I_O;
;             if (r < I_UP) { p0_transpose_item_f8<true>(args.in[15] + (size_t)l * DM * FF, DM, FF, FF / 32, (unsigned char*)(ws + WS_WUP + l * SZ_WUP), WUP8_SCALE, args.in[14] + l * DM, args.in[14] + l * DM, DM, scr, r, lane); continue; } r -= I_UP;
;             p0_transpose_item_f8<false>(args.in[16] + (size_t)l * FF * DM, FF, DM, DM / 32, (unsigned char*)(ws + WS_WDN + l * SZ_WDN), 128.f, args.in[16], args.in[16], 0, scr, r, lane);
.LBB0_575:
	s_waitcnt vmcnt(0)
	s_barrier
	s_cmpk_lt_u32 s77, 0xa0
	s_cbranch_scc1 .Llite_skip
	s_sub_i32 s16, s77, 160
	v_and_b32_e32 v133, 63, v0
	v_lshrrev_b32_e32 v134, 6, v0
	v_lshrrev_b32_e32 v130, 5, v133
	v_lshl_add_u32 v131, v134, 4, v130
	v_and_b32_e32 v132, 31, v133
	v_xor_b32_e32 v132, v132, v134
	v_lshlrev_b32_e32 v132, 4, v132
	v_lshl_add_u32 v120, v131, 9, v132
	v_add_u32_e32 v121, 0x10000, v120
	v_and_b32_e32 v132, 31, v133
	v_lshlrev_b32_e32 v132, 4, v132
	s_mov_b32 s21, 0x4000
	v_mad_u32_u24 v126, v131, s21, v132
	v_and_b32_e32 v130, 7, v133
	v_lshrrev_b32_e32 v131, 5, v133
	v_lshl_add_u32 v131, v134, 2, v131
	v_xor_b32_e32 v131, v131, v130
	v_lshlrev_b32_e32 v131, 4, v131
	v_lshl_add_u32 v131, v130, 13, v131
	v_bfe_u32 v132, v133, 3, 2
	v_lshl_add_u32 v122, v132, 2, v131
	v_add_u32_e32 v123, 0x10000, v122
	v_and_b32_e32 v130, 7, v133
	v_lshrrev_b32_e32 v131, 5, v133
	v_lshl_add_u32 v131, v134, 2, v131
	v_add_u32_e32 v131, 2, v131
	v_xor_b32_e32 v131, v131, v130
	v_lshlrev_b32_e32 v131, 4, v131
	v_lshl_add_u32 v131, v130, 13, v131
	v_bfe_u32 v132, v133, 3, 2
	v_lshl_add_u32 v124, v132, 2, v131
	v_add_u32_e32 v125, 0x10000, v124
	v_lshrrev_b32_e32 v130, 3, v133
	v_lshl_add_u32 v130, v134, 4, v130
	v_and_b32_e32 v131, 7, v133
	v_lshlrev_b32_e32 v131, 4, v131
	v_lshl_add_u32 v127, v130, 14, v131
	v_lshrrev_b32_e32 v130, 3, v133
	v_lshl_add_u32 v130, v134, 4, v130
	v_add_u32_e32 v130, 8, v130
	v_and_b32_e32 v131, 7, v133
	v_lshlrev_b32_e32 v131, 4, v131
	v_lshl_add_u32 v128, v130, 14, v131
	v_mov_b32_e32 v129, 0x43e00000
	s_mov_b32 s20, 0xc3e00000
	v_readlane_b32 s2, v253, 35
	v_readlane_b32 s3, v253, 36
	v_readlane_b32 s4, v253, 41
	v_readlane_b32 s5, v253, 42
	s_add_u32 s2, s2, 0x10000000
	s_addc_u32 s3, s3, 0
	s_add_u32 s4, s4, 0x27600000
	s_addc_u32 s5, s5, 0
	s_add_i32 s17, s16, 0
	s_min_u32 s17, s17, 0x3ff
	s_lshr_b32 s18, s17, 5
	s_add_i32 s18, s18, 96
	s_and_b32 s19, s17, 31
	s_lshl_b32 s18, s18, 21
	s_lshl_b32 s19, s19, 9
	s_add_u32 s18, s18, s19
	s_add_u32 s12, s2, s18
	s_addc_u32 s13, s3, 0
	global_load_dwordx4 v[36:39], v126, s[12:13]
	s_add_u32 s12, s12, 0x8000
	s_addc_u32 s13, s13, 0
	global_load_dwordx4 v[40:43], v126, s[12:13]
	s_add_u32 s12, s12, 0x8000
	s_addc_u32 s13, s13, 0
	global_load_dwordx4 v[44:47], v126, s[12:13]
	s_add_u32 s12, s12, 0x8000
	s_addc_u32 s13, s13, 0
	global_load_dwordx4 v[48:51], v126, s[12:13]
	s_add_u32 s12, s12, 0x8000
	s_addc_u32 s13, s13, 0
	global_load_dwordx4 v[52:55], v126, s[12:13]
	s_add_u32 s12, s12, 0x8000
	s_addc_u32 s13, s13, 0
	global_load_dwordx4 v[56:59], v126, s[12:13]
	s_add_u32 s12, s12, 0x8000
	s_addc_u32 s13, s13, 0
	global_load_dwordx4 v[60:63], v126, s[12:13]
	s_add_u32 s12, s12, 0x8000
	s_addc_u32 s13, s13, 0
	global_load_dwordx4 v[64:67], v126, s[12:13]
	s_add_i32 s17, s16, 96
	s_min_u32 s17, s17, 0x3ff
	s_lshr_b32 s18, s17, 5
	s_add_i32 s18, s18, 96
	s_and_b32 s19, s17, 31
	s_lshl_b32 s18, s18, 21
	s_lshl_b32 s19, s19, 9
	s_add_u32 s18, s18, s19
	s_add_u32 s12, s2, s18
	s_addc_u32 s13, s3, 0
	global_load_dwordx4 v[68:71], v126, s[12:13]
	s_add_u32 s12, s12, 0x8000
	s_addc_u32 s13, s13, 0
	global_load_dwordx4 v[72:75], v126, s[12:13]
	s_add_u32 s12, s12, 0x8000
	s_addc_u32 s13, s13, 0
	global_load_dwordx4 v[76:79], v126, s[12:13]
	s_add_u32 s12, s12, 0x8000
	s_addc_u32 s13, s13, 0
	global_load_dwordx4 v[80:83], v126, s[12:13]
	s_add_u32 s12, s12, 0x8000
	s_addc_u32 s13, s13, 0
	global_load_dwordx4 v[84:87], v126, s[12:13]
	s_add_u32 s12, s12, 0x8000
	s_addc_u32 s13, s13, 0
	global_load_dwordx4 v[88:91], v126, s[12:13]
	s_add_u32 s12, s12, 0x8000
	s_addc_u32 s13, s13, 0
	global_load_dwordx4 v[92:95], v126, s[12:13]
	s_add_u32 s12, s12, 0x8000
	s_addc_u32 s13, s13, 0
	global_load_dwordx4 v[96:99], v126, s[12:13]
	s_waitcnt vmcnt(8)
	v_mul_f32_e32 v36, 0x43000000, v36
	v_mul_f32_e32 v37, 0x43000000, v37
	v_mul_f32_e32 v38, 0x43000000, v38
	v_mul_f32_e32 v39, 0x43000000, v39
	ds_write_b128 v120, v[36:39]
	v_mul_f32_e32 v40, 0x43000000, v40
	v_mul_f32_e32 v41, 0x43000000, v41
	v_mul_f32_e32 v42, 0x43000000, v42
	v_mul_f32_e32 v43, 0x43000000, v43
	ds_write_b128 v120, v[40:43] offset:1024
	v_mul_f32_e32 v44, 0x43000000, v44
	v_mul_f32_e32 v45, 0x43000000, v45
	v_mul_f32_e32 v46, 0x43000000, v46
	v_mul_f32_e32 v47, 0x43000000, v47
	ds_write_b128 v120, v[44:47] offset:2048
	v_mul_f32_e32 v48, 0x43000000, v48
	v_mul_f32_e32 v49, 0x43000000, v49
	v_mul_f32_e32 v50, 0x43000000, v50
	v_mul_f32_e32 v51, 0x43000000, v51
	ds_write_b128 v120, v[48:51] offset:3072
	v_mul_f32_e32 v52, 0x43000000, v52
	v_mul_f32_e32 v53, 0x43000000, v53
	v_mul_f32_e32 v54, 0x43000000, v54
	v_mul_f32_e32 v55, 0x43000000, v55
	ds_write_b128 v120, v[52:55] offset:4096
	v_mul_f32_e32 v56, 0x43000000, v56
	v_mul_f32_e32 v57, 0x43000000, v57
	v_mul_f32_e32 v58, 0x43000000, v58
	v_mul_f32_e32 v59, 0x43000000, v59
	ds_write_b128 v120, v[56:59] offset:5120
	v_mul_f32_e32 v60, 0x43000000, v60
	v_mul_f32_e32 v61, 0x43000000, v61
	v_mul_f32_e32 v62, 0x43000000, v62
	v_mul_f32_e32 v63, 0x43000000, v63
	ds_write_b128 v120, v[60:63] offset:6144
	v_mul_f32_e32 v64, 0x43000000, v64
	v_mul_f32_e32 v65, 0x43000000, v65
	v_mul_f32_e32 v66, 0x43000000, v66
	v_mul_f32_e32 v67, 0x43000000, v67
	ds_write_b128 v120, v[64:67] offset:7168
	s_waitcnt lgkmcnt(0)
	s_barrier
; #define GAS __attribute__((address_space(1)))
; #define LAS __attribute__((address_space(3)))
; #define LDS_WAIT() asm volatile("s_waitcnt lgkmcnt(0)" ::: "memory")
;     const int pr = item >> 1, kb = 2 * (pr / nblk) + (item & 1), nb = pr % nblk, k0 = 64 * kb, n0 = 32 * nb;
;     const int nr = n0 + (lane & 31); const int sc = MAP == 1 ? src_col_in(nr) : nr;
;     float v[32];
; #pragma unroll
;     for (int i = 0; i < 32; ++i) v[i] = sc >= 0 ? W[(size_t)(k0 + 2 * i + (lane >> 5)) * Nsrc + sc] : 0.f;
; #pragma unroll
;     for (int i = 0; i < 32; ++i) { const int k = k0 + 2 * i + (lane >> 5); float x = v[i] * wscale; if (KS) x *= (k < ksplit ? ksA[k] : ksB[k - ksplit]); scr[(2 * i + (lane >> 5)) * 33 + (lane & 31)] = x; }
;     LDS_WAIT(); asm volatile("" ::: "memory");
;     const int c = lane & 7;
; #pragma unroll
;     for (int j = 0; j < 4; ++j) { const int n = (lane >> 3) + 8 * j; const LAS float* s = scr + (8 * c) * 33 + n;
;         const unsigned long long o = (unsigned long long)pg8::pk4_fp8(s[0 * 33], s[1 * 33], s[2 * 33], s[3 * 33]) | ((unsigned long long)pg8::pk4_fp8(s[4 * 33], s[5 * 33], s[6 * 33], s[7 * 33]) << 32);
;         *(GAS unsigned long long*)(WT + (size_t)(n0 + n) * K + k0 + 8 * c) = o; }
;     LDS_WAIT(); asm volatile("" ::: "memory");
; }
	s_add_i32 s17, s16, 192
	s_min_u32 s17, s17, 0x3ff
	s_lshr_b32 s18, s17, 5
	s_add_i32 s18, s18, 96
	s_and_b32 s19, s17, 31
	s_lshl_b32 s18, s18, 21
	s_lshl_b32 s19, s19, 9
	s_add_u32 s18, s18, s19
	s_add_u32 s12, s2, s18
	s_addc_u32 s13, s3, 0
	global_load_dwordx4 v[36:39], v126, s[12:13]
	s_add_u32 s12, s12, 0x8000
	s_addc_u32 s13, s13, 0
	global_load_dwordx4 v[40:43], v126, s[12:13]
	s_add_u32 s12, s12, 0x8000
	s_addc_u32 s13, s13, 0
	global_load_dwordx4 v[44:47], v126, s[12:13]
	s_add_u32 s12, s12, 0x8000
	s_addc_u32 s13, s13, 0
	global_load_dwordx4 v[48:51], v126, s[12:13]
	s_add_u32 s12, s12, 0x8000
	s_addc_u32 s13, s13, 0
	global_load_dwordx4 v[52:55], v126, s[12:13]
	s_add_u32 s12, s12, 0x8000
	s_addc_u32 s13, s13, 0
	global_load_dwordx4 v[56:59], v126, s[12:13]
	s_add_u32 s12, s12, 0x8000
	s_addc_u32 s13, s13, 0
	global_load_dwordx4 v[60:63], v126, s[12:13]
	s_add_u32 s12, s12, 0x8000
	s_addc_u32 s13, s13, 0
	global_load_dwordx4 v[64:67], v126, s[12:13]
	s_add_i32 s17, s16, 0
	s_min_u32 s17, s17, 0x3ff
	s_lshr_b32 s18, s17, 5
	s_add_i32 s18, s18, 96
	s_and_b32 s19, s17, 31
	s_lshl_b32 s19, s19, 21
	s_lshl_b32 s18, s18, 7
	s_add_u32 s18, s18, s19
	s_add_u32 s14, s4, s18
	s_addc_u32 s15, s5, 0
	ds_read_b32 v100, v122
	ds_read_b32 v101, v122 offset:512
	ds_read_b32 v102, v122 offset:1024
	ds_read_b32 v103, v122 offset:1536
	ds_read_b32 v104, v122 offset:2048
	ds_read_b32 v105, v122 offset:2560
	ds_read_b32 v106, v122 offset:3072
	ds_read_b32 v107, v122 offset:3584
	ds_read_b32 v108, v122 offset:4096
	ds_read_b32 v109, v122 offset:4608
	ds_read_b32 v110, v122 offset:5120
	ds_read_b32 v111, v122 offset:5632
	ds_read_b32 v112, v122 offset:6144
	ds_read_b32 v113, v122 offset:6656
	ds_read_b32 v114, v122 offset:7168
	ds_read_b32 v115, v122 offset:7680
	s_waitcnt lgkmcnt(0)
	v_max_f32_e32 v100, v100, v100
	v_max_f32_e32 v101, v101, v101
	v_max_f32_e32 v102, v102, v102
	v_max_f32_e32 v103, v103, v103
	v_max_f32_e32 v104, v104, v104
	v_max_f32_e32 v105, v105, v105
	v_max_f32_e32 v106, v106, v106
	v_max_f32_e32 v107, v107, v107
	v_max_f32_e32 v108, v108, v108
	v_max_f32_e32 v109, v109, v109
	v_max_f32_e32 v110, v110, v110
	v_max_f32_e32 v111, v111, v111
	v_max_f32_e32 v112, v112, v112
	v_max_f32_e32 v113, v113, v113
	v_max_f32_e32 v114, v114, v114
	v_max_f32_e32 v115, v115, v115
	v_med3_f32 v100, v100, s20, v129
	v_med3_f32 v101, v101, s20, v129
	v_med3_f32 v102, v102, s20, v129
	v_med3_f32 v103, v103, s20, v129
	v_med3_f32 v104, v104, s20, v129
	v_med3_f32 v105, v105, s20, v129
	v_med3_f32 v106, v106, s20, v129
	v_med3_f32 v107, v107, s20, v129
	v_med3_f32 v108, v108, s20, v129
	v_med3_f32 v109, v109, s20, v129
	v_med3_f32 v110, v110, s20, v129
	v_med3_f32 v111, v111, s20, v129
	v_med3_f32 v112, v112, s20, v129
	v_med3_f32 v113, v113, s20, v129
	v_med3_f32 v114, v114, s20, v129
	v_med3_f32 v115, v115, s20, v129
	v_mov_b32_e32 v116, 0
	v_mov_b32_e32 v117, 0
	v_mov_b32_e32 v118, 0
	v_mov_b32_e32 v119, 0
	v_cvt_pk_fp8_f32 v116, v100, v101
	v_cvt_pk_fp8_f32 v117, v104, v105
	v_cvt_pk_fp8_f32 v118, v108, v109
	v_cvt_pk_fp8_f32 v119, v112, v113
	v_cvt_pk_fp8_f32 v116, v102, v103 op_sel:[0,0,1]
	v_cvt_pk_fp8_f32 v117, v106, v107 op_sel:[0,0,1]
	v_cvt_pk_fp8_f32 v118, v110, v111 op_sel:[0,0,1]
	v_cvt_pk_fp8_f32 v119, v114, v115 op_sel:[0,0,1]
	s_nop 0
	global_store_dwordx4 v127, v[116:119], s[14:15]
	ds_read_b32 v100, v124
	ds_read_b32 v101, v124 offset:512
	ds_read_b32 v102, v124 offset:1024
	ds_read_b32 v103, v124 offset:1536
	ds_read_b32 v104, v124 offset:2048
	ds_read_b32 v105, v124 offset:2560
	ds_read_b32 v106, v124 offset:3072
	ds_read_b32 v107, v124 offset:3584
	ds_read_b32 v108, v124 offset:4096
	ds_read_b32 v109, v124 offset:4608
	ds_read_b32 v110, v124 offset:5120
	ds_read_b32 v111, v124 offset:5632
	ds_read_b32 v112, v124 offset:6144
	ds_read_b32 v113, v124 offset:6656
	ds_read_b32 v114, v124 offset:7168
	ds_read_b32 v115, v124 offset:7680
	s_waitcnt lgkmcnt(0)
	v_max_f32_e32 v100, v100, v100
	v_max_f32_e32 v101, v101, v101
	v_max_f32_e32 v102, v102, v102
	v_max_f32_e32 v103, v103, v103
	v_max_f32_e32 v104, v104, v104
	v_max_f32_e32 v105, v105, v105
	v_max_f32_e32 v106, v106, v106
	v_max_f32_e32 v107, v107, v107
	v_max_f32_e32 v108, v108, v108
	v_max_f32_e32 v109, v109, v109
	v_max_f32_e32 v110, v110, v110
	v_max_f32_e32 v111, v111, v111
	v_max_f32_e32 v112, v112, v112
	v_max_f32_e32 v113, v113, v113
	v_max_f32_e32 v114, v114, v114
	v_max_f32_e32 v115, v115, v115
	v_med3_f32 v100, v100, s20, v129
	v_med3_f32 v101, v101, s20, v129
	v_med3_f32 v102, v102, s20, v129
	v_med3_f32 v103, v103, s20, v129
	v_med3_f32 v104, v104, s20, v129
	v_med3_f32 v105, v105, s20, v129
	v_med3_f32 v106, v106, s20, v129
	v_med3_f32 v107, v107, s20, v129
	v_med3_f32 v108, v108, s20, v129
	v_med3_f32 v109, v109, s20, v129
	v_med3_f32 v110, v110, s20, v129
	v_med3_f32 v111, v111, s20, v129
	v_med3_f32 v112, v112, s20, v129
	v_med3_f32 v113, v113, s20, v129
	v_med3_f32 v114, v114, s20, v129
	v_med3_f32 v115, v115, s20, v129
	v_mov_b32_e32 v116, 0
	v_mov_b32_e32 v117, 0
	v_mov_b32_e32 v118, 0
	v_mov_b32_e32 v119, 0
	v_cvt_pk_fp8_f32 v116, v100, v101
	v_cvt_pk_fp8_f32 v117, v104, v105
	v_cvt_pk_fp8_f32 v118, v108, v109
	v_cvt_pk_fp8_f32 v119, v112, v113
	v_cvt_pk_fp8_f32 v116, v102, v103 op_sel:[0,0,1]
	v_cvt_pk_fp8_f32 v117, v106, v107 op_sel:[0,0,1]
	v_cvt_pk_fp8_f32 v118, v110, v111 op_sel:[0,0,1]
	v_cvt_pk_fp8_f32 v119, v114, v115 op_sel:[0,0,1]
	s_nop 0
	global_store_dwordx4 v128, v[116:119], s[14:15]
	s_waitcnt vmcnt(10)
	v_mul_f32_e32 v68, 0x43000000, v68
	v_mul_f32_e32 v69, 0x43000000, v69
	v_mul_f32_e32 v70, 0x43000000, v70
	v_mul_f32_e32 v71, 0x43000000, v71
	ds_write_b128 v121, v[68:71]
	v_mul_f32_e32 v72, 0x43000000, v72
	v_mul_f32_e32 v73, 0x43000000, v73
	v_mul_f32_e32 v74, 0x43000000, v74
	v_mul_f32_e32 v75, 0x43000000, v75
	ds_write_b128 v121, v[72:75] offset:1024
	v_mul_f32_e32 v76, 0x43000000, v76
	v_mul_f32_e32 v77, 0x43000000, v77
	v_mul_f32_e32 v78, 0x43000000, v78
	v_mul_f32_e32 v79, 0x43000000, v79
	ds_write_b128 v121, v[76:79] offset:2048
	v_mul_f32_e32 v80, 0x43000000, v80
	v_mul_f32_e32 v81, 0x43000000, v81
	v_mul_f32_e32 v82, 0x43000000, v82
	v_mul_f32_e32 v83, 0x43000000, v83
	ds_write_b128 v121, v[80:83] offset:3072
	v_mul_f32_e32 v84, 0x43000000, v84
	v_mul_f32_e32 v85, 0x43000000, v85
	v_mul_f32_e32 v86, 0x43000000, v86
	v_mul_f32_e32 v87, 0x43000000, v87
	ds_write_b128 v121, v[84:87] offset:4096
	v_mul_f32_e32 v88, 0x43000000, v88
	v_mul_f32_e32 v89, 0x43000000, v89
	v_mul_f32_e32 v90, 0x43000000, v90
	v_mul_f32_e32 v91, 0x43000000, v91
	ds_write_b128 v121, v[88:91] offset:5120
	v_mul_f32_e32 v92, 0x43000000, v92
	v_mul_f32_e32 v93, 0x43000000, v93
	v_mul_f32_e32 v94, 0x43000000, v94
	v_mul_f32_e32 v95, 0x43000000, v95
	ds_write_b128 v121, v[92:95] offset:6144
	v_mul_f32_e32 v96, 0x43000000, v96
	v_mul_f32_e32 v97, 0x43000000, v97
	v_mul_f32_e32 v98, 0x43000000, v98
	v_mul_f32_e32 v99, 0x43000000, v99
	ds_write_b128 v121, v[96:99] offset:7168
	s_waitcnt lgkmcnt(0)
	s_barrier
; #define GAS __attribute__((address_space(1)))
; #define LAS __attribute__((address_space(3)))
; #define LDS_WAIT() asm volatile("s_waitcnt lgkmcnt(0)" ::: "memory")
;     const int pr = item >> 1, kb = 2 * (pr / nblk) + (item & 1), nb = pr % nblk, k0 = 64 * kb, n0 = 32 * nb;
;     const int nr = n0 + (lane & 31); const int sc = MAP == 1 ? src_col_in(nr) : nr;
;     float v[32];
; #pragma unroll
;     for (int i = 0; i < 32; ++i) v[i] = sc >= 0 ? W[(size_t)(k0 + 2 * i + (lane >> 5)) * Nsrc + sc] : 0.f;
; #pragma unroll
;     for (int i = 0; i < 32; ++i) { const int k = k0 + 2 * i + (lane >> 5); float x = v[i] * wscale; if (KS) x *= (k < ksplit ? ksA[k] : ksB[k - ksplit]); scr[(2 * i + (lane >> 5)) * 33 + (lane & 31)] = x; }
;     LDS_WAIT(); asm volatile("" ::: "memory");
;     const int c = lane & 7;
; #pragma unroll
;     for (int j = 0; j < 4; ++j) { const int n = (lane >> 3) + 8 * j; const LAS float* s = scr + (8 * c) * 33 + n;
;         const unsigned long long o = (unsigned long long)pg8::pk4_fp8(s[0 * 33], s[1 * 33], s[2 * 33], s[3 * 33]) | ((unsigned long long)pg8::pk4_fp8(s[4 * 33], s[5 * 33], s[6 * 33], s[7 * 33]) << 32);
;         *(GAS unsigned long long*)(WT + (size_t)(n0 + n) * K + k0 + 8 * c) = o; }
;     LDS_WAIT(); asm volatile("" ::: "memory");
; }
	s_add_i32 s17, s16, 288
	s_min_u32 s17, s17, 0x3ff
	s_lshr_b32 s18, s17, 5
	s_add_i32 s18, s18, 96
	s_and_b32 s19, s17, 31
	s_lshl_b32 s18, s18, 21
	s_lshl_b32 s19, s19, 9
	s_add_u32 s18, s18, s19
	s_add_u32 s12, s2, s18
	s_addc_u32 s13, s3, 0
	global_load_dwordx4 v[68:71], v126, s[12:13]
	s_add_u32 s12, s12, 0x8000
	s_addc_u32 s13, s13, 0
	global_load_dwordx4 v[72:75], v126, s[12:13]
	s_add_u32 s12, s12, 0x8000
	s_addc_u32 s13, s13, 0
	global_load_dwordx4 v[76:79], v126, s[12:13]
	s_add_u32 s12, s12, 0x8000
	s_addc_u32 s13, s13, 0
	global_load_dwordx4 v[80:83], v126, s[12:13]
	s_add_u32 s12, s12, 0x8000
	s_addc_u32 s13, s13, 0
	global_load_dwordx4 v[84:87], v126, s[12:13]
	s_add_u32 s12, s12, 0x8000
	s_addc_u32 s13, s13, 0
	global_load_dwordx4 v[88:91], v126, s[12:13]
	s_add_u32 s12, s12, 0x8000
	s_addc_u32 s13, s13, 0
	global_load_dwordx4 v[92:95], v126, s[12:13]
	s_add_u32 s12, s12, 0x8000
	s_addc_u32 s13, s13, 0
	global_load_dwordx4 v[96:99], v126, s[12:13]
	s_add_i32 s17, s16, 96
	s_min_u32 s17, s17, 0x3ff
	s_lshr_b32 s18, s17, 5
	s_add_i32 s18, s18, 96
	s_and_b32 s19, s17, 31
	s_lshl_b32 s19, s19, 21
	s_lshl_b32 s18, s18, 7
	s_add_u32 s18, s18, s19
	s_add_u32 s14, s4, s18
	s_addc_u32 s15, s5, 0
	ds_read_b32 v100, v123
	ds_read_b32 v101, v123 offset:512
	ds_read_b32 v102, v123 offset:1024
	ds_read_b32 v103, v123 offset:1536
	ds_read_b32 v104, v123 offset:2048
	ds_read_b32 v105, v123 offset:2560
	ds_read_b32 v106, v123 offset:3072
	ds_read_b32 v107, v123 offset:3584
	ds_read_b32 v108, v123 offset:4096
	ds_read_b32 v109, v123 offset:4608
	ds_read_b32 v110, v123 offset:5120
	ds_read_b32 v111, v123 offset:5632
	ds_read_b32 v112, v123 offset:6144
	ds_read_b32 v113, v123 offset:6656
	ds_read_b32 v114, v123 offset:7168
	ds_read_b32 v115, v123 offset:7680
	s_waitcnt lgkmcnt(0)
	v_max_f32_e32 v100, v100, v100
	v_max_f32_e32 v101, v101, v101
	v_max_f32_e32 v102, v102, v102
	v_max_f32_e32 v103, v103, v103
	v_max_f32_e32 v104, v104, v104
	v_max_f32_e32 v105, v105, v105
	v_max_f32_e32 v106, v106, v106
	v_max_f32_e32 v107, v107, v107
	v_max_f32_e32 v108, v108, v108
	v_max_f32_e32 v109, v109, v109
	v_max_f32_e32 v110, v110, v110
	v_max_f32_e32 v111, v111, v111
	v_max_f32_e32 v112, v112, v112
	v_max_f32_e32 v113, v113, v113
	v_max_f32_e32 v114, v114, v114
	v_max_f32_e32 v115, v115, v115
	v_med3_f32 v100, v100, s20, v129
	v_med3_f32 v101, v101, s20, v129
	v_med3_f32 v102, v102, s20, v129
	v_med3_f32 v103, v103, s20, v129
	v_med3_f32 v104, v104, s20, v129
	v_med3_f32 v105, v105, s20, v129
	v_med3_f32 v106, v106, s20, v129
	v_med3_f32 v107, v107, s20, v129
	v_med3_f32 v108, v108, s20, v129
	v_med3_f32 v109, v109, s20, v129
	v_med3_f32 v110, v110, s20, v129
	v_med3_f32 v111, v111, s20, v129
	v_med3_f32 v112, v112, s20, v129
	v_med3_f32 v113, v113, s20, v129
	v_med3_f32 v114, v114, s20, v129
	v_med3_f32 v115, v115, s20, v129
	v_mov_b32_e32 v116, 0
	v_mov_b32_e32 v117, 0
	v_mov_b32_e32 v118, 0
	v_mov_b32_e32 v119, 0
	v_cvt_pk_fp8_f32 v116, v100, v101
	v_cvt_pk_fp8_f32 v117, v104, v105
	v_cvt_pk_fp8_f32 v118, v108, v109
	v_cvt_pk_fp8_f32 v119, v112, v113
	v_cvt_pk_fp8_f32 v116, v102, v103 op_sel:[0,0,1]
	v_cvt_pk_fp8_f32 v117, v106, v107 op_sel:[0,0,1]
	v_cvt_pk_fp8_f32 v118, v110, v111 op_sel:[0,0,1]
	v_cvt_pk_fp8_f32 v119, v114, v115 op_sel:[0,0,1]
	s_nop 0
	global_store_dwordx4 v127, v[116:119], s[14:15]
	ds_read_b32 v100, v125
	ds_read_b32 v101, v125 offset:512
	ds_read_b32 v102, v125 offset:1024
	ds_read_b32 v103, v125 offset:1536
	ds_read_b32 v104, v125 offset:2048
	ds_read_b32 v105, v125 offset:2560
	ds_read_b32 v106, v125 offset:3072
	ds_read_b32 v107, v125 offset:3584
	ds_read_b32 v108, v125 offset:4096
	ds_read_b32 v109, v125 offset:4608
	ds_read_b32 v110, v125 offset:5120
	ds_read_b32 v111, v125 offset:5632
	ds_read_b32 v112, v125 offset:6144
	ds_read_b32 v113, v125 offset:6656
	ds_read_b32 v114, v125 offset:7168
	ds_read_b32 v115, v125 offset:7680
	s_waitcnt lgkmcnt(0)
	v_max_f32_e32 v100, v100, v100
	v_max_f32_e32 v101, v101, v101
	v_max_f32_e32 v102, v102, v102
	v_max_f32_e32 v103, v103, v103
	v_max_f32_e32 v104, v104, v104
	v_max_f32_e32 v105, v105, v105
	v_max_f32_e32 v106, v106, v106
	v_max_f32_e32 v107, v107, v107
	v_max_f32_e32 v108, v108, v108
	v_max_f32_e32 v109, v109, v109
	v_max_f32_e32 v110, v110, v110
	v_max_f32_e32 v111, v111, v111
	v_max_f32_e32 v112, v112, v112
	v_max_f32_e32 v113, v113, v113
	v_max_f32_e32 v114, v114, v114
	v_max_f32_e32 v115, v115, v115
	v_med3_f32 v100, v100, s20, v129
	v_med3_f32 v101, v101, s20, v129
	v_med3_f32 v102, v102, s20, v129
	v_med3_f32 v103, v103, s20, v129
	v_med3_f32 v104, v104, s20, v129
	v_med3_f32 v105, v105, s20, v129
	v_med3_f32 v106, v106, s20, v129
	v_med3_f32 v107, v107, s20, v129
	v_med3_f32 v108, v108, s20, v129
	v_med3_f32 v109, v109, s20, v129
	v_med3_f32 v110, v110, s20, v129
	v_med3_f32 v111, v111, s20, v129
	v_med3_f32 v112, v112, s20, v129
	v_med3_f32 v113, v113, s20, v129
	v_med3_f32 v114, v114, s20, v129
	v_med3_f32 v115, v115, s20, v129
	v_mov_b32_e32 v116, 0
	v_mov_b32_e32 v117, 0
	v_mov_b32_e32 v118, 0
	v_mov_b32_e32 v119, 0
	v_cvt_pk_fp8_f32 v116, v100, v101
	v_cvt_pk_fp8_f32 v117, v104, v105
	v_cvt_pk_fp8_f32 v118, v108, v109
	v_cvt_pk_fp8_f32 v119, v112, v113
	v_cvt_pk_fp8_f32 v116, v102, v103 op_sel:[0,0,1]
	v_cvt_pk_fp8_f32 v117, v106, v107 op_sel:[0,0,1]
	v_cvt_pk_fp8_f32 v118, v110, v111 op_sel:[0,0,1]
	v_cvt_pk_fp8_f32 v119, v114, v115 op_sel:[0,0,1]
	s_nop 0
	global_store_dwordx4 v128, v[116:119], s[14:15]
	s_waitcnt vmcnt(12)
	v_mul_f32_e32 v36, 0x43000000, v36
	v_mul_f32_e32 v37, 0x43000000, v37
	v_mul_f32_e32 v38, 0x43000000, v38
	v_mul_f32_e32 v39, 0x43000000, v39
	ds_write_b128 v120, v[36:39]
	v_mul_f32_e32 v40, 0x43000000, v40
	v_mul_f32_e32 v41, 0x43000000, v41
	v_mul_f32_e32 v42, 0x43000000, v42
	v_mul_f32_e32 v43, 0x43000000, v43
	ds_write_b128 v120, v[40:43] offset:1024
	v_mul_f32_e32 v44, 0x43000000, v44
	v_mul_f32_e32 v45, 0x43000000, v45
	v_mul_f32_e32 v46, 0x43000000, v46
	v_mul_f32_e32 v47, 0x43000000, v47
	ds_write_b128 v120, v[44:47] offset:2048
	v_mul_f32_e32 v48, 0x43000000, v48
	v_mul_f32_e32 v49, 0x43000000, v49
	v_mul_f32_e32 v50, 0x43000000, v50
	v_mul_f32_e32 v51, 0x43000000, v51
	ds_write_b128 v120, v[48:51] offset:3072
	v_mul_f32_e32 v52, 0x43000000, v52
	v_mul_f32_e32 v53, 0x43000000, v53
	v_mul_f32_e32 v54, 0x43000000, v54
	v_mul_f32_e32 v55, 0x43000000, v55
	ds_write_b128 v120, v[52:55] offset:4096
	v_mul_f32_e32 v56, 0x43000000, v56
	v_mul_f32_e32 v57, 0x43000000, v57
	v_mul_f32_e32 v58, 0x43000000, v58
	v_mul_f32_e32 v59, 0x43000000, v59
	ds_write_b128 v120, v[56:59] offset:5120
	v_mul_f32_e32 v60, 0x43000000, v60
	v_mul_f32_e32 v61, 0x43000000, v61
	v_mul_f32_e32 v62, 0x43000000, v62
	v_mul_f32_e32 v63, 0x43000000, v63
	ds_write_b128 v120, v[60:63] offset:6144
	v_mul_f32_e32 v64, 0x43000000, v64
	v_mul_f32_e32 v65, 0x43000000, v65
	v_mul_f32_e32 v66, 0x43000000, v66
	v_mul_f32_e32 v67, 0x43000000, v67
	ds_write_b128 v120, v[64:67] offset:7168
	s_waitcnt lgkmcnt(0)
	s_barrier
; #define GAS __attribute__((address_space(1)))
; #define LAS __attribute__((address_space(3)))
; #define LDS_WAIT() asm volatile("s_waitcnt lgkmcnt(0)" ::: "memory")
;     const int pr = item >> 1, kb = 2 * (pr / nblk) + (item & 1), nb = pr % nblk, k0 = 64 * kb, n0 = 32 * nb;
;     const int nr = n0 + (lane & 31); const int sc = MAP == 1 ? src_col_in(nr) : nr;
;     float v[32];
; #pragma unroll
;     for (int i = 0; i < 32; ++i) v[i] = sc >= 0 ? W[(size_t)(k0 + 2 * i + (lane >> 5)) * Nsrc + sc] : 0.f;
; #pragma unroll
;     for (int i = 0; i < 32; ++i) { const int k = k0 + 2 * i + (lane >> 5); float x = v[i] * wscale; if (KS) x *= (k < ksplit ? ksA[k] : ksB[k - ksplit]); scr[(2 * i + (lane >> 5)) * 33 + (lane & 31)] = x; }
;     LDS_WAIT(); asm volatile("" ::: "memory");
;     const int c = lane & 7;
; #pragma unroll
;     for (int j = 0; j < 4; ++j) { const int n = (lane >> 3) + 8 * j; const LAS float* s = scr + (8 * c) * 33 + n;
;         const unsigned long long o = (unsigned long long)pg8::pk4_fp8(s[0 * 33], s[1 * 33], s[2 * 33], s[3 * 33]) | ((unsigned long long)pg8::pk4_fp8(s[4 * 33], s[5 * 33], s[6 * 33], s[7 * 33]) << 32);
;         *(GAS unsigned long long*)(WT + (size_t)(n0 + n) * K + k0 + 8 * c) = o; }
;     LDS_WAIT(); asm volatile("" ::: "memory");
; }
	s_add_i32 s17, s16, 384
	s_min_u32 s17, s17, 0x3ff
	s_lshr_b32 s18, s17, 5
	s_add_i32 s18, s18, 96
	s_and_b32 s19, s17, 31
	s_lshl_b32 s18, s18, 21
	s_lshl_b32 s19, s19, 9
	s_add_u32 s18, s18, s19
	s_add_u32 s12, s2, s18
	s_addc_u32 s13, s3, 0
	global_load_dwordx4 v[36:39], v126, s[12:13]
	s_add_u32 s12, s12, 0x8000
	s_addc_u32 s13, s13, 0
	global_load_dwordx4 v[40:43], v126, s[12:13]
	s_add_u32 s12, s12, 0x8000
	s_addc_u32 s13, s13, 0
	global_load_dwordx4 v[44:47], v126, s[12:13]
	s_add_u32 s12, s12, 0x8000
	s_addc_u32 s13, s13, 0
	global_load_dwordx4 v[48:51], v126, s[12:13]
	s_add_u32 s12, s12, 0x8000
	s_addc_u32 s13, s13, 0
	global_load_dwordx4 v[52:55], v126, s[12:13]
	s_add_u32 s12, s12, 0x8000
	s_addc_u32 s13, s13, 0
	global_load_dwordx4 v[56:59], v126, s[12:13]
	s_add_u32 s12, s12, 0x8000
	s_addc_u32 s13, s13, 0
	global_load_dwordx4 v[60:63], v126, s[12:13]
	s_add_u32 s12, s12, 0x8000
	s_addc_u32 s13, s13, 0
	global_load_dwordx4 v[64:67], v126, s[12:13]
	s_add_i32 s17, s16, 192
	s_min_u32 s17, s17, 0x3ff
	s_lshr_b32 s18, s17, 5
	s_add_i32 s18, s18, 96
	s_and_b32 s19, s17, 31
	s_lshl_b32 s19, s19, 21
	s_lshl_b32 s18, s18, 7
	s_add_u32 s18, s18, s19
	s_add_u32 s14, s4, s18
	s_addc_u32 s15, s5, 0
	ds_read_b32 v100, v122
	ds_read_b32 v101, v122 offset:512
	ds_read_b32 v102, v122 offset:1024
	ds_read_b32 v103, v122 offset:1536
	ds_read_b32 v104, v122 offset:2048
	ds_read_b32 v105, v122 offset:2560
	ds_read_b32 v106, v122 offset:3072
	ds_read_b32 v107, v122 offset:3584
	ds_read_b32 v108, v122 offset:4096
	ds_read_b32 v109, v122 offset:4608
	ds_read_b32 v110, v122 offset:5120
	ds_read_b32 v111, v122 offset:5632
	ds_read_b32 v112, v122 offset:6144
	ds_read_b32 v113, v122 offset:6656
	ds_read_b32 v114, v122 offset:7168
	ds_read_b32 v115, v122 offset:7680
	s_waitcnt lgkmcnt(0)
	v_max_f32_e32 v100, v100, v100
	v_max_f32_e32 v101, v101, v101
	v_max_f32_e32 v102, v102, v102
	v_max_f32_e32 v103, v103, v103
	v_max_f32_e32 v104, v104, v104
	v_max_f32_e32 v105, v105, v105
	v_max_f32_e32 v106, v106, v106
	v_max_f32_e32 v107, v107, v107
	v_max_f32_e32 v108, v108, v108
	v_max_f32_e32 v109, v109, v109
	v_max_f32_e32 v110, v110, v110
	v_max_f32_e32 v111, v111, v111
	v_max_f32_e32 v112, v112, v112
	v_max_f32_e32 v113, v113, v113
	v_max_f32_e32 v114, v114, v114
	v_max_f32_e32 v115, v115, v115
	v_med3_f32 v100, v100, s20, v129
	v_med3_f32 v101, v101, s20, v129
	v_med3_f32 v102, v102, s20, v129
	v_med3_f32 v103, v103, s20, v129
	v_med3_f32 v104, v104, s20, v129
	v_med3_f32 v105, v105, s20, v129
	v_med3_f32 v106, v106, s20, v129
	v_med3_f32 v107, v107, s20, v129
	v_med3_f32 v108, v108, s20, v129
	v_med3_f32 v109, v109, s20, v129
	v_med3_f32 v110, v110, s20, v129
	v_med3_f32 v111, v111, s20, v129
	v_med3_f32 v112, v112, s20, v129
	v_med3_f32 v113, v113, s20, v129
	v_med3_f32 v114, v114, s20, v129
	v_med3_f32 v115, v115, s20, v129
	v_mov_b32_e32 v116, 0
	v_mov_b32_e32 v117, 0
	v_mov_b32_e32 v118, 0
	v_mov_b32_e32 v119, 0
	v_cvt_pk_fp8_f32 v116, v100, v101
	v_cvt_pk_fp8_f32 v117, v104, v105
	v_cvt_pk_fp8_f32 v118, v108, v109
	v_cvt_pk_fp8_f32 v119, v112, v113
	v_cvt_pk_fp8_f32 v116, v102, v103 op_sel:[0,0,1]
	v_cvt_pk_fp8_f32 v117, v106, v107 op_sel:[0,0,1]
	v_cvt_pk_fp8_f32 v118, v110, v111 op_sel:[0,0,1]
	v_cvt_pk_fp8_f32 v119, v114, v115 op_sel:[0,0,1]
	s_nop 0
	global_store_dwordx4 v127, v[116:119], s[14:15]
	ds_read_b32 v100, v124
	ds_read_b32 v101, v124 offset:512
	ds_read_b32 v102, v124 offset:1024
	ds_read_b32 v103, v124 offset:1536
	ds_read_b32 v104, v124 offset:2048
	ds_read_b32 v105, v124 offset:2560
	ds_read_b32 v106, v124 offset:3072
	ds_read_b32 v107, v124 offset:3584
	ds_read_b32 v108, v124 offset:4096
	ds_read_b32 v109, v124 offset:4608
	ds_read_b32 v110, v124 offset:5120
	ds_read_b32 v111, v124 offset:5632
	ds_read_b32 v112, v124 offset:6144
	ds_read_b32 v113, v124 offset:6656
	ds_read_b32 v114, v124 offset:7168
	ds_read_b32 v115, v124 offset:7680
	s_waitcnt lgkmcnt(0)
	v_max_f32_e32 v100, v100, v100
	v_max_f32_e32 v101, v101, v101
	v_max_f32_e32 v102, v102, v102
	v_max_f32_e32 v103, v103, v103
	v_max_f32_e32 v104, v104, v104
	v_max_f32_e32 v105, v105, v105
	v_max_f32_e32 v106, v106, v106
	v_max_f32_e32 v107, v107, v107
	v_max_f32_e32 v108, v108, v108
	v_max_f32_e32 v109, v109, v109
	v_max_f32_e32 v110, v110, v110
	v_max_f32_e32 v111, v111, v111
	v_max_f32_e32 v112, v112, v112
	v_max_f32_e32 v113, v113, v113
	v_max_f32_e32 v114, v114, v114
	v_max_f32_e32 v115, v115, v115
	v_med3_f32 v100, v100, s20, v129
	v_med3_f32 v101, v101, s20, v129
	v_med3_f32 v102, v102, s20, v129
	v_med3_f32 v103, v103, s20, v129
	v_med3_f32 v104, v104, s20, v129
	v_med3_f32 v105, v105, s20, v129
	v_med3_f32 v106, v106, s20, v129
	v_med3_f32 v107, v107, s20, v129
	v_med3_f32 v108, v108, s20, v129
	v_med3_f32 v109, v109, s20, v129
	v_med3_f32 v110, v110, s20, v129
	v_med3_f32 v111, v111, s20, v129
	v_med3_f32 v112, v112, s20, v129
	v_med3_f32 v113, v113, s20, v129
	v_med3_f32 v114, v114, s20, v129
	v_med3_f32 v115, v115, s20, v129
	v_mov_b32_e32 v116, 0
	v_mov_b32_e32 v117, 0
	v_mov_b32_e32 v118, 0
	v_mov_b32_e32 v119, 0
	v_cvt_pk_fp8_f32 v116, v100, v101
	v_cvt_pk_fp8_f32 v117, v104, v105
	v_cvt_pk_fp8_f32 v118, v108, v109
	v_cvt_pk_fp8_f32 v119, v112, v113
	v_cvt_pk_fp8_f32 v116, v102, v103 op_sel:[0,0,1]
	v_cvt_pk_fp8_f32 v117, v106, v107 op_sel:[0,0,1]
	v_cvt_pk_fp8_f32 v118, v110, v111 op_sel:[0,0,1]
	v_cvt_pk_fp8_f32 v119, v114, v115 op_sel:[0,0,1]
	s_nop 0
	global_store_dwordx4 v128, v[116:119], s[14:15]
	s_waitcnt vmcnt(12)
	v_mul_f32_e32 v68, 0x43000000, v68
	v_mul_f32_e32 v69, 0x43000000, v69
	v_mul_f32_e32 v70, 0x43000000, v70
	v_mul_f32_e32 v71, 0x43000000, v71
	ds_write_b128 v121, v[68:71]
	v_mul_f32_e32 v72, 0x43000000, v72
	v_mul_f32_e32 v73, 0x43000000, v73
	v_mul_f32_e32 v74, 0x43000000, v74
	v_mul_f32_e32 v75, 0x43000000, v75
	ds_write_b128 v121, v[72:75] offset:1024
	v_mul_f32_e32 v76, 0x43000000, v76
	v_mul_f32_e32 v77, 0x43000000, v77
	v_mul_f32_e32 v78, 0x43000000, v78
	v_mul_f32_e32 v79, 0x43000000, v79
	ds_write_b128 v121, v[76:79] offset:2048
	v_mul_f32_e32 v80, 0x43000000, v80
	v_mul_f32_e32 v81, 0x43000000, v81
	v_mul_f32_e32 v82, 0x43000000, v82
	v_mul_f32_e32 v83, 0x43000000, v83
	ds_write_b128 v121, v[80:83] offset:3072
	v_mul_f32_e32 v84, 0x43000000, v84
	v_mul_f32_e32 v85, 0x43000000, v85
	v_mul_f32_e32 v86, 0x43000000, v86
	v_mul_f32_e32 v87, 0x43000000, v87
	ds_write_b128 v121, v[84:87] offset:4096
	v_mul_f32_e32 v88, 0x43000000, v88
	v_mul_f32_e32 v89, 0x43000000, v89
	v_mul_f32_e32 v90, 0x43000000, v90
	v_mul_f32_e32 v91, 0x43000000, v91
	ds_write_b128 v121, v[88:91] offset:5120
	v_mul_f32_e32 v92, 0x43000000, v92
	v_mul_f32_e32 v93, 0x43000000, v93
	v_mul_f32_e32 v94, 0x43000000, v94
	v_mul_f32_e32 v95, 0x43000000, v95
	ds_write_b128 v121, v[92:95] offset:6144
	v_mul_f32_e32 v96, 0x43000000, v96
	v_mul_f32_e32 v97, 0x43000000, v97
	v_mul_f32_e32 v98, 0x43000000, v98
	v_mul_f32_e32 v99, 0x43000000, v99
	ds_write_b128 v121, v[96:99] offset:7168
	s_waitcnt lgkmcnt(0)
	s_barrier
; #define GAS __attribute__((address_space(1)))
; #define LAS __attribute__((address_space(3)))
; #define LDS_WAIT() asm volatile("s_waitcnt lgkmcnt(0)" ::: "memory")
; __device__ __forceinline__ unsigned pk4_fp8(float a, float b, float c, float d) {
;     a = fminf(fmaxf(a, -448.f), 448.f); b = fminf(fmaxf(b, -448.f), 448.f); c = fminf(fmaxf(c, -448.f), 448.f); d = fminf(fmaxf(d, -448.f), 448.f);
;     int w = __builtin_amdgcn_cvt_pk_fp8_f32(a, b, 0, false); w = __builtin_amdgcn_cvt_pk_fp8_f32(c, d, w, true); return (unsigned)w; }
;     const int pr = item >> 1, kb = 2 * (pr / nblk) + (item & 1), nb = pr % nblk, k0 = 64 * kb, n0 = 32 * nb;
;     const int nr = n0 + (lane & 31); const int sc = MAP == 1 ? src_col_in(nr) : nr;
;     float v[32];
; #pragma unroll
;     for (int i = 0; i < 32; ++i) v[i] = sc >= 0 ? W[(size_t)(k0 + 2 * i + (lane >> 5)) * Nsrc + sc] : 0.f;
; #pragma unroll
;     for (int i = 0; i < 32; ++i) { const int k = k0 + 2 * i + (lane >> 5); float x = v[i] * wscale; if (KS) x *= (k < ksplit ? ksA[k] : ksB[k - ksplit]); scr[(2 * i + (lane >> 5)) * 33 + (lane & 31)] = x; }
;     LDS_WAIT(); asm volatile("" ::: "memory");
;     const int c = lane & 7;
; #pragma unroll
;     for (int j = 0; j < 4; ++j) { const int n = (lane >> 3) + 8 * j; const LAS float* s = scr + (8 * c) * 33 + n;
;         const unsigned long long o = (unsigned long long)pg8::pk4_fp8(s[0 * 33], s[1 * 33], s[2 * 33], s[3 * 33]) | ((unsigned long long)pg8::pk4_fp8(s[4 * 33], s[5 * 33], s[6 * 33], s[7 * 33]) << 32);
;         *(GAS unsigned long long*)(WT + (size_t)(n0 + n) * K + k0 + 8 * c) = o; }
;     LDS_WAIT(); asm volatile("" ::: "memory");
; }
	s_add_i32 s17, s16, 480
	s_min_u32 s17, s17, 0x3ff
	s_lshr_b32 s18, s17, 5
	s_add_i32 s18, s18, 96
	s_and_b32 s19, s17, 31
	s_lshl_b32 s18, s18, 21
	s_lshl_b32 s19, s19, 9
	s_add_u32 s18, s18, s19
	s_add_u32 s12, s2, s18
	s_addc_u32 s13, s3, 0
	global_load_dwordx4 v[68:71], v126, s[12:13]
	s_add_u32 s12, s12, 0x8000
	s_addc_u32 s13, s13, 0
	global_load_dwordx4 v[72:75], v126, s[12:13]
	s_add_u32 s12, s12, 0x8000
	s_addc_u32 s13, s13, 0
	global_load_dwordx4 v[76:79], v126, s[12:13]
	s_add_u32 s12, s12, 0x8000
	s_addc_u32 s13, s13, 0
	global_load_dwordx4 v[80:83], v126, s[12:13]
	s_add_u32 s12, s12, 0x8000
	s_addc_u32 s13, s13, 0
	global_load_dwordx4 v[84:87], v126, s[12:13]
	s_add_u32 s12, s12, 0x8000
	s_addc_u32 s13, s13, 0
	global_load_dwordx4 v[88:91], v126, s[12:13]
	s_add_u32 s12, s12, 0x8000
	s_addc_u32 s13, s13, 0
	global_load_dwordx4 v[92:95], v126, s[12:13]
	s_add_u32 s12, s12, 0x8000
	s_addc_u32 s13, s13, 0
	global_load_dwordx4 v[96:99], v126, s[12:13]
	s_add_i32 s17, s16, 288
	s_min_u32 s17, s17, 0x3ff
	s_lshr_b32 s18, s17, 5
	s_add_i32 s18, s18, 96
	s_and_b32 s19, s17, 31
	s_lshl_b32 s19, s19, 21
	s_lshl_b32 s18, s18, 7
	s_add_u32 s18, s18, s19
	s_add_u32 s14, s4, s18
	s_addc_u32 s15, s5, 0
	ds_read_b32 v100, v123
	ds_read_b32 v101, v123 offset:512
	ds_read_b32 v102, v123 offset:1024
	ds_read_b32 v103, v123 offset:1536
	ds_read_b32 v104, v123 offset:2048
	ds_read_b32 v105, v123 offset:2560
	ds_read_b32 v106, v123 offset:3072
	ds_read_b32 v107, v123 offset:3584
	ds_read_b32 v108, v123 offset:4096
	ds_read_b32 v109, v123 offset:4608
	ds_read_b32 v110, v123 offset:5120
	ds_read_b32 v111, v123 offset:5632
	ds_read_b32 v112, v123 offset:6144
	ds_read_b32 v113, v123 offset:6656
	ds_read_b32 v114, v123 offset:7168
	ds_read_b32 v115, v123 offset:7680
	s_waitcnt lgkmcnt(0)
	v_max_f32_e32 v100, v100, v100
	v_max_f32_e32 v101, v101, v101
	v_max_f32_e32 v102, v102, v102
	v_max_f32_e32 v103, v103, v103
	v_max_f32_e32 v104, v104, v104
	v_max_f32_e32 v105, v105, v105
	v_max_f32_e32 v106, v106, v106
	v_max_f32_e32 v107, v107, v107
	v_max_f32_e32 v108, v108, v108
	v_max_f32_e32 v109, v109, v109
	v_max_f32_e32 v110, v110, v110
	v_max_f32_e32 v111, v111, v111
	v_max_f32_e32 v112, v112, v112
	v_max_f32_e32 v113, v113, v113
	v_max_f32_e32 v114, v114, v114
	v_max_f32_e32 v115, v115, v115
	v_med3_f32 v100, v100, s20, v129
	v_med3_f32 v101, v101, s20, v129
	v_med3_f32 v102, v102, s20, v129
	v_med3_f32 v103, v103, s20, v129
	v_med3_f32 v104, v104, s20, v129
	v_med3_f32 v105, v105, s20, v129
	v_med3_f32 v106, v106, s20, v129
	v_med3_f32 v107, v107, s20, v129
	v_med3_f32 v108, v108, s20, v129
	v_med3_f32 v109, v109, s20, v129
	v_med3_f32 v110, v110, s20, v129
	v_med3_f32 v111, v111, s20, v129
	v_med3_f32 v112, v112, s20, v129
	v_med3_f32 v113, v113, s20, v129
	v_med3_f32 v114, v114, s20, v129
	v_med3_f32 v115, v115, s20, v129
	v_mov_b32_e32 v116, 0
	v_mov_b32_e32 v117, 0
	v_mov_b32_e32 v118, 0
	v_mov_b32_e32 v119, 0
	v_cvt_pk_fp8_f32 v116, v100, v101
	v_cvt_pk_fp8_f32 v117, v104, v105
	v_cvt_pk_fp8_f32 v118, v108, v109
	v_cvt_pk_fp8_f32 v119, v112, v113
	v_cvt_pk_fp8_f32 v116, v102, v103 op_sel:[0,0,1]
	v_cvt_pk_fp8_f32 v117, v106, v107 op_sel:[0,0,1]
	v_cvt_pk_fp8_f32 v118, v110, v111 op_sel:[0,0,1]
	v_cvt_pk_fp8_f32 v119, v114, v115 op_sel:[0,0,1]
	s_nop 0
	global_store_dwordx4 v127, v[116:119], s[14:15]
	ds_read_b32 v100, v125
	ds_read_b32 v101, v125 offset:512
	ds_read_b32 v102, v125 offset:1024
	ds_read_b32 v103, v125 offset:1536
	ds_read_b32 v104, v125 offset:2048
	ds_read_b32 v105, v125 offset:2560
	ds_read_b32 v106, v125 offset:3072
	ds_read_b32 v107, v125 offset:3584
	ds_read_b32 v108, v125 offset:4096
	ds_read_b32 v109, v125 offset:4608
	ds_read_b32 v110, v125 offset:5120
	ds_read_b32 v111, v125 offset:5632
	ds_read_b32 v112, v125 offset:6144
	ds_read_b32 v113, v125 offset:6656
	ds_read_b32 v114, v125 offset:7168
	ds_read_b32 v115, v125 offset:7680
	s_waitcnt lgkmcnt(0)
	v_max_f32_e32 v100, v100, v100
	v_max_f32_e32 v101, v101, v101
	v_max_f32_e32 v102, v102, v102
	v_max_f32_e32 v103, v103, v103
	v_max_f32_e32 v104, v104, v104
	v_max_f32_e32 v105, v105, v105
	v_max_f32_e32 v106, v106, v106
	v_max_f32_e32 v107, v107, v107
	v_max_f32_e32 v108, v108, v108
	v_max_f32_e32 v109, v109, v109
	v_max_f32_e32 v110, v110, v110
	v_max_f32_e32 v111, v111, v111
	v_max_f32_e32 v112, v112, v112
	v_max_f32_e32 v113, v113, v113
	v_max_f32_e32 v114, v114, v114
	v_max_f32_e32 v115, v115, v115
	v_med3_f32 v100, v100, s20, v129
	v_med3_f32 v101, v101, s20, v129
	v_med3_f32 v102, v102, s20, v129
	v_med3_f32 v103, v103, s20, v129
	v_med3_f32 v104, v104, s20, v129
	v_med3_f32 v105, v105, s20, v129
	v_med3_f32 v106, v106, s20, v129
	v_med3_f32 v107, v107, s20, v129
	v_med3_f32 v108, v108, s20, v129
	v_med3_f32 v109, v109, s20, v129
	v_med3_f32 v110, v110, s20, v129
	v_med3_f32 v111, v111, s20, v129
	v_med3_f32 v112, v112, s20, v129
	v_med3_f32 v113, v113, s20, v129
	v_med3_f32 v114, v114, s20, v129
	v_med3_f32 v115, v115, s20, v129
	v_mov_b32_e32 v116, 0
	v_mov_b32_e32 v117, 0
	v_mov_b32_e32 v118, 0
	v_mov_b32_e32 v119, 0
	v_cvt_pk_fp8_f32 v116, v100, v101
	v_cvt_pk_fp8_f32 v117, v104, v105
	v_cvt_pk_fp8_f32 v118, v108, v109
	v_cvt_pk_fp8_f32 v119, v112, v113
	v_cvt_pk_fp8_f32 v116, v102, v103 op_sel:[0,0,1]
	v_cvt_pk_fp8_f32 v117, v106, v107 op_sel:[0,0,1]
	v_cvt_pk_fp8_f32 v118, v110, v111 op_sel:[0,0,1]
	v_cvt_pk_fp8_f32 v119, v114, v115 op_sel:[0,0,1]
	s_nop 0
	global_store_dwordx4 v128, v[116:119], s[14:15]
	s_waitcnt vmcnt(12)
	v_mul_f32_e32 v36, 0x43000000, v36
	v_mul_f32_e32 v37, 0x43000000, v37
	v_mul_f32_e32 v38, 0x43000000, v38
	v_mul_f32_e32 v39, 0x43000000, v39
	ds_write_b128 v120, v[36:39]
	v_mul_f32_e32 v40, 0x43000000, v40
	v_mul_f32_e32 v41, 0x43000000, v41
	v_mul_f32_e32 v42, 0x43000000, v42
	v_mul_f32_e32 v43, 0x43000000, v43
	ds_write_b128 v120, v[40:43] offset:1024
	v_mul_f32_e32 v44, 0x43000000, v44
	v_mul_f32_e32 v45, 0x43000000, v45
	v_mul_f32_e32 v46, 0x43000000, v46
	v_mul_f32_e32 v47, 0x43000000, v47
	ds_write_b128 v120, v[44:47] offset:2048
	v_mul_f32_e32 v48, 0x43000000, v48
	v_mul_f32_e32 v49, 0x43000000, v49
	v_mul_f32_e32 v50, 0x43000000, v50
	v_mul_f32_e32 v51, 0x43000000, v51
	ds_write_b128 v120, v[48:51] offset:3072
	v_mul_f32_e32 v52, 0x43000000, v52
	v_mul_f32_e32 v53, 0x43000000, v53
	v_mul_f32_e32 v54, 0x43000000, v54
	v_mul_f32_e32 v55, 0x43000000, v55
	ds_write_b128 v120, v[52:55] offset:4096
	v_mul_f32_e32 v56, 0x43000000, v56
	v_mul_f32_e32 v57, 0x43000000, v57
	v_mul_f32_e32 v58, 0x43000000, v58
	v_mul_f32_e32 v59, 0x43000000, v59
	ds_write_b128 v120, v[56:59] offset:5120
	v_mul_f32_e32 v60, 0x43000000, v60
	v_mul_f32_e32 v61, 0x43000000, v61
	v_mul_f32_e32 v62, 0x43000000, v62
	v_mul_f32_e32 v63, 0x43000000, v63
	ds_write_b128 v120, v[60:63] offset:6144
	v_mul_f32_e32 v64, 0x43000000, v64
	v_mul_f32_e32 v65, 0x43000000, v65
	v_mul_f32_e32 v66, 0x43000000, v66
	v_mul_f32_e32 v67, 0x43000000, v67
	ds_write_b128 v120, v[64:67] offset:7168
	s_waitcnt lgkmcnt(0)
	s_barrier
; #define GAS __attribute__((address_space(1)))
; #define LAS __attribute__((address_space(3)))
; #define LDS_WAIT() asm volatile("s_waitcnt lgkmcnt(0)" ::: "memory")
; __device__ __forceinline__ unsigned pk4_fp8(float a, float b, float c, float d) {
;     a = fminf(fmaxf(a, -448.f), 448.f); b = fminf(fmaxf(b, -448.f), 448.f); c = fminf(fmaxf(c, -448.f), 448.f); d = fminf(fmaxf(d, -448.f), 448.f);
;     int w = __builtin_amdgcn_cvt_pk_fp8_f32(a, b, 0, false); w = __builtin_amdgcn_cvt_pk_fp8_f32(c, d, w, true); return (unsigned)w; }
;     const int pr = item >> 1, kb = 2 * (pr / nblk) + (item & 1), nb = pr % nblk, k0 = 64 * kb, n0 = 32 * nb;
;     const int nr = n0 + (lane & 31); const int sc = MAP == 1 ? src_col_in(nr) : nr;
;     float v[32];
; #pragma unroll
;     for (int i = 0; i < 32; ++i) v[i] = sc >= 0 ? W[(size_t)(k0 + 2 * i + (lane >> 5)) * Nsrc + sc] : 0.f;
; #pragma unroll
;     for (int i = 0; i < 32; ++i) { const int k = k0 + 2 * i + (lane >> 5); float x = v[i] * wscale; if (KS) x *= (k < ksplit ? ksA[k] : ksB[k - ksplit]); scr[(2 * i + (lane >> 5)) * 33 + (lane & 31)] = x; }
;     LDS_WAIT(); asm volatile("" ::: "memory");
;     const int c = lane & 7;
; #pragma unroll
;     for (int j = 0; j < 4; ++j) { const int n = (lane >> 3) + 8 * j; const LAS float* s = scr + (8 * c) * 33 + n;
;         const unsigned long long o = (unsigned long long)pg8::pk4_fp8(s[0 * 33], s[1 * 33], s[2 * 33], s[3 * 33]) | ((unsigned long long)pg8::pk4_fp8(s[4 * 33], s[5 * 33], s[6 * 33], s[7 * 33]) << 32);
;         *(GAS unsigned long long*)(WT + (size_t)(n0 + n) * K + k0 + 8 * c) = o; }
;     LDS_WAIT(); asm volatile("" ::: "memory");
; }
	s_add_i32 s17, s16, 576
	s_min_u32 s17, s17, 0x3ff
	s_lshr_b32 s18, s17, 5
	s_add_i32 s18, s18, 96
	s_and_b32 s19, s17, 31
	s_lshl_b32 s18, s18, 21
	s_lshl_b32 s19, s19, 9
	s_add_u32 s18, s18, s19
	s_add_u32 s12, s2, s18
	s_addc_u32 s13, s3, 0
	global_load_dwordx4 v[36:39], v126, s[12:13]
	s_add_u32 s12, s12, 0x8000
	s_addc_u32 s13, s13, 0
	global_load_dwordx4 v[40:43], v126, s[12:13]
	s_add_u32 s12, s12, 0x8000
	s_addc_u32 s13, s13, 0
	global_load_dwordx4 v[44:47], v126, s[12:13]
	s_add_u32 s12, s12, 0x8000
	s_addc_u32 s13, s13, 0
	global_load_dwordx4 v[48:51], v126, s[12:13]
	s_add_u32 s12, s12, 0x8000
	s_addc_u32 s13, s13, 0
	global_load_dwordx4 v[52:55], v126, s[12:13]
	s_add_u32 s12, s12, 0x8000
	s_addc_u32 s13, s13, 0
	global_load_dwordx4 v[56:59], v126, s[12:13]
	s_add_u32 s12, s12, 0x8000
	s_addc_u32 s13, s13, 0
	global_load_dwordx4 v[60:63], v126, s[12:13]
	s_add_u32 s12, s12, 0x8000
	s_addc_u32 s13, s13, 0
	global_load_dwordx4 v[64:67], v126, s[12:13]
	s_add_i32 s17, s16, 384
	s_min_u32 s17, s17, 0x3ff
	s_lshr_b32 s18, s17, 5
	s_add_i32 s18, s18, 96
	s_and_b32 s19, s17, 31
	s_lshl_b32 s19, s19, 21
	s_lshl_b32 s18, s18, 7
	s_add_u32 s18, s18, s19
	s_add_u32 s14, s4, s18
	s_addc_u32 s15, s5, 0
	ds_read_b32 v100, v122
	ds_read_b32 v101, v122 offset:512
	ds_read_b32 v102, v122 offset:1024
	ds_read_b32 v103, v122 offset:1536
	ds_read_b32 v104, v122 offset:2048
	ds_read_b32 v105, v122 offset:2560
	ds_read_b32 v106, v122 offset:3072
	ds_read_b32 v107, v122 offset:3584
	ds_read_b32 v108, v122 offset:4096
	ds_read_b32 v109, v122 offset:4608
	ds_read_b32 v110, v122 offset:5120
	ds_read_b32 v111, v122 offset:5632
	ds_read_b32 v112, v122 offset:6144
	ds_read_b32 v113, v122 offset:6656
	ds_read_b32 v114, v122 offset:7168
	ds_read_b32 v115, v122 offset:7680
	s_waitcnt lgkmcnt(0)
	v_max_f32_e32 v100, v100, v100
	v_max_f32_e32 v101, v101, v101
	v_max_f32_e32 v102, v102, v102
	v_max_f32_e32 v103, v103, v103
	v_max_f32_e32 v104, v104, v104
	v_max_f32_e32 v105, v105, v105
	v_max_f32_e32 v106, v106, v106
	v_max_f32_e32 v107, v107, v107
	v_max_f32_e32 v108, v108, v108
	v_max_f32_e32 v109, v109, v109
	v_max_f32_e32 v110, v110, v110
	v_max_f32_e32 v111, v111, v111
	v_max_f32_e32 v112, v112, v112
	v_max_f32_e32 v113, v113, v113
	v_max_f32_e32 v114, v114, v114
	v_max_f32_e32 v115, v115, v115
	v_med3_f32 v100, v100, s20, v129
	v_med3_f32 v101, v101, s20, v129
	v_med3_f32 v102, v102, s20, v129
	v_med3_f32 v103, v103, s20, v129
	v_med3_f32 v104, v104, s20, v129
	v_med3_f32 v105, v105, s20, v129
	v_med3_f32 v106, v106, s20, v129
	v_med3_f32 v107, v107, s20, v129
	v_med3_f32 v108, v108, s20, v129
	v_med3_f32 v109, v109, s20, v129
	v_med3_f32 v110, v110, s20, v129
	v_med3_f32 v111, v111, s20, v129
	v_med3_f32 v112, v112, s20, v129
	v_med3_f32 v113, v113, s20, v129
	v_med3_f32 v114, v114, s20, v129
	v_med3_f32 v115, v115, s20, v129
	v_mov_b32_e32 v116, 0
	v_mov_b32_e32 v117, 0
	v_mov_b32_e32 v118, 0
	v_mov_b32_e32 v119, 0
	v_cvt_pk_fp8_f32 v116, v100, v101
	v_cvt_pk_fp8_f32 v117, v104, v105
	v_cvt_pk_fp8_f32 v118, v108, v109
	v_cvt_pk_fp8_f32 v119, v112, v113
	v_cvt_pk_fp8_f32 v116, v102, v103 op_sel:[0,0,1]
	v_cvt_pk_fp8_f32 v117, v106, v107 op_sel:[0,0,1]
	v_cvt_pk_fp8_f32 v118, v110, v111 op_sel:[0,0,1]
	v_cvt_pk_fp8_f32 v119, v114, v115 op_sel:[0,0,1]
	s_nop 0
	global_store_dwordx4 v127, v[116:119], s[14:15]
	ds_read_b32 v100, v124
	ds_read_b32 v101, v124 offset:512
	ds_read_b32 v102, v124 offset:1024
	ds_read_b32 v103, v124 offset:1536
	ds_read_b32 v104, v124 offset:2048
	ds_read_b32 v105, v124 offset:2560
	ds_read_b32 v106, v124 offset:3072
	ds_read_b32 v107, v124 offset:3584
	ds_read_b32 v108, v124 offset:4096
	ds_read_b32 v109, v124 offset:4608
	ds_read_b32 v110, v124 offset:5120
	ds_read_b32 v111, v124 offset:5632
	ds_read_b32 v112, v124 offset:6144
	ds_read_b32 v113, v124 offset:6656
	ds_read_b32 v114, v124 offset:7168
	ds_read_b32 v115, v124 offset:7680
	s_waitcnt lgkmcnt(0)
	v_max_f32_e32 v100, v100, v100
	v_max_f32_e32 v101, v101, v101
	v_max_f32_e32 v102, v102, v102
	v_max_f32_e32 v103, v103, v103
	v_max_f32_e32 v104, v104, v104
	v_max_f32_e32 v105, v105, v105
	v_max_f32_e32 v106, v106, v106
	v_max_f32_e32 v107, v107, v107
	v_max_f32_e32 v108, v108, v108
	v_max_f32_e32 v109, v109, v109
	v_max_f32_e32 v110, v110, v110
	v_max_f32_e32 v111, v111, v111
	v_max_f32_e32 v112, v112, v112
	v_max_f32_e32 v113, v113, v113
	v_max_f32_e32 v114, v114, v114
	v_max_f32_e32 v115, v115, v115
	v_med3_f32 v100, v100, s20, v129
	v_med3_f32 v101, v101, s20, v129
	v_med3_f32 v102, v102, s20, v129
	v_med3_f32 v103, v103, s20, v129
	v_med3_f32 v104, v104, s20, v129
	v_med3_f32 v105, v105, s20, v129
	v_med3_f32 v106, v106, s20, v129
	v_med3_f32 v107, v107, s20, v129
	v_med3_f32 v108, v108, s20, v129
	v_med3_f32 v109, v109, s20, v129
	v_med3_f32 v110, v110, s20, v129
	v_med3_f32 v111, v111, s20, v129
	v_med3_f32 v112, v112, s20, v129
	v_med3_f32 v113, v113, s20, v129
	v_med3_f32 v114, v114, s20, v129
	v_med3_f32 v115, v115, s20, v129
	v_mov_b32_e32 v116, 0
	v_mov_b32_e32 v117, 0
	v_mov_b32_e32 v118, 0
	v_mov_b32_e32 v119, 0
	v_cvt_pk_fp8_f32 v116, v100, v101
	v_cvt_pk_fp8_f32 v117, v104, v105
	v_cvt_pk_fp8_f32 v118, v108, v109
	v_cvt_pk_fp8_f32 v119, v112, v113
	v_cvt_pk_fp8_f32 v116, v102, v103 op_sel:[0,0,1]
	v_cvt_pk_fp8_f32 v117, v106, v107 op_sel:[0,0,1]
	v_cvt_pk_fp8_f32 v118, v110, v111 op_sel:[0,0,1]
	v_cvt_pk_fp8_f32 v119, v114, v115 op_sel:[0,0,1]
	s_nop 0
	global_store_dwordx4 v128, v[116:119], s[14:15]
	s_waitcnt vmcnt(12)
	v_mul_f32_e32 v68, 0x43000000, v68
	v_mul_f32_e32 v69, 0x43000000, v69
	v_mul_f32_e32 v70, 0x43000000, v70
	v_mul_f32_e32 v71, 0x43000000, v71
	ds_write_b128 v121, v[68:71]
	v_mul_f32_e32 v72, 0x43000000, v72
	v_mul_f32_e32 v73, 0x43000000, v73
	v_mul_f32_e32 v74, 0x43000000, v74
	v_mul_f32_e32 v75, 0x43000000, v75
	ds_write_b128 v121, v[72:75] offset:1024
	v_mul_f32_e32 v76, 0x43000000, v76
	v_mul_f32_e32 v77, 0x43000000, v77
	v_mul_f32_e32 v78, 0x43000000, v78
	v_mul_f32_e32 v79, 0x43000000, v79
	ds_write_b128 v121, v[76:79] offset:2048
	v_mul_f32_e32 v80, 0x43000000, v80
	v_mul_f32_e32 v81, 0x43000000, v81
	v_mul_f32_e32 v82, 0x43000000, v82
	v_mul_f32_e32 v83, 0x43000000, v83
	ds_write_b128 v121, v[80:83] offset:3072
	v_mul_f32_e32 v84, 0x43000000, v84
	v_mul_f32_e32 v85, 0x43000000, v85
	v_mul_f32_e32 v86, 0x43000000, v86
	v_mul_f32_e32 v87, 0x43000000, v87
	ds_write_b128 v121, v[84:87] offset:4096
	v_mul_f32_e32 v88, 0x43000000, v88
	v_mul_f32_e32 v89, 0x43000000, v89
	v_mul_f32_e32 v90, 0x43000000, v90
	v_mul_f32_e32 v91, 0x43000000, v91
	ds_write_b128 v121, v[88:91] offset:5120
	v_mul_f32_e32 v92, 0x43000000, v92
	v_mul_f32_e32 v93, 0x43000000, v93
	v_mul_f32_e32 v94, 0x43000000, v94
	v_mul_f32_e32 v95, 0x43000000, v95
	ds_write_b128 v121, v[92:95] offset:6144
	v_mul_f32_e32 v96, 0x43000000, v96
	v_mul_f32_e32 v97, 0x43000000, v97
	v_mul_f32_e32 v98, 0x43000000, v98
	v_mul_f32_e32 v99, 0x43000000, v99
	ds_write_b128 v121, v[96:99] offset:7168
	s_waitcnt lgkmcnt(0)
	s_barrier
; #define GAS __attribute__((address_space(1)))
; #define LAS __attribute__((address_space(3)))
; #define LDS_WAIT() asm volatile("s_waitcnt lgkmcnt(0)" ::: "memory")
; __device__ __forceinline__ unsigned pk4_fp8(float a, float b, float c, float d) {
;     a = fminf(fmaxf(a, -448.f), 448.f); b = fminf(fmaxf(b, -448.f), 448.f); c = fminf(fmaxf(c, -448.f), 448.f); d = fminf(fmaxf(d, -448.f), 448.f);
;     int w = __builtin_amdgcn_cvt_pk_fp8_f32(a, b, 0, false); w = __builtin_amdgcn_cvt_pk_fp8_f32(c, d, w, true); return (unsigned)w; }
;     const int pr = item >> 1, kb = 2 * (pr / nblk) + (item & 1), nb = pr % nblk, k0 = 64 * kb, n0 = 32 * nb;
;     const int nr = n0 + (lane & 31); const int sc = MAP == 1 ? src_col_in(nr) : nr;
;     float v[32];
; #pragma unroll
;     for (int i = 0; i < 32; ++i) v[i] = sc >= 0 ? W[(size_t)(k0 + 2 * i + (lane >> 5)) * Nsrc + sc] : 0.f;
; #pragma unroll
;     for (int i = 0; i < 32; ++i) { const int k = k0 + 2 * i + (lane >> 5); float x = v[i] * wscale; if (KS) x *= (k < ksplit ? ksA[k] : ksB[k - ksplit]); scr[(2 * i + (lane >> 5)) * 33 + (lane & 31)] = x; }
;     LDS_WAIT(); asm volatile("" ::: "memory");
;     const int c = lane & 7;
; #pragma unroll
;     for (int j = 0; j < 4; ++j) { const int n = (lane >> 3) + 8 * j; const LAS float* s = scr + (8 * c) * 33 + n;
;         const unsigned long long o = (unsigned long long)pg8::pk4_fp8(s[0 * 33], s[1 * 33], s[2 * 33], s[3 * 33]) | ((unsigned long long)pg8::pk4_fp8(s[4 * 33], s[5 * 33], s[6 * 33], s[7 * 33]) << 32);
;         *(GAS unsigned long long*)(WT + (size_t)(n0 + n) * K + k0 + 8 * c) = o; }
;     LDS_WAIT(); asm volatile("" ::: "memory");
; }
	s_add_i32 s17, s16, 672
	s_min_u32 s17, s17, 0x3ff
	s_lshr_b32 s18, s17, 5
	s_add_i32 s18, s18, 96
	s_and_b32 s19, s17, 31
	s_lshl_b32 s18, s18, 21
	s_lshl_b32 s19, s19, 9
	s_add_u32 s18, s18, s19
	s_add_u32 s12, s2, s18
	s_addc_u32 s13, s3, 0
	global_load_dwordx4 v[68:71], v126, s[12:13]
	s_add_u32 s12, s12, 0x8000
	s_addc_u32 s13, s13, 0
	global_load_dwordx4 v[72:75], v126, s[12:13]
	s_add_u32 s12, s12, 0x8000
	s_addc_u32 s13, s13, 0
	global_load_dwordx4 v[76:79], v126, s[12:13]
	s_add_u32 s12, s12, 0x8000
	s_addc_u32 s13, s13, 0
	global_load_dwordx4 v[80:83], v126, s[12:13]
	s_add_u32 s12, s12, 0x8000
	s_addc_u32 s13, s13, 0
	global_load_dwordx4 v[84:87], v126, s[12:13]
	s_add_u32 s12, s12, 0x8000
	s_addc_u32 s13, s13, 0
	global_load_dwordx4 v[88:91], v126, s[12:13]
	s_add_u32 s12, s12, 0x8000
	s_addc_u32 s13, s13, 0
	global_load_dwordx4 v[92:95], v126, s[12:13]
	s_add_u32 s12, s12, 0x8000
	s_addc_u32 s13, s13, 0
	global_load_dwordx4 v[96:99], v126, s[12:13]
	s_add_i32 s17, s16, 480
	s_min_u32 s17, s17, 0x3ff
	s_lshr_b32 s18, s17, 5
	s_add_i32 s18, s18, 96
	s_and_b32 s19, s17, 31
	s_lshl_b32 s19, s19, 21
	s_lshl_b32 s18, s18, 7
	s_add_u32 s18, s18, s19
	s_add_u32 s14, s4, s18
	s_addc_u32 s15, s5, 0
	ds_read_b32 v100, v123
	ds_read_b32 v101, v123 offset:512
	ds_read_b32 v102, v123 offset:1024
	ds_read_b32 v103, v123 offset:1536
	ds_read_b32 v104, v123 offset:2048
	ds_read_b32 v105, v123 offset:2560
	ds_read_b32 v106, v123 offset:3072
	ds_read_b32 v107, v123 offset:3584
	ds_read_b32 v108, v123 offset:4096
	ds_read_b32 v109, v123 offset:4608
	ds_read_b32 v110, v123 offset:5120
	ds_read_b32 v111, v123 offset:5632
	ds_read_b32 v112, v123 offset:6144
	ds_read_b32 v113, v123 offset:6656
	ds_read_b32 v114, v123 offset:7168
	ds_read_b32 v115, v123 offset:7680
	s_waitcnt lgkmcnt(0)
	v_max_f32_e32 v100, v100, v100
	v_max_f32_e32 v101, v101, v101
	v_max_f32_e32 v102, v102, v102
	v_max_f32_e32 v103, v103, v103
	v_max_f32_e32 v104, v104, v104
	v_max_f32_e32 v105, v105, v105
	v_max_f32_e32 v106, v106, v106
	v_max_f32_e32 v107, v107, v107
	v_max_f32_e32 v108, v108, v108
	v_max_f32_e32 v109, v109, v109
	v_max_f32_e32 v110, v110, v110
	v_max_f32_e32 v111, v111, v111
	v_max_f32_e32 v112, v112, v112
	v_max_f32_e32 v113, v113, v113
	v_max_f32_e32 v114, v114, v114
	v_max_f32_e32 v115, v115, v115
	v_med3_f32 v100, v100, s20, v129
	v_med3_f32 v101, v101, s20, v129
	v_med3_f32 v102, v102, s20, v129
	v_med3_f32 v103, v103, s20, v129
	v_med3_f32 v104, v104, s20, v129
	v_med3_f32 v105, v105, s20, v129
	v_med3_f32 v106, v106, s20, v129
	v_med3_f32 v107, v107, s20, v129
	v_med3_f32 v108, v108, s20, v129
	v_med3_f32 v109, v109, s20, v129
	v_med3_f32 v110, v110, s20, v129
	v_med3_f32 v111, v111, s20, v129
	v_med3_f32 v112, v112, s20, v129
	v_med3_f32 v113, v113, s20, v129
	v_med3_f32 v114, v114, s20, v129
	v_med3_f32 v115, v115, s20, v129
	v_mov_b32_e32 v116, 0
	v_mov_b32_e32 v117, 0
	v_mov_b32_e32 v118, 0
	v_mov_b32_e32 v119, 0
	v_cvt_pk_fp8_f32 v116, v100, v101
	v_cvt_pk_fp8_f32 v117, v104, v105
	v_cvt_pk_fp8_f32 v118, v108, v109
	v_cvt_pk_fp8_f32 v119, v112, v113
	v_cvt_pk_fp8_f32 v116, v102, v103 op_sel:[0,0,1]
	v_cvt_pk_fp8_f32 v117, v106, v107 op_sel:[0,0,1]
	v_cvt_pk_fp8_f32 v118, v110, v111 op_sel:[0,0,1]
	v_cvt_pk_fp8_f32 v119, v114, v115 op_sel:[0,0,1]
	s_nop 0
	global_store_dwordx4 v127, v[116:119], s[14:15]
	ds_read_b32 v100, v125
	ds_read_b32 v101, v125 offset:512
	ds_read_b32 v102, v125 offset:1024
	ds_read_b32 v103, v125 offset:1536
	ds_read_b32 v104, v125 offset:2048
	ds_read_b32 v105, v125 offset:2560
	ds_read_b32 v106, v125 offset:3072
	ds_read_b32 v107, v125 offset:3584
	ds_read_b32 v108, v125 offset:4096
	ds_read_b32 v109, v125 offset:4608
	ds_read_b32 v110, v125 offset:5120
	ds_read_b32 v111, v125 offset:5632
	ds_read_b32 v112, v125 offset:6144
	ds_read_b32 v113, v125 offset:6656
	ds_read_b32 v114, v125 offset:7168
	ds_read_b32 v115, v125 offset:7680
	s_waitcnt lgkmcnt(0)
	v_max_f32_e32 v100, v100, v100
	v_max_f32_e32 v101, v101, v101
	v_max_f32_e32 v102, v102, v102
	v_max_f32_e32 v103, v103, v103
	v_max_f32_e32 v104, v104, v104
	v_max_f32_e32 v105, v105, v105
	v_max_f32_e32 v106, v106, v106
	v_max_f32_e32 v107, v107, v107
	v_max_f32_e32 v108, v108, v108
	v_max_f32_e32 v109, v109, v109
	v_max_f32_e32 v110, v110, v110
	v_max_f32_e32 v111, v111, v111
	v_max_f32_e32 v112, v112, v112
	v_max_f32_e32 v113, v113, v113
	v_max_f32_e32 v114, v114, v114
	v_max_f32_e32 v115, v115, v115
	v_med3_f32 v100, v100, s20, v129
	v_med3_f32 v101, v101, s20, v129
	v_med3_f32 v102, v102, s20, v129
	v_med3_f32 v103, v103, s20, v129
	v_med3_f32 v104, v104, s20, v129
	v_med3_f32 v105, v105, s20, v129
	v_med3_f32 v106, v106, s20, v129
	v_med3_f32 v107, v107, s20, v129
	v_med3_f32 v108, v108, s20, v129
	v_med3_f32 v109, v109, s20, v129
	v_med3_f32 v110, v110, s20, v129
	v_med3_f32 v111, v111, s20, v129
	v_med3_f32 v112, v112, s20, v129
	v_med3_f32 v113, v113, s20, v129
	v_med3_f32 v114, v114, s20, v129
	v_med3_f32 v115, v115, s20, v129
	v_mov_b32_e32 v116, 0
	v_mov_b32_e32 v117, 0
	v_mov_b32_e32 v118, 0
	v_mov_b32_e32 v119, 0
	v_cvt_pk_fp8_f32 v116, v100, v101
	v_cvt_pk_fp8_f32 v117, v104, v105
	v_cvt_pk_fp8_f32 v118, v108, v109
	v_cvt_pk_fp8_f32 v119, v112, v113
	v_cvt_pk_fp8_f32 v116, v102, v103 op_sel:[0,0,1]
	v_cvt_pk_fp8_f32 v117, v106, v107 op_sel:[0,0,1]
	v_cvt_pk_fp8_f32 v118, v110, v111 op_sel:[0,0,1]
	v_cvt_pk_fp8_f32 v119, v114, v115 op_sel:[0,0,1]
	s_nop 0
	global_store_dwordx4 v128, v[116:119], s[14:15]
	s_waitcnt vmcnt(12)
	v_mul_f32_e32 v36, 0x43000000, v36
	v_mul_f32_e32 v37, 0x43000000, v37
	v_mul_f32_e32 v38, 0x43000000, v38
	v_mul_f32_e32 v39, 0x43000000, v39
	ds_write_b128 v120, v[36:39]
	v_mul_f32_e32 v40, 0x43000000, v40
	v_mul_f32_e32 v41, 0x43000000, v41
	v_mul_f32_e32 v42, 0x43000000, v42
	v_mul_f32_e32 v43, 0x43000000, v43
	ds_write_b128 v120, v[40:43] offset:1024
	v_mul_f32_e32 v44, 0x43000000, v44
	v_mul_f32_e32 v45, 0x43000000, v45
	v_mul_f32_e32 v46, 0x43000000, v46
	v_mul_f32_e32 v47, 0x43000000, v47
	ds_write_b128 v120, v[44:47] offset:2048
	v_mul_f32_e32 v48, 0x43000000, v48
	v_mul_f32_e32 v49, 0x43000000, v49
	v_mul_f32_e32 v50, 0x43000000, v50
	v_mul_f32_e32 v51, 0x43000000, v51
	ds_write_b128 v120, v[48:51] offset:3072
	v_mul_f32_e32 v52, 0x43000000, v52
	v_mul_f32_e32 v53, 0x43000000, v53
	v_mul_f32_e32 v54, 0x43000000, v54
	v_mul_f32_e32 v55, 0x43000000, v55
	ds_write_b128 v120, v[52:55] offset:4096
	v_mul_f32_e32 v56, 0x43000000, v56
	v_mul_f32_e32 v57, 0x43000000, v57
	v_mul_f32_e32 v58, 0x43000000, v58
	v_mul_f32_e32 v59, 0x43000000, v59
	ds_write_b128 v120, v[56:59] offset:5120
	v_mul_f32_e32 v60, 0x43000000, v60
	v_mul_f32_e32 v61, 0x43000000, v61
	v_mul_f32_e32 v62, 0x43000000, v62
	v_mul_f32_e32 v63, 0x43000000, v63
	ds_write_b128 v120, v[60:63] offset:6144
	v_mul_f32_e32 v64, 0x43000000, v64
	v_mul_f32_e32 v65, 0x43000000, v65
	v_mul_f32_e32 v66, 0x43000000, v66
	v_mul_f32_e32 v67, 0x43000000, v67
	ds_write_b128 v120, v[64:67] offset:7168
	s_waitcnt lgkmcnt(0)
	s_barrier
; #define GAS __attribute__((address_space(1)))
; #define LAS __attribute__((address_space(3)))
; #define LDS_WAIT() asm volatile("s_waitcnt lgkmcnt(0)" ::: "memory")
; __device__ __forceinline__ unsigned pk4_fp8(float a, float b, float c, float d) {
;     a = fminf(fmaxf(a, -448.f), 448.f); b = fminf(fmaxf(b, -448.f), 448.f); c = fminf(fmaxf(c, -448.f), 448.f); d = fminf(fmaxf(d, -448.f), 448.f);
;     int w = __builtin_amdgcn_cvt_pk_fp8_f32(a, b, 0, false); w = __builtin_amdgcn_cvt_pk_fp8_f32(c, d, w, true); return (unsigned)w; }
;     const int pr = item >> 1, kb = 2 * (pr / nblk) + (item & 1), nb = pr % nblk, k0 = 64 * kb, n0 = 32 * nb;
;     const int nr = n0 + (lane & 31); const int sc = MAP == 1 ? src_col_in(nr) : nr;
;     float v[32];
; #pragma unroll
;     for (int i = 0; i < 32; ++i) v[i] = sc >= 0 ? W[(size_t)(k0 + 2 * i + (lane >> 5)) * Nsrc + sc] : 0.f;
; #pragma unroll
;     for (int i = 0; i < 32; ++i) { const int k = k0 + 2 * i + (lane >> 5); float x = v[i] * wscale; if (KS) x *= (k < ksplit ? ksA[k] : ksB[k - ksplit]); scr[(2 * i + (lane >> 5)) * 33 + (lane & 31)] = x; }
;     LDS_WAIT(); asm volatile("" ::: "memory");
;     const int c = lane & 7;
; #pragma unroll
;     for (int j = 0; j < 4; ++j) { const int n = (lane >> 3) + 8 * j; const LAS float* s = scr + (8 * c) * 33 + n;
;         const unsigned long long o = (unsigned long long)pg8::pk4_fp8(s[0 * 33], s[1 * 33], s[2 * 33], s[3 * 33]) | ((unsigned long long)pg8::pk4_fp8(s[4 * 33], s[5 * 33], s[6 * 33], s[7 * 33]) << 32);
;         *(GAS unsigned long long*)(WT + (size_t)(n0 + n) * K + k0 + 8 * c) = o; }
;     LDS_WAIT(); asm volatile("" ::: "memory");
; }
	s_add_i32 s17, s16, 768
	s_min_u32 s17, s17, 0x3ff
	s_lshr_b32 s18, s17, 5
	s_add_i32 s18, s18, 96
	s_and_b32 s19, s17, 31
	s_lshl_b32 s18, s18, 21
	s_lshl_b32 s19, s19, 9
	s_add_u32 s18, s18, s19
	s_add_u32 s12, s2, s18
	s_addc_u32 s13, s3, 0
	global_load_dwordx4 v[36:39], v126, s[12:13]
	s_add_u32 s12, s12, 0x8000
	s_addc_u32 s13, s13, 0
	global_load_dwordx4 v[40:43], v126, s[12:13]
	s_add_u32 s12, s12, 0x8000
	s_addc_u32 s13, s13, 0
	global_load_dwordx4 v[44:47], v126, s[12:13]
	s_add_u32 s12, s12, 0x8000
	s_addc_u32 s13, s13, 0
	global_load_dwordx4 v[48:51], v126, s[12:13]
	s_add_u32 s12, s12, 0x8000
	s_addc_u32 s13, s13, 0
	global_load_dwordx4 v[52:55], v126, s[12:13]
	s_add_u32 s12, s12, 0x8000
	s_addc_u32 s13, s13, 0
	global_load_dwordx4 v[56:59], v126, s[12:13]
	s_add_u32 s12, s12, 0x8000
	s_addc_u32 s13, s13, 0
	global_load_dwordx4 v[60:63], v126, s[12:13]
	s_add_u32 s12, s12, 0x8000
	s_addc_u32 s13, s13, 0
	global_load_dwordx4 v[64:67], v126, s[12:13]
	s_add_i32 s17, s16, 576
	s_min_u32 s17, s17, 0x3ff
	s_lshr_b32 s18, s17, 5
	s_add_i32 s18, s18, 96
	s_and_b32 s19, s17, 31
	s_lshl_b32 s19, s19, 21
	s_lshl_b32 s18, s18, 7
	s_add_u32 s18, s18, s19
	s_add_u32 s14, s4, s18
	s_addc_u32 s15, s5, 0
	ds_read_b32 v100, v122
	ds_read_b32 v101, v122 offset:512
	ds_read_b32 v102, v122 offset:1024
	ds_read_b32 v103, v122 offset:1536
	ds_read_b32 v104, v122 offset:2048
	ds_read_b32 v105, v122 offset:2560
	ds_read_b32 v106, v122 offset:3072
	ds_read_b32 v107, v122 offset:3584
	ds_read_b32 v108, v122 offset:4096
	ds_read_b32 v109, v122 offset:4608
	ds_read_b32 v110, v122 offset:5120
	ds_read_b32 v111, v122 offset:5632
	ds_read_b32 v112, v122 offset:6144
	ds_read_b32 v113, v122 offset:6656
	ds_read_b32 v114, v122 offset:7168
	ds_read_b32 v115, v122 offset:7680
	s_waitcnt lgkmcnt(0)
	v_max_f32_e32 v100, v100, v100
	v_max_f32_e32 v101, v101, v101
	v_max_f32_e32 v102, v102, v102
	v_max_f32_e32 v103, v103, v103
	v_max_f32_e32 v104, v104, v104
	v_max_f32_e32 v105, v105, v105
	v_max_f32_e32 v106, v106, v106
	v_max_f32_e32 v107, v107, v107
	v_max_f32_e32 v108, v108, v108
	v_max_f32_e32 v109, v109, v109
	v_max_f32_e32 v110, v110, v110
	v_max_f32_e32 v111, v111, v111
	v_max_f32_e32 v112, v112, v112
	v_max_f32_e32 v113, v113, v113
	v_max_f32_e32 v114, v114, v114
	v_max_f32_e32 v115, v115, v115
	v_med3_f32 v100, v100, s20, v129
	v_med3_f32 v101, v101, s20, v129
	v_med3_f32 v102, v102, s20, v129
	v_med3_f32 v103, v103, s20, v129
	v_med3_f32 v104, v104, s20, v129
	v_med3_f32 v105, v105, s20, v129
	v_med3_f32 v106, v106, s20, v129
	v_med3_f32 v107, v107, s20, v129
	v_med3_f32 v108, v108, s20, v129
	v_med3_f32 v109, v109, s20, v129
	v_med3_f32 v110, v110, s20, v129
	v_med3_f32 v111, v111, s20, v129
	v_med3_f32 v112, v112, s20, v129
	v_med3_f32 v113, v113, s20, v129
	v_med3_f32 v114, v114, s20, v129
	v_med3_f32 v115, v115, s20, v129
	v_mov_b32_e32 v116, 0
	v_mov_b32_e32 v117, 0
	v_mov_b32_e32 v118, 0
	v_mov_b32_e32 v119, 0
	v_cvt_pk_fp8_f32 v116, v100, v101
	v_cvt_pk_fp8_f32 v117, v104, v105
	v_cvt_pk_fp8_f32 v118, v108, v109
	v_cvt_pk_fp8_f32 v119, v112, v113
	v_cvt_pk_fp8_f32 v116, v102, v103 op_sel:[0,0,1]
	v_cvt_pk_fp8_f32 v117, v106, v107 op_sel:[0,0,1]
	v_cvt_pk_fp8_f32 v118, v110, v111 op_sel:[0,0,1]
	v_cvt_pk_fp8_f32 v119, v114, v115 op_sel:[0,0,1]
	s_nop 0
	global_store_dwordx4 v127, v[116:119], s[14:15]
	ds_read_b32 v100, v124
	ds_read_b32 v101, v124 offset:512
	ds_read_b32 v102, v124 offset:1024
	ds_read_b32 v103, v124 offset:1536
	ds_read_b32 v104, v124 offset:2048
	ds_read_b32 v105, v124 offset:2560
	ds_read_b32 v106, v124 offset:3072
	ds_read_b32 v107, v124 offset:3584
	ds_read_b32 v108, v124 offset:4096
	ds_read_b32 v109, v124 offset:4608
	ds_read_b32 v110, v124 offset:5120
	ds_read_b32 v111, v124 offset:5632
	ds_read_b32 v112, v124 offset:6144
	ds_read_b32 v113, v124 offset:6656
	ds_read_b32 v114, v124 offset:7168
	ds_read_b32 v115, v124 offset:7680
	s_waitcnt lgkmcnt(0)
	v_max_f32_e32 v100, v100, v100
	v_max_f32_e32 v101, v101, v101
	v_max_f32_e32 v102, v102, v102
	v_max_f32_e32 v103, v103, v103
	v_max_f32_e32 v104, v104, v104
	v_max_f32_e32 v105, v105, v105
	v_max_f32_e32 v106, v106, v106
	v_max_f32_e32 v107, v107, v107
	v_max_f32_e32 v108, v108, v108
	v_max_f32_e32 v109, v109, v109
	v_max_f32_e32 v110, v110, v110
	v_max_f32_e32 v111, v111, v111
	v_max_f32_e32 v112, v112, v112
	v_max_f32_e32 v113, v113, v113
	v_max_f32_e32 v114, v114, v114
	v_max_f32_e32 v115, v115, v115
	v_med3_f32 v100, v100, s20, v129
	v_med3_f32 v101, v101, s20, v129
	v_med3_f32 v102, v102, s20, v129
	v_med3_f32 v103, v103, s20, v129
	v_med3_f32 v104, v104, s20, v129
	v_med3_f32 v105, v105, s20, v129
	v_med3_f32 v106, v106, s20, v129
	v_med3_f32 v107, v107, s20, v129
	v_med3_f32 v108, v108, s20, v129
	v_med3_f32 v109, v109, s20, v129
	v_med3_f32 v110, v110, s20, v129
	v_med3_f32 v111, v111, s20, v129
	v_med3_f32 v112, v112, s20, v129
	v_med3_f32 v113, v113, s20, v129
	v_med3_f32 v114, v114, s20, v129
	v_med3_f32 v115, v115, s20, v129
	v_mov_b32_e32 v116, 0
	v_mov_b32_e32 v117, 0
	v_mov_b32_e32 v118, 0
	v_mov_b32_e32 v119, 0
	v_cvt_pk_fp8_f32 v116, v100, v101
	v_cvt_pk_fp8_f32 v117, v104, v105
	v_cvt_pk_fp8_f32 v118, v108, v109
	v_cvt_pk_fp8_f32 v119, v112, v113
	v_cvt_pk_fp8_f32 v116, v102, v103 op_sel:[0,0,1]
	v_cvt_pk_fp8_f32 v117, v106, v107 op_sel:[0,0,1]
	v_cvt_pk_fp8_f32 v118, v110, v111 op_sel:[0,0,1]
	v_cvt_pk_fp8_f32 v119, v114, v115 op_sel:[0,0,1]
	s_nop 0
	global_store_dwordx4 v128, v[116:119], s[14:15]
	s_waitcnt vmcnt(12)
	v_mul_f32_e32 v68, 0x43000000, v68
	v_mul_f32_e32 v69, 0x43000000, v69
	v_mul_f32_e32 v70, 0x43000000, v70
	v_mul_f32_e32 v71, 0x43000000, v71
	ds_write_b128 v121, v[68:71]
	v_mul_f32_e32 v72, 0x43000000, v72
	v_mul_f32_e32 v73, 0x43000000, v73
	v_mul_f32_e32 v74, 0x43000000, v74
	v_mul_f32_e32 v75, 0x43000000, v75
	ds_write_b128 v121, v[72:75] offset:1024
	v_mul_f32_e32 v76, 0x43000000, v76
	v_mul_f32_e32 v77, 0x43000000, v77
	v_mul_f32_e32 v78, 0x43000000, v78
	v_mul_f32_e32 v79, 0x43000000, v79
	ds_write_b128 v121, v[76:79] offset:2048
	v_mul_f32_e32 v80, 0x43000000, v80
	v_mul_f32_e32 v81, 0x43000000, v81
	v_mul_f32_e32 v82, 0x43000000, v82
	v_mul_f32_e32 v83, 0x43000000, v83
	ds_write_b128 v121, v[80:83] offset:3072
	v_mul_f32_e32 v84, 0x43000000, v84
	v_mul_f32_e32 v85, 0x43000000, v85
	v_mul_f32_e32 v86, 0x43000000, v86
	v_mul_f32_e32 v87, 0x43000000, v87
	ds_write_b128 v121, v[84:87] offset:4096
	v_mul_f32_e32 v88, 0x43000000, v88
	v_mul_f32_e32 v89, 0x43000000, v89
	v_mul_f32_e32 v90, 0x43000000, v90
	v_mul_f32_e32 v91, 0x43000000, v91
	ds_write_b128 v121, v[88:91] offset:5120
	v_mul_f32_e32 v92, 0x43000000, v92
	v_mul_f32_e32 v93, 0x43000000, v93
	v_mul_f32_e32 v94, 0x43000000, v94
	v_mul_f32_e32 v95, 0x43000000, v95
	ds_write_b128 v121, v[92:95] offset:6144
	v_mul_f32_e32 v96, 0x43000000, v96
	v_mul_f32_e32 v97, 0x43000000, v97
	v_mul_f32_e32 v98, 0x43000000, v98
	v_mul_f32_e32 v99, 0x43000000, v99
	ds_write_b128 v121, v[96:99] offset:7168
	s_waitcnt lgkmcnt(0)
	s_barrier
; #define GAS __attribute__((address_space(1)))
; #define LAS __attribute__((address_space(3)))
; #define LDS_WAIT() asm volatile("s_waitcnt lgkmcnt(0)" ::: "memory")
; __device__ __forceinline__ unsigned pk4_fp8(float a, float b, float c, float d) {
;     a = fminf(fmaxf(a, -448.f), 448.f); b = fminf(fmaxf(b, -448.f), 448.f); c = fminf(fmaxf(c, -448.f), 448.f); d = fminf(fmaxf(d, -448.f), 448.f);
;     int w = __builtin_amdgcn_cvt_pk_fp8_f32(a, b, 0, false); w = __builtin_amdgcn_cvt_pk_fp8_f32(c, d, w, true); return (unsigned)w; }
;     const int pr = item >> 1, kb = 2 * (pr / nblk) + (item & 1), nb = pr % nblk, k0 = 64 * kb, n0 = 32 * nb;
;     const int nr = n0 + (lane & 31); const int sc = MAP == 1 ? src_col_in(nr) : nr;
;     float v[32];
; #pragma unroll
;     for (int i = 0; i < 32; ++i) v[i] = sc >= 0 ? W[(size_t)(k0 + 2 * i + (lane >> 5)) * Nsrc + sc] : 0.f;
; #pragma unroll
;     for (int i = 0; i < 32; ++i) { const int k = k0 + 2 * i + (lane >> 5); float x = v[i] * wscale; if (KS) x *= (k < ksplit ? ksA[k] : ksB[k - ksplit]); scr[(2 * i + (lane >> 5)) * 33 + (lane & 31)] = x; }
;     LDS_WAIT(); asm volatile("" ::: "memory");
;     const int c = lane & 7;
; #pragma unroll
;     for (int j = 0; j < 4; ++j) { const int n = (lane >> 3) + 8 * j; const LAS float* s = scr + (8 * c) * 33 + n;
;         const unsigned long long o = (unsigned long long)pg8::pk4_fp8(s[0 * 33], s[1 * 33], s[2 * 33], s[3 * 33]) | ((unsigned long long)pg8::pk4_fp8(s[4 * 33], s[5 * 33], s[6 * 33], s[7 * 33]) << 32);
;         *(GAS unsigned long long*)(WT + (size_t)(n0 + n) * K + k0 + 8 * c) = o; }
;     LDS_WAIT(); asm volatile("" ::: "memory");
; }
	s_add_i32 s17, s16, 864
	s_min_u32 s17, s17, 0x3ff
	s_lshr_b32 s18, s17, 5
	s_add_i32 s18, s18, 96
	s_and_b32 s19, s17, 31
	s_lshl_b32 s18, s18, 21
	s_lshl_b32 s19, s19, 9
	s_add_u32 s18, s18, s19
	s_add_u32 s12, s2, s18
	s_addc_u32 s13, s3, 0
	global_load_dwordx4 v[68:71], v126, s[12:13]
	s_add_u32 s12, s12, 0x8000
	s_addc_u32 s13, s13, 0
	global_load_dwordx4 v[72:75], v126, s[12:13]
	s_add_u32 s12, s12, 0x8000
	s_addc_u32 s13, s13, 0
	global_load_dwordx4 v[76:79], v126, s[12:13]
	s_add_u32 s12, s12, 0x8000
	s_addc_u32 s13, s13, 0
	global_load_dwordx4 v[80:83], v126, s[12:13]
	s_add_u32 s12, s12, 0x8000
	s_addc_u32 s13, s13, 0
	global_load_dwordx4 v[84:87], v126, s[12:13]
	s_add_u32 s12, s12, 0x8000
	s_addc_u32 s13, s13, 0
	global_load_dwordx4 v[88:91], v126, s[12:13]
	s_add_u32 s12, s12, 0x8000
	s_addc_u32 s13, s13, 0
	global_load_dwordx4 v[92:95], v126, s[12:13]
	s_add_u32 s12, s12, 0x8000
	s_addc_u32 s13, s13, 0
	global_load_dwordx4 v[96:99], v126, s[12:13]
	s_add_i32 s17, s16, 672
	s_min_u32 s17, s17, 0x3ff
	s_lshr_b32 s18, s17, 5
	s_add_i32 s18, s18, 96
	s_and_b32 s19, s17, 31
	s_lshl_b32 s19, s19, 21
	s_lshl_b32 s18, s18, 7
	s_add_u32 s18, s18, s19
	s_add_u32 s14, s4, s18
	s_addc_u32 s15, s5, 0
	ds_read_b32 v100, v123
	ds_read_b32 v101, v123 offset:512
	ds_read_b32 v102, v123 offset:1024
	ds_read_b32 v103, v123 offset:1536
	ds_read_b32 v104, v123 offset:2048
	ds_read_b32 v105, v123 offset:2560
	ds_read_b32 v106, v123 offset:3072
	ds_read_b32 v107, v123 offset:3584
	ds_read_b32 v108, v123 offset:4096
	ds_read_b32 v109, v123 offset:4608
	ds_read_b32 v110, v123 offset:5120
	ds_read_b32 v111, v123 offset:5632
	ds_read_b32 v112, v123 offset:6144
	ds_read_b32 v113, v123 offset:6656
	ds_read_b32 v114, v123 offset:7168
	ds_read_b32 v115, v123 offset:7680
	s_waitcnt lgkmcnt(0)
	v_max_f32_e32 v100, v100, v100
	v_max_f32_e32 v101, v101, v101
	v_max_f32_e32 v102, v102, v102
	v_max_f32_e32 v103, v103, v103
	v_max_f32_e32 v104, v104, v104
	v_max_f32_e32 v105, v105, v105
	v_max_f32_e32 v106, v106, v106
	v_max_f32_e32 v107, v107, v107
	v_max_f32_e32 v108, v108, v108
	v_max_f32_e32 v109, v109, v109
	v_max_f32_e32 v110, v110, v110
	v_max_f32_e32 v111, v111, v111
	v_max_f32_e32 v112, v112, v112
	v_max_f32_e32 v113, v113, v113
	v_max_f32_e32 v114, v114, v114
	v_max_f32_e32 v115, v115, v115
	v_med3_f32 v100, v100, s20, v129
	v_med3_f32 v101, v101, s20, v129
	v_med3_f32 v102, v102, s20, v129
	v_med3_f32 v103, v103, s20, v129
	v_med3_f32 v104, v104, s20, v129
	v_med3_f32 v105, v105, s20, v129
	v_med3_f32 v106, v106, s20, v129
	v_med3_f32 v107, v107, s20, v129
	v_med3_f32 v108, v108, s20, v129
	v_med3_f32 v109, v109, s20, v129
	v_med3_f32 v110, v110, s20, v129
	v_med3_f32 v111, v111, s20, v129
	v_med3_f32 v112, v112, s20, v129
	v_med3_f32 v113, v113, s20, v129
	v_med3_f32 v114, v114, s20, v129
	v_med3_f32 v115, v115, s20, v129
	v_mov_b32_e32 v116, 0
	v_mov_b32_e32 v117, 0
	v_mov_b32_e32 v118, 0
	v_mov_b32_e32 v119, 0
	v_cvt_pk_fp8_f32 v116, v100, v101
	v_cvt_pk_fp8_f32 v117, v104, v105
	v_cvt_pk_fp8_f32 v118, v108, v109
	v_cvt_pk_fp8_f32 v119, v112, v113
	v_cvt_pk_fp8_f32 v116, v102, v103 op_sel:[0,0,1]
	v_cvt_pk_fp8_f32 v117, v106, v107 op_sel:[0,0,1]
	v_cvt_pk_fp8_f32 v118, v110, v111 op_sel:[0,0,1]
	v_cvt_pk_fp8_f32 v119, v114, v115 op_sel:[0,0,1]
	s_nop 0
	global_store_dwordx4 v127, v[116:119], s[14:15]
	ds_read_b32 v100, v125
	ds_read_b32 v101, v125 offset:512
	ds_read_b32 v102, v125 offset:1024
	ds_read_b32 v103, v125 offset:1536
	ds_read_b32 v104, v125 offset:2048
	ds_read_b32 v105, v125 offset:2560
	ds_read_b32 v106, v125 offset:3072
	ds_read_b32 v107, v125 offset:3584
	ds_read_b32 v108, v125 offset:4096
	ds_read_b32 v109, v125 offset:4608
	ds_read_b32 v110, v125 offset:5120
	ds_read_b32 v111, v125 offset:5632
	ds_read_b32 v112, v125 offset:6144
	ds_read_b32 v113, v125 offset:6656
	ds_read_b32 v114, v125 offset:7168
	ds_read_b32 v115, v125 offset:7680
	s_waitcnt lgkmcnt(0)
	v_max_f32_e32 v100, v100, v100
	v_max_f32_e32 v101, v101, v101
	v_max_f32_e32 v102, v102, v102
	v_max_f32_e32 v103, v103, v103
	v_max_f32_e32 v104, v104, v104
	v_max_f32_e32 v105, v105, v105
	v_max_f32_e32 v106, v106, v106
	v_max_f32_e32 v107, v107, v107
	v_max_f32_e32 v108, v108, v108
	v_max_f32_e32 v109, v109, v109
	v_max_f32_e32 v110, v110, v110
	v_max_f32_e32 v111, v111, v111
	v_max_f32_e32 v112, v112, v112
	v_max_f32_e32 v113, v113, v113
	v_max_f32_e32 v114, v114, v114
	v_max_f32_e32 v115, v115, v115
	v_med3_f32 v100, v100, s20, v129
	v_med3_f32 v101, v101, s20, v129
	v_med3_f32 v102, v102, s20, v129
	v_med3_f32 v103, v103, s20, v129
	v_med3_f32 v104, v104, s20, v129
	v_med3_f32 v105, v105, s20, v129
	v_med3_f32 v106, v106, s20, v129
	v_med3_f32 v107, v107, s20, v129
	v_med3_f32 v108, v108, s20, v129
	v_med3_f32 v109, v109, s20, v129
	v_med3_f32 v110, v110, s20, v129
	v_med3_f32 v111, v111, s20, v129
	v_med3_f32 v112, v112, s20, v129
	v_med3_f32 v113, v113, s20, v129
	v_med3_f32 v114, v114, s20, v129
	v_med3_f32 v115, v115, s20, v129
	v_mov_b32_e32 v116, 0
	v_mov_b32_e32 v117, 0
	v_mov_b32_e32 v118, 0
	v_mov_b32_e32 v119, 0
	v_cvt_pk_fp8_f32 v116, v100, v101
	v_cvt_pk_fp8_f32 v117, v104, v105
	v_cvt_pk_fp8_f32 v118, v108, v109
	v_cvt_pk_fp8_f32 v119, v112, v113
	v_cvt_pk_fp8_f32 v116, v102, v103 op_sel:[0,0,1]
	v_cvt_pk_fp8_f32 v117, v106, v107 op_sel:[0,0,1]
	v_cvt_pk_fp8_f32 v118, v110, v111 op_sel:[0,0,1]
	v_cvt_pk_fp8_f32 v119, v114, v115 op_sel:[0,0,1]
	s_nop 0
	global_store_dwordx4 v128, v[116:119], s[14:15]
	s_waitcnt vmcnt(12)
	v_mul_f32_e32 v36, 0x43000000, v36
	v_mul_f32_e32 v37, 0x43000000, v37
	v_mul_f32_e32 v38, 0x43000000, v38
	v_mul_f32_e32 v39, 0x43000000, v39
	ds_write_b128 v120, v[36:39]
	v_mul_f32_e32 v40, 0x43000000, v40
	v_mul_f32_e32 v41, 0x43000000, v41
	v_mul_f32_e32 v42, 0x43000000, v42
	v_mul_f32_e32 v43, 0x43000000, v43
	ds_write_b128 v120, v[40:43] offset:1024
	v_mul_f32_e32 v44, 0x43000000, v44
	v_mul_f32_e32 v45, 0x43000000, v45
	v_mul_f32_e32 v46, 0x43000000, v46
	v_mul_f32_e32 v47, 0x43000000, v47
	ds_write_b128 v120, v[44:47] offset:2048
	v_mul_f32_e32 v48, 0x43000000, v48
	v_mul_f32_e32 v49, 0x43000000, v49
	v_mul_f32_e32 v50, 0x43000000, v50
	v_mul_f32_e32 v51, 0x43000000, v51
	ds_write_b128 v120, v[48:51] offset:3072
	v_mul_f32_e32 v52, 0x43000000, v52
	v_mul_f32_e32 v53, 0x43000000, v53
	v_mul_f32_e32 v54, 0x43000000, v54
	v_mul_f32_e32 v55, 0x43000000, v55
	ds_write_b128 v120, v[52:55] offset:4096
	v_mul_f32_e32 v56, 0x43000000, v56
	v_mul_f32_e32 v57, 0x43000000, v57
	v_mul_f32_e32 v58, 0x43000000, v58
	v_mul_f32_e32 v59, 0x43000000, v59
	ds_write_b128 v120, v[56:59] offset:5120
	v_mul_f32_e32 v60, 0x43000000, v60
	v_mul_f32_e32 v61, 0x43000000, v61
	v_mul_f32_e32 v62, 0x43000000, v62
	v_mul_f32_e32 v63, 0x43000000, v63
	ds_write_b128 v120, v[60:63] offset:6144
	v_mul_f32_e32 v64, 0x43000000, v64
	v_mul_f32_e32 v65, 0x43000000, v65
	v_mul_f32_e32 v66, 0x43000000, v66
	v_mul_f32_e32 v67, 0x43000000, v67
	ds_write_b128 v120, v[64:67] offset:7168
	s_waitcnt lgkmcnt(0)
	s_barrier
; #define GAS __attribute__((address_space(1)))
; #define LAS __attribute__((address_space(3)))
; #define LDS_WAIT() asm volatile("s_waitcnt lgkmcnt(0)" ::: "memory")
; __device__ __forceinline__ unsigned pk4_fp8(float a, float b, float c, float d) {
;     a = fminf(fmaxf(a, -448.f), 448.f); b = fminf(fmaxf(b, -448.f), 448.f); c = fminf(fmaxf(c, -448.f), 448.f); d = fminf(fmaxf(d, -448.f), 448.f);
;     int w = __builtin_amdgcn_cvt_pk_fp8_f32(a, b, 0, false); w = __builtin_amdgcn_cvt_pk_fp8_f32(c, d, w, true); return (unsigned)w; }
;     const int pr = item >> 1, kb = 2 * (pr / nblk) + (item & 1), nb = pr % nblk, k0 = 64 * kb, n0 = 32 * nb;
;     const int nr = n0 + (lane & 31); const int sc = MAP == 1 ? src_col_in(nr) : nr;
;     float v[32];
; #pragma unroll
;     for (int i = 0; i < 32; ++i) v[i] = sc >= 0 ? W[(size_t)(k0 + 2 * i + (lane >> 5)) * Nsrc + sc] : 0.f;
; #pragma unroll
;     for (int i = 0; i < 32; ++i) { const int k = k0 + 2 * i + (lane >> 5); float x = v[i] * wscale; if (KS) x *= (k < ksplit ? ksA[k] : ksB[k - ksplit]); scr[(2 * i + (lane >> 5)) * 33 + (lane & 31)] = x; }
;     LDS_WAIT(); asm volatile("" ::: "memory");
;     const int c = lane & 7;
; #pragma unroll
;     for (int j = 0; j < 4; ++j) { const int n = (lane >> 3) + 8 * j; const LAS float* s = scr + (8 * c) * 33 + n;
;         const unsigned long long o = (unsigned long long)pg8::pk4_fp8(s[0 * 33], s[1 * 33], s[2 * 33], s[3 * 33]) | ((unsigned long long)pg8::pk4_fp8(s[4 * 33], s[5 * 33], s[6 * 33], s[7 * 33]) << 32);
;         *(GAS unsigned long long*)(WT + (size_t)(n0 + n) * K + k0 + 8 * c) = o; }
;     LDS_WAIT(); asm volatile("" ::: "memory");
; }
	s_add_i32 s17, s16, 960
	s_min_u32 s17, s17, 0x3ff
	s_lshr_b32 s18, s17, 5
	s_add_i32 s18, s18, 96
	s_and_b32 s19, s17, 31
	s_lshl_b32 s18, s18, 21
	s_lshl_b32 s19, s19, 9
	s_add_u32 s18, s18, s19
	s_add_u32 s12, s2, s18
	s_addc_u32 s13, s3, 0
	global_load_dwordx4 v[36:39], v126, s[12:13]
	s_add_u32 s12, s12, 0x8000
	s_addc_u32 s13, s13, 0
	global_load_dwordx4 v[40:43], v126, s[12:13]
	s_add_u32 s12, s12, 0x8000
	s_addc_u32 s13, s13, 0
	global_load_dwordx4 v[44:47], v126, s[12:13]
	s_add_u32 s12, s12, 0x8000
	s_addc_u32 s13, s13, 0
	global_load_dwordx4 v[48:51], v126, s[12:13]
	s_add_u32 s12, s12, 0x8000
	s_addc_u32 s13, s13, 0
	global_load_dwordx4 v[52:55], v126, s[12:13]
	s_add_u32 s12, s12, 0x8000
	s_addc_u32 s13, s13, 0
	global_load_dwordx4 v[56:59], v126, s[12:13]
	s_add_u32 s12, s12, 0x8000
	s_addc_u32 s13, s13, 0
	global_load_dwordx4 v[60:63], v126, s[12:13]
	s_add_u32 s12, s12, 0x8000
	s_addc_u32 s13, s13, 0
	global_load_dwordx4 v[64:67], v126, s[12:13]
	s_add_i32 s17, s16, 768
	s_min_u32 s17, s17, 0x3ff
	s_lshr_b32 s18, s17, 5
	s_add_i32 s18, s18, 96
	s_and_b32 s19, s17, 31
	s_lshl_b32 s19, s19, 21
	s_lshl_b32 s18, s18, 7
	s_add_u32 s18, s18, s19
	s_add_u32 s14, s4, s18
	s_addc_u32 s15, s5, 0
	ds_read_b32 v100, v122
	ds_read_b32 v101, v122 offset:512
	ds_read_b32 v102, v122 offset:1024
	ds_read_b32 v103, v122 offset:1536
	ds_read_b32 v104, v122 offset:2048
	ds_read_b32 v105, v122 offset:2560
	ds_read_b32 v106, v122 offset:3072
	ds_read_b32 v107, v122 offset:3584
	ds_read_b32 v108, v122 offset:4096
	ds_read_b32 v109, v122 offset:4608
	ds_read_b32 v110, v122 offset:5120
	ds_read_b32 v111, v122 offset:5632
	ds_read_b32 v112, v122 offset:6144
	ds_read_b32 v113, v122 offset:6656
	ds_read_b32 v114, v122 offset:7168
	ds_read_b32 v115, v122 offset:7680
	s_waitcnt lgkmcnt(0)
	v_max_f32_e32 v100, v100, v100
	v_max_f32_e32 v101, v101, v101
	v_max_f32_e32 v102, v102, v102
	v_max_f32_e32 v103, v103, v103
	v_max_f32_e32 v104, v104, v104
	v_max_f32_e32 v105, v105, v105
	v_max_f32_e32 v106, v106, v106
	v_max_f32_e32 v107, v107, v107
	v_max_f32_e32 v108, v108, v108
	v_max_f32_e32 v109, v109, v109
	v_max_f32_e32 v110, v110, v110
	v_max_f32_e32 v111, v111, v111
	v_max_f32_e32 v112, v112, v112
	v_max_f32_e32 v113, v113, v113
	v_max_f32_e32 v114, v114, v114
	v_max_f32_e32 v115, v115, v115
	v_med3_f32 v100, v100, s20, v129
	v_med3_f32 v101, v101, s20, v129
	v_med3_f32 v102, v102, s20, v129
	v_med3_f32 v103, v103, s20, v129
	v_med3_f32 v104, v104, s20, v129
	v_med3_f32 v105, v105, s20, v129
	v_med3_f32 v106, v106, s20, v129
	v_med3_f32 v107, v107, s20, v129
	v_med3_f32 v108, v108, s20, v129
	v_med3_f32 v109, v109, s20, v129
	v_med3_f32 v110, v110, s20, v129
	v_med3_f32 v111, v111, s20, v129
	v_med3_f32 v112, v112, s20, v129
	v_med3_f32 v113, v113, s20, v129
	v_med3_f32 v114, v114, s20, v129
	v_med3_f32 v115, v115, s20, v129
	v_mov_b32_e32 v116, 0
	v_mov_b32_e32 v117, 0
	v_mov_b32_e32 v118, 0
	v_mov_b32_e32 v119, 0
	v_cvt_pk_fp8_f32 v116, v100, v101
	v_cvt_pk_fp8_f32 v117, v104, v105
	v_cvt_pk_fp8_f32 v118, v108, v109
	v_cvt_pk_fp8_f32 v119, v112, v113
	v_cvt_pk_fp8_f32 v116, v102, v103 op_sel:[0,0,1]
	v_cvt_pk_fp8_f32 v117, v106, v107 op_sel:[0,0,1]
	v_cvt_pk_fp8_f32 v118, v110, v111 op_sel:[0,0,1]
	v_cvt_pk_fp8_f32 v119, v114, v115 op_sel:[0,0,1]
	s_nop 0
	global_store_dwordx4 v127, v[116:119], s[14:15]
	ds_read_b32 v100, v124
	ds_read_b32 v101, v124 offset:512
	ds_read_b32 v102, v124 offset:1024
	ds_read_b32 v103, v124 offset:1536
	ds_read_b32 v104, v124 offset:2048
	ds_read_b32 v105, v124 offset:2560
	ds_read_b32 v106, v124 offset:3072
	ds_read_b32 v107, v124 offset:3584
	ds_read_b32 v108, v124 offset:4096
	ds_read_b32 v109, v124 offset:4608
	ds_read_b32 v110, v124 offset:5120
	ds_read_b32 v111, v124 offset:5632
	ds_read_b32 v112, v124 offset:6144
	ds_read_b32 v113, v124 offset:6656
	ds_read_b32 v114, v124 offset:7168
	ds_read_b32 v115, v124 offset:7680
	s_waitcnt lgkmcnt(0)
	v_max_f32_e32 v100, v100, v100
	v_max_f32_e32 v101, v101, v101
	v_max_f32_e32 v102, v102, v102
	v_max_f32_e32 v103, v103, v103
	v_max_f32_e32 v104, v104, v104
	v_max_f32_e32 v105, v105, v105
	v_max_f32_e32 v106, v106, v106
	v_max_f32_e32 v107, v107, v107
	v_max_f32_e32 v108, v108, v108
	v_max_f32_e32 v109, v109, v109
	v_max_f32_e32 v110, v110, v110
	v_max_f32_e32 v111, v111, v111
	v_max_f32_e32 v112, v112, v112
	v_max_f32_e32 v113, v113, v113
	v_max_f32_e32 v114, v114, v114
	v_max_f32_e32 v115, v115, v115
	v_med3_f32 v100, v100, s20, v129
	v_med3_f32 v101, v101, s20, v129
	v_med3_f32 v102, v102, s20, v129
	v_med3_f32 v103, v103, s20, v129
	v_med3_f32 v104, v104, s20, v129
	v_med3_f32 v105, v105, s20, v129
	v_med3_f32 v106, v106, s20, v129
	v_med3_f32 v107, v107, s20, v129
	v_med3_f32 v108, v108, s20, v129
	v_med3_f32 v109, v109, s20, v129
	v_med3_f32 v110, v110, s20, v129
	v_med3_f32 v111, v111, s20, v129
	v_med3_f32 v112, v112, s20, v129
	v_med3_f32 v113, v113, s20, v129
	v_med3_f32 v114, v114, s20, v129
	v_med3_f32 v115, v115, s20, v129
	v_mov_b32_e32 v116, 0
	v_mov_b32_e32 v117, 0
	v_mov_b32_e32 v118, 0
	v_mov_b32_e32 v119, 0
	v_cvt_pk_fp8_f32 v116, v100, v101
	v_cvt_pk_fp8_f32 v117, v104, v105
	v_cvt_pk_fp8_f32 v118, v108, v109
	v_cvt_pk_fp8_f32 v119, v112, v113
	v_cvt_pk_fp8_f32 v116, v102, v103 op_sel:[0,0,1]
	v_cvt_pk_fp8_f32 v117, v106, v107 op_sel:[0,0,1]
	v_cvt_pk_fp8_f32 v118, v110, v111 op_sel:[0,0,1]
	v_cvt_pk_fp8_f32 v119, v114, v115 op_sel:[0,0,1]
	s_nop 0
	global_store_dwordx4 v128, v[116:119], s[14:15]
	s_waitcnt vmcnt(12)
	v_mul_f32_e32 v68, 0x43000000, v68
	v_mul_f32_e32 v69, 0x43000000, v69
	v_mul_f32_e32 v70, 0x43000000, v70
	v_mul_f32_e32 v71, 0x43000000, v71
	ds_write_b128 v121, v[68:71]
	v_mul_f32_e32 v72, 0x43000000, v72
	v_mul_f32_e32 v73, 0x43000000, v73
	v_mul_f32_e32 v74, 0x43000000, v74
	v_mul_f32_e32 v75, 0x43000000, v75
	ds_write_b128 v121, v[72:75] offset:1024
	v_mul_f32_e32 v76, 0x43000000, v76
	v_mul_f32_e32 v77, 0x43000000, v77
	v_mul_f32_e32 v78, 0x43000000, v78
	v_mul_f32_e32 v79, 0x43000000, v79
	ds_write_b128 v121, v[76:79] offset:2048
	v_mul_f32_e32 v80, 0x43000000, v80
	v_mul_f32_e32 v81, 0x43000000, v81
	v_mul_f32_e32 v82, 0x43000000, v82
	v_mul_f32_e32 v83, 0x43000000, v83
	ds_write_b128 v121, v[80:83] offset:3072
	v_mul_f32_e32 v84, 0x43000000, v84
	v_mul_f32_e32 v85, 0x43000000, v85
	v_mul_f32_e32 v86, 0x43000000, v86
	v_mul_f32_e32 v87, 0x43000000, v87
	ds_write_b128 v121, v[84:87] offset:4096
	v_mul_f32_e32 v88, 0x43000000, v88
	v_mul_f32_e32 v89, 0x43000000, v89
	v_mul_f32_e32 v90, 0x43000000, v90
	v_mul_f32_e32 v91, 0x43000000, v91
	ds_write_b128 v121, v[88:91] offset:5120
	v_mul_f32_e32 v92, 0x43000000, v92
	v_mul_f32_e32 v93, 0x43000000, v93
	v_mul_f32_e32 v94, 0x43000000, v94
	v_mul_f32_e32 v95, 0x43000000, v95
	ds_write_b128 v121, v[92:95] offset:6144
	v_mul_f32_e32 v96, 0x43000000, v96
	v_mul_f32_e32 v97, 0x43000000, v97
	v_mul_f32_e32 v98, 0x43000000, v98
	v_mul_f32_e32 v99, 0x43000000, v99
	ds_write_b128 v121, v[96:99] offset:7168
	s_waitcnt lgkmcnt(0)
	s_barrier
; #define GAS __attribute__((address_space(1)))
; #define LAS __attribute__((address_space(3)))
; #define LDS_WAIT() asm volatile("s_waitcnt lgkmcnt(0)" ::: "memory")
; __device__ __forceinline__ unsigned pk4_fp8(float a, float b, float c, float d) {
;     a = fminf(fmaxf(a, -448.f), 448.f); b = fminf(fmaxf(b, -448.f), 448.f); c = fminf(fmaxf(c, -448.f), 448.f); d = fminf(fmaxf(d, -448.f), 448.f);
;     int w = __builtin_amdgcn_cvt_pk_fp8_f32(a, b, 0, false); w = __builtin_amdgcn_cvt_pk_fp8_f32(c, d, w, true); return (unsigned)w; }
;     const int pr = item >> 1, kb = 2 * (pr / nblk) + (item & 1), nb = pr % nblk, k0 = 64 * kb, n0 = 32 * nb;
;     const int nr = n0 + (lane & 31); const int sc = MAP == 1 ? src_col_in(nr) : nr;
;     float v[32];
; #pragma unroll
;     for (int i = 0; i < 32; ++i) v[i] = sc >= 0 ? W[(size_t)(k0 + 2 * i + (lane >> 5)) * Nsrc + sc] : 0.f;
; #pragma unroll
;     for (int i = 0; i < 32; ++i) { const int k = k0 + 2 * i + (lane >> 5); float x = v[i] * wscale; if (KS) x *= (k < ksplit ? ksA[k] : ksB[k - ksplit]); scr[(2 * i + (lane >> 5)) * 33 + (lane & 31)] = x; }
;     LDS_WAIT(); asm volatile("" ::: "memory");
;     const int c = lane & 7;
; #pragma unroll
;     for (int j = 0; j < 4; ++j) { const int n = (lane >> 3) + 8 * j; const LAS float* s = scr + (8 * c) * 33 + n;
;         const unsigned long long o = (unsigned long long)pg8::pk4_fp8(s[0 * 33], s[1 * 33], s[2 * 33], s[3 * 33]) | ((unsigned long long)pg8::pk4_fp8(s[4 * 33], s[5 * 33], s[6 * 33], s[7 * 33]) << 32);
;         *(GAS unsigned long long*)(WT + (size_t)(n0 + n) * K + k0 + 8 * c) = o; }
;     LDS_WAIT(); asm volatile("" ::: "memory");
; }
	s_add_i32 s17, s16, 864
	s_min_u32 s17, s17, 0x3ff
	s_lshr_b32 s18, s17, 5
	s_add_i32 s18, s18, 96
	s_and_b32 s19, s17, 31
	s_lshl_b32 s19, s19, 21
	s_lshl_b32 s18, s18, 7
	s_add_u32 s18, s18, s19
	s_add_u32 s14, s4, s18
	s_addc_u32 s15, s5, 0
	ds_read_b32 v100, v123
	ds_read_b32 v101, v123 offset:512
	ds_read_b32 v102, v123 offset:1024
	ds_read_b32 v103, v123 offset:1536
	ds_read_b32 v104, v123 offset:2048
	ds_read_b32 v105, v123 offset:2560
	ds_read_b32 v106, v123 offset:3072
	ds_read_b32 v107, v123 offset:3584
	ds_read_b32 v108, v123 offset:4096
	ds_read_b32 v109, v123 offset:4608
	ds_read_b32 v110, v123 offset:5120
	ds_read_b32 v111, v123 offset:5632
	ds_read_b32 v112, v123 offset:6144
	ds_read_b32 v113, v123 offset:6656
	ds_read_b32 v114, v123 offset:7168
	ds_read_b32 v115, v123 offset:7680
	s_waitcnt lgkmcnt(0)
	v_max_f32_e32 v100, v100, v100
	v_max_f32_e32 v101, v101, v101
	v_max_f32_e32 v102, v102, v102
	v_max_f32_e32 v103, v103, v103
	v_max_f32_e32 v104, v104, v104
	v_max_f32_e32 v105, v105, v105
	v_max_f32_e32 v106, v106, v106
	v_max_f32_e32 v107, v107, v107
	v_max_f32_e32 v108, v108, v108
	v_max_f32_e32 v109, v109, v109
	v_max_f32_e32 v110, v110, v110
	v_max_f32_e32 v111, v111, v111
	v_max_f32_e32 v112, v112, v112
	v_max_f32_e32 v113, v113, v113
	v_max_f32_e32 v114, v114, v114
	v_max_f32_e32 v115, v115, v115
	v_med3_f32 v100, v100, s20, v129
	v_med3_f32 v101, v101, s20, v129
	v_med3_f32 v102, v102, s20, v129
	v_med3_f32 v103, v103, s20, v129
	v_med3_f32 v104, v104, s20, v129
	v_med3_f32 v105, v105, s20, v129
	v_med3_f32 v106, v106, s20, v129
	v_med3_f32 v107, v107, s20, v129
	v_med3_f32 v108, v108, s20, v129
	v_med3_f32 v109, v109, s20, v129
	v_med3_f32 v110, v110, s20, v129
	v_med3_f32 v111, v111, s20, v129
	v_med3_f32 v112, v112, s20, v129
	v_med3_f32 v113, v113, s20, v129
	v_med3_f32 v114, v114, s20, v129
	v_med3_f32 v115, v115, s20, v129
	v_mov_b32_e32 v116, 0
	v_mov_b32_e32 v117, 0
	v_mov_b32_e32 v118, 0
	v_mov_b32_e32 v119, 0
	v_cvt_pk_fp8_f32 v116, v100, v101
	v_cvt_pk_fp8_f32 v117, v104, v105
	v_cvt_pk_fp8_f32 v118, v108, v109
	v_cvt_pk_fp8_f32 v119, v112, v113
	v_cvt_pk_fp8_f32 v116, v102, v103 op_sel:[0,0,1]
	v_cvt_pk_fp8_f32 v117, v106, v107 op_sel:[0,0,1]
	v_cvt_pk_fp8_f32 v118, v110, v111 op_sel:[0,0,1]
	v_cvt_pk_fp8_f32 v119, v114, v115 op_sel:[0,0,1]
	s_nop 0
	global_store_dwordx4 v127, v[116:119], s[14:15]
	ds_read_b32 v100, v125
	ds_read_b32 v101, v125 offset:512
	ds_read_b32 v102, v125 offset:1024
	ds_read_b32 v103, v125 offset:1536
	ds_read_b32 v104, v125 offset:2048
	ds_read_b32 v105, v125 offset:2560
	ds_read_b32 v106, v125 offset:3072
	ds_read_b32 v107, v125 offset:3584
	ds_read_b32 v108, v125 offset:4096
	ds_read_b32 v109, v125 offset:4608
	ds_read_b32 v110, v125 offset:5120
	ds_read_b32 v111, v125 offset:5632
	ds_read_b32 v112, v125 offset:6144
	ds_read_b32 v113, v125 offset:6656
	ds_read_b32 v114, v125 offset:7168
	ds_read_b32 v115, v125 offset:7680
	s_waitcnt lgkmcnt(0)
	v_max_f32_e32 v100, v100, v100
	v_max_f32_e32 v101, v101, v101
	v_max_f32_e32 v102, v102, v102
	v_max_f32_e32 v103, v103, v103
	v_max_f32_e32 v104, v104, v104
	v_max_f32_e32 v105, v105, v105
	v_max_f32_e32 v106, v106, v106
	v_max_f32_e32 v107, v107, v107
	v_max_f32_e32 v108, v108, v108
	v_max_f32_e32 v109, v109, v109
	v_max_f32_e32 v110, v110, v110
	v_max_f32_e32 v111, v111, v111
	v_max_f32_e32 v112, v112, v112
	v_max_f32_e32 v113, v113, v113
	v_max_f32_e32 v114, v114, v114
	v_max_f32_e32 v115, v115, v115
	v_med3_f32 v100, v100, s20, v129
	v_med3_f32 v101, v101, s20, v129
	v_med3_f32 v102, v102, s20, v129
	v_med3_f32 v103, v103, s20, v129
	v_med3_f32 v104, v104, s20, v129
	v_med3_f32 v105, v105, s20, v129
	v_med3_f32 v106, v106, s20, v129
	v_med3_f32 v107, v107, s20, v129
	v_med3_f32 v108, v108, s20, v129
	v_med3_f32 v109, v109, s20, v129
	v_med3_f32 v110, v110, s20, v129
	v_med3_f32 v111, v111, s20, v129
	v_med3_f32 v112, v112, s20, v129
	v_med3_f32 v113, v113, s20, v129
	v_med3_f32 v114, v114, s20, v129
	v_med3_f32 v115, v115, s20, v129
	v_mov_b32_e32 v116, 0
	v_mov_b32_e32 v117, 0
	v_mov_b32_e32 v118, 0
	v_mov_b32_e32 v119, 0
	v_cvt_pk_fp8_f32 v116, v100, v101
	v_cvt_pk_fp8_f32 v117, v104, v105
	v_cvt_pk_fp8_f32 v118, v108, v109
	v_cvt_pk_fp8_f32 v119, v112, v113
	v_cvt_pk_fp8_f32 v116, v102, v103 op_sel:[0,0,1]
	v_cvt_pk_fp8_f32 v117, v106, v107 op_sel:[0,0,1]
	v_cvt_pk_fp8_f32 v118, v110, v111 op_sel:[0,0,1]
	v_cvt_pk_fp8_f32 v119, v114, v115 op_sel:[0,0,1]
	s_nop 0
	global_store_dwordx4 v128, v[116:119], s[14:15]
	s_waitcnt vmcnt(4)
	v_mul_f32_e32 v36, 0x43000000, v36
	v_mul_f32_e32 v37, 0x43000000, v37
	v_mul_f32_e32 v38, 0x43000000, v38
	v_mul_f32_e32 v39, 0x43000000, v39
	ds_write_b128 v120, v[36:39]
	v_mul_f32_e32 v40, 0x43000000, v40
	v_mul_f32_e32 v41, 0x43000000, v41
	v_mul_f32_e32 v42, 0x43000000, v42
	v_mul_f32_e32 v43, 0x43000000, v43
	ds_write_b128 v120, v[40:43] offset:1024
	v_mul_f32_e32 v44, 0x43000000, v44
	v_mul_f32_e32 v45, 0x43000000, v45
	v_mul_f32_e32 v46, 0x43000000, v46
	v_mul_f32_e32 v47, 0x43000000, v47
	ds_write_b128 v120, v[44:47] offset:2048
	v_mul_f32_e32 v48, 0x43000000, v48
	v_mul_f32_e32 v49, 0x43000000, v49
	v_mul_f32_e32 v50, 0x43000000, v50
	v_mul_f32_e32 v51, 0x43000000, v51
	ds_write_b128 v120, v[48:51] offset:3072
	v_mul_f32_e32 v52, 0x43000000, v52
	v_mul_f32_e32 v53, 0x43000000, v53
	v_mul_f32_e32 v54, 0x43000000, v54
	v_mul_f32_e32 v55, 0x43000000, v55
	ds_write_b128 v120, v[52:55] offset:4096
	v_mul_f32_e32 v56, 0x43000000, v56
	v_mul_f32_e32 v57, 0x43000000, v57
	v_mul_f32_e32 v58, 0x43000000, v58
	v_mul_f32_e32 v59, 0x43000000, v59
	ds_write_b128 v120, v[56:59] offset:5120
	v_mul_f32_e32 v60, 0x43000000, v60
	v_mul_f32_e32 v61, 0x43000000, v61
	v_mul_f32_e32 v62, 0x43000000, v62
	v_mul_f32_e32 v63, 0x43000000, v63
	ds_write_b128 v120, v[60:63] offset:6144
	v_mul_f32_e32 v64, 0x43000000, v64
	v_mul_f32_e32 v65, 0x43000000, v65
	v_mul_f32_e32 v66, 0x43000000, v66
	v_mul_f32_e32 v67, 0x43000000, v67
	ds_write_b128 v120, v[64:67] offset:7168
	s_waitcnt lgkmcnt(0)
	s_barrier
; #define GAS __attribute__((address_space(1)))
; #define LAS __attribute__((address_space(3)))
;     const int pr = item >> 1, kb = 2 * (pr / nblk) + (item & 1), nb = pr % nblk, k0 = 64 * kb, n0 = 32 * nb;
;     const int nr = n0 + (lane & 31); const int sc = MAP == 1 ? src_col_in(nr) : nr;
;     float v[32];
; #pragma unroll
;     for (int i = 0; i < 32; ++i) v[i] = sc >= 0 ? W[(size_t)(k0 + 2 * i + (lane >> 5)) * Nsrc + sc] : 0.f;
; #pragma unroll
;     for (int i = 0; i < 32; ++i) { const int k = k0 + 2 * i + (lane >> 5); float x = v[i] * wscale; if (KS) x *= (k < ksplit ? ksA[k] : ksB[k - ksplit]); scr[(2 * i + (lane >> 5)) * 33 + (lane & 31)] = x; }
;     LDS_WAIT(); asm volatile("" ::: "memory");
;     const int c = lane & 7;
; #pragma unroll
;     for (int j = 0; j < 4; ++j) { const int n = (lane >> 3) + 8 * j; const LAS float* s = scr + (8 * c) * 33 + n;
;         const unsigned long long o = (unsigned long long)pg8::pk4_fp8(s[0 * 33], s[1 * 33], s[2 * 33], s[3 * 33]) | ((unsigned long long)pg8::pk4_fp8(s[4 * 33], s[5 * 33], s[6 * 33], s[7 * 33]) << 32);
;         *(GAS unsigned long long*)(WT + (size_t)(n0 + n) * K + k0 + 8 * c) = o; }
;     LDS_WAIT(); asm volatile("" ::: "memory");
; }
; __global__ void __launch_bounds__(NWAVES * 64, 2) hybrid_fwd(Args args) {
;     ...
;     for (int L = 0; L < DEPTH; ++L) {
;         { unsigned long long wz = 0; asm volatile("" : "+s"(wz)); ws = args.ws + wz; }
;         bf16* Hres = (bf16*)(ws + WS_H);     static_assert(DEPTH == 2 && WO_F8_FROM == 1 && PROJ_F8_FROM == 1, "the phase instantiations below are written for this precision plan");
;         bf16* XN = (bf16*)(ws + WS_XN); bf16* PROJ = (bf16*)(ws + WS_PROJ); bf16* ACT = (bf16*)(ws + WS_ACT); unsigned char* CAT = (unsigned char*)(ws + WS_CAT);     const bool wo_f8 = L >= WO_F8_FROM;
;         float* ATT = (float*)(ws + WS_ATT); bf16* XBC = (bf16*)(ws + WS_XBC); bf16* Y = (bf16*)(ws + WS_Y);
;         bf16* KC = (bf16*)(ws + WS_KC); bf16* VC = (bf16*)(ws + WS_VC); float* DT = (float*)(ws + WS_DT); float* ADT = (float*)(ws + WS_ADT);
;         float* COS = (float*)(ws + WS_COS); float* SIN = (float*)(ws + WS_SIN); unsigned* BMP = (unsigned*)(ws + WS_BMP);
;         bf16* AO = (bf16*)(ws + WS_ACT);     float* STT = (float*)(ws + WS_ST); bf16* PREVB = (bf16*)(ws + WS_PREV);     float* ACSG = (float*)(ws + WS_ACSG); float* DEC = (float*)(ws + WS_DEC);
	s_add_i32 s17, s16, 960
	s_min_u32 s17, s17, 0x3ff
	s_lshr_b32 s18, s17, 5
	s_add_i32 s18, s18, 96
	s_and_b32 s19, s17, 31
	s_lshl_b32 s19, s19, 21
	s_lshl_b32 s18, s18, 7
	s_add_u32 s18, s18, s19
	s_add_u32 s14, s4, s18
	s_addc_u32 s15, s5, 0
	ds_read_b32 v100, v122
	ds_read_b32 v101, v122 offset:512
	ds_read_b32 v102, v122 offset:1024
	ds_read_b32 v103, v122 offset:1536
	ds_read_b32 v104, v122 offset:2048
	ds_read_b32 v105, v122 offset:2560
	ds_read_b32 v106, v122 offset:3072
	ds_read_b32 v107, v122 offset:3584
	ds_read_b32 v108, v122 offset:4096
	ds_read_b32 v109, v122 offset:4608
	ds_read_b32 v110, v122 offset:5120
	ds_read_b32 v111, v122 offset:5632
	ds_read_b32 v112, v122 offset:6144
	ds_read_b32 v113, v122 offset:6656
	ds_read_b32 v114, v122 offset:7168
	ds_read_b32 v115, v122 offset:7680
	s_waitcnt lgkmcnt(0)
	v_max_f32_e32 v100, v100, v100
	v_max_f32_e32 v101, v101, v101
	v_max_f32_e32 v102, v102, v102
	v_max_f32_e32 v103, v103, v103
	v_max_f32_e32 v104, v104, v104
	v_max_f32_e32 v105, v105, v105
	v_max_f32_e32 v106, v106, v106
	v_max_f32_e32 v107, v107, v107
	v_max_f32_e32 v108, v108, v108
	v_max_f32_e32 v109, v109, v109
	v_max_f32_e32 v110, v110, v110
	v_max_f32_e32 v111, v111, v111
	v_max_f32_e32 v112, v112, v112
	v_max_f32_e32 v113, v113, v113
	v_max_f32_e32 v114, v114, v114
	v_max_f32_e32 v115, v115, v115
	v_med3_f32 v100, v100, s20, v129
	v_med3_f32 v101, v101, s20, v129
	v_med3_f32 v102, v102, s20, v129
	v_med3_f32 v103, v103, s20, v129
	v_med3_f32 v104, v104, s20, v129
	v_med3_f32 v105, v105, s20, v129
	v_med3_f32 v106, v106, s20, v129
	v_med3_f32 v107, v107, s20, v129
	v_med3_f32 v108, v108, s20, v129
	v_med3_f32 v109, v109, s20, v129
	v_med3_f32 v110, v110, s20, v129
	v_med3_f32 v111, v111, s20, v129
	v_med3_f32 v112, v112, s20, v129
	v_med3_f32 v113, v113, s20, v129
	v_med3_f32 v114, v114, s20, v129
	v_med3_f32 v115, v115, s20, v129
	v_mov_b32_e32 v116, 0
	v_mov_b32_e32 v117, 0
	v_mov_b32_e32 v118, 0
	v_mov_b32_e32 v119, 0
	v_cvt_pk_fp8_f32 v116, v100, v101
	v_cvt_pk_fp8_f32 v117, v104, v105
	v_cvt_pk_fp8_f32 v118, v108, v109
	v_cvt_pk_fp8_f32 v119, v112, v113
	v_cvt_pk_fp8_f32 v116, v102, v103 op_sel:[0,0,1]
	v_cvt_pk_fp8_f32 v117, v106, v107 op_sel:[0,0,1]
	v_cvt_pk_fp8_f32 v118, v110, v111 op_sel:[0,0,1]
	v_cvt_pk_fp8_f32 v119, v114, v115 op_sel:[0,0,1]
	s_nop 0
	global_store_dwordx4 v127, v[116:119], s[14:15]
	ds_read_b32 v100, v124
	ds_read_b32 v101, v124 offset:512
	ds_read_b32 v102, v124 offset:1024
	ds_read_b32 v103, v124 offset:1536
	ds_read_b32 v104, v124 offset:2048
	ds_read_b32 v105, v124 offset:2560
	ds_read_b32 v106, v124 offset:3072
	ds_read_b32 v107, v124 offset:3584
	ds_read_b32 v108, v124 offset:4096
	ds_read_b32 v109, v124 offset:4608
	ds_read_b32 v110, v124 offset:5120
	ds_read_b32 v111, v124 offset:5632
	ds_read_b32 v112, v124 offset:6144
	ds_read_b32 v113, v124 offset:6656
	ds_read_b32 v114, v124 offset:7168
	ds_read_b32 v115, v124 offset:7680
	s_waitcnt lgkmcnt(0)
	v_max_f32_e32 v100, v100, v100
	v_max_f32_e32 v101, v101, v101
	v_max_f32_e32 v102, v102, v102
	v_max_f32_e32 v103, v103, v103
	v_max_f32_e32 v104, v104, v104
	v_max_f32_e32 v105, v105, v105
	v_max_f32_e32 v106, v106, v106
	v_max_f32_e32 v107, v107, v107
	v_max_f32_e32 v108, v108, v108
	v_max_f32_e32 v109, v109, v109
	v_max_f32_e32 v110, v110, v110
	v_max_f32_e32 v111, v111, v111
	v_max_f32_e32 v112, v112, v112
	v_max_f32_e32 v113, v113, v113
	v_max_f32_e32 v114, v114, v114
	v_max_f32_e32 v115, v115, v115
	v_med3_f32 v100, v100, s20, v129
	v_med3_f32 v101, v101, s20, v129
	v_med3_f32 v102, v102, s20, v129
	v_med3_f32 v103, v103, s20, v129
	v_med3_f32 v104, v104, s20, v129
	v_med3_f32 v105, v105, s20, v129
	v_med3_f32 v106, v106, s20, v129
	v_med3_f32 v107, v107, s20, v129
	v_med3_f32 v108, v108, s20, v129
	v_med3_f32 v109, v109, s20, v129
	v_med3_f32 v110, v110, s20, v129
	v_med3_f32 v111, v111, s20, v129
	v_med3_f32 v112, v112, s20, v129
	v_med3_f32 v113, v113, s20, v129
	v_med3_f32 v114, v114, s20, v129
	v_med3_f32 v115, v115, s20, v129
	v_mov_b32_e32 v116, 0
	v_mov_b32_e32 v117, 0
	v_mov_b32_e32 v118, 0
	v_mov_b32_e32 v119, 0
	v_cvt_pk_fp8_f32 v116, v100, v101
	v_cvt_pk_fp8_f32 v117, v104, v105
	v_cvt_pk_fp8_f32 v118, v108, v109
	v_cvt_pk_fp8_f32 v119, v112, v113
	v_cvt_pk_fp8_f32 v116, v102, v103 op_sel:[0,0,1]
	v_cvt_pk_fp8_f32 v117, v106, v107 op_sel:[0,0,1]
	v_cvt_pk_fp8_f32 v118, v110, v111 op_sel:[0,0,1]
	v_cvt_pk_fp8_f32 v119, v114, v115 op_sel:[0,0,1]
	s_nop 0
	global_store_dwordx4 v128, v[116:119], s[14:15]
	s_waitcnt vmcnt(0) lgkmcnt(0)
	s_barrier
.Llite_skip:
.LBB0_576:
	s_xor_b64 s[0:1], s[8:9], -1
	v_writelane_b32 v255, s0, 2
	s_xor_b64 s[20:21], s[10:11], -1
	s_mov_b32 s2, s56
	v_writelane_b32 v255, s1, 3
	s_xor_b64 s[0:1], s[6:7], -1
	s_add_u32 s64, s28, 0x5ea00000
	s_addc_u32 s65, s29, 0
	s_add_u32 s68, s28, 0x6aa00000
	s_addc_u32 s69, s29, 0
	v_writelane_b32 v255, s0, 4
	s_add_u32 s38, s28, 0x6aa80000
	s_addc_u32 s39, s29, 0
	v_writelane_b32 v255, s1, 5
	s_mov_b32 s0, s77
	s_cmpk_gt_i32 s0, 0x9f
	s_cselect_b64 s[0:1], -1, 0
	s_and_b64 s[22:23], s[10:11], s[0:1]
	s_lshl_b32 s45, s56, 1
	s_add_u32 s82, s28, 0x6b281000
	s_addc_u32 s77, s29, 0
	s_add_u32 s56, s28, 0x6b681000
	s_addc_u32 s46, s29, 0
	s_add_u32 s47, s28, 0x6b6a1000
	s_mov_b32 s3, s43
	v_readlane_b32 s4, v253, 3
	s_addc_u32 s57, s29, 0
	s_lshl_b64 s[0:1], s[2:3], 16
	v_readlane_b32 s18, v253, 17
	v_readlane_b32 s19, v253, 18
	s_add_u32 s0, s18, s0
	s_addc_u32 s1, s19, s1
	v_writelane_b32 v255, s0, 6
	v_readlane_b32 s5, v253, 4
	v_readlane_b32 s6, v253, 5
	v_writelane_b32 v255, s1, 7
	s_mov_b32 s0, s2
	v_readlane_b32 s7, v253, 6
	v_readlane_b32 s8, v253, 7
	v_readlane_b32 s9, v253, 8
	v_readlane_b32 s10, v253, 9
	v_readlane_b32 s11, v253, 10
	v_readlane_b32 s12, v253, 11
	v_readlane_b32 s13, v253, 12
	v_readlane_b32 s14, v253, 13
	v_readlane_b32 s15, v253, 14
	v_readlane_b32 s16, v253, 15
	v_readlane_b32 s17, v253, 16
	v_writelane_b32 v255, s0, 8
	v_readlane_b32 s4, v253, 19
	v_readlane_b32 s5, v253, 20
	v_writelane_b32 v255, s1, 9
	s_lshl_b64 s[0:1], s[2:3], 14
	s_add_u32 s0, s4, s0
	s_addc_u32 s1, s5, s1
	v_readlane_b32 s8, v253, 23
	v_readlane_b32 s9, v253, 24
	v_readlane_b32 s12, v253, 27
	v_readlane_b32 s13, v253, 28
	v_writelane_b32 v255, s0, 10
	s_mov_b64 s[50:51], -1
	s_mov_b64 s[12:13], s[22:23]
	s_mov_b64 s[8:9], s[20:21]
	v_writelane_b32 v255, s1, 11
	v_readlane_b32 s6, v253, 21
	v_readlane_b32 s7, v253, 22
	v_readlane_b32 s10, v253, 25
	v_readlane_b32 s11, v253, 26
	v_readlane_b32 s14, v253, 29
	v_readlane_b32 s15, v253, 30
	v_readlane_b32 s16, v253, 31
	v_readlane_b32 s17, v253, 32
	v_readlane_b32 s18, v253, 33
	v_readlane_b32 s19, v253, 34
	s_branch .LBB0_580
